# dead m0 save/restore pairs around LDS-DMA removed everywhere (122); 69 LDS-DMA sites issue the m0 write before the address computation so that it fills the wait state instead of s_nop 0
# baseline (speedup 1.0000x reference)
; #define PG8_STAGE_B(bufoff, gbase) do { _Pragma("unroll") for (int _i = 0; _i < 2; ++_i) \
;         __builtin_amdgcn_global_load_lds((const unsigned*)((const char*)(gbase) + voffB[_i]), (LAS unsigned*)(lds + (bufoff) + ldsw + _i * 8192), 16, 0, 0); } while (0)
; #define PG8_LDA(dst, b, h) do { _Pragma("unroll") for (int m = 0; m < 4; ++m) _Pragma("unroll") for (int k = 0; k < 2; ++k) dst[m][k] = *(const LAS bf16x8*)(lds + PG8_SA(b, h) + aoff + m * 2048 + k * 1024); } while (0)
; #define PG8_LDB(dst, b, h) do { _Pragma("unroll") for (int n = 0; n < 2; ++n) _Pragma("unroll") for (int k = 0; k < 2; ++k) dst[n][k] = *(const LAS bf16x8*)(lds + PG8_SB(b, h) + boff + n * 2048 + k * 1024); } while (0)
; #define PG8_MMA(ai, bj, At, Bt) do { __builtin_amdgcn_s_setprio(1); _Pragma("unroll") for (int m = 0; m < 4; ++m) _Pragma("unroll") for (int n = 0; n < 2; ++n) _Pragma("unroll") for (int k = 0; k < 2; ++k) \
;         acc[ai][bj][m][n] = __builtin_amdgcn_mfma_f32_16x16x32_bf16(Bt[n][k], At[m][k], acc[ai][bj][m][n], 0, 0, 0); __builtin_amdgcn_s_setprio(0); } while (0)
; #define PG8_WAIT_V(n) asm volatile("s_waitcnt vmcnt(" #n ")" ::: "memory")
; #define PG8_WAIT_L(n) asm volatile("s_waitcnt lgkmcnt(" #n ")" ::: "memory")
; template <class Epi, class Sched, bool GATHER = false>
; __device__ __forceinline__ void gemm_phase(LAS unsigned char* lds, const Gemm g, const Sched& S, const Epi& E) {
;     ...
;         for (int t = 0; t < nt; t += 2) {
;             const bool last = (t == nt - 2);
;             const char* a1 = cA + (size_t)(t + 1) * kstep;
;             const char* a2 = last ? nA : cA + (size_t)(t + 2) * kstep; const char* b2 = last ? nB : cB + (size_t)(t + 2) * kstep;
;             const char* a3 = a2 + kstep; const char* b3 = b2 + kstep;
;             unsigned vo2[2][2];
;             if constexpr (GATHER) {
; #pragma unroll
;             for (int _h = 0; _h < 2; ++_h)
; #pragma unroll
;                 for (int _i = 0; _i < 2; ++_i) vo2[_h][_i] = last ? voN[_h][_i] : voC[_h][_i]; }
;             PG8_LDB(B0, 0, 0); PG8_LDB(B1, 0, 1); PG8_SCHED; PG8_LDA(At, 0, 0); PG8_STAGE_A(PG8_SA(1, 1), a1, voC, 1);
;             PG8_WAIT_V(8); PG8_WAIT_L(0); PG8_BAR; PG8_MMA(0, 0, At, B0); PG8_MMA(0, 1, At, B1); PG8_BAR; PG8_SCHED;
;             PG8_LDA(At, 0, 1); PG8_STAGE_B(PG8_SB(0, 0), b2); PG8_STAGE_B(PG8_SB(0, 1), b2 + hstepB); PG8_STAGE_A(PG8_SA(0, 0), a2, vo2, 0);
.LBB0_325:
	s_add_u32 s14, s28, 0xfffc0080
	s_addc_u32 s15, s29, -1
	s_add_i32 s50, 0, 0x10000
	s_cmp_eq_u32 s49, 12
	s_cselect_b32 s31, s21, s15
	s_cselect_b32 s30, s45, s14
	v_add_u32_e32 v139, s50, v136
	s_cselect_b32 s15, s11, s48
	s_cselect_b32 s14, s46, s47
	s_add_i32 s52, 0, 0x14000
	ds_read_b128 v[140:143], v139
	ds_read_b128 v[144:147], v139 offset:1024
	ds_read_b128 v[148:151], v139 offset:2048
	ds_read_b128 v[152:155], v139 offset:3072
	v_add_u32_e32 v139, s52, v136
	ds_read_b128 v[156:159], v139
	ds_read_b128 v[160:163], v139 offset:1024
	ds_read_b128 v[164:167], v139 offset:2048
	ds_read_b128 v[168:171], v139 offset:3072
	v_lshl_add_u64 v[192:193], s[28:29], 0, v[132:133]
	s_add_i32 m0, s36, 0xc000
	ds_read_b128 v[172:175], v138
	ds_read_b128 v[176:179], v138 offset:1024
	ds_read_b128 v[180:183], v138 offset:2048
	ds_read_b128 v[184:187], v138 offset:3072
	ds_read_b128 v[188:191], v138 offset:4096
	ds_read_b128 v[204:207], v138 offset:5120
	ds_read_b128 v[208:211], v138 offset:6144
	ds_read_b128 v[212:215], v138 offset:7168
	global_load_lds_dwordx4 v[192:193], off
	s_add_i32 m0, s36, 0xe000
	v_lshl_add_u64 v[192:193], s[28:29], 0, v[134:135]
	global_load_lds_dwordx4 v[192:193], off
	s_waitcnt vmcnt(8)
	s_waitcnt lgkmcnt(0)
	s_barrier
	s_setprio 1
	s_waitcnt lgkmcnt(0)
	v_mfma_f32_16x16x32_bf16 v[126:129], v[140:143], v[172:175], v[126:129]
	v_mfma_f32_16x16x32_bf16 v[122:125], v[148:151], v[172:175], v[122:125]
	v_mfma_f32_16x16x32_bf16 v[118:121], v[140:143], v[180:183], v[118:121]
	v_mfma_f32_16x16x32_bf16 v[114:117], v[148:151], v[180:183], v[114:117]
	v_mfma_f32_16x16x32_bf16 v[106:109], v[140:143], v[188:191], v[106:109]
	v_mfma_f32_16x16x32_bf16 v[98:101], v[148:151], v[188:191], v[98:101]
	v_mfma_f32_16x16x32_bf16 v[90:93], v[140:143], v[208:211], v[90:93]
	v_mfma_f32_16x16x32_bf16 v[82:85], v[148:151], v[208:211], v[82:85]
	v_mfma_f32_16x16x32_bf16 v[126:129], v[144:147], v[176:179], v[126:129]
	v_mfma_f32_16x16x32_bf16 v[122:125], v[152:155], v[176:179], v[122:125]
	v_mfma_f32_16x16x32_bf16 v[118:121], v[144:147], v[184:187], v[118:121]
	v_mfma_f32_16x16x32_bf16 v[114:117], v[152:155], v[184:187], v[114:117]
	v_mfma_f32_16x16x32_bf16 v[106:109], v[144:147], v[204:207], v[106:109]
	v_mfma_f32_16x16x32_bf16 v[98:101], v[152:155], v[204:207], v[98:101]
	v_mfma_f32_16x16x32_bf16 v[90:93], v[144:147], v[212:215], v[90:93]
	v_mfma_f32_16x16x32_bf16 v[82:85], v[152:155], v[212:215], v[82:85]
	s_setprio 0
	s_setprio 1
	v_mfma_f32_16x16x32_bf16 v[110:113], v[156:159], v[172:175], v[110:113]
	v_mfma_f32_16x16x32_bf16 v[102:105], v[164:167], v[172:175], v[102:105]
	v_mfma_f32_16x16x32_bf16 v[94:97], v[156:159], v[180:183], v[94:97]
	v_mfma_f32_16x16x32_bf16 v[86:89], v[164:167], v[180:183], v[86:89]
	v_mfma_f32_16x16x32_bf16 v[78:81], v[156:159], v[188:191], v[78:81]
	v_mfma_f32_16x16x32_bf16 v[74:77], v[164:167], v[188:191], v[74:77]
	v_mfma_f32_16x16x32_bf16 v[70:73], v[156:159], v[208:211], v[70:73]
	v_mfma_f32_16x16x32_bf16 v[66:69], v[164:167], v[208:211], v[66:69]
	v_mfma_f32_16x16x32_bf16 v[110:113], v[160:163], v[176:179], v[110:113]
	v_mfma_f32_16x16x32_bf16 v[102:105], v[168:171], v[176:179], v[102:105]
	v_mfma_f32_16x16x32_bf16 v[94:97], v[160:163], v[184:187], v[94:97]
	v_mfma_f32_16x16x32_bf16 v[86:89], v[168:171], v[184:187], v[86:89]
	v_mfma_f32_16x16x32_bf16 v[78:81], v[160:163], v[204:207], v[78:81]
	v_mfma_f32_16x16x32_bf16 v[74:77], v[168:171], v[204:207], v[74:77]
	v_mfma_f32_16x16x32_bf16 v[70:73], v[160:163], v[212:215], v[70:73]
	v_mfma_f32_16x16x32_bf16 v[66:69], v[168:171], v[212:215], v[66:69]
	s_setprio 0
	s_barrier
	s_add_i32 s50, s50, s35
	v_lshl_add_u64 v[192:193], s[14:15], 0, v[194:195]
	s_mov_b32 m0, s50
	ds_read_b128 v[172:175], v138 offset:16384
	ds_read_b128 v[176:179], v138 offset:17408
	ds_read_b128 v[180:183], v138 offset:18432
	ds_read_b128 v[184:187], v138 offset:19456
	ds_read_b128 v[188:191], v138 offset:20480
	ds_read_b128 v[204:207], v138 offset:21504
	ds_read_b128 v[208:211], v138 offset:22528
	ds_read_b128 v[212:215], v138 offset:23552
	global_load_lds_dwordx4 v[192:193], off
	s_add_i32 m0, s50, 0x2000
	s_add_u32 s50, s14, 0x40000
	v_lshl_add_u64 v[198:199], s[14:15], 0, v[130:131]
	s_addc_u32 s51, s15, 0
	s_add_i32 s52, s52, s35
	global_load_lds_dwordx4 v[198:199], off
	v_lshl_add_u64 v[200:201], s[50:51], 0, v[194:195]
	s_mov_b32 m0, s52
	v_lshl_add_u64 v[216:217], s[30:31], 0, v[130:131]
	global_load_lds_dwordx4 v[200:201], off
	s_add_i32 m0, s52, 0x2000
	v_lshl_add_u64 v[200:201], s[50:51], 0, v[130:131]
	global_load_lds_dwordx4 v[200:201], off
	s_mov_b32 m0, s36
	v_lshl_add_u64 v[200:201], s[30:31], 0, v[194:195]
	global_load_lds_dwordx4 v[200:201], off
	s_mov_b32 m0, s37
	s_nop 0
	global_load_lds_dwordx4 v[216:217], off
	s_waitcnt vmcnt(8)
	s_waitcnt lgkmcnt(0)
	s_barrier
; #define PG8_LDA(dst, b, h) do { _Pragma("unroll") for (int m = 0; m < 4; ++m) _Pragma("unroll") for (int k = 0; k < 2; ++k) dst[m][k] = *(const LAS bf16x8*)(lds + PG8_SA(b, h) + aoff + m * 2048 + k * 1024); } while (0)
; #define PG8_LDB(dst, b, h) do { _Pragma("unroll") for (int n = 0; n < 2; ++n) _Pragma("unroll") for (int k = 0; k < 2; ++k) dst[n][k] = *(const LAS bf16x8*)(lds + PG8_SB(b, h) + boff + n * 2048 + k * 1024); } while (0)
; #define PG8_MMA(ai, bj, At, Bt) do { __builtin_amdgcn_s_setprio(1); _Pragma("unroll") for (int m = 0; m < 4; ++m) _Pragma("unroll") for (int n = 0; n < 2; ++n) _Pragma("unroll") for (int k = 0; k < 2; ++k) \
;         acc[ai][bj][m][n] = __builtin_amdgcn_mfma_f32_16x16x32_bf16(Bt[n][k], At[m][k], acc[ai][bj][m][n], 0, 0, 0); __builtin_amdgcn_s_setprio(0); } while (0)
; #define PG8_WAIT_V(n) asm volatile("s_waitcnt vmcnt(" #n ")" ::: "memory")
; #define PG8_WAIT_L(n) asm volatile("s_waitcnt lgkmcnt(" #n ")" ::: "memory")
; #define PG8_BAR __builtin_amdgcn_s_barrier()
; #define PG8_SCHED __builtin_amdgcn_sched_barrier(0)
; template <class Epi, class Sched, bool GATHER = false>
; __device__ __forceinline__ void gemm_phase(LAS unsigned char* lds, const Gemm g, const Sched& S, const Epi& E) {
;     ...
;             PG8_WAIT_V(8); PG8_WAIT_L(0); PG8_BAR; PG8_MMA(1, 0, At, B0); PG8_MMA(1, 1, At, B1); PG8_BAR; PG8_SCHED;
;             PG8_LDB(B0, 1, 0); PG8_LDB(B1, 1, 1); PG8_SCHED; PG8_LDA(At, 1, 0); PG8_STAGE_A(PG8_SA(0, 1), a2, vo2, 1);
;             PG8_WAIT_V(8); PG8_WAIT_L(0); PG8_BAR; PG8_MMA(0, 0, At, B0); PG8_MMA(0, 1, At, B1); PG8_BAR; PG8_SCHED;
	s_setprio 1
	s_waitcnt lgkmcnt(0)
	v_mfma_f32_16x16x32_bf16 v[62:65], v[140:143], v[172:175], v[62:65]
	v_mfma_f32_16x16x32_bf16 v[58:61], v[148:151], v[172:175], v[58:61]
	v_mfma_f32_16x16x32_bf16 v[54:57], v[140:143], v[180:183], v[54:57]
	v_mfma_f32_16x16x32_bf16 v[50:53], v[148:151], v[180:183], v[50:53]
	v_mfma_f32_16x16x32_bf16 v[42:45], v[140:143], v[188:191], v[42:45]
	v_mfma_f32_16x16x32_bf16 v[34:37], v[148:151], v[188:191], v[34:37]
	v_mfma_f32_16x16x32_bf16 v[22:25], v[140:143], v[208:211], v[22:25]
	v_mfma_f32_16x16x32_bf16 v[18:21], v[148:151], v[208:211], v[18:21]
	v_mfma_f32_16x16x32_bf16 v[62:65], v[144:147], v[176:179], v[62:65]
	v_mfma_f32_16x16x32_bf16 v[58:61], v[152:155], v[176:179], v[58:61]
	v_mfma_f32_16x16x32_bf16 v[54:57], v[144:147], v[184:187], v[54:57]
	v_mfma_f32_16x16x32_bf16 v[50:53], v[152:155], v[184:187], v[50:53]
	v_mfma_f32_16x16x32_bf16 v[42:45], v[144:147], v[204:207], v[42:45]
	v_mfma_f32_16x16x32_bf16 v[34:37], v[152:155], v[204:207], v[34:37]
	v_mfma_f32_16x16x32_bf16 v[22:25], v[144:147], v[212:215], v[22:25]
	v_mfma_f32_16x16x32_bf16 v[18:21], v[152:155], v[212:215], v[18:21]
	s_setprio 0
	s_setprio 1
	v_mfma_f32_16x16x32_bf16 v[46:49], v[156:159], v[172:175], v[46:49]
	v_mfma_f32_16x16x32_bf16 v[38:41], v[164:167], v[172:175], v[38:41]
	v_mfma_f32_16x16x32_bf16 v[30:33], v[156:159], v[180:183], v[30:33]
	v_mfma_f32_16x16x32_bf16 v[26:29], v[164:167], v[180:183], v[26:29]
	v_mfma_f32_16x16x32_bf16 v[14:17], v[156:159], v[188:191], v[14:17]
	v_mfma_f32_16x16x32_bf16 v[10:13], v[164:167], v[188:191], v[10:13]
	v_mfma_f32_16x16x32_bf16 v[6:9], v[156:159], v[208:211], v[6:9]
	v_mfma_f32_16x16x32_bf16 v[2:5], v[164:167], v[208:211], v[2:5]
	v_mfma_f32_16x16x32_bf16 v[46:49], v[160:163], v[176:179], v[46:49]
	v_mfma_f32_16x16x32_bf16 v[38:41], v[168:171], v[176:179], v[38:41]
	v_mfma_f32_16x16x32_bf16 v[30:33], v[160:163], v[184:187], v[30:33]
	v_mfma_f32_16x16x32_bf16 v[26:29], v[168:171], v[184:187], v[26:29]
	v_mfma_f32_16x16x32_bf16 v[14:17], v[160:163], v[204:207], v[14:17]
	v_mfma_f32_16x16x32_bf16 v[10:13], v[168:171], v[204:207], v[10:13]
	v_mfma_f32_16x16x32_bf16 v[6:9], v[160:163], v[212:215], v[6:9]
	v_mfma_f32_16x16x32_bf16 v[2:5], v[168:171], v[212:215], v[2:5]
	s_setprio 0
	s_barrier
	s_add_i32 s50, 0, 0x18000
	v_add_u32_e32 v139, s50, v136
	s_add_i32 s51, 0, 0x1c000
	ds_read_b128 v[140:143], v139
	ds_read_b128 v[144:147], v139 offset:1024
	ds_read_b128 v[148:151], v139 offset:2048
	ds_read_b128 v[152:155], v139 offset:3072
	v_add_u32_e32 v139, s51, v136
	ds_read_b128 v[156:159], v139
	ds_read_b128 v[160:163], v139 offset:1024
	ds_read_b128 v[164:167], v139 offset:2048
	ds_read_b128 v[168:171], v139 offset:3072
	s_add_u32 s30, s30, 0x40000
	s_addc_u32 s31, s31, 0
	s_mov_b32 m0, s38
	v_lshl_add_u64 v[218:219], s[30:31], 0, v[194:195]
	ds_read_b128 v[172:175], v138 offset:32768
	ds_read_b128 v[176:179], v138 offset:33792
	ds_read_b128 v[180:183], v138 offset:34816
	ds_read_b128 v[184:187], v138 offset:35840
	ds_read_b128 v[188:191], v138 offset:36864
	ds_read_b128 v[204:207], v138 offset:37888
	ds_read_b128 v[208:211], v138 offset:38912
	ds_read_b128 v[212:215], v138 offset:39936
	global_load_lds_dwordx4 v[218:219], off
	s_mov_b32 m0, s40
	v_lshl_add_u64 v[218:219], s[30:31], 0, v[130:131]
	global_load_lds_dwordx4 v[218:219], off
	s_waitcnt vmcnt(8)
	s_waitcnt lgkmcnt(0)
	s_barrier
	s_setprio 1
	s_waitcnt lgkmcnt(0)
	v_mfma_f32_16x16x32_bf16 v[126:129], v[140:143], v[172:175], v[126:129]
	v_mfma_f32_16x16x32_bf16 v[122:125], v[148:151], v[172:175], v[122:125]
	v_mfma_f32_16x16x32_bf16 v[118:121], v[140:143], v[180:183], v[118:121]
	v_mfma_f32_16x16x32_bf16 v[114:117], v[148:151], v[180:183], v[114:117]
	v_mfma_f32_16x16x32_bf16 v[106:109], v[140:143], v[188:191], v[106:109]
	v_mfma_f32_16x16x32_bf16 v[98:101], v[148:151], v[188:191], v[98:101]
	v_mfma_f32_16x16x32_bf16 v[90:93], v[140:143], v[208:211], v[90:93]
	v_mfma_f32_16x16x32_bf16 v[82:85], v[148:151], v[208:211], v[82:85]
	v_mfma_f32_16x16x32_bf16 v[126:129], v[144:147], v[176:179], v[126:129]
	v_mfma_f32_16x16x32_bf16 v[122:125], v[152:155], v[176:179], v[122:125]
	v_mfma_f32_16x16x32_bf16 v[118:121], v[144:147], v[184:187], v[118:121]
	v_mfma_f32_16x16x32_bf16 v[114:117], v[152:155], v[184:187], v[114:117]
	v_mfma_f32_16x16x32_bf16 v[106:109], v[144:147], v[204:207], v[106:109]
	v_mfma_f32_16x16x32_bf16 v[98:101], v[152:155], v[204:207], v[98:101]
	v_mfma_f32_16x16x32_bf16 v[90:93], v[144:147], v[212:215], v[90:93]
	v_mfma_f32_16x16x32_bf16 v[82:85], v[152:155], v[212:215], v[82:85]
	s_setprio 0
	s_setprio 1
	v_mfma_f32_16x16x32_bf16 v[110:113], v[156:159], v[172:175], v[110:113]
	v_mfma_f32_16x16x32_bf16 v[102:105], v[164:167], v[172:175], v[102:105]
	v_mfma_f32_16x16x32_bf16 v[94:97], v[156:159], v[180:183], v[94:97]
	v_mfma_f32_16x16x32_bf16 v[86:89], v[164:167], v[180:183], v[86:89]
	v_mfma_f32_16x16x32_bf16 v[78:81], v[156:159], v[188:191], v[78:81]
	v_mfma_f32_16x16x32_bf16 v[74:77], v[164:167], v[188:191], v[74:77]
	v_mfma_f32_16x16x32_bf16 v[70:73], v[156:159], v[208:211], v[70:73]
	v_mfma_f32_16x16x32_bf16 v[66:69], v[164:167], v[208:211], v[66:69]
	v_mfma_f32_16x16x32_bf16 v[110:113], v[160:163], v[176:179], v[110:113]
	v_mfma_f32_16x16x32_bf16 v[102:105], v[168:171], v[176:179], v[102:105]
	v_mfma_f32_16x16x32_bf16 v[94:97], v[160:163], v[184:187], v[94:97]
	v_mfma_f32_16x16x32_bf16 v[86:89], v[168:171], v[184:187], v[86:89]
	v_mfma_f32_16x16x32_bf16 v[78:81], v[160:163], v[204:207], v[78:81]
	v_mfma_f32_16x16x32_bf16 v[74:77], v[168:171], v[204:207], v[74:77]
	v_mfma_f32_16x16x32_bf16 v[70:73], v[160:163], v[212:215], v[70:73]
	v_mfma_f32_16x16x32_bf16 v[66:69], v[168:171], v[212:215], v[66:69]
	s_setprio 0
	s_barrier
; #define PG8_STAGE_B(bufoff, gbase) do { _Pragma("unroll") for (int _i = 0; _i < 2; ++_i) \
;         __builtin_amdgcn_global_load_lds((const unsigned*)((const char*)(gbase) + voffB[_i]), (LAS unsigned*)(lds + (bufoff) + ldsw + _i * 8192), 16, 0, 0); } while (0)
; #define PG8_LDA(dst, b, h) do { _Pragma("unroll") for (int m = 0; m < 4; ++m) _Pragma("unroll") for (int k = 0; k < 2; ++k) dst[m][k] = *(const LAS bf16x8*)(lds + PG8_SA(b, h) + aoff + m * 2048 + k * 1024); } while (0)
; #define PG8_MMA(ai, bj, At, Bt) do { __builtin_amdgcn_s_setprio(1); _Pragma("unroll") for (int m = 0; m < 4; ++m) _Pragma("unroll") for (int n = 0; n < 2; ++n) _Pragma("unroll") for (int k = 0; k < 2; ++k) \
;         acc[ai][bj][m][n] = __builtin_amdgcn_mfma_f32_16x16x32_bf16(Bt[n][k], At[m][k], acc[ai][bj][m][n], 0, 0, 0); __builtin_amdgcn_s_setprio(0); } while (0)
; #define PG8_WAIT_V(n) asm volatile("s_waitcnt vmcnt(" #n ")" ::: "memory")
; #define PG8_WAIT_L(n) asm volatile("s_waitcnt lgkmcnt(" #n ")" ::: "memory")
; #define PG8_BAR __builtin_amdgcn_s_barrier()
; #define PG8_SCHED __builtin_amdgcn_sched_barrier(0)
; template <class Epi, class Sched, bool GATHER = false>
; __device__ __forceinline__ void gemm_phase(LAS unsigned char* lds, const Gemm g, const Sched& S, const Epi& E) {
;     ...
;             PG8_LDA(At, 1, 1); PG8_STAGE_B(PG8_SB(1, 0), b3); PG8_STAGE_B(PG8_SB(1, 1), b3 + hstepB); PG8_STAGE_A(PG8_SA(1, 0), a3, vo2, 0);
;             PG8_WAIT_V(8); PG8_WAIT_L(0); PG8_BAR; PG8_MMA(1, 0, At, B0); PG8_MMA(1, 1, At, B1); PG8_BAR; PG8_SCHED;
;         }
	s_add_i32 s30, s50, s35
	v_lshl_add_u64 v[192:193], v[192:193], 0, s[66:67]
	s_mov_b32 m0, s30
	ds_read_b128 v[172:175], v138 offset:49152
	ds_read_b128 v[176:179], v138 offset:50176
	ds_read_b128 v[180:183], v138 offset:51200
	ds_read_b128 v[184:187], v138 offset:52224
	ds_read_b128 v[188:191], v138 offset:53248
	ds_read_b128 v[204:207], v138 offset:54272
	ds_read_b128 v[208:211], v138 offset:55296
	ds_read_b128 v[212:215], v138 offset:56320
	global_load_lds_dwordx4 v[192:193], off
	s_add_i32 m0, s30, 0x2000
	s_add_u32 s14, s14, 0x40080
	v_lshl_add_u64 v[192:193], v[198:199], 0, s[66:67]
	s_addc_u32 s15, s15, 0
	s_add_i32 s30, s51, s35
	global_load_lds_dwordx4 v[192:193], off
	s_mov_b32 m0, s30
	v_lshl_add_u64 v[192:193], s[14:15], 0, v[194:195]
	global_load_lds_dwordx4 v[192:193], off
	s_add_i32 m0, s30, 0x2000
	v_lshl_add_u64 v[192:193], s[14:15], 0, v[130:131]
	global_load_lds_dwordx4 v[192:193], off
	s_mov_b32 m0, s16
	v_lshl_add_u64 v[192:193], v[200:201], 0, s[66:67]
	global_load_lds_dwordx4 v[192:193], off
	s_mov_b32 m0, s17
	v_lshl_add_u64 v[192:193], v[216:217], 0, s[66:67]
	global_load_lds_dwordx4 v[192:193], off
	s_waitcnt vmcnt(8)
	s_waitcnt lgkmcnt(0)
	s_barrier
	s_setprio 1
	s_waitcnt lgkmcnt(0)
	v_mfma_f32_16x16x32_bf16 v[62:65], v[140:143], v[172:175], v[62:65]
	v_mfma_f32_16x16x32_bf16 v[58:61], v[148:151], v[172:175], v[58:61]
	v_mfma_f32_16x16x32_bf16 v[54:57], v[140:143], v[180:183], v[54:57]
	v_mfma_f32_16x16x32_bf16 v[50:53], v[148:151], v[180:183], v[50:53]
	v_mfma_f32_16x16x32_bf16 v[42:45], v[140:143], v[188:191], v[42:45]
	v_mfma_f32_16x16x32_bf16 v[34:37], v[148:151], v[188:191], v[34:37]
	v_mfma_f32_16x16x32_bf16 v[22:25], v[140:143], v[208:211], v[22:25]
	v_mfma_f32_16x16x32_bf16 v[18:21], v[148:151], v[208:211], v[18:21]
	v_mfma_f32_16x16x32_bf16 v[62:65], v[144:147], v[176:179], v[62:65]
	v_mfma_f32_16x16x32_bf16 v[58:61], v[152:155], v[176:179], v[58:61]
	v_mfma_f32_16x16x32_bf16 v[54:57], v[144:147], v[184:187], v[54:57]
	v_mfma_f32_16x16x32_bf16 v[50:53], v[152:155], v[184:187], v[50:53]
	v_mfma_f32_16x16x32_bf16 v[42:45], v[144:147], v[204:207], v[42:45]
	v_mfma_f32_16x16x32_bf16 v[34:37], v[152:155], v[204:207], v[34:37]
	v_mfma_f32_16x16x32_bf16 v[22:25], v[144:147], v[212:215], v[22:25]
	v_mfma_f32_16x16x32_bf16 v[18:21], v[152:155], v[212:215], v[18:21]
	s_setprio 0
	s_setprio 1
	v_mfma_f32_16x16x32_bf16 v[46:49], v[156:159], v[172:175], v[46:49]
	v_mfma_f32_16x16x32_bf16 v[38:41], v[164:167], v[172:175], v[38:41]
	v_mfma_f32_16x16x32_bf16 v[30:33], v[156:159], v[180:183], v[30:33]
	v_mfma_f32_16x16x32_bf16 v[26:29], v[164:167], v[180:183], v[26:29]
	v_mfma_f32_16x16x32_bf16 v[14:17], v[156:159], v[188:191], v[14:17]
	v_mfma_f32_16x16x32_bf16 v[10:13], v[164:167], v[188:191], v[10:13]
	v_mfma_f32_16x16x32_bf16 v[6:9], v[156:159], v[208:211], v[6:9]
	v_mfma_f32_16x16x32_bf16 v[2:5], v[164:167], v[208:211], v[2:5]
	v_mfma_f32_16x16x32_bf16 v[46:49], v[160:163], v[176:179], v[46:49]
	v_mfma_f32_16x16x32_bf16 v[38:41], v[168:171], v[176:179], v[38:41]
	v_mfma_f32_16x16x32_bf16 v[30:33], v[160:163], v[184:187], v[30:33]
	v_mfma_f32_16x16x32_bf16 v[26:29], v[168:171], v[184:187], v[26:29]
	v_mfma_f32_16x16x32_bf16 v[14:17], v[160:163], v[204:207], v[14:17]
	v_mfma_f32_16x16x32_bf16 v[10:13], v[168:171], v[204:207], v[10:13]
	v_mfma_f32_16x16x32_bf16 v[6:9], v[160:163], v[212:215], v[6:9]
	v_mfma_f32_16x16x32_bf16 v[2:5], v[168:171], v[212:215], v[2:5]
	s_setprio 0
	s_barrier
	s_add_i32 s49, s49, 2
	s_add_u32 s28, s28, 0x100
	s_addc_u32 s29, s29, 0
	s_add_u32 s47, s47, 0x100
	s_addc_u32 s48, s48, 0
	s_cmp_gt_u32 s49, 13
	s_cbranch_scc0 .LBB0_325
	s_and_b64 vcc, exec, s[8:9]
	s_cbranch_vccz .LBB0_328
	s_barrier

; #define PG8_STAGE_B(bufoff, gbase) do { _Pragma("unroll") for (int _i = 0; _i < 2; ++_i) \
;         __builtin_amdgcn_global_load_lds((const unsigned*)((const char*)(gbase) + voffB[_i]), (LAS unsigned*)(lds + (bufoff) + ldsw + _i * 8192), 16, 0, 0); } while (0)
; #define PG8_LDA(dst, b, h) do { _Pragma("unroll") for (int m = 0; m < 4; ++m) _Pragma("unroll") for (int k = 0; k < 2; ++k) dst[m][k] = *(const LAS bf16x8*)(lds + PG8_SA(b, h) + aoff + m * 2048 + k * 1024); } while (0)
; #define PG8_LDB(dst, b, h) do { _Pragma("unroll") for (int n = 0; n < 2; ++n) _Pragma("unroll") for (int k = 0; k < 2; ++k) dst[n][k] = *(const LAS bf16x8*)(lds + PG8_SB(b, h) + boff + n * 2048 + k * 1024); } while (0)
; #define PG8_MMA(ai, bj, At, Bt) do { __builtin_amdgcn_s_setprio(1); _Pragma("unroll") for (int m = 0; m < 4; ++m) _Pragma("unroll") for (int n = 0; n < 2; ++n) _Pragma("unroll") for (int k = 0; k < 2; ++k) \
;         acc[ai][bj][m][n] = __builtin_amdgcn_mfma_f32_16x16x32_bf16(Bt[n][k], At[m][k], acc[ai][bj][m][n], 0, 0, 0); __builtin_amdgcn_s_setprio(0); } while (0)
; #define PG8_WAIT_V(n) asm volatile("s_waitcnt vmcnt(" #n ")" ::: "memory")
; #define PG8_WAIT_L(n) asm volatile("s_waitcnt lgkmcnt(" #n ")" ::: "memory")
; template <class Epi, class Sched, bool GATHER = false>
; __device__ __forceinline__ void gemm_phase(LAS unsigned char* lds, const Gemm g, const Sched& S, const Epi& E) {
;     ...
;         for (int t = 0; t < nt; t += 2) {
;             const bool last = (t == nt - 2);
;             const char* a1 = cA + (size_t)(t + 1) * kstep;
;             const char* a2 = last ? nA : cA + (size_t)(t + 2) * kstep; const char* b2 = last ? nB : cB + (size_t)(t + 2) * kstep;
;             const char* a3 = a2 + kstep; const char* b3 = b2 + kstep;
;             unsigned vo2[2][2];
;             if constexpr (GATHER) {
; #pragma unroll
;             for (int _h = 0; _h < 2; ++_h)
; #pragma unroll
;                 for (int _i = 0; _i < 2; ++_i) vo2[_h][_i] = last ? voN[_h][_i] : voC[_h][_i]; }
;             PG8_LDB(B0, 0, 0); PG8_LDB(B1, 0, 1); PG8_SCHED; PG8_LDA(At, 0, 0); PG8_STAGE_A(PG8_SA(1, 1), a1, voC, 1);
;             PG8_WAIT_V(8); PG8_WAIT_L(0); PG8_BAR; PG8_MMA(0, 0, At, B0); PG8_MMA(0, 1, At, B1); PG8_BAR; PG8_SCHED;
;             PG8_LDA(At, 0, 1); PG8_STAGE_B(PG8_SB(0, 0), b2); PG8_STAGE_B(PG8_SB(0, 1), b2 + hstepB); PG8_STAGE_A(PG8_SA(0, 0), a2, vo2, 0);
.LBB0_479:
	s_add_u32 s54, s36, s14
	s_addc_u32 s55, s37, 0
	s_add_u32 s15, s54, 0x100
	s_addc_u32 s58, s55, 0
	s_and_b64 s[48:49], s[30:31], exec
	s_cselect_b32 vcc_hi, s45, s58
	s_cselect_b32 vcc_lo, s70, s15
	s_add_u32 s14, s28, s14
	s_addc_u32 s15, s29, 0
	s_add_u32 s48, s14, 0x100
	s_addc_u32 s49, s15, 0
	s_add_i32 s63, 0, 0x10000
	s_and_b64 s[14:15], s[30:31], exec
	s_cselect_b32 s15, s41, s49
	s_cselect_b32 s14, s71, s48
	s_add_i32 s31, 0, 0x14000
	s_add_u32 s76, s54, 0x20080
	s_addc_u32 s77, s55, 0
	s_add_i32 s55, s63, s42
	s_add_i32 m0, s74, 0xc000
	s_add_i32 s11, s74, 0xe000
	s_add_i32 s62, s55, 0x2000
	s_add_u32 s58, s14, 0x10000
	v_add_u32_e32 v152, s63, v137
	v_add_u32_e32 v168, s31, v137
	s_addc_u32 s59, s15, 0
	s_add_i32 s65, s31, s42
	ds_read_b128 v[140:143], v152
	ds_read_b128 v[144:147], v152 offset:1024
	ds_read_b128 v[148:151], v152 offset:2048
	ds_read_b128 v[152:155], v152 offset:3072
	ds_read_b128 v[156:159], v168
	ds_read_b128 v[160:163], v168 offset:1024
	ds_read_b128 v[164:167], v168 offset:2048
	ds_read_b128 v[168:171], v168 offset:3072
	s_add_i32 s64, s65, 0x2000
	s_add_i32 s73, 0, 0x18000
	s_add_i32 s83, 0, 0x1c000
	s_add_u32 s48, vcc_lo, 0x20000
	s_addc_u32 s49, vcc_hi, 0
	s_add_i32 s72, s73, s42
	s_add_i32 s54, s72, 0x2000
	s_add_u32 s30, s14, 0x10080
	s_addc_u32 s31, s15, 0
	s_add_i32 s63, s83, s42
	s_add_i32 s78, s63, 0x2000
	v_lshl_add_u64 v[192:193], s[76:77], 0, v[132:133]
	ds_read_b128 v[172:175], v139
	ds_read_b128 v[176:179], v139 offset:1024
	ds_read_b128 v[180:183], v139 offset:2048
	ds_read_b128 v[184:187], v139 offset:3072
	ds_read_b128 v[188:191], v139 offset:4096
	ds_read_b128 v[204:207], v139 offset:5120
	ds_read_b128 v[208:211], v139 offset:6144
	ds_read_b128 v[212:215], v139 offset:7168
	global_load_lds_dwordx4 v[192:193], off
	s_mov_b32 m0, s11
	v_lshl_add_u64 v[192:193], s[76:77], 0, v[130:131]
	global_load_lds_dwordx4 v[192:193], off
	s_waitcnt vmcnt(8)
	s_waitcnt lgkmcnt(0)
	s_barrier
	s_setprio 1
	s_waitcnt lgkmcnt(0)
	v_mfma_f32_16x16x32_bf16 v[126:129], v[140:143], v[172:175], v[126:129]
	v_mfma_f32_16x16x32_bf16 v[122:125], v[148:151], v[172:175], v[122:125]
	v_mfma_f32_16x16x32_bf16 v[118:121], v[140:143], v[180:183], v[118:121]
	v_mfma_f32_16x16x32_bf16 v[114:117], v[148:151], v[180:183], v[114:117]
	v_mfma_f32_16x16x32_bf16 v[102:105], v[140:143], v[188:191], v[102:105]
	v_mfma_f32_16x16x32_bf16 v[98:101], v[148:151], v[188:191], v[98:101]
	v_mfma_f32_16x16x32_bf16 v[86:89], v[140:143], v[208:211], v[86:89]
	v_mfma_f32_16x16x32_bf16 v[82:85], v[148:151], v[208:211], v[82:85]
	v_mfma_f32_16x16x32_bf16 v[126:129], v[144:147], v[176:179], v[126:129]
	v_mfma_f32_16x16x32_bf16 v[122:125], v[152:155], v[176:179], v[122:125]
	v_mfma_f32_16x16x32_bf16 v[118:121], v[144:147], v[184:187], v[118:121]
	v_mfma_f32_16x16x32_bf16 v[114:117], v[152:155], v[184:187], v[114:117]
	v_mfma_f32_16x16x32_bf16 v[102:105], v[144:147], v[204:207], v[102:105]
	v_mfma_f32_16x16x32_bf16 v[98:101], v[152:155], v[204:207], v[98:101]
	v_mfma_f32_16x16x32_bf16 v[86:89], v[144:147], v[212:215], v[86:89]
	v_mfma_f32_16x16x32_bf16 v[82:85], v[152:155], v[212:215], v[82:85]
	s_setprio 0
	s_setprio 1
	v_mfma_f32_16x16x32_bf16 v[110:113], v[156:159], v[172:175], v[110:113]
	v_mfma_f32_16x16x32_bf16 v[106:109], v[164:167], v[172:175], v[106:109]
	v_mfma_f32_16x16x32_bf16 v[94:97], v[156:159], v[180:183], v[94:97]
	v_mfma_f32_16x16x32_bf16 v[90:93], v[164:167], v[180:183], v[90:93]
	v_mfma_f32_16x16x32_bf16 v[78:81], v[156:159], v[188:191], v[78:81]
	v_mfma_f32_16x16x32_bf16 v[74:77], v[164:167], v[188:191], v[74:77]
	v_mfma_f32_16x16x32_bf16 v[70:73], v[156:159], v[208:211], v[70:73]
	v_mfma_f32_16x16x32_bf16 v[66:69], v[164:167], v[208:211], v[66:69]
	v_mfma_f32_16x16x32_bf16 v[110:113], v[160:163], v[176:179], v[110:113]
	v_mfma_f32_16x16x32_bf16 v[106:109], v[168:171], v[176:179], v[106:109]
	v_mfma_f32_16x16x32_bf16 v[94:97], v[160:163], v[184:187], v[94:97]
	v_mfma_f32_16x16x32_bf16 v[90:93], v[168:171], v[184:187], v[90:93]
	v_mfma_f32_16x16x32_bf16 v[78:81], v[160:163], v[204:207], v[78:81]
	v_mfma_f32_16x16x32_bf16 v[74:77], v[168:171], v[204:207], v[74:77]
	v_mfma_f32_16x16x32_bf16 v[70:73], v[160:163], v[212:215], v[70:73]
	v_mfma_f32_16x16x32_bf16 v[66:69], v[168:171], v[212:215], v[66:69]
	s_setprio 0
	s_barrier
	s_mov_b32 m0, s55
	v_lshl_add_u64 v[192:193], s[14:15], 0, v[194:195]
	ds_read_b128 v[172:175], v139 offset:16384
	ds_read_b128 v[176:179], v139 offset:17408
	ds_read_b128 v[180:183], v139 offset:18432
	ds_read_b128 v[184:187], v139 offset:19456
	ds_read_b128 v[188:191], v139 offset:20480
	ds_read_b128 v[204:207], v139 offset:21504
	ds_read_b128 v[208:211], v139 offset:22528
	ds_read_b128 v[212:215], v139 offset:23552
	global_load_lds_dwordx4 v[192:193], off
	v_lshl_add_u64 v[198:199], s[14:15], 0, v[134:135]
	s_mov_b32 m0, s62
	v_lshl_add_u64 v[200:201], s[58:59], 0, v[194:195]
	global_load_lds_dwordx4 v[198:199], off
	s_mov_b32 m0, s65
	v_lshl_add_u64 v[216:217], vcc, 0, v[130:131]
	global_load_lds_dwordx4 v[200:201], off
	s_mov_b32 m0, s64
	v_lshl_add_u64 v[200:201], s[58:59], 0, v[134:135]
	global_load_lds_dwordx4 v[200:201], off
	s_mov_b32 m0, s74
	v_lshl_add_u64 v[200:201], vcc, 0, v[132:133]
	global_load_lds_dwordx4 v[200:201], off
	s_mov_b32 m0, s84
	s_nop 0
	global_load_lds_dwordx4 v[216:217], off
	s_waitcnt vmcnt(8)
	s_waitcnt lgkmcnt(0)
	s_barrier
; #define PG8_LDA(dst, b, h) do { _Pragma("unroll") for (int m = 0; m < 4; ++m) _Pragma("unroll") for (int k = 0; k < 2; ++k) dst[m][k] = *(const LAS bf16x8*)(lds + PG8_SA(b, h) + aoff + m * 2048 + k * 1024); } while (0)
; #define PG8_LDB(dst, b, h) do { _Pragma("unroll") for (int n = 0; n < 2; ++n) _Pragma("unroll") for (int k = 0; k < 2; ++k) dst[n][k] = *(const LAS bf16x8*)(lds + PG8_SB(b, h) + boff + n * 2048 + k * 1024); } while (0)
; #define PG8_MMA(ai, bj, At, Bt) do { __builtin_amdgcn_s_setprio(1); _Pragma("unroll") for (int m = 0; m < 4; ++m) _Pragma("unroll") for (int n = 0; n < 2; ++n) _Pragma("unroll") for (int k = 0; k < 2; ++k) \
;         acc[ai][bj][m][n] = __builtin_amdgcn_mfma_f32_16x16x32_bf16(Bt[n][k], At[m][k], acc[ai][bj][m][n], 0, 0, 0); __builtin_amdgcn_s_setprio(0); } while (0)
; #define PG8_WAIT_V(n) asm volatile("s_waitcnt vmcnt(" #n ")" ::: "memory")
; #define PG8_WAIT_L(n) asm volatile("s_waitcnt lgkmcnt(" #n ")" ::: "memory")
; #define PG8_BAR __builtin_amdgcn_s_barrier()
; #define PG8_SCHED __builtin_amdgcn_sched_barrier(0)
; template <class Epi, class Sched, bool GATHER = false>
; __device__ __forceinline__ void gemm_phase(LAS unsigned char* lds, const Gemm g, const Sched& S, const Epi& E) {
;     ...
;             PG8_WAIT_V(8); PG8_WAIT_L(0); PG8_BAR; PG8_MMA(1, 0, At, B0); PG8_MMA(1, 1, At, B1); PG8_BAR; PG8_SCHED;
;             PG8_LDB(B0, 1, 0); PG8_LDB(B1, 1, 1); PG8_SCHED; PG8_LDA(At, 1, 0); PG8_STAGE_A(PG8_SA(0, 1), a2, vo2, 1);
;             PG8_WAIT_V(8); PG8_WAIT_L(0); PG8_BAR; PG8_MMA(0, 0, At, B0); PG8_MMA(0, 1, At, B1); PG8_BAR; PG8_SCHED;
	s_setprio 1
	s_waitcnt lgkmcnt(0)
	v_mfma_f32_16x16x32_bf16 v[62:65], v[140:143], v[172:175], v[62:65]
	v_mfma_f32_16x16x32_bf16 v[58:61], v[148:151], v[172:175], v[58:61]
	v_mfma_f32_16x16x32_bf16 v[54:57], v[140:143], v[180:183], v[54:57]
	v_mfma_f32_16x16x32_bf16 v[50:53], v[148:151], v[180:183], v[50:53]
	v_mfma_f32_16x16x32_bf16 v[38:41], v[140:143], v[188:191], v[38:41]
	v_mfma_f32_16x16x32_bf16 v[34:37], v[148:151], v[188:191], v[34:37]
	v_mfma_f32_16x16x32_bf16 v[22:25], v[140:143], v[208:211], v[22:25]
	v_mfma_f32_16x16x32_bf16 v[18:21], v[148:151], v[208:211], v[18:21]
	v_mfma_f32_16x16x32_bf16 v[62:65], v[144:147], v[176:179], v[62:65]
	v_mfma_f32_16x16x32_bf16 v[58:61], v[152:155], v[176:179], v[58:61]
	v_mfma_f32_16x16x32_bf16 v[54:57], v[144:147], v[184:187], v[54:57]
	v_mfma_f32_16x16x32_bf16 v[50:53], v[152:155], v[184:187], v[50:53]
	v_mfma_f32_16x16x32_bf16 v[38:41], v[144:147], v[204:207], v[38:41]
	v_mfma_f32_16x16x32_bf16 v[34:37], v[152:155], v[204:207], v[34:37]
	v_mfma_f32_16x16x32_bf16 v[22:25], v[144:147], v[212:215], v[22:25]
	v_mfma_f32_16x16x32_bf16 v[18:21], v[152:155], v[212:215], v[18:21]
	s_setprio 0
	s_setprio 1
	v_mfma_f32_16x16x32_bf16 v[46:49], v[156:159], v[172:175], v[46:49]
	v_mfma_f32_16x16x32_bf16 v[42:45], v[164:167], v[172:175], v[42:45]
	v_mfma_f32_16x16x32_bf16 v[30:33], v[156:159], v[180:183], v[30:33]
	v_mfma_f32_16x16x32_bf16 v[26:29], v[164:167], v[180:183], v[26:29]
	v_mfma_f32_16x16x32_bf16 v[14:17], v[156:159], v[188:191], v[14:17]
	v_mfma_f32_16x16x32_bf16 v[10:13], v[164:167], v[188:191], v[10:13]
	v_mfma_f32_16x16x32_bf16 v[6:9], v[156:159], v[208:211], v[6:9]
	v_mfma_f32_16x16x32_bf16 v[2:5], v[164:167], v[208:211], v[2:5]
	v_mfma_f32_16x16x32_bf16 v[46:49], v[160:163], v[176:179], v[46:49]
	v_mfma_f32_16x16x32_bf16 v[42:45], v[168:171], v[176:179], v[42:45]
	v_mfma_f32_16x16x32_bf16 v[30:33], v[160:163], v[184:187], v[30:33]
	v_mfma_f32_16x16x32_bf16 v[26:29], v[168:171], v[184:187], v[26:29]
	v_mfma_f32_16x16x32_bf16 v[14:17], v[160:163], v[204:207], v[14:17]
	v_mfma_f32_16x16x32_bf16 v[10:13], v[168:171], v[204:207], v[10:13]
	v_mfma_f32_16x16x32_bf16 v[6:9], v[160:163], v[212:215], v[6:9]
	v_mfma_f32_16x16x32_bf16 v[2:5], v[168:171], v[212:215], v[2:5]
	s_setprio 0
	s_barrier
	v_add_u32_e32 v152, s73, v137
	v_add_u32_e32 v168, s83, v137
	ds_read_b128 v[140:143], v152
	ds_read_b128 v[144:147], v152 offset:1024
	ds_read_b128 v[148:151], v152 offset:2048
	ds_read_b128 v[152:155], v152 offset:3072
	ds_read_b128 v[156:159], v168
	ds_read_b128 v[160:163], v168 offset:1024
	ds_read_b128 v[164:167], v168 offset:2048
	ds_read_b128 v[168:171], v168 offset:3072
	s_mov_b32 m0, s85
	v_lshl_add_u64 v[218:219], s[48:49], 0, v[132:133]
	ds_read_b128 v[172:175], v139 offset:32768
	ds_read_b128 v[176:179], v139 offset:33792
	ds_read_b128 v[180:183], v139 offset:34816
	ds_read_b128 v[184:187], v139 offset:35840
	ds_read_b128 v[188:191], v139 offset:36864
	ds_read_b128 v[204:207], v139 offset:37888
	ds_read_b128 v[208:211], v139 offset:38912
	ds_read_b128 v[212:215], v139 offset:39936
	global_load_lds_dwordx4 v[218:219], off
	s_mov_b32 m0, s86
	v_lshl_add_u64 v[218:219], s[48:49], 0, v[130:131]
	global_load_lds_dwordx4 v[218:219], off
	s_waitcnt vmcnt(8)
	s_waitcnt lgkmcnt(0)
	s_barrier
	s_setprio 1
	s_waitcnt lgkmcnt(0)
	v_mfma_f32_16x16x32_bf16 v[126:129], v[140:143], v[172:175], v[126:129]
	v_mfma_f32_16x16x32_bf16 v[122:125], v[148:151], v[172:175], v[122:125]
	v_mfma_f32_16x16x32_bf16 v[118:121], v[140:143], v[180:183], v[118:121]
	v_mfma_f32_16x16x32_bf16 v[114:117], v[148:151], v[180:183], v[114:117]
	v_mfma_f32_16x16x32_bf16 v[102:105], v[140:143], v[188:191], v[102:105]
	v_mfma_f32_16x16x32_bf16 v[98:101], v[148:151], v[188:191], v[98:101]
	v_mfma_f32_16x16x32_bf16 v[86:89], v[140:143], v[208:211], v[86:89]
	v_mfma_f32_16x16x32_bf16 v[82:85], v[148:151], v[208:211], v[82:85]
	v_mfma_f32_16x16x32_bf16 v[126:129], v[144:147], v[176:179], v[126:129]
	v_mfma_f32_16x16x32_bf16 v[122:125], v[152:155], v[176:179], v[122:125]
	v_mfma_f32_16x16x32_bf16 v[118:121], v[144:147], v[184:187], v[118:121]
	v_mfma_f32_16x16x32_bf16 v[114:117], v[152:155], v[184:187], v[114:117]
	v_mfma_f32_16x16x32_bf16 v[102:105], v[144:147], v[204:207], v[102:105]
	v_mfma_f32_16x16x32_bf16 v[98:101], v[152:155], v[204:207], v[98:101]
	v_mfma_f32_16x16x32_bf16 v[86:89], v[144:147], v[212:215], v[86:89]
	v_mfma_f32_16x16x32_bf16 v[82:85], v[152:155], v[212:215], v[82:85]
	s_setprio 0
	s_setprio 1
	v_mfma_f32_16x16x32_bf16 v[110:113], v[156:159], v[172:175], v[110:113]
	v_mfma_f32_16x16x32_bf16 v[106:109], v[164:167], v[172:175], v[106:109]
	v_mfma_f32_16x16x32_bf16 v[94:97], v[156:159], v[180:183], v[94:97]
	v_mfma_f32_16x16x32_bf16 v[90:93], v[164:167], v[180:183], v[90:93]
	v_mfma_f32_16x16x32_bf16 v[78:81], v[156:159], v[188:191], v[78:81]
	v_mfma_f32_16x16x32_bf16 v[74:77], v[164:167], v[188:191], v[74:77]
	v_mfma_f32_16x16x32_bf16 v[70:73], v[156:159], v[208:211], v[70:73]
	v_mfma_f32_16x16x32_bf16 v[66:69], v[164:167], v[208:211], v[66:69]
	v_mfma_f32_16x16x32_bf16 v[110:113], v[160:163], v[176:179], v[110:113]
	v_mfma_f32_16x16x32_bf16 v[106:109], v[168:171], v[176:179], v[106:109]
	v_mfma_f32_16x16x32_bf16 v[94:97], v[160:163], v[184:187], v[94:97]
	v_mfma_f32_16x16x32_bf16 v[90:93], v[168:171], v[184:187], v[90:93]
	v_mfma_f32_16x16x32_bf16 v[78:81], v[160:163], v[204:207], v[78:81]
	v_mfma_f32_16x16x32_bf16 v[74:77], v[168:171], v[204:207], v[74:77]
	v_mfma_f32_16x16x32_bf16 v[70:73], v[160:163], v[212:215], v[70:73]
	v_mfma_f32_16x16x32_bf16 v[66:69], v[168:171], v[212:215], v[66:69]
	s_setprio 0
	s_barrier
; #define PG8_STAGE_B(bufoff, gbase) do { _Pragma("unroll") for (int _i = 0; _i < 2; ++_i) \
;         __builtin_amdgcn_global_load_lds((const unsigned*)((const char*)(gbase) + voffB[_i]), (LAS unsigned*)(lds + (bufoff) + ldsw + _i * 8192), 16, 0, 0); } while (0)
; #define PG8_LDA(dst, b, h) do { _Pragma("unroll") for (int m = 0; m < 4; ++m) _Pragma("unroll") for (int k = 0; k < 2; ++k) dst[m][k] = *(const LAS bf16x8*)(lds + PG8_SA(b, h) + aoff + m * 2048 + k * 1024); } while (0)
; #define PG8_MMA(ai, bj, At, Bt) do { __builtin_amdgcn_s_setprio(1); _Pragma("unroll") for (int m = 0; m < 4; ++m) _Pragma("unroll") for (int n = 0; n < 2; ++n) _Pragma("unroll") for (int k = 0; k < 2; ++k) \
;         acc[ai][bj][m][n] = __builtin_amdgcn_mfma_f32_16x16x32_bf16(Bt[n][k], At[m][k], acc[ai][bj][m][n], 0, 0, 0); __builtin_amdgcn_s_setprio(0); } while (0)
; #define PG8_WAIT_V(n) asm volatile("s_waitcnt vmcnt(" #n ")" ::: "memory")
; #define PG8_WAIT_L(n) asm volatile("s_waitcnt lgkmcnt(" #n ")" ::: "memory")
; #define PG8_BAR __builtin_amdgcn_s_barrier()
; #define PG8_SCHED __builtin_amdgcn_sched_barrier(0)
; template <class Epi, class Sched, bool GATHER = false>
; __device__ __forceinline__ void gemm_phase(LAS unsigned char* lds, const Gemm g, const Sched& S, const Epi& E) {
;     ...
;             PG8_LDA(At, 1, 1); PG8_STAGE_B(PG8_SB(1, 0), b3); PG8_STAGE_B(PG8_SB(1, 1), b3 + hstepB); PG8_STAGE_A(PG8_SA(1, 0), a3, vo2, 0);
;             PG8_WAIT_V(8); PG8_WAIT_L(0); PG8_BAR; PG8_MMA(1, 0, At, B0); PG8_MMA(1, 1, At, B1); PG8_BAR; PG8_SCHED;
;         }
	s_mov_b32 m0, s72
	v_lshl_add_u64 v[192:193], v[192:193], 0, s[66:67]
	ds_read_b128 v[172:175], v139 offset:49152
	ds_read_b128 v[176:179], v139 offset:50176
	ds_read_b128 v[180:183], v139 offset:51200
	ds_read_b128 v[184:187], v139 offset:52224
	ds_read_b128 v[188:191], v139 offset:53248
	ds_read_b128 v[204:207], v139 offset:54272
	ds_read_b128 v[208:211], v139 offset:55296
	ds_read_b128 v[212:215], v139 offset:56320
	global_load_lds_dwordx4 v[192:193], off
	s_mov_b32 m0, s54
	v_lshl_add_u64 v[192:193], v[198:199], 0, s[66:67]
	global_load_lds_dwordx4 v[192:193], off
	s_mov_b32 m0, s63
	v_lshl_add_u64 v[192:193], s[30:31], 0, v[194:195]
	global_load_lds_dwordx4 v[192:193], off
	s_mov_b32 m0, s78
	v_lshl_add_u64 v[192:193], s[30:31], 0, v[134:135]
	global_load_lds_dwordx4 v[192:193], off
	s_mov_b32 m0, s87
	v_lshl_add_u64 v[192:193], v[200:201], 0, s[66:67]
	global_load_lds_dwordx4 v[192:193], off
	s_mov_b32 m0, s88
	v_lshl_add_u64 v[192:193], v[216:217], 0, s[66:67]
	global_load_lds_dwordx4 v[192:193], off
	s_waitcnt vmcnt(8)
	s_waitcnt lgkmcnt(0)
	s_barrier
	s_setprio 1
	s_waitcnt lgkmcnt(0)
	v_mfma_f32_16x16x32_bf16 v[62:65], v[140:143], v[172:175], v[62:65]
	v_mfma_f32_16x16x32_bf16 v[58:61], v[148:151], v[172:175], v[58:61]
	v_mfma_f32_16x16x32_bf16 v[54:57], v[140:143], v[180:183], v[54:57]
	v_mfma_f32_16x16x32_bf16 v[50:53], v[148:151], v[180:183], v[50:53]
	v_mfma_f32_16x16x32_bf16 v[38:41], v[140:143], v[188:191], v[38:41]
	v_mfma_f32_16x16x32_bf16 v[34:37], v[148:151], v[188:191], v[34:37]
	v_mfma_f32_16x16x32_bf16 v[22:25], v[140:143], v[208:211], v[22:25]
	v_mfma_f32_16x16x32_bf16 v[18:21], v[148:151], v[208:211], v[18:21]
	v_mfma_f32_16x16x32_bf16 v[62:65], v[144:147], v[176:179], v[62:65]
	v_mfma_f32_16x16x32_bf16 v[58:61], v[152:155], v[176:179], v[58:61]
	v_mfma_f32_16x16x32_bf16 v[54:57], v[144:147], v[184:187], v[54:57]
	v_mfma_f32_16x16x32_bf16 v[50:53], v[152:155], v[184:187], v[50:53]
	v_mfma_f32_16x16x32_bf16 v[38:41], v[144:147], v[204:207], v[38:41]
	v_mfma_f32_16x16x32_bf16 v[34:37], v[152:155], v[204:207], v[34:37]
	v_mfma_f32_16x16x32_bf16 v[22:25], v[144:147], v[212:215], v[22:25]
	v_mfma_f32_16x16x32_bf16 v[18:21], v[152:155], v[212:215], v[18:21]
	s_setprio 0
	s_setprio 1
	v_mfma_f32_16x16x32_bf16 v[46:49], v[156:159], v[172:175], v[46:49]
	v_mfma_f32_16x16x32_bf16 v[42:45], v[164:167], v[172:175], v[42:45]
	v_mfma_f32_16x16x32_bf16 v[30:33], v[156:159], v[180:183], v[30:33]
	v_mfma_f32_16x16x32_bf16 v[26:29], v[164:167], v[180:183], v[26:29]
	v_mfma_f32_16x16x32_bf16 v[14:17], v[156:159], v[188:191], v[14:17]
	v_mfma_f32_16x16x32_bf16 v[10:13], v[164:167], v[188:191], v[10:13]
	v_mfma_f32_16x16x32_bf16 v[6:9], v[156:159], v[208:211], v[6:9]
	v_mfma_f32_16x16x32_bf16 v[2:5], v[164:167], v[208:211], v[2:5]
	v_mfma_f32_16x16x32_bf16 v[46:49], v[160:163], v[176:179], v[46:49]
	v_mfma_f32_16x16x32_bf16 v[42:45], v[168:171], v[176:179], v[42:45]
	v_mfma_f32_16x16x32_bf16 v[30:33], v[160:163], v[184:187], v[30:33]
	v_mfma_f32_16x16x32_bf16 v[26:29], v[168:171], v[184:187], v[26:29]
	v_mfma_f32_16x16x32_bf16 v[14:17], v[160:163], v[204:207], v[14:17]
	v_mfma_f32_16x16x32_bf16 v[10:13], v[168:171], v[204:207], v[10:13]
	v_mfma_f32_16x16x32_bf16 v[6:9], v[160:163], v[212:215], v[6:9]
	v_mfma_f32_16x16x32_bf16 v[2:5], v[168:171], v[212:215], v[2:5]
	s_setprio 0
	s_barrier
	s_movk_i32 s14, 0x100
	s_andn2_b64 vcc, exec, s[52:53]
	s_mov_b64 s[30:31], -1
	s_mov_b64 s[52:53], 0
	s_cbranch_vccz .LBB0_479
	s_and_b64 vcc, exec, s[22:23]
	s_cbranch_vccz .LBB0_482
	s_barrier

; #define PG8_STAGE_B(bufoff, gbase) do { _Pragma("unroll") for (int _i = 0; _i < 2; ++_i) \
;         __builtin_amdgcn_global_load_lds((const unsigned*)((const char*)(gbase) + voffB[_i]), (LAS unsigned*)(lds + (bufoff) + ldsw + _i * 8192), 16, 0, 0); } while (0)
; #define PG8_LDA(dst, b, h) do { _Pragma("unroll") for (int m = 0; m < 4; ++m) _Pragma("unroll") for (int k = 0; k < 2; ++k) dst[m][k] = *(const LAS bf16x8*)(lds + PG8_SA(b, h) + aoff + m * 2048 + k * 1024); } while (0)
; #define PG8_LDB(dst, b, h) do { _Pragma("unroll") for (int n = 0; n < 2; ++n) _Pragma("unroll") for (int k = 0; k < 2; ++k) dst[n][k] = *(const LAS bf16x8*)(lds + PG8_SB(b, h) + boff + n * 2048 + k * 1024); } while (0)
; #define PG8_MMA(ai, bj, At, Bt) do { __builtin_amdgcn_s_setprio(1); _Pragma("unroll") for (int m = 0; m < 4; ++m) _Pragma("unroll") for (int n = 0; n < 2; ++n) _Pragma("unroll") for (int k = 0; k < 2; ++k) \
;         acc[ai][bj][m][n] = __builtin_amdgcn_mfma_f32_16x16x32_bf16(Bt[n][k], At[m][k], acc[ai][bj][m][n], 0, 0, 0); __builtin_amdgcn_s_setprio(0); } while (0)
; #define PG8_WAIT_V(n) asm volatile("s_waitcnt vmcnt(" #n ")" ::: "memory")
; #define PG8_WAIT_L(n) asm volatile("s_waitcnt lgkmcnt(" #n ")" ::: "memory")
; #define PG8_BAR __builtin_amdgcn_s_barrier()
; #define PG8_SCHED __builtin_amdgcn_sched_barrier(0)
; template <class Epi, class Sched, bool GATHER = false>
; __device__ __forceinline__ void gemm_phase(LAS unsigned char* lds, const Gemm g, const Sched& S, const Epi& E) {
;     ...
;             PG8_LDB(B0, 0, 0); PG8_LDB(B1, 0, 1); PG8_SCHED; PG8_LDA(At, 0, 0); PG8_STAGE_A(PG8_SA(1, 1), a1, voC, 1);
;             PG8_WAIT_V(8); PG8_WAIT_L(0); PG8_BAR; PG8_MMA(0, 0, At, B0); PG8_MMA(0, 1, At, B1); PG8_BAR; PG8_SCHED;
;             PG8_LDA(At, 0, 1); PG8_STAGE_B(PG8_SB(0, 0), b2); PG8_STAGE_B(PG8_SB(0, 1), b2 + hstepB); PG8_STAGE_A(PG8_SA(0, 0), a2, vo2, 0);
;             PG8_WAIT_V(8); PG8_WAIT_L(0); PG8_BAR; PG8_MMA(1, 0, At, B0); PG8_MMA(1, 1, At, B1); PG8_BAR; PG8_SCHED;
.LBB0_496:
	s_add_i32 s71, s14, 2
	s_add_u32 s15, vcc_lo, 0xfffe0080
	s_addc_u32 s50, vcc_hi, -1
	s_add_i32 s54, 0, 0x10000
	s_cmp_eq_u32 s87, s14
	s_cselect_b32 s51, s16, s50
	s_cselect_b32 s50, s41, s15
	s_cselect_b32 s15, s45, s53
	s_cselect_b32 s14, s70, s52
	s_add_i32 s62, 0, 0x14000
	v_add_u32_e32 v156, s54, v141
	v_add_u32_e32 v172, s62, v141
	ds_read_b128 v[144:147], v156
	ds_read_b128 v[148:151], v156 offset:1024
	ds_read_b128 v[152:155], v156 offset:2048
	ds_read_b128 v[156:159], v156 offset:3072
	ds_read_b128 v[160:163], v172
	ds_read_b128 v[164:167], v172 offset:1024
	ds_read_b128 v[168:171], v172 offset:2048
	ds_read_b128 v[172:175], v172 offset:3072
	v_lshl_add_u64 v[192:193], vcc, 0, v[136:137]
	s_add_i32 m0, s47, 0xc000
	ds_read_b128 v[176:179], v143
	ds_read_b128 v[180:183], v143 offset:1024
	ds_read_b128 v[184:187], v143 offset:2048
	ds_read_b128 v[188:191], v143 offset:3072
	ds_read_b128 v[204:207], v143 offset:4096
	ds_read_b128 v[208:211], v143 offset:5120
	ds_read_b128 v[212:215], v143 offset:6144
	ds_read_b128 v[216:219], v143 offset:7168
	global_load_lds_dwordx4 v[192:193], off
	s_add_i32 m0, s47, 0xe000
	v_lshl_add_u64 v[192:193], vcc, 0, v[138:139]
	global_load_lds_dwordx4 v[192:193], off
	s_waitcnt vmcnt(8)
	s_waitcnt lgkmcnt(0)
	s_barrier
	s_setprio 1
	s_waitcnt lgkmcnt(0)
	v_mfma_f32_16x16x32_bf16 v[122:125], v[144:147], v[176:179], v[122:125]
	v_mfma_f32_16x16x32_bf16 v[126:129], v[152:155], v[176:179], v[126:129]
	v_mfma_f32_16x16x32_bf16 v[110:113], v[144:147], v[184:187], v[110:113]
	v_mfma_f32_16x16x32_bf16 v[106:109], v[152:155], v[184:187], v[106:109]
	v_mfma_f32_16x16x32_bf16 v[94:97], v[144:147], v[204:207], v[94:97]
	v_mfma_f32_16x16x32_bf16 v[90:93], v[152:155], v[204:207], v[90:93]
	v_mfma_f32_16x16x32_bf16 v[78:81], v[144:147], v[212:215], v[78:81]
	v_mfma_f32_16x16x32_bf16 v[74:77], v[152:155], v[212:215], v[74:77]
	v_mfma_f32_16x16x32_bf16 v[122:125], v[148:151], v[180:183], v[122:125]
	v_mfma_f32_16x16x32_bf16 v[126:129], v[156:159], v[180:183], v[126:129]
	v_mfma_f32_16x16x32_bf16 v[110:113], v[148:151], v[188:191], v[110:113]
	v_mfma_f32_16x16x32_bf16 v[106:109], v[156:159], v[188:191], v[106:109]
	v_mfma_f32_16x16x32_bf16 v[94:97], v[148:151], v[208:211], v[94:97]
	v_mfma_f32_16x16x32_bf16 v[90:93], v[156:159], v[208:211], v[90:93]
	v_mfma_f32_16x16x32_bf16 v[78:81], v[148:151], v[216:219], v[78:81]
	v_mfma_f32_16x16x32_bf16 v[74:77], v[156:159], v[216:219], v[74:77]
	s_setprio 0
	s_setprio 1
	v_mfma_f32_16x16x32_bf16 v[118:121], v[160:163], v[176:179], v[118:121]
	v_mfma_f32_16x16x32_bf16 v[114:117], v[168:171], v[176:179], v[114:117]
	v_mfma_f32_16x16x32_bf16 v[102:105], v[160:163], v[184:187], v[102:105]
	v_mfma_f32_16x16x32_bf16 v[98:101], v[168:171], v[184:187], v[98:101]
	v_mfma_f32_16x16x32_bf16 v[86:89], v[160:163], v[204:207], v[86:89]
	v_mfma_f32_16x16x32_bf16 v[82:85], v[168:171], v[204:207], v[82:85]
	v_mfma_f32_16x16x32_bf16 v[70:73], v[160:163], v[212:215], v[70:73]
	v_mfma_f32_16x16x32_bf16 v[66:69], v[168:171], v[212:215], v[66:69]
	v_mfma_f32_16x16x32_bf16 v[118:121], v[164:167], v[180:183], v[118:121]
	v_mfma_f32_16x16x32_bf16 v[114:117], v[172:175], v[180:183], v[114:117]
	v_mfma_f32_16x16x32_bf16 v[102:105], v[164:167], v[188:191], v[102:105]
	v_mfma_f32_16x16x32_bf16 v[98:101], v[172:175], v[188:191], v[98:101]
	v_mfma_f32_16x16x32_bf16 v[86:89], v[164:167], v[208:211], v[86:89]
	v_mfma_f32_16x16x32_bf16 v[82:85], v[172:175], v[208:211], v[82:85]
	v_mfma_f32_16x16x32_bf16 v[70:73], v[164:167], v[216:219], v[70:73]
	v_mfma_f32_16x16x32_bf16 v[66:69], v[172:175], v[216:219], v[66:69]
	s_setprio 0
	s_barrier
	s_add_i32 s54, s54, s76
	v_lshl_add_u64 v[192:193], s[14:15], 0, v[194:195]
	s_mov_b32 m0, s54
	ds_read_b128 v[176:179], v143 offset:16384
	ds_read_b128 v[180:183], v143 offset:17408
	ds_read_b128 v[184:187], v143 offset:18432
	ds_read_b128 v[188:191], v143 offset:19456
	ds_read_b128 v[204:207], v143 offset:20480
	ds_read_b128 v[208:211], v143 offset:21504
	ds_read_b128 v[212:215], v143 offset:22528
	ds_read_b128 v[216:219], v143 offset:23552
	global_load_lds_dwordx4 v[192:193], off
	s_add_i32 m0, s54, 0x2000
	s_add_u32 s54, s14, 0x10000
	v_lshl_add_u64 v[198:199], s[14:15], 0, v[134:135]
	s_addc_u32 s55, s15, 0
	s_add_i32 s62, s62, s76
	global_load_lds_dwordx4 v[198:199], off
	v_lshl_add_u64 v[200:201], s[54:55], 0, v[194:195]
	s_mov_b32 m0, s62
	v_lshl_add_u64 v[220:221], s[50:51], 0, v[130:131]
	global_load_lds_dwordx4 v[200:201], off
	s_add_i32 m0, s62, 0x2000
	v_lshl_add_u64 v[200:201], s[54:55], 0, v[134:135]
	global_load_lds_dwordx4 v[200:201], off
	s_mov_b32 m0, s47
	v_lshl_add_u64 v[200:201], s[50:51], 0, v[132:133]
	global_load_lds_dwordx4 v[200:201], off
	s_mov_b32 m0, s80
	s_nop 0
	global_load_lds_dwordx4 v[220:221], off
	s_waitcnt vmcnt(8)
	s_waitcnt lgkmcnt(0)
	s_barrier
; #define PG8_LDA(dst, b, h) do { _Pragma("unroll") for (int m = 0; m < 4; ++m) _Pragma("unroll") for (int k = 0; k < 2; ++k) dst[m][k] = *(const LAS bf16x8*)(lds + PG8_SA(b, h) + aoff + m * 2048 + k * 1024); } while (0)
; #define PG8_LDB(dst, b, h) do { _Pragma("unroll") for (int n = 0; n < 2; ++n) _Pragma("unroll") for (int k = 0; k < 2; ++k) dst[n][k] = *(const LAS bf16x8*)(lds + PG8_SB(b, h) + boff + n * 2048 + k * 1024); } while (0)
; #define PG8_MMA(ai, bj, At, Bt) do { __builtin_amdgcn_s_setprio(1); _Pragma("unroll") for (int m = 0; m < 4; ++m) _Pragma("unroll") for (int n = 0; n < 2; ++n) _Pragma("unroll") for (int k = 0; k < 2; ++k) \
;         acc[ai][bj][m][n] = __builtin_amdgcn_mfma_f32_16x16x32_bf16(Bt[n][k], At[m][k], acc[ai][bj][m][n], 0, 0, 0); __builtin_amdgcn_s_setprio(0); } while (0)
; #define PG8_WAIT_V(n) asm volatile("s_waitcnt vmcnt(" #n ")" ::: "memory")
; #define PG8_WAIT_L(n) asm volatile("s_waitcnt lgkmcnt(" #n ")" ::: "memory")
; #define PG8_BAR __builtin_amdgcn_s_barrier()
; #define PG8_SCHED __builtin_amdgcn_sched_barrier(0)
; template <class Epi, class Sched, bool GATHER = false>
; __device__ __forceinline__ void gemm_phase(LAS unsigned char* lds, const Gemm g, const Sched& S, const Epi& E) {
;     ...
;             PG8_WAIT_V(8); PG8_WAIT_L(0); PG8_BAR; PG8_MMA(1, 0, At, B0); PG8_MMA(1, 1, At, B1); PG8_BAR; PG8_SCHED;
;             PG8_LDB(B0, 1, 0); PG8_LDB(B1, 1, 1); PG8_SCHED; PG8_LDA(At, 1, 0); PG8_STAGE_A(PG8_SA(0, 1), a2, vo2, 1);
;             PG8_WAIT_V(8); PG8_WAIT_L(0); PG8_BAR; PG8_MMA(0, 0, At, B0); PG8_MMA(0, 1, At, B1); PG8_BAR; PG8_SCHED;
	s_setprio 1
	s_waitcnt lgkmcnt(0)
	v_mfma_f32_16x16x32_bf16 v[62:65], v[144:147], v[176:179], v[62:65]
	v_mfma_f32_16x16x32_bf16 v[58:61], v[152:155], v[176:179], v[58:61]
	v_mfma_f32_16x16x32_bf16 v[46:49], v[144:147], v[184:187], v[46:49]
	v_mfma_f32_16x16x32_bf16 v[42:45], v[152:155], v[184:187], v[42:45]
	v_mfma_f32_16x16x32_bf16 v[30:33], v[144:147], v[204:207], v[30:33]
	v_mfma_f32_16x16x32_bf16 v[26:29], v[152:155], v[204:207], v[26:29]
	v_mfma_f32_16x16x32_bf16 v[14:17], v[144:147], v[212:215], v[14:17]
	v_mfma_f32_16x16x32_bf16 v[10:13], v[152:155], v[212:215], v[10:13]
	v_mfma_f32_16x16x32_bf16 v[62:65], v[148:151], v[180:183], v[62:65]
	v_mfma_f32_16x16x32_bf16 v[58:61], v[156:159], v[180:183], v[58:61]
	v_mfma_f32_16x16x32_bf16 v[46:49], v[148:151], v[188:191], v[46:49]
	v_mfma_f32_16x16x32_bf16 v[42:45], v[156:159], v[188:191], v[42:45]
	v_mfma_f32_16x16x32_bf16 v[30:33], v[148:151], v[208:211], v[30:33]
	v_mfma_f32_16x16x32_bf16 v[26:29], v[156:159], v[208:211], v[26:29]
	v_mfma_f32_16x16x32_bf16 v[14:17], v[148:151], v[216:219], v[14:17]
	v_mfma_f32_16x16x32_bf16 v[10:13], v[156:159], v[216:219], v[10:13]
	s_setprio 0
	s_setprio 1
	v_mfma_f32_16x16x32_bf16 v[54:57], v[160:163], v[176:179], v[54:57]
	v_mfma_f32_16x16x32_bf16 v[50:53], v[168:171], v[176:179], v[50:53]
	v_mfma_f32_16x16x32_bf16 v[38:41], v[160:163], v[184:187], v[38:41]
	v_mfma_f32_16x16x32_bf16 v[34:37], v[168:171], v[184:187], v[34:37]
	v_mfma_f32_16x16x32_bf16 v[22:25], v[160:163], v[204:207], v[22:25]
	v_mfma_f32_16x16x32_bf16 v[18:21], v[168:171], v[204:207], v[18:21]
	v_mfma_f32_16x16x32_bf16 v[6:9], v[160:163], v[212:215], v[6:9]
	v_mfma_f32_16x16x32_bf16 v[2:5], v[168:171], v[212:215], v[2:5]
	v_mfma_f32_16x16x32_bf16 v[54:57], v[164:167], v[180:183], v[54:57]
	v_mfma_f32_16x16x32_bf16 v[50:53], v[172:175], v[180:183], v[50:53]
	v_mfma_f32_16x16x32_bf16 v[38:41], v[164:167], v[188:191], v[38:41]
	v_mfma_f32_16x16x32_bf16 v[34:37], v[172:175], v[188:191], v[34:37]
	v_mfma_f32_16x16x32_bf16 v[22:25], v[164:167], v[208:211], v[22:25]
	v_mfma_f32_16x16x32_bf16 v[18:21], v[172:175], v[208:211], v[18:21]
	v_mfma_f32_16x16x32_bf16 v[6:9], v[164:167], v[216:219], v[6:9]
	v_mfma_f32_16x16x32_bf16 v[2:5], v[172:175], v[216:219], v[2:5]
	s_setprio 0
	s_barrier
	s_add_i32 s54, 0, 0x18000
	s_add_i32 s55, 0, 0x1c000
	v_add_u32_e32 v156, s54, v141
	v_add_u32_e32 v172, s55, v141
	ds_read_b128 v[144:147], v156
	ds_read_b128 v[148:151], v156 offset:1024
	ds_read_b128 v[152:155], v156 offset:2048
	ds_read_b128 v[156:159], v156 offset:3072
	ds_read_b128 v[160:163], v172
	ds_read_b128 v[164:167], v172 offset:1024
	ds_read_b128 v[168:171], v172 offset:2048
	ds_read_b128 v[172:175], v172 offset:3072
	s_add_u32 s50, s50, 0x20000
	s_addc_u32 s51, s51, 0
	s_mov_b32 m0, s81
	v_lshl_add_u64 v[222:223], s[50:51], 0, v[132:133]
	ds_read_b128 v[176:179], v143 offset:32768
	ds_read_b128 v[180:183], v143 offset:33792
	ds_read_b128 v[184:187], v143 offset:34816
	ds_read_b128 v[188:191], v143 offset:35840
	ds_read_b128 v[204:207], v143 offset:36864
	ds_read_b128 v[208:211], v143 offset:37888
	ds_read_b128 v[212:215], v143 offset:38912
	ds_read_b128 v[216:219], v143 offset:39936
	global_load_lds_dwordx4 v[222:223], off
	s_mov_b32 m0, s84
	v_lshl_add_u64 v[222:223], s[50:51], 0, v[130:131]
	global_load_lds_dwordx4 v[222:223], off
	s_waitcnt vmcnt(8)
	s_waitcnt lgkmcnt(0)
	s_barrier
	s_setprio 1
	s_waitcnt lgkmcnt(0)
	v_mfma_f32_16x16x32_bf16 v[122:125], v[144:147], v[176:179], v[122:125]
	v_mfma_f32_16x16x32_bf16 v[126:129], v[152:155], v[176:179], v[126:129]
	v_mfma_f32_16x16x32_bf16 v[110:113], v[144:147], v[184:187], v[110:113]
	v_mfma_f32_16x16x32_bf16 v[106:109], v[152:155], v[184:187], v[106:109]
	v_mfma_f32_16x16x32_bf16 v[94:97], v[144:147], v[204:207], v[94:97]
	v_mfma_f32_16x16x32_bf16 v[90:93], v[152:155], v[204:207], v[90:93]
	v_mfma_f32_16x16x32_bf16 v[78:81], v[144:147], v[212:215], v[78:81]
	v_mfma_f32_16x16x32_bf16 v[74:77], v[152:155], v[212:215], v[74:77]
	v_mfma_f32_16x16x32_bf16 v[122:125], v[148:151], v[180:183], v[122:125]
	v_mfma_f32_16x16x32_bf16 v[126:129], v[156:159], v[180:183], v[126:129]
	v_mfma_f32_16x16x32_bf16 v[110:113], v[148:151], v[188:191], v[110:113]
	v_mfma_f32_16x16x32_bf16 v[106:109], v[156:159], v[188:191], v[106:109]
	v_mfma_f32_16x16x32_bf16 v[94:97], v[148:151], v[208:211], v[94:97]
	v_mfma_f32_16x16x32_bf16 v[90:93], v[156:159], v[208:211], v[90:93]
	v_mfma_f32_16x16x32_bf16 v[78:81], v[148:151], v[216:219], v[78:81]
	v_mfma_f32_16x16x32_bf16 v[74:77], v[156:159], v[216:219], v[74:77]
	s_setprio 0
	s_setprio 1
	v_mfma_f32_16x16x32_bf16 v[118:121], v[160:163], v[176:179], v[118:121]
	v_mfma_f32_16x16x32_bf16 v[114:117], v[168:171], v[176:179], v[114:117]
	v_mfma_f32_16x16x32_bf16 v[102:105], v[160:163], v[184:187], v[102:105]
	v_mfma_f32_16x16x32_bf16 v[98:101], v[168:171], v[184:187], v[98:101]
	v_mfma_f32_16x16x32_bf16 v[86:89], v[160:163], v[204:207], v[86:89]
	v_mfma_f32_16x16x32_bf16 v[82:85], v[168:171], v[204:207], v[82:85]
	v_mfma_f32_16x16x32_bf16 v[70:73], v[160:163], v[212:215], v[70:73]
	v_mfma_f32_16x16x32_bf16 v[66:69], v[168:171], v[212:215], v[66:69]
	v_mfma_f32_16x16x32_bf16 v[118:121], v[164:167], v[180:183], v[118:121]
	v_mfma_f32_16x16x32_bf16 v[114:117], v[172:175], v[180:183], v[114:117]
	v_mfma_f32_16x16x32_bf16 v[102:105], v[164:167], v[188:191], v[102:105]
	v_mfma_f32_16x16x32_bf16 v[98:101], v[172:175], v[188:191], v[98:101]
	v_mfma_f32_16x16x32_bf16 v[86:89], v[164:167], v[208:211], v[86:89]
	v_mfma_f32_16x16x32_bf16 v[82:85], v[172:175], v[208:211], v[82:85]
	v_mfma_f32_16x16x32_bf16 v[70:73], v[164:167], v[216:219], v[70:73]
	v_mfma_f32_16x16x32_bf16 v[66:69], v[172:175], v[216:219], v[66:69]
	s_setprio 0
	s_barrier
; #define PG8_STAGE_B(bufoff, gbase) do { _Pragma("unroll") for (int _i = 0; _i < 2; ++_i) \
;         __builtin_amdgcn_global_load_lds((const unsigned*)((const char*)(gbase) + voffB[_i]), (LAS unsigned*)(lds + (bufoff) + ldsw + _i * 8192), 16, 0, 0); } while (0)
; #define PG8_LDA(dst, b, h) do { _Pragma("unroll") for (int m = 0; m < 4; ++m) _Pragma("unroll") for (int k = 0; k < 2; ++k) dst[m][k] = *(const LAS bf16x8*)(lds + PG8_SA(b, h) + aoff + m * 2048 + k * 1024); } while (0)
; #define PG8_MMA(ai, bj, At, Bt) do { __builtin_amdgcn_s_setprio(1); _Pragma("unroll") for (int m = 0; m < 4; ++m) _Pragma("unroll") for (int n = 0; n < 2; ++n) _Pragma("unroll") for (int k = 0; k < 2; ++k) \
;         acc[ai][bj][m][n] = __builtin_amdgcn_mfma_f32_16x16x32_bf16(Bt[n][k], At[m][k], acc[ai][bj][m][n], 0, 0, 0); __builtin_amdgcn_s_setprio(0); } while (0)
; #define PG8_WAIT_V(n) asm volatile("s_waitcnt vmcnt(" #n ")" ::: "memory")
; #define PG8_WAIT_L(n) asm volatile("s_waitcnt lgkmcnt(" #n ")" ::: "memory")
; #define PG8_BAR __builtin_amdgcn_s_barrier()
; #define PG8_SCHED __builtin_amdgcn_sched_barrier(0)
; template <class Epi, class Sched, bool GATHER = false>
; __device__ __forceinline__ void gemm_phase(LAS unsigned char* lds, const Gemm g, const Sched& S, const Epi& E) {
;     ...
;             PG8_LDA(At, 1, 1); PG8_STAGE_B(PG8_SB(1, 0), b3); PG8_STAGE_B(PG8_SB(1, 1), b3 + hstepB); PG8_STAGE_A(PG8_SA(1, 0), a3, vo2, 0);
;             PG8_WAIT_V(8); PG8_WAIT_L(0); PG8_BAR; PG8_MMA(1, 0, At, B0); PG8_MMA(1, 1, At, B1); PG8_BAR; PG8_SCHED;
;         }
	s_add_i32 s50, s54, s76
	v_lshl_add_u64 v[192:193], v[192:193], 0, s[66:67]
	s_mov_b32 m0, s50
	ds_read_b128 v[176:179], v143 offset:49152
	ds_read_b128 v[180:183], v143 offset:50176
	ds_read_b128 v[184:187], v143 offset:51200
	ds_read_b128 v[188:191], v143 offset:52224
	ds_read_b128 v[204:207], v143 offset:53248
	ds_read_b128 v[208:211], v143 offset:54272
	ds_read_b128 v[212:215], v143 offset:55296
	ds_read_b128 v[216:219], v143 offset:56320
	global_load_lds_dwordx4 v[192:193], off
	s_add_i32 m0, s50, 0x2000
	s_add_u32 s14, s14, 0x10080
	v_lshl_add_u64 v[192:193], v[198:199], 0, s[66:67]
	s_addc_u32 s15, s15, 0
	s_add_i32 s50, s55, s76
	global_load_lds_dwordx4 v[192:193], off
	s_mov_b32 m0, s50
	v_lshl_add_u64 v[192:193], s[14:15], 0, v[194:195]
	global_load_lds_dwordx4 v[192:193], off
	s_add_i32 m0, s50, 0x2000
	v_lshl_add_u64 v[192:193], s[14:15], 0, v[134:135]
	global_load_lds_dwordx4 v[192:193], off
	s_mov_b32 m0, s85
	v_lshl_add_u64 v[192:193], v[200:201], 0, s[66:67]
	global_load_lds_dwordx4 v[192:193], off
	s_mov_b32 m0, s86
	v_lshl_add_u64 v[192:193], v[220:221], 0, s[66:67]
	global_load_lds_dwordx4 v[192:193], off
	s_waitcnt vmcnt(8)
	s_waitcnt lgkmcnt(0)
	s_barrier
	s_setprio 1
	s_waitcnt lgkmcnt(0)
	v_mfma_f32_16x16x32_bf16 v[62:65], v[144:147], v[176:179], v[62:65]
	v_mfma_f32_16x16x32_bf16 v[58:61], v[152:155], v[176:179], v[58:61]
	v_mfma_f32_16x16x32_bf16 v[46:49], v[144:147], v[184:187], v[46:49]
	v_mfma_f32_16x16x32_bf16 v[42:45], v[152:155], v[184:187], v[42:45]
	v_mfma_f32_16x16x32_bf16 v[30:33], v[144:147], v[204:207], v[30:33]
	v_mfma_f32_16x16x32_bf16 v[26:29], v[152:155], v[204:207], v[26:29]
	v_mfma_f32_16x16x32_bf16 v[14:17], v[144:147], v[212:215], v[14:17]
	v_mfma_f32_16x16x32_bf16 v[10:13], v[152:155], v[212:215], v[10:13]
	v_mfma_f32_16x16x32_bf16 v[62:65], v[148:151], v[180:183], v[62:65]
	v_mfma_f32_16x16x32_bf16 v[58:61], v[156:159], v[180:183], v[58:61]
	v_mfma_f32_16x16x32_bf16 v[46:49], v[148:151], v[188:191], v[46:49]
	v_mfma_f32_16x16x32_bf16 v[42:45], v[156:159], v[188:191], v[42:45]
	v_mfma_f32_16x16x32_bf16 v[30:33], v[148:151], v[208:211], v[30:33]
	v_mfma_f32_16x16x32_bf16 v[26:29], v[156:159], v[208:211], v[26:29]
	v_mfma_f32_16x16x32_bf16 v[14:17], v[148:151], v[216:219], v[14:17]
	v_mfma_f32_16x16x32_bf16 v[10:13], v[156:159], v[216:219], v[10:13]
	s_setprio 0
	s_setprio 1
	v_mfma_f32_16x16x32_bf16 v[54:57], v[160:163], v[176:179], v[54:57]
	v_mfma_f32_16x16x32_bf16 v[50:53], v[168:171], v[176:179], v[50:53]
	v_mfma_f32_16x16x32_bf16 v[38:41], v[160:163], v[184:187], v[38:41]
	v_mfma_f32_16x16x32_bf16 v[34:37], v[168:171], v[184:187], v[34:37]
	v_mfma_f32_16x16x32_bf16 v[22:25], v[160:163], v[204:207], v[22:25]
	v_mfma_f32_16x16x32_bf16 v[18:21], v[168:171], v[204:207], v[18:21]
	v_mfma_f32_16x16x32_bf16 v[6:9], v[160:163], v[212:215], v[6:9]
	v_mfma_f32_16x16x32_bf16 v[2:5], v[168:171], v[212:215], v[2:5]
	v_mfma_f32_16x16x32_bf16 v[54:57], v[164:167], v[180:183], v[54:57]
	v_mfma_f32_16x16x32_bf16 v[50:53], v[172:175], v[180:183], v[50:53]
	v_mfma_f32_16x16x32_bf16 v[38:41], v[164:167], v[188:191], v[38:41]
	v_mfma_f32_16x16x32_bf16 v[34:37], v[172:175], v[188:191], v[34:37]
	v_mfma_f32_16x16x32_bf16 v[22:25], v[164:167], v[208:211], v[22:25]
	v_mfma_f32_16x16x32_bf16 v[18:21], v[172:175], v[208:211], v[18:21]
	v_mfma_f32_16x16x32_bf16 v[6:9], v[164:167], v[216:219], v[6:9]
	v_mfma_f32_16x16x32_bf16 v[2:5], v[172:175], v[216:219], v[2:5]
	s_setprio 0
	s_barrier
	s_add_u32 vcc_lo, vcc_lo, 0x100
	s_addc_u32 vcc_hi, vcc_hi, 0
	s_add_u32 s52, s52, 0x100
	s_addc_u32 s53, s53, 0
	s_cmp_ge_i32 s71, s25
	s_mov_b32 s14, s71
	s_cbranch_scc0 .LBB0_496
	v_readlane_b32 s0, v255, 29
	v_readlane_b32 s1, v255, 30
	v_readlane_b32 s70, v255, 36

; #define PG8_STAGE_B(bufoff, gbase) do { _Pragma("unroll") for (int _i = 0; _i < 2; ++_i) \
;         __builtin_amdgcn_global_load_lds((const unsigned*)((const char*)(gbase) + voffB[_i]), (LAS unsigned*)(lds + (bufoff) + ldsw + _i * 8192), 16, 0, 0); } while (0)
; #define PG8_LDA(dst, b, h) do { _Pragma("unroll") for (int m = 0; m < 4; ++m) _Pragma("unroll") for (int k = 0; k < 2; ++k) dst[m][k] = *(const LAS bf16x8*)(lds + PG8_SA(b, h) + aoff + m * 2048 + k * 1024); } while (0)
; #define PG8_LDB(dst, b, h) do { _Pragma("unroll") for (int n = 0; n < 2; ++n) _Pragma("unroll") for (int k = 0; k < 2; ++k) dst[n][k] = *(const LAS bf16x8*)(lds + PG8_SB(b, h) + boff + n * 2048 + k * 1024); } while (0)
; #define PG8_MMA(ai, bj, At, Bt) do { __builtin_amdgcn_s_setprio(1); _Pragma("unroll") for (int m = 0; m < 4; ++m) _Pragma("unroll") for (int n = 0; n < 2; ++n) _Pragma("unroll") for (int k = 0; k < 2; ++k) \
;         acc[ai][bj][m][n] = __builtin_amdgcn_mfma_f32_16x16x32_bf16(Bt[n][k], At[m][k], acc[ai][bj][m][n], 0, 0, 0); __builtin_amdgcn_s_setprio(0); } while (0)
; #define PG8_WAIT_V(n) asm volatile("s_waitcnt vmcnt(" #n ")" ::: "memory")
; #define PG8_WAIT_L(n) asm volatile("s_waitcnt lgkmcnt(" #n ")" ::: "memory")
; #define PG8_BAR __builtin_amdgcn_s_barrier()
; #define PG8_SCHED __builtin_amdgcn_sched_barrier(0)
; template <class Epi, class Sched, bool GATHER = false>
; __device__ __forceinline__ void gemm_phase(LAS unsigned char* lds, const Gemm g, const Sched& S, const Epi& E) {
;     ...
;             PG8_LDB(B0, 0, 0); PG8_LDB(B1, 0, 1); PG8_SCHED; PG8_LDA(At, 0, 0); PG8_STAGE_A(PG8_SA(1, 1), a1, voC, 1);
;             PG8_WAIT_V(8); PG8_WAIT_L(0); PG8_BAR; PG8_MMA(0, 0, At, B0); PG8_MMA(0, 1, At, B1); PG8_BAR; PG8_SCHED;
;             PG8_LDA(At, 0, 1); PG8_STAGE_B(PG8_SB(0, 0), b2); PG8_STAGE_B(PG8_SB(0, 1), b2 + hstepB); PG8_STAGE_A(PG8_SA(0, 0), a2, vo2, 0);
;             PG8_WAIT_V(8); PG8_WAIT_L(0); PG8_BAR; PG8_MMA(1, 0, At, B0); PG8_MMA(1, 1, At, B1); PG8_BAR; PG8_SCHED;
.LBB0_514:
	s_add_i32 s71, s14, 2
	s_add_u32 s15, vcc_lo, 0xffff0080
	s_addc_u32 s30, vcc_hi, -1
	s_add_i32 s54, 0, 0x10000
	s_cmp_eq_u32 s38, s14
	s_cselect_b32 s31, s16, s30
	s_cselect_b32 s30, s45, s15
	s_cselect_b32 s15, s47, s49
	s_cselect_b32 s14, s70, s48
	s_add_i32 s62, 0, 0x14000
	v_add_u32_e32 v156, s54, v141
	v_add_u32_e32 v172, s62, v141
	ds_read_b128 v[144:147], v156
	ds_read_b128 v[148:151], v156 offset:1024
	ds_read_b128 v[152:155], v156 offset:2048
	ds_read_b128 v[156:159], v156 offset:3072
	ds_read_b128 v[160:163], v172
	ds_read_b128 v[164:167], v172 offset:1024
	ds_read_b128 v[168:171], v172 offset:2048
	ds_read_b128 v[172:175], v172 offset:3072
	v_lshl_add_u64 v[192:193], vcc, 0, v[136:137]
	s_add_i32 m0, s41, 0xc000
	ds_read_b128 v[176:179], v143
	ds_read_b128 v[180:183], v143 offset:1024
	ds_read_b128 v[184:187], v143 offset:2048
	ds_read_b128 v[188:191], v143 offset:3072
	ds_read_b128 v[204:207], v143 offset:4096
	ds_read_b128 v[208:211], v143 offset:5120
	ds_read_b128 v[212:215], v143 offset:6144
	ds_read_b128 v[216:219], v143 offset:7168
	global_load_lds_dwordx4 v[192:193], off
	s_add_i32 m0, s41, 0xe000
	v_lshl_add_u64 v[192:193], vcc, 0, v[138:139]
	global_load_lds_dwordx4 v[192:193], off
	s_waitcnt vmcnt(8)
	s_waitcnt lgkmcnt(0)
	s_barrier
	s_setprio 1
	s_waitcnt lgkmcnt(0)
	v_mfma_f32_16x16x32_bf16 v[122:125], v[144:147], v[176:179], v[122:125]
	v_mfma_f32_16x16x32_bf16 v[126:129], v[152:155], v[176:179], v[126:129]
	v_mfma_f32_16x16x32_bf16 v[110:113], v[144:147], v[184:187], v[110:113]
	v_mfma_f32_16x16x32_bf16 v[106:109], v[152:155], v[184:187], v[106:109]
	v_mfma_f32_16x16x32_bf16 v[94:97], v[144:147], v[204:207], v[94:97]
	v_mfma_f32_16x16x32_bf16 v[90:93], v[152:155], v[204:207], v[90:93]
	v_mfma_f32_16x16x32_bf16 v[78:81], v[144:147], v[212:215], v[78:81]
	v_mfma_f32_16x16x32_bf16 v[74:77], v[152:155], v[212:215], v[74:77]
	v_mfma_f32_16x16x32_bf16 v[122:125], v[148:151], v[180:183], v[122:125]
	v_mfma_f32_16x16x32_bf16 v[126:129], v[156:159], v[180:183], v[126:129]
	v_mfma_f32_16x16x32_bf16 v[110:113], v[148:151], v[188:191], v[110:113]
	v_mfma_f32_16x16x32_bf16 v[106:109], v[156:159], v[188:191], v[106:109]
	v_mfma_f32_16x16x32_bf16 v[94:97], v[148:151], v[208:211], v[94:97]
	v_mfma_f32_16x16x32_bf16 v[90:93], v[156:159], v[208:211], v[90:93]
	v_mfma_f32_16x16x32_bf16 v[78:81], v[148:151], v[216:219], v[78:81]
	v_mfma_f32_16x16x32_bf16 v[74:77], v[156:159], v[216:219], v[74:77]
	s_setprio 0
	s_setprio 1
	v_mfma_f32_16x16x32_bf16 v[118:121], v[160:163], v[176:179], v[118:121]
	v_mfma_f32_16x16x32_bf16 v[114:117], v[168:171], v[176:179], v[114:117]
	v_mfma_f32_16x16x32_bf16 v[102:105], v[160:163], v[184:187], v[102:105]
	v_mfma_f32_16x16x32_bf16 v[98:101], v[168:171], v[184:187], v[98:101]
	v_mfma_f32_16x16x32_bf16 v[86:89], v[160:163], v[204:207], v[86:89]
	v_mfma_f32_16x16x32_bf16 v[82:85], v[168:171], v[204:207], v[82:85]
	v_mfma_f32_16x16x32_bf16 v[70:73], v[160:163], v[212:215], v[70:73]
	v_mfma_f32_16x16x32_bf16 v[66:69], v[168:171], v[212:215], v[66:69]
	v_mfma_f32_16x16x32_bf16 v[118:121], v[164:167], v[180:183], v[118:121]
	v_mfma_f32_16x16x32_bf16 v[114:117], v[172:175], v[180:183], v[114:117]
	v_mfma_f32_16x16x32_bf16 v[102:105], v[164:167], v[188:191], v[102:105]
	v_mfma_f32_16x16x32_bf16 v[98:101], v[172:175], v[188:191], v[98:101]
	v_mfma_f32_16x16x32_bf16 v[86:89], v[164:167], v[208:211], v[86:89]
	v_mfma_f32_16x16x32_bf16 v[82:85], v[172:175], v[208:211], v[82:85]
	v_mfma_f32_16x16x32_bf16 v[70:73], v[164:167], v[216:219], v[70:73]
	v_mfma_f32_16x16x32_bf16 v[66:69], v[172:175], v[216:219], v[66:69]
	s_setprio 0
	s_barrier
	s_add_i32 s54, s54, s59
	v_lshl_add_u64 v[192:193], s[14:15], 0, v[194:195]
	s_mov_b32 m0, s54
	ds_read_b128 v[176:179], v143 offset:16384
	ds_read_b128 v[180:183], v143 offset:17408
	ds_read_b128 v[184:187], v143 offset:18432
	ds_read_b128 v[188:191], v143 offset:19456
	ds_read_b128 v[204:207], v143 offset:20480
	ds_read_b128 v[208:211], v143 offset:21504
	ds_read_b128 v[212:215], v143 offset:22528
	ds_read_b128 v[216:219], v143 offset:23552
	global_load_lds_dwordx4 v[192:193], off
	s_add_i32 m0, s54, 0x2000
	s_add_u32 s54, s14, 0x20000
	v_lshl_add_u64 v[198:199], s[14:15], 0, v[134:135]
	s_addc_u32 s55, s15, 0
	s_add_i32 s62, s62, s59
	global_load_lds_dwordx4 v[198:199], off
	v_lshl_add_u64 v[200:201], s[54:55], 0, v[194:195]
	s_mov_b32 m0, s62
	v_lshl_add_u64 v[220:221], s[30:31], 0, v[130:131]
	global_load_lds_dwordx4 v[200:201], off
	s_add_i32 m0, s62, 0x2000
	v_lshl_add_u64 v[200:201], s[54:55], 0, v[134:135]
	global_load_lds_dwordx4 v[200:201], off
	s_mov_b32 m0, s41
	v_lshl_add_u64 v[200:201], s[30:31], 0, v[132:133]
	global_load_lds_dwordx4 v[200:201], off
	s_mov_b32 m0, s76
	s_nop 0
	global_load_lds_dwordx4 v[220:221], off
	s_waitcnt vmcnt(8)
	s_waitcnt lgkmcnt(0)
	s_barrier
; #define PG8_LDA(dst, b, h) do { _Pragma("unroll") for (int m = 0; m < 4; ++m) _Pragma("unroll") for (int k = 0; k < 2; ++k) dst[m][k] = *(const LAS bf16x8*)(lds + PG8_SA(b, h) + aoff + m * 2048 + k * 1024); } while (0)
; #define PG8_LDB(dst, b, h) do { _Pragma("unroll") for (int n = 0; n < 2; ++n) _Pragma("unroll") for (int k = 0; k < 2; ++k) dst[n][k] = *(const LAS bf16x8*)(lds + PG8_SB(b, h) + boff + n * 2048 + k * 1024); } while (0)
; #define PG8_MMA(ai, bj, At, Bt) do { __builtin_amdgcn_s_setprio(1); _Pragma("unroll") for (int m = 0; m < 4; ++m) _Pragma("unroll") for (int n = 0; n < 2; ++n) _Pragma("unroll") for (int k = 0; k < 2; ++k) \
;         acc[ai][bj][m][n] = __builtin_amdgcn_mfma_f32_16x16x32_bf16(Bt[n][k], At[m][k], acc[ai][bj][m][n], 0, 0, 0); __builtin_amdgcn_s_setprio(0); } while (0)
; #define PG8_WAIT_V(n) asm volatile("s_waitcnt vmcnt(" #n ")" ::: "memory")
; #define PG8_WAIT_L(n) asm volatile("s_waitcnt lgkmcnt(" #n ")" ::: "memory")
; #define PG8_BAR __builtin_amdgcn_s_barrier()
; #define PG8_SCHED __builtin_amdgcn_sched_barrier(0)
; template <class Epi, class Sched, bool GATHER = false>
; __device__ __forceinline__ void gemm_phase(LAS unsigned char* lds, const Gemm g, const Sched& S, const Epi& E) {
;     ...
;             PG8_WAIT_V(8); PG8_WAIT_L(0); PG8_BAR; PG8_MMA(1, 0, At, B0); PG8_MMA(1, 1, At, B1); PG8_BAR; PG8_SCHED;
;             PG8_LDB(B0, 1, 0); PG8_LDB(B1, 1, 1); PG8_SCHED; PG8_LDA(At, 1, 0); PG8_STAGE_A(PG8_SA(0, 1), a2, vo2, 1);
;             PG8_WAIT_V(8); PG8_WAIT_L(0); PG8_BAR; PG8_MMA(0, 0, At, B0); PG8_MMA(0, 1, At, B1); PG8_BAR; PG8_SCHED;
	s_setprio 1
	s_waitcnt lgkmcnt(0)
	v_mfma_f32_16x16x32_bf16 v[62:65], v[144:147], v[176:179], v[62:65]
	v_mfma_f32_16x16x32_bf16 v[58:61], v[152:155], v[176:179], v[58:61]
	v_mfma_f32_16x16x32_bf16 v[46:49], v[144:147], v[184:187], v[46:49]
	v_mfma_f32_16x16x32_bf16 v[42:45], v[152:155], v[184:187], v[42:45]
	v_mfma_f32_16x16x32_bf16 v[30:33], v[144:147], v[204:207], v[30:33]
	v_mfma_f32_16x16x32_bf16 v[26:29], v[152:155], v[204:207], v[26:29]
	v_mfma_f32_16x16x32_bf16 v[14:17], v[144:147], v[212:215], v[14:17]
	v_mfma_f32_16x16x32_bf16 v[10:13], v[152:155], v[212:215], v[10:13]
	v_mfma_f32_16x16x32_bf16 v[62:65], v[148:151], v[180:183], v[62:65]
	v_mfma_f32_16x16x32_bf16 v[58:61], v[156:159], v[180:183], v[58:61]
	v_mfma_f32_16x16x32_bf16 v[46:49], v[148:151], v[188:191], v[46:49]
	v_mfma_f32_16x16x32_bf16 v[42:45], v[156:159], v[188:191], v[42:45]
	v_mfma_f32_16x16x32_bf16 v[30:33], v[148:151], v[208:211], v[30:33]
	v_mfma_f32_16x16x32_bf16 v[26:29], v[156:159], v[208:211], v[26:29]
	v_mfma_f32_16x16x32_bf16 v[14:17], v[148:151], v[216:219], v[14:17]
	v_mfma_f32_16x16x32_bf16 v[10:13], v[156:159], v[216:219], v[10:13]
	s_setprio 0
	s_setprio 1
	v_mfma_f32_16x16x32_bf16 v[54:57], v[160:163], v[176:179], v[54:57]
	v_mfma_f32_16x16x32_bf16 v[50:53], v[168:171], v[176:179], v[50:53]
	v_mfma_f32_16x16x32_bf16 v[38:41], v[160:163], v[184:187], v[38:41]
	v_mfma_f32_16x16x32_bf16 v[34:37], v[168:171], v[184:187], v[34:37]
	v_mfma_f32_16x16x32_bf16 v[22:25], v[160:163], v[204:207], v[22:25]
	v_mfma_f32_16x16x32_bf16 v[18:21], v[168:171], v[204:207], v[18:21]
	v_mfma_f32_16x16x32_bf16 v[6:9], v[160:163], v[212:215], v[6:9]
	v_mfma_f32_16x16x32_bf16 v[2:5], v[168:171], v[212:215], v[2:5]
	v_mfma_f32_16x16x32_bf16 v[54:57], v[164:167], v[180:183], v[54:57]
	v_mfma_f32_16x16x32_bf16 v[50:53], v[172:175], v[180:183], v[50:53]
	v_mfma_f32_16x16x32_bf16 v[38:41], v[164:167], v[188:191], v[38:41]
	v_mfma_f32_16x16x32_bf16 v[34:37], v[172:175], v[188:191], v[34:37]
	v_mfma_f32_16x16x32_bf16 v[22:25], v[164:167], v[208:211], v[22:25]
	v_mfma_f32_16x16x32_bf16 v[18:21], v[172:175], v[208:211], v[18:21]
	v_mfma_f32_16x16x32_bf16 v[6:9], v[164:167], v[216:219], v[6:9]
	v_mfma_f32_16x16x32_bf16 v[2:5], v[172:175], v[216:219], v[2:5]
	s_setprio 0
	s_barrier
	s_add_i32 s54, 0, 0x18000
	s_add_i32 s55, 0, 0x1c000
	v_add_u32_e32 v156, s54, v141
	v_add_u32_e32 v172, s55, v141
	ds_read_b128 v[144:147], v156
	ds_read_b128 v[148:151], v156 offset:1024
	ds_read_b128 v[152:155], v156 offset:2048
	ds_read_b128 v[156:159], v156 offset:3072
	ds_read_b128 v[160:163], v172
	ds_read_b128 v[164:167], v172 offset:1024
	ds_read_b128 v[168:171], v172 offset:2048
	ds_read_b128 v[172:175], v172 offset:3072
	s_add_u32 s30, s30, 0x10000
	s_addc_u32 s31, s31, 0
	s_mov_b32 m0, s77
	v_lshl_add_u64 v[222:223], s[30:31], 0, v[132:133]
	ds_read_b128 v[176:179], v143 offset:32768
	ds_read_b128 v[180:183], v143 offset:33792
	ds_read_b128 v[184:187], v143 offset:34816
	ds_read_b128 v[188:191], v143 offset:35840
	ds_read_b128 v[204:207], v143 offset:36864
	ds_read_b128 v[208:211], v143 offset:37888
	ds_read_b128 v[212:215], v143 offset:38912
	ds_read_b128 v[216:219], v143 offset:39936
	global_load_lds_dwordx4 v[222:223], off
	s_mov_b32 m0, s80
	v_lshl_add_u64 v[222:223], s[30:31], 0, v[130:131]
	global_load_lds_dwordx4 v[222:223], off
	s_waitcnt vmcnt(8)
	s_waitcnt lgkmcnt(0)
	s_barrier
	s_setprio 1
	s_waitcnt lgkmcnt(0)
	v_mfma_f32_16x16x32_bf16 v[122:125], v[144:147], v[176:179], v[122:125]
	v_mfma_f32_16x16x32_bf16 v[126:129], v[152:155], v[176:179], v[126:129]
	v_mfma_f32_16x16x32_bf16 v[110:113], v[144:147], v[184:187], v[110:113]
	v_mfma_f32_16x16x32_bf16 v[106:109], v[152:155], v[184:187], v[106:109]
	v_mfma_f32_16x16x32_bf16 v[94:97], v[144:147], v[204:207], v[94:97]
	v_mfma_f32_16x16x32_bf16 v[90:93], v[152:155], v[204:207], v[90:93]
	v_mfma_f32_16x16x32_bf16 v[78:81], v[144:147], v[212:215], v[78:81]
	v_mfma_f32_16x16x32_bf16 v[74:77], v[152:155], v[212:215], v[74:77]
	v_mfma_f32_16x16x32_bf16 v[122:125], v[148:151], v[180:183], v[122:125]
	v_mfma_f32_16x16x32_bf16 v[126:129], v[156:159], v[180:183], v[126:129]
	v_mfma_f32_16x16x32_bf16 v[110:113], v[148:151], v[188:191], v[110:113]
	v_mfma_f32_16x16x32_bf16 v[106:109], v[156:159], v[188:191], v[106:109]
	v_mfma_f32_16x16x32_bf16 v[94:97], v[148:151], v[208:211], v[94:97]
	v_mfma_f32_16x16x32_bf16 v[90:93], v[156:159], v[208:211], v[90:93]
	v_mfma_f32_16x16x32_bf16 v[78:81], v[148:151], v[216:219], v[78:81]
	v_mfma_f32_16x16x32_bf16 v[74:77], v[156:159], v[216:219], v[74:77]
	s_setprio 0
	s_setprio 1
	v_mfma_f32_16x16x32_bf16 v[118:121], v[160:163], v[176:179], v[118:121]
	v_mfma_f32_16x16x32_bf16 v[114:117], v[168:171], v[176:179], v[114:117]
	v_mfma_f32_16x16x32_bf16 v[102:105], v[160:163], v[184:187], v[102:105]
	v_mfma_f32_16x16x32_bf16 v[98:101], v[168:171], v[184:187], v[98:101]
	v_mfma_f32_16x16x32_bf16 v[86:89], v[160:163], v[204:207], v[86:89]
	v_mfma_f32_16x16x32_bf16 v[82:85], v[168:171], v[204:207], v[82:85]
	v_mfma_f32_16x16x32_bf16 v[70:73], v[160:163], v[212:215], v[70:73]
	v_mfma_f32_16x16x32_bf16 v[66:69], v[168:171], v[212:215], v[66:69]
	v_mfma_f32_16x16x32_bf16 v[118:121], v[164:167], v[180:183], v[118:121]
	v_mfma_f32_16x16x32_bf16 v[114:117], v[172:175], v[180:183], v[114:117]
	v_mfma_f32_16x16x32_bf16 v[102:105], v[164:167], v[188:191], v[102:105]
	v_mfma_f32_16x16x32_bf16 v[98:101], v[172:175], v[188:191], v[98:101]
	v_mfma_f32_16x16x32_bf16 v[86:89], v[164:167], v[208:211], v[86:89]
	v_mfma_f32_16x16x32_bf16 v[82:85], v[172:175], v[208:211], v[82:85]
	v_mfma_f32_16x16x32_bf16 v[70:73], v[164:167], v[216:219], v[70:73]
	v_mfma_f32_16x16x32_bf16 v[66:69], v[172:175], v[216:219], v[66:69]
	s_setprio 0
	s_barrier
; #define PG8_STAGE_B(bufoff, gbase) do { _Pragma("unroll") for (int _i = 0; _i < 2; ++_i) \
;         __builtin_amdgcn_global_load_lds((const unsigned*)((const char*)(gbase) + voffB[_i]), (LAS unsigned*)(lds + (bufoff) + ldsw + _i * 8192), 16, 0, 0); } while (0)
; #define PG8_LDA(dst, b, h) do { _Pragma("unroll") for (int m = 0; m < 4; ++m) _Pragma("unroll") for (int k = 0; k < 2; ++k) dst[m][k] = *(const LAS bf16x8*)(lds + PG8_SA(b, h) + aoff + m * 2048 + k * 1024); } while (0)
; #define PG8_MMA(ai, bj, At, Bt) do { __builtin_amdgcn_s_setprio(1); _Pragma("unroll") for (int m = 0; m < 4; ++m) _Pragma("unroll") for (int n = 0; n < 2; ++n) _Pragma("unroll") for (int k = 0; k < 2; ++k) \
;         acc[ai][bj][m][n] = __builtin_amdgcn_mfma_f32_16x16x32_bf16(Bt[n][k], At[m][k], acc[ai][bj][m][n], 0, 0, 0); __builtin_amdgcn_s_setprio(0); } while (0)
; #define PG8_WAIT_V(n) asm volatile("s_waitcnt vmcnt(" #n ")" ::: "memory")
; #define PG8_WAIT_L(n) asm volatile("s_waitcnt lgkmcnt(" #n ")" ::: "memory")
; #define PG8_BAR __builtin_amdgcn_s_barrier()
; #define PG8_SCHED __builtin_amdgcn_sched_barrier(0)
; template <class Epi, class Sched, bool GATHER = false>
; __device__ __forceinline__ void gemm_phase(LAS unsigned char* lds, const Gemm g, const Sched& S, const Epi& E) {
;     ...
;             PG8_LDA(At, 1, 1); PG8_STAGE_B(PG8_SB(1, 0), b3); PG8_STAGE_B(PG8_SB(1, 1), b3 + hstepB); PG8_STAGE_A(PG8_SA(1, 0), a3, vo2, 0);
;             PG8_WAIT_V(8); PG8_WAIT_L(0); PG8_BAR; PG8_MMA(1, 0, At, B0); PG8_MMA(1, 1, At, B1); PG8_BAR; PG8_SCHED;
;         }
	s_add_i32 s30, s54, s59
	v_lshl_add_u64 v[192:193], v[192:193], 0, s[66:67]
	s_mov_b32 m0, s30
	ds_read_b128 v[176:179], v143 offset:49152
	ds_read_b128 v[180:183], v143 offset:50176
	ds_read_b128 v[184:187], v143 offset:51200
	ds_read_b128 v[188:191], v143 offset:52224
	ds_read_b128 v[204:207], v143 offset:53248
	ds_read_b128 v[208:211], v143 offset:54272
	ds_read_b128 v[212:215], v143 offset:55296
	ds_read_b128 v[216:219], v143 offset:56320
	global_load_lds_dwordx4 v[192:193], off
	s_add_i32 m0, s30, 0x2000
	s_add_u32 s14, s14, 0x20080
	v_lshl_add_u64 v[192:193], v[198:199], 0, s[66:67]
	s_addc_u32 s15, s15, 0
	s_add_i32 s30, s55, s59
	global_load_lds_dwordx4 v[192:193], off
	s_mov_b32 m0, s30
	v_lshl_add_u64 v[192:193], s[14:15], 0, v[194:195]
	global_load_lds_dwordx4 v[192:193], off
	s_add_i32 m0, s30, 0x2000
	v_lshl_add_u64 v[192:193], s[14:15], 0, v[134:135]
	global_load_lds_dwordx4 v[192:193], off
	s_mov_b32 m0, s81
	v_lshl_add_u64 v[192:193], v[200:201], 0, s[66:67]
	global_load_lds_dwordx4 v[192:193], off
	s_mov_b32 m0, s84
	v_lshl_add_u64 v[192:193], v[220:221], 0, s[66:67]
	global_load_lds_dwordx4 v[192:193], off
	s_waitcnt vmcnt(8)
	s_waitcnt lgkmcnt(0)
	s_barrier
	s_setprio 1
	s_waitcnt lgkmcnt(0)
	v_mfma_f32_16x16x32_bf16 v[62:65], v[144:147], v[176:179], v[62:65]
	v_mfma_f32_16x16x32_bf16 v[58:61], v[152:155], v[176:179], v[58:61]
	v_mfma_f32_16x16x32_bf16 v[46:49], v[144:147], v[184:187], v[46:49]
	v_mfma_f32_16x16x32_bf16 v[42:45], v[152:155], v[184:187], v[42:45]
	v_mfma_f32_16x16x32_bf16 v[30:33], v[144:147], v[204:207], v[30:33]
	v_mfma_f32_16x16x32_bf16 v[26:29], v[152:155], v[204:207], v[26:29]
	v_mfma_f32_16x16x32_bf16 v[14:17], v[144:147], v[212:215], v[14:17]
	v_mfma_f32_16x16x32_bf16 v[10:13], v[152:155], v[212:215], v[10:13]
	v_mfma_f32_16x16x32_bf16 v[62:65], v[148:151], v[180:183], v[62:65]
	v_mfma_f32_16x16x32_bf16 v[58:61], v[156:159], v[180:183], v[58:61]
	v_mfma_f32_16x16x32_bf16 v[46:49], v[148:151], v[188:191], v[46:49]
	v_mfma_f32_16x16x32_bf16 v[42:45], v[156:159], v[188:191], v[42:45]
	v_mfma_f32_16x16x32_bf16 v[30:33], v[148:151], v[208:211], v[30:33]
	v_mfma_f32_16x16x32_bf16 v[26:29], v[156:159], v[208:211], v[26:29]
	v_mfma_f32_16x16x32_bf16 v[14:17], v[148:151], v[216:219], v[14:17]
	v_mfma_f32_16x16x32_bf16 v[10:13], v[156:159], v[216:219], v[10:13]
	s_setprio 0
	s_setprio 1
	v_mfma_f32_16x16x32_bf16 v[54:57], v[160:163], v[176:179], v[54:57]
	v_mfma_f32_16x16x32_bf16 v[50:53], v[168:171], v[176:179], v[50:53]
	v_mfma_f32_16x16x32_bf16 v[38:41], v[160:163], v[184:187], v[38:41]
	v_mfma_f32_16x16x32_bf16 v[34:37], v[168:171], v[184:187], v[34:37]
	v_mfma_f32_16x16x32_bf16 v[22:25], v[160:163], v[204:207], v[22:25]
	v_mfma_f32_16x16x32_bf16 v[18:21], v[168:171], v[204:207], v[18:21]
	v_mfma_f32_16x16x32_bf16 v[6:9], v[160:163], v[212:215], v[6:9]
	v_mfma_f32_16x16x32_bf16 v[2:5], v[168:171], v[212:215], v[2:5]
	v_mfma_f32_16x16x32_bf16 v[54:57], v[164:167], v[180:183], v[54:57]
	v_mfma_f32_16x16x32_bf16 v[50:53], v[172:175], v[180:183], v[50:53]
	v_mfma_f32_16x16x32_bf16 v[38:41], v[164:167], v[188:191], v[38:41]
	v_mfma_f32_16x16x32_bf16 v[34:37], v[172:175], v[188:191], v[34:37]
	v_mfma_f32_16x16x32_bf16 v[22:25], v[164:167], v[208:211], v[22:25]
	v_mfma_f32_16x16x32_bf16 v[18:21], v[172:175], v[208:211], v[18:21]
	v_mfma_f32_16x16x32_bf16 v[6:9], v[164:167], v[216:219], v[6:9]
	v_mfma_f32_16x16x32_bf16 v[2:5], v[172:175], v[216:219], v[2:5]
	s_setprio 0
	s_barrier
	s_add_u32 vcc_lo, vcc_lo, 0x100
	s_addc_u32 vcc_hi, vcc_hi, 0
	s_add_u32 s48, s48, 0x100
	s_addc_u32 s49, s49, 0
	s_cmp_ge_i32 s71, s25
	s_mov_b32 s14, s71
	s_cbranch_scc0 .LBB0_514
	v_readlane_b32 s0, v255, 29
	v_readlane_b32 s1, v255, 30
	v_readlane_b32 s70, v255, 36

; #define ATT_DMA_K(t, sl) do { glds16(ksrc + (size_t)(t) * 64 * kpitch, (unsigned)__builtin_amdgcn_readfirstlane(kdst + (sl) * KSLOT)); \
;         if constexpr (DQK == 96) glds16(krsrc + (size_t)(t) * 64 * 32, (unsigned)__builtin_amdgcn_readfirstlane(krdst + (sl) * KSLOT)); } while (0)
; template <int DQK, int DV, bool LEAD> ...
;     ...
;     const int kc_l = (lane & 7) ^ (((krow_l >> 1) & 1) | (((krow_l >> 3) & 1) << 1) | (((krow_l >> 4) & 1) << 2));
;     const int vc_l = (lane & 7) ^ ((krow_l >> 1) & 7);
;     const bf16_t* ksrc = K + (size_t)(krow0 + krow_l) * kpitch + kc_l * 8;
;     const int rrow_l = (wid & 3) * 16 + (lane >> 2), rc_l = (lane & 3) ^ (((rrow_l >> 4) & 1) << 1);
;     const bf16_t* krsrc = (DQK == 96) ? KR + (size_t)(krow0 + rrow_l) * 32 + rc_l * 8 : nullptr;
;     const bf16_t* vsrc = Vt + (size_t)krow_l * NR + krow0 + vc_l * 8;
;     const unsigned kdst = lds0 + KOFF + wid * 1024, krdst = lds0 + KOFF + 8192 + (wid & 3) * 1024, vdst = lds0 + VOFF + wid * 1024;
;     ...
;     const int kr0 = 8 * (q16 >> 2) + (q16 & 3);
;     const int fk = ((kr0 >> 1) & 1) | (((kr0 >> 3) & 1) << 1) | (((kr0 >> 4) & 1) << 2);
;     ...
;     ATT_DMA_K(0, 0); ATT_DMA_V(0, 0); ATT_DMA_K(1, 1); ATT_DMA_K(2, 2);
;     bf16x8 qf[NQB * NDS];
;     {
;       const float c2 = (DQK == 64) ? C2_EVEN : C2_ODD; const bool lat = tq0 >= 0;
; #pragma unroll
;       for (int qb = 0; qb < NQB; ++qb) {
;           const bf16_t* qp = Q + (size_t)(qrow0 + qoff + qb * 16 + q16) * qpitch + g4 * 8;
;           bf16x8 raw[NDS];
; #pragma unroll
;           for (int ds = 0; ds < NDS; ++ds) raw[ds] = *(const bf16x8*)(qp + ds * 32);
;           float x[NDS][8];
; #pragma unroll
;           for (int ds = 0; ds < NDS; ++ds)
; #pragma unroll
;               for (int j = 0; j < 8; ++j) x[ds][j] = __uint_as_float(((unsigned)(unsigned short)raw[ds][j]) << 16);
;           const int tq = tq0 + qoff + qb * 16 + q16, prow = (tq >> 6) & 127, pcol = tq & 63;
;           float sn = 0.f;
; #pragma unroll
;           for (int ds = 0; ds < 2; ++ds)
; #pragma unroll
;               for (int j = 0; j < 8; ++j) sn += x[ds][j] * x[ds][j];
;           sn = lanes4_sum(sn);
;           const float rn = rsqrtf(sn * (1.f / 64.f) + EPS);
; #pragma unroll
;           for (int ds = 0; ds < 2; ++ds)
; #pragma unroll
;               for (int j = 0; j < 8; ++j) x[ds][j] *= rn * qgain[32 * ds + 8 * g4 + j];
.LBB0_641:
	s_bfe_u32 s24, s4, 0x40005
	s_ashr_i32 s5, s4, 9
	s_mul_i32 s6, s24, 0xc0
	s_add_u32 s46, s8, s6
	s_addc_u32 s47, s9, 0
	s_lshl_b32 s6, s24, 7
	s_add_u32 s50, s10, s6
	s_addc_u32 s51, s11, 0
	s_mul_i32 s6, s24, 0x840000
	s_add_u32 s52, s22, s6
	s_mov_b64 s[6:7], s[0:1]
	s_load_dwordx2 s[6:7], s[6:7], 0x98
	s_addc_u32 s53, s23, 0
	s_lshl_b32 s4, s4, 8
	s_mul_i32 s40, s5, 0x2100
	s_and_b32 s31, s4, 0x1f00
	s_add_i32 s25, s40, s31
	s_lshl_b64 s[4:5], s[20:21], 2
	s_waitcnt lgkmcnt(0)
	s_add_u32 s44, s6, s4
	s_addc_u32 s45, s7, s5
	v_readfirstlane_b32 s4, v0
	s_cmpk_gt_u32 s4, 0xff
	s_mov_b64 s[4:5], -1
	s_cbranch_scc0 .LBB0_648
	v_mov_b32_e32 v236, v0
	v_mov_b64_e32 v[6:7], s[52:53]
	v_readfirstlane_b32 s38, v236
	s_ashr_i32 s4, s38, 6
	v_bfe_u32 v2, v236, 3, 3
	v_lshl_or_b32 v8, s4, 3, v2
	v_ashrrev_i32_e32 v3, 1, v8
	v_and_b32_e32 v4, 1, v3
	s_lshl_b32 s5, s4, 1
	s_lshr_b32 s7, s38, 5
	v_and_b32_e32 v2, 7, v236
	s_and_b32 s6, s5, 2
	v_and_or_b32 v4, s7, 4, v4
	s_and_b32 s30, s4, 3
	v_bitop3_b32 v9, v4, v2, s6 bitop3:0x36
	v_bfe_u32 v4, v236, 2, 4
	v_add_u32_e32 v2, s40, v8
	v_lshl_or_b32 v4, s30, 4, v4
	v_xor_b32_e32 v10, v3, v236
	v_ashrrev_i32_e32 v3, 31, v2
	v_or_b32_e32 v4, s40, v4
	v_lshlrev_b64 v[2:3], 11, v[2:3]
	v_and_b32_e32 v12, 3, v236
	v_ashrrev_i32_e32 v5, 31, v4
	v_bitop3_b32 v11, s5, v12, 2 bitop3:0x6c
	v_lshlrev_b64 v[4:5], 6, v[4:5]
	s_lshl_b32 s42, s4, 10
	s_lshl_b32 s6, s30, 10
	v_lshl_add_u64 v[2:3], s[50:51], 0, v[2:3]
	v_lshlrev_b32_e32 v194, 4, v9
	s_ashr_i32 s41, s40, 31
	s_add_i32 s42, s42, 0
	v_lshl_add_u64 v[4:5], s[28:29], 0, v[4:5]
	v_mad_i64_i32 v[6:7], s[4:5], v8, s91, v[6:7]
	v_lshl_add_u64 v[192:193], v[2:3], 0, v[194:195]
	v_lshlrev_b32_e32 v194, 4, v11
	v_lshlrev_b32_e32 v2, 4, v10
	s_add_i32 s43, s6, 0
	s_mov_b32 m0, s42
	s_nop 0
	global_load_lds_dwordx4 v[192:193], off
	v_lshl_add_u64 v[6:7], s[40:41], 1, v[6:7]
	v_lshl_add_u64 v[204:205], v[4:5], 0, v[194:195]
	v_and_b32_e32 v194, 0x70, v2
	s_addk_i32 s43, 0x2000
	s_mov_b32 m0, s43
	s_nop 0
	global_load_lds_dwordx4 v[204:205], off
	s_add_i32 s41, s42, 0x9000
	v_lshl_add_u64 v[206:207], v[6:7], 0, v[194:195]
	s_mov_b32 m0, s41
	s_nop 0
	global_load_lds_dwordx4 v[206:207], off
	s_mov_b64 s[4:5], 0x20000
	v_lshl_add_u64 v[2:3], v[192:193], 0, s[4:5]
	s_add_i32 s4, s42, 0x3000
	s_mov_b32 m0, s4
	s_nop 0
	global_load_lds_dwordx4 v[2:3], off
	v_lshl_add_u64 v[2:3], v[204:205], 0, s[60:61]
	s_add_i32 s4, s43, 0x3000
	s_mov_b32 m0, s4
	s_nop 0
	global_load_lds_dwordx4 v[2:3], off
	s_mov_b64 s[4:5], 0x40000
	v_lshl_add_u64 v[2:3], v[192:193], 0, s[4:5]
	s_add_i32 s4, s42, 0x6000
	s_mov_b32 m0, s4
	s_nop 0
	global_load_lds_dwordx4 v[2:3], off
	s_mov_b64 s[4:5], 0x2000
	v_and_b32_e32 v237, 15, v236
	v_lshl_add_u64 v[2:3], v[204:205], 0, s[4:5]
	s_add_i32 s4, s43, 0x6000
	s_mov_b32 m0, s4
	s_nop 0
	global_load_lds_dwordx4 v[2:3], off
	v_lshl_or_b32 v2, s30, 6, v237
	v_and_b32_e32 v8, 48, v236
	v_or_b32_e32 v6, s25, v2
	v_mov_b32_e32 v9, v195
	v_lshl_add_u64 v[2:3], s[46:47], 0, v[8:9]
	v_or_b32_e32 v7, 16, v6
	v_mad_i64_i32 v[4:5], s[4:5], v6, s90, v[2:3]
	v_mad_i64_i32 v[10:11], s[4:5], v7, s90, v[2:3]
	v_or_b32_e32 v7, 32, v6
	v_or_b32_e32 v6, 48, v6
	v_mad_i64_i32 v[14:15], s[4:5], v7, s90, v[2:3]
	v_mad_i64_i32 v[16:17], s[4:5], v6, s90, v[2:3]
	global_load_dwordx4 v[54:57], v[4:5], off offset:64
	global_load_dwordx4 v[62:65], v[10:11], off offset:64
	global_load_dwordx4 v[84:87], v[14:15], off offset:64
	global_load_dwordx4 v[122:125], v[16:17], off offset:64
	global_load_dwordx4 v[138:141], v[4:5], off
	global_load_dwordx4 v[144:147], v[10:11], off
	global_load_dwordx4 v[80:83], v[14:15], off
	global_load_dwordx4 v[6:9], v[16:17], off
	s_lshr_b32 s4, s31, 6
	v_and_b32_e32 v194, 63, v236
	v_lshlrev_b32_e32 v2, 1, v236
	s_or_b32 s4, s4, s30
	v_and_or_b32 v239, v2, 24, v12
	v_bfe_u32 v241, v236, 3, 1
	v_mov_b32_e32 v18, s4
	v_cmp_gt_u32_e32 vcc, 32, v194
	v_or_b32_e32 v19, 16, v237
	v_bfe_u32 v238, v236, 4, 2
	s_ashr_i32 s16, s38, 8
	v_bfe_u32 v242, v236, 1, 2
	v_lshlrev_b32_e32 v243, 2, v241
	v_lshl_add_u32 v240, v239, 7, 0
	v_cndmask_b32_e32 v12, v237, v18, vcc
	v_cndmask_b32_e32 v19, v19, v18, vcc
	v_lshl_add_u32 v244, s16, 12, v240
	v_bitop3_b32 v2, v243, v238, v242 bitop3:0x36
	v_lshlrev_b32_e32 v12, 6, v12
	v_lshlrev_b32_e32 v19, 6, v19
	v_lshl_add_u32 v203, v2, 4, v244
	global_load_dwordx4 v[2:5], v[4:5], off offset:128
	s_nop 0
	global_load_dwordx4 v[112:115], v12, s[36:37] offset:48
	global_load_dwordx4 v[108:111], v12, s[36:37] offset:32
	global_load_dwordx4 v[104:107], v12, s[36:37] offset:16
	global_load_dwordx4 v[100:103], v12, s[36:37]
	s_nop 0
	global_load_dwordx4 v[10:13], v[10:11], off offset:128
	s_nop 0
	global_load_dwordx4 v[96:99], v19, s[36:37] offset:48
	global_load_dwordx4 v[92:95], v19, s[36:37] offset:32
	global_load_dwordx4 v[88:91], v19, s[36:37] offset:16
	global_load_dwordx4 v[58:61], v19, s[36:37]
	global_load_dwordx4 v[34:37], v[14:15], off offset:128
	v_or_b32_e32 v14, 32, v237
	v_cndmask_b32_e32 v14, v14, v18, vcc
	v_lshlrev_b32_e32 v14, 6, v14
	global_load_dwordx4 v[76:79], v14, s[36:37] offset:48
	global_load_dwordx4 v[70:73], v14, s[36:37] offset:32
	global_load_dwordx4 v[66:69], v14, s[36:37] offset:16
	global_load_dwordx4 v[50:53], v14, s[36:37]
	global_load_dwordx4 v[46:49], v[16:17], off offset:128
	v_or_b32_e32 v14, 48, v237
	v_cndmask_b32_e32 v14, v14, v18, vcc
	v_lshlrev_b32_e32 v18, 6, v14
	v_lshlrev_b32_e32 v162, 5, v238
	global_load_dwordx4 v[14:17], v18, s[36:37] offset:48
	global_load_dwordx4 v[20:23], v18, s[36:37] offset:32
	global_load_dwordx4 v[24:27], v18, s[36:37] offset:16
	global_load_dwordx4 v[30:33], v18, s[36:37]
	global_load_dwordx4 v[38:41], v162, s[44:45] offset:144
	global_load_dwordx4 v[42:45], v162, s[44:45] offset:128
	v_and_b32_e32 v160, 16, v236
	v_cmp_eq_u32_e32 vcc, 0, v160
	s_mov_b32 s6, 0x3d000000
	s_brev_b32 s7, 60
	s_mov_b32 s4, 0x358637bd
	s_mov_b32 s7, 0x3c800000
	v_mov_b64_e32 v[170:171], s[4:5]
	s_mov_b32 s48, 2
	s_waitcnt vmcnt(26)
; template <int DQK, int DV, bool LEAD> ...
;     ...
;           float x[NDS][8];
; #pragma unroll
;           for (int ds = 0; ds < NDS; ++ds)
; #pragma unroll
;               for (int j = 0; j < 8; ++j) x[ds][j] = __uint_as_float(((unsigned)(unsigned short)raw[ds][j]) << 16);
;           const int tq = tq0 + qoff + qb * 16 + q16, prow = (tq >> 6) & 127, pcol = tq & 63;
;           float sn = 0.f;
; #pragma unroll
;           for (int ds = 0; ds < 2; ++ds)
; #pragma unroll
;               for (int j = 0; j < 8; ++j) sn += x[ds][j] * x[ds][j];
;           sn = lanes4_sum(sn);
	v_and_b32_e32 v117, 0xffff0000, v125
	s_waitcnt vmcnt(25)
	v_and_b32_e32 v191, 0xffff0000, v138
	v_lshlrev_b32_e32 v190, 16, v138
	v_lshlrev_b32_e32 v116, 16, v125
	s_waitcnt vmcnt(22)
	v_and_b32_e32 v127, 0xffff0000, v8
	v_lshlrev_b32_e32 v126, 16, v8
	v_mul_f32_e32 v8, v191, v191
	v_and_b32_e32 v119, 0xffff0000, v124
	v_lshlrev_b32_e32 v118, 16, v124
	v_and_b32_e32 v125, 0xffff0000, v9
	v_lshlrev_b32_e32 v124, 16, v9
	v_and_b32_e32 v211, 0xffff0000, v139
	v_lshlrev_b32_e32 v210, 16, v139
	v_pk_fma_f32 v[8:9], v[190:191], v[190:191], v[8:9] op_sel_hi:[1,1,0]
	v_and_b32_e32 v187, 0xffff0000, v141
	v_lshlrev_b32_e32 v186, 16, v141
	v_and_b32_e32 v189, 0xffff0000, v140
	v_lshlrev_b32_e32 v188, 16, v140
	v_and_b32_e32 v141, 0xffff0000, v82
	v_lshlrev_b32_e32 v140, 16, v82
	v_pk_fma_f32 v[8:9], v[210:211], v[210:211], v[8:9]
	v_mul_f32_e32 v82, v211, v211
	v_pk_add_f32 v[8:9], v[82:83], v[8:9] op_sel_hi:[0,1]
	v_pk_fma_f32 v[8:9], v[188:189], v[188:189], v[8:9]
	v_mul_f32_e32 v82, v189, v189
	v_pk_add_f32 v[8:9], v[82:83], v[8:9] op_sel_hi:[0,1]
	v_pk_fma_f32 v[8:9], v[186:187], v[186:187], v[8:9]
	v_mul_f32_e32 v82, v187, v187
	v_and_b32_e32 v185, 0xffff0000, v54
	v_lshlrev_b32_e32 v184, 16, v54
	v_pk_add_f32 v[8:9], v[82:83], v[8:9] op_sel_hi:[0,1]
	v_pk_fma_f32 v[8:9], v[184:185], v[184:185], v[8:9]
	v_mul_f32_e32 v82, v185, v185
	v_and_b32_e32 v179, 0xffff0000, v55
	v_lshlrev_b32_e32 v178, 16, v55
	v_pk_add_f32 v[8:9], v[82:83], v[8:9] op_sel_hi:[0,1]
	v_pk_fma_f32 v[8:9], v[178:179], v[178:179], v[8:9]
	v_mul_f32_e32 v82, v179, v179
	v_and_b32_e32 v177, 0xffff0000, v56
	v_lshlrev_b32_e32 v176, 16, v56
	v_pk_add_f32 v[8:9], v[82:83], v[8:9] op_sel_hi:[0,1]
	v_pk_fma_f32 v[8:9], v[176:177], v[176:177], v[8:9]
	v_mul_f32_e32 v82, v177, v177
	v_and_b32_e32 v175, 0xffff0000, v57
	v_lshlrev_b32_e32 v174, 16, v57
	v_pk_add_f32 v[8:9], v[82:83], v[8:9] op_sel_hi:[0,1]
	v_pk_fma_f32 v[8:9], v[174:175], v[174:175], v[8:9]
	v_mul_f32_e32 v82, v175, v175
	v_pk_add_f32 v[8:9], v[82:83], v[8:9] op_sel_hi:[0,1]
	v_and_b32_e32 v129, 0xffff0000, v7
	v_lshlrev_b32_e32 v128, 16, v7
	v_mov_b32_e32 v7, v8
	s_nop 1
	v_permlane16_swap_b32_e32 v8, v7
	v_add_f32_e32 v7, v8, v7
	v_mov_b32_e32 v9, v7
	v_and_b32_e32 v167, 0xffff0000, v144
	s_nop 0
	v_permlane32_swap_b32_e32 v7, v9
	v_lshlrev_b32_e32 v166, 16, v144
	v_mul_f32_e32 v8, v167, v167
	v_and_b32_e32 v137, 0xffff0000, v83
	v_lshlrev_b32_e32 v136, 16, v83
	v_and_b32_e32 v159, 0xffff0000, v145
	v_lshlrev_b32_e32 v158, 16, v145
	v_pk_fma_f32 v[82:83], v[166:167], v[166:167], v[8:9] op_sel_hi:[1,1,0]
	v_mul_f32_e32 v8, v159, v159
	v_pk_fma_f32 v[82:83], v[158:159], v[158:159], v[82:83]
	v_and_b32_e32 v157, 0xffff0000, v146
	v_lshlrev_b32_e32 v156, 16, v146
	v_pk_add_f32 v[82:83], v[8:9], v[82:83] op_sel_hi:[0,1]
	v_pk_fma_f32 v[82:83], v[156:157], v[156:157], v[82:83]
	v_mul_f32_e32 v8, v157, v157
	v_and_b32_e32 v155, 0xffff0000, v147
	v_lshlrev_b32_e32 v154, 16, v147
	v_pk_add_f32 v[82:83], v[8:9], v[82:83] op_sel_hi:[0,1]
	v_pk_fma_f32 v[82:83], v[154:155], v[154:155], v[82:83]
	v_mul_f32_e32 v8, v155, v155
	v_and_b32_e32 v153, 0xffff0000, v62
	v_lshlrev_b32_e32 v152, 16, v62
	v_pk_add_f32 v[82:83], v[8:9], v[82:83] op_sel_hi:[0,1]
	v_pk_fma_f32 v[82:83], v[152:153], v[152:153], v[82:83]
	v_mul_f32_e32 v8, v153, v153
	v_and_b32_e32 v151, 0xffff0000, v63
	v_lshlrev_b32_e32 v150, 16, v63
	v_pk_add_f32 v[82:83], v[8:9], v[82:83] op_sel_hi:[0,1]
	v_pk_fma_f32 v[82:83], v[150:151], v[150:151], v[82:83]
	v_mul_f32_e32 v8, v151, v151
	v_and_b32_e32 v29, 0xffff0000, v64
	v_lshlrev_b32_e32 v28, 16, v64
	v_pk_add_f32 v[82:83], v[8:9], v[82:83] op_sel_hi:[0,1]
	v_pk_fma_f32 v[82:83], v[28:29], v[28:29], v[82:83]
	v_mul_f32_e32 v8, v29, v29
	v_and_b32_e32 v19, 0xffff0000, v65
	v_lshlrev_b32_e32 v18, 16, v65
	v_pk_add_f32 v[82:83], v[8:9], v[82:83] op_sel_hi:[0,1]
	v_pk_fma_f32 v[82:83], v[18:19], v[18:19], v[82:83]
	v_mul_f32_e32 v8, v19, v19
	v_pk_add_f32 v[82:83], v[8:9], v[82:83] op_sel_hi:[0,1]
	v_mov_b32_e32 v8, v82
	s_nop 1
	v_permlane16_swap_b32_e32 v82, v8
	v_and_b32_e32 v149, 0xffff0000, v80
	v_add_f32_e32 v181, v82, v8
	v_lshlrev_b32_e32 v148, 16, v80
	v_mul_f32_e32 v8, v149, v149
	v_and_b32_e32 v143, 0xffff0000, v81
	v_lshlrev_b32_e32 v142, 16, v81
	v_pk_fma_f32 v[80:81], v[148:149], v[148:149], v[8:9] op_sel_hi:[1,1,0]
	v_mul_f32_e32 v8, v143, v143
	v_pk_fma_f32 v[80:81], v[142:143], v[142:143], v[80:81]
	v_and_b32_e32 v135, 0xffff0000, v84
	v_pk_add_f32 v[80:81], v[8:9], v[80:81] op_sel_hi:[0,1]
	v_pk_fma_f32 v[80:81], v[140:141], v[140:141], v[80:81]
	v_mul_f32_e32 v8, v141, v141
	v_pk_add_f32 v[80:81], v[8:9], v[80:81] op_sel_hi:[0,1]
	v_pk_fma_f32 v[80:81], v[136:137], v[136:137], v[80:81]
	v_mul_f32_e32 v8, v137, v137
	v_lshlrev_b32_e32 v134, 16, v84
	v_pk_add_f32 v[80:81], v[8:9], v[80:81] op_sel_hi:[0,1]
	v_pk_fma_f32 v[80:81], v[134:135], v[134:135], v[80:81]
	v_mul_f32_e32 v8, v135, v135
	v_and_b32_e32 v133, 0xffff0000, v85
	v_lshlrev_b32_e32 v132, 16, v85
	v_pk_add_f32 v[80:81], v[8:9], v[80:81] op_sel_hi:[0,1]
	v_pk_fma_f32 v[80:81], v[132:133], v[132:133], v[80:81]
	v_mul_f32_e32 v8, v133, v133
	v_and_b32_e32 v131, 0xffff0000, v86
	v_lshlrev_b32_e32 v130, 16, v86
	v_pk_add_f32 v[80:81], v[8:9], v[80:81] op_sel_hi:[0,1]
	v_pk_fma_f32 v[80:81], v[130:131], v[130:131], v[80:81]
	v_mul_f32_e32 v8, v131, v131
	v_and_b32_e32 v75, 0xffff0000, v87
	v_lshlrev_b32_e32 v74, 16, v87
	v_pk_add_f32 v[80:81], v[8:9], v[80:81] op_sel_hi:[0,1]
	v_pk_fma_f32 v[80:81], v[74:75], v[74:75], v[80:81]
	v_mul_f32_e32 v8, v75, v75
	v_pk_add_f32 v[80:81], v[8:9], v[80:81] op_sel_hi:[0,1]
	v_mov_b32_e32 v8, v80
; template <int DQK, int DV, bool LEAD> ...
;     ...
;           float sn = 0.f;
; #pragma unroll
;           for (int ds = 0; ds < 2; ++ds)
; #pragma unroll
;               for (int j = 0; j < 8; ++j) sn += x[ds][j] * x[ds][j];
;           sn = lanes4_sum(sn);
;           const float rn = rsqrtf(sn * (1.f / 64.f) + EPS);
; #pragma unroll
;           for (int ds = 0; ds < 2; ++ds)
; #pragma unroll
;               for (int j = 0; j < 8; ++j) x[ds][j] *= rn * qgain[32 * ds + 8 * g4 + j];
;           if constexpr (DQK == 64) {
; #pragma unroll
;               for (int ds = 0; ds < 2; ++ds)
; #pragma unroll
;                   for (int j = 0; j < 8; ++j) {
;                       auto rr = __builtin_amdgcn_permlane32_swap(__float_as_uint(x[ds][j]), __float_as_uint(x[ds][j]), false, false);
;                       const float other = hi ? __uint_as_float(rr[0]) : __uint_as_float(rr[1]);
;                       float cc = 1.f, sg = 0.f;
;                       if (lat) { const f32x2 cs = rope[(ds ? pcol : prow) * 16 + 8 * (g4 & 1) + j]; cc = cs.x; sg = hi ? cs.y : -cs.y; }
;                       x[ds][j] = x[ds][j] * cc + other * sg; }
;           } else {
;               float sr = 0.f;
; #pragma unroll
;               for (int j = 0; j < 8; ++j) sr += x[2][j] * x[2][j];
;               sr = lanes4_sum(sr);
;               const float rq = rsqrtf(sr * (1.f / 32.f) + EPS);
; #pragma unroll
;               for (int j = 0; j < 8; ++j) { const float av = x[2][j] * rq * qgain[64 + 8 * g4 + j];
;                   auto rr = __builtin_amdgcn_permlane16_swap(__float_as_uint(av), __float_as_uint(av), false, false);
;                   const float other = (g4 & 1) ? __uint_as_float(rr[0]) : __uint_as_float(rr[1]);
;                   float cc = 1.f, sg = 0.f;
;                   if (lat) { const f32x2 cs = rope[((g4 & 2) ? pcol : prow) * 8 + j]; cc = cs.x; sg = (g4 & 1) ? cs.y : -cs.y; }
;                   x[2][j] = av * cc + other * sg; }
	v_and_b32_e32 v139, 0xffff0000, v6
	s_nop 0
	v_permlane16_swap_b32_e32 v80, v8
	v_lshlrev_b32_e32 v138, 16, v6
	v_mul_f32_e32 v6, v139, v139
	v_add_f32_e32 v161, v80, v8
	v_pk_fma_f32 v[80:81], v[138:139], v[138:139], v[6:7] op_sel_hi:[1,1,0]
	v_mul_f32_e32 v6, v129, v129
	v_pk_fma_f32 v[80:81], v[128:129], v[128:129], v[80:81]
	global_load_dwordx4 v[54:57], v162, s[44:45] offset:16
	global_load_dwordx4 v[62:65], v162, s[44:45]
	v_pk_add_f32 v[80:81], v[6:7], v[80:81] op_sel_hi:[0,1]
	v_pk_fma_f32 v[80:81], v[126:127], v[126:127], v[80:81]
	v_mul_f32_e32 v6, v127, v127
	v_pk_add_f32 v[80:81], v[6:7], v[80:81] op_sel_hi:[0,1]
	v_pk_fma_f32 v[80:81], v[124:125], v[124:125], v[80:81]
	v_mul_f32_e32 v6, v125, v125
	v_and_b32_e32 v121, 0xffff0000, v123
	v_lshlrev_b32_e32 v120, 16, v123
	v_and_b32_e32 v123, 0xffff0000, v122
	v_lshlrev_b32_e32 v122, 16, v122
	v_pk_add_f32 v[80:81], v[6:7], v[80:81] op_sel_hi:[0,1]
	v_pk_fma_f32 v[80:81], v[122:123], v[122:123], v[80:81]
	v_mul_f32_e32 v6, v123, v123
	v_pk_add_f32 v[80:81], v[6:7], v[80:81] op_sel_hi:[0,1]
	v_pk_fma_f32 v[80:81], v[120:121], v[120:121], v[80:81]
	v_mul_f32_e32 v6, v121, v121
	v_pk_add_f32 v[80:81], v[6:7], v[80:81] op_sel_hi:[0,1]
	v_pk_fma_f32 v[80:81], v[118:119], v[118:119], v[80:81]
	v_mul_f32_e32 v6, v119, v119
	v_pk_add_f32 v[80:81], v[6:7], v[80:81] op_sel_hi:[0,1]
	v_pk_fma_f32 v[80:81], v[116:117], v[116:117], v[80:81]
	v_mul_f32_e32 v6, v117, v117
	v_pk_add_f32 v[80:81], v[6:7], v[80:81] op_sel_hi:[0,1]
	v_mov_b32_e32 v6, v80
	s_nop 1
	v_permlane16_swap_b32_e32 v80, v6
	v_add_f32_e32 v145, v80, v6
	global_load_dwordx4 v[80:83], v162, s[44:45] offset:272
	global_load_dwordx4 v[84:87], v162, s[44:45] offset:256
	s_waitcnt vmcnt(25)
	v_and_b32_e32 v201, 0xffff0000, v2
	v_lshlrev_b32_e32 v200, 16, v2
	v_mul_f32_e32 v2, v201, v201
	s_waitcnt vmcnt(20)
	v_and_b32_e32 v213, 0xffff0000, v13
	v_lshlrev_b32_e32 v212, 16, v13
	v_and_b32_e32 v217, 0xffff0000, v12
	v_lshlrev_b32_e32 v216, 16, v12
	v_and_b32_e32 v13, 0xffff0000, v3
	v_lshlrev_b32_e32 v12, 16, v3
	v_pk_fma_f32 v[2:3], v[200:201], v[200:201], v[2:3] op_sel_hi:[1,1,0]
	v_cndmask_b32_e64 v219, v115, -v115, vcc
	v_cndmask_b32_e64 v218, v113, -v113, vcc
	v_mov_b32_e32 v113, v114
	s_waitcnt vmcnt(14)
	v_cndmask_b32_e64 v115, v79, -v79, vcc
	v_cndmask_b32_e64 v114, v77, -v77, vcc
	v_mov_b32_e32 v77, v78
	s_waitcnt vmcnt(9)
	v_cndmask_b32_e64 v79, v17, -v17, vcc
	v_cndmask_b32_e64 v78, v15, -v15, vcc
	v_mov_b32_e32 v15, v16
	v_and_b32_e32 v17, 0xffff0000, v4
	v_lshlrev_b32_e32 v16, 16, v4
	v_pk_fma_f32 v[2:3], v[12:13], v[12:13], v[2:3]
	v_mul_f32_e32 v4, v13, v13
	v_pk_add_f32 v[2:3], v[4:5], v[2:3] op_sel_hi:[0,1]
	v_pk_fma_f32 v[2:3], v[16:17], v[16:17], v[2:3]
	v_mul_f32_e32 v4, v17, v17
	v_and_b32_e32 v221, 0xffff0000, v5
	v_lshlrev_b32_e32 v220, 16, v5
	v_pk_add_f32 v[2:3], v[4:5], v[2:3] op_sel_hi:[0,1]
	v_pk_fma_f32 v[2:3], v[220:221], v[220:221], v[2:3]
	v_mul_f32_e32 v4, v221, v221
	v_pk_add_f32 v[2:3], v[4:5], v[2:3] op_sel_hi:[0,1]
	v_mov_b32_e32 v3, v2
	s_nop 1
	v_permlane16_swap_b32_e32 v2, v3
	v_add_f32_e32 v6, v2, v3
	v_mov_b32_e32 v8, v6
	s_nop 1
	v_permlane32_swap_b32_e32 v6, v8
	v_pk_add_f32 v[2:3], v[6:7], v[8:9]
	v_mov_b32_e32 v147, v145
	v_pk_fma_f32 v[6:7], v[2:3], s[6:7], v[170:171] op_sel_hi:[1,1,0]
	s_nop 0
	v_permlane32_swap_b32_e32 v145, v147
	v_mul_f32_e32 v2, 0x4b800000, v7
	v_cmp_gt_f32_e64 s[4:5], s95, v7
	v_cndmask_b32_e64 v215, v95, -v95, vcc
	v_cndmask_b32_e64 v214, v93, -v93, vcc
	v_cndmask_b32_e64 v2, v7, v2, s[4:5]
	v_rsq_f32_e32 v2, v2
	v_mov_b32_e32 v93, v94
	s_waitcnt vmcnt(8)
	v_cndmask_b32_e64 v95, v23, -v23, vcc
	v_cndmask_b32_e64 v94, v21, -v21, vcc
	v_mul_f32_e32 v3, 0x45800000, v2
	v_cndmask_b32_e64 v144, v2, v3, s[4:5]
	s_waitcnt vmcnt(5)
	v_pk_mul_f32 v[2:3], v[144:145], v[40:41] op_sel_hi:[0,1]
	v_pk_mul_f32 v[2:3], v[2:3], v[174:175]
	v_pk_mul_f32 v[4:5], v[144:145], v[38:39] op_sel_hi:[0,1]
	v_pk_mul_f32 v[2:3], v[2:3], s[82:83] op_sel_hi:[1,0]
	v_pk_mul_f32 v[8:9], v[4:5], v[176:177]
	v_cvt_pk_bf16_f32 v5, v2, v3
	v_pk_mul_f32 v[2:3], v[8:9], s[82:83] op_sel_hi:[1,0]
	s_waitcnt vmcnt(4)
	v_pk_mul_f32 v[8:9], v[42:43], v[144:145] op_sel_hi:[1,0]
	v_cvt_pk_bf16_f32 v4, v2, v3
	v_pk_mul_f32 v[2:3], v[144:145], v[44:45] op_sel_hi:[0,1]
	v_pk_mul_f32 v[2:3], v[2:3], v[178:179]
	v_pk_mul_f32 v[8:9], v[8:9], v[184:185]
	v_pk_mul_f32 v[2:3], v[2:3], s[82:83] op_sel_hi:[1,0]
	v_pk_mul_f32 v[8:9], v[8:9], s[82:83] op_sel_hi:[1,0]
	v_mov_b32_e32 v21, v22
	v_cvt_pk_bf16_f32 v3, v2, v3
	v_cvt_pk_bf16_f32 v2, v8, v9
	s_waitcnt vmcnt(3)
	v_pk_mul_f32 v[8:9], v[56:57], v[144:145] op_sel_hi:[1,0]
	v_pk_mul_f32 v[22:23], v[54:55], v[144:145] op_sel_hi:[1,0]
	v_pk_mul_f32 v[8:9], v[8:9], v[186:187]
	v_pk_mul_f32 v[22:23], v[22:23], v[188:189]
	v_pk_mul_f32 v[8:9], v[8:9], s[82:83] op_sel_hi:[1,0]
	v_pk_mul_f32 v[22:23], v[22:23], s[82:83] op_sel_hi:[1,0]
	v_and_b32_e32 v165, 0xffff0000, v37
	v_lshlrev_b32_e32 v164, 16, v37
	v_and_b32_e32 v173, 0xffff0000, v36
	v_lshlrev_b32_e32 v172, 16, v36
	v_cndmask_b32_e64 v37, v107, -v107, vcc
	v_cndmask_b32_e64 v36, v105, -v105, vcc
	v_mov_b32_e32 v105, v106
	v_and_b32_e32 v107, 0xffff0000, v11
	v_lshlrev_b32_e32 v106, 16, v11
	v_cvt_pk_bf16_f32 v9, v8, v9
	v_cvt_pk_bf16_f32 v8, v22, v23
	s_waitcnt vmcnt(2)
; template <int DQK, int DV, bool LEAD> ...
;     ...
;           const float rn = rsqrtf(sn * (1.f / 64.f) + EPS);
; #pragma unroll
;           for (int ds = 0; ds < 2; ++ds)
; #pragma unroll
;               for (int j = 0; j < 8; ++j) x[ds][j] *= rn * qgain[32 * ds + 8 * g4 + j];
;           if constexpr (DQK == 64) {
; #pragma unroll
;               for (int ds = 0; ds < 2; ++ds)
; #pragma unroll
;                   for (int j = 0; j < 8; ++j) {
;                       auto rr = __builtin_amdgcn_permlane32_swap(__float_as_uint(x[ds][j]), __float_as_uint(x[ds][j]), false, false);
;                       const float other = hi ? __uint_as_float(rr[0]) : __uint_as_float(rr[1]);
;                       float cc = 1.f, sg = 0.f;
;                       if (lat) { const f32x2 cs = rope[(ds ? pcol : prow) * 16 + 8 * (g4 & 1) + j]; cc = cs.x; sg = hi ? cs.y : -cs.y; }
;                       x[ds][j] = x[ds][j] * cc + other * sg; }
;           } else {
;               float sr = 0.f;
; #pragma unroll
;               for (int j = 0; j < 8; ++j) sr += x[2][j] * x[2][j];
;               sr = lanes4_sum(sr);
;               const float rq = rsqrtf(sr * (1.f / 32.f) + EPS);
; #pragma unroll
;               for (int j = 0; j < 8; ++j) { const float av = x[2][j] * rq * qgain[64 + 8 * g4 + j];
;                   auto rr = __builtin_amdgcn_permlane16_swap(__float_as_uint(av), __float_as_uint(av), false, false);
;                   const float other = (g4 & 1) ? __uint_as_float(rr[0]) : __uint_as_float(rr[1]);
;                   float cc = 1.f, sg = 0.f;
;                   if (lat) { const f32x2 cs = rope[((g4 & 2) ? pcol : prow) * 8 + j]; cc = cs.x; sg = (g4 & 1) ? cs.y : -cs.y; }
;                   x[2][j] = av * cc + other * sg; }
	v_pk_mul_f32 v[22:23], v[64:65], v[144:145] op_sel_hi:[1,0]
	v_mul_f32_e32 v11, 0x4b800000, v6
	v_cmp_gt_f32_e64 s[4:5], s95, v6
	v_pk_mul_f32 v[22:23], v[22:23], v[210:211]
	v_cndmask_b32_e64 v209, v99, -v99, vcc
	v_cndmask_b32_e64 v6, v6, v11, s[4:5]
	v_pk_mul_f32 v[22:23], v[22:23], s[82:83] op_sel_hi:[1,0]
	v_rsq_f32_e32 v11, v6
	v_cvt_pk_bf16_f32 v7, v22, v23
	v_cndmask_b32_e64 v23, v27, -v27, vcc
	v_cndmask_b32_e64 v22, v25, -v25, vcc
	v_mov_b32_e32 v25, v26
	v_pk_mul_f32 v[26:27], v[62:63], v[144:145] op_sel_hi:[1,0]
	v_cndmask_b32_e64 v208, v97, -v97, vcc
	v_pk_mul_f32 v[26:27], v[26:27], v[190:191]
	v_mov_b32_e32 v97, v98
	v_pk_mul_f32 v[26:27], v[26:27], s[82:83] op_sel_hi:[1,0]
	v_and_b32_e32 v99, 0xffff0000, v49
	v_cvt_pk_bf16_f32 v6, v26, v27
	v_mul_f32_e32 v26, 0x45800000, v11
	v_cndmask_b32_e64 v26, v11, v26, s[4:5]
	v_pk_mul_f32 v[176:177], v[26:27], v[12:13] op_sel_hi:[0,1]
	v_pk_mul_f32 v[12:13], v[26:27], v[220:221] op_sel_hi:[0,1]
	s_waitcnt vmcnt(1)
	v_pk_mul_f32 v[12:13], v[12:13], v[82:83]
	v_lshlrev_b32_e32 v98, 16, v49
	v_cndmask_b32_e64 v199, v111, -v111, vcc
	v_cndmask_b32_e64 v198, v109, -v109, vcc
	v_mov_b32_e32 v109, v110
	v_and_b32_e32 v111, 0xffff0000, v48
	v_lshlrev_b32_e32 v110, 16, v48
	v_and_b32_e32 v49, 0xffff0000, v35
	v_lshlrev_b32_e32 v48, 16, v35
	v_pk_mul_f32 v[174:175], v[26:27], v[200:201] op_sel_hi:[0,1]
	v_pk_mul_f32 v[16:17], v[26:27], v[16:17] op_sel_hi:[0,1]
	v_mov_b32_e32 v11, v12
	v_mov_b32_e32 v26, v12
	v_mov_b32_e32 v27, v13
	v_mov_b32_e32 v35, v13
	v_permlane16_swap_b32_e32 v11, v26
	s_nop 0
	v_permlane16_swap_b32_e32 v27, v35
	v_cndmask_b32_e32 v27, v27, v35, vcc
	v_cndmask_b32_e32 v26, v11, v26, vcc
	v_pk_mul_f32 v[26:27], v[218:219], v[26:27]
	v_pk_mul_f32 v[16:17], v[16:17], v[80:81]
	v_pk_fma_f32 v[12:13], v[12:13], v[112:113], v[26:27]
	v_mov_b32_e32 v11, v16
	v_pk_mul_f32 v[12:13], v[12:13], s[82:83] op_sel_hi:[1,0]
	v_mov_b32_e32 v26, v17
	v_cvt_pk_bf16_f32 v13, v12, v13
	v_mov_b32_e32 v12, v16
	v_mov_b32_e32 v27, v17
	s_nop 0
	v_permlane16_swap_b32_e32 v11, v12
	v_permlane16_swap_b32_e32 v26, v27
	v_cndmask_b32_e32 v27, v26, v27, vcc
	v_cndmask_b32_e32 v26, v11, v12, vcc
	v_pk_mul_f32 v[26:27], v[198:199], v[26:27]
	v_cndmask_b32_e64 v178, v101, -v101, vcc
	v_pk_fma_f32 v[16:17], v[16:17], v[108:109], v[26:27]
	v_mov_b32_e32 v101, v102
	v_pk_mul_f32 v[16:17], v[16:17], s[82:83] op_sel_hi:[1,0]
	v_cndmask_b32_e64 v179, v103, -v103, vcc
	v_cvt_pk_bf16_f32 v12, v16, v17
	s_waitcnt vmcnt(0)
	v_pk_mul_f32 v[16:17], v[86:87], v[176:177]
	v_mov_b32_e32 v183, v181
	v_mov_b32_e32 v11, v16
	v_mov_b32_e32 v26, v16
	v_mov_b32_e32 v27, v17
	v_mov_b32_e32 v35, v17
	v_permlane16_swap_b32_e32 v11, v26
	s_nop 0
	v_permlane16_swap_b32_e32 v27, v35
	v_cndmask_b32_e32 v27, v27, v35, vcc
	v_cndmask_b32_e32 v26, v11, v26, vcc
	v_pk_mul_f32 v[26:27], v[36:37], v[26:27]
	v_and_b32_e32 v37, 0xffff0000, v10
	v_pk_fma_f32 v[16:17], v[104:105], v[16:17], v[26:27]
	v_permlane32_swap_b32_e32 v181, v183
	v_pk_mul_f32 v[16:17], v[16:17], s[82:83] op_sel_hi:[1,0]
	v_cndmask_b32_e64 v169, v73, -v73, vcc
	v_cvt_pk_bf16_f32 v11, v16, v17
	v_pk_mul_f32 v[16:17], v[84:85], v[174:175]
	v_cndmask_b32_e64 v168, v71, -v71, vcc
	v_mov_b32_e32 v26, v16
	v_mov_b32_e32 v35, v16
	v_mov_b32_e32 v27, v17
	v_mov_b32_e32 v36, v17
	v_permlane16_swap_b32_e32 v26, v35
	s_nop 0
	v_permlane16_swap_b32_e32 v27, v36
	v_cndmask_b32_e32 v27, v27, v36, vcc
	v_cndmask_b32_e32 v26, v26, v35, vcc
	v_pk_mul_f32 v[16:17], v[100:101], v[16:17]
	v_lshlrev_b32_e32 v36, 16, v10
	v_mul_f32_e32 v10, v37, v37
	v_pk_fma_f32 v[16:17], v[178:179], v[26:27], v[16:17]
	v_pk_fma_f32 v[26:27], v[36:37], v[36:37], v[10:11] op_sel_hi:[1,1,0]
	v_mul_f32_e32 v10, v107, v107
	v_pk_fma_f32 v[26:27], v[106:107], v[106:107], v[26:27]
	v_pk_mul_f32 v[16:17], v[16:17], s[82:83] op_sel_hi:[1,0]
	v_pk_add_f32 v[26:27], v[10:11], v[26:27] op_sel_hi:[0,1]
	v_pk_fma_f32 v[26:27], v[216:217], v[216:217], v[26:27]
	v_mul_f32_e32 v10, v217, v217
	v_pk_add_f32 v[26:27], v[10:11], v[26:27] op_sel_hi:[0,1]
	v_pk_fma_f32 v[26:27], v[212:213], v[212:213], v[26:27]
	v_mul_f32_e32 v10, v213, v213
	v_pk_add_f32 v[26:27], v[10:11], v[26:27] op_sel_hi:[0,1]
	v_mov_b32_e32 v10, v26
	s_nop 1
	v_permlane16_swap_b32_e32 v26, v10
	v_add_f32_e32 v180, v26, v10
	v_mov_b32_e32 v182, v180
	s_nop 1
	v_permlane32_swap_b32_e32 v180, v182
	v_pk_add_f32 v[26:27], v[180:181], v[182:183]
	v_mov_b32_e32 v71, v72
	v_pk_fma_f32 v[26:27], v[26:27], s[6:7], v[170:171] op_sel_hi:[1,1,0]
	v_cndmask_b32_e64 v73, v91, -v91, vcc
	v_mul_f32_e32 v10, 0x4b800000, v27
	v_cmp_gt_f32_e64 s[4:5], s95, v27
	v_mul_f32_e32 v35, 0x4b800000, v26
	v_cndmask_b32_e64 v72, v89, -v89, vcc
	v_cndmask_b32_e64 v10, v27, v10, s[4:5]
	v_rsq_f32_e32 v27, v10
	v_cvt_pk_bf16_f32 v10, v16, v17
	v_mov_b32_e32 v89, v90
	v_cndmask_b32_e64 v91, v69, -v69, vcc
	v_mul_f32_e32 v16, 0x45800000, v27
	v_cndmask_b32_e64 v102, v27, v16, s[4:5]
	v_pk_mul_f32 v[16:17], v[40:41], v[102:103] op_sel_hi:[1,0]
	v_cmp_gt_f32_e64 s[4:5], s95, v26
	v_pk_mul_f32 v[16:17], v[16:17], v[18:19]
	v_pk_mul_f32 v[104:105], v[54:55], v[102:103] op_sel_hi:[1,0]
	v_pk_mul_f32 v[16:17], v[16:17], s[82:83] op_sel_hi:[1,0]
	v_cndmask_b32_e64 v26, v26, v35, s[4:5]
	v_cvt_pk_bf16_f32 v19, v16, v17
	v_pk_mul_f32 v[16:17], v[38:39], v[102:103] op_sel_hi:[1,0]
	v_pk_mul_f32 v[104:105], v[104:105], v[156:157]
	v_pk_mul_f32 v[16:17], v[16:17], v[28:29]
	v_pk_mul_f32 v[28:29], v[42:43], v[102:103] op_sel_hi:[1,0]
	v_pk_mul_f32 v[16:17], v[16:17], s[82:83] op_sel_hi:[1,0]
	v_pk_mul_f32 v[28:29], v[28:29], v[152:153]
	v_cvt_pk_bf16_f32 v18, v16, v17
; __device__ __forceinline__ unsigned cvtpk(float lo, float hi) { f32x2 v = {lo, hi}; bf16x2_t b = __builtin_convertvector(v, bf16x2_t); return __builtin_bit_cast(unsigned, b); }
; template <int DQK, int DV, bool LEAD> ...
;     ...
;           const float rn = rsqrtf(sn * (1.f / 64.f) + EPS);
; #pragma unroll
;           for (int ds = 0; ds < 2; ++ds)
; #pragma unroll
;               for (int j = 0; j < 8; ++j) x[ds][j] *= rn * qgain[32 * ds + 8 * g4 + j];
;           if constexpr (DQK == 64) {
; #pragma unroll
;               for (int ds = 0; ds < 2; ++ds)
; #pragma unroll
;                   for (int j = 0; j < 8; ++j) {
;                       auto rr = __builtin_amdgcn_permlane32_swap(__float_as_uint(x[ds][j]), __float_as_uint(x[ds][j]), false, false);
;                       const float other = hi ? __uint_as_float(rr[0]) : __uint_as_float(rr[1]);
;                       float cc = 1.f, sg = 0.f;
;                       if (lat) { const f32x2 cs = rope[(ds ? pcol : prow) * 16 + 8 * (g4 & 1) + j]; cc = cs.x; sg = hi ? cs.y : -cs.y; }
;                       x[ds][j] = x[ds][j] * cc + other * sg; }
;           } else {
;               float sr = 0.f;
; #pragma unroll
;               for (int j = 0; j < 8; ++j) sr += x[2][j] * x[2][j];
;               sr = lanes4_sum(sr);
;               const float rq = rsqrtf(sr * (1.f / 32.f) + EPS);
; #pragma unroll
;               for (int j = 0; j < 8; ++j) { const float av = x[2][j] * rq * qgain[64 + 8 * g4 + j];
;                   auto rr = __builtin_amdgcn_permlane16_swap(__float_as_uint(av), __float_as_uint(av), false, false);
;                   const float other = (g4 & 1) ? __uint_as_float(rr[0]) : __uint_as_float(rr[1]);
;                   float cc = 1.f, sg = 0.f;
;                   if (lat) { const f32x2 cs = rope[((g4 & 2) ? pcol : prow) * 8 + j]; cc = cs.x; sg = (g4 & 1) ? cs.y : -cs.y; }
;                   x[2][j] = av * cc + other * sg; }
;           }
; #pragma unroll
;           for (int ds = 0; ds < NDS; ++ds) { u32x4 w;
; #pragma unroll
;               for (int i = 0; i < 4; ++i) w[i] = cvtpk(x[ds][2 * i] * c2, x[ds][2 * i + 1] * c2);
;               qf[qb * NDS + ds] = __builtin_bit_cast(bf16x8, w); }
	v_pk_mul_f32 v[16:17], v[44:45], v[102:103] op_sel_hi:[1,0]
	v_pk_mul_f32 v[28:29], v[28:29], s[82:83] op_sel_hi:[1,0]
	v_pk_mul_f32 v[16:17], v[16:17], v[150:151]
	v_rsq_f32_e32 v35, v26
	v_pk_mul_f32 v[16:17], v[16:17], s[82:83] op_sel_hi:[1,0]
	v_pk_mul_f32 v[104:105], v[104:105], s[82:83] op_sel_hi:[1,0]
	v_cvt_pk_bf16_f32 v17, v16, v17
	v_cvt_pk_bf16_f32 v16, v28, v29
	v_pk_mul_f32 v[28:29], v[56:57], v[102:103] op_sel_hi:[1,0]
	v_cndmask_b32_e64 v90, v67, -v67, vcc
	v_pk_mul_f32 v[28:29], v[28:29], v[154:155]
	v_mov_b32_e32 v67, v68
	v_pk_mul_f32 v[28:29], v[28:29], s[82:83] op_sel_hi:[1,0]
	v_and_b32_e32 v69, 0xffff0000, v47
	v_cvt_pk_bf16_f32 v29, v28, v29
	v_cvt_pk_bf16_f32 v28, v104, v105
	v_pk_mul_f32 v[104:105], v[64:65], v[102:103] op_sel_hi:[1,0]
	v_pk_mul_f32 v[102:103], v[62:63], v[102:103] op_sel_hi:[1,0]
	v_lshlrev_b32_e32 v68, 16, v47
	v_pk_mul_f32 v[102:103], v[102:103], v[166:167]
	v_pk_mul_f32 v[104:105], v[104:105], v[158:159]
	v_pk_mul_f32 v[102:103], v[102:103], s[82:83] op_sel_hi:[1,0]
	v_mul_f32_e32 v47, 0x45800000, v35
	v_pk_mul_f32 v[104:105], v[104:105], s[82:83] op_sel_hi:[1,0]
	v_cvt_pk_bf16_f32 v26, v102, v103
	v_cndmask_b32_e64 v102, v35, v47, s[4:5]
	v_cvt_pk_bf16_f32 v27, v104, v105
	v_pk_mul_f32 v[104:105], v[102:103], v[36:37] op_sel_hi:[0,1]
	v_pk_mul_f32 v[36:37], v[102:103], v[212:213] op_sel_hi:[0,1]
	v_pk_mul_f32 v[36:37], v[82:83], v[36:37]
	v_cndmask_b32_e64 v101, v61, -v61, vcc
	v_cndmask_b32_e64 v100, v59, -v59, vcc
	v_mov_b32_e32 v35, v36
	v_mov_b32_e32 v47, v36
	v_mov_b32_e32 v59, v37
	v_mov_b32_e32 v61, v37
	v_permlane16_swap_b32_e32 v35, v47
	s_nop 0
	v_permlane16_swap_b32_e32 v59, v61
	v_pk_mul_f32 v[106:107], v[102:103], v[106:107] op_sel_hi:[0,1]
	v_pk_mul_f32 v[108:109], v[102:103], v[216:217] op_sel_hi:[0,1]
	v_cndmask_b32_e32 v103, v59, v61, vcc
	v_cndmask_b32_e32 v102, v35, v47, vcc
	v_pk_mul_f32 v[102:103], v[208:209], v[102:103]
	v_mov_b32_e32 v163, v161
	v_pk_fma_f32 v[36:37], v[36:37], v[96:97], v[102:103]
	v_pk_mul_f32 v[96:97], v[80:81], v[108:109]
	v_pk_mul_f32 v[36:37], v[36:37], s[82:83] op_sel_hi:[1,0]
	v_mov_b32_e32 v35, v96
	v_cvt_pk_bf16_f32 v37, v36, v37
	v_mov_b32_e32 v36, v96
	v_mov_b32_e32 v47, v97
	v_mov_b32_e32 v59, v97
	v_permlane16_swap_b32_e32 v35, v36
	s_nop 0
	v_permlane16_swap_b32_e32 v47, v59
	v_cndmask_b32_e32 v103, v47, v59, vcc
	v_cndmask_b32_e32 v102, v35, v36, vcc
	v_pk_mul_f32 v[102:103], v[214:215], v[102:103]
	v_permlane32_swap_b32_e32 v161, v163
	v_pk_fma_f32 v[92:93], v[92:93], v[96:97], v[102:103]
	s_nop 0
	v_pk_mul_f32 v[92:93], v[92:93], s[82:83] op_sel_hi:[1,0]
	s_nop 0
	v_cvt_pk_bf16_f32 v36, v92, v93
	v_pk_mul_f32 v[92:93], v[86:87], v[106:107]
	s_nop 0
	v_mov_b32_e32 v35, v92
	v_mov_b32_e32 v47, v92
	v_mov_b32_e32 v59, v93
	v_mov_b32_e32 v61, v93
	v_permlane16_swap_b32_e32 v35, v47
	s_nop 0
	v_permlane16_swap_b32_e32 v59, v61
	v_cndmask_b32_e32 v97, v59, v61, vcc
	v_cndmask_b32_e32 v96, v35, v47, vcc
	v_pk_mul_f32 v[88:89], v[88:89], v[92:93]
	v_cndmask_b32_e64 v92, v51, -v51, vcc
	v_pk_fma_f32 v[72:73], v[72:73], v[96:97], v[88:89]
	v_cndmask_b32_e64 v93, v53, -v53, vcc
	v_pk_mul_f32 v[72:73], v[72:73], s[82:83] op_sel_hi:[1,0]
	s_nop 0
	v_cvt_pk_bf16_f32 v35, v72, v73
	v_pk_mul_f32 v[72:73], v[84:85], v[104:105]
	s_nop 0
	v_mov_b32_e32 v47, v72
	v_mov_b32_e32 v59, v72
	v_mov_b32_e32 v61, v73
	v_mov_b32_e32 v88, v73
	v_permlane16_swap_b32_e32 v47, v59
	s_nop 0
	v_permlane16_swap_b32_e32 v61, v88
	v_cndmask_b32_e32 v89, v61, v88, vcc
	v_cndmask_b32_e32 v88, v47, v59, vcc
	v_mov_b32_e32 v59, v60
	v_pk_mul_f32 v[58:59], v[58:59], v[72:73]
	s_nop 0
	v_pk_fma_f32 v[58:59], v[100:101], v[88:89], v[58:59]
	v_and_b32_e32 v89, 0xffff0000, v34
	v_lshlrev_b32_e32 v88, 16, v34
	v_mul_f32_e32 v34, v89, v89
	v_pk_fma_f32 v[60:61], v[88:89], v[88:89], v[34:35] op_sel_hi:[1,1,0]
	v_mul_f32_e32 v34, v49, v49
	v_pk_fma_f32 v[60:61], v[48:49], v[48:49], v[60:61]
	v_pk_mul_f32 v[58:59], v[58:59], s[82:83] op_sel_hi:[1,0]
	v_pk_add_f32 v[60:61], v[34:35], v[60:61] op_sel_hi:[0,1]
	v_pk_fma_f32 v[60:61], v[172:173], v[172:173], v[60:61]
	v_mul_f32_e32 v34, v173, v173
	v_pk_add_f32 v[60:61], v[34:35], v[60:61] op_sel_hi:[0,1]
	v_pk_fma_f32 v[60:61], v[164:165], v[164:165], v[60:61]
	v_mul_f32_e32 v34, v165, v165
	v_pk_add_f32 v[60:61], v[34:35], v[60:61] op_sel_hi:[0,1]
	v_mov_b32_e32 v34, v60
	s_nop 1
	v_permlane16_swap_b32_e32 v60, v34
	v_add_f32_e32 v160, v60, v34
	v_mov_b32_e32 v162, v160
	s_nop 1
	v_permlane32_swap_b32_e32 v160, v162
	v_pk_add_f32 v[60:61], v[160:161], v[162:163]
	s_nop 0
	v_pk_fma_f32 v[72:73], v[60:61], s[6:7], v[170:171] op_sel_hi:[1,1,0]
	s_nop 0
	v_mul_f32_e32 v34, 0x4b800000, v73
	v_cmp_gt_f32_e64 s[4:5], s95, v73
	s_nop 1
	v_cndmask_b32_e64 v34, v73, v34, s[4:5]
	v_rsq_f32_e32 v47, v34
	v_cvt_pk_bf16_f32 v34, v58, v59
	v_mul_f32_e32 v51, 0x45800000, v47
	v_cndmask_b32_e64 v96, v47, v51, s[4:5]
	v_pk_mul_f32 v[58:59], v[40:41], v[96:97] op_sel_hi:[1,0]
	v_mul_f32_e32 v47, 0x4b800000, v72
	v_pk_mul_f32 v[58:59], v[58:59], v[74:75]
	v_pk_mul_f32 v[74:75], v[42:43], v[96:97] op_sel_hi:[1,0]
	v_pk_mul_f32 v[58:59], v[58:59], s[82:83] op_sel_hi:[1,0]
	v_pk_mul_f32 v[74:75], v[74:75], v[134:135]
	v_cvt_pk_bf16_f32 v61, v58, v59
	v_pk_mul_f32 v[58:59], v[38:39], v[96:97] op_sel_hi:[1,0]
	v_pk_mul_f32 v[74:75], v[74:75], s[82:83] op_sel_hi:[1,0]
	v_pk_mul_f32 v[58:59], v[58:59], v[130:131]
	v_cmp_gt_f32_e64 s[4:5], s95, v72
	v_pk_mul_f32 v[58:59], v[58:59], s[82:83] op_sel_hi:[1,0]
	v_pk_mul_f32 v[100:101], v[54:55], v[96:97] op_sel_hi:[1,0]
	v_cvt_pk_bf16_f32 v60, v58, v59
	v_pk_mul_f32 v[58:59], v[44:45], v[96:97] op_sel_hi:[1,0]
; __device__ __forceinline__ unsigned cvtpk(float lo, float hi) { f32x2 v = {lo, hi}; bf16x2_t b = __builtin_convertvector(v, bf16x2_t); return __builtin_bit_cast(unsigned, b); }
; template <int DQK, int DV, bool LEAD> ...
;     ...
;           const float rn = rsqrtf(sn * (1.f / 64.f) + EPS);
; #pragma unroll
;           for (int ds = 0; ds < 2; ++ds)
; #pragma unroll
;               for (int j = 0; j < 8; ++j) x[ds][j] *= rn * qgain[32 * ds + 8 * g4 + j];
;           if constexpr (DQK == 64) {
; #pragma unroll
;               for (int ds = 0; ds < 2; ++ds)
; #pragma unroll
;                   for (int j = 0; j < 8; ++j) {
;                       auto rr = __builtin_amdgcn_permlane32_swap(__float_as_uint(x[ds][j]), __float_as_uint(x[ds][j]), false, false);
;                       const float other = hi ? __uint_as_float(rr[0]) : __uint_as_float(rr[1]);
;                       float cc = 1.f, sg = 0.f;
;                       if (lat) { const f32x2 cs = rope[(ds ? pcol : prow) * 16 + 8 * (g4 & 1) + j]; cc = cs.x; sg = hi ? cs.y : -cs.y; }
;                       x[ds][j] = x[ds][j] * cc + other * sg; }
;           } else {
;               float sr = 0.f;
; #pragma unroll
;               for (int j = 0; j < 8; ++j) sr += x[2][j] * x[2][j];
;               sr = lanes4_sum(sr);
;               const float rq = rsqrtf(sr * (1.f / 32.f) + EPS);
; #pragma unroll
;               for (int j = 0; j < 8; ++j) { const float av = x[2][j] * rq * qgain[64 + 8 * g4 + j];
;                   auto rr = __builtin_amdgcn_permlane16_swap(__float_as_uint(av), __float_as_uint(av), false, false);
;                   const float other = (g4 & 1) ? __uint_as_float(rr[0]) : __uint_as_float(rr[1]);
;                   float cc = 1.f, sg = 0.f;
;                   if (lat) { const f32x2 cs = rope[((g4 & 2) ? pcol : prow) * 8 + j]; cc = cs.x; sg = (g4 & 1) ? cs.y : -cs.y; }
;                   x[2][j] = av * cc + other * sg; }
;           }
; #pragma unroll
;           for (int ds = 0; ds < NDS; ++ds) { u32x4 w;
; #pragma unroll
;               for (int i = 0; i < 4; ++i) w[i] = cvtpk(x[ds][2 * i] * c2, x[ds][2 * i + 1] * c2);
;               qf[qb * NDS + ds] = __builtin_bit_cast(bf16x8, w); }
	v_cndmask_b32_e64 v47, v72, v47, s[4:5]
	v_pk_mul_f32 v[58:59], v[58:59], v[132:133]
	v_pk_mul_f32 v[100:101], v[100:101], v[140:141]
	v_pk_mul_f32 v[58:59], v[58:59], s[82:83] op_sel_hi:[1,0]
	v_rsq_f32_e32 v47, v47
	v_cvt_pk_bf16_f32 v59, v58, v59
	v_cvt_pk_bf16_f32 v58, v74, v75
	v_pk_mul_f32 v[74:75], v[56:57], v[96:97] op_sel_hi:[1,0]
	v_pk_mul_f32 v[100:101], v[100:101], s[82:83] op_sel_hi:[1,0]
	v_pk_mul_f32 v[74:75], v[74:75], v[136:137]
	v_mul_f32_e32 v51, 0x45800000, v47
	v_pk_mul_f32 v[74:75], v[74:75], s[82:83] op_sel_hi:[1,0]
	s_nop 0
	v_cvt_pk_bf16_f32 v75, v74, v75
	v_cvt_pk_bf16_f32 v74, v100, v101
	v_pk_mul_f32 v[100:101], v[64:65], v[96:97] op_sel_hi:[1,0]
	v_pk_mul_f32 v[96:97], v[62:63], v[96:97] op_sel_hi:[1,0]
	v_pk_mul_f32 v[100:101], v[100:101], v[142:143]
	v_pk_mul_f32 v[96:97], v[96:97], v[148:149]
	v_pk_mul_f32 v[100:101], v[100:101], s[82:83] op_sel_hi:[1,0]
	v_pk_mul_f32 v[96:97], v[96:97], s[82:83] op_sel_hi:[1,0]
	v_cvt_pk_bf16_f32 v73, v100, v101
	v_cvt_pk_bf16_f32 v72, v96, v97
	v_cndmask_b32_e64 v96, v47, v51, s[4:5]
	v_pk_mul_f32 v[100:101], v[96:97], v[48:49] op_sel_hi:[0,1]
	v_pk_mul_f32 v[48:49], v[96:97], v[164:165] op_sel_hi:[0,1]
	v_pk_mul_f32 v[48:49], v[82:83], v[48:49]
	v_pk_mul_f32 v[88:89], v[96:97], v[88:89] op_sel_hi:[0,1]
	v_pk_mul_f32 v[102:103], v[96:97], v[172:173] op_sel_hi:[0,1]
	v_mov_b32_e32 v47, v48
	v_mov_b32_e32 v51, v48
	v_mov_b32_e32 v53, v49
	v_mov_b32_e32 v96, v49
	v_permlane16_swap_b32_e32 v47, v51
	s_nop 0
	v_permlane16_swap_b32_e32 v53, v96
	v_cndmask_b32_e32 v97, v53, v96, vcc
	v_cndmask_b32_e32 v96, v47, v51, vcc
	v_pk_mul_f32 v[96:97], v[114:115], v[96:97]
	s_nop 0
	v_pk_fma_f32 v[48:49], v[48:49], v[76:77], v[96:97]
	v_pk_mul_f32 v[76:77], v[80:81], v[102:103]
	v_pk_mul_f32 v[48:49], v[48:49], s[82:83] op_sel_hi:[1,0]
	v_mov_b32_e32 v47, v76
	v_cvt_pk_bf16_f32 v49, v48, v49
	v_mov_b32_e32 v48, v76
	v_mov_b32_e32 v51, v77
	v_mov_b32_e32 v53, v77
	v_permlane16_swap_b32_e32 v47, v48
	s_nop 0
	v_permlane16_swap_b32_e32 v51, v53
	v_cndmask_b32_e32 v97, v51, v53, vcc
	v_cndmask_b32_e32 v96, v47, v48, vcc
	v_pk_mul_f32 v[96:97], v[168:169], v[96:97]
	s_nop 0
	v_pk_fma_f32 v[70:71], v[70:71], v[76:77], v[96:97]
	s_nop 0
	v_pk_mul_f32 v[70:71], v[70:71], s[82:83] op_sel_hi:[1,0]
	s_nop 0
	v_cvt_pk_bf16_f32 v48, v70, v71
	v_pk_mul_f32 v[70:71], v[86:87], v[100:101]
	s_nop 0
	v_mov_b32_e32 v47, v70
	v_mov_b32_e32 v51, v70
	v_mov_b32_e32 v53, v71
	v_mov_b32_e32 v76, v71
	v_permlane16_swap_b32_e32 v47, v51
	s_nop 0
	v_permlane16_swap_b32_e32 v53, v76
	v_cndmask_b32_e32 v77, v53, v76, vcc
	v_cndmask_b32_e32 v76, v47, v51, vcc
	v_pk_mul_f32 v[66:67], v[66:67], v[70:71]
	s_nop 0
	v_pk_fma_f32 v[66:67], v[90:91], v[76:77], v[66:67]
	s_nop 0
	v_pk_mul_f32 v[66:67], v[66:67], s[82:83] op_sel_hi:[1,0]
	s_nop 0
	v_cvt_pk_bf16_f32 v47, v66, v67
	v_pk_mul_f32 v[66:67], v[84:85], v[88:89]
	s_nop 0
	v_mov_b32_e32 v51, v66
	v_mov_b32_e32 v53, v66
	v_mov_b32_e32 v70, v67
	v_mov_b32_e32 v71, v67
	v_permlane16_swap_b32_e32 v51, v53
	s_nop 0
	v_permlane16_swap_b32_e32 v70, v71
	v_cndmask_b32_e32 v71, v70, v71, vcc
	v_cndmask_b32_e32 v70, v51, v53, vcc
	v_and_b32_e32 v53, 0xffff0000, v46
	v_mov_b32_e32 v51, v52
	v_lshlrev_b32_e32 v52, 16, v46
	v_mul_f32_e32 v46, v53, v53
	v_pk_mul_f32 v[50:51], v[50:51], v[66:67]
	v_pk_fma_f32 v[66:67], v[52:53], v[52:53], v[46:47] op_sel_hi:[1,1,0]
	v_mul_f32_e32 v46, v69, v69
	v_pk_fma_f32 v[66:67], v[68:69], v[68:69], v[66:67]
	v_pk_fma_f32 v[50:51], v[92:93], v[70:71], v[50:51]
	v_pk_add_f32 v[66:67], v[46:47], v[66:67] op_sel_hi:[0,1]
	v_pk_fma_f32 v[66:67], v[110:111], v[110:111], v[66:67]
	v_mul_f32_e32 v46, v111, v111
	v_pk_add_f32 v[66:67], v[46:47], v[66:67] op_sel_hi:[0,1]
	v_pk_fma_f32 v[66:67], v[98:99], v[98:99], v[66:67]
	v_mul_f32_e32 v46, v99, v99
	v_pk_add_f32 v[66:67], v[46:47], v[66:67] op_sel_hi:[0,1]
	v_mov_b32_e32 v46, v66
	s_nop 1
	v_permlane16_swap_b32_e32 v66, v46
	v_add_f32_e32 v144, v66, v46
	v_mov_b32_e32 v146, v144
	s_nop 1
	v_permlane32_swap_b32_e32 v144, v146
	v_pk_add_f32 v[66:67], v[144:145], v[146:147]
	v_pk_mul_f32 v[50:51], v[50:51], s[82:83] op_sel_hi:[1,0]
	v_pk_fma_f32 v[66:67], v[66:67], s[6:7], v[170:171] op_sel_hi:[1,1,0]
	s_mov_b64 s[6:7], 0x60000
	v_mul_f32_e32 v46, 0x4b800000, v67
	v_cmp_gt_f32_e64 s[4:5], s95, v67
	s_nop 1
	v_cndmask_b32_e64 v46, v67, v46, s[4:5]
	v_rsq_f32_e32 v67, v46
	v_cvt_pk_bf16_f32 v46, v50, v51
	v_cndmask_b32_e64 v50, v31, -v31, vcc
	v_cndmask_b32_e64 v51, v33, -v33, vcc
	v_mul_f32_e32 v31, 0x45800000, v67
	v_cndmask_b32_e64 v70, v67, v31, s[4:5]
	v_mul_f32_e32 v31, 0x4b800000, v66
	v_cmp_gt_f32_e64 s[4:5], s95, v66
	v_pk_mul_f32 v[62:63], v[62:63], v[70:71] op_sel_hi:[1,0]
	v_pk_mul_f32 v[64:65], v[64:65], v[70:71] op_sel_hi:[1,0]
	v_cndmask_b32_e64 v31, v66, v31, s[4:5]
	v_pk_mul_f32 v[38:39], v[38:39], v[70:71] op_sel_hi:[1,0]
	v_rsq_f32_e32 v31, v31
	v_pk_mul_f32 v[62:63], v[62:63], v[138:139]
	v_pk_mul_f32 v[64:65], v[64:65], v[128:129]
	v_pk_mul_f32 v[54:55], v[54:55], v[70:71] op_sel_hi:[1,0]
	v_pk_mul_f32 v[56:57], v[56:57], v[70:71] op_sel_hi:[1,0]
	v_pk_mul_f32 v[42:43], v[42:43], v[70:71] op_sel_hi:[1,0]
	v_pk_mul_f32 v[44:45], v[44:45], v[70:71] op_sel_hi:[1,0]
	v_pk_mul_f32 v[76:77], v[38:39], v[118:119]
	v_pk_mul_f32 v[38:39], v[40:41], v[70:71] op_sel_hi:[1,0]
	v_pk_mul_f32 v[54:55], v[54:55], v[126:127]
	v_pk_mul_f32 v[56:57], v[56:57], v[124:125]
	v_pk_mul_f32 v[42:43], v[42:43], v[122:123]
	v_pk_mul_f32 v[44:45], v[44:45], v[120:121]
	v_pk_mul_f32 v[70:71], v[38:39], v[116:117]
	v_pk_mul_f32 v[38:39], v[62:63], s[82:83] op_sel_hi:[1,0]
	v_pk_mul_f32 v[40:41], v[64:65], s[82:83] op_sel_hi:[1,0]
; __device__ __forceinline__ unsigned cvtpk(float lo, float hi) { f32x2 v = {lo, hi}; bf16x2_t b = __builtin_convertvector(v, bf16x2_t); return __builtin_bit_cast(unsigned, b); }
; #define ATT_SB() __builtin_amdgcn_sched_barrier(0)
; #define ATT_DMA_K(t, sl) do { glds16(ksrc + (size_t)(t) * 64 * kpitch, (unsigned)__builtin_amdgcn_readfirstlane(kdst + (sl) * KSLOT)); \
;         if constexpr (DQK == 96) glds16(krsrc + (size_t)(t) * 64 * 32, (unsigned)__builtin_amdgcn_readfirstlane(krdst + (sl) * KSLOT)); } while (0)
; #define ATT_DMA_V(t, sl) do { glds16(vsrc + (size_t)(t) * 64, (unsigned)__builtin_amdgcn_readfirstlane(vdst + (sl) * VSLOT)); \
;         if constexpr (DV == 128) glds16(vsrc + (size_t)64 * NR + (size_t)(t) * 64, (unsigned)__builtin_amdgcn_readfirstlane(vdst + (sl) * VSLOT + 8192)); } while (0)
; #define ATT_KLOAD(sl) do { _Pragma("unroll") for (int kb_ = 0; kb_ < NKW; ++kb_) _Pragma("unroll") for (int ds_ = 0; ds_ < NDS; ++ds_) { \
;         if (ds_ < 2) kf[kb_ * NDS + ds_] = *(const LAS bf16x8*)(kp[ds_ & 1] + (sl) * KSLOT + (kb_ & 1) * 512 + (kb_ >> 1) * 4096); \
;         else kf[kb_ * NDS + ds_] = *(const LAS bf16x8*)(krp + (sl) * KSLOT + (kb_ & 1) * 256 + (kb_ >> 1) * 2048); } } while (0)
; template <int DQK, int DV, bool LEAD> ...
;     ...
;           for (int ds = 0; ds < NDS; ++ds) { u32x4 w;
; #pragma unroll
;               for (int i = 0; i < 4; ++i) w[i] = cvtpk(x[ds][2 * i] * c2, x[ds][2 * i + 1] * c2);
;               qf[qb * NDS + ds] = __builtin_bit_cast(bf16x8, w); }
;       }
; #pragma unroll
;       for (int d0 = 0; d0 < NQB * NDS; ++d0) asm volatile("" : "+v"(qf[d0])); }
;     wait_bar<0>();
;     bf16x8 kf[NKW * NDS], vf[NVF];
;     ATT_KLOAD(0);
;     asm volatile("s_waitcnt lgkmcnt(0)\n\ts_barrier" ::: "memory");
;     float lsum[NQB];
; #pragma unroll
;     for (int qb = 0; qb < NQB; ++qb) lsum[qb] = 0.f;
;     const f32x4 zero4 = {0.f, 0.f, 0.f, 0.f};
;     f32x4 o[NDB][NQB], c[NKW][NQB]; u32x4 pw[4];
; #pragma unroll
;     for (int i = 0; i < NDB; ++i)
; #pragma unroll
;         for (int qb = 0; qb < NQB; ++qb) o[i][qb] = zero4;
;     ATT_DMA_K(3, 0); ATT_DMA_V(1, 1);
;     ATT_QK(); ATT_SB();
	v_cvt_pk_bf16_f32 v38, v38, v39
	v_cvt_pk_bf16_f32 v39, v40, v41
	v_pk_mul_f32 v[40:41], v[54:55], s[82:83] op_sel_hi:[1,0]
	v_pk_mul_f32 v[54:55], v[56:57], s[82:83] op_sel_hi:[1,0]
	v_pk_mul_f32 v[42:43], v[42:43], s[82:83] op_sel_hi:[1,0]
	v_pk_mul_f32 v[44:45], v[44:45], s[82:83] op_sel_hi:[1,0]
	v_cvt_pk_bf16_f32 v40, v40, v41
	v_cvt_pk_bf16_f32 v41, v54, v55
	v_cvt_pk_bf16_f32 v42, v42, v43
	v_cvt_pk_bf16_f32 v43, v44, v45
	v_pk_mul_f32 v[44:45], v[76:77], s[82:83] op_sel_hi:[1,0]
	v_pk_mul_f32 v[54:55], v[70:71], s[82:83] op_sel_hi:[1,0]
	v_mul_f32_e32 v33, 0x45800000, v31
	v_cvt_pk_bf16_f32 v44, v44, v45
	v_cvt_pk_bf16_f32 v45, v54, v55
	v_cndmask_b32_e64 v54, v31, v33, s[4:5]
	v_pk_mul_f32 v[52:53], v[54:55], v[52:53] op_sel_hi:[0,1]
	v_pk_mul_f32 v[52:53], v[84:85], v[52:53]
	s_lshl_b32 s4, s16, 11
	v_mov_b32_e32 v31, v52
	v_mov_b32_e32 v33, v52
	v_mov_b32_e32 v55, v53
	v_mov_b32_e32 v56, v53
	v_permlane16_swap_b32_e32 v31, v33
	s_nop 0
	v_permlane16_swap_b32_e32 v55, v56
	v_cndmask_b32_e32 v57, v55, v56, vcc
	v_cndmask_b32_e32 v56, v31, v33, vcc
	v_mov_b32_e32 v31, v32
	v_pk_mul_f32 v[32:33], v[54:55], v[68:69] op_sel_hi:[0,1]
	v_pk_mul_f32 v[30:31], v[30:31], v[52:53]
	v_pk_mul_f32 v[32:33], v[86:87], v[32:33]
	v_pk_fma_f32 v[30:31], v[50:51], v[56:57], v[30:31]
	v_mov_b32_e32 v50, v32
	v_mov_b32_e32 v52, v32
	v_mov_b32_e32 v51, v33
	v_mov_b32_e32 v53, v33
	v_permlane16_swap_b32_e32 v50, v52
	s_nop 0
	v_permlane16_swap_b32_e32 v51, v53
	v_cndmask_b32_e32 v51, v51, v53, vcc
	v_cndmask_b32_e32 v50, v50, v52, vcc
	v_pk_mul_f32 v[24:25], v[24:25], v[32:33]
	s_cmpk_lt_u32 s38, 0x100
	v_pk_fma_f32 v[22:23], v[22:23], v[50:51], v[24:25]
	v_pk_mul_f32 v[24:25], v[54:55], v[110:111] op_sel_hi:[0,1]
	v_pk_mul_f32 v[24:25], v[80:81], v[24:25]
	v_pk_mul_f32 v[22:23], v[22:23], s[82:83] op_sel_hi:[1,0]
	v_mov_b32_e32 v32, v24
	v_mov_b32_e32 v50, v24
	v_mov_b32_e32 v33, v25
	v_mov_b32_e32 v51, v25
	v_permlane16_swap_b32_e32 v32, v50
	s_nop 0
	v_permlane16_swap_b32_e32 v33, v51
	v_cndmask_b32_e32 v33, v33, v51, vcc
	v_cndmask_b32_e32 v32, v32, v50, vcc
	v_pk_mul_f32 v[32:33], v[94:95], v[32:33]
	s_mov_b32 s16, 1
	v_pk_fma_f32 v[20:21], v[20:21], v[24:25], v[32:33]
	v_pk_mul_f32 v[24:25], v[54:55], v[98:99] op_sel_hi:[0,1]
	v_pk_mul_f32 v[24:25], v[82:83], v[24:25]
	v_pk_mul_f32 v[20:21], v[20:21], s[82:83] op_sel_hi:[1,0]
	v_mov_b32_e32 v32, v24
	v_mov_b32_e32 v50, v24
	v_mov_b32_e32 v33, v25
	v_mov_b32_e32 v51, v25
	v_permlane16_swap_b32_e32 v32, v50
	s_nop 0
	v_permlane16_swap_b32_e32 v33, v51
	v_cndmask_b32_e32 v33, v33, v51, vcc
	v_cndmask_b32_e32 v32, v32, v50, vcc
	v_pk_mul_f32 v[32:33], v[78:79], v[32:33]
	v_cvt_pk_bf16_f32 v55, v22, v23
	v_pk_fma_f32 v[14:15], v[24:25], v[14:15], v[32:33]
	v_pk_mul_f32 v[24:25], v[30:31], s[82:83] op_sel_hi:[1,0]
	v_pk_mul_f32 v[14:15], v[14:15], s[82:83] op_sel_hi:[1,0]
	v_cvt_pk_bf16_f32 v54, v24, v25
	v_cvt_pk_bf16_f32 v56, v20, v21
	v_cvt_pk_bf16_f32 v57, v14, v15
	s_waitcnt vmcnt(0) lgkmcnt(0)
	s_barrier
	ds_read_b128 v[20:23], v203
	ds_read_b128 v[30:33], v203 offset:512
	v_or_b32_e32 v24, 4, v238
	v_bitop3_b32 v14, v243, v24, v242 bitop3:0x36
	v_lshl_add_u32 v211, v14, 4, v244
	s_waitcnt lgkmcnt(1)
	v_mfma_f32_16x16x32_bf16 v[50:53], v[20:23], v[6:9], 0
	ds_read_b128 v[76:79], v211
	ds_read_b128 v[80:83], v211 offset:512
	v_lshlrev_b32_e32 v14, 5, v241
	v_lshlrev_b32_e32 v15, 6, v239
	v_mfma_f32_16x16x32_bf16 v[62:65], v[20:23], v[26:29], 0
	v_bitop3_b32 v14, v14, v236, 48 bitop3:0x78
	v_sub_u32_e32 v15, v240, v15
	v_add3_u32 v212, v15, v14, s4
	v_mfma_f32_16x16x32_bf16 v[66:69], v[20:23], v[72:75], 0
	v_lshl_add_u64 v[14:15], v[192:193], 0, s[6:7]
	s_mov_b64 s[6:7], 0x3000
	s_mov_b32 s4, 0
	v_mfma_f32_16x16x32_bf16 v[20:23], v[20:23], v[38:41], 0
	s_cselect_b64 vcc, -1, 0
	v_lshrrev_b32_e32 v25, 1, v236
	s_waitcnt lgkmcnt(1)
	v_mfma_f32_16x16x32_bf16 v[50:53], v[76:79], v[2:5], v[50:53]
	v_mfma_f32_16x16x32_bf16 v[62:65], v[76:79], v[16:19], v[62:65]
	v_mfma_f32_16x16x32_bf16 v[66:69], v[76:79], v[58:61], v[66:69]
	v_mfma_f32_16x16x32_bf16 v[20:23], v[76:79], v[42:45], v[20:23]
	ds_read_b128 v[76:79], v212 offset:8192
	ds_read_b128 v[84:87], v212 offset:8448
	s_waitcnt lgkmcnt(0)
	s_barrier
; #define ATT_SB() __builtin_amdgcn_sched_barrier(0)
; #define ATT_DMA_K(t, sl) do { glds16(ksrc + (size_t)(t) * 64 * kpitch, (unsigned)__builtin_amdgcn_readfirstlane(kdst + (sl) * KSLOT)); \
;         if constexpr (DQK == 96) glds16(krsrc + (size_t)(t) * 64 * 32, (unsigned)__builtin_amdgcn_readfirstlane(krdst + (sl) * KSLOT)); } while (0)
; #define ATT_DMA_V(t, sl) do { glds16(vsrc + (size_t)(t) * 64, (unsigned)__builtin_amdgcn_readfirstlane(vdst + (sl) * VSLOT)); \
;         if constexpr (DV == 128) glds16(vsrc + (size_t)64 * NR + (size_t)(t) * 64, (unsigned)__builtin_amdgcn_readfirstlane(vdst + (sl) * VSLOT + 8192)); } while (0)
; #define ATT_KLOAD(sl) do { _Pragma("unroll") for (int kb_ = 0; kb_ < NKW; ++kb_) _Pragma("unroll") for (int ds_ = 0; ds_ < NDS; ++ds_) { \
;         if (ds_ < 2) kf[kb_ * NDS + ds_] = *(const LAS bf16x8*)(kp[ds_ & 1] + (sl) * KSLOT + (kb_ & 1) * 512 + (kb_ >> 1) * 4096); \
;         else kf[kb_ * NDS + ds_] = *(const LAS bf16x8*)(krp + (sl) * KSLOT + (kb_ & 1) * 256 + (kb_ >> 1) * 2048); } } while (0)
; #define ATT_QK() do { _Pragma("unroll") for (int kb_ = 0; kb_ < NKW; ++kb_) _Pragma("unroll") for (int ds_ = 0; ds_ < NDS; ++ds_) _Pragma("unroll") for (int qb_ = 0; qb_ < NQB; ++qb_) \
;         c[kb_][qb_] = __builtin_amdgcn_mfma_f32_16x16x32_bf16(kf[kb_ * NDS + ds_], qf[qb_ * NDS + ds_], ds_ == 0 ? zero4 : c[kb_][qb_], 0, 0, 0); } while (0)
; #define ATT_EXP() do { _Pragma("unroll") for (int kb_ = 0; kb_ < NKW; ++kb_) _Pragma("unroll") for (int qb_ = 0; qb_ < NQB; ++qb_) _Pragma("unroll") for (int i_ = 0; i_ < 4; ++i_) \
;         c[kb_][qb_][i_] = __builtin_amdgcn_exp2f(c[kb_][qb_][i_]); } while (0)
; template <int DQK, int DV, bool LEAD> ...
;     ...
;     const f32x4 zero4 = {0.f, 0.f, 0.f, 0.f};
;     f32x4 o[NDB][NQB], c[NKW][NQB]; u32x4 pw[4];
; #pragma unroll
;     for (int i = 0; i < NDB; ++i)
; #pragma unroll
;         for (int qb = 0; qb < NQB; ++qb) o[i][qb] = zero4;
;     ATT_DMA_K(3, 0); ATT_DMA_V(1, 1);
;     ATT_QK(); ATT_SB();
;     ATT_KLOAD(1); ATT_SB();
;     if constexpr (LEAD) { ATT_EXP(); ATT_SUMPACK(); }
;     wait_bar<NDMA>();
;     int s_prev = 0, s_cur = 1, s_next = 2;
	s_mov_b32 m0, s42
	s_nop 0
	global_load_lds_dwordx4 v[14:15], off
	s_waitcnt lgkmcnt(1)
	v_mfma_f32_16x16x32_bf16 v[164:167], v[76:79], v[10:13], v[50:53]
	v_lshl_add_u64 v[14:15], v[204:205], 0, s[6:7]
	s_mov_b32 m0, s43
	s_nop 0
	global_load_lds_dwordx4 v[14:15], off
	v_lshl_add_u64 v[14:15], v[206:207], 0, s[66:67]
	v_mfma_f32_16x16x32_bf16 v[152:155], v[76:79], v[34:37], v[62:65]
	s_add_i32 s5, s41, 0x2000
	s_mov_b32 m0, s5
	s_nop 0
	global_load_lds_dwordx4 v[14:15], off
	s_mov_b32 s6, s4
	v_mfma_f32_16x16x32_bf16 v[136:139], v[76:79], v[54:57], v[20:23]
	s_mov_b32 s7, s4
	s_mov_b32 s5, s4
	v_mfma_f32_16x16x32_bf16 v[20:23], v[30:33], v[6:9], 0
	v_mfma_f32_16x16x32_bf16 v[50:53], v[30:33], v[26:29], 0
	v_mfma_f32_16x16x32_bf16 v[62:65], v[30:33], v[72:75], 0
	v_mfma_f32_16x16x32_bf16 v[30:33], v[30:33], v[38:41], 0
	v_mfma_f32_16x16x32_bf16 v[20:23], v[80:83], v[2:5], v[20:23]
	v_mfma_f32_16x16x32_bf16 v[50:53], v[80:83], v[16:19], v[50:53]
	v_mfma_f32_16x16x32_bf16 v[62:65], v[80:83], v[58:61], v[62:65]
	v_mfma_f32_16x16x32_bf16 v[30:33], v[80:83], v[42:45], v[30:33]
	v_mfma_f32_16x16x32_bf16 v[144:147], v[76:79], v[46:49], v[66:69]
	s_waitcnt lgkmcnt(0)
	v_mfma_f32_16x16x32_bf16 v[172:175], v[84:87], v[10:13], v[20:23]
	s_nop 0
	v_lshlrev_b32_e32 v66, 7, v237
	v_mfma_f32_16x16x32_bf16 v[168:171], v[84:87], v[34:37], v[50:53]
	v_mov_b64_e32 v[22:23], s[6:7]
	v_mov_b64_e32 v[20:21], s[4:5]
	v_mfma_f32_16x16x32_bf16 v[160:163], v[84:87], v[46:49], v[62:65]
	v_mfma_f32_16x16x32_bf16 v[156:159], v[84:87], v[54:57], v[30:33]
	ds_read_b128 v[120:123], v203 offset:12288
	ds_read_b128 v[132:135], v203 offset:12800
	ds_read_b128 v[124:127], v211 offset:12288
	ds_read_b128 v[140:143], v211 offset:12800
	ds_read_b128 v[128:131], v212 offset:20480
	ds_read_b128 v[148:151], v212 offset:20736
	v_cndmask_b32_e32 v14, v24, v238, vcc
	v_bitop3_b32 v14, v14, v25, 7 bitop3:0x78
	v_lshlrev_b32_e32 v14, 4, v14
	v_add3_u32 v210, 0, v66, v14
	s_waitcnt vmcnt(3) lgkmcnt(0)
	s_barrier
	s_mov_b32 s5, 1
	v_mov_b32_e32 v14, 0
	s_cmp_lg_u32 s5, 0
	v_mov_b64_e32 v[32:33], v[22:23]
	v_mov_b64_e32 v[52:53], v[22:23]
	v_mov_b64_e32 v[64:65], v[22:23]
	v_mov_b64_e32 v[68:69], v[22:23]
	v_mov_b64_e32 v[78:79], v[22:23]
	v_mov_b64_e32 v[82:83], v[22:23]
	v_mov_b64_e32 v[86:87], v[22:23]
	v_mov_b64_e32 v[90:91], v[22:23]
	v_mov_b64_e32 v[94:95], v[22:23]
	v_mov_b64_e32 v[98:99], v[22:23]
	v_mov_b64_e32 v[102:103], v[22:23]
	v_mov_b64_e32 v[106:107], v[22:23]
	v_mov_b64_e32 v[110:111], v[22:23]
	v_mov_b64_e32 v[114:115], v[22:23]
	v_mov_b64_e32 v[118:119], v[22:23]
	s_cselect_b64 s[6:7], -1, 0
	v_mov_b64_e32 v[30:31], v[20:21]
	v_mov_b64_e32 v[50:51], v[20:21]
	v_mov_b64_e32 v[62:63], v[20:21]
	v_mov_b64_e32 v[66:67], v[20:21]
	v_mov_b64_e32 v[76:77], v[20:21]
	v_mov_b64_e32 v[80:81], v[20:21]
	v_mov_b64_e32 v[84:85], v[20:21]
	v_mov_b64_e32 v[88:89], v[20:21]
	v_mov_b64_e32 v[92:93], v[20:21]
	v_mov_b64_e32 v[96:97], v[20:21]
	v_mov_b64_e32 v[100:101], v[20:21]
	v_mov_b64_e32 v[104:105], v[20:21]
	v_mov_b64_e32 v[108:109], v[20:21]
	v_mov_b64_e32 v[112:113], v[20:21]
	v_mov_b64_e32 v[116:117], v[20:21]
	s_mov_b32 s38, 2
	v_mov_b32_e32 v15, v14
	v_mov_b32_e32 v24, v14
	v_mov_b32_e32 v25, v14

; #define ATT_DMA_K(t, sl) do { glds16(ksrc + (size_t)(t) * 64 * kpitch, (unsigned)__builtin_amdgcn_readfirstlane(kdst + (sl) * KSLOT)); \
;         if constexpr (DQK == 96) glds16(krsrc + (size_t)(t) * 64 * 32, (unsigned)__builtin_amdgcn_readfirstlane(krdst + (sl) * KSLOT)); } while (0)
; #define ATT_DMA_V(t, sl) do { glds16(vsrc + (size_t)(t) * 64, (unsigned)__builtin_amdgcn_readfirstlane(vdst + (sl) * VSLOT)); \
;         if constexpr (DV == 128) glds16(vsrc + (size_t)64 * NR + (size_t)(t) * 64, (unsigned)__builtin_amdgcn_readfirstlane(vdst + (sl) * VSLOT + 8192)); } while (0)
; template <int DQK, int DV, bool LEAD> ...
;     ...
;     const int kc_l = (lane & 7) ^ (((krow_l >> 1) & 1) | (((krow_l >> 3) & 1) << 1) | (((krow_l >> 4) & 1) << 2));
;     const int vc_l = (lane & 7) ^ ((krow_l >> 1) & 7);
;     const bf16_t* ksrc = K + (size_t)(krow0 + krow_l) * kpitch + kc_l * 8;
;     const int rrow_l = (wid & 3) * 16 + (lane >> 2), rc_l = (lane & 3) ^ (((rrow_l >> 4) & 1) << 1);
;     const bf16_t* krsrc = (DQK == 96) ? KR + (size_t)(krow0 + rrow_l) * 32 + rc_l * 8 : nullptr;
;     const bf16_t* vsrc = Vt + (size_t)krow_l * NR + krow0 + vc_l * 8;
;     const unsigned kdst = lds0 + KOFF + wid * 1024, krdst = lds0 + KOFF + 8192 + (wid & 3) * 1024, vdst = lds0 + VOFF + wid * 1024;
;     ...
;     const int kr0 = 8 * (q16 >> 2) + (q16 & 3);
;     const int fk = ((kr0 >> 1) & 1) | (((kr0 >> 3) & 1) << 1) | (((kr0 >> 4) & 1) << 2);
;     ...
;     ATT_DMA_K(0, 0); ATT_DMA_V(0, 0); ATT_DMA_K(1, 1); ATT_DMA_K(2, 2);
;     bf16x8 qf[NQB * NDS];
;     {
;       const float c2 = (DQK == 64) ? C2_EVEN : C2_ODD; const bool lat = tq0 >= 0;
; #pragma unroll
;       for (int qb = 0; qb < NQB; ++qb) {
;           const bf16_t* qp = Q + (size_t)(qrow0 + qoff + qb * 16 + q16) * qpitch + g4 * 8;
;           bf16x8 raw[NDS];
; #pragma unroll
;           for (int ds = 0; ds < NDS; ++ds) raw[ds] = *(const bf16x8*)(qp + ds * 32);
;           float x[NDS][8];
; #pragma unroll
;           for (int ds = 0; ds < NDS; ++ds)
; #pragma unroll
;               for (int j = 0; j < 8; ++j) x[ds][j] = __uint_as_float(((unsigned)(unsigned short)raw[ds][j]) << 16);
;           const int tq = tq0 + qoff + qb * 16 + q16, prow = (tq >> 6) & 127, pcol = tq & 63;
.LBB0_648:
	s_and_b64 vcc, exec, s[4:5]
	s_cbranch_vccz .LBB0_640
	v_mov_b32_e32 v220, v0
	v_mov_b64_e32 v[6:7], s[52:53]
	v_readfirstlane_b32 s38, v220
	s_ashr_i32 s4, s38, 6
	v_bfe_u32 v203, v220, 3, 3
	v_lshl_or_b32 v8, s4, 3, v203
	v_ashrrev_i32_e32 v2, 1, v8
	s_and_b32 s30, s4, 3
	v_and_b32_e32 v3, 1, v2
	s_lshl_b32 s5, s4, 1
	s_lshr_b32 s7, s38, 5
	v_bfe_u32 v4, v220, 2, 4
	v_and_b32_e32 v216, 7, v220
	s_and_b32 s6, s5, 2
	v_and_or_b32 v3, s7, 4, v3
	v_xor_b32_e32 v10, v2, v220
	v_add_u32_e32 v2, s40, v8
	v_lshl_or_b32 v4, s30, 4, v4
	v_bitop3_b32 v9, v3, v216, s6 bitop3:0x36
	v_ashrrev_i32_e32 v3, 31, v2
	v_and_b32_e32 v12, 3, v220
	v_or_b32_e32 v4, s40, v4
	s_lshl_b32 s4, s4, 10
	v_lshlrev_b64 v[2:3], 11, v[2:3]
	v_bitop3_b32 v11, s5, v12, 2 bitop3:0x6c
	v_ashrrev_i32_e32 v5, 31, v4
	s_add_i32 s42, s4, 0
	s_lshl_b32 s6, s30, 10
	v_mad_i64_i32 v[6:7], s[4:5], v8, s91, v[6:7]
	v_lshlrev_b64 v[4:5], 6, v[4:5]
	s_ashr_i32 s41, s40, 31
	v_lshl_add_u64 v[2:3], s[50:51], 0, v[2:3]
	v_lshlrev_b32_e32 v194, 4, v9
	s_add_i32 s5, s6, 0
	v_lshl_add_u64 v[4:5], s[28:29], 0, v[4:5]
	v_lshl_add_u64 v[6:7], s[40:41], 1, v[6:7]
	v_lshl_add_u64 v[186:187], v[2:3], 0, v[194:195]
	v_lshlrev_b32_e32 v194, 4, v11
	v_lshlrev_b32_e32 v2, 4, v10
	s_add_i32 s41, s5, 0x2000
	s_mov_b32 m0, s42
	s_nop 0
	global_load_lds_dwordx4 v[186:187], off
	v_lshl_add_u64 v[188:189], v[4:5], 0, v[194:195]
	v_and_b32_e32 v194, 0x70, v2
	s_mov_b32 m0, s41
	s_nop 0
	global_load_lds_dwordx4 v[188:189], off
	s_add_i32 s40, s42, 0x9000
	v_lshl_add_u64 v[190:191], v[6:7], 0, v[194:195]
	s_mov_b32 m0, s40
	s_nop 0
	global_load_lds_dwordx4 v[190:191], off
	s_mov_b64 s[6:7], 0x20000
	v_lshl_add_u64 v[2:3], v[186:187], 0, s[6:7]
	s_add_i32 s5, s42, 0x3000
	s_mov_b32 m0, s5
	s_nop 0
	global_load_lds_dwordx4 v[2:3], off
	v_lshl_add_u64 v[2:3], v[188:189], 0, s[60:61]
	s_add_i32 s5, s41, 0x3000
	s_mov_b32 m0, s5
	s_nop 0
	global_load_lds_dwordx4 v[2:3], off
	s_mov_b64 s[6:7], 0x40000
	s_lshl_b32 s4, s30, 6
	v_lshl_add_u64 v[2:3], v[186:187], 0, s[6:7]
	s_add_i32 s5, s42, 0x6000
	s_mov_b32 m0, s5
	s_nop 0
	global_load_lds_dwordx4 v[2:3], off
	v_and_b32_e32 v221, 15, v220
	s_mov_b64 s[6:7], 0x2000
	s_or_b32 s25, s4, s25
	v_and_b32_e32 v8, 48, v220
	v_lshl_add_u64 v[2:3], v[188:189], 0, s[6:7]
	v_or_b32_e32 v6, s25, v221
	v_mov_b32_e32 v9, v195
	s_add_i32 s5, s41, 0x6000
	s_mov_b32 m0, s5
	s_nop 0
	global_load_lds_dwordx4 v[2:3], off
	v_lshl_add_u64 v[2:3], s[46:47], 0, v[8:9]
	v_or_b32_e32 v7, 16, v6
	v_mad_i64_i32 v[4:5], s[4:5], v6, s90, v[2:3]
	v_mad_i64_i32 v[10:11], s[4:5], v7, s90, v[2:3]
	v_or_b32_e32 v7, 32, v6
	v_or_b32_e32 v6, 48, v6
	v_mad_i64_i32 v[22:23], s[4:5], v7, s90, v[2:3]
	v_mad_i64_i32 v[34:35], s[4:5], v6, s90, v[2:3]
	global_load_dwordx4 v[66:69], v[4:5], off offset:64
	global_load_dwordx4 v[70:73], v[10:11], off offset:64
	global_load_dwordx4 v[90:93], v[22:23], off offset:64
	global_load_dwordx4 v[116:119], v[34:35], off offset:64
	global_load_dwordx4 v[134:137], v[4:5], off
	global_load_dwordx4 v[140:143], v[10:11], off
	global_load_dwordx4 v[86:89], v[22:23], off
	global_load_dwordx4 v[6:9], v[34:35], off
	s_lshr_b32 s4, s31, 6
	v_and_b32_e32 v218, 63, v220
	v_lshlrev_b32_e32 v217, 1, v220
	s_or_b32 s4, s4, s30
	v_and_or_b32 v236, v217, 24, v12
	v_bfe_u32 v238, v220, 3, 1
	v_mov_b32_e32 v38, s4
	v_cmp_gt_u32_e32 vcc, 32, v218
	v_or_b32_e32 v24, 16, v221
	v_bfe_u32 v194, v220, 4, 2
	s_ashr_i32 s16, s38, 8
	v_bfe_u32 v239, v220, 1, 2
	v_lshlrev_b32_e32 v240, 2, v238
	v_lshl_add_u32 v237, v236, 7, 0
	v_cndmask_b32_e32 v12, v221, v38, vcc
	v_cndmask_b32_e32 v24, v24, v38, vcc
	v_lshl_add_u32 v241, s16, 12, v237
	v_bitop3_b32 v2, v240, v194, v239 bitop3:0x36
	v_lshlrev_b32_e32 v12, 6, v12
	v_lshlrev_b32_e32 v24, 6, v24
	v_lshl_add_u32 v219, v2, 4, v241
	global_load_dwordx4 v[2:5], v[4:5], off offset:128
	s_nop 0
	global_load_dwordx4 v[106:109], v12, s[36:37] offset:48
	global_load_dwordx4 v[102:105], v12, s[36:37] offset:32
	global_load_dwordx4 v[18:21], v12, s[36:37] offset:16
	global_load_dwordx4 v[14:17], v12, s[36:37]
	s_nop 0
	global_load_dwordx4 v[10:13], v[10:11], off offset:128
	s_nop 0
	global_load_dwordx4 v[98:101], v24, s[36:37] offset:48
	global_load_dwordx4 v[94:97], v24, s[36:37] offset:32
	global_load_dwordx4 v[30:33], v24, s[36:37] offset:16
	global_load_dwordx4 v[26:29], v24, s[36:37]
	s_nop 0
	global_load_dwordx4 v[22:25], v[22:23], off offset:128
	v_or_b32_e32 v36, 32, v221
	v_or_b32_e32 v39, 48, v221
	v_cndmask_b32_e32 v36, v36, v38, vcc
	v_cndmask_b32_e32 v38, v39, v38, vcc
	v_lshlrev_b32_e32 v36, 6, v36
	v_lshlrev_b32_e32 v50, 6, v38
	v_lshlrev_b32_e32 v162, 5, v194
	global_load_dwordx4 v[82:85], v36, s[36:37] offset:48
	global_load_dwordx4 v[78:81], v36, s[36:37] offset:32
	global_load_dwordx4 v[74:77], v36, s[36:37] offset:16
	global_load_dwordx4 v[62:65], v36, s[36:37]
	s_nop 0
	global_load_dwordx4 v[34:37], v[34:35], off offset:128
	s_nop 0
	global_load_dwordx4 v[38:41], v50, s[36:37] offset:48
	global_load_dwordx4 v[42:45], v50, s[36:37] offset:32
	global_load_dwordx4 v[46:49], v50, s[36:37] offset:16
	s_nop 0
	global_load_dwordx4 v[50:53], v50, s[36:37]
	s_nop 0
	global_load_dwordx4 v[54:57], v162, s[44:45] offset:144
	global_load_dwordx4 v[58:61], v162, s[44:45] offset:128
	v_and_b32_e32 v160, 16, v220
	v_cmp_eq_u32_e32 vcc, 0, v160
	s_mov_b32 s6, 0x3d000000
	s_brev_b32 s7, 60
	s_mov_b32 s4, 0x358637bd
	s_mov_b32 s7, 0x3c800000
	s_waitcnt vmcnt(26)
	v_and_b32_e32 v111, 0xffff0000, v119
	s_waitcnt vmcnt(25)
	v_and_b32_e32 v193, 0xffff0000, v134
	v_lshlrev_b32_e32 v192, 16, v134
	v_lshlrev_b32_e32 v110, 16, v119
	s_waitcnt vmcnt(22)
; template <int DQK, int DV, bool LEAD> ...
;     ...
;           float x[NDS][8];
; #pragma unroll
;           for (int ds = 0; ds < NDS; ++ds)
; #pragma unroll
;               for (int j = 0; j < 8; ++j) x[ds][j] = __uint_as_float(((unsigned)(unsigned short)raw[ds][j]) << 16);
;           const int tq = tq0 + qoff + qb * 16 + q16, prow = (tq >> 6) & 127, pcol = tq & 63;
;           float sn = 0.f;
; #pragma unroll
;           for (int ds = 0; ds < 2; ++ds)
; #pragma unroll
;               for (int j = 0; j < 8; ++j) sn += x[ds][j] * x[ds][j];
;           sn = lanes4_sum(sn);
	v_and_b32_e32 v121, 0xffff0000, v8
	v_lshlrev_b32_e32 v120, 16, v8
	v_mul_f32_e32 v8, v193, v193
	v_and_b32_e32 v113, 0xffff0000, v118
	v_lshlrev_b32_e32 v112, 16, v118
	v_and_b32_e32 v119, 0xffff0000, v9
	v_lshlrev_b32_e32 v118, 16, v9
	v_and_b32_e32 v207, 0xffff0000, v135
	v_lshlrev_b32_e32 v206, 16, v135
	v_pk_fma_f32 v[8:9], v[192:193], v[192:193], v[8:9] op_sel_hi:[1,1,0]
	v_and_b32_e32 v181, 0xffff0000, v137
	v_lshlrev_b32_e32 v180, 16, v137
	v_and_b32_e32 v185, 0xffff0000, v136
	v_lshlrev_b32_e32 v184, 16, v136
	v_and_b32_e32 v137, 0xffff0000, v88
	v_lshlrev_b32_e32 v136, 16, v88
	v_pk_fma_f32 v[8:9], v[206:207], v[206:207], v[8:9]
	v_mul_f32_e32 v88, v207, v207
	v_pk_add_f32 v[8:9], v[88:89], v[8:9] op_sel_hi:[0,1]
	v_pk_fma_f32 v[8:9], v[184:185], v[184:185], v[8:9]
	v_mul_f32_e32 v88, v185, v185
	v_pk_add_f32 v[8:9], v[88:89], v[8:9] op_sel_hi:[0,1]
	v_pk_fma_f32 v[8:9], v[180:181], v[180:181], v[8:9]
	v_mul_f32_e32 v88, v181, v181
	v_and_b32_e32 v179, 0xffff0000, v66
	v_lshlrev_b32_e32 v178, 16, v66
	v_pk_add_f32 v[8:9], v[88:89], v[8:9] op_sel_hi:[0,1]
	v_pk_fma_f32 v[8:9], v[178:179], v[178:179], v[8:9]
	v_mul_f32_e32 v88, v179, v179
	v_and_b32_e32 v177, 0xffff0000, v67
	v_lshlrev_b32_e32 v176, 16, v67
	v_pk_add_f32 v[8:9], v[88:89], v[8:9] op_sel_hi:[0,1]
	v_pk_fma_f32 v[8:9], v[176:177], v[176:177], v[8:9]
	v_mul_f32_e32 v88, v177, v177
	v_and_b32_e32 v171, 0xffff0000, v68
	v_lshlrev_b32_e32 v170, 16, v68
	v_pk_add_f32 v[8:9], v[88:89], v[8:9] op_sel_hi:[0,1]
	v_pk_fma_f32 v[8:9], v[170:171], v[170:171], v[8:9]
	v_mul_f32_e32 v88, v171, v171
	v_and_b32_e32 v169, 0xffff0000, v69
	v_lshlrev_b32_e32 v168, 16, v69
	v_pk_add_f32 v[8:9], v[88:89], v[8:9] op_sel_hi:[0,1]
	v_pk_fma_f32 v[8:9], v[168:169], v[168:169], v[8:9]
	v_mul_f32_e32 v88, v169, v169
	v_pk_add_f32 v[8:9], v[88:89], v[8:9] op_sel_hi:[0,1]
	v_and_b32_e32 v123, 0xffff0000, v7
	v_lshlrev_b32_e32 v122, 16, v7
	v_mov_b32_e32 v7, v8
	s_nop 1
	v_permlane16_swap_b32_e32 v8, v7
	v_add_f32_e32 v7, v8, v7
	v_mov_b32_e32 v9, v7
	v_and_b32_e32 v167, 0xffff0000, v140
	s_nop 0
	v_permlane32_swap_b32_e32 v7, v9
	v_lshlrev_b32_e32 v166, 16, v140
	v_mul_f32_e32 v8, v167, v167
	v_and_b32_e32 v133, 0xffff0000, v89
	v_lshlrev_b32_e32 v132, 16, v89
	v_and_b32_e32 v159, 0xffff0000, v141
	v_lshlrev_b32_e32 v158, 16, v141
	v_pk_fma_f32 v[88:89], v[166:167], v[166:167], v[8:9] op_sel_hi:[1,1,0]
	v_mul_f32_e32 v8, v159, v159
	v_pk_fma_f32 v[88:89], v[158:159], v[158:159], v[88:89]
	v_and_b32_e32 v157, 0xffff0000, v142
	v_lshlrev_b32_e32 v156, 16, v142
	v_pk_add_f32 v[88:89], v[8:9], v[88:89] op_sel_hi:[0,1]
	v_pk_fma_f32 v[88:89], v[156:157], v[156:157], v[88:89]
	v_mul_f32_e32 v8, v157, v157
	v_and_b32_e32 v155, 0xffff0000, v143
	v_lshlrev_b32_e32 v154, 16, v143
	v_pk_add_f32 v[88:89], v[8:9], v[88:89] op_sel_hi:[0,1]
	v_pk_fma_f32 v[88:89], v[154:155], v[154:155], v[88:89]
	v_mul_f32_e32 v8, v155, v155
	v_and_b32_e32 v153, 0xffff0000, v70
	v_lshlrev_b32_e32 v152, 16, v70
	v_pk_add_f32 v[88:89], v[8:9], v[88:89] op_sel_hi:[0,1]
	v_pk_fma_f32 v[88:89], v[152:153], v[152:153], v[88:89]
	v_mul_f32_e32 v8, v153, v153
	v_and_b32_e32 v151, 0xffff0000, v71
	v_lshlrev_b32_e32 v150, 16, v71
	v_pk_add_f32 v[88:89], v[8:9], v[88:89] op_sel_hi:[0,1]
	v_pk_fma_f32 v[88:89], v[150:151], v[150:151], v[88:89]
	v_mul_f32_e32 v8, v151, v151
	v_and_b32_e32 v149, 0xffff0000, v72
	v_lshlrev_b32_e32 v148, 16, v72
	v_pk_add_f32 v[88:89], v[8:9], v[88:89] op_sel_hi:[0,1]
	v_pk_fma_f32 v[88:89], v[148:149], v[148:149], v[88:89]
	v_mul_f32_e32 v8, v149, v149
	v_and_b32_e32 v147, 0xffff0000, v73
	v_lshlrev_b32_e32 v146, 16, v73
	v_pk_add_f32 v[88:89], v[8:9], v[88:89] op_sel_hi:[0,1]
	v_pk_fma_f32 v[88:89], v[146:147], v[146:147], v[88:89]
	v_mul_f32_e32 v8, v147, v147
	v_pk_add_f32 v[88:89], v[8:9], v[88:89] op_sel_hi:[0,1]
	v_mov_b32_e32 v8, v88
	s_nop 1
	v_permlane16_swap_b32_e32 v88, v8
	v_and_b32_e32 v145, 0xffff0000, v86
	v_add_f32_e32 v173, v88, v8
	v_lshlrev_b32_e32 v144, 16, v86
	v_mul_f32_e32 v8, v145, v145
	v_and_b32_e32 v139, 0xffff0000, v87
	v_lshlrev_b32_e32 v138, 16, v87
	v_pk_fma_f32 v[86:87], v[144:145], v[144:145], v[8:9] op_sel_hi:[1,1,0]
	v_mul_f32_e32 v8, v139, v139
	v_pk_fma_f32 v[86:87], v[138:139], v[138:139], v[86:87]
	v_and_b32_e32 v131, 0xffff0000, v90
	v_pk_add_f32 v[86:87], v[8:9], v[86:87] op_sel_hi:[0,1]
	v_pk_fma_f32 v[86:87], v[136:137], v[136:137], v[86:87]
	v_mul_f32_e32 v8, v137, v137
	v_pk_add_f32 v[86:87], v[8:9], v[86:87] op_sel_hi:[0,1]
	v_pk_fma_f32 v[86:87], v[132:133], v[132:133], v[86:87]
	v_mul_f32_e32 v8, v133, v133
	v_lshlrev_b32_e32 v130, 16, v90
	v_pk_add_f32 v[86:87], v[8:9], v[86:87] op_sel_hi:[0,1]
	v_pk_fma_f32 v[86:87], v[130:131], v[130:131], v[86:87]
	v_mul_f32_e32 v8, v131, v131
	v_and_b32_e32 v129, 0xffff0000, v91
	v_lshlrev_b32_e32 v128, 16, v91
	v_pk_add_f32 v[86:87], v[8:9], v[86:87] op_sel_hi:[0,1]
	v_pk_fma_f32 v[86:87], v[128:129], v[128:129], v[86:87]
	v_mul_f32_e32 v8, v129, v129
	v_and_b32_e32 v127, 0xffff0000, v92
	v_lshlrev_b32_e32 v126, 16, v92
	v_pk_add_f32 v[86:87], v[8:9], v[86:87] op_sel_hi:[0,1]
	v_pk_fma_f32 v[86:87], v[126:127], v[126:127], v[86:87]
	v_mul_f32_e32 v8, v127, v127
	v_and_b32_e32 v125, 0xffff0000, v93
	v_lshlrev_b32_e32 v124, 16, v93
	v_pk_add_f32 v[86:87], v[8:9], v[86:87] op_sel_hi:[0,1]
	v_pk_fma_f32 v[86:87], v[124:125], v[124:125], v[86:87]
	v_mul_f32_e32 v8, v125, v125
	v_pk_add_f32 v[86:87], v[8:9], v[86:87] op_sel_hi:[0,1]
	v_mov_b32_e32 v8, v86
	v_and_b32_e32 v135, 0xffff0000, v6
	s_nop 0
	v_permlane16_swap_b32_e32 v86, v8
	v_lshlrev_b32_e32 v134, 16, v6
	v_mul_f32_e32 v6, v135, v135
	v_add_f32_e32 v161, v86, v8
; template <int DQK, int DV, bool LEAD> ...
;     ...
;           float sn = 0.f;
; #pragma unroll
;           for (int ds = 0; ds < 2; ++ds)
; #pragma unroll
;               for (int j = 0; j < 8; ++j) sn += x[ds][j] * x[ds][j];
;           sn = lanes4_sum(sn);
;           const float rn = rsqrtf(sn * (1.f / 64.f) + EPS);
; #pragma unroll
;           for (int ds = 0; ds < 2; ++ds)
; #pragma unroll
;               for (int j = 0; j < 8; ++j) x[ds][j] *= rn * qgain[32 * ds + 8 * g4 + j];
;           if constexpr (DQK == 64) {
; #pragma unroll
;               for (int ds = 0; ds < 2; ++ds)
; #pragma unroll
;                   for (int j = 0; j < 8; ++j) {
;                       auto rr = __builtin_amdgcn_permlane32_swap(__float_as_uint(x[ds][j]), __float_as_uint(x[ds][j]), false, false);
;                       const float other = hi ? __uint_as_float(rr[0]) : __uint_as_float(rr[1]);
;                       float cc = 1.f, sg = 0.f;
;                       if (lat) { const f32x2 cs = rope[(ds ? pcol : prow) * 16 + 8 * (g4 & 1) + j]; cc = cs.x; sg = hi ? cs.y : -cs.y; }
;                       x[ds][j] = x[ds][j] * cc + other * sg; }
;           } else {
;               float sr = 0.f;
; #pragma unroll
;               for (int j = 0; j < 8; ++j) sr += x[2][j] * x[2][j];
;               sr = lanes4_sum(sr);
;               const float rq = rsqrtf(sr * (1.f / 32.f) + EPS);
; #pragma unroll
;               for (int j = 0; j < 8; ++j) { const float av = x[2][j] * rq * qgain[64 + 8 * g4 + j];
;                   auto rr = __builtin_amdgcn_permlane16_swap(__float_as_uint(av), __float_as_uint(av), false, false);
;                   const float other = (g4 & 1) ? __uint_as_float(rr[0]) : __uint_as_float(rr[1]);
;                   float cc = 1.f, sg = 0.f;
;                   if (lat) { const f32x2 cs = rope[((g4 & 2) ? pcol : prow) * 8 + j]; cc = cs.x; sg = (g4 & 1) ? cs.y : -cs.y; }
;                   x[2][j] = av * cc + other * sg; }
	v_pk_fma_f32 v[86:87], v[134:135], v[134:135], v[6:7] op_sel_hi:[1,1,0]
	v_mul_f32_e32 v6, v123, v123
	v_pk_fma_f32 v[86:87], v[122:123], v[122:123], v[86:87]
	v_and_b32_e32 v115, 0xffff0000, v117
	v_pk_add_f32 v[86:87], v[6:7], v[86:87] op_sel_hi:[0,1]
	v_pk_fma_f32 v[86:87], v[120:121], v[120:121], v[86:87]
	v_mul_f32_e32 v6, v121, v121
	v_pk_add_f32 v[86:87], v[6:7], v[86:87] op_sel_hi:[0,1]
	v_pk_fma_f32 v[86:87], v[118:119], v[118:119], v[86:87]
	v_mul_f32_e32 v6, v119, v119
	v_lshlrev_b32_e32 v114, 16, v117
	v_and_b32_e32 v117, 0xffff0000, v116
	v_lshlrev_b32_e32 v116, 16, v116
	v_pk_add_f32 v[86:87], v[6:7], v[86:87] op_sel_hi:[0,1]
	v_pk_fma_f32 v[86:87], v[116:117], v[116:117], v[86:87]
	v_mul_f32_e32 v6, v117, v117
	global_load_dwordx4 v[66:69], v162, s[44:45] offset:16
	global_load_dwordx4 v[70:73], v162, s[44:45]
	v_pk_add_f32 v[86:87], v[6:7], v[86:87] op_sel_hi:[0,1]
	v_pk_fma_f32 v[86:87], v[114:115], v[114:115], v[86:87]
	v_mul_f32_e32 v6, v115, v115
	v_pk_add_f32 v[86:87], v[6:7], v[86:87] op_sel_hi:[0,1]
	v_pk_fma_f32 v[86:87], v[112:113], v[112:113], v[86:87]
	v_mul_f32_e32 v6, v113, v113
	v_pk_add_f32 v[86:87], v[6:7], v[86:87] op_sel_hi:[0,1]
	v_pk_fma_f32 v[86:87], v[110:111], v[110:111], v[86:87]
	v_mul_f32_e32 v6, v111, v111
	v_pk_add_f32 v[86:87], v[6:7], v[86:87] op_sel_hi:[0,1]
	v_mov_b32_e32 v6, v86
	s_nop 1
	v_permlane16_swap_b32_e32 v86, v6
	v_add_f32_e32 v141, v86, v6
	global_load_dwordx4 v[86:89], v162, s[44:45] offset:272
	global_load_dwordx4 v[90:93], v162, s[44:45] offset:256
	s_waitcnt vmcnt(15)
	v_and_b32_e32 v165, 0xffff0000, v25
	v_lshlrev_b32_e32 v164, 16, v25
	v_and_b32_e32 v25, 0xffff0000, v2
	v_cndmask_b32_e64 v201, v105, -v105, vcc
	v_cndmask_b32_e64 v200, v103, -v103, vcc
	v_mov_b32_e32 v103, v104
	v_and_b32_e32 v105, 0xffff0000, v24
	v_lshlrev_b32_e32 v104, 16, v24
	v_lshlrev_b32_e32 v24, 16, v2
	v_mul_f32_e32 v2, v25, v25
	v_and_b32_e32 v205, 0xffff0000, v13
	v_lshlrev_b32_e32 v204, 16, v13
	v_and_b32_e32 v211, 0xffff0000, v12
	v_lshlrev_b32_e32 v210, 16, v12
	v_and_b32_e32 v13, 0xffff0000, v3
	v_lshlrev_b32_e32 v12, 16, v3
	v_pk_fma_f32 v[2:3], v[24:25], v[24:25], v[2:3] op_sel_hi:[1,1,0]
	v_and_b32_e32 v199, 0xffff0000, v4
	v_lshlrev_b32_e32 v198, 16, v4
	v_pk_fma_f32 v[2:3], v[12:13], v[12:13], v[2:3]
	v_mul_f32_e32 v4, v13, v13
	v_pk_add_f32 v[2:3], v[4:5], v[2:3] op_sel_hi:[0,1]
	v_pk_fma_f32 v[2:3], v[198:199], v[198:199], v[2:3]
	v_mul_f32_e32 v4, v199, v199
	v_and_b32_e32 v215, 0xffff0000, v5
	v_lshlrev_b32_e32 v214, 16, v5
	v_pk_add_f32 v[2:3], v[4:5], v[2:3] op_sel_hi:[0,1]
	v_pk_fma_f32 v[2:3], v[214:215], v[214:215], v[2:3]
	v_mul_f32_e32 v4, v215, v215
	v_pk_add_f32 v[2:3], v[4:5], v[2:3] op_sel_hi:[0,1]
	v_mov_b32_e32 v3, v2
	s_nop 1
	v_permlane16_swap_b32_e32 v2, v3
	v_add_f32_e32 v6, v2, v3
	v_mov_b32_e32 v8, v6
	s_nop 1
	v_permlane32_swap_b32_e32 v6, v8
	v_cndmask_b32_e64 v213, v109, -v109, vcc
	v_cndmask_b32_e64 v212, v107, -v107, vcc
	v_mov_b32_e32 v107, v108
	s_waitcnt vmcnt(14)
	v_cndmask_b32_e64 v109, v85, -v85, vcc
	v_cndmask_b32_e64 v108, v83, -v83, vcc
	v_mov_b32_e32 v83, v84
	s_waitcnt vmcnt(9)
	v_cndmask_b32_e64 v85, v41, -v41, vcc
	v_cndmask_b32_e64 v84, v39, -v39, vcc
	v_mov_b32_e32 v39, v40
	s_waitcnt vmcnt(8)
	v_cndmask_b32_e64 v41, v45, -v45, vcc
	v_cndmask_b32_e64 v40, v43, -v43, vcc
	v_mov_b32_e32 v43, v44
	v_pk_add_f32 v[2:3], v[6:7], v[8:9]
	v_mov_b64_e32 v[44:45], s[4:5]
	v_pk_fma_f32 v[6:7], v[2:3], s[6:7], v[44:45] op_sel_hi:[1,1,0]
	v_cndmask_b32_e64 v222, v19, -v19, vcc
	v_mul_f32_e32 v2, 0x4b800000, v7
	v_cmp_gt_f32_e64 s[4:5], s95, v7
	v_mov_b32_e32 v19, v20
	v_and_b32_e32 v229, 0xffff0000, v11
	v_cndmask_b32_e64 v2, v7, v2, s[4:5]
	v_rsq_f32_e32 v2, v2
	v_lshlrev_b32_e32 v228, 16, v11
	v_mul_f32_e32 v11, 0x4b800000, v6
	v_cndmask_b32_e64 v223, v21, -v21, vcc
	v_mul_f32_e32 v3, 0x45800000, v2
	v_cndmask_b32_e64 v20, v2, v3, s[4:5]
	s_waitcnt vmcnt(5)
	v_pk_mul_f32 v[2:3], v[20:21], v[56:57] op_sel_hi:[0,1]
	v_pk_mul_f32 v[2:3], v[2:3], v[168:169]
	v_pk_mul_f32 v[4:5], v[20:21], v[54:55] op_sel_hi:[0,1]
	v_pk_mul_f32 v[2:3], v[2:3], s[82:83] op_sel_hi:[1,0]
	v_pk_mul_f32 v[8:9], v[4:5], v[170:171]
	v_cvt_pk_bf16_f32 v5, v2, v3
	v_pk_mul_f32 v[2:3], v[8:9], s[82:83] op_sel_hi:[1,0]
	s_waitcnt vmcnt(4)
	v_pk_mul_f32 v[8:9], v[58:59], v[20:21] op_sel_hi:[1,0]
	v_cvt_pk_bf16_f32 v4, v2, v3
	v_pk_mul_f32 v[2:3], v[20:21], v[60:61] op_sel_hi:[0,1]
	v_pk_mul_f32 v[2:3], v[2:3], v[176:177]
	v_pk_mul_f32 v[8:9], v[8:9], v[178:179]
	v_pk_mul_f32 v[2:3], v[2:3], s[82:83] op_sel_hi:[1,0]
	v_pk_mul_f32 v[8:9], v[8:9], s[82:83] op_sel_hi:[1,0]
	v_cvt_pk_bf16_f32 v3, v2, v3
	v_cndmask_b32_e64 v177, v33, -v33, vcc
	v_cndmask_b32_e64 v176, v31, -v31, vcc
	v_mov_b32_e32 v31, v32
	v_cvt_pk_bf16_f32 v2, v8, v9
	s_waitcnt vmcnt(3)
	v_pk_mul_f32 v[8:9], v[68:69], v[20:21] op_sel_hi:[1,0]
	v_pk_mul_f32 v[32:33], v[66:67], v[20:21] op_sel_hi:[1,0]
	v_cmp_gt_f32_e64 s[4:5], s95, v6
	v_pk_mul_f32 v[8:9], v[8:9], v[180:181]
	v_pk_mul_f32 v[32:33], v[32:33], v[184:185]
	v_cndmask_b32_e64 v6, v6, v11, s[4:5]
	v_pk_mul_f32 v[8:9], v[8:9], s[82:83] op_sel_hi:[1,0]
	v_pk_mul_f32 v[32:33], v[32:33], s[82:83] op_sel_hi:[1,0]
	v_rsq_f32_e32 v11, v6
	v_cvt_pk_bf16_f32 v9, v8, v9
	v_cvt_pk_bf16_f32 v8, v32, v33
	s_waitcnt vmcnt(2)
	v_pk_mul_f32 v[32:33], v[72:73], v[20:21] op_sel_hi:[1,0]
	v_pk_mul_f32 v[20:21], v[70:71], v[20:21] op_sel_hi:[1,0]
	v_pk_mul_f32 v[32:33], v[32:33], v[206:207]
	v_pk_mul_f32 v[20:21], v[20:21], v[192:193]
	v_pk_mul_f32 v[32:33], v[32:33], s[82:83] op_sel_hi:[1,0]
	v_pk_mul_f32 v[20:21], v[20:21], s[82:83] op_sel_hi:[1,0]
	v_cvt_pk_bf16_f32 v7, v32, v33
	v_cvt_pk_bf16_f32 v6, v20, v21
	v_mul_f32_e32 v20, 0x45800000, v11
	v_cndmask_b32_e64 v20, v11, v20, s[4:5]
	v_pk_mul_f32 v[32:33], v[20:21], v[12:13] op_sel_hi:[0,1]
	v_pk_mul_f32 v[12:13], v[20:21], v[214:215] op_sel_hi:[0,1]
	s_waitcnt vmcnt(1)
; template <int DQK, int DV, bool LEAD> ...
;     ...
;           const float rn = rsqrtf(sn * (1.f / 64.f) + EPS);
; #pragma unroll
;           for (int ds = 0; ds < 2; ++ds)
; #pragma unroll
;               for (int j = 0; j < 8; ++j) x[ds][j] *= rn * qgain[32 * ds + 8 * g4 + j];
;           if constexpr (DQK == 64) {
; #pragma unroll
;               for (int ds = 0; ds < 2; ++ds)
; #pragma unroll
;                   for (int j = 0; j < 8; ++j) {
;                       auto rr = __builtin_amdgcn_permlane32_swap(__float_as_uint(x[ds][j]), __float_as_uint(x[ds][j]), false, false);
;                       const float other = hi ? __uint_as_float(rr[0]) : __uint_as_float(rr[1]);
;                       float cc = 1.f, sg = 0.f;
;                       if (lat) { const f32x2 cs = rope[(ds ? pcol : prow) * 16 + 8 * (g4 & 1) + j]; cc = cs.x; sg = hi ? cs.y : -cs.y; }
;                       x[ds][j] = x[ds][j] * cc + other * sg; }
;           } else {
;               float sr = 0.f;
; #pragma unroll
;               for (int j = 0; j < 8; ++j) sr += x[2][j] * x[2][j];
;               sr = lanes4_sum(sr);
;               const float rq = rsqrtf(sr * (1.f / 32.f) + EPS);
; #pragma unroll
;               for (int j = 0; j < 8; ++j) { const float av = x[2][j] * rq * qgain[64 + 8 * g4 + j];
;                   auto rr = __builtin_amdgcn_permlane16_swap(__float_as_uint(av), __float_as_uint(av), false, false);
;                   const float other = (g4 & 1) ? __uint_as_float(rr[0]) : __uint_as_float(rr[1]);
;                   float cc = 1.f, sg = 0.f;
;                   if (lat) { const f32x2 cs = rope[((g4 & 2) ? pcol : prow) * 8 + j]; cc = cs.x; sg = (g4 & 1) ? cs.y : -cs.y; }
;                   x[2][j] = av * cc + other * sg; }
	v_pk_mul_f32 v[12:13], v[12:13], v[88:89]
	v_cndmask_b32_e64 v183, v101, -v101, vcc
	v_cndmask_b32_e64 v182, v99, -v99, vcc
	v_mov_b32_e32 v99, v100
	v_and_b32_e32 v101, 0xffff0000, v37
	v_lshlrev_b32_e32 v100, 16, v37
	v_cndmask_b32_e64 v209, v97, -v97, vcc
	v_cndmask_b32_e64 v208, v95, -v95, vcc
	v_mov_b32_e32 v95, v96
	v_cndmask_b32_e64 v97, v81, -v81, vcc
	v_cndmask_b32_e64 v96, v79, -v79, vcc
	v_mov_b32_e32 v79, v80
	v_and_b32_e32 v81, 0xffff0000, v36
	v_lshlrev_b32_e32 v80, 16, v36
	v_and_b32_e32 v37, 0xffff0000, v23
	v_lshlrev_b32_e32 v36, 16, v23
	v_pk_mul_f32 v[24:25], v[20:21], v[24:25] op_sel_hi:[0,1]
	v_pk_mul_f32 v[178:179], v[20:21], v[198:199] op_sel_hi:[0,1]
	v_mov_b32_e32 v11, v12
	v_mov_b32_e32 v20, v12
	v_mov_b32_e32 v21, v13
	v_mov_b32_e32 v23, v13
	v_permlane16_swap_b32_e32 v11, v20
	s_nop 0
	v_permlane16_swap_b32_e32 v21, v23
	v_cndmask_b32_e32 v21, v21, v23, vcc
	v_cndmask_b32_e32 v20, v11, v20, vcc
	v_pk_mul_f32 v[20:21], v[212:213], v[20:21]
	v_cndmask_b32_e64 v169, v49, -v49, vcc
	v_pk_fma_f32 v[12:13], v[12:13], v[106:107], v[20:21]
	v_pk_mul_f32 v[20:21], v[178:179], v[86:87]
	v_pk_mul_f32 v[12:13], v[12:13], s[82:83] op_sel_hi:[1,0]
	v_cndmask_b32_e64 v168, v47, -v47, vcc
	v_mov_b32_e32 v47, v48
	v_cndmask_b32_e64 v49, v17, -v17, vcc
	v_cndmask_b32_e64 v48, v15, -v15, vcc
	v_cvt_pk_bf16_f32 v13, v12, v13
	v_mov_b32_e32 v11, v20
	v_mov_b32_e32 v12, v20
	v_mov_b32_e32 v15, v21
	v_mov_b32_e32 v17, v21
	v_permlane16_swap_b32_e32 v11, v12
	s_nop 0
	v_permlane16_swap_b32_e32 v15, v17
	v_cndmask_b32_e32 v107, v15, v17, vcc
	v_cndmask_b32_e32 v106, v11, v12, vcc
	v_pk_mul_f32 v[106:107], v[200:201], v[106:107]
	v_mov_b32_e32 v175, v173
	v_pk_fma_f32 v[20:21], v[20:21], v[102:103], v[106:107]
	s_nop 0
	v_permlane32_swap_b32_e32 v173, v175
	v_pk_mul_f32 v[20:21], v[20:21], s[82:83] op_sel_hi:[1,0]
	v_cndmask_b32_e64 v171, v77, -v77, vcc
	v_cvt_pk_bf16_f32 v12, v20, v21
	s_waitcnt vmcnt(0)
	v_pk_mul_f32 v[20:21], v[92:93], v[32:33]
	v_cndmask_b32_e64 v170, v75, -v75, vcc
	v_mov_b32_e32 v11, v20
	v_mov_b32_e32 v15, v20
	v_mov_b32_e32 v17, v21
	v_mov_b32_e32 v23, v21
	v_permlane16_swap_b32_e32 v11, v15
	s_nop 0
	v_permlane16_swap_b32_e32 v17, v23
	v_cndmask_b32_e32 v33, v17, v23, vcc
	v_cndmask_b32_e32 v32, v11, v15, vcc
	v_pk_mul_f32 v[32:33], v[222:223], v[32:33]
	v_mov_b32_e32 v75, v76
	v_pk_fma_f32 v[18:19], v[18:19], v[20:21], v[32:33]
	v_cndmask_b32_e64 v32, v27, -v27, vcc
	v_pk_mul_f32 v[18:19], v[18:19], s[82:83] op_sel_hi:[1,0]
	v_and_b32_e32 v77, 0xffff0000, v35
	v_cvt_pk_bf16_f32 v11, v18, v19
	v_pk_mul_f32 v[18:19], v[90:91], v[24:25]
	v_and_b32_e32 v25, 0xffff0000, v10
	v_mov_b32_e32 v15, v18
	v_mov_b32_e32 v17, v18
	v_mov_b32_e32 v20, v19
	v_mov_b32_e32 v21, v19
	v_permlane16_swap_b32_e32 v15, v17
	s_nop 0
	v_permlane16_swap_b32_e32 v20, v21
	v_lshlrev_b32_e32 v24, 16, v10
	v_mul_f32_e32 v10, v25, v25
	v_cndmask_b32_e32 v21, v20, v21, vcc
	v_cndmask_b32_e32 v20, v15, v17, vcc
	v_mov_b32_e32 v15, v16
	v_pk_fma_f32 v[16:17], v[24:25], v[24:25], v[10:11] op_sel_hi:[1,1,0]
	v_mul_f32_e32 v10, v229, v229
	v_pk_fma_f32 v[16:17], v[228:229], v[228:229], v[16:17]
	v_pk_mul_f32 v[14:15], v[14:15], v[18:19]
	v_pk_add_f32 v[16:17], v[10:11], v[16:17] op_sel_hi:[0,1]
	v_pk_fma_f32 v[16:17], v[210:211], v[210:211], v[16:17]
	v_mul_f32_e32 v10, v211, v211
	v_pk_add_f32 v[16:17], v[10:11], v[16:17] op_sel_hi:[0,1]
	v_pk_fma_f32 v[16:17], v[204:205], v[204:205], v[16:17]
	v_mul_f32_e32 v10, v205, v205
	v_pk_add_f32 v[16:17], v[10:11], v[16:17] op_sel_hi:[0,1]
	v_mov_b32_e32 v10, v16
	s_nop 1
	v_permlane16_swap_b32_e32 v16, v10
	v_add_f32_e32 v172, v16, v10
	v_mov_b32_e32 v174, v172
	s_nop 1
	v_permlane32_swap_b32_e32 v172, v174
	v_pk_add_f32 v[16:17], v[172:173], v[174:175]
	v_pk_fma_f32 v[14:15], v[48:49], v[20:21], v[14:15]
	v_pk_fma_f32 v[18:19], v[16:17], s[6:7], v[44:45] op_sel_hi:[1,1,0]
	v_pk_mul_f32 v[14:15], v[14:15], s[82:83] op_sel_hi:[1,0]
	v_mul_f32_e32 v10, 0x4b800000, v19
	v_cmp_gt_f32_e64 s[4:5], s95, v19
	v_mul_f32_e32 v23, 0x4b800000, v18
	v_lshlrev_b32_e32 v76, 16, v35
	v_cndmask_b32_e64 v10, v19, v10, s[4:5]
	v_rsq_f32_e32 v16, v10
	v_cvt_pk_bf16_f32 v10, v14, v15
	v_cndmask_b32_e64 v33, v29, -v29, vcc
	v_mov_b32_e32 v163, v161
	v_mul_f32_e32 v14, 0x45800000, v16
	v_cndmask_b32_e64 v48, v16, v14, s[4:5]
	v_pk_mul_f32 v[14:15], v[56:57], v[48:49] op_sel_hi:[1,0]
	v_pk_mul_f32 v[20:21], v[58:59], v[48:49] op_sel_hi:[1,0]
	v_pk_mul_f32 v[14:15], v[14:15], v[146:147]
	v_pk_mul_f32 v[20:21], v[20:21], v[152:153]
	v_pk_mul_f32 v[14:15], v[14:15], s[82:83] op_sel_hi:[1,0]
	v_pk_mul_f32 v[20:21], v[20:21], s[82:83] op_sel_hi:[1,0]
	v_cvt_pk_bf16_f32 v17, v14, v15
	v_pk_mul_f32 v[14:15], v[54:55], v[48:49] op_sel_hi:[1,0]
	v_cmp_gt_f32_e64 s[4:5], s95, v18
	v_pk_mul_f32 v[14:15], v[14:15], v[148:149]
	v_pk_mul_f32 v[102:103], v[66:67], v[48:49] op_sel_hi:[1,0]
	v_pk_mul_f32 v[14:15], v[14:15], s[82:83] op_sel_hi:[1,0]
	v_cndmask_b32_e64 v18, v18, v23, s[4:5]
	v_cvt_pk_bf16_f32 v16, v14, v15
	v_pk_mul_f32 v[14:15], v[60:61], v[48:49] op_sel_hi:[1,0]
	v_pk_mul_f32 v[102:103], v[102:103], v[156:157]
	v_pk_mul_f32 v[14:15], v[14:15], v[150:151]
	v_rsq_f32_e32 v23, v18
	v_pk_mul_f32 v[14:15], v[14:15], s[82:83] op_sel_hi:[1,0]
	v_pk_mul_f32 v[102:103], v[102:103], s[82:83] op_sel_hi:[1,0]
	v_cvt_pk_bf16_f32 v15, v14, v15
	v_cvt_pk_bf16_f32 v14, v20, v21
	v_pk_mul_f32 v[20:21], v[68:69], v[48:49] op_sel_hi:[1,0]
	v_mul_f32_e32 v27, 0x45800000, v23
	v_pk_mul_f32 v[20:21], v[20:21], v[154:155]
	v_permlane32_swap_b32_e32 v161, v163
	v_pk_mul_f32 v[20:21], v[20:21], s[82:83] op_sel_hi:[1,0]
	v_mov_b32_e32 v143, v141
; __device__ __forceinline__ unsigned cvtpk(float lo, float hi) { f32x2 v = {lo, hi}; bf16x2_t b = __builtin_convertvector(v, bf16x2_t); return __builtin_bit_cast(unsigned, b); }
; template <int DQK, int DV, bool LEAD> ...
;     ...
;           const float rn = rsqrtf(sn * (1.f / 64.f) + EPS);
; #pragma unroll
;           for (int ds = 0; ds < 2; ++ds)
; #pragma unroll
;               for (int j = 0; j < 8; ++j) x[ds][j] *= rn * qgain[32 * ds + 8 * g4 + j];
;           if constexpr (DQK == 64) {
; #pragma unroll
;               for (int ds = 0; ds < 2; ++ds)
; #pragma unroll
;                   for (int j = 0; j < 8; ++j) {
;                       auto rr = __builtin_amdgcn_permlane32_swap(__float_as_uint(x[ds][j]), __float_as_uint(x[ds][j]), false, false);
;                       const float other = hi ? __uint_as_float(rr[0]) : __uint_as_float(rr[1]);
;                       float cc = 1.f, sg = 0.f;
;                       if (lat) { const f32x2 cs = rope[(ds ? pcol : prow) * 16 + 8 * (g4 & 1) + j]; cc = cs.x; sg = hi ? cs.y : -cs.y; }
;                       x[ds][j] = x[ds][j] * cc + other * sg; }
;           } else {
;               float sr = 0.f;
; #pragma unroll
;               for (int j = 0; j < 8; ++j) sr += x[2][j] * x[2][j];
;               sr = lanes4_sum(sr);
;               const float rq = rsqrtf(sr * (1.f / 32.f) + EPS);
; #pragma unroll
;               for (int j = 0; j < 8; ++j) { const float av = x[2][j] * rq * qgain[64 + 8 * g4 + j];
;                   auto rr = __builtin_amdgcn_permlane16_swap(__float_as_uint(av), __float_as_uint(av), false, false);
;                   const float other = (g4 & 1) ? __uint_as_float(rr[0]) : __uint_as_float(rr[1]);
;                   float cc = 1.f, sg = 0.f;
;                   if (lat) { const f32x2 cs = rope[((g4 & 2) ? pcol : prow) * 8 + j]; cc = cs.x; sg = (g4 & 1) ? cs.y : -cs.y; }
;                   x[2][j] = av * cc + other * sg; }
;           }
; #pragma unroll
;           for (int ds = 0; ds < NDS; ++ds) { u32x4 w;
; #pragma unroll
;               for (int i = 0; i < 4; ++i) w[i] = cvtpk(x[ds][2 * i] * c2, x[ds][2 * i + 1] * c2);
;               qf[qb * NDS + ds] = __builtin_bit_cast(bf16x8, w); }
	v_cvt_pk_bf16_f32 v21, v20, v21
	v_cvt_pk_bf16_f32 v20, v102, v103
	v_pk_mul_f32 v[102:103], v[72:73], v[48:49] op_sel_hi:[1,0]
	v_pk_mul_f32 v[48:49], v[70:71], v[48:49] op_sel_hi:[1,0]
	v_pk_mul_f32 v[102:103], v[102:103], v[158:159]
	v_pk_mul_f32 v[48:49], v[48:49], v[166:167]
	v_pk_mul_f32 v[102:103], v[102:103], s[82:83] op_sel_hi:[1,0]
	v_pk_mul_f32 v[48:49], v[48:49], s[82:83] op_sel_hi:[1,0]
	v_cvt_pk_bf16_f32 v19, v102, v103
	v_cvt_pk_bf16_f32 v18, v48, v49
	v_cndmask_b32_e64 v48, v23, v27, s[4:5]
	v_pk_mul_f32 v[102:103], v[48:49], v[24:25] op_sel_hi:[0,1]
	v_pk_mul_f32 v[24:25], v[48:49], v[204:205] op_sel_hi:[0,1]
	v_pk_mul_f32 v[24:25], v[88:89], v[24:25]
	v_pk_mul_f32 v[106:107], v[48:49], v[228:229] op_sel_hi:[0,1]
	v_mov_b32_e32 v23, v24
	v_mov_b32_e32 v27, v24
	v_mov_b32_e32 v29, v25
	v_mov_b32_e32 v35, v25
	v_permlane16_swap_b32_e32 v23, v27
	s_nop 0
	v_permlane16_swap_b32_e32 v29, v35
	v_pk_mul_f32 v[146:147], v[48:49], v[210:211] op_sel_hi:[0,1]
	v_cndmask_b32_e32 v49, v29, v35, vcc
	v_cndmask_b32_e32 v48, v23, v27, vcc
	v_pk_mul_f32 v[48:49], v[182:183], v[48:49]
	v_permlane32_swap_b32_e32 v141, v143
	v_pk_fma_f32 v[24:25], v[24:25], v[98:99], v[48:49]
	v_pk_mul_f32 v[48:49], v[86:87], v[146:147]
	v_pk_mul_f32 v[24:25], v[24:25], s[82:83] op_sel_hi:[1,0]
	v_mov_b32_e32 v23, v48
	v_cvt_pk_bf16_f32 v25, v24, v25
	v_mov_b32_e32 v24, v48
	v_mov_b32_e32 v27, v49
	v_mov_b32_e32 v29, v49
	v_permlane16_swap_b32_e32 v23, v24
	s_nop 0
	v_permlane16_swap_b32_e32 v27, v29
	v_cndmask_b32_e32 v99, v27, v29, vcc
	v_cndmask_b32_e32 v98, v23, v24, vcc
	v_pk_mul_f32 v[98:99], v[208:209], v[98:99]
	s_nop 0
	v_pk_fma_f32 v[48:49], v[94:95], v[48:49], v[98:99]
	v_or_b32_e32 v206, 4, v194
	v_pk_mul_f32 v[48:49], v[48:49], s[82:83] op_sel_hi:[1,0]
	v_lshlrev_b32_e32 v207, 7, v221
	v_cvt_pk_bf16_f32 v24, v48, v49
	v_pk_mul_f32 v[48:49], v[92:93], v[106:107]
	v_lshrrev_b32_e32 v106, 1, v220
	v_mov_b32_e32 v23, v48
	v_mov_b32_e32 v27, v48
	v_mov_b32_e32 v29, v49
	v_mov_b32_e32 v35, v49
	v_permlane16_swap_b32_e32 v23, v27
	s_nop 0
	v_permlane16_swap_b32_e32 v29, v35
	v_cndmask_b32_e32 v95, v29, v35, vcc
	v_cndmask_b32_e32 v94, v23, v27, vcc
	v_pk_mul_f32 v[30:31], v[30:31], v[48:49]
	s_nop 0
	v_pk_fma_f32 v[30:31], v[176:177], v[94:95], v[30:31]
	v_cndmask_b32_e64 v94, v63, -v63, vcc
	v_pk_mul_f32 v[30:31], v[30:31], s[82:83] op_sel_hi:[1,0]
	v_cndmask_b32_e64 v95, v65, -v65, vcc
	v_cvt_pk_bf16_f32 v23, v30, v31
	v_pk_mul_f32 v[30:31], v[90:91], v[102:103]
	s_nop 0
	v_mov_b32_e32 v27, v30
	v_mov_b32_e32 v29, v30
	v_mov_b32_e32 v35, v31
	v_mov_b32_e32 v48, v31
	v_permlane16_swap_b32_e32 v27, v29
	s_nop 0
	v_permlane16_swap_b32_e32 v35, v48
	v_cndmask_b32_e32 v49, v35, v48, vcc
	v_cndmask_b32_e32 v48, v27, v29, vcc
	v_mov_b32_e32 v27, v28
	v_pk_mul_f32 v[26:27], v[26:27], v[30:31]
	s_nop 0
	v_pk_fma_f32 v[26:27], v[32:33], v[48:49], v[26:27]
	v_and_b32_e32 v49, 0xffff0000, v22
	v_lshlrev_b32_e32 v48, 16, v22
	v_mul_f32_e32 v22, v49, v49
	v_pk_fma_f32 v[28:29], v[48:49], v[48:49], v[22:23] op_sel_hi:[1,1,0]
	v_mul_f32_e32 v22, v37, v37
	v_pk_fma_f32 v[28:29], v[36:37], v[36:37], v[28:29]
	v_pk_mul_f32 v[26:27], v[26:27], s[82:83] op_sel_hi:[1,0]
	v_pk_add_f32 v[28:29], v[22:23], v[28:29] op_sel_hi:[0,1]
	v_pk_fma_f32 v[28:29], v[104:105], v[104:105], v[28:29]
	v_mul_f32_e32 v22, v105, v105
	v_pk_add_f32 v[28:29], v[22:23], v[28:29] op_sel_hi:[0,1]
	v_pk_fma_f32 v[28:29], v[164:165], v[164:165], v[28:29]
	v_mul_f32_e32 v22, v165, v165
	v_pk_add_f32 v[28:29], v[22:23], v[28:29] op_sel_hi:[0,1]
	v_mov_b32_e32 v22, v28
	s_nop 1
	v_permlane16_swap_b32_e32 v28, v22
	v_add_f32_e32 v160, v28, v22
	v_mov_b32_e32 v162, v160
	s_nop 1
	v_permlane32_swap_b32_e32 v160, v162
	v_pk_add_f32 v[28:29], v[160:161], v[162:163]
	s_nop 0
	v_pk_fma_f32 v[30:31], v[28:29], s[6:7], v[44:45] op_sel_hi:[1,1,0]
	s_nop 0
	v_mul_f32_e32 v22, 0x4b800000, v31
	v_cmp_gt_f32_e64 s[4:5], s95, v31
	v_mul_f32_e32 v35, 0x4b800000, v30
	s_nop 0
	v_cndmask_b32_e64 v22, v31, v22, s[4:5]
	v_rsq_f32_e32 v28, v22
	v_cvt_pk_bf16_f32 v22, v26, v27
	v_mul_f32_e32 v26, 0x45800000, v28
	v_cndmask_b32_e64 v98, v28, v26, s[4:5]
	v_pk_mul_f32 v[26:27], v[56:57], v[98:99] op_sel_hi:[1,0]
	v_pk_mul_f32 v[32:33], v[58:59], v[98:99] op_sel_hi:[1,0]
	v_pk_mul_f32 v[26:27], v[26:27], v[124:125]
	v_pk_mul_f32 v[32:33], v[32:33], v[130:131]
	v_pk_mul_f32 v[26:27], v[26:27], s[82:83] op_sel_hi:[1,0]
	v_pk_mul_f32 v[32:33], v[32:33], s[82:83] op_sel_hi:[1,0]
	v_cvt_pk_bf16_f32 v29, v26, v27
	v_pk_mul_f32 v[26:27], v[54:55], v[98:99] op_sel_hi:[1,0]
	v_cmp_gt_f32_e64 s[4:5], s95, v30
	v_pk_mul_f32 v[26:27], v[26:27], v[126:127]
	v_pk_mul_f32 v[102:103], v[66:67], v[98:99] op_sel_hi:[1,0]
	v_pk_mul_f32 v[26:27], v[26:27], s[82:83] op_sel_hi:[1,0]
	v_cndmask_b32_e64 v30, v30, v35, s[4:5]
	v_cvt_pk_bf16_f32 v28, v26, v27
	v_pk_mul_f32 v[26:27], v[60:61], v[98:99] op_sel_hi:[1,0]
	v_pk_mul_f32 v[102:103], v[102:103], v[136:137]
	v_pk_mul_f32 v[26:27], v[26:27], v[128:129]
	v_rsq_f32_e32 v35, v30
	v_pk_mul_f32 v[26:27], v[26:27], s[82:83] op_sel_hi:[1,0]
	v_pk_mul_f32 v[102:103], v[102:103], s[82:83] op_sel_hi:[1,0]
	v_cvt_pk_bf16_f32 v27, v26, v27
	v_cvt_pk_bf16_f32 v26, v32, v33
	v_pk_mul_f32 v[32:33], v[68:69], v[98:99] op_sel_hi:[1,0]
	v_mul_f32_e32 v63, 0x45800000, v35
	v_pk_mul_f32 v[32:33], v[32:33], v[132:133]
	s_nop 0
	v_pk_mul_f32 v[32:33], v[32:33], s[82:83] op_sel_hi:[1,0]
	s_nop 0
	v_cvt_pk_bf16_f32 v33, v32, v33
	v_cvt_pk_bf16_f32 v32, v102, v103
	v_pk_mul_f32 v[102:103], v[72:73], v[98:99] op_sel_hi:[1,0]
	v_pk_mul_f32 v[98:99], v[70:71], v[98:99] op_sel_hi:[1,0]
	v_pk_mul_f32 v[102:103], v[102:103], v[138:139]
; __device__ __forceinline__ unsigned cvtpk(float lo, float hi) { f32x2 v = {lo, hi}; bf16x2_t b = __builtin_convertvector(v, bf16x2_t); return __builtin_bit_cast(unsigned, b); }
; template <int DQK, int DV, bool LEAD> ...
;     ...
;           const float rn = rsqrtf(sn * (1.f / 64.f) + EPS);
; #pragma unroll
;           for (int ds = 0; ds < 2; ++ds)
; #pragma unroll
;               for (int j = 0; j < 8; ++j) x[ds][j] *= rn * qgain[32 * ds + 8 * g4 + j];
;           if constexpr (DQK == 64) {
; #pragma unroll
;               for (int ds = 0; ds < 2; ++ds)
; #pragma unroll
;                   for (int j = 0; j < 8; ++j) {
;                       auto rr = __builtin_amdgcn_permlane32_swap(__float_as_uint(x[ds][j]), __float_as_uint(x[ds][j]), false, false);
;                       const float other = hi ? __uint_as_float(rr[0]) : __uint_as_float(rr[1]);
;                       float cc = 1.f, sg = 0.f;
;                       if (lat) { const f32x2 cs = rope[(ds ? pcol : prow) * 16 + 8 * (g4 & 1) + j]; cc = cs.x; sg = hi ? cs.y : -cs.y; }
;                       x[ds][j] = x[ds][j] * cc + other * sg; }
;           } else {
;               float sr = 0.f;
; #pragma unroll
;               for (int j = 0; j < 8; ++j) sr += x[2][j] * x[2][j];
;               sr = lanes4_sum(sr);
;               const float rq = rsqrtf(sr * (1.f / 32.f) + EPS);
; #pragma unroll
;               for (int j = 0; j < 8; ++j) { const float av = x[2][j] * rq * qgain[64 + 8 * g4 + j];
;                   auto rr = __builtin_amdgcn_permlane16_swap(__float_as_uint(av), __float_as_uint(av), false, false);
;                   const float other = (g4 & 1) ? __uint_as_float(rr[0]) : __uint_as_float(rr[1]);
;                   float cc = 1.f, sg = 0.f;
;                   if (lat) { const f32x2 cs = rope[((g4 & 2) ? pcol : prow) * 8 + j]; cc = cs.x; sg = (g4 & 1) ? cs.y : -cs.y; }
;                   x[2][j] = av * cc + other * sg; }
;           }
; #pragma unroll
;           for (int ds = 0; ds < NDS; ++ds) { u32x4 w;
; #pragma unroll
;               for (int i = 0; i < 4; ++i) w[i] = cvtpk(x[ds][2 * i] * c2, x[ds][2 * i + 1] * c2);
;               qf[qb * NDS + ds] = __builtin_bit_cast(bf16x8, w); }
	v_pk_mul_f32 v[98:99], v[98:99], v[144:145]
	v_pk_mul_f32 v[102:103], v[102:103], s[82:83] op_sel_hi:[1,0]
	v_pk_mul_f32 v[98:99], v[98:99], s[82:83] op_sel_hi:[1,0]
	v_cvt_pk_bf16_f32 v31, v102, v103
	v_cvt_pk_bf16_f32 v30, v98, v99
	v_cndmask_b32_e64 v98, v35, v63, s[4:5]
	v_pk_mul_f32 v[102:103], v[98:99], v[36:37] op_sel_hi:[0,1]
	v_pk_mul_f32 v[36:37], v[98:99], v[164:165] op_sel_hi:[0,1]
	v_pk_mul_f32 v[36:37], v[88:89], v[36:37]
	v_pk_mul_f32 v[48:49], v[98:99], v[48:49] op_sel_hi:[0,1]
	v_pk_mul_f32 v[104:105], v[98:99], v[104:105] op_sel_hi:[0,1]
	v_mov_b32_e32 v35, v36
	v_mov_b32_e32 v63, v36
	v_mov_b32_e32 v65, v37
	v_mov_b32_e32 v98, v37
	v_permlane16_swap_b32_e32 v35, v63
	s_nop 0
	v_permlane16_swap_b32_e32 v65, v98
	v_cndmask_b32_e32 v99, v65, v98, vcc
	v_cndmask_b32_e32 v98, v35, v63, vcc
	v_pk_mul_f32 v[98:99], v[108:109], v[98:99]
	v_pk_mul_f32 v[48:49], v[90:91], v[48:49]
	v_pk_fma_f32 v[36:37], v[36:37], v[82:83], v[98:99]
	v_pk_mul_f32 v[82:83], v[86:87], v[104:105]
	v_pk_mul_f32 v[36:37], v[36:37], s[82:83] op_sel_hi:[1,0]
	v_mov_b32_e32 v35, v82
	v_cvt_pk_bf16_f32 v37, v36, v37
	v_mov_b32_e32 v36, v82
	v_mov_b32_e32 v63, v83
	v_mov_b32_e32 v65, v83
	v_permlane16_swap_b32_e32 v35, v36
	s_nop 0
	v_permlane16_swap_b32_e32 v63, v65
	v_cndmask_b32_e32 v99, v63, v65, vcc
	v_cndmask_b32_e32 v98, v35, v36, vcc
	v_pk_mul_f32 v[96:97], v[96:97], v[98:99]
	s_nop 0
	v_pk_fma_f32 v[78:79], v[78:79], v[82:83], v[96:97]
	s_nop 0
	v_pk_mul_f32 v[78:79], v[78:79], s[82:83] op_sel_hi:[1,0]
	s_nop 0
	v_cvt_pk_bf16_f32 v36, v78, v79
	v_pk_mul_f32 v[78:79], v[92:93], v[102:103]
	s_nop 0
	v_mov_b32_e32 v35, v78
	v_mov_b32_e32 v63, v78
	v_mov_b32_e32 v65, v79
	v_mov_b32_e32 v82, v79
	v_permlane16_swap_b32_e32 v35, v63
	s_nop 0
	v_permlane16_swap_b32_e32 v65, v82
	v_cndmask_b32_e32 v83, v65, v82, vcc
	v_cndmask_b32_e32 v82, v35, v63, vcc
	v_pk_mul_f32 v[74:75], v[74:75], v[78:79]
	v_mov_b32_e32 v63, v48
	v_pk_fma_f32 v[74:75], v[170:171], v[82:83], v[74:75]
	v_mov_b32_e32 v65, v48
	v_pk_mul_f32 v[74:75], v[74:75], s[82:83] op_sel_hi:[1,0]
	s_nop 0
	v_permlane16_swap_b32_e32 v63, v65
	v_cvt_pk_bf16_f32 v35, v74, v75
	v_mov_b32_e32 v74, v49
	v_mov_b32_e32 v75, v49
	s_nop 1
	v_permlane16_swap_b32_e32 v74, v75
	v_cndmask_b32_e32 v75, v74, v75, vcc
	v_cndmask_b32_e32 v74, v63, v65, vcc
	v_mov_b32_e32 v63, v64
	v_pk_mul_f32 v[48:49], v[62:63], v[48:49]
	v_and_b32_e32 v63, 0xffff0000, v34
	v_lshlrev_b32_e32 v62, 16, v34
	v_mul_f32_e32 v34, v63, v63
	v_pk_fma_f32 v[64:65], v[62:63], v[62:63], v[34:35] op_sel_hi:[1,1,0]
	v_mul_f32_e32 v34, v77, v77
	v_pk_fma_f32 v[64:65], v[76:77], v[76:77], v[64:65]
	v_pk_fma_f32 v[48:49], v[94:95], v[74:75], v[48:49]
	v_pk_add_f32 v[64:65], v[34:35], v[64:65] op_sel_hi:[0,1]
	v_pk_fma_f32 v[64:65], v[80:81], v[80:81], v[64:65]
	v_mul_f32_e32 v34, v81, v81
	v_pk_add_f32 v[64:65], v[34:35], v[64:65] op_sel_hi:[0,1]
	v_pk_fma_f32 v[64:65], v[100:101], v[100:101], v[64:65]
	v_mul_f32_e32 v34, v101, v101
	v_pk_add_f32 v[64:65], v[34:35], v[64:65] op_sel_hi:[0,1]
	v_mov_b32_e32 v34, v64
	s_nop 1
	v_permlane16_swap_b32_e32 v64, v34
	v_add_f32_e32 v140, v64, v34
	v_mov_b32_e32 v142, v140
	s_nop 1
	v_permlane32_swap_b32_e32 v140, v142
	v_pk_add_f32 v[64:65], v[140:141], v[142:143]
	v_pk_mul_f32 v[48:49], v[48:49], s[82:83] op_sel_hi:[1,0]
	v_pk_fma_f32 v[44:45], v[64:65], s[6:7], v[44:45] op_sel_hi:[1,1,0]
	v_lshlrev_b32_e32 v78, 5, v238
	v_mul_f32_e32 v34, 0x4b800000, v45
	v_cmp_gt_f32_e64 s[4:5], s95, v45
	v_lshlrev_b32_e32 v79, 6, v236
	v_bitop3_b32 v78, v78, v220, 48 bitop3:0x78
	v_cndmask_b32_e64 v34, v45, v34, s[4:5]
	v_rsq_f32_e32 v45, v34
	v_cvt_pk_bf16_f32 v34, v48, v49
	v_cndmask_b32_e64 v48, v51, -v51, vcc
	v_cndmask_b32_e64 v49, v53, -v53, vcc
	v_mul_f32_e32 v51, 0x45800000, v45
	v_cndmask_b32_e64 v64, v45, v51, s[4:5]
	v_mul_f32_e32 v45, 0x4b800000, v44
	v_cmp_gt_f32_e64 s[4:5], s95, v44
	v_pk_mul_f32 v[58:59], v[58:59], v[64:65] op_sel_hi:[1,0]
	v_pk_mul_f32 v[60:61], v[60:61], v[64:65] op_sel_hi:[1,0]
	v_cndmask_b32_e64 v44, v44, v45, s[4:5]
	v_pk_mul_f32 v[54:55], v[54:55], v[64:65] op_sel_hi:[1,0]
	v_rsq_f32_e32 v51, v44
	v_pk_mul_f32 v[58:59], v[58:59], v[116:117]
	v_pk_mul_f32 v[60:61], v[60:61], v[114:115]
	v_pk_mul_f32 v[74:75], v[54:55], v[112:113]
	v_pk_mul_f32 v[54:55], v[56:57], v[64:65] op_sel_hi:[1,0]
	v_pk_mul_f32 v[70:71], v[70:71], v[64:65] op_sel_hi:[1,0]
	v_pk_mul_f32 v[72:73], v[72:73], v[64:65] op_sel_hi:[1,0]
	v_pk_mul_f32 v[66:67], v[66:67], v[64:65] op_sel_hi:[1,0]
	v_pk_mul_f32 v[68:69], v[68:69], v[64:65] op_sel_hi:[1,0]
	v_pk_mul_f32 v[64:65], v[54:55], v[110:111]
	v_pk_mul_f32 v[58:59], v[58:59], s[82:83] op_sel_hi:[1,0]
	v_pk_mul_f32 v[60:61], v[60:61], s[82:83] op_sel_hi:[1,0]
	v_cvt_pk_bf16_f32 v58, v58, v59
	v_cvt_pk_bf16_f32 v59, v60, v61
	v_pk_mul_f32 v[60:61], v[74:75], s[82:83] op_sel_hi:[1,0]
	v_pk_mul_f32 v[44:45], v[64:65], s[82:83] op_sel_hi:[1,0]
	v_cvt_pk_bf16_f32 v60, v60, v61
	v_cvt_pk_bf16_f32 v61, v44, v45
	v_mul_f32_e32 v44, 0x45800000, v51
	v_cndmask_b32_e64 v44, v51, v44, s[4:5]
	v_pk_mul_f32 v[62:63], v[44:45], v[62:63] op_sel_hi:[0,1]
	v_pk_mul_f32 v[62:63], v[90:91], v[62:63]
	v_pk_mul_f32 v[70:71], v[70:71], v[134:135]
	v_mov_b32_e32 v45, v62
	v_mov_b32_e32 v51, v62
	v_mov_b32_e32 v53, v63
	v_mov_b32_e32 v64, v63
	v_permlane16_swap_b32_e32 v45, v51
	s_nop 0
	v_permlane16_swap_b32_e32 v53, v64
	v_cndmask_b32_e32 v65, v53, v64, vcc
	v_cndmask_b32_e32 v64, v45, v51, vcc
	v_mov_b32_e32 v51, v52
	v_pk_mul_f32 v[50:51], v[50:51], v[62:63]
	v_pk_mul_f32 v[72:73], v[72:73], v[122:123]
	v_pk_fma_f32 v[48:49], v[48:49], v[64:65], v[50:51]
; __device__ __forceinline__ unsigned cvtpk(float lo, float hi) { f32x2 v = {lo, hi}; bf16x2_t b = __builtin_convertvector(v, bf16x2_t); return __builtin_bit_cast(unsigned, b); }
; #define ATT_SB() __builtin_amdgcn_sched_barrier(0)
; #define ATT_DMA_K(t, sl) do { glds16(ksrc + (size_t)(t) * 64 * kpitch, (unsigned)__builtin_amdgcn_readfirstlane(kdst + (sl) * KSLOT)); \
;         if constexpr (DQK == 96) glds16(krsrc + (size_t)(t) * 64 * 32, (unsigned)__builtin_amdgcn_readfirstlane(krdst + (sl) * KSLOT)); } while (0)
; #define ATT_DMA_V(t, sl) do { glds16(vsrc + (size_t)(t) * 64, (unsigned)__builtin_amdgcn_readfirstlane(vdst + (sl) * VSLOT)); \
;         if constexpr (DV == 128) glds16(vsrc + (size_t)64 * NR + (size_t)(t) * 64, (unsigned)__builtin_amdgcn_readfirstlane(vdst + (sl) * VSLOT + 8192)); } while (0)
; #define ATT_KLOAD(sl) do { _Pragma("unroll") for (int kb_ = 0; kb_ < NKW; ++kb_) _Pragma("unroll") for (int ds_ = 0; ds_ < NDS; ++ds_) { \
;         if (ds_ < 2) kf[kb_ * NDS + ds_] = *(const LAS bf16x8*)(kp[ds_ & 1] + (sl) * KSLOT + (kb_ & 1) * 512 + (kb_ >> 1) * 4096); \
;         else kf[kb_ * NDS + ds_] = *(const LAS bf16x8*)(krp + (sl) * KSLOT + (kb_ & 1) * 256 + (kb_ >> 1) * 2048); } } while (0)
; template <int DQK, int DV, bool LEAD> ...
;     ...
;           for (int ds = 0; ds < NDS; ++ds) { u32x4 w;
; #pragma unroll
;               for (int i = 0; i < 4; ++i) w[i] = cvtpk(x[ds][2 * i] * c2, x[ds][2 * i + 1] * c2);
;               qf[qb * NDS + ds] = __builtin_bit_cast(bf16x8, w); }
;       }
; #pragma unroll
;       for (int d0 = 0; d0 < NQB * NDS; ++d0) asm volatile("" : "+v"(qf[d0])); }
;     wait_bar<0>();
;     bf16x8 kf[NKW * NDS], vf[NVF];
;     ATT_KLOAD(0);
;     asm volatile("s_waitcnt lgkmcnt(0)\n\ts_barrier" ::: "memory");
;     float lsum[NQB];
; #pragma unroll
;     for (int qb = 0; qb < NQB; ++qb) lsum[qb] = 0.f;
;     const f32x4 zero4 = {0.f, 0.f, 0.f, 0.f};
;     f32x4 o[NDB][NQB], c[NKW][NQB]; u32x4 pw[4];
; #pragma unroll
;     for (int i = 0; i < NDB; ++i)
; #pragma unroll
;         for (int qb = 0; qb < NQB; ++qb) o[i][qb] = zero4;
;     ATT_DMA_K(3, 0); ATT_DMA_V(1, 1);
;     ATT_QK(); ATT_SB();
	v_pk_mul_f32 v[50:51], v[44:45], v[76:77] op_sel_hi:[0,1]
	v_pk_mul_f32 v[50:51], v[92:93], v[50:51]
	v_pk_mul_f32 v[66:67], v[66:67], v[120:121]
	v_mov_b32_e32 v45, v50
	v_mov_b32_e32 v52, v50
	s_nop 1
	v_permlane16_swap_b32_e32 v45, v52
	v_mov_b32_e32 v53, v51
	v_mov_b32_e32 v62, v51
	s_nop 1
	v_permlane16_swap_b32_e32 v53, v62
	v_pk_mul_f32 v[46:47], v[46:47], v[50:51]
	v_pk_mul_f32 v[50:51], v[44:45], v[80:81] op_sel_hi:[0,1]
	v_cndmask_b32_e32 v53, v53, v62, vcc
	v_cndmask_b32_e32 v52, v45, v52, vcc
	v_pk_mul_f32 v[50:51], v[86:87], v[50:51]
	v_pk_fma_f32 v[46:47], v[168:169], v[52:53], v[46:47]
	v_mov_b32_e32 v45, v50
	v_mov_b32_e32 v52, v50
	v_mov_b32_e32 v53, v51
	v_mov_b32_e32 v62, v51
	v_permlane16_swap_b32_e32 v45, v52
	s_nop 0
	v_permlane16_swap_b32_e32 v53, v62
	v_cndmask_b32_e32 v53, v53, v62, vcc
	v_cndmask_b32_e32 v52, v45, v52, vcc
	v_pk_mul_f32 v[40:41], v[40:41], v[52:53]
	v_pk_mul_f32 v[68:69], v[68:69], v[118:119]
	v_pk_fma_f32 v[40:41], v[42:43], v[50:51], v[40:41]
	v_pk_mul_f32 v[42:43], v[44:45], v[100:101] op_sel_hi:[0,1]
	v_pk_mul_f32 v[42:43], v[88:89], v[42:43]
	v_pk_mul_f32 v[54:55], v[70:71], s[82:83] op_sel_hi:[1,0]
	v_mov_b32_e32 v44, v42
	v_mov_b32_e32 v50, v42
	v_mov_b32_e32 v45, v43
	v_mov_b32_e32 v51, v43
	v_permlane16_swap_b32_e32 v44, v50
	s_nop 0
	v_permlane16_swap_b32_e32 v45, v51
	v_cndmask_b32_e32 v45, v45, v51, vcc
	v_cndmask_b32_e32 v44, v44, v50, vcc
	v_pk_mul_f32 v[44:45], v[84:85], v[44:45]
	v_pk_mul_f32 v[56:57], v[72:73], s[82:83] op_sel_hi:[1,0]
	v_pk_fma_f32 v[42:43], v[42:43], v[38:39], v[44:45]
	v_cvt_pk_bf16_f32 v54, v54, v55
	v_cvt_pk_bf16_f32 v55, v56, v57
	v_pk_mul_f32 v[56:57], v[66:67], s[82:83] op_sel_hi:[1,0]
	v_pk_mul_f32 v[66:67], v[68:69], s[82:83] op_sel_hi:[1,0]
	v_pk_mul_f32 v[38:39], v[48:49], s[82:83] op_sel_hi:[1,0]
	v_pk_mul_f32 v[44:45], v[46:47], s[82:83] op_sel_hi:[1,0]
	v_pk_mul_f32 v[40:41], v[40:41], s[82:83] op_sel_hi:[1,0]
	v_pk_mul_f32 v[42:43], v[42:43], s[82:83] op_sel_hi:[1,0]
	v_cvt_pk_bf16_f32 v56, v56, v57
	v_cvt_pk_bf16_f32 v57, v66, v67
	v_cvt_pk_bf16_f32 v38, v38, v39
	v_cvt_pk_bf16_f32 v39, v44, v45
	v_cvt_pk_bf16_f32 v40, v40, v41
	v_cvt_pk_bf16_f32 v41, v42, v43
	s_waitcnt vmcnt(0) lgkmcnt(0)
	s_barrier
	ds_read_b128 v[42:45], v219
	ds_read_b128 v[46:49], v219 offset:512
	v_bitop3_b32 v70, v240, v206, v239 bitop3:0x36
	v_lshl_add_u32 v208, v70, 4, v241
	s_waitcnt lgkmcnt(1)
	v_mfma_f32_16x16x32_bf16 v[50:53], v[42:45], v[6:9], 0
	ds_read_b128 v[70:73], v208
	ds_read_b128 v[74:77], v208 offset:512
	s_lshl_b32 s4, s16, 11
	v_sub_u32_e32 v79, v237, v79
	v_mfma_f32_16x16x32_bf16 v[62:65], v[42:45], v[18:21], 0
	v_add3_u32 v209, v79, v78, s4
	s_mov_b64 s[4:5], 0x60000
	s_lshl_b32 s6, s24, 6
	v_mfma_f32_16x16x32_bf16 v[66:69], v[42:45], v[30:33], 0
	s_cmpk_lt_u32 s38, 0x100
	s_cselect_b64 vcc, -1, 0
	s_mov_b32 s16, 1
	v_mfma_f32_16x16x32_bf16 v[42:45], v[42:45], v[54:57], 0
	s_mov_b32 s7, 2
	s_mov_b32 s24, 0
	s_waitcnt lgkmcnt(1)
	v_mfma_f32_16x16x32_bf16 v[50:53], v[70:73], v[2:5], v[50:53]
	v_mfma_f32_16x16x32_bf16 v[62:65], v[70:73], v[14:17], v[62:65]
	v_mfma_f32_16x16x32_bf16 v[66:69], v[70:73], v[26:29], v[66:69]
	v_mfma_f32_16x16x32_bf16 v[42:45], v[70:73], v[58:61], v[42:45]
	ds_read_b128 v[70:73], v209 offset:8192
	ds_read_b128 v[78:81], v209 offset:8448
	s_waitcnt lgkmcnt(0)
	s_barrier
; #define ATT_SB() __builtin_amdgcn_sched_barrier(0)
; #define ATT_DMA_K(t, sl) do { glds16(ksrc + (size_t)(t) * 64 * kpitch, (unsigned)__builtin_amdgcn_readfirstlane(kdst + (sl) * KSLOT)); \
;         if constexpr (DQK == 96) glds16(krsrc + (size_t)(t) * 64 * 32, (unsigned)__builtin_amdgcn_readfirstlane(krdst + (sl) * KSLOT)); } while (0)
; #define ATT_DMA_V(t, sl) do { glds16(vsrc + (size_t)(t) * 64, (unsigned)__builtin_amdgcn_readfirstlane(vdst + (sl) * VSLOT)); \
;         if constexpr (DV == 128) glds16(vsrc + (size_t)64 * NR + (size_t)(t) * 64, (unsigned)__builtin_amdgcn_readfirstlane(vdst + (sl) * VSLOT + 8192)); } while (0)
; #define ATT_KLOAD(sl) do { _Pragma("unroll") for (int kb_ = 0; kb_ < NKW; ++kb_) _Pragma("unroll") for (int ds_ = 0; ds_ < NDS; ++ds_) { \
;         if (ds_ < 2) kf[kb_ * NDS + ds_] = *(const LAS bf16x8*)(kp[ds_ & 1] + (sl) * KSLOT + (kb_ & 1) * 512 + (kb_ >> 1) * 4096); \
;         else kf[kb_ * NDS + ds_] = *(const LAS bf16x8*)(krp + (sl) * KSLOT + (kb_ & 1) * 256 + (kb_ >> 1) * 2048); } } while (0)
; #define ATT_QK() do { _Pragma("unroll") for (int kb_ = 0; kb_ < NKW; ++kb_) _Pragma("unroll") for (int ds_ = 0; ds_ < NDS; ++ds_) _Pragma("unroll") for (int qb_ = 0; qb_ < NQB; ++qb_) \
;         c[kb_][qb_] = __builtin_amdgcn_mfma_f32_16x16x32_bf16(kf[kb_ * NDS + ds_], qf[qb_ * NDS + ds_], ds_ == 0 ? zero4 : c[kb_][qb_], 0, 0, 0); } while (0)
; #define ATT_EXP() do { _Pragma("unroll") for (int kb_ = 0; kb_ < NKW; ++kb_) _Pragma("unroll") for (int qb_ = 0; qb_ < NQB; ++qb_) _Pragma("unroll") for (int i_ = 0; i_ < 4; ++i_) \
;         c[kb_][qb_][i_] = __builtin_amdgcn_exp2f(c[kb_][qb_][i_]); } while (0)
; template <int DQK, int DV, bool LEAD> ...
;     ...
;     ATT_DMA_K(3, 0); ATT_DMA_V(1, 1);
;     ATT_QK(); ATT_SB();
;     ATT_KLOAD(1); ATT_SB();
;     if constexpr (LEAD) { ATT_EXP(); ATT_SUMPACK(); }
;     wait_bar<NDMA>();
;     int s_prev = 0, s_cur = 1, s_next = 2;
	s_waitcnt lgkmcnt(1)
	v_mfma_f32_16x16x32_bf16 v[94:97], v[70:73], v[38:41], v[42:45]
	v_mfma_f32_16x16x32_bf16 v[42:45], v[46:49], v[6:9], 0
	v_mfma_f32_16x16x32_bf16 v[82:85], v[70:73], v[10:13], v[50:53]
	v_mfma_f32_16x16x32_bf16 v[86:89], v[70:73], v[22:25], v[62:65]
	v_mfma_f32_16x16x32_bf16 v[50:53], v[46:49], v[18:21], 0
	v_mfma_f32_16x16x32_bf16 v[62:65], v[46:49], v[30:33], 0
	v_mfma_f32_16x16x32_bf16 v[46:49], v[46:49], v[54:57], 0
	v_mfma_f32_16x16x32_bf16 v[42:45], v[74:77], v[2:5], v[42:45]
	v_mfma_f32_16x16x32_bf16 v[50:53], v[74:77], v[14:17], v[50:53]
	v_mfma_f32_16x16x32_bf16 v[62:65], v[74:77], v[26:29], v[62:65]
	v_mfma_f32_16x16x32_bf16 v[46:49], v[74:77], v[58:61], v[46:49]
	s_waitcnt lgkmcnt(0)
	v_mfma_f32_16x16x32_bf16 v[74:77], v[78:81], v[10:13], v[42:45]
	s_nop 2
	v_lshl_add_u64 v[42:43], v[186:187], 0, s[4:5]
	s_mov_b32 m0, s42
	s_nop 0
	global_load_lds_dwordx4 v[42:43], off
	s_mov_b64 s[4:5], 0x3000
	v_mfma_f32_16x16x32_bf16 v[90:93], v[70:73], v[34:37], v[66:69]
	v_lshl_add_u64 v[42:43], v[188:189], 0, s[4:5]
	s_mov_b32 m0, s41
	s_nop 0
	global_load_lds_dwordx4 v[42:43], off
	v_lshl_add_u64 v[42:43], v[190:191], 0, s[66:67]
	v_mfma_f32_16x16x32_bf16 v[98:101], v[78:81], v[22:25], v[50:53]
	s_add_i32 s4, s40, 0x2000
	s_mov_b32 m0, s4
	s_nop 0
	global_load_lds_dwordx4 v[42:43], off
	v_mfma_f32_16x16x32_bf16 v[102:105], v[78:81], v[34:37], v[62:65]
	v_mfma_f32_16x16x32_bf16 v[78:81], v[78:81], v[38:41], v[46:49]
	ds_read_b128 v[42:45], v219 offset:12288
	s_nop 1
	ds_read_b128 v[46:49], v219 offset:12800
	ds_read_b128 v[50:53], v208 offset:12288
	ds_read_b128 v[62:65], v208 offset:12800
	ds_read_b128 v[66:69], v209 offset:20480
	ds_read_b128 v[70:73], v209 offset:20736
	v_exp_f32_e32 v82, v82
	v_exp_f32_e32 v83, v83
	v_exp_f32_e32 v84, v84
	v_exp_f32_e32 v85, v85
	v_exp_f32_e32 v86, v86
	v_exp_f32_e32 v87, v87
	v_exp_f32_e32 v88, v88
	v_exp_f32_e32 v89, v89
	v_exp_f32_e32 v90, v90
	v_exp_f32_e32 v91, v91
	v_exp_f32_e32 v92, v92
	v_exp_f32_e32 v93, v93
	v_exp_f32_e32 v94, v94
	v_exp_f32_e32 v95, v95
	v_exp_f32_e32 v96, v96
	v_exp_f32_e32 v97, v97
	v_exp_f32_e32 v107, v74
	v_exp_f32_e32 v108, v75
	v_add_f32_e32 v74, v82, v83
	v_add_f32_e32 v75, v84, v85
	v_exp_f32_e32 v109, v76
	v_exp_f32_e32 v98, v98
	v_exp_f32_e32 v102, v102
	v_exp_f32_e32 v78, v78
	v_add_f32_e32 v74, v74, v75
	v_add_f32_e32 v75, v86, v87
	v_add_f32_e32 v76, v88, v89
	v_exp_f32_e32 v110, v77
	v_add_f32_e32 v75, v75, v76
	v_add_f32_e32 v76, v90, v91
	v_add_f32_e32 v77, v92, v93
	v_exp_f32_e32 v99, v99
	v_exp_f32_e32 v103, v103
	v_exp_f32_e32 v79, v79
	v_add_f32_e32 v76, v76, v77
	v_add_f32_e32 v77, v94, v95
	v_add_f32_e32 v111, v96, v97
	v_add_f32_e32 v77, v77, v111
	v_exp_f32_e32 v100, v100
	v_exp_f32_e32 v104, v104
	v_exp_f32_e32 v80, v80
	v_add_f32_e32 v74, v74, v107
	v_add_f32_e32 v75, v75, v98
	v_add_f32_e32 v76, v76, v102
	v_add_f32_e32 v77, v77, v78
	v_exp_f32_e32 v101, v101
	v_exp_f32_e32 v105, v105
	v_exp_f32_e32 v81, v81
	v_add_f32_e32 v74, v108, v74
	v_add_f32_e32 v75, v99, v75
	v_add_f32_e32 v76, v103, v76
	v_add_f32_e32 v77, v79, v77
	s_mov_b32 s4, 1
	v_add_f32_e32 v74, v109, v74
	v_add_f32_e32 v111, v100, v75
	v_add_f32_e32 v76, v104, v76
	v_add_f32_e32 v112, v80, v77
	v_cvt_pk_bf16_f32 v138, v82, v83
	v_add_f32_e32 v75, v110, v74
	v_add_f32_e32 v74, v101, v111
	v_add_f32_e32 v77, v105, v76
	v_add_f32_e32 v76, v81, v112
	s_waitcnt vmcnt(3) lgkmcnt(0)
	s_barrier
	s_cmp_lg_u32 s4, 0
	v_pk_add_f32 v[204:205], v[74:75], 0 op_sel_hi:[1,0]
	v_cndmask_b32_e32 v74, v206, v194, vcc
	v_bitop3_b32 v74, v74, v106, 7 bitop3:0x78
	v_lshlrev_b32_e32 v74, 4, v74
	v_add3_u32 v210, 0, v207, v74
	v_mov_b32_e32 v74, 0
	v_pk_add_f32 v[192:193], v[76:77], 0 op_sel_hi:[1,0]
	v_cvt_pk_bf16_f32 v139, v84, v85
	v_cvt_pk_bf16_f32 v140, v107, v108
	v_cvt_pk_bf16_f32 v141, v109, v110
	v_cvt_pk_bf16_f32 v142, v86, v87
	v_cvt_pk_bf16_f32 v143, v88, v89
	v_cvt_pk_bf16_f32 v144, v98, v99
	v_cvt_pk_bf16_f32 v145, v100, v101
	v_cvt_pk_bf16_f32 v146, v90, v91
	v_cvt_pk_bf16_f32 v147, v92, v93
	v_cvt_pk_bf16_f32 v148, v102, v103
	v_cvt_pk_bf16_f32 v149, v104, v105
	v_cvt_pk_bf16_f32 v150, v94, v95
	v_cvt_pk_bf16_f32 v151, v96, v97
	v_cvt_pk_bf16_f32 v152, v78, v79
	v_cvt_pk_bf16_f32 v153, v80, v81
	s_cselect_b64 s[4:5], -1, 0
	s_mov_b32 s38, 2
	v_mov_b32_e32 v75, v74
	v_mov_b32_e32 v76, v74
	v_mov_b32_e32 v77, v74
	v_mov_b32_e32 v78, v74
	v_mov_b32_e32 v79, v74
	v_mov_b32_e32 v80, v74
	v_mov_b32_e32 v81, v74
	v_mov_b32_e32 v82, v74
	v_mov_b32_e32 v83, v74
	v_mov_b32_e32 v84, v74
	v_mov_b32_e32 v85, v74
	v_mov_b32_e32 v86, v74
	v_mov_b32_e32 v87, v74
	v_mov_b32_e32 v88, v74
	v_mov_b32_e32 v89, v74
	v_mov_b32_e32 v90, v74
	v_mov_b32_e32 v91, v74
	v_mov_b32_e32 v92, v74
	v_mov_b32_e32 v93, v74
	v_mov_b32_e32 v94, v74
	v_mov_b32_e32 v95, v74
	v_mov_b32_e32 v96, v74
	v_mov_b32_e32 v97, v74
	v_mov_b32_e32 v98, v74
	v_mov_b32_e32 v99, v74
	v_mov_b32_e32 v100, v74
	v_mov_b32_e32 v101, v74
	v_mov_b32_e32 v102, v74
	v_mov_b32_e32 v103, v74
	v_mov_b32_e32 v104, v74
	v_mov_b32_e32 v105, v74
	v_mov_b32_e32 v106, v74
	v_mov_b32_e32 v107, v74
	v_mov_b32_e32 v108, v74
	v_mov_b32_e32 v109, v74
	v_mov_b32_e32 v110, v74
	v_mov_b32_e32 v111, v74
	v_mov_b32_e32 v112, v74
	v_mov_b32_e32 v113, v74
	v_mov_b32_e32 v114, v74
	v_mov_b32_e32 v115, v74
	v_mov_b32_e32 v116, v74
	v_mov_b32_e32 v117, v74
	v_mov_b32_e32 v118, v74
	v_mov_b32_e32 v119, v74
	v_mov_b32_e32 v120, v74
	v_mov_b32_e32 v121, v74
	v_mov_b32_e32 v122, v74
	v_mov_b32_e32 v123, v74
	v_mov_b32_e32 v124, v74
	v_mov_b32_e32 v125, v74
	v_mov_b32_e32 v126, v74
	v_mov_b32_e32 v127, v74
	v_mov_b32_e32 v128, v74
	v_mov_b32_e32 v129, v74
	v_mov_b32_e32 v130, v74
	v_mov_b32_e32 v131, v74
	v_mov_b32_e32 v132, v74
	v_mov_b32_e32 v133, v74
	v_mov_b32_e32 v134, v74
	v_mov_b32_e32 v135, v74
	v_mov_b32_e32 v136, v74
	v_mov_b32_e32 v137, v74

; #define ATT_DMA_K(t, sl) do { glds16(ksrc + (size_t)(t) * 64 * kpitch, (unsigned)__builtin_amdgcn_readfirstlane(kdst + (sl) * KSLOT)); \
;         if constexpr (DQK == 96) glds16(krsrc + (size_t)(t) * 64 * 32, (unsigned)__builtin_amdgcn_readfirstlane(krdst + (sl) * KSLOT)); } while (0)
; template <int DQK, int DV, bool LEAD> ...
;     ...
;     const int krow_l = wid * 8 + (lane >> 3);
;     const int kc_l = (lane & 7) ^ (((krow_l >> 1) & 1) | (((krow_l >> 3) & 1) << 1) | (((krow_l >> 4) & 1) << 2));
;     const int vc_l = (lane & 7) ^ ((krow_l >> 1) & 7);
;     const bf16_t* ksrc = K + (size_t)(krow0 + krow_l) * kpitch + kc_l * 8;
;     const int rrow_l = (wid & 3) * 16 + (lane >> 2), rc_l = (lane & 3) ^ (((rrow_l >> 4) & 1) << 1);
;     const bf16_t* krsrc = (DQK == 96) ? KR + (size_t)(krow0 + rrow_l) * 32 + rc_l * 8 : nullptr;
;     const bf16_t* vsrc = Vt + (size_t)krow_l * NR + krow0 + vc_l * 8;
;     const unsigned kdst = lds0 + KOFF + wid * 1024, krdst = lds0 + KOFF + 8192 + (wid & 3) * 1024, vdst = lds0 + VOFF + wid * 1024;
;     ...
;     ATT_DMA_K(0, 0); ATT_DMA_V(0, 0); ATT_DMA_K(1, 1); ATT_DMA_K(2, 2);
;     bf16x8 qf[NQB * NDS];
;     {
;       const float c2 = (DQK == 64) ? C2_EVEN : C2_ODD; const bool lat = tq0 >= 0;
; #pragma unroll
;       for (int qb = 0; qb < NQB; ++qb) {
;           const bf16_t* qp = Q + (size_t)(qrow0 + qoff + qb * 16 + q16) * qpitch + g4 * 8;
;           bf16x8 raw[NDS];
; #pragma unroll
;           for (int ds = 0; ds < NDS; ++ds) raw[ds] = *(const bf16x8*)(qp + ds * 32);
;           float x[NDS][8];
; #pragma unroll
;           for (int ds = 0; ds < NDS; ++ds)
; #pragma unroll
;               for (int j = 0; j < 8; ++j) x[ds][j] = __uint_as_float(((unsigned)(unsigned short)raw[ds][j]) << 16);
;           const int tq = tq0 + qoff + qb * 16 + q16, prow = (tq >> 6) & 127, pcol = tq & 63;
;           float sn = 0.f;
; #pragma unroll
;           for (int ds = 0; ds < 2; ++ds)
; #pragma unroll
;               for (int j = 0; j < 8; ++j) sn += x[ds][j] * x[ds][j];
;           sn = lanes4_sum(sn);
;           const float rn = rsqrtf(sn * (1.f / 64.f) + EPS);
.LBB0_661:
	v_mov_b32_e32 v142, v0
	v_mov_b64_e32 v[6:7], s[46:47]
	v_readfirstlane_b32 s16, v142
	s_ashr_i32 s4, s16, 6
	v_bfe_u32 v2, v142, 3, 3
	v_lshl_or_b32 v8, s4, 3, v2
	v_ashrrev_i32_e32 v3, 1, v8
	v_and_b32_e32 v4, 1, v3
	s_lshl_b32 s5, s4, 1
	s_lshr_b32 s7, s16, 5
	v_and_b32_e32 v2, 7, v142
	s_and_b32 s6, s5, 2
	v_and_or_b32 v4, s7, 4, v4
	s_and_b32 s24, s4, 3
	v_bitop3_b32 v9, v4, v2, s6 bitop3:0x36
	v_bfe_u32 v4, v142, 2, 4
	v_add_u32_e32 v2, s40, v8
	v_lshl_or_b32 v4, s24, 4, v4
	v_xor_b32_e32 v10, v3, v142
	v_ashrrev_i32_e32 v3, 31, v2
	v_or_b32_e32 v4, s40, v4
	v_lshlrev_b64 v[2:3], 11, v[2:3]
	v_and_b32_e32 v18, 3, v142
	v_ashrrev_i32_e32 v5, 31, v4
	v_bitop3_b32 v11, s5, v18, 2 bitop3:0x6c
	v_lshlrev_b64 v[4:5], 6, v[4:5]
	s_ashr_i32 s41, s40, 31
	s_lshl_b32 s30, s4, 10
	s_lshl_b32 s6, s24, 10
	v_lshl_add_u64 v[2:3], s[44:45], 0, v[2:3]
	v_mad_i64_i32 v[6:7], s[4:5], v8, s91, v[6:7]
	v_lshlrev_b32_e32 v194, 4, v9
	s_add_i32 s30, s30, 0
	v_lshl_add_u64 v[4:5], s[28:29], 0, v[4:5]
	v_lshl_add_u64 v[6:7], s[40:41], 1, v[6:7]
	v_lshl_add_u64 v[62:63], v[2:3], 0, v[194:195]
	v_lshlrev_b32_e32 v194, 4, v11
	v_lshlrev_b32_e32 v2, 4, v10
	s_add_i32 s41, s6, 0
	s_mov_b32 m0, s30
	s_nop 0
	global_load_lds_dwordx4 v[62:63], off
	v_lshl_add_u64 v[64:65], v[4:5], 0, v[194:195]
	v_and_b32_e32 v194, 0x70, v2
	s_addk_i32 s41, 0x2000
	s_mov_b32 m0, s41
	s_nop 0
	global_load_lds_dwordx4 v[64:65], off
	s_add_i32 s31, s30, 0x9000
	v_lshl_add_u64 v[186:187], v[6:7], 0, v[194:195]
	s_mov_b32 m0, s31
	s_nop 0
	global_load_lds_dwordx4 v[186:187], off
	s_mov_b64 s[4:5], 0x20000
	v_lshl_add_u64 v[2:3], v[62:63], 0, s[4:5]
	s_add_i32 s4, s30, 0x3000
	s_mov_b32 m0, s4
	s_nop 0
	global_load_lds_dwordx4 v[2:3], off
	v_lshl_add_u64 v[2:3], v[64:65], 0, s[60:61]
	s_add_i32 s4, s41, 0x3000
	s_mov_b32 m0, s4
	s_nop 0
	global_load_lds_dwordx4 v[2:3], off
	s_mov_b64 s[4:5], 0x40000
	v_lshl_add_u64 v[2:3], v[62:63], 0, s[4:5]
	s_add_i32 s4, s30, 0x6000
	s_mov_b32 m0, s4
	s_nop 0
	global_load_lds_dwordx4 v[2:3], off
	s_mov_b64 s[4:5], 0x2000
	v_and_b32_e32 v143, 15, v142
	v_lshl_add_u64 v[2:3], v[64:65], 0, s[4:5]
	s_add_i32 s4, s41, 0x6000
	s_mov_b32 m0, s4
	s_nop 0
	global_load_lds_dwordx4 v[2:3], off
	v_lshl_or_b32 v2, s24, 6, v143
	v_and_b32_e32 v8, 48, v142
	v_or_b32_e32 v6, s40, v2
	v_mov_b32_e32 v9, v195
	v_lshl_add_u64 v[2:3], s[36:37], 0, v[8:9]
	v_or_b32_e32 v7, 16, v6
	v_mad_i64_i32 v[4:5], s[4:5], v6, s90, v[2:3]
	v_mad_i64_i32 v[10:11], s[4:5], v7, s90, v[2:3]
	v_or_b32_e32 v7, 32, v6
	v_or_b32_e32 v6, 48, v6
	v_mad_i64_i32 v[14:15], s[4:5], v7, s90, v[2:3]
	v_mad_i64_i32 v[16:17], s[4:5], v6, s90, v[2:3]
	global_load_dwordx4 v[46:49], v[4:5], off offset:64
	global_load_dwordx4 v[50:53], v[10:11], off offset:64
	global_load_dwordx4 v[54:57], v[14:15], off offset:64
	global_load_dwordx4 v[58:61], v[16:17], off offset:64
	global_load_dwordx4 v[88:91], v[4:5], off
	global_load_dwordx4 v[94:97], v[10:11], off
	global_load_dwordx4 v[98:101], v[14:15], off
	global_load_dwordx4 v[6:9], v[16:17], off
	s_nop 0
	global_load_dwordx4 v[10:13], v[10:11], off offset:128
	v_lshlrev_b32_e32 v2, 1, v142
	v_and_or_b32 v144, v2, 24, v18
	v_bfe_u32 v146, v142, 3, 1
	v_bfe_u32 v170, v142, 4, 2
	s_ashr_i32 s38, s16, 8
	v_bfe_u32 v147, v142, 1, 2
	v_lshlrev_b32_e32 v148, 2, v146
	v_lshl_add_u32 v145, v144, 7, 0
	v_lshl_add_u32 v149, s38, 12, v145
	v_bitop3_b32 v2, v148, v170, v147 bitop3:0x36
	v_lshl_add_u32 v194, v2, 4, v149
	global_load_dwordx4 v[2:5], v[4:5], off offset:128
	v_lshlrev_b32_e32 v82, 5, v170
	global_load_dwordx4 v[22:25], v[14:15], off offset:128
	global_load_dwordx4 v[42:45], v[16:17], off offset:128
	global_load_dwordx4 v[30:33], v82, s[26:27] offset:144
	global_load_dwordx4 v[38:41], v82, s[26:27] offset:128
	s_mov_b32 s6, 0x3d000000
	s_brev_b32 s7, 60
	s_mov_b32 s4, 0x358637bd
	s_mov_b32 s7, 0x3c800000
	v_mov_b64_e32 v[106:107], s[4:5]
	v_and_b32_e32 v112, 16, v142
	v_and_b32_e32 v203, 63, v142
	s_mov_b32 s42, 1
	s_mov_b32 s43, 2
	s_waitcnt vmcnt(10)
	v_and_b32_e32 v73, 0xffff0000, v58
	s_waitcnt vmcnt(9)
	v_and_b32_e32 v137, 0xffff0000, v88
	v_lshlrev_b32_e32 v136, 16, v88
	v_and_b32_e32 v135, 0xffff0000, v89
	s_waitcnt vmcnt(6)
	v_and_b32_e32 v77, 0xffff0000, v8
	v_lshlrev_b32_e32 v76, 16, v8
	v_mul_f32_e32 v8, v137, v137
	v_and_b32_e32 v75, 0xffff0000, v9
	v_lshlrev_b32_e32 v74, 16, v9
	v_lshlrev_b32_e32 v134, 16, v89
	v_pk_fma_f32 v[8:9], v[136:137], v[136:137], v[8:9] op_sel_hi:[1,1,0]
	v_and_b32_e32 v81, 0xffff0000, v54
	v_lshlrev_b32_e32 v80, 16, v54
	v_pk_fma_f32 v[8:9], v[134:135], v[134:135], v[8:9]
	v_mul_f32_e32 v54, v135, v135
	v_and_b32_e32 v133, 0xffff0000, v90
	v_lshlrev_b32_e32 v132, 16, v90
	v_pk_add_f32 v[8:9], v[54:55], v[8:9] op_sel_hi:[0,1]
	v_pk_fma_f32 v[8:9], v[132:133], v[132:133], v[8:9]
	v_mul_f32_e32 v54, v133, v133
	v_and_b32_e32 v127, 0xffff0000, v91
	v_lshlrev_b32_e32 v126, 16, v91
	v_pk_add_f32 v[8:9], v[54:55], v[8:9] op_sel_hi:[0,1]
	v_pk_fma_f32 v[8:9], v[126:127], v[126:127], v[8:9]
	v_mul_f32_e32 v54, v127, v127
	v_and_b32_e32 v125, 0xffff0000, v46
	v_lshlrev_b32_e32 v124, 16, v46
	v_pk_add_f32 v[8:9], v[54:55], v[8:9] op_sel_hi:[0,1]
	v_pk_fma_f32 v[8:9], v[124:125], v[124:125], v[8:9]
	v_mul_f32_e32 v54, v125, v125
	v_and_b32_e32 v123, 0xffff0000, v47
	v_lshlrev_b32_e32 v122, 16, v47
	v_pk_add_f32 v[8:9], v[54:55], v[8:9] op_sel_hi:[0,1]
	v_pk_fma_f32 v[8:9], v[122:123], v[122:123], v[8:9]
	v_mul_f32_e32 v54, v123, v123
	v_and_b32_e32 v121, 0xffff0000, v48
	v_lshlrev_b32_e32 v120, 16, v48
	v_pk_add_f32 v[8:9], v[54:55], v[8:9] op_sel_hi:[0,1]
	v_pk_fma_f32 v[8:9], v[120:121], v[120:121], v[8:9]
; template <int DQK, int DV, bool LEAD> ...
;     ...
;           const bf16_t* qp = Q + (size_t)(qrow0 + qoff + qb * 16 + q16) * qpitch + g4 * 8;
;           bf16x8 raw[NDS];
; #pragma unroll
;           for (int ds = 0; ds < NDS; ++ds) raw[ds] = *(const bf16x8*)(qp + ds * 32);
;           float x[NDS][8];
; #pragma unroll
;           for (int ds = 0; ds < NDS; ++ds)
; #pragma unroll
;               for (int j = 0; j < 8; ++j) x[ds][j] = __uint_as_float(((unsigned)(unsigned short)raw[ds][j]) << 16);
;           const int tq = tq0 + qoff + qb * 16 + q16, prow = (tq >> 6) & 127, pcol = tq & 63;
;           float sn = 0.f;
; #pragma unroll
;           for (int ds = 0; ds < 2; ++ds)
; #pragma unroll
;               for (int j = 0; j < 8; ++j) sn += x[ds][j] * x[ds][j];
;           sn = lanes4_sum(sn);
	v_mul_f32_e32 v54, v121, v121
	v_and_b32_e32 v17, 0xffff0000, v49
	v_lshlrev_b32_e32 v16, 16, v49
	v_pk_add_f32 v[8:9], v[54:55], v[8:9] op_sel_hi:[0,1]
	v_pk_fma_f32 v[8:9], v[16:17], v[16:17], v[8:9]
	v_mul_f32_e32 v54, v17, v17
	v_pk_add_f32 v[8:9], v[54:55], v[8:9] op_sel_hi:[0,1]
	v_and_b32_e32 v79, 0xffff0000, v7
	v_lshlrev_b32_e32 v78, 16, v7
	v_mov_b32_e32 v7, v8
	s_nop 1
	v_permlane16_swap_b32_e32 v8, v7
	v_add_f32_e32 v7, v8, v7
	v_mov_b32_e32 v9, v7
	v_and_b32_e32 v119, 0xffff0000, v94
	s_nop 0
	v_permlane32_swap_b32_e32 v7, v9
	v_lshlrev_b32_e32 v118, 16, v94
	v_mul_f32_e32 v8, v119, v119
	v_and_b32_e32 v37, 0xffff0000, v55
	v_lshlrev_b32_e32 v36, 16, v55
	v_and_b32_e32 v109, 0xffff0000, v95
	v_lshlrev_b32_e32 v108, 16, v95
	v_pk_fma_f32 v[54:55], v[118:119], v[118:119], v[8:9] op_sel_hi:[1,1,0]
	v_mul_f32_e32 v8, v109, v109
	v_pk_fma_f32 v[54:55], v[108:109], v[108:109], v[54:55]
	v_and_b32_e32 v105, 0xffff0000, v96
	v_lshlrev_b32_e32 v104, 16, v96
	v_pk_add_f32 v[54:55], v[8:9], v[54:55] op_sel_hi:[0,1]
	v_pk_fma_f32 v[54:55], v[104:105], v[104:105], v[54:55]
	v_mul_f32_e32 v8, v105, v105
	v_and_b32_e32 v103, 0xffff0000, v97
	v_lshlrev_b32_e32 v102, 16, v97
	v_pk_add_f32 v[54:55], v[8:9], v[54:55] op_sel_hi:[0,1]
	v_pk_fma_f32 v[54:55], v[102:103], v[102:103], v[54:55]
	v_mul_f32_e32 v8, v103, v103
	v_and_b32_e32 v29, 0xffff0000, v50
	v_lshlrev_b32_e32 v28, 16, v50
	v_pk_add_f32 v[54:55], v[8:9], v[54:55] op_sel_hi:[0,1]
	v_pk_fma_f32 v[54:55], v[28:29], v[28:29], v[54:55]
	v_mul_f32_e32 v8, v29, v29
	v_and_b32_e32 v21, 0xffff0000, v51
	v_lshlrev_b32_e32 v20, 16, v51
	v_pk_add_f32 v[54:55], v[8:9], v[54:55] op_sel_hi:[0,1]
	v_pk_fma_f32 v[54:55], v[20:21], v[20:21], v[54:55]
	v_mul_f32_e32 v8, v21, v21
	v_and_b32_e32 v19, 0xffff0000, v52
	v_lshlrev_b32_e32 v18, 16, v52
	v_pk_add_f32 v[54:55], v[8:9], v[54:55] op_sel_hi:[0,1]
	v_pk_fma_f32 v[54:55], v[18:19], v[18:19], v[54:55]
	v_mul_f32_e32 v8, v19, v19
	v_and_b32_e32 v15, 0xffff0000, v53
	v_lshlrev_b32_e32 v14, 16, v53
	v_pk_add_f32 v[54:55], v[8:9], v[54:55] op_sel_hi:[0,1]
	v_pk_fma_f32 v[54:55], v[14:15], v[14:15], v[54:55]
	v_mul_f32_e32 v8, v15, v15
	v_pk_add_f32 v[54:55], v[8:9], v[54:55] op_sel_hi:[0,1]
	v_mov_b32_e32 v8, v54
	v_and_b32_e32 v85, 0xffff0000, v101
	v_lshlrev_b32_e32 v84, 16, v101
	v_permlane16_swap_b32_e32 v54, v8
	v_and_b32_e32 v101, 0xffff0000, v98
	v_and_b32_e32 v87, 0xffff0000, v100
	v_lshlrev_b32_e32 v86, 16, v100
	v_add_f32_e32 v129, v54, v8
	v_lshlrev_b32_e32 v100, 16, v98
	v_mul_f32_e32 v8, v101, v101
	v_and_b32_e32 v93, 0xffff0000, v99
	v_lshlrev_b32_e32 v92, 16, v99
	v_pk_fma_f32 v[54:55], v[100:101], v[100:101], v[8:9] op_sel_hi:[1,1,0]
	v_mul_f32_e32 v8, v93, v93
	v_pk_fma_f32 v[54:55], v[92:93], v[92:93], v[54:55]
	v_and_b32_e32 v35, 0xffff0000, v56
	v_pk_add_f32 v[54:55], v[8:9], v[54:55] op_sel_hi:[0,1]
	v_pk_fma_f32 v[54:55], v[86:87], v[86:87], v[54:55]
	v_mul_f32_e32 v8, v87, v87
	v_pk_add_f32 v[54:55], v[8:9], v[54:55] op_sel_hi:[0,1]
	v_pk_fma_f32 v[54:55], v[84:85], v[84:85], v[54:55]
	v_mul_f32_e32 v8, v85, v85
	v_pk_add_f32 v[54:55], v[8:9], v[54:55] op_sel_hi:[0,1]
	v_pk_fma_f32 v[54:55], v[80:81], v[80:81], v[54:55]
	v_mul_f32_e32 v8, v81, v81
	v_pk_add_f32 v[54:55], v[8:9], v[54:55] op_sel_hi:[0,1]
	v_pk_fma_f32 v[54:55], v[36:37], v[36:37], v[54:55]
	v_mul_f32_e32 v8, v37, v37
	v_lshlrev_b32_e32 v34, 16, v56
	v_pk_add_f32 v[54:55], v[8:9], v[54:55] op_sel_hi:[0,1]
	v_pk_fma_f32 v[54:55], v[34:35], v[34:35], v[54:55]
	v_mul_f32_e32 v8, v35, v35
	v_and_b32_e32 v27, 0xffff0000, v57
	v_lshlrev_b32_e32 v26, 16, v57
	v_pk_add_f32 v[54:55], v[8:9], v[54:55] op_sel_hi:[0,1]
	v_pk_fma_f32 v[54:55], v[26:27], v[26:27], v[54:55]
	v_mul_f32_e32 v8, v27, v27
	v_pk_add_f32 v[54:55], v[8:9], v[54:55] op_sel_hi:[0,1]
	v_mov_b32_e32 v8, v54
	v_and_b32_e32 v89, 0xffff0000, v6
	s_nop 0
	v_permlane16_swap_b32_e32 v54, v8
	v_lshlrev_b32_e32 v88, 16, v6
	v_mul_f32_e32 v6, v89, v89
	v_add_f32_e32 v113, v54, v8
	v_pk_fma_f32 v[54:55], v[88:89], v[88:89], v[6:7] op_sel_hi:[1,1,0]
	v_mul_f32_e32 v6, v79, v79
	v_pk_fma_f32 v[54:55], v[78:79], v[78:79], v[54:55]
	global_load_dwordx4 v[46:49], v82, s[26:27] offset:16
	global_load_dwordx4 v[50:53], v82, s[26:27]
	v_pk_add_f32 v[54:55], v[6:7], v[54:55] op_sel_hi:[0,1]
	v_pk_fma_f32 v[54:55], v[76:77], v[76:77], v[54:55]
	v_mul_f32_e32 v6, v77, v77
	v_pk_add_f32 v[54:55], v[6:7], v[54:55] op_sel_hi:[0,1]
	v_pk_fma_f32 v[54:55], v[74:75], v[74:75], v[54:55]
	v_mul_f32_e32 v6, v75, v75
	v_lshlrev_b32_e32 v72, 16, v58
	v_pk_add_f32 v[54:55], v[6:7], v[54:55] op_sel_hi:[0,1]
	v_pk_fma_f32 v[54:55], v[72:73], v[72:73], v[54:55]
	v_mul_f32_e32 v6, v73, v73
	v_and_b32_e32 v71, 0xffff0000, v59
	v_lshlrev_b32_e32 v70, 16, v59
	v_pk_add_f32 v[54:55], v[6:7], v[54:55] op_sel_hi:[0,1]
	v_pk_fma_f32 v[54:55], v[70:71], v[70:71], v[54:55]
	v_mul_f32_e32 v6, v71, v71
	v_and_b32_e32 v69, 0xffff0000, v60
	v_lshlrev_b32_e32 v68, 16, v60
	v_pk_add_f32 v[54:55], v[6:7], v[54:55] op_sel_hi:[0,1]
	v_pk_fma_f32 v[54:55], v[68:69], v[68:69], v[54:55]
	v_mul_f32_e32 v6, v69, v69
	v_and_b32_e32 v67, 0xffff0000, v61
	v_lshlrev_b32_e32 v66, 16, v61
	v_pk_add_f32 v[54:55], v[6:7], v[54:55] op_sel_hi:[0,1]
	v_pk_fma_f32 v[54:55], v[66:67], v[66:67], v[54:55]
	v_mul_f32_e32 v6, v67, v67
	v_pk_add_f32 v[54:55], v[6:7], v[54:55] op_sel_hi:[0,1]
	v_mov_b32_e32 v6, v54
	s_nop 1
	v_permlane16_swap_b32_e32 v54, v6
	v_add_f32_e32 v95, v54, v6
	global_load_dwordx4 v[54:57], v82, s[26:27] offset:272
	global_load_dwordx4 v[58:61], v82, s[26:27] offset:256
	s_waitcnt vmcnt(8)
; __device__ __forceinline__ unsigned cvtpk(float lo, float hi) { f32x2 v = {lo, hi}; bf16x2_t b = __builtin_convertvector(v, bf16x2_t); return __builtin_bit_cast(unsigned, b); }
; template <int DQK, int DV, bool LEAD> ...
;     ...
;           const float rn = rsqrtf(sn * (1.f / 64.f) + EPS);
; #pragma unroll
;           for (int ds = 0; ds < 2; ++ds)
; #pragma unroll
;               for (int j = 0; j < 8; ++j) x[ds][j] *= rn * qgain[32 * ds + 8 * g4 + j];
;           if constexpr (DQK == 64) {
; #pragma unroll
;               for (int ds = 0; ds < 2; ++ds)
; #pragma unroll
;                   for (int j = 0; j < 8; ++j) {
;                       auto rr = __builtin_amdgcn_permlane32_swap(__float_as_uint(x[ds][j]), __float_as_uint(x[ds][j]), false, false);
;                       const float other = hi ? __uint_as_float(rr[0]) : __uint_as_float(rr[1]);
;                       float cc = 1.f, sg = 0.f;
;                       if (lat) { const f32x2 cs = rope[(ds ? pcol : prow) * 16 + 8 * (g4 & 1) + j]; cc = cs.x; sg = hi ? cs.y : -cs.y; }
;                       x[ds][j] = x[ds][j] * cc + other * sg; }
;           } else {
;               float sr = 0.f;
; #pragma unroll
;               for (int j = 0; j < 8; ++j) sr += x[2][j] * x[2][j];
;               sr = lanes4_sum(sr);
;               const float rq = rsqrtf(sr * (1.f / 32.f) + EPS);
; #pragma unroll
;               for (int j = 0; j < 8; ++j) { const float av = x[2][j] * rq * qgain[64 + 8 * g4 + j];
;                   auto rr = __builtin_amdgcn_permlane16_swap(__float_as_uint(av), __float_as_uint(av), false, false);
;                   const float other = (g4 & 1) ? __uint_as_float(rr[0]) : __uint_as_float(rr[1]);
;                   float cc = 1.f, sg = 0.f;
;                   if (lat) { const f32x2 cs = rope[((g4 & 2) ? pcol : prow) * 8 + j]; cc = cs.x; sg = (g4 & 1) ? cs.y : -cs.y; }
;                   x[2][j] = av * cc + other * sg; }
;           }
; #pragma unroll
;           for (int ds = 0; ds < NDS; ++ds) { u32x4 w;
; #pragma unroll
;               for (int i = 0; i < 4; ++i) w[i] = cvtpk(x[ds][2 * i] * c2, x[ds][2 * i + 1] * c2);
;               qf[qb * NDS + ds] = __builtin_bit_cast(bf16x8, w); }
	v_and_b32_e32 v155, 0xffff0000, v2
	v_lshlrev_b32_e32 v154, 16, v2
	v_mul_f32_e32 v2, v155, v155
	v_and_b32_e32 v139, 0xffff0000, v13
	v_lshlrev_b32_e32 v138, 16, v13
	v_and_b32_e32 v141, 0xffff0000, v12
	v_lshlrev_b32_e32 v140, 16, v12
	v_and_b32_e32 v13, 0xffff0000, v3
	v_lshlrev_b32_e32 v12, 16, v3
	v_pk_fma_f32 v[2:3], v[154:155], v[154:155], v[2:3] op_sel_hi:[1,1,0]
	v_and_b32_e32 v153, 0xffff0000, v4
	v_lshlrev_b32_e32 v152, 16, v4
	v_pk_fma_f32 v[2:3], v[12:13], v[12:13], v[2:3]
	v_mul_f32_e32 v4, v13, v13
	v_pk_add_f32 v[2:3], v[4:5], v[2:3] op_sel_hi:[0,1]
	v_pk_fma_f32 v[2:3], v[152:153], v[152:153], v[2:3]
	v_mul_f32_e32 v4, v153, v153
	v_and_b32_e32 v151, 0xffff0000, v5
	v_lshlrev_b32_e32 v150, 16, v5
	v_pk_add_f32 v[2:3], v[4:5], v[2:3] op_sel_hi:[0,1]
	v_pk_fma_f32 v[2:3], v[150:151], v[150:151], v[2:3]
	v_mul_f32_e32 v4, v151, v151
	v_pk_add_f32 v[2:3], v[4:5], v[2:3] op_sel_hi:[0,1]
	v_mov_b32_e32 v3, v2
	s_nop 1
	v_permlane16_swap_b32_e32 v2, v3
	v_add_f32_e32 v6, v2, v3
	v_mov_b32_e32 v8, v6
	s_nop 1
	v_permlane32_swap_b32_e32 v6, v8
	v_pk_add_f32 v[2:3], v[6:7], v[8:9]
	v_mov_b32_e32 v97, v95
	v_pk_fma_f32 v[6:7], v[2:3], s[6:7], v[106:107] op_sel_hi:[1,1,0]
	s_nop 0
	v_permlane32_swap_b32_e32 v95, v97
	v_mul_f32_e32 v2, 0x4b800000, v7
	v_cmp_gt_f32_e32 vcc, s95, v7
	s_waitcnt vmcnt(7)
	v_and_b32_e32 v111, 0xffff0000, v25
	v_lshlrev_b32_e32 v110, 16, v25
	v_cndmask_b32_e32 v2, v7, v2, vcc
	v_rsq_f32_e32 v2, v2
	v_and_b32_e32 v117, 0xffff0000, v24
	v_lshlrev_b32_e32 v116, 16, v24
	v_and_b32_e32 v25, 0xffff0000, v11
	v_mul_f32_e32 v3, 0x45800000, v2
	v_cndmask_b32_e32 v94, v2, v3, vcc
	s_waitcnt vmcnt(5)
	v_pk_mul_f32 v[2:3], v[94:95], v[32:33] op_sel_hi:[0,1]
	v_pk_mul_f32 v[2:3], v[2:3], v[16:17]
	s_waitcnt vmcnt(4)
	v_pk_mul_f32 v[8:9], v[38:39], v[94:95] op_sel_hi:[1,0]
	v_pk_mul_f32 v[2:3], v[2:3], s[82:83] op_sel_hi:[1,0]
	v_pk_mul_f32 v[8:9], v[8:9], v[124:125]
	v_cvt_pk_bf16_f32 v5, v2, v3
	v_pk_mul_f32 v[2:3], v[94:95], v[30:31] op_sel_hi:[0,1]
	v_pk_mul_f32 v[2:3], v[2:3], v[120:121]
	v_pk_mul_f32 v[8:9], v[8:9], s[82:83] op_sel_hi:[1,0]
	v_pk_mul_f32 v[2:3], v[2:3], s[82:83] op_sel_hi:[1,0]
	s_waitcnt vmcnt(3)
	v_pk_mul_f32 v[16:17], v[46:47], v[94:95] op_sel_hi:[1,0]
	v_cvt_pk_bf16_f32 v4, v2, v3
	v_pk_mul_f32 v[2:3], v[94:95], v[40:41] op_sel_hi:[0,1]
	v_pk_mul_f32 v[2:3], v[2:3], v[122:123]
	v_pk_mul_f32 v[16:17], v[16:17], v[132:133]
	v_pk_mul_f32 v[2:3], v[2:3], s[82:83] op_sel_hi:[1,0]
	v_pk_mul_f32 v[16:17], v[16:17], s[82:83] op_sel_hi:[1,0]
	v_cvt_pk_bf16_f32 v3, v2, v3
	v_cvt_pk_bf16_f32 v2, v8, v9
	v_pk_mul_f32 v[8:9], v[48:49], v[94:95] op_sel_hi:[1,0]
	v_lshlrev_b32_e32 v24, 16, v11
	v_pk_mul_f32 v[8:9], v[8:9], v[126:127]
	v_mul_f32_e32 v11, 0x4b800000, v6
	v_pk_mul_f32 v[8:9], v[8:9], s[82:83] op_sel_hi:[1,0]
	v_cmp_gt_f32_e32 vcc, s95, v6
	v_cvt_pk_bf16_f32 v9, v8, v9
	v_cvt_pk_bf16_f32 v8, v16, v17
	s_waitcnt vmcnt(2)
	v_pk_mul_f32 v[16:17], v[52:53], v[94:95] op_sel_hi:[1,0]
	v_cndmask_b32_e32 v6, v6, v11, vcc
	v_pk_mul_f32 v[16:17], v[16:17], v[134:135]
	v_rsq_f32_e32 v11, v6
	v_pk_mul_f32 v[16:17], v[16:17], s[82:83] op_sel_hi:[1,0]
	v_and_b32_e32 v83, 0xffff0000, v45
	v_cvt_pk_bf16_f32 v7, v16, v17
	v_pk_mul_f32 v[16:17], v[50:51], v[94:95] op_sel_hi:[1,0]
	v_lshlrev_b32_e32 v82, 16, v45
	v_pk_mul_f32 v[16:17], v[16:17], v[136:137]
	v_and_b32_e32 v91, 0xffff0000, v44
	v_pk_mul_f32 v[16:17], v[16:17], s[82:83] op_sel_hi:[1,0]
	v_lshlrev_b32_e32 v90, 16, v44
	v_cvt_pk_bf16_f32 v6, v16, v17
	v_mul_f32_e32 v16, 0x45800000, v11
	v_cndmask_b32_e32 v16, v11, v16, vcc
	v_pk_mul_f32 v[122:123], v[16:17], v[12:13] op_sel_hi:[0,1]
	v_pk_mul_f32 v[12:13], v[16:17], v[150:151] op_sel_hi:[0,1]
	s_waitcnt vmcnt(1)
	v_pk_mul_f32 v[12:13], v[12:13], v[56:57]
	v_and_b32_e32 v45, 0xffff0000, v23
	v_lshlrev_b32_e32 v44, 16, v23
	v_pk_mul_f32 v[120:121], v[16:17], v[154:155] op_sel_hi:[0,1]
	v_pk_mul_f32 v[124:125], v[16:17], v[152:153] op_sel_hi:[0,1]
	v_mov_b32_e32 v11, v12
	v_mov_b32_e32 v16, v12
	v_mov_b32_e32 v17, v13
	v_mov_b32_e32 v23, v13
	v_permlane16_swap_b32_e32 v11, v16
	s_nop 0
	v_permlane16_swap_b32_e32 v17, v23
	v_cmp_eq_u32_e32 vcc, 0, v112
	v_and_b32_e32 v99, 0xffff0000, v43
	v_lshlrev_b32_e32 v98, 16, v43
	v_cndmask_b32_e32 v17, v17, v23, vcc
	v_cndmask_b32_e32 v16, v11, v16, vcc
	v_pk_fma_f32 v[12:13], v[16:17], 0, v[12:13] op_sel_hi:[1,0,1]
	v_pk_mul_f32 v[16:17], v[54:55], v[124:125]
	v_pk_mul_f32 v[12:13], v[12:13], s[82:83] op_sel_hi:[1,0]
	v_mov_b32_e32 v11, v16
	v_cvt_pk_bf16_f32 v13, v12, v13
	v_mov_b32_e32 v12, v16
	v_mov_b32_e32 v23, v17
	v_mov_b32_e32 v43, v17
	v_permlane16_swap_b32_e32 v11, v12
	s_nop 0
	v_permlane16_swap_b32_e32 v23, v43
	v_cndmask_b32_e32 v125, v23, v43, vcc
	v_cndmask_b32_e32 v124, v11, v12, vcc
	v_pk_fma_f32 v[16:17], v[124:125], 0, v[16:17] op_sel_hi:[1,0,1]
	v_mov_b32_e32 v131, v129
	v_pk_mul_f32 v[16:17], v[16:17], s[82:83] op_sel_hi:[1,0]
	s_nop 0
	v_permlane32_swap_b32_e32 v129, v131
	v_cvt_pk_bf16_f32 v12, v16, v17
	s_waitcnt vmcnt(0)
; __device__ __forceinline__ unsigned cvtpk(float lo, float hi) { f32x2 v = {lo, hi}; bf16x2_t b = __builtin_convertvector(v, bf16x2_t); return __builtin_bit_cast(unsigned, b); }
; template <int DQK, int DV, bool LEAD> ...
;     ...
;           const float rn = rsqrtf(sn * (1.f / 64.f) + EPS);
; #pragma unroll
;           for (int ds = 0; ds < 2; ++ds)
; #pragma unroll
;               for (int j = 0; j < 8; ++j) x[ds][j] *= rn * qgain[32 * ds + 8 * g4 + j];
;           if constexpr (DQK == 64) {
; #pragma unroll
;               for (int ds = 0; ds < 2; ++ds)
; #pragma unroll
;                   for (int j = 0; j < 8; ++j) {
;                       auto rr = __builtin_amdgcn_permlane32_swap(__float_as_uint(x[ds][j]), __float_as_uint(x[ds][j]), false, false);
;                       const float other = hi ? __uint_as_float(rr[0]) : __uint_as_float(rr[1]);
;                       float cc = 1.f, sg = 0.f;
;                       if (lat) { const f32x2 cs = rope[(ds ? pcol : prow) * 16 + 8 * (g4 & 1) + j]; cc = cs.x; sg = hi ? cs.y : -cs.y; }
;                       x[ds][j] = x[ds][j] * cc + other * sg; }
;           } else {
;               float sr = 0.f;
; #pragma unroll
;               for (int j = 0; j < 8; ++j) sr += x[2][j] * x[2][j];
;               sr = lanes4_sum(sr);
;               const float rq = rsqrtf(sr * (1.f / 32.f) + EPS);
; #pragma unroll
;               for (int j = 0; j < 8; ++j) { const float av = x[2][j] * rq * qgain[64 + 8 * g4 + j];
;                   auto rr = __builtin_amdgcn_permlane16_swap(__float_as_uint(av), __float_as_uint(av), false, false);
;                   const float other = (g4 & 1) ? __uint_as_float(rr[0]) : __uint_as_float(rr[1]);
;                   float cc = 1.f, sg = 0.f;
;                   if (lat) { const f32x2 cs = rope[((g4 & 2) ? pcol : prow) * 8 + j]; cc = cs.x; sg = (g4 & 1) ? cs.y : -cs.y; }
;                   x[2][j] = av * cc + other * sg; }
;           }
; #pragma unroll
;           for (int ds = 0; ds < NDS; ++ds) { u32x4 w;
; #pragma unroll
;               for (int i = 0; i < 4; ++i) w[i] = cvtpk(x[ds][2 * i] * c2, x[ds][2 * i + 1] * c2);
;               qf[qb * NDS + ds] = __builtin_bit_cast(bf16x8, w); }
	v_pk_mul_f32 v[16:17], v[60:61], v[122:123]
	v_mov_b32_e32 v115, v113
	v_mov_b32_e32 v11, v16
	v_mov_b32_e32 v23, v16
	v_mov_b32_e32 v43, v17
	v_mov_b32_e32 v94, v17
	v_permlane16_swap_b32_e32 v11, v23
	s_nop 0
	v_permlane16_swap_b32_e32 v43, v94
	v_cndmask_b32_e32 v123, v43, v94, vcc
	v_cndmask_b32_e32 v122, v11, v23, vcc
	v_pk_fma_f32 v[16:17], v[122:123], 0, v[16:17] op_sel_hi:[1,0,1]
	v_and_b32_e32 v123, 0xffff0000, v10
	v_pk_mul_f32 v[16:17], v[16:17], s[82:83] op_sel_hi:[1,0]
	v_lshlrev_b32_e32 v122, 16, v10
	v_cvt_pk_bf16_f32 v11, v16, v17
	v_mul_f32_e32 v10, v123, v123
	v_pk_fma_f32 v[124:125], v[122:123], v[122:123], v[10:11] op_sel_hi:[1,1,0]
	v_mul_f32_e32 v10, v25, v25
	v_pk_fma_f32 v[124:125], v[24:25], v[24:25], v[124:125]
	v_pk_mul_f32 v[16:17], v[58:59], v[120:121]
	v_pk_add_f32 v[124:125], v[10:11], v[124:125] op_sel_hi:[0,1]
	v_pk_fma_f32 v[124:125], v[140:141], v[140:141], v[124:125]
	v_mul_f32_e32 v10, v141, v141
	v_pk_add_f32 v[124:125], v[10:11], v[124:125] op_sel_hi:[0,1]
	v_pk_fma_f32 v[124:125], v[138:139], v[138:139], v[124:125]
	v_mul_f32_e32 v10, v139, v139
	v_pk_add_f32 v[124:125], v[10:11], v[124:125] op_sel_hi:[0,1]
	v_mov_b32_e32 v10, v124
	s_nop 1
	v_permlane16_swap_b32_e32 v124, v10
	v_add_f32_e32 v128, v124, v10
	v_mov_b32_e32 v130, v128
	s_nop 1
	v_permlane32_swap_b32_e32 v128, v130
	v_pk_add_f32 v[124:125], v[128:129], v[130:131]
	v_mov_b32_e32 v23, v16
	v_pk_fma_f32 v[124:125], v[124:125], s[6:7], v[106:107] op_sel_hi:[1,1,0]
	v_mov_b32_e32 v43, v16
	v_mul_f32_e32 v10, 0x4b800000, v125
	v_cmp_gt_f32_e64 s[4:5], s95, v125
	v_permlane16_swap_b32_e32 v23, v43
	v_mov_b32_e32 v94, v17
	v_mov_b32_e32 v96, v17
	v_cndmask_b32_e64 v10, v125, v10, s[4:5]
	s_nop 0
	v_permlane16_swap_b32_e32 v94, v96
	v_cndmask_b32_e32 v120, v23, v43, vcc
	v_rsq_f32_e32 v23, v10
	v_cndmask_b32_e32 v121, v94, v96, vcc
	v_pk_fma_f32 v[16:17], v[120:121], 0, v[16:17] op_sel_hi:[1,0,1]
	v_permlane32_swap_b32_e32 v113, v115
	v_pk_mul_f32 v[16:17], v[16:17], s[82:83] op_sel_hi:[1,0]
	s_nop 0
	v_cvt_pk_bf16_f32 v10, v16, v17
	v_mul_f32_e32 v16, 0x45800000, v23
	v_cndmask_b32_e64 v94, v23, v16, s[4:5]
	v_pk_mul_f32 v[16:17], v[32:33], v[94:95] op_sel_hi:[1,0]
	v_cmp_gt_f32_e64 s[4:5], s95, v124
	v_pk_mul_f32 v[14:15], v[16:17], v[14:15]
	s_nop 0
	v_pk_mul_f32 v[14:15], v[14:15], s[82:83] op_sel_hi:[1,0]
	s_nop 0
	v_cvt_pk_bf16_f32 v17, v14, v15
	v_pk_mul_f32 v[14:15], v[30:31], v[94:95] op_sel_hi:[1,0]
	s_nop 0
	v_pk_mul_f32 v[14:15], v[14:15], v[18:19]
	v_pk_mul_f32 v[18:19], v[38:39], v[94:95] op_sel_hi:[1,0]
	v_pk_mul_f32 v[14:15], v[14:15], s[82:83] op_sel_hi:[1,0]
	v_pk_mul_f32 v[18:19], v[18:19], v[28:29]
	v_cvt_pk_bf16_f32 v16, v14, v15
	v_pk_mul_f32 v[14:15], v[40:41], v[94:95] op_sel_hi:[1,0]
	v_pk_mul_f32 v[18:19], v[18:19], s[82:83] op_sel_hi:[1,0]
	v_pk_mul_f32 v[14:15], v[14:15], v[20:21]
	v_pk_mul_f32 v[28:29], v[50:51], v[94:95] op_sel_hi:[1,0]
	v_pk_mul_f32 v[14:15], v[14:15], s[82:83] op_sel_hi:[1,0]
	v_pk_mul_f32 v[28:29], v[28:29], v[118:119]
	v_cvt_pk_bf16_f32 v15, v14, v15
	v_cvt_pk_bf16_f32 v14, v18, v19
	v_pk_mul_f32 v[18:19], v[48:49], v[94:95] op_sel_hi:[1,0]
	v_pk_mul_f32 v[28:29], v[28:29], s[82:83] op_sel_hi:[1,0]
	v_pk_mul_f32 v[18:19], v[18:19], v[102:103]
	s_nop 0
	v_pk_mul_f32 v[18:19], v[18:19], s[82:83] op_sel_hi:[1,0]
	s_nop 0
	v_cvt_pk_bf16_f32 v21, v18, v19
	v_pk_mul_f32 v[18:19], v[46:47], v[94:95] op_sel_hi:[1,0]
	s_nop 0
	v_pk_mul_f32 v[18:19], v[18:19], v[104:105]
	s_nop 0
	v_pk_mul_f32 v[18:19], v[18:19], s[82:83] op_sel_hi:[1,0]
	s_nop 0
	v_cvt_pk_bf16_f32 v20, v18, v19
	v_pk_mul_f32 v[18:19], v[52:53], v[94:95] op_sel_hi:[1,0]
	s_nop 0
	v_pk_mul_f32 v[18:19], v[18:19], v[108:109]
	s_nop 0
	v_pk_mul_f32 v[18:19], v[18:19], s[82:83] op_sel_hi:[1,0]
	s_nop 0
	v_cvt_pk_bf16_f32 v19, v18, v19
	v_mul_f32_e32 v18, 0x4b800000, v124
	v_cndmask_b32_e64 v18, v124, v18, s[4:5]
	v_rsq_f32_e32 v23, v18
	v_cvt_pk_bf16_f32 v18, v28, v29
	v_mul_f32_e32 v28, 0x45800000, v23
	v_cndmask_b32_e64 v28, v23, v28, s[4:5]
	v_pk_mul_f32 v[104:105], v[28:29], v[24:25] op_sel_hi:[0,1]
	v_pk_mul_f32 v[24:25], v[28:29], v[138:139] op_sel_hi:[0,1]
	v_pk_mul_f32 v[24:25], v[56:57], v[24:25]
	v_pk_mul_f32 v[102:103], v[28:29], v[122:123] op_sel_hi:[0,1]
	v_pk_mul_f32 v[108:109], v[28:29], v[140:141] op_sel_hi:[0,1]
	v_mov_b32_e32 v23, v24
	v_mov_b32_e32 v28, v24
	v_mov_b32_e32 v29, v25
	v_mov_b32_e32 v43, v25
	v_permlane16_swap_b32_e32 v23, v28
	s_nop 0
	v_permlane16_swap_b32_e32 v29, v43
	v_cndmask_b32_e32 v29, v29, v43, vcc
	v_cndmask_b32_e32 v28, v23, v28, vcc
	v_pk_fma_f32 v[24:25], v[28:29], 0, v[24:25] op_sel_hi:[1,0,1]
	v_pk_mul_f32 v[28:29], v[54:55], v[108:109]
	v_pk_mul_f32 v[24:25], v[24:25], s[82:83] op_sel_hi:[1,0]
	v_mov_b32_e32 v23, v28
	v_cvt_pk_bf16_f32 v25, v24, v25
	v_mov_b32_e32 v24, v28
	v_mov_b32_e32 v43, v29
	v_mov_b32_e32 v94, v29
	v_permlane16_swap_b32_e32 v23, v24
	s_nop 0
	v_permlane16_swap_b32_e32 v43, v94
	v_cndmask_b32_e32 v109, v43, v94, vcc
	v_cndmask_b32_e32 v108, v23, v24, vcc
	v_pk_fma_f32 v[28:29], v[108:109], 0, v[28:29] op_sel_hi:[1,0,1]
	s_nop 0
	v_pk_mul_f32 v[28:29], v[28:29], s[82:83] op_sel_hi:[1,0]
	s_nop 0
	v_cvt_pk_bf16_f32 v24, v28, v29
	v_pk_mul_f32 v[28:29], v[60:61], v[104:105]
	s_nop 0
	v_mov_b32_e32 v23, v28
	v_mov_b32_e32 v43, v28
	v_mov_b32_e32 v94, v29
	v_mov_b32_e32 v96, v29
	v_permlane16_swap_b32_e32 v23, v43
	s_nop 0
	v_permlane16_swap_b32_e32 v94, v96
	v_cndmask_b32_e32 v105, v94, v96, vcc
	v_cndmask_b32_e32 v104, v23, v43, vcc
	v_pk_fma_f32 v[28:29], v[104:105], 0, v[28:29] op_sel_hi:[1,0,1]
	v_and_b32_e32 v105, 0xffff0000, v22
	v_pk_mul_f32 v[28:29], v[28:29], s[82:83] op_sel_hi:[1,0]
; __device__ __forceinline__ unsigned cvtpk(float lo, float hi) { f32x2 v = {lo, hi}; bf16x2_t b = __builtin_convertvector(v, bf16x2_t); return __builtin_bit_cast(unsigned, b); }
; template <int DQK, int DV, bool LEAD> ...
;     ...
;           const float rn = rsqrtf(sn * (1.f / 64.f) + EPS);
; #pragma unroll
;           for (int ds = 0; ds < 2; ++ds)
; #pragma unroll
;               for (int j = 0; j < 8; ++j) x[ds][j] *= rn * qgain[32 * ds + 8 * g4 + j];
;           if constexpr (DQK == 64) {
; #pragma unroll
;               for (int ds = 0; ds < 2; ++ds)
; #pragma unroll
;                   for (int j = 0; j < 8; ++j) {
;                       auto rr = __builtin_amdgcn_permlane32_swap(__float_as_uint(x[ds][j]), __float_as_uint(x[ds][j]), false, false);
;                       const float other = hi ? __uint_as_float(rr[0]) : __uint_as_float(rr[1]);
;                       float cc = 1.f, sg = 0.f;
;                       if (lat) { const f32x2 cs = rope[(ds ? pcol : prow) * 16 + 8 * (g4 & 1) + j]; cc = cs.x; sg = hi ? cs.y : -cs.y; }
;                       x[ds][j] = x[ds][j] * cc + other * sg; }
;           } else {
;               float sr = 0.f;
; #pragma unroll
;               for (int j = 0; j < 8; ++j) sr += x[2][j] * x[2][j];
;               sr = lanes4_sum(sr);
;               const float rq = rsqrtf(sr * (1.f / 32.f) + EPS);
; #pragma unroll
;               for (int j = 0; j < 8; ++j) { const float av = x[2][j] * rq * qgain[64 + 8 * g4 + j];
;                   auto rr = __builtin_amdgcn_permlane16_swap(__float_as_uint(av), __float_as_uint(av), false, false);
;                   const float other = (g4 & 1) ? __uint_as_float(rr[0]) : __uint_as_float(rr[1]);
;                   float cc = 1.f, sg = 0.f;
;                   if (lat) { const f32x2 cs = rope[((g4 & 2) ? pcol : prow) * 8 + j]; cc = cs.x; sg = (g4 & 1) ? cs.y : -cs.y; }
;                   x[2][j] = av * cc + other * sg; }
;           }
; #pragma unroll
;           for (int ds = 0; ds < NDS; ++ds) { u32x4 w;
; #pragma unroll
;               for (int i = 0; i < 4; ++i) w[i] = cvtpk(x[ds][2 * i] * c2, x[ds][2 * i + 1] * c2);
;               qf[qb * NDS + ds] = __builtin_bit_cast(bf16x8, w); }
	v_lshlrev_b32_e32 v104, 16, v22
	v_cvt_pk_bf16_f32 v23, v28, v29
	v_mul_f32_e32 v22, v105, v105
	v_pk_fma_f32 v[108:109], v[104:105], v[104:105], v[22:23] op_sel_hi:[1,1,0]
	v_mul_f32_e32 v22, v45, v45
	v_pk_fma_f32 v[108:109], v[44:45], v[44:45], v[108:109]
	v_pk_mul_f32 v[28:29], v[58:59], v[102:103]
	v_pk_add_f32 v[108:109], v[22:23], v[108:109] op_sel_hi:[0,1]
	v_pk_fma_f32 v[108:109], v[116:117], v[116:117], v[108:109]
	v_mul_f32_e32 v22, v117, v117
	v_pk_add_f32 v[108:109], v[22:23], v[108:109] op_sel_hi:[0,1]
	v_pk_fma_f32 v[108:109], v[110:111], v[110:111], v[108:109]
	v_mul_f32_e32 v22, v111, v111
	v_pk_add_f32 v[108:109], v[22:23], v[108:109] op_sel_hi:[0,1]
	v_mov_b32_e32 v22, v108
	s_nop 1
	v_permlane16_swap_b32_e32 v108, v22
	v_add_f32_e32 v112, v108, v22
	v_mov_b32_e32 v114, v112
	s_nop 1
	v_permlane32_swap_b32_e32 v112, v114
	v_pk_add_f32 v[108:109], v[112:113], v[114:115]
	v_mov_b32_e32 v43, v28
	v_pk_fma_f32 v[108:109], v[108:109], s[6:7], v[106:107] op_sel_hi:[1,1,0]
	v_mov_b32_e32 v94, v28
	v_mov_b32_e32 v96, v29
	v_mov_b32_e32 v102, v29
	v_mul_f32_e32 v22, 0x4b800000, v109
	v_cmp_gt_f32_e64 s[4:5], s95, v109
	v_permlane16_swap_b32_e32 v43, v94
	v_permlane16_swap_b32_e32 v96, v102
	v_cndmask_b32_e64 v22, v109, v22, s[4:5]
	v_cndmask_b32_e32 v103, v96, v102, vcc
	v_cndmask_b32_e32 v102, v43, v94, vcc
	v_rsq_f32_e32 v43, v22
	v_pk_fma_f32 v[28:29], v[102:103], 0, v[28:29] op_sel_hi:[1,0,1]
	s_nop 0
	v_pk_mul_f32 v[28:29], v[28:29], s[82:83] op_sel_hi:[1,0]
	s_nop 0
	v_cvt_pk_bf16_f32 v22, v28, v29
	v_mul_f32_e32 v28, 0x45800000, v43
	v_cndmask_b32_e64 v94, v43, v28, s[4:5]
	v_pk_mul_f32 v[28:29], v[32:33], v[94:95] op_sel_hi:[1,0]
	v_cmp_gt_f32_e64 s[4:5], s95, v108
	v_pk_mul_f32 v[26:27], v[28:29], v[26:27]
	s_nop 0
	v_pk_mul_f32 v[26:27], v[26:27], s[82:83] op_sel_hi:[1,0]
	s_nop 0
	v_cvt_pk_bf16_f32 v29, v26, v27
	v_pk_mul_f32 v[26:27], v[30:31], v[94:95] op_sel_hi:[1,0]
	s_nop 0
	v_pk_mul_f32 v[26:27], v[26:27], v[34:35]
	v_pk_mul_f32 v[34:35], v[38:39], v[94:95] op_sel_hi:[1,0]
	v_pk_mul_f32 v[26:27], v[26:27], s[82:83] op_sel_hi:[1,0]
	v_pk_mul_f32 v[34:35], v[34:35], v[80:81]
	v_cvt_pk_bf16_f32 v28, v26, v27
	v_pk_mul_f32 v[26:27], v[40:41], v[94:95] op_sel_hi:[1,0]
	v_pk_mul_f32 v[34:35], v[34:35], s[82:83] op_sel_hi:[1,0]
	v_pk_mul_f32 v[26:27], v[26:27], v[36:37]
	v_pk_mul_f32 v[80:81], v[50:51], v[94:95] op_sel_hi:[1,0]
	v_pk_mul_f32 v[26:27], v[26:27], s[82:83] op_sel_hi:[1,0]
	v_pk_mul_f32 v[80:81], v[80:81], v[100:101]
	v_cvt_pk_bf16_f32 v27, v26, v27
	v_cvt_pk_bf16_f32 v26, v34, v35
	v_pk_mul_f32 v[34:35], v[48:49], v[94:95] op_sel_hi:[1,0]
	v_pk_mul_f32 v[80:81], v[80:81], s[82:83] op_sel_hi:[1,0]
	v_pk_mul_f32 v[34:35], v[34:35], v[84:85]
	s_nop 0
	v_pk_mul_f32 v[34:35], v[34:35], s[82:83] op_sel_hi:[1,0]
	s_nop 0
	v_cvt_pk_bf16_f32 v37, v34, v35
	v_pk_mul_f32 v[34:35], v[46:47], v[94:95] op_sel_hi:[1,0]
	s_nop 0
	v_pk_mul_f32 v[34:35], v[34:35], v[86:87]
	s_nop 0
	v_pk_mul_f32 v[34:35], v[34:35], s[82:83] op_sel_hi:[1,0]
	s_nop 0
	v_cvt_pk_bf16_f32 v36, v34, v35
	v_pk_mul_f32 v[34:35], v[52:53], v[94:95] op_sel_hi:[1,0]
	s_nop 0
	v_pk_mul_f32 v[34:35], v[34:35], v[92:93]
	s_nop 0
	v_pk_mul_f32 v[34:35], v[34:35], s[82:83] op_sel_hi:[1,0]
	s_nop 0
	v_cvt_pk_bf16_f32 v35, v34, v35
	v_mul_f32_e32 v34, 0x4b800000, v108
	v_cndmask_b32_e64 v34, v108, v34, s[4:5]
	v_rsq_f32_e32 v43, v34
	v_cvt_pk_bf16_f32 v34, v80, v81
	v_mul_f32_e32 v80, 0x45800000, v43
	v_cndmask_b32_e64 v80, v43, v80, s[4:5]
	v_pk_mul_f32 v[86:87], v[80:81], v[44:45] op_sel_hi:[0,1]
	v_pk_mul_f32 v[44:45], v[80:81], v[110:111] op_sel_hi:[0,1]
	v_pk_mul_f32 v[44:45], v[56:57], v[44:45]
	v_pk_mul_f32 v[84:85], v[80:81], v[104:105] op_sel_hi:[0,1]
	v_pk_mul_f32 v[92:93], v[80:81], v[116:117] op_sel_hi:[0,1]
	v_mov_b32_e32 v43, v44
	v_mov_b32_e32 v80, v44
	v_mov_b32_e32 v81, v45
	v_mov_b32_e32 v94, v45
	v_permlane16_swap_b32_e32 v43, v80
	s_nop 0
	v_permlane16_swap_b32_e32 v81, v94
	v_cndmask_b32_e32 v81, v81, v94, vcc
	v_cndmask_b32_e32 v80, v43, v80, vcc
	v_pk_fma_f32 v[44:45], v[80:81], 0, v[44:45] op_sel_hi:[1,0,1]
	v_pk_mul_f32 v[80:81], v[54:55], v[92:93]
	v_pk_mul_f32 v[44:45], v[44:45], s[82:83] op_sel_hi:[1,0]
	v_mov_b32_e32 v43, v80
	v_cvt_pk_bf16_f32 v45, v44, v45
	v_mov_b32_e32 v44, v80
	v_mov_b32_e32 v92, v81
	v_mov_b32_e32 v93, v81
	v_permlane16_swap_b32_e32 v43, v44
	s_nop 0
	v_permlane16_swap_b32_e32 v92, v93
	v_cndmask_b32_e32 v93, v92, v93, vcc
	v_cndmask_b32_e32 v92, v43, v44, vcc
	v_pk_fma_f32 v[80:81], v[92:93], 0, v[80:81] op_sel_hi:[1,0,1]
	s_nop 0
	v_pk_mul_f32 v[80:81], v[80:81], s[82:83] op_sel_hi:[1,0]
	s_nop 0
	v_cvt_pk_bf16_f32 v44, v80, v81
	v_pk_mul_f32 v[80:81], v[60:61], v[86:87]
	s_nop 0
	v_mov_b32_e32 v43, v80
	v_mov_b32_e32 v86, v80
	v_mov_b32_e32 v87, v81
	v_mov_b32_e32 v92, v81
	v_permlane16_swap_b32_e32 v43, v86
	s_nop 0
	v_permlane16_swap_b32_e32 v87, v92
	v_cndmask_b32_e32 v87, v87, v92, vcc
	v_cndmask_b32_e32 v86, v43, v86, vcc
	v_pk_fma_f32 v[80:81], v[86:87], 0, v[80:81] op_sel_hi:[1,0,1]
	s_nop 0
	v_pk_mul_f32 v[80:81], v[80:81], s[82:83] op_sel_hi:[1,0]
	s_nop 0
	v_cvt_pk_bf16_f32 v43, v80, v81
	v_pk_mul_f32 v[80:81], v[58:59], v[84:85]
	s_nop 0
	v_mov_b32_e32 v85, v81
	v_mov_b32_e32 v87, v81
	v_mov_b32_e32 v84, v80
	v_mov_b32_e32 v86, v80
	v_permlane16_swap_b32_e32 v85, v87
	s_nop 0
	v_permlane16_swap_b32_e32 v84, v86
	v_cndmask_b32_e32 v85, v85, v87, vcc
	v_and_b32_e32 v87, 0xffff0000, v42
	v_cndmask_b32_e32 v84, v84, v86, vcc
	v_lshlrev_b32_e32 v86, 16, v42
	v_mul_f32_e32 v42, v87, v87
	v_pk_fma_f32 v[92:93], v[86:87], v[86:87], v[42:43] op_sel_hi:[1,1,0]
	v_mul_f32_e32 v42, v99, v99
; __device__ __forceinline__ unsigned cvtpk(float lo, float hi) { f32x2 v = {lo, hi}; bf16x2_t b = __builtin_convertvector(v, bf16x2_t); return __builtin_bit_cast(unsigned, b); }
; template <int DQK, int DV, bool LEAD> ...
;     ...
;           } else {
;               float sr = 0.f;
; #pragma unroll
;               for (int j = 0; j < 8; ++j) sr += x[2][j] * x[2][j];
;               sr = lanes4_sum(sr);
;               const float rq = rsqrtf(sr * (1.f / 32.f) + EPS);
; #pragma unroll
;               for (int j = 0; j < 8; ++j) { const float av = x[2][j] * rq * qgain[64 + 8 * g4 + j];
;                   auto rr = __builtin_amdgcn_permlane16_swap(__float_as_uint(av), __float_as_uint(av), false, false);
;                   const float other = (g4 & 1) ? __uint_as_float(rr[0]) : __uint_as_float(rr[1]);
;                   float cc = 1.f, sg = 0.f;
;                   if (lat) { const f32x2 cs = rope[((g4 & 2) ? pcol : prow) * 8 + j]; cc = cs.x; sg = (g4 & 1) ? cs.y : -cs.y; }
;                   x[2][j] = av * cc + other * sg; }
;           }
; #pragma unroll
;           for (int ds = 0; ds < NDS; ++ds) { u32x4 w;
; #pragma unroll
;               for (int i = 0; i < 4; ++i) w[i] = cvtpk(x[ds][2 * i] * c2, x[ds][2 * i + 1] * c2);
;               qf[qb * NDS + ds] = __builtin_bit_cast(bf16x8, w); }
;       }
; #pragma unroll
;       for (int d0 = 0; d0 < NQB * NDS; ++d0) asm volatile("" : "+v"(qf[d0])); }
;     wait_bar<0>();
	v_pk_fma_f32 v[92:93], v[98:99], v[98:99], v[92:93]
	v_pk_fma_f32 v[80:81], v[84:85], 0, v[80:81] op_sel_hi:[1,0,1]
	v_pk_add_f32 v[92:93], v[42:43], v[92:93] op_sel_hi:[0,1]
	v_pk_fma_f32 v[92:93], v[90:91], v[90:91], v[92:93]
	v_mul_f32_e32 v42, v91, v91
	v_pk_add_f32 v[92:93], v[42:43], v[92:93] op_sel_hi:[0,1]
	v_pk_fma_f32 v[92:93], v[82:83], v[82:83], v[92:93]
	v_mul_f32_e32 v42, v83, v83
	v_pk_add_f32 v[92:93], v[42:43], v[92:93] op_sel_hi:[0,1]
	v_mov_b32_e32 v42, v92
	s_nop 1
	v_permlane16_swap_b32_e32 v92, v42
	v_add_f32_e32 v94, v92, v42
	v_mov_b32_e32 v96, v94
	s_nop 1
	v_permlane32_swap_b32_e32 v94, v96
	v_pk_add_f32 v[92:93], v[94:95], v[96:97]
	v_pk_mul_f32 v[80:81], v[80:81], s[82:83] op_sel_hi:[1,0]
	v_pk_fma_f32 v[92:93], v[92:93], s[6:7], v[106:107] op_sel_hi:[1,1,0]
	s_mov_b64 s[6:7], 0x60000
	v_mul_f32_e32 v42, 0x4b800000, v93
	v_cmp_gt_f32_e64 s[4:5], s95, v93
	v_lshl_add_u64 v[192:193], v[62:63], 0, s[6:7]
	s_mov_b64 s[6:7], 0x3000
	v_cndmask_b32_e64 v42, v93, v42, s[4:5]
	v_rsq_f32_e32 v93, v42
	v_cvt_pk_bf16_f32 v42, v80, v81
	v_lshl_add_u64 v[204:205], v[64:65], 0, s[6:7]
	v_mul_f32_e32 v80, 0x45800000, v93
	v_cndmask_b32_e64 v80, v93, v80, s[4:5]
	v_pk_mul_f32 v[50:51], v[50:51], v[80:81] op_sel_hi:[1,0]
	v_pk_mul_f32 v[52:53], v[52:53], v[80:81] op_sel_hi:[1,0]
	v_pk_mul_f32 v[30:31], v[30:31], v[80:81] op_sel_hi:[1,0]
	v_pk_mul_f32 v[50:51], v[50:51], v[88:89]
	v_pk_mul_f32 v[52:53], v[52:53], v[78:79]
	v_pk_mul_f32 v[46:47], v[46:47], v[80:81] op_sel_hi:[1,0]
	v_pk_mul_f32 v[48:49], v[48:49], v[80:81] op_sel_hi:[1,0]
	v_pk_mul_f32 v[68:69], v[30:31], v[68:69]
	v_pk_mul_f32 v[30:31], v[32:33], v[80:81] op_sel_hi:[1,0]
	v_pk_mul_f32 v[46:47], v[46:47], v[76:77]
	v_pk_mul_f32 v[48:49], v[48:49], v[74:75]
	v_pk_mul_f32 v[66:67], v[30:31], v[66:67]
	v_pk_mul_f32 v[30:31], v[50:51], s[82:83] op_sel_hi:[1,0]
	v_pk_mul_f32 v[32:33], v[52:53], s[82:83] op_sel_hi:[1,0]
	v_cvt_pk_bf16_f32 v30, v30, v31
	v_cvt_pk_bf16_f32 v31, v32, v33
	v_pk_mul_f32 v[32:33], v[46:47], s[82:83] op_sel_hi:[1,0]
	v_pk_mul_f32 v[46:47], v[48:49], s[82:83] op_sel_hi:[1,0]
	v_cvt_pk_bf16_f32 v32, v32, v33
	v_cvt_pk_bf16_f32 v33, v46, v47
	v_mul_f32_e32 v46, 0x4b800000, v92
	v_cmp_gt_f32_e64 s[4:5], s95, v92
	v_pk_mul_f32 v[38:39], v[38:39], v[80:81] op_sel_hi:[1,0]
	v_pk_mul_f32 v[40:41], v[40:41], v[80:81] op_sel_hi:[1,0]
	v_cndmask_b32_e64 v46, v92, v46, s[4:5]
	v_rsq_f32_e32 v48, v46
	v_pk_mul_f32 v[38:39], v[38:39], v[72:73]
	v_pk_mul_f32 v[40:41], v[40:41], v[70:71]
	v_pk_mul_f32 v[38:39], v[38:39], s[82:83] op_sel_hi:[1,0]
	v_pk_mul_f32 v[40:41], v[40:41], s[82:83] op_sel_hi:[1,0]
	v_cvt_pk_bf16_f32 v38, v38, v39
	v_cvt_pk_bf16_f32 v39, v40, v41
	v_pk_mul_f32 v[40:41], v[68:69], s[82:83] op_sel_hi:[1,0]
	v_pk_mul_f32 v[46:47], v[66:67], s[82:83] op_sel_hi:[1,0]
	v_cvt_pk_bf16_f32 v40, v40, v41
	v_cvt_pk_bf16_f32 v41, v46, v47
	v_mul_f32_e32 v46, 0x45800000, v48
	v_cndmask_b32_e64 v46, v48, v46, s[4:5]
	v_pk_mul_f32 v[48:49], v[46:47], v[86:87] op_sel_hi:[0,1]
	v_pk_mul_f32 v[48:49], v[58:59], v[48:49]
	v_or_b32_e32 v86, 4, v170
	v_mov_b32_e32 v47, v48
	v_mov_b32_e32 v50, v48
	v_mov_b32_e32 v51, v49
	v_mov_b32_e32 v52, v49
	v_permlane16_swap_b32_e32 v47, v50
	s_nop 0
	v_permlane16_swap_b32_e32 v51, v52
	v_cndmask_b32_e32 v51, v51, v52, vcc
	v_cndmask_b32_e32 v50, v47, v50, vcc
	v_pk_fma_f32 v[48:49], v[50:51], 0, v[48:49] op_sel_hi:[1,0,1]
	v_pk_mul_f32 v[50:51], v[46:47], v[98:99] op_sel_hi:[0,1]
	v_pk_mul_f32 v[50:51], v[60:61], v[50:51]
	v_pk_mul_f32 v[48:49], v[48:49], s[82:83] op_sel_hi:[1,0]
	v_mov_b32_e32 v47, v50
	v_mov_b32_e32 v52, v50
	v_mov_b32_e32 v53, v51
	v_mov_b32_e32 v58, v51
	v_permlane16_swap_b32_e32 v47, v52
	s_nop 0
	v_permlane16_swap_b32_e32 v53, v58
	v_cndmask_b32_e32 v53, v53, v58, vcc
	v_cndmask_b32_e32 v52, v47, v52, vcc
	v_pk_fma_f32 v[52:53], v[52:53], 0, v[50:51] op_sel_hi:[1,0,1]
	v_pk_mul_f32 v[50:51], v[46:47], v[90:91] op_sel_hi:[0,1]
	v_pk_mul_f32 v[50:51], v[54:55], v[50:51]
	v_bitop3_b32 v74, v148, v86, v147 bitop3:0x36
	v_mov_b32_e32 v47, v50
	v_mov_b32_e32 v54, v50
	s_nop 1
	v_permlane16_swap_b32_e32 v47, v54
	v_mov_b32_e32 v55, v51
	v_mov_b32_e32 v58, v51
	s_nop 1
	v_permlane16_swap_b32_e32 v55, v58
	v_cndmask_b32_e32 v54, v47, v54, vcc
	v_pk_mul_f32 v[46:47], v[46:47], v[82:83] op_sel_hi:[0,1]
	v_cndmask_b32_e32 v55, v55, v58, vcc
	v_pk_mul_f32 v[46:47], v[56:57], v[46:47]
	v_pk_fma_f32 v[54:55], v[54:55], 0, v[50:51] op_sel_hi:[1,0,1]
	v_mov_b32_e32 v50, v46
	v_mov_b32_e32 v56, v46
	v_mov_b32_e32 v51, v47
	v_mov_b32_e32 v57, v47
	v_permlane16_swap_b32_e32 v50, v56
	s_nop 0
	v_permlane16_swap_b32_e32 v51, v57
	v_cndmask_b32_e32 v51, v51, v57, vcc
	v_cndmask_b32_e32 v50, v50, v56, vcc
	v_pk_fma_f32 v[46:47], v[50:51], 0, v[46:47] op_sel_hi:[1,0,1]
	v_cvt_pk_bf16_f32 v50, v48, v49
	v_pk_mul_f32 v[48:49], v[52:53], s[82:83] op_sel_hi:[1,0]
	v_pk_mul_f32 v[46:47], v[46:47], s[82:83] op_sel_hi:[1,0]
	v_cvt_pk_bf16_f32 v51, v48, v49
	v_pk_mul_f32 v[48:49], v[54:55], s[82:83] op_sel_hi:[1,0]
	v_cvt_pk_bf16_f32 v53, v46, v47
	v_cvt_pk_bf16_f32 v52, v48, v49
	s_waitcnt vmcnt(0) lgkmcnt(0)
	s_barrier
; #define ATT_SB() __builtin_amdgcn_sched_barrier(0)
; #define ATT_DMA_K(t, sl) do { glds16(ksrc + (size_t)(t) * 64 * kpitch, (unsigned)__builtin_amdgcn_readfirstlane(kdst + (sl) * KSLOT)); \
;         if constexpr (DQK == 96) glds16(krsrc + (size_t)(t) * 64 * 32, (unsigned)__builtin_amdgcn_readfirstlane(krdst + (sl) * KSLOT)); } while (0)
; #define ATT_DMA_V(t, sl) do { glds16(vsrc + (size_t)(t) * 64, (unsigned)__builtin_amdgcn_readfirstlane(vdst + (sl) * VSLOT)); \
;         if constexpr (DV == 128) glds16(vsrc + (size_t)64 * NR + (size_t)(t) * 64, (unsigned)__builtin_amdgcn_readfirstlane(vdst + (sl) * VSLOT + 8192)); } while (0)
; #define ATT_KLOAD(sl) do { _Pragma("unroll") for (int kb_ = 0; kb_ < NKW; ++kb_) _Pragma("unroll") for (int ds_ = 0; ds_ < NDS; ++ds_) { \
;         if (ds_ < 2) kf[kb_ * NDS + ds_] = *(const LAS bf16x8*)(kp[ds_ & 1] + (sl) * KSLOT + (kb_ & 1) * 512 + (kb_ >> 1) * 4096); \
;         else kf[kb_ * NDS + ds_] = *(const LAS bf16x8*)(krp + (sl) * KSLOT + (kb_ & 1) * 256 + (kb_ >> 1) * 2048); } } while (0)
; #define ATT_QK() do { _Pragma("unroll") for (int kb_ = 0; kb_ < NKW; ++kb_) _Pragma("unroll") for (int ds_ = 0; ds_ < NDS; ++ds_) _Pragma("unroll") for (int qb_ = 0; qb_ < NQB; ++qb_) \
;         c[kb_][qb_] = __builtin_amdgcn_mfma_f32_16x16x32_bf16(kf[kb_ * NDS + ds_], qf[qb_ * NDS + ds_], ds_ == 0 ? zero4 : c[kb_][qb_], 0, 0, 0); } while (0)
; template <int DQK, int DV, bool LEAD> ...
;     ...
;     bf16x8 kf[NKW * NDS], vf[NVF];
;     ATT_KLOAD(0);
;     asm volatile("s_waitcnt lgkmcnt(0)\n\ts_barrier" ::: "memory");
;     float lsum[NQB];
; #pragma unroll
;     for (int qb = 0; qb < NQB; ++qb) lsum[qb] = 0.f;
;     const f32x4 zero4 = {0.f, 0.f, 0.f, 0.f};
;     f32x4 o[NDB][NQB], c[NKW][NQB]; u32x4 pw[4];
; #pragma unroll
;     for (int i = 0; i < NDB; ++i)
; #pragma unroll
;         for (int qb = 0; qb < NQB; ++qb) o[i][qb] = zero4;
;     ATT_DMA_K(3, 0); ATT_DMA_V(1, 1);
;     ATT_QK(); ATT_SB();
;     ATT_KLOAD(1); ATT_SB();
;     if constexpr (LEAD) { ATT_EXP(); ATT_SUMPACK(); }
;     wait_bar<NDMA>();
;     int s_prev = 0, s_cur = 1, s_next = 2;
;     int one_ = 1; asm volatile("" : "+s"(one_));
	ds_read_b128 v[46:49], v194
	ds_read_b128 v[54:57], v194 offset:512
	v_lshl_add_u32 v211, v74, 4, v149
	s_waitcnt lgkmcnt(1)
	v_mfma_f32_16x16x32_bf16 v[58:61], v[46:49], v[6:9], 0
	ds_read_b128 v[74:77], v211
	ds_read_b128 v[78:81], v211 offset:512
	v_lshlrev_b32_e32 v82, 5, v146
	v_lshlrev_b32_e32 v83, 6, v144
	v_mfma_f32_16x16x32_bf16 v[66:69], v[46:49], v[18:21], 0
	v_bitop3_b32 v82, v82, v142, 48 bitop3:0x78
	s_lshl_b32 s4, s38, 11
	v_sub_u32_e32 v83, v145, v83
	v_mfma_f32_16x16x32_bf16 v[70:73], v[46:49], v[34:37], 0
	v_add3_u32 v212, v83, v82, s4
	s_cmpk_lt_u32 s16, 0x100
	s_mov_b32 s4, 0
	v_mfma_f32_16x16x32_bf16 v[46:49], v[46:49], v[30:33], 0
	s_cselect_b64 vcc, -1, 0
	s_mov_b32 s7, s4
	s_waitcnt lgkmcnt(1)
	v_mfma_f32_16x16x32_bf16 v[58:61], v[74:77], v[2:5], v[58:61]
	v_mfma_f32_16x16x32_bf16 v[66:69], v[74:77], v[14:17], v[66:69]
	v_mfma_f32_16x16x32_bf16 v[70:73], v[74:77], v[26:29], v[70:73]
	v_mfma_f32_16x16x32_bf16 v[46:49], v[74:77], v[38:41], v[46:49]
	ds_read_b128 v[74:77], v212 offset:8192
	ds_read_b128 v[82:85], v212 offset:8448
	s_waitcnt lgkmcnt(0)
	s_barrier
	s_mov_b32 m0, s30
	s_nop 0
	global_load_lds_dwordx4 v[192:193], off
	s_waitcnt lgkmcnt(1)
	v_mfma_f32_16x16x32_bf16 v[150:153], v[74:77], v[10:13], v[58:61]
	s_mov_b32 m0, s41
	s_nop 0
	global_load_lds_dwordx4 v[204:205], off
	s_add_i32 s5, s31, 0x2000
	v_mfma_f32_16x16x32_bf16 v[138:141], v[74:77], v[22:25], v[66:69]
	v_mfma_f32_16x16x32_bf16 v[122:125], v[74:77], v[50:53], v[46:49]
	v_mfma_f32_16x16x32_bf16 v[46:49], v[54:57], v[6:9], 0
	v_mfma_f32_16x16x32_bf16 v[58:61], v[54:57], v[18:21], 0
	v_mfma_f32_16x16x32_bf16 v[66:69], v[54:57], v[34:37], 0
	v_mfma_f32_16x16x32_bf16 v[54:57], v[54:57], v[30:33], 0
	v_mfma_f32_16x16x32_bf16 v[46:49], v[78:81], v[2:5], v[46:49]
	v_mfma_f32_16x16x32_bf16 v[58:61], v[78:81], v[14:17], v[58:61]
	v_mfma_f32_16x16x32_bf16 v[66:69], v[78:81], v[26:29], v[66:69]
	v_mfma_f32_16x16x32_bf16 v[54:57], v[78:81], v[38:41], v[54:57]
	v_mfma_f32_16x16x32_bf16 v[130:133], v[74:77], v[42:45], v[70:73]
	s_waitcnt lgkmcnt(0)
	v_mfma_f32_16x16x32_bf16 v[166:169], v[82:85], v[10:13], v[46:49]
	s_nop 0
	v_lshrrev_b32_e32 v70, 1, v142
	v_lshlrev_b32_e32 v71, 7, v143
	v_lshl_add_u64 v[46:47], v[186:187], 0, s[66:67]
	v_mfma_f32_16x16x32_bf16 v[162:165], v[82:85], v[22:25], v[58:61]
	s_mov_b32 m0, s5
	s_nop 0
	global_load_lds_dwordx4 v[46:47], off
	s_mov_b32 s6, s4
	s_mov_b32 s5, s4
	v_mfma_f32_16x16x32_bf16 v[154:157], v[82:85], v[42:45], v[66:69]
	v_mov_b64_e32 v[48:49], s[6:7]
	v_mov_b64_e32 v[46:47], s[4:5]
	v_mfma_f32_16x16x32_bf16 v[146:149], v[82:85], v[50:53], v[54:57]
	ds_read_b128 v[114:117], v194 offset:12288
	ds_read_b128 v[134:137], v194 offset:12800
	ds_read_b128 v[118:121], v211 offset:12288
	ds_read_b128 v[142:145], v211 offset:12800
	ds_read_b128 v[126:129], v212 offset:20480
	ds_read_b128 v[158:161], v212 offset:20736
	v_cndmask_b32_e32 v54, v86, v170, vcc
	v_bitop3_b32 v54, v54, v70, 7 bitop3:0x78
	v_lshlrev_b32_e32 v54, 4, v54
	v_add3_u32 v210, 0, v71, v54
	s_waitcnt vmcnt(3) lgkmcnt(0)
	s_barrier
	s_mov_b32 s5, 1
	v_mov_b32_e32 v188, 0
	s_cmp_lg_u32 s5, 0
	v_mov_b64_e32 v[56:57], v[48:49]
	v_mov_b64_e32 v[60:61], v[48:49]
	v_mov_b64_e32 v[64:65], v[48:49]
	v_mov_b64_e32 v[68:69], v[48:49]
	v_mov_b64_e32 v[72:73], v[48:49]
	v_mov_b64_e32 v[76:77], v[48:49]
	v_mov_b64_e32 v[80:81], v[48:49]
	v_mov_b64_e32 v[84:85], v[48:49]
	v_mov_b64_e32 v[88:89], v[48:49]
	v_mov_b64_e32 v[92:93], v[48:49]
	v_mov_b64_e32 v[96:97], v[48:49]
	v_mov_b64_e32 v[100:101], v[48:49]
	v_mov_b64_e32 v[104:105], v[48:49]
	v_mov_b64_e32 v[108:109], v[48:49]
	v_mov_b64_e32 v[112:113], v[48:49]
	s_cselect_b64 s[6:7], -1, 0
	v_mov_b64_e32 v[54:55], v[46:47]
	v_mov_b64_e32 v[58:59], v[46:47]
	v_mov_b64_e32 v[62:63], v[46:47]
	v_mov_b64_e32 v[66:67], v[46:47]
	v_mov_b64_e32 v[70:71], v[46:47]
	v_mov_b64_e32 v[74:75], v[46:47]
	v_mov_b64_e32 v[78:79], v[46:47]
	v_mov_b64_e32 v[82:83], v[46:47]
	v_mov_b64_e32 v[86:87], v[46:47]
	v_mov_b64_e32 v[90:91], v[46:47]
	v_mov_b64_e32 v[94:95], v[46:47]
	v_mov_b64_e32 v[98:99], v[46:47]
	v_mov_b64_e32 v[102:103], v[46:47]
	v_mov_b64_e32 v[106:107], v[46:47]
	v_mov_b64_e32 v[110:111], v[46:47]
	s_mov_b32 s16, 2
	v_mov_b32_e32 v189, v188
	v_mov_b32_e32 v190, v188
	v_mov_b32_e32 v191, v188
; #define ATT_SB() __builtin_amdgcn_sched_barrier(0)
; #define ATT_DMA_K(t, sl) do { glds16(ksrc + (size_t)(t) * 64 * kpitch, (unsigned)__builtin_amdgcn_readfirstlane(kdst + (sl) * KSLOT)); \
;         if constexpr (DQK == 96) glds16(krsrc + (size_t)(t) * 64 * 32, (unsigned)__builtin_amdgcn_readfirstlane(krdst + (sl) * KSLOT)); } while (0)
; #define ATT_DMA_V(t, sl) do { glds16(vsrc + (size_t)(t) * 64, (unsigned)__builtin_amdgcn_readfirstlane(vdst + (sl) * VSLOT)); \
;         if constexpr (DV == 128) glds16(vsrc + (size_t)64 * NR + (size_t)(t) * 64, (unsigned)__builtin_amdgcn_readfirstlane(vdst + (sl) * VSLOT + 8192)); } while (0)
; template <int DQK, int DV, bool LEAD> ...
;     ...
;     for (int t = 1; t < NT; ++t) {
;         __builtin_amdgcn_s_waitcnt(0xC07F);
;         if constexpr (!LEAD) { ATT_EXP(); ATT_SUMPACK(); ATT_SB(); }
;         ATT_VLOAD(s_prev, 0); ATT_SB();
;         { const int tk = (t + 3 < NT) ? t + 3 : NT - 1; ATT_DMA_K(tk, s_cur); }
;         { const int tv = (t + 1 < NT) ? t + 1 : NT - 1; ATT_DMA_V(tv, s_next); }
;         ATT_SB();
;         if constexpr (LEAD) {
;             ATT_QK(); ATT_SB();
;             ATT_PVP(0); ATT_SB();
;             if constexpr (DV == 128) { ATT_VLOAD(s_prev, 1); ATT_SB(); ATT_EXP(); ATT_SB(); ATT_PVP(1); ATT_SB(); }
;             if (one_) ATT_KLOAD(s_next);
;             ATT_SB();
;             if constexpr (DV == 64) ATT_EXP();
;             ATT_SUMPACK();
;             asm volatile("" : "+v"(pw[0]), "+v"(pw[1]), "+v"(pw[2]), "+v"(pw[3]));
; #pragma unroll
;             for (int qb = 0; qb < NQB; ++qb) asm volatile("" : "+v"(lsum[qb]));
;         } else {
;             if constexpr (DV == 128) {
;                 ATT_PVP(0); ATT_SB();
;                 ATT_VLOAD(s_prev, 1); ATT_SB();
;                 ATT_QK(); ATT_SB();
;                 if (one_) { ATT_KLOAD(s_next); ATT_SB(); ATT_PVP(1); }
;                 ATT_SB();
;             } else {
;                 __builtin_amdgcn_s_setprio(1);
;                 ATT_QK(); ATT_SB();
;                 if (one_) { ATT_KLOAD(s_next); ATT_SB(); ATT_PVP(0); }
;                 ATT_SB();
;                 __builtin_amdgcn_s_setprio(0);
;             }
; #pragma unroll
;             for (int kb = 0; kb < NKW; ++kb)
; #pragma unroll
;                 for (int qb = 0; qb < NQB; ++qb) asm volatile("" : "+v"(c[kb][qb]));
.LBB0_662:
	v_exp_f32_e32 v213, v150
	v_exp_f32_e32 v214, v151
	v_exp_f32_e32 v215, v152
	v_exp_f32_e32 v216, v153
	v_exp_f32_e32 v217, v138
	v_exp_f32_e32 v218, v139
	v_exp_f32_e32 v219, v140
	v_exp_f32_e32 v220, v141
	v_exp_f32_e32 v221, v130
	v_exp_f32_e32 v236, v131
	v_exp_f32_e32 v238, v132
	v_exp_f32_e32 v240, v133
	v_exp_f32_e32 v243, v122
	v_exp_f32_e32 v244, v123
	v_exp_f32_e32 v246, v124
	v_exp_f32_e32 v248, v125
	v_add_f32_e32 v122, v213, v214
	v_add_f32_e32 v123, v215, v216
	v_exp_f32_e32 v237, v166
	v_exp_f32_e32 v245, v162
	v_exp_f32_e32 v223, v154
	v_exp_f32_e32 v251, v146
	v_add_f32_e32 v122, v122, v123
	v_add_f32_e32 v123, v217, v218
	v_add_f32_e32 v124, v219, v220
	v_add_f32_e32 v123, v123, v124
	v_add_f32_e32 v124, v221, v236
	v_add_f32_e32 v125, v238, v240
	v_exp_f32_e32 v239, v167
	v_exp_f32_e32 v247, v163
	v_exp_f32_e32 v197, v155
	v_exp_f32_e32 v252, v147
	v_add_f32_e32 v124, v124, v125
	v_add_f32_e32 v125, v243, v244
	v_add_f32_e32 v130, v246, v248
	v_add_f32_e32 v125, v125, v130
	v_exp_f32_e32 v241, v168
	v_exp_f32_e32 v249, v164
	v_exp_f32_e32 v232, v156
	v_exp_f32_e32 v253, v148
	v_add_f32_e32 v122, v237, v122
	v_add_f32_e32 v123, v245, v123
	v_add_f32_e32 v124, v223, v124
	v_add_f32_e32 v125, v251, v125
	s_waitcnt lgkmcnt(0)
	v_exp_f32_e32 v242, v169
	v_exp_f32_e32 v250, v165
	v_exp_f32_e32 v235, v157
	v_exp_f32_e32 v254, v149
	s_mov_b32 s5, s42
	v_add_f32_e32 v122, v239, v122
	v_add_f32_e32 v123, v247, v123
	v_add_f32_e32 v124, v197, v124
	v_add_f32_e32 v125, v252, v125
	s_mov_b32 s42, s16
	v_add_f32_e32 v122, v241, v122
	v_add_f32_e32 v123, v249, v123
	v_add_f32_e32 v124, v232, v124
	v_add_f32_e32 v125, v253, v125
	s_nop 0
	v_add_f32_e32 v209, v242, v122
	v_add_f32_e32 v208, v250, v123
	v_add_f32_e32 v207, v235, v124
	v_add_f32_e32 v206, v254, v125
	v_lshl_add_u32 v122, s4, 13, v210
	ds_read_b128 v[182:185], v122 offset:36864
	ds_read_b128 v[178:181], v122 offset:38912
	ds_read_b128 v[174:177], v122 offset:40960
	ds_read_b128 v[170:173], v122 offset:43008
	s_mul_i32 s16, s5, 0x3000
	s_add_i32 s38, s16, s30
	s_mov_b32 m0, s38
	s_nop 0
	global_load_lds_dwordx4 v[192:193], off
	s_add_i32 s16, s16, s41
	s_mov_b32 m0, s16
	s_nop 0
	global_load_lds_dwordx4 v[204:205], off
	s_min_u32 s16, s43, 3
	s_lshl_b32 s38, s16, 7
	s_lshl_b32 s16, s42, 13
	v_lshl_add_u64 v[122:123], v[186:187], 0, s[38:39]
	s_add_i32 s16, s16, s31
	s_mov_b32 m0, s16
	s_nop 0
	global_load_lds_dwordx4 v[122:123], off
	s_setprio 1
	v_mfma_f32_16x16x32_bf16 v[122:125], v[114:117], v[6:9], 0
	v_mfma_f32_16x16x32_bf16 v[130:133], v[114:117], v[18:21], 0
	v_mfma_f32_16x16x32_bf16 v[138:141], v[114:117], v[34:37], 0
	v_mfma_f32_16x16x32_bf16 v[146:149], v[114:117], v[30:33], 0
	v_mfma_f32_16x16x32_bf16 v[122:125], v[118:121], v[2:5], v[122:125]
	v_mfma_f32_16x16x32_bf16 v[130:133], v[118:121], v[14:17], v[130:133]
	v_mfma_f32_16x16x32_bf16 v[154:157], v[118:121], v[26:29], v[138:141]
	v_mfma_f32_16x16x32_bf16 v[146:149], v[118:121], v[38:41], v[146:149]
	v_mfma_f32_16x16x32_bf16 v[150:153], v[126:129], v[10:13], v[122:125]
	v_mfma_f32_16x16x32_bf16 v[138:141], v[126:129], v[22:25], v[130:133]
	v_mfma_f32_16x16x32_bf16 v[130:133], v[126:129], v[42:45], v[154:157]
	v_mfma_f32_16x16x32_bf16 v[122:125], v[126:129], v[50:53], v[146:149]
	v_mfma_f32_16x16x32_bf16 v[146:149], v[134:137], v[6:9], 0
	v_mfma_f32_16x16x32_bf16 v[154:157], v[134:137], v[18:21], 0
	v_mfma_f32_16x16x32_bf16 v[162:165], v[134:137], v[34:37], 0
	v_mfma_f32_16x16x32_bf16 v[166:169], v[134:137], v[30:33], 0
	v_mfma_f32_16x16x32_bf16 v[146:149], v[142:145], v[2:5], v[146:149]
	v_mfma_f32_16x16x32_bf16 v[154:157], v[142:145], v[14:17], v[154:157]
	v_mfma_f32_16x16x32_bf16 v[198:201], v[142:145], v[26:29], v[162:165]
	v_mfma_f32_16x16x32_bf16 v[228:231], v[142:145], v[38:41], v[166:169]
	v_mfma_f32_16x16x32_bf16 v[166:169], v[158:161], v[10:13], v[146:149]
	v_mfma_f32_16x16x32_bf16 v[162:165], v[158:161], v[22:25], v[154:157]
	v_mfma_f32_16x16x32_bf16 v[154:157], v[158:161], v[42:45], v[198:201]
	v_mfma_f32_16x16x32_bf16 v[146:149], v[158:161], v[50:53], v[228:231]
	s_andn2_b64 vcc, exec, s[6:7]
	s_cbranch_vccnz .LBB0_664
	s_mul_i32 s16, s42, 0x3000
	v_add_u32_e32 v158, s16, v212
	v_add_u32_e32 v134, s16, v194
	v_add_u32_e32 v142, s16, v211
	ds_read_b128 v[114:117], v134
	ds_read_b128 v[118:121], v142
	ds_read_b128 v[126:129], v158 offset:8192
	ds_read_b128 v[134:137], v134 offset:512
	ds_read_b128 v[142:145], v142 offset:512
	ds_read_b128 v[158:161], v158 offset:8448
	v_cvt_pk_bf16_f32 v201, v253, v254
	v_cvt_pk_bf16_f32 v200, v251, v252
	v_cvt_pk_bf16_f32 v199, v246, v248
	v_cvt_pk_bf16_f32 v198, v243, v244
	v_cvt_pk_bf16_f32 v231, v232, v235
	v_cvt_pk_bf16_f32 v230, v223, v197
	v_cvt_pk_bf16_f32 v229, v238, v240
	v_cvt_pk_bf16_f32 v228, v221, v236
	v_cvt_pk_bf16_f32 v223, v249, v250
	v_cvt_pk_bf16_f32 v222, v245, v247
	v_cvt_pk_bf16_f32 v221, v219, v220
	v_cvt_pk_bf16_f32 v220, v217, v218
	v_cvt_pk_bf16_f32 v219, v241, v242
	v_cvt_pk_bf16_f32 v218, v237, v239
	v_cvt_pk_bf16_f32 v217, v215, v216
	v_cvt_pk_bf16_f32 v216, v213, v214
	s_waitcnt lgkmcnt(9)
	s_nop 0
	v_mfma_f32_16x16x32_bf16 v[110:113], v[182:185], v[216:219], v[110:113]
	v_mfma_f32_16x16x32_bf16 v[106:109], v[182:185], v[220:223], v[106:109]
	v_mfma_f32_16x16x32_bf16 v[102:105], v[182:185], v[228:231], v[102:105]
	v_mfma_f32_16x16x32_bf16 v[98:101], v[182:185], v[198:201], v[98:101]
	s_waitcnt lgkmcnt(8)
	v_mfma_f32_16x16x32_bf16 v[94:97], v[178:181], v[216:219], v[94:97]
	v_mfma_f32_16x16x32_bf16 v[90:93], v[178:181], v[220:223], v[90:93]
	v_mfma_f32_16x16x32_bf16 v[86:89], v[178:181], v[228:231], v[86:89]
	v_mfma_f32_16x16x32_bf16 v[82:85], v[178:181], v[198:201], v[82:85]
	s_waitcnt lgkmcnt(7)
	v_mfma_f32_16x16x32_bf16 v[78:81], v[174:177], v[216:219], v[78:81]
	v_mfma_f32_16x16x32_bf16 v[74:77], v[174:177], v[220:223], v[74:77]
	v_mfma_f32_16x16x32_bf16 v[70:73], v[174:177], v[228:231], v[70:73]
	v_mfma_f32_16x16x32_bf16 v[66:69], v[174:177], v[198:201], v[66:69]
	s_waitcnt lgkmcnt(6)
	v_mfma_f32_16x16x32_bf16 v[62:65], v[170:173], v[216:219], v[62:65]
	v_mfma_f32_16x16x32_bf16 v[58:61], v[170:173], v[220:223], v[58:61]
	v_mfma_f32_16x16x32_bf16 v[54:57], v[170:173], v[228:231], v[54:57]
	v_mfma_f32_16x16x32_bf16 v[46:49], v[170:173], v[198:201], v[46:49]

; #define ATT_DMA_K(t, sl) do { glds16(ksrc + (size_t)(t) * 64 * kpitch, (unsigned)__builtin_amdgcn_readfirstlane(kdst + (sl) * KSLOT)); \
;         if constexpr (DQK == 96) glds16(krsrc + (size_t)(t) * 64 * 32, (unsigned)__builtin_amdgcn_readfirstlane(krdst + (sl) * KSLOT)); } while (0)
; template <int DQK, int DV, bool LEAD> ...
;     ...
;     const int krow_l = wid * 8 + (lane >> 3);
;     const int kc_l = (lane & 7) ^ (((krow_l >> 1) & 1) | (((krow_l >> 3) & 1) << 1) | (((krow_l >> 4) & 1) << 2));
;     const int vc_l = (lane & 7) ^ ((krow_l >> 1) & 7);
;     const bf16_t* ksrc = K + (size_t)(krow0 + krow_l) * kpitch + kc_l * 8;
;     const int rrow_l = (wid & 3) * 16 + (lane >> 2), rc_l = (lane & 3) ^ (((rrow_l >> 4) & 1) << 1);
;     const bf16_t* krsrc = (DQK == 96) ? KR + (size_t)(krow0 + rrow_l) * 32 + rc_l * 8 : nullptr;
;     const bf16_t* vsrc = Vt + (size_t)krow_l * NR + krow0 + vc_l * 8;
;     const unsigned kdst = lds0 + KOFF + wid * 1024, krdst = lds0 + KOFF + 8192 + (wid & 3) * 1024, vdst = lds0 + VOFF + wid * 1024;
;     ...
;     ATT_DMA_K(0, 0); ATT_DMA_V(0, 0); ATT_DMA_K(1, 1); ATT_DMA_K(2, 2);
;     bf16x8 qf[NQB * NDS];
;     {
;       const float c2 = (DQK == 64) ? C2_EVEN : C2_ODD; const bool lat = tq0 >= 0;
; #pragma unroll
;       for (int qb = 0; qb < NQB; ++qb) {
;           const bf16_t* qp = Q + (size_t)(qrow0 + qoff + qb * 16 + q16) * qpitch + g4 * 8;
;           bf16x8 raw[NDS];
; #pragma unroll
;           for (int ds = 0; ds < NDS; ++ds) raw[ds] = *(const bf16x8*)(qp + ds * 32);
;           float x[NDS][8];
; #pragma unroll
;           for (int ds = 0; ds < NDS; ++ds)
; #pragma unroll
;               for (int j = 0; j < 8; ++j) x[ds][j] = __uint_as_float(((unsigned)(unsigned short)raw[ds][j]) << 16);
;           const int tq = tq0 + qoff + qb * 16 + q16, prow = (tq >> 6) & 127, pcol = tq & 63;
;           float sn = 0.f;
; #pragma unroll
;           for (int ds = 0; ds < 2; ++ds)
; #pragma unroll
;               for (int j = 0; j < 8; ++j) sn += x[ds][j] * x[ds][j];
;           sn = lanes4_sum(sn);
;           const float rn = rsqrtf(sn * (1.f / 64.f) + EPS);
.LBB0_667:
	v_mov_b32_e32 v142, v0
	v_mov_b64_e32 v[6:7], s[46:47]
	v_readfirstlane_b32 s16, v142
	s_ashr_i32 s4, s16, 6
	v_bfe_u32 v203, v142, 3, 3
	v_lshl_or_b32 v8, s4, 3, v203
	v_ashrrev_i32_e32 v2, 1, v8
	s_and_b32 s30, s4, 3
	v_and_b32_e32 v3, 1, v2
	s_lshl_b32 s5, s4, 1
	s_lshr_b32 s7, s16, 5
	v_bfe_u32 v4, v142, 2, 4
	v_and_b32_e32 v206, 7, v142
	s_and_b32 s6, s5, 2
	v_and_or_b32 v3, s7, 4, v3
	v_xor_b32_e32 v10, v2, v142
	v_add_u32_e32 v2, s40, v8
	v_lshl_or_b32 v4, s30, 4, v4
	v_bitop3_b32 v9, v3, v206, s6 bitop3:0x36
	v_ashrrev_i32_e32 v3, 31, v2
	v_and_b32_e32 v18, 3, v142
	v_or_b32_e32 v4, s40, v4
	s_lshl_b32 s4, s4, 10
	v_lshlrev_b64 v[2:3], 11, v[2:3]
	v_bitop3_b32 v11, s5, v18, 2 bitop3:0x6c
	v_ashrrev_i32_e32 v5, 31, v4
	s_add_i32 s31, s4, 0
	s_lshl_b32 s6, s30, 10
	v_mad_i64_i32 v[6:7], s[4:5], v8, s91, v[6:7]
	v_lshlrev_b64 v[4:5], 6, v[4:5]
	v_lshl_add_u64 v[2:3], s[44:45], 0, v[2:3]
	v_lshlrev_b32_e32 v194, 4, v9
	s_add_i32 s5, s6, 0
	s_ashr_i32 s41, s40, 31
	v_lshl_add_u64 v[4:5], s[28:29], 0, v[4:5]
	v_lshl_add_u64 v[62:63], v[2:3], 0, v[194:195]
	v_lshlrev_b32_e32 v194, 4, v11
	v_lshlrev_b32_e32 v2, 4, v10
	s_add_i32 s42, s5, 0x2000
	s_mov_b32 m0, s31
	s_nop 0
	global_load_lds_dwordx4 v[62:63], off
	v_lshl_add_u64 v[6:7], s[40:41], 1, v[6:7]
	v_lshl_add_u64 v[64:65], v[4:5], 0, v[194:195]
	v_and_b32_e32 v194, 0x70, v2
	s_mov_b32 m0, s42
	s_nop 0
	global_load_lds_dwordx4 v[64:65], off
	s_add_i32 s41, s31, 0x9000
	v_lshl_add_u64 v[186:187], v[6:7], 0, v[194:195]
	s_mov_b32 m0, s41
	s_nop 0
	global_load_lds_dwordx4 v[186:187], off
	s_mov_b64 s[6:7], 0x20000
	v_lshl_add_u64 v[2:3], v[62:63], 0, s[6:7]
	s_add_i32 s5, s31, 0x3000
	s_mov_b32 m0, s5
	s_nop 0
	global_load_lds_dwordx4 v[2:3], off
	v_lshl_add_u64 v[2:3], v[64:65], 0, s[60:61]
	s_add_i32 s5, s42, 0x3000
	s_mov_b32 m0, s5
	s_nop 0
	global_load_lds_dwordx4 v[2:3], off
	s_mov_b64 s[6:7], 0x40000
	s_lshl_b32 s4, s30, 6
	v_lshl_add_u64 v[2:3], v[62:63], 0, s[6:7]
	s_add_i32 s5, s31, 0x6000
	s_mov_b32 m0, s5
	s_nop 0
	global_load_lds_dwordx4 v[2:3], off
	v_and_b32_e32 v143, 15, v142
	s_mov_b64 s[6:7], 0x2000
	s_or_b32 s24, s4, s40
	v_and_b32_e32 v8, 48, v142
	v_lshl_add_u64 v[2:3], v[64:65], 0, s[6:7]
	v_or_b32_e32 v6, s24, v143
	v_mov_b32_e32 v9, v195
	s_add_i32 s5, s42, 0x6000
	s_mov_b32 m0, s5
	s_nop 0
	global_load_lds_dwordx4 v[2:3], off
	v_lshl_add_u64 v[2:3], s[36:37], 0, v[8:9]
	v_or_b32_e32 v7, 16, v6
	v_mad_i64_i32 v[4:5], s[4:5], v6, s90, v[2:3]
	v_mad_i64_i32 v[10:11], s[4:5], v7, s90, v[2:3]
	v_or_b32_e32 v7, 32, v6
	v_or_b32_e32 v6, 48, v6
	v_mad_i64_i32 v[14:15], s[4:5], v7, s90, v[2:3]
	v_mad_i64_i32 v[16:17], s[4:5], v6, s90, v[2:3]
	global_load_dwordx4 v[28:31], v[4:5], off offset:64
	global_load_dwordx4 v[46:49], v[10:11], off offset:64
	global_load_dwordx4 v[50:53], v[14:15], off offset:64
	global_load_dwordx4 v[54:57], v[16:17], off offset:64
	global_load_dwordx4 v[58:61], v[4:5], off
	global_load_dwordx4 v[88:91], v[10:11], off
	global_load_dwordx4 v[94:97], v[14:15], off
	global_load_dwordx4 v[6:9], v[16:17], off
	s_nop 0
	global_load_dwordx4 v[10:13], v[10:11], off offset:128
	v_lshlrev_b32_e32 v207, 1, v142
	v_and_or_b32 v144, v207, 24, v18
	v_bfe_u32 v146, v142, 3, 1
	v_bfe_u32 v194, v142, 4, 2
	s_ashr_i32 s36, s16, 8
	v_bfe_u32 v147, v142, 1, 2
	v_lshlrev_b32_e32 v148, 2, v146
	v_lshl_add_u32 v145, v144, 7, 0
	v_lshl_add_u32 v149, s36, 12, v145
	v_bitop3_b32 v2, v148, v194, v147 bitop3:0x36
	v_lshl_add_u32 v208, v2, 4, v149
	global_load_dwordx4 v[2:5], v[4:5], off offset:128
	v_lshlrev_b32_e32 v82, 5, v194
	global_load_dwordx4 v[22:25], v[14:15], off offset:128
	global_load_dwordx4 v[34:37], v[16:17], off offset:128
	global_load_dwordx4 v[38:41], v82, s[26:27] offset:144
	global_load_dwordx4 v[42:45], v82, s[26:27] offset:128
	s_mov_b32 s6, 0x3d000000
	s_brev_b32 s7, 60
	s_mov_b32 s4, 0x358637bd
	s_mov_b32 s7, 0x3c800000
	v_mov_b64_e32 v[106:107], s[4:5]
	v_and_b32_e32 v112, 16, v142
	v_or_b32_e32 v209, 4, v194
	v_and_b32_e32 v210, 63, v142
	v_lshlrev_b32_e32 v211, 7, v143
	s_waitcnt vmcnt(10)
	v_and_b32_e32 v73, 0xffff0000, v54
	s_waitcnt vmcnt(9)
	v_and_b32_e32 v137, 0xffff0000, v58
	v_lshlrev_b32_e32 v136, 16, v58
	v_and_b32_e32 v135, 0xffff0000, v59
	s_waitcnt vmcnt(6)
; template <int DQK, int DV, bool LEAD> ...
;     ...
;           const bf16_t* qp = Q + (size_t)(qrow0 + qoff + qb * 16 + q16) * qpitch + g4 * 8;
;           bf16x8 raw[NDS];
; #pragma unroll
;           for (int ds = 0; ds < NDS; ++ds) raw[ds] = *(const bf16x8*)(qp + ds * 32);
;           float x[NDS][8];
; #pragma unroll
;           for (int ds = 0; ds < NDS; ++ds)
; #pragma unroll
;               for (int j = 0; j < 8; ++j) x[ds][j] = __uint_as_float(((unsigned)(unsigned short)raw[ds][j]) << 16);
;           const int tq = tq0 + qoff + qb * 16 + q16, prow = (tq >> 6) & 127, pcol = tq & 63;
;           float sn = 0.f;
; #pragma unroll
;           for (int ds = 0; ds < 2; ++ds)
; #pragma unroll
;               for (int j = 0; j < 8; ++j) sn += x[ds][j] * x[ds][j];
;           sn = lanes4_sum(sn);
	v_and_b32_e32 v77, 0xffff0000, v8
	v_lshlrev_b32_e32 v76, 16, v8
	v_mul_f32_e32 v8, v137, v137
	v_and_b32_e32 v75, 0xffff0000, v9
	v_lshlrev_b32_e32 v74, 16, v9
	v_lshlrev_b32_e32 v134, 16, v59
	v_pk_fma_f32 v[8:9], v[136:137], v[136:137], v[8:9] op_sel_hi:[1,1,0]
	v_lshlrev_b32_e32 v72, 16, v54
	v_pk_fma_f32 v[8:9], v[134:135], v[134:135], v[8:9]
	v_mul_f32_e32 v54, v135, v135
	v_and_b32_e32 v133, 0xffff0000, v60
	v_lshlrev_b32_e32 v132, 16, v60
	v_pk_add_f32 v[8:9], v[54:55], v[8:9] op_sel_hi:[0,1]
	v_pk_fma_f32 v[8:9], v[132:133], v[132:133], v[8:9]
	v_mul_f32_e32 v54, v133, v133
	v_and_b32_e32 v127, 0xffff0000, v61
	v_lshlrev_b32_e32 v126, 16, v61
	v_pk_add_f32 v[8:9], v[54:55], v[8:9] op_sel_hi:[0,1]
	v_pk_fma_f32 v[8:9], v[126:127], v[126:127], v[8:9]
	v_mul_f32_e32 v54, v127, v127
	v_and_b32_e32 v125, 0xffff0000, v28
	v_lshlrev_b32_e32 v124, 16, v28
	v_pk_add_f32 v[8:9], v[54:55], v[8:9] op_sel_hi:[0,1]
	v_pk_fma_f32 v[8:9], v[124:125], v[124:125], v[8:9]
	v_mul_f32_e32 v54, v125, v125
	v_and_b32_e32 v123, 0xffff0000, v29
	v_lshlrev_b32_e32 v122, 16, v29
	v_pk_add_f32 v[8:9], v[54:55], v[8:9] op_sel_hi:[0,1]
	v_pk_fma_f32 v[8:9], v[122:123], v[122:123], v[8:9]
	v_mul_f32_e32 v54, v123, v123
	v_and_b32_e32 v121, 0xffff0000, v30
	v_lshlrev_b32_e32 v120, 16, v30
	v_pk_add_f32 v[8:9], v[54:55], v[8:9] op_sel_hi:[0,1]
	v_pk_fma_f32 v[8:9], v[120:121], v[120:121], v[8:9]
	v_mul_f32_e32 v54, v121, v121
	v_and_b32_e32 v17, 0xffff0000, v31
	v_lshlrev_b32_e32 v16, 16, v31
	v_pk_add_f32 v[8:9], v[54:55], v[8:9] op_sel_hi:[0,1]
	v_pk_fma_f32 v[8:9], v[16:17], v[16:17], v[8:9]
	v_mul_f32_e32 v54, v17, v17
	v_pk_add_f32 v[8:9], v[54:55], v[8:9] op_sel_hi:[0,1]
	v_and_b32_e32 v79, 0xffff0000, v7
	v_lshlrev_b32_e32 v78, 16, v7
	v_mov_b32_e32 v7, v8
	s_nop 1
	v_permlane16_swap_b32_e32 v8, v7
	v_add_f32_e32 v7, v8, v7
	v_mov_b32_e32 v9, v7
	v_and_b32_e32 v119, 0xffff0000, v88
	s_nop 0
	v_permlane32_swap_b32_e32 v7, v9
	v_lshlrev_b32_e32 v118, 16, v88
	v_mul_f32_e32 v8, v119, v119
	v_and_b32_e32 v71, 0xffff0000, v55
	v_lshlrev_b32_e32 v70, 16, v55
	v_and_b32_e32 v109, 0xffff0000, v89
	v_lshlrev_b32_e32 v108, 16, v89
	v_pk_fma_f32 v[54:55], v[118:119], v[118:119], v[8:9] op_sel_hi:[1,1,0]
	v_mul_f32_e32 v8, v109, v109
	v_pk_fma_f32 v[54:55], v[108:109], v[108:109], v[54:55]
	v_and_b32_e32 v105, 0xffff0000, v90
	v_lshlrev_b32_e32 v104, 16, v90
	v_pk_add_f32 v[54:55], v[8:9], v[54:55] op_sel_hi:[0,1]
	v_pk_fma_f32 v[54:55], v[104:105], v[104:105], v[54:55]
	v_mul_f32_e32 v8, v105, v105
	v_and_b32_e32 v103, 0xffff0000, v91
	v_lshlrev_b32_e32 v102, 16, v91
	v_pk_add_f32 v[54:55], v[8:9], v[54:55] op_sel_hi:[0,1]
	v_pk_fma_f32 v[54:55], v[102:103], v[102:103], v[54:55]
	v_mul_f32_e32 v8, v103, v103
	v_and_b32_e32 v29, 0xffff0000, v46
	v_lshlrev_b32_e32 v28, 16, v46
	v_pk_add_f32 v[54:55], v[8:9], v[54:55] op_sel_hi:[0,1]
	v_pk_fma_f32 v[54:55], v[28:29], v[28:29], v[54:55]
	v_mul_f32_e32 v8, v29, v29
	v_and_b32_e32 v21, 0xffff0000, v47
	v_lshlrev_b32_e32 v20, 16, v47
	v_pk_add_f32 v[54:55], v[8:9], v[54:55] op_sel_hi:[0,1]
	v_pk_fma_f32 v[54:55], v[20:21], v[20:21], v[54:55]
	v_mul_f32_e32 v8, v21, v21
	v_and_b32_e32 v19, 0xffff0000, v48
	v_lshlrev_b32_e32 v18, 16, v48
	v_pk_add_f32 v[54:55], v[8:9], v[54:55] op_sel_hi:[0,1]
	v_pk_fma_f32 v[54:55], v[18:19], v[18:19], v[54:55]
	v_mul_f32_e32 v8, v19, v19
	v_and_b32_e32 v15, 0xffff0000, v49
	v_lshlrev_b32_e32 v14, 16, v49
	v_pk_add_f32 v[54:55], v[8:9], v[54:55] op_sel_hi:[0,1]
	v_pk_fma_f32 v[54:55], v[14:15], v[14:15], v[54:55]
	v_mul_f32_e32 v8, v15, v15
	v_pk_add_f32 v[54:55], v[8:9], v[54:55] op_sel_hi:[0,1]
	v_mov_b32_e32 v8, v54
	s_nop 1
	v_permlane16_swap_b32_e32 v54, v8
	v_and_b32_e32 v101, 0xffff0000, v94
	v_add_f32_e32 v129, v54, v8
	v_lshlrev_b32_e32 v100, 16, v94
	v_mul_f32_e32 v8, v101, v101
	v_and_b32_e32 v93, 0xffff0000, v95
	v_lshlrev_b32_e32 v92, 16, v95
	v_pk_fma_f32 v[54:55], v[100:101], v[100:101], v[8:9] op_sel_hi:[1,1,0]
	v_mul_f32_e32 v8, v93, v93
	v_pk_fma_f32 v[54:55], v[92:93], v[92:93], v[54:55]
	v_and_b32_e32 v87, 0xffff0000, v96
	v_lshlrev_b32_e32 v86, 16, v96
	v_pk_add_f32 v[54:55], v[8:9], v[54:55] op_sel_hi:[0,1]
	v_pk_fma_f32 v[54:55], v[86:87], v[86:87], v[54:55]
	v_mul_f32_e32 v8, v87, v87
	v_and_b32_e32 v85, 0xffff0000, v97
	v_lshlrev_b32_e32 v84, 16, v97
	v_pk_add_f32 v[54:55], v[8:9], v[54:55] op_sel_hi:[0,1]
	v_pk_fma_f32 v[54:55], v[84:85], v[84:85], v[54:55]
	v_mul_f32_e32 v8, v85, v85
	v_and_b32_e32 v81, 0xffff0000, v50
	v_lshlrev_b32_e32 v80, 16, v50
	v_pk_add_f32 v[54:55], v[8:9], v[54:55] op_sel_hi:[0,1]
	v_pk_fma_f32 v[54:55], v[80:81], v[80:81], v[54:55]
	v_mul_f32_e32 v8, v81, v81
	v_and_b32_e32 v33, 0xffff0000, v51
	v_lshlrev_b32_e32 v32, 16, v51
	v_pk_add_f32 v[54:55], v[8:9], v[54:55] op_sel_hi:[0,1]
	v_pk_fma_f32 v[54:55], v[32:33], v[32:33], v[54:55]
	v_mul_f32_e32 v8, v33, v33
	v_and_b32_e32 v31, 0xffff0000, v52
	v_lshlrev_b32_e32 v30, 16, v52
	v_pk_add_f32 v[54:55], v[8:9], v[54:55] op_sel_hi:[0,1]
	v_pk_fma_f32 v[54:55], v[30:31], v[30:31], v[54:55]
	v_mul_f32_e32 v8, v31, v31
	v_and_b32_e32 v27, 0xffff0000, v53
	v_lshlrev_b32_e32 v26, 16, v53
	v_pk_add_f32 v[54:55], v[8:9], v[54:55] op_sel_hi:[0,1]
	v_pk_fma_f32 v[54:55], v[26:27], v[26:27], v[54:55]
	v_mul_f32_e32 v8, v27, v27
	v_pk_add_f32 v[54:55], v[8:9], v[54:55] op_sel_hi:[0,1]
	v_mov_b32_e32 v8, v54
	v_and_b32_e32 v89, 0xffff0000, v6
	s_nop 0
	v_permlane16_swap_b32_e32 v54, v8
	v_lshlrev_b32_e32 v88, 16, v6
	v_mul_f32_e32 v6, v89, v89
	v_add_f32_e32 v113, v54, v8
	v_pk_fma_f32 v[54:55], v[88:89], v[88:89], v[6:7] op_sel_hi:[1,1,0]
	v_mul_f32_e32 v6, v79, v79
	v_pk_fma_f32 v[54:55], v[78:79], v[78:79], v[54:55]
	global_load_dwordx4 v[46:49], v82, s[26:27] offset:16
	global_load_dwordx4 v[50:53], v82, s[26:27]
	v_pk_add_f32 v[54:55], v[6:7], v[54:55] op_sel_hi:[0,1]
	v_pk_fma_f32 v[54:55], v[76:77], v[76:77], v[54:55]
	v_mul_f32_e32 v6, v77, v77
	v_pk_add_f32 v[54:55], v[6:7], v[54:55] op_sel_hi:[0,1]
	v_pk_fma_f32 v[54:55], v[74:75], v[74:75], v[54:55]
	v_mul_f32_e32 v6, v75, v75
	v_pk_add_f32 v[54:55], v[6:7], v[54:55] op_sel_hi:[0,1]
	v_pk_fma_f32 v[54:55], v[72:73], v[72:73], v[54:55]
	v_mul_f32_e32 v6, v73, v73
	v_pk_add_f32 v[54:55], v[6:7], v[54:55] op_sel_hi:[0,1]
	v_pk_fma_f32 v[54:55], v[70:71], v[70:71], v[54:55]
	v_mul_f32_e32 v6, v71, v71
	v_and_b32_e32 v69, 0xffff0000, v56
	v_lshlrev_b32_e32 v68, 16, v56
	v_pk_add_f32 v[54:55], v[6:7], v[54:55] op_sel_hi:[0,1]
	v_pk_fma_f32 v[54:55], v[68:69], v[68:69], v[54:55]
	v_mul_f32_e32 v6, v69, v69
	v_and_b32_e32 v67, 0xffff0000, v57
	v_lshlrev_b32_e32 v66, 16, v57
	v_pk_add_f32 v[54:55], v[6:7], v[54:55] op_sel_hi:[0,1]
	v_pk_fma_f32 v[54:55], v[66:67], v[66:67], v[54:55]
	v_mul_f32_e32 v6, v67, v67
	v_pk_add_f32 v[54:55], v[6:7], v[54:55] op_sel_hi:[0,1]
	v_mov_b32_e32 v6, v54
	s_nop 1
	v_permlane16_swap_b32_e32 v54, v6
	v_add_f32_e32 v95, v54, v6
	global_load_dwordx4 v[54:57], v82, s[26:27] offset:272
	global_load_dwordx4 v[58:61], v82, s[26:27] offset:256
	s_waitcnt vmcnt(8)
; __device__ __forceinline__ unsigned cvtpk(float lo, float hi) { f32x2 v = {lo, hi}; bf16x2_t b = __builtin_convertvector(v, bf16x2_t); return __builtin_bit_cast(unsigned, b); }
; template <int DQK, int DV, bool LEAD> ...
;     ...
;           const float rn = rsqrtf(sn * (1.f / 64.f) + EPS);
; #pragma unroll
;           for (int ds = 0; ds < 2; ++ds)
; #pragma unroll
;               for (int j = 0; j < 8; ++j) x[ds][j] *= rn * qgain[32 * ds + 8 * g4 + j];
;           if constexpr (DQK == 64) {
; #pragma unroll
;               for (int ds = 0; ds < 2; ++ds)
; #pragma unroll
;                   for (int j = 0; j < 8; ++j) {
;                       auto rr = __builtin_amdgcn_permlane32_swap(__float_as_uint(x[ds][j]), __float_as_uint(x[ds][j]), false, false);
;                       const float other = hi ? __uint_as_float(rr[0]) : __uint_as_float(rr[1]);
;                       float cc = 1.f, sg = 0.f;
;                       if (lat) { const f32x2 cs = rope[(ds ? pcol : prow) * 16 + 8 * (g4 & 1) + j]; cc = cs.x; sg = hi ? cs.y : -cs.y; }
;                       x[ds][j] = x[ds][j] * cc + other * sg; }
;           } else {
;               float sr = 0.f;
; #pragma unroll
;               for (int j = 0; j < 8; ++j) sr += x[2][j] * x[2][j];
;               sr = lanes4_sum(sr);
;               const float rq = rsqrtf(sr * (1.f / 32.f) + EPS);
; #pragma unroll
;               for (int j = 0; j < 8; ++j) { const float av = x[2][j] * rq * qgain[64 + 8 * g4 + j];
;                   auto rr = __builtin_amdgcn_permlane16_swap(__float_as_uint(av), __float_as_uint(av), false, false);
;                   const float other = (g4 & 1) ? __uint_as_float(rr[0]) : __uint_as_float(rr[1]);
;                   float cc = 1.f, sg = 0.f;
;                   if (lat) { const f32x2 cs = rope[((g4 & 2) ? pcol : prow) * 8 + j]; cc = cs.x; sg = (g4 & 1) ? cs.y : -cs.y; }
;                   x[2][j] = av * cc + other * sg; }
;           }
; #pragma unroll
;           for (int ds = 0; ds < NDS; ++ds) { u32x4 w;
; #pragma unroll
;               for (int i = 0; i < 4; ++i) w[i] = cvtpk(x[ds][2 * i] * c2, x[ds][2 * i + 1] * c2);
;               qf[qb * NDS + ds] = __builtin_bit_cast(bf16x8, w); }
	v_and_b32_e32 v155, 0xffff0000, v2
	v_lshlrev_b32_e32 v154, 16, v2
	v_mul_f32_e32 v2, v155, v155
	v_and_b32_e32 v139, 0xffff0000, v13
	v_lshlrev_b32_e32 v138, 16, v13
	v_and_b32_e32 v141, 0xffff0000, v12
	v_lshlrev_b32_e32 v140, 16, v12
	v_and_b32_e32 v13, 0xffff0000, v3
	v_lshlrev_b32_e32 v12, 16, v3
	v_pk_fma_f32 v[2:3], v[154:155], v[154:155], v[2:3] op_sel_hi:[1,1,0]
	v_and_b32_e32 v153, 0xffff0000, v4
	v_lshlrev_b32_e32 v152, 16, v4
	v_pk_fma_f32 v[2:3], v[12:13], v[12:13], v[2:3]
	v_mul_f32_e32 v4, v13, v13
	v_pk_add_f32 v[2:3], v[4:5], v[2:3] op_sel_hi:[0,1]
	v_pk_fma_f32 v[2:3], v[152:153], v[152:153], v[2:3]
	v_mul_f32_e32 v4, v153, v153
	v_and_b32_e32 v151, 0xffff0000, v5
	v_lshlrev_b32_e32 v150, 16, v5
	v_pk_add_f32 v[2:3], v[4:5], v[2:3] op_sel_hi:[0,1]
	v_pk_fma_f32 v[2:3], v[150:151], v[150:151], v[2:3]
	v_mul_f32_e32 v4, v151, v151
	v_pk_add_f32 v[2:3], v[4:5], v[2:3] op_sel_hi:[0,1]
	v_mov_b32_e32 v3, v2
	s_nop 1
	v_permlane16_swap_b32_e32 v2, v3
	v_add_f32_e32 v6, v2, v3
	v_mov_b32_e32 v8, v6
	s_nop 1
	v_permlane32_swap_b32_e32 v6, v8
	v_pk_add_f32 v[2:3], v[6:7], v[8:9]
	v_mov_b32_e32 v97, v95
	v_pk_fma_f32 v[6:7], v[2:3], s[6:7], v[106:107] op_sel_hi:[1,1,0]
	s_nop 0
	v_permlane32_swap_b32_e32 v95, v97
	v_mul_f32_e32 v2, 0x4b800000, v7
	v_cmp_gt_f32_e32 vcc, s95, v7
	s_waitcnt vmcnt(7)
	v_and_b32_e32 v111, 0xffff0000, v25
	v_lshlrev_b32_e32 v110, 16, v25
	v_cndmask_b32_e32 v2, v7, v2, vcc
	v_rsq_f32_e32 v2, v2
	v_and_b32_e32 v117, 0xffff0000, v24
	v_lshlrev_b32_e32 v116, 16, v24
	v_and_b32_e32 v25, 0xffff0000, v11
	v_mul_f32_e32 v3, 0x45800000, v2
	v_cndmask_b32_e32 v94, v2, v3, vcc
	s_waitcnt vmcnt(5)
	v_pk_mul_f32 v[2:3], v[94:95], v[40:41] op_sel_hi:[0,1]
	v_pk_mul_f32 v[2:3], v[2:3], v[16:17]
	s_waitcnt vmcnt(4)
	v_pk_mul_f32 v[8:9], v[42:43], v[94:95] op_sel_hi:[1,0]
	v_pk_mul_f32 v[2:3], v[2:3], s[82:83] op_sel_hi:[1,0]
	v_pk_mul_f32 v[8:9], v[8:9], v[124:125]
	v_cvt_pk_bf16_f32 v5, v2, v3
	v_pk_mul_f32 v[2:3], v[94:95], v[38:39] op_sel_hi:[0,1]
	v_pk_mul_f32 v[2:3], v[2:3], v[120:121]
	v_pk_mul_f32 v[8:9], v[8:9], s[82:83] op_sel_hi:[1,0]
	v_pk_mul_f32 v[2:3], v[2:3], s[82:83] op_sel_hi:[1,0]
	s_waitcnt vmcnt(3)
	v_pk_mul_f32 v[16:17], v[46:47], v[94:95] op_sel_hi:[1,0]
	v_cvt_pk_bf16_f32 v4, v2, v3
	v_pk_mul_f32 v[2:3], v[94:95], v[44:45] op_sel_hi:[0,1]
	v_pk_mul_f32 v[2:3], v[2:3], v[122:123]
	v_pk_mul_f32 v[16:17], v[16:17], v[132:133]
	v_pk_mul_f32 v[2:3], v[2:3], s[82:83] op_sel_hi:[1,0]
	v_pk_mul_f32 v[16:17], v[16:17], s[82:83] op_sel_hi:[1,0]
	v_cvt_pk_bf16_f32 v3, v2, v3
	v_cvt_pk_bf16_f32 v2, v8, v9
	v_pk_mul_f32 v[8:9], v[48:49], v[94:95] op_sel_hi:[1,0]
	v_lshlrev_b32_e32 v24, 16, v11
	v_pk_mul_f32 v[8:9], v[8:9], v[126:127]
	v_mul_f32_e32 v11, 0x4b800000, v6
	v_pk_mul_f32 v[8:9], v[8:9], s[82:83] op_sel_hi:[1,0]
	v_cmp_gt_f32_e32 vcc, s95, v6
	v_cvt_pk_bf16_f32 v9, v8, v9
	v_cvt_pk_bf16_f32 v8, v16, v17
	s_waitcnt vmcnt(2)
	v_pk_mul_f32 v[16:17], v[52:53], v[94:95] op_sel_hi:[1,0]
	v_cndmask_b32_e32 v6, v6, v11, vcc
	v_pk_mul_f32 v[16:17], v[16:17], v[134:135]
	v_rsq_f32_e32 v11, v6
	v_pk_mul_f32 v[16:17], v[16:17], s[82:83] op_sel_hi:[1,0]
	v_and_b32_e32 v83, 0xffff0000, v37
	v_cvt_pk_bf16_f32 v7, v16, v17
	v_pk_mul_f32 v[16:17], v[50:51], v[94:95] op_sel_hi:[1,0]
	v_lshlrev_b32_e32 v82, 16, v37
	v_pk_mul_f32 v[16:17], v[16:17], v[136:137]
	v_and_b32_e32 v91, 0xffff0000, v36
	v_pk_mul_f32 v[16:17], v[16:17], s[82:83] op_sel_hi:[1,0]
	v_lshlrev_b32_e32 v90, 16, v36
	v_cvt_pk_bf16_f32 v6, v16, v17
	v_mul_f32_e32 v16, 0x45800000, v11
	v_cndmask_b32_e32 v16, v11, v16, vcc
	v_pk_mul_f32 v[122:123], v[16:17], v[12:13] op_sel_hi:[0,1]
	v_pk_mul_f32 v[12:13], v[16:17], v[150:151] op_sel_hi:[0,1]
	s_waitcnt vmcnt(1)
	v_pk_mul_f32 v[12:13], v[12:13], v[56:57]
	v_and_b32_e32 v37, 0xffff0000, v23
	v_lshlrev_b32_e32 v36, 16, v23
	v_pk_mul_f32 v[120:121], v[16:17], v[154:155] op_sel_hi:[0,1]
	v_pk_mul_f32 v[124:125], v[16:17], v[152:153] op_sel_hi:[0,1]
	v_mov_b32_e32 v11, v12
	v_mov_b32_e32 v16, v12
	v_mov_b32_e32 v17, v13
	v_mov_b32_e32 v23, v13
	v_permlane16_swap_b32_e32 v11, v16
	s_nop 0
	v_permlane16_swap_b32_e32 v17, v23
	v_cmp_eq_u32_e32 vcc, 0, v112
	v_and_b32_e32 v99, 0xffff0000, v35
	v_lshlrev_b32_e32 v98, 16, v35
	v_cndmask_b32_e32 v17, v17, v23, vcc
	v_cndmask_b32_e32 v16, v11, v16, vcc
	v_pk_fma_f32 v[12:13], v[16:17], 0, v[12:13] op_sel_hi:[1,0,1]
	v_pk_mul_f32 v[16:17], v[54:55], v[124:125]
	v_pk_mul_f32 v[12:13], v[12:13], s[82:83] op_sel_hi:[1,0]
	v_mov_b32_e32 v11, v16
	v_cvt_pk_bf16_f32 v13, v12, v13
	v_mov_b32_e32 v12, v16
	v_mov_b32_e32 v23, v17
	v_mov_b32_e32 v35, v17
	v_permlane16_swap_b32_e32 v11, v12
	s_nop 0
	v_permlane16_swap_b32_e32 v23, v35
	v_cndmask_b32_e32 v125, v23, v35, vcc
	v_cndmask_b32_e32 v124, v11, v12, vcc
	v_pk_fma_f32 v[16:17], v[124:125], 0, v[16:17] op_sel_hi:[1,0,1]
	v_mov_b32_e32 v131, v129
	v_pk_mul_f32 v[16:17], v[16:17], s[82:83] op_sel_hi:[1,0]
	s_nop 0
	v_permlane32_swap_b32_e32 v129, v131
	v_cvt_pk_bf16_f32 v12, v16, v17
	s_waitcnt vmcnt(0)
; __device__ __forceinline__ unsigned cvtpk(float lo, float hi) { f32x2 v = {lo, hi}; bf16x2_t b = __builtin_convertvector(v, bf16x2_t); return __builtin_bit_cast(unsigned, b); }
; template <int DQK, int DV, bool LEAD> ...
;     ...
;           const float rn = rsqrtf(sn * (1.f / 64.f) + EPS);
; #pragma unroll
;           for (int ds = 0; ds < 2; ++ds)
; #pragma unroll
;               for (int j = 0; j < 8; ++j) x[ds][j] *= rn * qgain[32 * ds + 8 * g4 + j];
;           if constexpr (DQK == 64) {
; #pragma unroll
;               for (int ds = 0; ds < 2; ++ds)
; #pragma unroll
;                   for (int j = 0; j < 8; ++j) {
;                       auto rr = __builtin_amdgcn_permlane32_swap(__float_as_uint(x[ds][j]), __float_as_uint(x[ds][j]), false, false);
;                       const float other = hi ? __uint_as_float(rr[0]) : __uint_as_float(rr[1]);
;                       float cc = 1.f, sg = 0.f;
;                       if (lat) { const f32x2 cs = rope[(ds ? pcol : prow) * 16 + 8 * (g4 & 1) + j]; cc = cs.x; sg = hi ? cs.y : -cs.y; }
;                       x[ds][j] = x[ds][j] * cc + other * sg; }
;           } else {
;               float sr = 0.f;
; #pragma unroll
;               for (int j = 0; j < 8; ++j) sr += x[2][j] * x[2][j];
;               sr = lanes4_sum(sr);
;               const float rq = rsqrtf(sr * (1.f / 32.f) + EPS);
; #pragma unroll
;               for (int j = 0; j < 8; ++j) { const float av = x[2][j] * rq * qgain[64 + 8 * g4 + j];
;                   auto rr = __builtin_amdgcn_permlane16_swap(__float_as_uint(av), __float_as_uint(av), false, false);
;                   const float other = (g4 & 1) ? __uint_as_float(rr[0]) : __uint_as_float(rr[1]);
;                   float cc = 1.f, sg = 0.f;
;                   if (lat) { const f32x2 cs = rope[((g4 & 2) ? pcol : prow) * 8 + j]; cc = cs.x; sg = (g4 & 1) ? cs.y : -cs.y; }
;                   x[2][j] = av * cc + other * sg; }
;           }
; #pragma unroll
;           for (int ds = 0; ds < NDS; ++ds) { u32x4 w;
; #pragma unroll
;               for (int i = 0; i < 4; ++i) w[i] = cvtpk(x[ds][2 * i] * c2, x[ds][2 * i + 1] * c2);
;               qf[qb * NDS + ds] = __builtin_bit_cast(bf16x8, w); }
	v_pk_mul_f32 v[16:17], v[60:61], v[122:123]
	v_mov_b32_e32 v115, v113
	v_mov_b32_e32 v11, v16
	v_mov_b32_e32 v23, v16
	v_mov_b32_e32 v35, v17
	v_mov_b32_e32 v94, v17
	v_permlane16_swap_b32_e32 v11, v23
	s_nop 0
	v_permlane16_swap_b32_e32 v35, v94
	v_cndmask_b32_e32 v123, v35, v94, vcc
	v_cndmask_b32_e32 v122, v11, v23, vcc
	v_pk_fma_f32 v[16:17], v[122:123], 0, v[16:17] op_sel_hi:[1,0,1]
	v_and_b32_e32 v123, 0xffff0000, v10
	v_pk_mul_f32 v[16:17], v[16:17], s[82:83] op_sel_hi:[1,0]
	v_lshlrev_b32_e32 v122, 16, v10
	v_cvt_pk_bf16_f32 v11, v16, v17
	v_mul_f32_e32 v10, v123, v123
	v_pk_fma_f32 v[124:125], v[122:123], v[122:123], v[10:11] op_sel_hi:[1,1,0]
	v_mul_f32_e32 v10, v25, v25
	v_pk_fma_f32 v[124:125], v[24:25], v[24:25], v[124:125]
	v_pk_mul_f32 v[16:17], v[58:59], v[120:121]
	v_pk_add_f32 v[124:125], v[10:11], v[124:125] op_sel_hi:[0,1]
	v_pk_fma_f32 v[124:125], v[140:141], v[140:141], v[124:125]
	v_mul_f32_e32 v10, v141, v141
	v_pk_add_f32 v[124:125], v[10:11], v[124:125] op_sel_hi:[0,1]
	v_pk_fma_f32 v[124:125], v[138:139], v[138:139], v[124:125]
	v_mul_f32_e32 v10, v139, v139
	v_pk_add_f32 v[124:125], v[10:11], v[124:125] op_sel_hi:[0,1]
	v_mov_b32_e32 v10, v124
	s_nop 1
	v_permlane16_swap_b32_e32 v124, v10
	v_add_f32_e32 v128, v124, v10
	v_mov_b32_e32 v130, v128
	s_nop 1
	v_permlane32_swap_b32_e32 v128, v130
	v_pk_add_f32 v[124:125], v[128:129], v[130:131]
	v_mov_b32_e32 v23, v16
	v_pk_fma_f32 v[124:125], v[124:125], s[6:7], v[106:107] op_sel_hi:[1,1,0]
	v_mov_b32_e32 v35, v16
	v_mul_f32_e32 v10, 0x4b800000, v125
	v_cmp_gt_f32_e64 s[4:5], s95, v125
	v_permlane16_swap_b32_e32 v23, v35
	v_mov_b32_e32 v94, v17
	v_mov_b32_e32 v96, v17
	v_cndmask_b32_e64 v10, v125, v10, s[4:5]
	s_nop 0
	v_permlane16_swap_b32_e32 v94, v96
	v_cndmask_b32_e32 v120, v23, v35, vcc
	v_rsq_f32_e32 v23, v10
	v_cndmask_b32_e32 v121, v94, v96, vcc
	v_pk_fma_f32 v[16:17], v[120:121], 0, v[16:17] op_sel_hi:[1,0,1]
	v_permlane32_swap_b32_e32 v113, v115
	v_pk_mul_f32 v[16:17], v[16:17], s[82:83] op_sel_hi:[1,0]
	s_mov_b32 s26, 0
	v_cvt_pk_bf16_f32 v10, v16, v17
	v_mul_f32_e32 v16, 0x45800000, v23
	v_cndmask_b32_e64 v94, v23, v16, s[4:5]
	v_pk_mul_f32 v[16:17], v[40:41], v[94:95] op_sel_hi:[1,0]
	v_cmp_gt_f32_e64 s[4:5], s95, v124
	v_pk_mul_f32 v[14:15], v[16:17], v[14:15]
	s_nop 0
	v_pk_mul_f32 v[14:15], v[14:15], s[82:83] op_sel_hi:[1,0]
	s_nop 0
	v_cvt_pk_bf16_f32 v17, v14, v15
	v_pk_mul_f32 v[14:15], v[38:39], v[94:95] op_sel_hi:[1,0]
	s_nop 0
	v_pk_mul_f32 v[14:15], v[14:15], v[18:19]
	v_pk_mul_f32 v[18:19], v[42:43], v[94:95] op_sel_hi:[1,0]
	v_pk_mul_f32 v[14:15], v[14:15], s[82:83] op_sel_hi:[1,0]
	v_pk_mul_f32 v[18:19], v[18:19], v[28:29]
	v_cvt_pk_bf16_f32 v16, v14, v15
	v_pk_mul_f32 v[14:15], v[44:45], v[94:95] op_sel_hi:[1,0]
	v_pk_mul_f32 v[18:19], v[18:19], s[82:83] op_sel_hi:[1,0]
	v_pk_mul_f32 v[14:15], v[14:15], v[20:21]
	v_pk_mul_f32 v[28:29], v[50:51], v[94:95] op_sel_hi:[1,0]
	v_pk_mul_f32 v[14:15], v[14:15], s[82:83] op_sel_hi:[1,0]
	v_pk_mul_f32 v[28:29], v[28:29], v[118:119]
	v_cvt_pk_bf16_f32 v15, v14, v15
	v_cvt_pk_bf16_f32 v14, v18, v19
	v_pk_mul_f32 v[18:19], v[48:49], v[94:95] op_sel_hi:[1,0]
	v_pk_mul_f32 v[28:29], v[28:29], s[82:83] op_sel_hi:[1,0]
	v_pk_mul_f32 v[18:19], v[18:19], v[102:103]
	s_nop 0
	v_pk_mul_f32 v[18:19], v[18:19], s[82:83] op_sel_hi:[1,0]
	s_nop 0
	v_cvt_pk_bf16_f32 v21, v18, v19
	v_pk_mul_f32 v[18:19], v[46:47], v[94:95] op_sel_hi:[1,0]
	s_nop 0
	v_pk_mul_f32 v[18:19], v[18:19], v[104:105]
	s_nop 0
	v_pk_mul_f32 v[18:19], v[18:19], s[82:83] op_sel_hi:[1,0]
	s_nop 0
	v_cvt_pk_bf16_f32 v20, v18, v19
	v_pk_mul_f32 v[18:19], v[52:53], v[94:95] op_sel_hi:[1,0]
	s_nop 0
	v_pk_mul_f32 v[18:19], v[18:19], v[108:109]
	s_nop 0
	v_pk_mul_f32 v[18:19], v[18:19], s[82:83] op_sel_hi:[1,0]
	s_nop 0
	v_cvt_pk_bf16_f32 v19, v18, v19
	v_mul_f32_e32 v18, 0x4b800000, v124
	v_cndmask_b32_e64 v18, v124, v18, s[4:5]
	v_rsq_f32_e32 v23, v18
	v_cvt_pk_bf16_f32 v18, v28, v29
	v_mul_f32_e32 v28, 0x45800000, v23
	v_cndmask_b32_e64 v28, v23, v28, s[4:5]
	v_pk_mul_f32 v[104:105], v[28:29], v[24:25] op_sel_hi:[0,1]
	v_pk_mul_f32 v[24:25], v[28:29], v[138:139] op_sel_hi:[0,1]
	v_pk_mul_f32 v[24:25], v[56:57], v[24:25]
	v_pk_mul_f32 v[102:103], v[28:29], v[122:123] op_sel_hi:[0,1]
	v_pk_mul_f32 v[108:109], v[28:29], v[140:141] op_sel_hi:[0,1]
	v_mov_b32_e32 v23, v24
	v_mov_b32_e32 v28, v24
	v_mov_b32_e32 v29, v25
	v_mov_b32_e32 v35, v25
	v_permlane16_swap_b32_e32 v23, v28
	s_nop 0
	v_permlane16_swap_b32_e32 v29, v35
	v_cndmask_b32_e32 v29, v29, v35, vcc
	v_cndmask_b32_e32 v28, v23, v28, vcc
	v_pk_fma_f32 v[24:25], v[28:29], 0, v[24:25] op_sel_hi:[1,0,1]
	v_pk_mul_f32 v[28:29], v[54:55], v[108:109]
	v_pk_mul_f32 v[24:25], v[24:25], s[82:83] op_sel_hi:[1,0]
	v_mov_b32_e32 v23, v28
	v_cvt_pk_bf16_f32 v25, v24, v25
	v_mov_b32_e32 v24, v28
	v_mov_b32_e32 v35, v29
	v_mov_b32_e32 v94, v29
	v_permlane16_swap_b32_e32 v23, v24
	s_nop 0
	v_permlane16_swap_b32_e32 v35, v94
	v_cndmask_b32_e32 v109, v35, v94, vcc
	v_cndmask_b32_e32 v108, v23, v24, vcc
	v_pk_fma_f32 v[28:29], v[108:109], 0, v[28:29] op_sel_hi:[1,0,1]
	s_nop 0
	v_pk_mul_f32 v[28:29], v[28:29], s[82:83] op_sel_hi:[1,0]
	s_nop 0
	v_cvt_pk_bf16_f32 v24, v28, v29
	v_pk_mul_f32 v[28:29], v[60:61], v[104:105]
	s_nop 0
	v_mov_b32_e32 v23, v28
	v_mov_b32_e32 v35, v28
	v_mov_b32_e32 v94, v29
	v_mov_b32_e32 v96, v29
	v_permlane16_swap_b32_e32 v23, v35
	s_nop 0
	v_permlane16_swap_b32_e32 v94, v96
	v_cndmask_b32_e32 v105, v94, v96, vcc
	v_cndmask_b32_e32 v104, v23, v35, vcc
	v_pk_fma_f32 v[28:29], v[104:105], 0, v[28:29] op_sel_hi:[1,0,1]
	v_and_b32_e32 v105, 0xffff0000, v22
; __device__ __forceinline__ unsigned cvtpk(float lo, float hi) { f32x2 v = {lo, hi}; bf16x2_t b = __builtin_convertvector(v, bf16x2_t); return __builtin_bit_cast(unsigned, b); }
; template <int DQK, int DV, bool LEAD> ...
;     ...
;           const float rn = rsqrtf(sn * (1.f / 64.f) + EPS);
; #pragma unroll
;           for (int ds = 0; ds < 2; ++ds)
; #pragma unroll
;               for (int j = 0; j < 8; ++j) x[ds][j] *= rn * qgain[32 * ds + 8 * g4 + j];
;           if constexpr (DQK == 64) {
; #pragma unroll
;               for (int ds = 0; ds < 2; ++ds)
; #pragma unroll
;                   for (int j = 0; j < 8; ++j) {
;                       auto rr = __builtin_amdgcn_permlane32_swap(__float_as_uint(x[ds][j]), __float_as_uint(x[ds][j]), false, false);
;                       const float other = hi ? __uint_as_float(rr[0]) : __uint_as_float(rr[1]);
;                       float cc = 1.f, sg = 0.f;
;                       if (lat) { const f32x2 cs = rope[(ds ? pcol : prow) * 16 + 8 * (g4 & 1) + j]; cc = cs.x; sg = hi ? cs.y : -cs.y; }
;                       x[ds][j] = x[ds][j] * cc + other * sg; }
;           } else {
;               float sr = 0.f;
; #pragma unroll
;               for (int j = 0; j < 8; ++j) sr += x[2][j] * x[2][j];
;               sr = lanes4_sum(sr);
;               const float rq = rsqrtf(sr * (1.f / 32.f) + EPS);
; #pragma unroll
;               for (int j = 0; j < 8; ++j) { const float av = x[2][j] * rq * qgain[64 + 8 * g4 + j];
;                   auto rr = __builtin_amdgcn_permlane16_swap(__float_as_uint(av), __float_as_uint(av), false, false);
;                   const float other = (g4 & 1) ? __uint_as_float(rr[0]) : __uint_as_float(rr[1]);
;                   float cc = 1.f, sg = 0.f;
;                   if (lat) { const f32x2 cs = rope[((g4 & 2) ? pcol : prow) * 8 + j]; cc = cs.x; sg = (g4 & 1) ? cs.y : -cs.y; }
;                   x[2][j] = av * cc + other * sg; }
;           }
; #pragma unroll
;           for (int ds = 0; ds < NDS; ++ds) { u32x4 w;
; #pragma unroll
;               for (int i = 0; i < 4; ++i) w[i] = cvtpk(x[ds][2 * i] * c2, x[ds][2 * i + 1] * c2);
;               qf[qb * NDS + ds] = __builtin_bit_cast(bf16x8, w); }
	v_pk_mul_f32 v[28:29], v[28:29], s[82:83] op_sel_hi:[1,0]
	v_lshlrev_b32_e32 v104, 16, v22
	v_cvt_pk_bf16_f32 v23, v28, v29
	v_mul_f32_e32 v22, v105, v105
	v_pk_fma_f32 v[108:109], v[104:105], v[104:105], v[22:23] op_sel_hi:[1,1,0]
	v_mul_f32_e32 v22, v37, v37
	v_pk_fma_f32 v[108:109], v[36:37], v[36:37], v[108:109]
	v_pk_mul_f32 v[28:29], v[58:59], v[102:103]
	v_pk_add_f32 v[108:109], v[22:23], v[108:109] op_sel_hi:[0,1]
	v_pk_fma_f32 v[108:109], v[116:117], v[116:117], v[108:109]
	v_mul_f32_e32 v22, v117, v117
	v_pk_add_f32 v[108:109], v[22:23], v[108:109] op_sel_hi:[0,1]
	v_pk_fma_f32 v[108:109], v[110:111], v[110:111], v[108:109]
	v_mul_f32_e32 v22, v111, v111
	v_pk_add_f32 v[108:109], v[22:23], v[108:109] op_sel_hi:[0,1]
	v_mov_b32_e32 v22, v108
	s_nop 1
	v_permlane16_swap_b32_e32 v108, v22
	v_add_f32_e32 v112, v108, v22
	v_mov_b32_e32 v114, v112
	s_nop 1
	v_permlane32_swap_b32_e32 v112, v114
	v_pk_add_f32 v[108:109], v[112:113], v[114:115]
	v_mov_b32_e32 v35, v28
	v_pk_fma_f32 v[108:109], v[108:109], s[6:7], v[106:107] op_sel_hi:[1,1,0]
	v_mov_b32_e32 v94, v28
	v_mov_b32_e32 v96, v29
	v_mov_b32_e32 v102, v29
	v_mul_f32_e32 v22, 0x4b800000, v109
	v_cmp_gt_f32_e64 s[4:5], s95, v109
	v_permlane16_swap_b32_e32 v35, v94
	v_permlane16_swap_b32_e32 v96, v102
	v_cndmask_b32_e64 v22, v109, v22, s[4:5]
	v_cndmask_b32_e32 v103, v96, v102, vcc
	v_cndmask_b32_e32 v102, v35, v94, vcc
	v_rsq_f32_e32 v35, v22
	v_pk_fma_f32 v[28:29], v[102:103], 0, v[28:29] op_sel_hi:[1,0,1]
	s_nop 0
	v_pk_mul_f32 v[28:29], v[28:29], s[82:83] op_sel_hi:[1,0]
	s_nop 0
	v_cvt_pk_bf16_f32 v22, v28, v29
	v_mul_f32_e32 v28, 0x45800000, v35
	v_cndmask_b32_e64 v94, v35, v28, s[4:5]
	v_pk_mul_f32 v[28:29], v[40:41], v[94:95] op_sel_hi:[1,0]
	v_cmp_gt_f32_e64 s[4:5], s95, v108
	v_pk_mul_f32 v[26:27], v[28:29], v[26:27]
	s_nop 0
	v_pk_mul_f32 v[26:27], v[26:27], s[82:83] op_sel_hi:[1,0]
	s_nop 0
	v_cvt_pk_bf16_f32 v29, v26, v27
	v_pk_mul_f32 v[26:27], v[38:39], v[94:95] op_sel_hi:[1,0]
	s_nop 0
	v_pk_mul_f32 v[26:27], v[26:27], v[30:31]
	v_pk_mul_f32 v[30:31], v[42:43], v[94:95] op_sel_hi:[1,0]
	v_pk_mul_f32 v[26:27], v[26:27], s[82:83] op_sel_hi:[1,0]
	v_pk_mul_f32 v[30:31], v[30:31], v[80:81]
	v_cvt_pk_bf16_f32 v28, v26, v27
	v_pk_mul_f32 v[26:27], v[44:45], v[94:95] op_sel_hi:[1,0]
	v_pk_mul_f32 v[30:31], v[30:31], s[82:83] op_sel_hi:[1,0]
	v_pk_mul_f32 v[26:27], v[26:27], v[32:33]
	v_pk_mul_f32 v[80:81], v[50:51], v[94:95] op_sel_hi:[1,0]
	v_pk_mul_f32 v[26:27], v[26:27], s[82:83] op_sel_hi:[1,0]
	v_pk_mul_f32 v[80:81], v[80:81], v[100:101]
	v_cvt_pk_bf16_f32 v27, v26, v27
	v_cvt_pk_bf16_f32 v26, v30, v31
	v_pk_mul_f32 v[30:31], v[48:49], v[94:95] op_sel_hi:[1,0]
	v_pk_mul_f32 v[80:81], v[80:81], s[82:83] op_sel_hi:[1,0]
	v_pk_mul_f32 v[30:31], v[30:31], v[84:85]
	s_nop 0
	v_pk_mul_f32 v[30:31], v[30:31], s[82:83] op_sel_hi:[1,0]
	s_nop 0
	v_cvt_pk_bf16_f32 v33, v30, v31
	v_pk_mul_f32 v[30:31], v[46:47], v[94:95] op_sel_hi:[1,0]
	s_nop 0
	v_pk_mul_f32 v[30:31], v[30:31], v[86:87]
	s_nop 0
	v_pk_mul_f32 v[30:31], v[30:31], s[82:83] op_sel_hi:[1,0]
	s_nop 0
	v_cvt_pk_bf16_f32 v32, v30, v31
	v_pk_mul_f32 v[30:31], v[52:53], v[94:95] op_sel_hi:[1,0]
	s_nop 0
	v_pk_mul_f32 v[30:31], v[30:31], v[92:93]
	s_nop 0
	v_pk_mul_f32 v[30:31], v[30:31], s[82:83] op_sel_hi:[1,0]
	s_nop 0
	v_cvt_pk_bf16_f32 v31, v30, v31
	v_mul_f32_e32 v30, 0x4b800000, v108
	v_cndmask_b32_e64 v30, v108, v30, s[4:5]
	v_rsq_f32_e32 v35, v30
	v_cvt_pk_bf16_f32 v30, v80, v81
	v_mul_f32_e32 v80, 0x45800000, v35
	v_cndmask_b32_e64 v80, v35, v80, s[4:5]
	v_pk_mul_f32 v[86:87], v[80:81], v[36:37] op_sel_hi:[0,1]
	v_pk_mul_f32 v[36:37], v[80:81], v[110:111] op_sel_hi:[0,1]
	v_pk_mul_f32 v[36:37], v[56:57], v[36:37]
	v_pk_mul_f32 v[84:85], v[80:81], v[104:105] op_sel_hi:[0,1]
	v_pk_mul_f32 v[92:93], v[80:81], v[116:117] op_sel_hi:[0,1]
	v_mov_b32_e32 v35, v36
	v_mov_b32_e32 v80, v36
	v_mov_b32_e32 v81, v37
	v_mov_b32_e32 v94, v37
	v_permlane16_swap_b32_e32 v35, v80
	s_nop 0
	v_permlane16_swap_b32_e32 v81, v94
	v_cndmask_b32_e32 v81, v81, v94, vcc
	v_cndmask_b32_e32 v80, v35, v80, vcc
	v_pk_fma_f32 v[36:37], v[80:81], 0, v[36:37] op_sel_hi:[1,0,1]
	v_pk_mul_f32 v[80:81], v[54:55], v[92:93]
	v_pk_mul_f32 v[36:37], v[36:37], s[82:83] op_sel_hi:[1,0]
	v_mov_b32_e32 v35, v80
	v_cvt_pk_bf16_f32 v37, v36, v37
	v_mov_b32_e32 v36, v80
	v_mov_b32_e32 v92, v81
	v_mov_b32_e32 v93, v81
	v_permlane16_swap_b32_e32 v35, v36
	s_nop 0
	v_permlane16_swap_b32_e32 v92, v93
	v_cndmask_b32_e32 v93, v92, v93, vcc
	v_cndmask_b32_e32 v92, v35, v36, vcc
	v_pk_fma_f32 v[80:81], v[92:93], 0, v[80:81] op_sel_hi:[1,0,1]
	s_nop 0
	v_pk_mul_f32 v[80:81], v[80:81], s[82:83] op_sel_hi:[1,0]
	s_nop 0
	v_cvt_pk_bf16_f32 v36, v80, v81
	v_pk_mul_f32 v[80:81], v[60:61], v[86:87]
	s_nop 0
	v_mov_b32_e32 v35, v80
	v_mov_b32_e32 v86, v80
	v_mov_b32_e32 v87, v81
	v_mov_b32_e32 v92, v81
	v_permlane16_swap_b32_e32 v35, v86
	s_nop 0
	v_permlane16_swap_b32_e32 v87, v92
	v_cndmask_b32_e32 v87, v87, v92, vcc
	v_cndmask_b32_e32 v86, v35, v86, vcc
	v_pk_fma_f32 v[80:81], v[86:87], 0, v[80:81] op_sel_hi:[1,0,1]
	s_nop 0
	v_pk_mul_f32 v[80:81], v[80:81], s[82:83] op_sel_hi:[1,0]
	s_nop 0
	v_cvt_pk_bf16_f32 v35, v80, v81
	v_pk_mul_f32 v[80:81], v[58:59], v[84:85]
	s_nop 0
	v_mov_b32_e32 v85, v81
	v_mov_b32_e32 v87, v81
	v_mov_b32_e32 v84, v80
	v_mov_b32_e32 v86, v80
	v_permlane16_swap_b32_e32 v85, v87
	s_nop 0
	v_permlane16_swap_b32_e32 v84, v86
	v_cndmask_b32_e32 v85, v85, v87, vcc
	v_and_b32_e32 v87, 0xffff0000, v34
	v_cndmask_b32_e32 v84, v84, v86, vcc
	v_lshlrev_b32_e32 v86, 16, v34
	v_mul_f32_e32 v34, v87, v87
	v_pk_fma_f32 v[92:93], v[86:87], v[86:87], v[34:35] op_sel_hi:[1,1,0]
; __device__ __forceinline__ unsigned cvtpk(float lo, float hi) { f32x2 v = {lo, hi}; bf16x2_t b = __builtin_convertvector(v, bf16x2_t); return __builtin_bit_cast(unsigned, b); }
; template <int DQK, int DV, bool LEAD> ...
;     ...
;           } else {
;               float sr = 0.f;
; #pragma unroll
;               for (int j = 0; j < 8; ++j) sr += x[2][j] * x[2][j];
;               sr = lanes4_sum(sr);
;               const float rq = rsqrtf(sr * (1.f / 32.f) + EPS);
; #pragma unroll
;               for (int j = 0; j < 8; ++j) { const float av = x[2][j] * rq * qgain[64 + 8 * g4 + j];
;                   auto rr = __builtin_amdgcn_permlane16_swap(__float_as_uint(av), __float_as_uint(av), false, false);
;                   const float other = (g4 & 1) ? __uint_as_float(rr[0]) : __uint_as_float(rr[1]);
;                   float cc = 1.f, sg = 0.f;
;                   if (lat) { const f32x2 cs = rope[((g4 & 2) ? pcol : prow) * 8 + j]; cc = cs.x; sg = (g4 & 1) ? cs.y : -cs.y; }
;                   x[2][j] = av * cc + other * sg; }
;           }
; #pragma unroll
;           for (int ds = 0; ds < NDS; ++ds) { u32x4 w;
; #pragma unroll
;               for (int i = 0; i < 4; ++i) w[i] = cvtpk(x[ds][2 * i] * c2, x[ds][2 * i + 1] * c2);
;               qf[qb * NDS + ds] = __builtin_bit_cast(bf16x8, w); }
;       }
; #pragma unroll
;       for (int d0 = 0; d0 < NQB * NDS; ++d0) asm volatile("" : "+v"(qf[d0])); }
;     wait_bar<0>();
	v_mul_f32_e32 v34, v99, v99
	v_pk_fma_f32 v[92:93], v[98:99], v[98:99], v[92:93]
	v_pk_fma_f32 v[80:81], v[84:85], 0, v[80:81] op_sel_hi:[1,0,1]
	v_pk_add_f32 v[92:93], v[34:35], v[92:93] op_sel_hi:[0,1]
	v_pk_fma_f32 v[92:93], v[90:91], v[90:91], v[92:93]
	v_mul_f32_e32 v34, v91, v91
	v_pk_add_f32 v[92:93], v[34:35], v[92:93] op_sel_hi:[0,1]
	v_pk_fma_f32 v[92:93], v[82:83], v[82:83], v[92:93]
	v_mul_f32_e32 v34, v83, v83
	v_pk_add_f32 v[92:93], v[34:35], v[92:93] op_sel_hi:[0,1]
	v_mov_b32_e32 v34, v92
	s_nop 1
	v_permlane16_swap_b32_e32 v92, v34
	v_add_f32_e32 v94, v92, v34
	v_mov_b32_e32 v96, v94
	s_nop 1
	v_permlane32_swap_b32_e32 v94, v96
	v_pk_add_f32 v[92:93], v[94:95], v[96:97]
	v_pk_mul_f32 v[80:81], v[80:81], s[82:83] op_sel_hi:[1,0]
	v_pk_fma_f32 v[92:93], v[92:93], s[6:7], v[106:107] op_sel_hi:[1,1,0]
	s_lshl_b32 s6, s25, 6
	v_mul_f32_e32 v34, 0x4b800000, v93
	v_cmp_gt_f32_e64 s[4:5], s95, v93
	s_mov_b32 s25, 1
	s_mov_b32 s7, 2
	v_cndmask_b32_e64 v34, v93, v34, s[4:5]
	v_rsq_f32_e32 v93, v34
	v_cvt_pk_bf16_f32 v34, v80, v81
	v_lshrrev_b32_e32 v106, 1, v142
	v_mul_f32_e32 v80, 0x45800000, v93
	v_cndmask_b32_e64 v80, v93, v80, s[4:5]
	v_pk_mul_f32 v[50:51], v[50:51], v[80:81] op_sel_hi:[1,0]
	v_pk_mul_f32 v[52:53], v[52:53], v[80:81] op_sel_hi:[1,0]
	v_pk_mul_f32 v[38:39], v[38:39], v[80:81] op_sel_hi:[1,0]
	v_pk_mul_f32 v[50:51], v[50:51], v[88:89]
	v_pk_mul_f32 v[52:53], v[52:53], v[78:79]
	v_pk_mul_f32 v[46:47], v[46:47], v[80:81] op_sel_hi:[1,0]
	v_pk_mul_f32 v[48:49], v[48:49], v[80:81] op_sel_hi:[1,0]
	v_pk_mul_f32 v[68:69], v[38:39], v[68:69]
	v_pk_mul_f32 v[38:39], v[40:41], v[80:81] op_sel_hi:[1,0]
	v_pk_mul_f32 v[46:47], v[46:47], v[76:77]
	v_pk_mul_f32 v[48:49], v[48:49], v[74:75]
	v_pk_mul_f32 v[66:67], v[38:39], v[66:67]
	v_pk_mul_f32 v[38:39], v[50:51], s[82:83] op_sel_hi:[1,0]
	v_pk_mul_f32 v[40:41], v[52:53], s[82:83] op_sel_hi:[1,0]
	v_cvt_pk_bf16_f32 v38, v38, v39
	v_cvt_pk_bf16_f32 v39, v40, v41
	v_pk_mul_f32 v[40:41], v[46:47], s[82:83] op_sel_hi:[1,0]
	v_pk_mul_f32 v[46:47], v[48:49], s[82:83] op_sel_hi:[1,0]
	v_cvt_pk_bf16_f32 v40, v40, v41
	v_cvt_pk_bf16_f32 v41, v46, v47
	v_mul_f32_e32 v46, 0x4b800000, v92
	v_cmp_gt_f32_e64 s[4:5], s95, v92
	v_pk_mul_f32 v[42:43], v[42:43], v[80:81] op_sel_hi:[1,0]
	v_pk_mul_f32 v[44:45], v[44:45], v[80:81] op_sel_hi:[1,0]
	v_cndmask_b32_e64 v46, v92, v46, s[4:5]
	v_rsq_f32_e32 v48, v46
	v_pk_mul_f32 v[42:43], v[42:43], v[72:73]
	v_pk_mul_f32 v[44:45], v[44:45], v[70:71]
	v_pk_mul_f32 v[42:43], v[42:43], s[82:83] op_sel_hi:[1,0]
	v_pk_mul_f32 v[44:45], v[44:45], s[82:83] op_sel_hi:[1,0]
	v_cvt_pk_bf16_f32 v42, v42, v43
	v_cvt_pk_bf16_f32 v43, v44, v45
	v_pk_mul_f32 v[44:45], v[68:69], s[82:83] op_sel_hi:[1,0]
	v_pk_mul_f32 v[46:47], v[66:67], s[82:83] op_sel_hi:[1,0]
	v_cvt_pk_bf16_f32 v44, v44, v45
	v_cvt_pk_bf16_f32 v45, v46, v47
	v_mul_f32_e32 v46, 0x45800000, v48
	v_cndmask_b32_e64 v46, v48, v46, s[4:5]
	v_pk_mul_f32 v[48:49], v[46:47], v[86:87] op_sel_hi:[0,1]
	v_pk_mul_f32 v[48:49], v[58:59], v[48:49]
	v_bitop3_b32 v74, v148, v209, v147 bitop3:0x36
	v_mov_b32_e32 v47, v48
	v_mov_b32_e32 v50, v48
	v_mov_b32_e32 v51, v49
	v_mov_b32_e32 v52, v49
	v_permlane16_swap_b32_e32 v47, v50
	s_nop 0
	v_permlane16_swap_b32_e32 v51, v52
	v_cndmask_b32_e32 v51, v51, v52, vcc
	v_cndmask_b32_e32 v50, v47, v50, vcc
	v_pk_fma_f32 v[48:49], v[50:51], 0, v[48:49] op_sel_hi:[1,0,1]
	v_pk_mul_f32 v[50:51], v[46:47], v[98:99] op_sel_hi:[0,1]
	v_pk_mul_f32 v[50:51], v[60:61], v[50:51]
	v_lshl_add_u32 v212, v74, 4, v149
	v_mov_b32_e32 v47, v50
	v_mov_b32_e32 v52, v50
	v_mov_b32_e32 v53, v51
	v_mov_b32_e32 v58, v51
	v_permlane16_swap_b32_e32 v47, v52
	s_nop 0
	v_permlane16_swap_b32_e32 v53, v58
	v_cndmask_b32_e32 v53, v53, v58, vcc
	v_cndmask_b32_e32 v52, v47, v52, vcc
	v_pk_fma_f32 v[50:51], v[52:53], 0, v[50:51] op_sel_hi:[1,0,1]
	v_pk_mul_f32 v[52:53], v[46:47], v[90:91] op_sel_hi:[0,1]
	v_pk_mul_f32 v[52:53], v[54:55], v[52:53]
	s_lshl_b32 s4, s36, 11
	v_mov_b32_e32 v47, v52
	v_mov_b32_e32 v54, v52
	s_nop 1
	v_permlane16_swap_b32_e32 v47, v54
	v_mov_b32_e32 v55, v53
	v_mov_b32_e32 v58, v53
	s_nop 1
	v_permlane16_swap_b32_e32 v55, v58
	v_cndmask_b32_e32 v54, v47, v54, vcc
	v_pk_mul_f32 v[46:47], v[46:47], v[82:83] op_sel_hi:[0,1]
	v_cndmask_b32_e32 v55, v55, v58, vcc
	v_pk_mul_f32 v[46:47], v[56:57], v[46:47]
	v_pk_fma_f32 v[52:53], v[54:55], 0, v[52:53] op_sel_hi:[1,0,1]
	v_mov_b32_e32 v54, v46
	v_mov_b32_e32 v56, v46
	v_mov_b32_e32 v55, v47
	v_mov_b32_e32 v57, v47
	v_permlane16_swap_b32_e32 v54, v56
	s_nop 0
	v_permlane16_swap_b32_e32 v55, v57
	v_cndmask_b32_e32 v55, v55, v57, vcc
	v_cndmask_b32_e32 v54, v54, v56, vcc
	v_pk_fma_f32 v[54:55], v[54:55], 0, v[46:47] op_sel_hi:[1,0,1]
	v_pk_mul_f32 v[46:47], v[48:49], s[82:83] op_sel_hi:[1,0]
	v_pk_mul_f32 v[48:49], v[50:51], s[82:83] op_sel_hi:[1,0]
	v_cvt_pk_bf16_f32 v46, v46, v47
	v_cvt_pk_bf16_f32 v47, v48, v49
	v_pk_mul_f32 v[48:49], v[52:53], s[82:83] op_sel_hi:[1,0]
	v_pk_mul_f32 v[50:51], v[54:55], s[82:83] op_sel_hi:[1,0]
	v_cvt_pk_bf16_f32 v48, v48, v49
	v_cvt_pk_bf16_f32 v49, v50, v51
	s_waitcnt vmcnt(0) lgkmcnt(0)
	s_barrier
; #define ATT_SB() __builtin_amdgcn_sched_barrier(0)
; #define ATT_DMA_K(t, sl) do { glds16(ksrc + (size_t)(t) * 64 * kpitch, (unsigned)__builtin_amdgcn_readfirstlane(kdst + (sl) * KSLOT)); \
;         if constexpr (DQK == 96) glds16(krsrc + (size_t)(t) * 64 * 32, (unsigned)__builtin_amdgcn_readfirstlane(krdst + (sl) * KSLOT)); } while (0)
; #define ATT_DMA_V(t, sl) do { glds16(vsrc + (size_t)(t) * 64, (unsigned)__builtin_amdgcn_readfirstlane(vdst + (sl) * VSLOT)); \
;         if constexpr (DV == 128) glds16(vsrc + (size_t)64 * NR + (size_t)(t) * 64, (unsigned)__builtin_amdgcn_readfirstlane(vdst + (sl) * VSLOT + 8192)); } while (0)
; #define ATT_KLOAD(sl) do { _Pragma("unroll") for (int kb_ = 0; kb_ < NKW; ++kb_) _Pragma("unroll") for (int ds_ = 0; ds_ < NDS; ++ds_) { \
;         if (ds_ < 2) kf[kb_ * NDS + ds_] = *(const LAS bf16x8*)(kp[ds_ & 1] + (sl) * KSLOT + (kb_ & 1) * 512 + (kb_ >> 1) * 4096); \
;         else kf[kb_ * NDS + ds_] = *(const LAS bf16x8*)(krp + (sl) * KSLOT + (kb_ & 1) * 256 + (kb_ >> 1) * 2048); } } while (0)
; #define ATT_QK() do { _Pragma("unroll") for (int kb_ = 0; kb_ < NKW; ++kb_) _Pragma("unroll") for (int ds_ = 0; ds_ < NDS; ++ds_) _Pragma("unroll") for (int qb_ = 0; qb_ < NQB; ++qb_) \
;         c[kb_][qb_] = __builtin_amdgcn_mfma_f32_16x16x32_bf16(kf[kb_ * NDS + ds_], qf[qb_ * NDS + ds_], ds_ == 0 ? zero4 : c[kb_][qb_], 0, 0, 0); } while (0)
; template <int DQK, int DV, bool LEAD> ...
;     ...
;     bf16x8 kf[NKW * NDS], vf[NVF];
;     ATT_KLOAD(0);
;     asm volatile("s_waitcnt lgkmcnt(0)\n\ts_barrier" ::: "memory");
;     float lsum[NQB];
; #pragma unroll
;     for (int qb = 0; qb < NQB; ++qb) lsum[qb] = 0.f;
;     const f32x4 zero4 = {0.f, 0.f, 0.f, 0.f};
;     f32x4 o[NDB][NQB], c[NKW][NQB]; u32x4 pw[4];
; #pragma unroll
;     for (int i = 0; i < NDB; ++i)
; #pragma unroll
;         for (int qb = 0; qb < NQB; ++qb) o[i][qb] = zero4;
;     ATT_DMA_K(3, 0); ATT_DMA_V(1, 1);
;     ATT_QK(); ATT_SB();
;     ATT_KLOAD(1); ATT_SB();
;     if constexpr (LEAD) { ATT_EXP(); ATT_SUMPACK(); }
;     wait_bar<NDMA>();
;     int s_prev = 0, s_cur = 1, s_next = 2;
;     int one_ = 1; asm volatile("" : "+s"(one_));
	ds_read_b128 v[50:53], v208
	ds_read_b128 v[54:57], v208 offset:512
	s_waitcnt lgkmcnt(1)
	v_mfma_f32_16x16x32_bf16 v[58:61], v[50:53], v[6:9], 0
	ds_read_b128 v[74:77], v212
	ds_read_b128 v[78:81], v212 offset:512
	v_lshlrev_b32_e32 v82, 5, v146
	v_lshlrev_b32_e32 v83, 6, v144
	v_mfma_f32_16x16x32_bf16 v[66:69], v[50:53], v[18:21], 0
	v_bitop3_b32 v82, v82, v142, 48 bitop3:0x78
	v_sub_u32_e32 v83, v145, v83
	v_add3_u32 v213, v83, v82, s4
	v_mfma_f32_16x16x32_bf16 v[70:73], v[50:53], v[30:33], 0
	s_mov_b64 s[4:5], 0x60000
	v_lshl_add_u64 v[192:193], v[62:63], 0, s[4:5]
	s_cmpk_lt_u32 s16, 0x100
	v_mfma_f32_16x16x32_bf16 v[50:53], v[50:53], v[38:41], 0
	s_cselect_b64 vcc, -1, 0
	s_waitcnt lgkmcnt(1)
	v_mfma_f32_16x16x32_bf16 v[58:61], v[74:77], v[2:5], v[58:61]
	v_mfma_f32_16x16x32_bf16 v[66:69], v[74:77], v[14:17], v[66:69]
	v_mfma_f32_16x16x32_bf16 v[70:73], v[74:77], v[26:29], v[70:73]
	v_mfma_f32_16x16x32_bf16 v[50:53], v[74:77], v[42:45], v[50:53]
	ds_read_b128 v[74:77], v213 offset:8192
	ds_read_b128 v[82:85], v213 offset:8448
	s_waitcnt lgkmcnt(0)
	s_barrier
	s_mov_b32 m0, s31
	s_nop 0
	global_load_lds_dwordx4 v[192:193], off
	s_waitcnt lgkmcnt(1)
	v_mfma_f32_16x16x32_bf16 v[86:89], v[74:77], v[10:13], v[58:61]
	s_mov_b64 s[4:5], 0x3000
	v_lshl_add_u64 v[204:205], v[64:65], 0, s[4:5]
	s_mov_b32 m0, s42
	s_nop 0
	global_load_lds_dwordx4 v[204:205], off
	v_mfma_f32_16x16x32_bf16 v[90:93], v[74:77], v[22:25], v[66:69]
	s_add_i32 s4, s41, 0x2000
	v_mfma_f32_16x16x32_bf16 v[94:97], v[74:77], v[34:37], v[70:73]
	v_mfma_f32_16x16x32_bf16 v[74:77], v[74:77], v[46:49], v[50:53]
	v_mfma_f32_16x16x32_bf16 v[50:53], v[54:57], v[6:9], 0
	v_mfma_f32_16x16x32_bf16 v[58:61], v[54:57], v[18:21], 0
	v_mfma_f32_16x16x32_bf16 v[66:69], v[54:57], v[30:33], 0
	v_mfma_f32_16x16x32_bf16 v[54:57], v[54:57], v[38:41], 0
	v_mfma_f32_16x16x32_bf16 v[50:53], v[78:81], v[2:5], v[50:53]
	v_mfma_f32_16x16x32_bf16 v[58:61], v[78:81], v[14:17], v[58:61]
	v_mfma_f32_16x16x32_bf16 v[66:69], v[78:81], v[26:29], v[66:69]
	v_mfma_f32_16x16x32_bf16 v[54:57], v[78:81], v[42:45], v[54:57]
	s_waitcnt lgkmcnt(0)
	v_mfma_f32_16x16x32_bf16 v[78:81], v[82:85], v[10:13], v[50:53]
	v_mfma_f32_16x16x32_bf16 v[98:101], v[82:85], v[22:25], v[58:61]
	s_nop 1
	v_lshl_add_u64 v[50:51], v[186:187], 0, s[66:67]
	s_mov_b32 m0, s4
	s_nop 0
	global_load_lds_dwordx4 v[50:51], off
	v_mfma_f32_16x16x32_bf16 v[102:105], v[82:85], v[34:37], v[66:69]
	v_mfma_f32_16x16x32_bf16 v[82:85], v[82:85], v[46:49], v[54:57]
	ds_read_b128 v[50:53], v208 offset:12288
	s_nop 1
	ds_read_b128 v[54:57], v208 offset:12800
	ds_read_b128 v[58:61], v212 offset:12288
	ds_read_b128 v[62:65], v212 offset:12800
	ds_read_b128 v[66:69], v213 offset:20480
	ds_read_b128 v[70:73], v213 offset:20736
	v_exp_f32_e32 v86, v86
	v_exp_f32_e32 v87, v87
	v_exp_f32_e32 v88, v88
	v_exp_f32_e32 v89, v89
	v_exp_f32_e32 v90, v90
	v_exp_f32_e32 v91, v91
	v_exp_f32_e32 v92, v92
	v_exp_f32_e32 v93, v93
	v_exp_f32_e32 v94, v94
	v_exp_f32_e32 v95, v95
	v_exp_f32_e32 v96, v96
	v_exp_f32_e32 v97, v97
	v_exp_f32_e32 v107, v74
	v_exp_f32_e32 v108, v75
	v_exp_f32_e32 v109, v76
	v_exp_f32_e32 v110, v77
	v_add_f32_e32 v74, v86, v87
	v_add_f32_e32 v75, v88, v89
	v_exp_f32_e32 v78, v78
	v_exp_f32_e32 v98, v98
	v_exp_f32_e32 v102, v102
	v_exp_f32_e32 v82, v82
	v_add_f32_e32 v74, v74, v75
	v_add_f32_e32 v75, v90, v91
	v_add_f32_e32 v76, v92, v93
	v_add_f32_e32 v75, v75, v76
	v_add_f32_e32 v76, v94, v95
	v_add_f32_e32 v77, v96, v97
	v_exp_f32_e32 v79, v79
	v_exp_f32_e32 v99, v99
	v_exp_f32_e32 v103, v103
	v_exp_f32_e32 v83, v83
	v_add_f32_e32 v76, v76, v77
	v_add_f32_e32 v77, v107, v108
	v_add_f32_e32 v111, v109, v110
	v_add_f32_e32 v77, v77, v111
	v_exp_f32_e32 v80, v80
	v_exp_f32_e32 v100, v100
	v_exp_f32_e32 v104, v104
	v_exp_f32_e32 v84, v84
	v_add_f32_e32 v74, v74, v78
	v_add_f32_e32 v75, v75, v98
	v_add_f32_e32 v76, v76, v102
	v_add_f32_e32 v77, v77, v82
	v_exp_f32_e32 v81, v81
	v_exp_f32_e32 v101, v101
	v_exp_f32_e32 v105, v105
	v_exp_f32_e32 v85, v85
	v_add_f32_e32 v74, v79, v74
	v_add_f32_e32 v75, v99, v75
	v_add_f32_e32 v76, v103, v76
	v_add_f32_e32 v77, v83, v77
	s_mov_b32 s4, 1
	v_add_f32_e32 v74, v80, v74
	v_add_f32_e32 v111, v100, v75
	v_add_f32_e32 v76, v104, v76
	v_add_f32_e32 v112, v84, v77
	v_cvt_pk_bf16_f32 v134, v86, v87
	v_add_f32_e32 v75, v81, v74
	v_add_f32_e32 v74, v101, v111
	v_add_f32_e32 v77, v105, v76
	v_add_f32_e32 v76, v85, v112
	s_waitcnt vmcnt(3) lgkmcnt(0)
	s_barrier
	s_cmp_lg_u32 s4, 0
	v_pk_add_f32 v[190:191], v[74:75], 0 op_sel_hi:[1,0]
	v_cndmask_b32_e32 v74, v209, v194, vcc
	v_bitop3_b32 v74, v74, v106, 7 bitop3:0x78
	v_lshlrev_b32_e32 v74, 4, v74
	v_add3_u32 v214, 0, v211, v74
	v_mov_b32_e32 v74, 0
	v_pk_add_f32 v[188:189], v[76:77], 0 op_sel_hi:[1,0]
	v_cvt_pk_bf16_f32 v135, v88, v89
	v_cvt_pk_bf16_f32 v136, v78, v79
	v_cvt_pk_bf16_f32 v137, v80, v81
	v_cvt_pk_bf16_f32 v142, v90, v91
	v_cvt_pk_bf16_f32 v143, v92, v93
	v_cvt_pk_bf16_f32 v144, v98, v99
	v_cvt_pk_bf16_f32 v145, v100, v101
	v_cvt_pk_bf16_f32 v146, v94, v95
	v_cvt_pk_bf16_f32 v147, v96, v97
	v_cvt_pk_bf16_f32 v148, v102, v103
	v_cvt_pk_bf16_f32 v149, v104, v105
	v_cvt_pk_bf16_f32 v150, v107, v108
	v_cvt_pk_bf16_f32 v151, v109, v110
	v_cvt_pk_bf16_f32 v152, v82, v83
	v_cvt_pk_bf16_f32 v153, v84, v85
	s_cselect_b64 s[4:5], -1, 0
	s_mov_b32 s27, 2
	v_mov_b32_e32 v75, v74
	v_mov_b32_e32 v76, v74
	v_mov_b32_e32 v77, v74
	v_mov_b32_e32 v78, v74
	v_mov_b32_e32 v79, v74
	v_mov_b32_e32 v80, v74
	v_mov_b32_e32 v81, v74
	v_mov_b32_e32 v82, v74
	v_mov_b32_e32 v83, v74
	v_mov_b32_e32 v84, v74
	v_mov_b32_e32 v85, v74
	v_mov_b32_e32 v86, v74
	v_mov_b32_e32 v87, v74
	v_mov_b32_e32 v88, v74
	v_mov_b32_e32 v89, v74
	v_mov_b32_e32 v90, v74
	v_mov_b32_e32 v91, v74
	v_mov_b32_e32 v92, v74
	v_mov_b32_e32 v93, v74
	v_mov_b32_e32 v94, v74
	v_mov_b32_e32 v95, v74
	v_mov_b32_e32 v96, v74
	v_mov_b32_e32 v97, v74
	v_mov_b32_e32 v98, v74
	v_mov_b32_e32 v99, v74
	v_mov_b32_e32 v100, v74
	v_mov_b32_e32 v101, v74
	v_mov_b32_e32 v102, v74
	v_mov_b32_e32 v103, v74
	v_mov_b32_e32 v104, v74
	v_mov_b32_e32 v105, v74
	v_mov_b32_e32 v106, v74
	v_mov_b32_e32 v107, v74
	v_mov_b32_e32 v108, v74
	v_mov_b32_e32 v109, v74
	v_mov_b32_e32 v110, v74
	v_mov_b32_e32 v111, v74
	v_mov_b32_e32 v112, v74
	v_mov_b32_e32 v113, v74
	v_mov_b32_e32 v114, v74
	v_mov_b32_e32 v115, v74
	v_mov_b32_e32 v116, v74
	v_mov_b32_e32 v117, v74
	v_mov_b32_e32 v118, v74
	v_mov_b32_e32 v119, v74
	v_mov_b32_e32 v120, v74
	v_mov_b32_e32 v121, v74
	v_mov_b32_e32 v122, v74
	v_mov_b32_e32 v123, v74
	v_mov_b32_e32 v124, v74
	v_mov_b32_e32 v125, v74
	v_mov_b32_e32 v126, v74
	v_mov_b32_e32 v127, v74
	v_mov_b32_e32 v128, v74
	v_mov_b32_e32 v129, v74
	v_mov_b32_e32 v130, v74
	v_mov_b32_e32 v131, v74
	v_mov_b32_e32 v132, v74
	v_mov_b32_e32 v133, v74
	v_mov_b32_e32 v138, v74
	v_mov_b32_e32 v139, v74
	v_mov_b32_e32 v140, v74
	v_mov_b32_e32 v141, v74
	s_branch .LBB0_669

; #define ATT_SB() __builtin_amdgcn_sched_barrier(0)
; #define ATT_DMA_K(t, sl) do { glds16(ksrc + (size_t)(t) * 64 * kpitch, (unsigned)__builtin_amdgcn_readfirstlane(kdst + (sl) * KSLOT)); \
;         if constexpr (DQK == 96) glds16(krsrc + (size_t)(t) * 64 * 32, (unsigned)__builtin_amdgcn_readfirstlane(krdst + (sl) * KSLOT)); } while (0)
; #define ATT_DMA_V(t, sl) do { glds16(vsrc + (size_t)(t) * 64, (unsigned)__builtin_amdgcn_readfirstlane(vdst + (sl) * VSLOT)); \
;         if constexpr (DV == 128) glds16(vsrc + (size_t)64 * NR + (size_t)(t) * 64, (unsigned)__builtin_amdgcn_readfirstlane(vdst + (sl) * VSLOT + 8192)); } while (0)
; #define ATT_KLOAD(sl) do { _Pragma("unroll") for (int kb_ = 0; kb_ < NKW; ++kb_) _Pragma("unroll") for (int ds_ = 0; ds_ < NDS; ++ds_) { \
;         if (ds_ < 2) kf[kb_ * NDS + ds_] = *(const LAS bf16x8*)(kp[ds_ & 1] + (sl) * KSLOT + (kb_ & 1) * 512 + (kb_ >> 1) * 4096); \
;         else kf[kb_ * NDS + ds_] = *(const LAS bf16x8*)(krp + (sl) * KSLOT + (kb_ & 1) * 256 + (kb_ >> 1) * 2048); } } while (0)
; #define ATT_QK() do { _Pragma("unroll") for (int kb_ = 0; kb_ < NKW; ++kb_) _Pragma("unroll") for (int ds_ = 0; ds_ < NDS; ++ds_) _Pragma("unroll") for (int qb_ = 0; qb_ < NQB; ++qb_) \
;         c[kb_][qb_] = __builtin_amdgcn_mfma_f32_16x16x32_bf16(kf[kb_ * NDS + ds_], qf[qb_ * NDS + ds_], ds_ == 0 ? zero4 : c[kb_][qb_], 0, 0, 0); } while (0)
; template <int DQK, int DV, bool LEAD> ...
;     ...
;     for (int t = 1; t < NT; ++t) {
;         __builtin_amdgcn_s_waitcnt(0xC07F);
;         if constexpr (!LEAD) { ATT_EXP(); ATT_SUMPACK(); ATT_SB(); }
;         ATT_VLOAD(s_prev, 0); ATT_SB();
;         { const int tk = (t + 3 < NT) ? t + 3 : NT - 1; ATT_DMA_K(tk, s_cur); }
;         { const int tv = (t + 1 < NT) ? t + 1 : NT - 1; ATT_DMA_V(tv, s_next); }
;         ATT_SB();
;         if constexpr (LEAD) {
;             ATT_QK(); ATT_SB();
;             ATT_PVP(0); ATT_SB();
;             if constexpr (DV == 128) { ATT_VLOAD(s_prev, 1); ATT_SB(); ATT_EXP(); ATT_SB(); ATT_PVP(1); ATT_SB(); }
;             if (one_) ATT_KLOAD(s_next);
;             ATT_SB();
;             if constexpr (DV == 64) ATT_EXP();
;             ATT_SUMPACK();
;             asm volatile("" : "+v"(pw[0]), "+v"(pw[1]), "+v"(pw[2]), "+v"(pw[3]));
; #pragma unroll
;             for (int qb = 0; qb < NQB; ++qb) asm volatile("" : "+v"(lsum[qb]));
.LBB0_669:
	v_lshl_add_u32 v154, s26, 13, v214
	s_waitcnt lgkmcnt(0)
	ds_read_b128 v[198:201], v154 offset:36864
	ds_read_b128 v[216:219], v154 offset:38912
	ds_read_b128 v[220:223], v154 offset:40960
	ds_read_b128 v[228:231], v154 offset:43008
	s_mov_b32 s16, s25
	s_mov_b32 s25, s27
	s_mul_i32 s27, s16, 0x3000
	s_add_i32 s36, s27, s31
	s_mov_b32 m0, s36
	s_nop 0
	global_load_lds_dwordx4 v[192:193], off
	s_add_i32 s27, s27, s42
	s_mov_b32 m0, s27
	s_nop 0
	global_load_lds_dwordx4 v[204:205], off
	s_min_u32 s27, s7, 3
	s_lshl_b32 s38, s27, 7
	s_lshl_b32 s27, s25, 13
	v_lshl_add_u64 v[154:155], v[186:187], 0, s[38:39]
	s_add_i32 s27, s27, s41
	s_mov_b32 m0, s27
	s_nop 0
	global_load_lds_dwordx4 v[154:155], off
	v_mfma_f32_16x16x32_bf16 v[154:157], v[50:53], v[6:9], 0
	v_mfma_f32_16x16x32_bf16 v[158:161], v[50:53], v[18:21], 0
	v_mfma_f32_16x16x32_bf16 v[162:165], v[50:53], v[30:33], 0
	v_mfma_f32_16x16x32_bf16 v[166:169], v[50:53], v[38:41], 0
	v_mfma_f32_16x16x32_bf16 v[154:157], v[58:61], v[2:5], v[154:157]
	v_mfma_f32_16x16x32_bf16 v[158:161], v[58:61], v[14:17], v[158:161]
	v_mfma_f32_16x16x32_bf16 v[162:165], v[58:61], v[26:29], v[162:165]
	v_mfma_f32_16x16x32_bf16 v[166:169], v[58:61], v[42:45], v[166:169]
	v_mfma_f32_16x16x32_bf16 v[182:185], v[66:69], v[10:13], v[154:157]
	v_mfma_f32_16x16x32_bf16 v[178:181], v[66:69], v[22:25], v[158:161]
	v_mfma_f32_16x16x32_bf16 v[170:173], v[66:69], v[34:37], v[162:165]
	v_mfma_f32_16x16x32_bf16 v[162:165], v[66:69], v[46:49], v[166:169]
	v_mfma_f32_16x16x32_bf16 v[154:157], v[54:57], v[6:9], 0
	v_mfma_f32_16x16x32_bf16 v[158:161], v[54:57], v[18:21], 0
	v_mfma_f32_16x16x32_bf16 v[166:169], v[54:57], v[30:33], 0
	v_mfma_f32_16x16x32_bf16 v[174:177], v[54:57], v[38:41], 0
	v_mfma_f32_16x16x32_bf16 v[154:157], v[62:65], v[2:5], v[154:157]
	v_mfma_f32_16x16x32_bf16 v[158:161], v[62:65], v[14:17], v[158:161]
	v_mfma_f32_16x16x32_bf16 v[236:239], v[62:65], v[26:29], v[166:169]
	v_mfma_f32_16x16x32_bf16 v[240:243], v[62:65], v[42:45], v[174:177]
	v_mfma_f32_16x16x32_bf16 v[174:177], v[70:73], v[10:13], v[154:157]
	v_mfma_f32_16x16x32_bf16 v[166:169], v[70:73], v[22:25], v[158:161]
	v_mfma_f32_16x16x32_bf16 v[158:161], v[70:73], v[34:37], v[236:239]
	v_mfma_f32_16x16x32_bf16 v[154:157], v[70:73], v[46:49], v[240:243]
	s_waitcnt lgkmcnt(3)
	v_mfma_f32_16x16x32_bf16 v[138:141], v[198:201], v[134:137], v[138:141]
	v_mfma_f32_16x16x32_bf16 v[130:133], v[198:201], v[142:145], v[130:133]
	v_mfma_f32_16x16x32_bf16 v[126:129], v[198:201], v[146:149], v[126:129]
	v_mfma_f32_16x16x32_bf16 v[122:125], v[198:201], v[150:153], v[122:125]
	s_waitcnt lgkmcnt(2)
	v_mfma_f32_16x16x32_bf16 v[118:121], v[216:219], v[134:137], v[118:121]
	v_mfma_f32_16x16x32_bf16 v[114:117], v[216:219], v[142:145], v[114:117]
	v_mfma_f32_16x16x32_bf16 v[110:113], v[216:219], v[146:149], v[110:113]
	v_mfma_f32_16x16x32_bf16 v[106:109], v[216:219], v[150:153], v[106:109]
	s_waitcnt lgkmcnt(1)
	v_mfma_f32_16x16x32_bf16 v[102:105], v[220:223], v[134:137], v[102:105]
	v_mfma_f32_16x16x32_bf16 v[98:101], v[220:223], v[142:145], v[98:101]
	v_mfma_f32_16x16x32_bf16 v[94:97], v[220:223], v[146:149], v[94:97]
	v_mfma_f32_16x16x32_bf16 v[90:93], v[220:223], v[150:153], v[90:93]
	s_waitcnt lgkmcnt(0)
	v_mfma_f32_16x16x32_bf16 v[86:89], v[228:231], v[134:137], v[86:89]
	v_mfma_f32_16x16x32_bf16 v[82:85], v[228:231], v[142:145], v[82:85]
	v_mfma_f32_16x16x32_bf16 v[78:81], v[228:231], v[146:149], v[78:81]
	v_mfma_f32_16x16x32_bf16 v[74:77], v[228:231], v[150:153], v[74:77]
	s_andn2_b64 vcc, exec, s[4:5]
	s_cbranch_vccnz .LBB0_668
	s_mul_i32 s27, s25, 0x3000
	v_add_u32_e32 v70, s27, v213
	v_add_u32_e32 v54, s27, v208
	v_add_u32_e32 v62, s27, v212
	ds_read_b128 v[50:53], v54
	ds_read_b128 v[54:57], v54 offset:512
	ds_read_b128 v[58:61], v62
	ds_read_b128 v[62:65], v62 offset:512
	ds_read_b128 v[66:69], v70 offset:8192
	ds_read_b128 v[70:73], v70 offset:8448
	s_branch .LBB0_668

; #define PG8_STAGE_B(bufoff, gbase) do { _Pragma("unroll") for (int _i = 0; _i < 2; ++_i) \
;         __builtin_amdgcn_global_load_lds((const unsigned*)((const char*)(gbase) + voffB[_i]), (LAS unsigned*)(lds + (bufoff) + ldsw + _i * 8192), 16, 0, 0); } while (0)
; #define PG8_LDA(dst, b, h) do { _Pragma("unroll") for (int m = 0; m < 4; ++m) _Pragma("unroll") for (int k = 0; k < 2; ++k) dst[m][k] = *(const LAS bf16x8*)(lds + PG8_SA(b, h) + aoff + m * 2048 + k * 1024); } while (0)
; #define PG8_LDB(dst, b, h) do { _Pragma("unroll") for (int n = 0; n < 2; ++n) _Pragma("unroll") for (int k = 0; k < 2; ++k) dst[n][k] = *(const LAS bf16x8*)(lds + PG8_SB(b, h) + boff + n * 2048 + k * 1024); } while (0)
; #define PG8_MMA(ai, bj, At, Bt) do { __builtin_amdgcn_s_setprio(1); _Pragma("unroll") for (int m = 0; m < 4; ++m) _Pragma("unroll") for (int n = 0; n < 2; ++n) _Pragma("unroll") for (int k = 0; k < 2; ++k) \
;         acc[ai][bj][m][n] = __builtin_amdgcn_mfma_f32_16x16x32_bf16(Bt[n][k], At[m][k], acc[ai][bj][m][n], 0, 0, 0); __builtin_amdgcn_s_setprio(0); } while (0)
; #define PG8_WAIT_V(n) asm volatile("s_waitcnt vmcnt(" #n ")" ::: "memory")
; #define PG8_WAIT_L(n) asm volatile("s_waitcnt lgkmcnt(" #n ")" ::: "memory")
; #define PG8_BAR __builtin_amdgcn_s_barrier()
; #define PG8_SCHED __builtin_amdgcn_sched_barrier(0)
; template <class Epi, class Sched, bool GATHER = false>
; __device__ __forceinline__ void gemm_phase(LAS unsigned char* lds, const Gemm g, const Sched& S, const Epi& E) {
;     ...
;             PG8_LDB(B0, 0, 0); PG8_LDB(B1, 0, 1); PG8_SCHED; PG8_LDA(At, 0, 0); PG8_STAGE_A(PG8_SA(1, 1), a1, voC, 1);
;             PG8_WAIT_V(8); PG8_WAIT_L(0); PG8_BAR; PG8_MMA(0, 0, At, B0); PG8_MMA(0, 1, At, B1); PG8_BAR; PG8_SCHED;
;             PG8_LDA(At, 0, 1); PG8_STAGE_B(PG8_SB(0, 0), b2); PG8_STAGE_B(PG8_SB(0, 1), b2 + hstepB); PG8_STAGE_A(PG8_SA(0, 0), a2, vo2, 0);
;             PG8_WAIT_V(8); PG8_WAIT_L(0); PG8_BAR; PG8_MMA(1, 0, At, B0); PG8_MMA(1, 1, At, B1); PG8_BAR; PG8_SCHED;
.LBB0_733:
	s_add_u32 s14, s28, 0xfffc0080
	s_addc_u32 s15, s29, -1
	s_add_i32 s50, 0, 0x10000
	s_cmp_eq_u32 s49, 12
	s_cselect_b32 s31, s21, s15
	s_cselect_b32 s30, s45, s14
	v_add_u32_e32 v143, s50, v140
	s_cselect_b32 s15, s11, s48
	s_cselect_b32 s14, s46, s47
	s_add_i32 s52, 0, 0x14000
	ds_read_b128 v[144:147], v143
	ds_read_b128 v[148:151], v143 offset:1024
	ds_read_b128 v[152:155], v143 offset:2048
	ds_read_b128 v[156:159], v143 offset:3072
	v_add_u32_e32 v143, s52, v140
	ds_read_b128 v[160:163], v143
	ds_read_b128 v[164:167], v143 offset:1024
	ds_read_b128 v[168:171], v143 offset:2048
	ds_read_b128 v[172:175], v143 offset:3072
	v_lshl_add_u64 v[192:193], s[28:29], 0, v[136:137]
	s_add_i32 m0, s35, 0xc000
	ds_read_b128 v[176:179], v142
	ds_read_b128 v[180:183], v142 offset:1024
	ds_read_b128 v[184:187], v142 offset:2048
	ds_read_b128 v[188:191], v142 offset:3072
	ds_read_b128 v[204:207], v142 offset:4096
	ds_read_b128 v[208:211], v142 offset:5120
	ds_read_b128 v[212:215], v142 offset:6144
	ds_read_b128 v[216:219], v142 offset:7168
	global_load_lds_dwordx4 v[192:193], off
	s_add_i32 m0, s35, 0xe000
	v_lshl_add_u64 v[192:193], s[28:29], 0, v[138:139]
	global_load_lds_dwordx4 v[192:193], off
	s_waitcnt vmcnt(8)
	s_waitcnt lgkmcnt(0)
	s_barrier
	s_setprio 1
	s_waitcnt lgkmcnt(0)
	v_mfma_f32_16x16x32_bf16 v[126:129], v[144:147], v[176:179], v[126:129]
	v_mfma_f32_16x16x32_bf16 v[122:125], v[152:155], v[176:179], v[122:125]
	v_mfma_f32_16x16x32_bf16 v[118:121], v[144:147], v[184:187], v[118:121]
	v_mfma_f32_16x16x32_bf16 v[114:117], v[152:155], v[184:187], v[114:117]
	v_mfma_f32_16x16x32_bf16 v[102:105], v[144:147], v[204:207], v[102:105]
	v_mfma_f32_16x16x32_bf16 v[98:101], v[152:155], v[204:207], v[98:101]
	v_mfma_f32_16x16x32_bf16 v[86:89], v[144:147], v[212:215], v[86:89]
	v_mfma_f32_16x16x32_bf16 v[82:85], v[152:155], v[212:215], v[82:85]
	v_mfma_f32_16x16x32_bf16 v[126:129], v[148:151], v[180:183], v[126:129]
	v_mfma_f32_16x16x32_bf16 v[122:125], v[156:159], v[180:183], v[122:125]
	v_mfma_f32_16x16x32_bf16 v[118:121], v[148:151], v[188:191], v[118:121]
	v_mfma_f32_16x16x32_bf16 v[114:117], v[156:159], v[188:191], v[114:117]
	v_mfma_f32_16x16x32_bf16 v[102:105], v[148:151], v[208:211], v[102:105]
	v_mfma_f32_16x16x32_bf16 v[98:101], v[156:159], v[208:211], v[98:101]
	v_mfma_f32_16x16x32_bf16 v[86:89], v[148:151], v[216:219], v[86:89]
	v_mfma_f32_16x16x32_bf16 v[82:85], v[156:159], v[216:219], v[82:85]
	s_setprio 0
	s_setprio 1
	v_mfma_f32_16x16x32_bf16 v[110:113], v[160:163], v[176:179], v[110:113]
	v_mfma_f32_16x16x32_bf16 v[106:109], v[168:171], v[176:179], v[106:109]
	v_mfma_f32_16x16x32_bf16 v[94:97], v[160:163], v[184:187], v[94:97]
	v_mfma_f32_16x16x32_bf16 v[90:93], v[168:171], v[184:187], v[90:93]
	v_mfma_f32_16x16x32_bf16 v[78:81], v[160:163], v[204:207], v[78:81]
	v_mfma_f32_16x16x32_bf16 v[74:77], v[168:171], v[204:207], v[74:77]
	v_mfma_f32_16x16x32_bf16 v[70:73], v[160:163], v[212:215], v[70:73]
	v_mfma_f32_16x16x32_bf16 v[66:69], v[168:171], v[212:215], v[66:69]
	v_mfma_f32_16x16x32_bf16 v[110:113], v[164:167], v[180:183], v[110:113]
	v_mfma_f32_16x16x32_bf16 v[106:109], v[172:175], v[180:183], v[106:109]
	v_mfma_f32_16x16x32_bf16 v[94:97], v[164:167], v[188:191], v[94:97]
	v_mfma_f32_16x16x32_bf16 v[90:93], v[172:175], v[188:191], v[90:93]
	v_mfma_f32_16x16x32_bf16 v[78:81], v[164:167], v[208:211], v[78:81]
	v_mfma_f32_16x16x32_bf16 v[74:77], v[172:175], v[208:211], v[74:77]
	v_mfma_f32_16x16x32_bf16 v[70:73], v[164:167], v[216:219], v[70:73]
	v_mfma_f32_16x16x32_bf16 v[66:69], v[172:175], v[216:219], v[66:69]
	s_setprio 0
	s_barrier
	s_add_i32 s50, s50, s34
	v_lshl_add_u64 v[192:193], s[14:15], 0, v[194:195]
	s_mov_b32 m0, s50
	ds_read_b128 v[176:179], v142 offset:16384
	ds_read_b128 v[180:183], v142 offset:17408
	ds_read_b128 v[184:187], v142 offset:18432
	ds_read_b128 v[188:191], v142 offset:19456
	ds_read_b128 v[204:207], v142 offset:20480
	ds_read_b128 v[208:211], v142 offset:21504
	ds_read_b128 v[212:215], v142 offset:22528
	ds_read_b128 v[216:219], v142 offset:23552
	global_load_lds_dwordx4 v[192:193], off
	s_add_i32 m0, s50, 0x2000
	s_add_u32 s50, s14, 0x40000
	v_lshl_add_u64 v[198:199], s[14:15], 0, v[134:135]
	s_addc_u32 s51, s15, 0
	s_add_i32 s52, s52, s34
	global_load_lds_dwordx4 v[198:199], off
	v_lshl_add_u64 v[200:201], s[50:51], 0, v[194:195]
	s_mov_b32 m0, s52
	v_lshl_add_u64 v[220:221], s[30:31], 0, v[130:131]
	global_load_lds_dwordx4 v[200:201], off
	s_add_i32 m0, s52, 0x2000
	v_lshl_add_u64 v[200:201], s[50:51], 0, v[134:135]
	global_load_lds_dwordx4 v[200:201], off
	s_mov_b32 m0, s35
	v_lshl_add_u64 v[200:201], s[30:31], 0, v[132:133]
	global_load_lds_dwordx4 v[200:201], off
	s_mov_b32 m0, s36
	s_nop 0
	global_load_lds_dwordx4 v[220:221], off
	s_waitcnt vmcnt(8)
	s_waitcnt lgkmcnt(0)
	s_barrier
; #define PG8_LDA(dst, b, h) do { _Pragma("unroll") for (int m = 0; m < 4; ++m) _Pragma("unroll") for (int k = 0; k < 2; ++k) dst[m][k] = *(const LAS bf16x8*)(lds + PG8_SA(b, h) + aoff + m * 2048 + k * 1024); } while (0)
; #define PG8_LDB(dst, b, h) do { _Pragma("unroll") for (int n = 0; n < 2; ++n) _Pragma("unroll") for (int k = 0; k < 2; ++k) dst[n][k] = *(const LAS bf16x8*)(lds + PG8_SB(b, h) + boff + n * 2048 + k * 1024); } while (0)
; #define PG8_MMA(ai, bj, At, Bt) do { __builtin_amdgcn_s_setprio(1); _Pragma("unroll") for (int m = 0; m < 4; ++m) _Pragma("unroll") for (int n = 0; n < 2; ++n) _Pragma("unroll") for (int k = 0; k < 2; ++k) \
;         acc[ai][bj][m][n] = __builtin_amdgcn_mfma_f32_16x16x32_bf16(Bt[n][k], At[m][k], acc[ai][bj][m][n], 0, 0, 0); __builtin_amdgcn_s_setprio(0); } while (0)
; #define PG8_WAIT_V(n) asm volatile("s_waitcnt vmcnt(" #n ")" ::: "memory")
; #define PG8_WAIT_L(n) asm volatile("s_waitcnt lgkmcnt(" #n ")" ::: "memory")
; #define PG8_BAR __builtin_amdgcn_s_barrier()
; #define PG8_SCHED __builtin_amdgcn_sched_barrier(0)
; template <class Epi, class Sched, bool GATHER = false>
; __device__ __forceinline__ void gemm_phase(LAS unsigned char* lds, const Gemm g, const Sched& S, const Epi& E) {
;     ...
;             PG8_WAIT_V(8); PG8_WAIT_L(0); PG8_BAR; PG8_MMA(1, 0, At, B0); PG8_MMA(1, 1, At, B1); PG8_BAR; PG8_SCHED;
;             PG8_LDB(B0, 1, 0); PG8_LDB(B1, 1, 1); PG8_SCHED; PG8_LDA(At, 1, 0); PG8_STAGE_A(PG8_SA(0, 1), a2, vo2, 1);
;             PG8_WAIT_V(8); PG8_WAIT_L(0); PG8_BAR; PG8_MMA(0, 0, At, B0); PG8_MMA(0, 1, At, B1); PG8_BAR; PG8_SCHED;
	s_setprio 1
	s_waitcnt lgkmcnt(0)
	v_mfma_f32_16x16x32_bf16 v[62:65], v[144:147], v[176:179], v[62:65]
	v_mfma_f32_16x16x32_bf16 v[58:61], v[152:155], v[176:179], v[58:61]
	v_mfma_f32_16x16x32_bf16 v[54:57], v[144:147], v[184:187], v[54:57]
	v_mfma_f32_16x16x32_bf16 v[50:53], v[152:155], v[184:187], v[50:53]
	v_mfma_f32_16x16x32_bf16 v[38:41], v[144:147], v[204:207], v[38:41]
	v_mfma_f32_16x16x32_bf16 v[34:37], v[152:155], v[204:207], v[34:37]
	v_mfma_f32_16x16x32_bf16 v[22:25], v[144:147], v[212:215], v[22:25]
	v_mfma_f32_16x16x32_bf16 v[18:21], v[152:155], v[212:215], v[18:21]
	v_mfma_f32_16x16x32_bf16 v[62:65], v[148:151], v[180:183], v[62:65]
	v_mfma_f32_16x16x32_bf16 v[58:61], v[156:159], v[180:183], v[58:61]
	v_mfma_f32_16x16x32_bf16 v[54:57], v[148:151], v[188:191], v[54:57]
	v_mfma_f32_16x16x32_bf16 v[50:53], v[156:159], v[188:191], v[50:53]
	v_mfma_f32_16x16x32_bf16 v[38:41], v[148:151], v[208:211], v[38:41]
	v_mfma_f32_16x16x32_bf16 v[34:37], v[156:159], v[208:211], v[34:37]
	v_mfma_f32_16x16x32_bf16 v[22:25], v[148:151], v[216:219], v[22:25]
	v_mfma_f32_16x16x32_bf16 v[18:21], v[156:159], v[216:219], v[18:21]
	s_setprio 0
	s_setprio 1
	v_mfma_f32_16x16x32_bf16 v[46:49], v[160:163], v[176:179], v[46:49]
	v_mfma_f32_16x16x32_bf16 v[42:45], v[168:171], v[176:179], v[42:45]
	v_mfma_f32_16x16x32_bf16 v[30:33], v[160:163], v[184:187], v[30:33]
	v_mfma_f32_16x16x32_bf16 v[26:29], v[168:171], v[184:187], v[26:29]
	v_mfma_f32_16x16x32_bf16 v[14:17], v[160:163], v[204:207], v[14:17]
	v_mfma_f32_16x16x32_bf16 v[10:13], v[168:171], v[204:207], v[10:13]
	v_mfma_f32_16x16x32_bf16 v[6:9], v[160:163], v[212:215], v[6:9]
	v_mfma_f32_16x16x32_bf16 v[2:5], v[168:171], v[212:215], v[2:5]
	v_mfma_f32_16x16x32_bf16 v[46:49], v[164:167], v[180:183], v[46:49]
	v_mfma_f32_16x16x32_bf16 v[42:45], v[172:175], v[180:183], v[42:45]
	v_mfma_f32_16x16x32_bf16 v[30:33], v[164:167], v[188:191], v[30:33]
	v_mfma_f32_16x16x32_bf16 v[26:29], v[172:175], v[188:191], v[26:29]
	v_mfma_f32_16x16x32_bf16 v[14:17], v[164:167], v[208:211], v[14:17]
	v_mfma_f32_16x16x32_bf16 v[10:13], v[172:175], v[208:211], v[10:13]
	v_mfma_f32_16x16x32_bf16 v[6:9], v[164:167], v[216:219], v[6:9]
	v_mfma_f32_16x16x32_bf16 v[2:5], v[172:175], v[216:219], v[2:5]
	s_setprio 0
	s_barrier
	s_add_i32 s50, 0, 0x18000
	v_add_u32_e32 v143, s50, v140
	s_add_i32 s51, 0, 0x1c000
	ds_read_b128 v[144:147], v143
	ds_read_b128 v[148:151], v143 offset:1024
	ds_read_b128 v[152:155], v143 offset:2048
	ds_read_b128 v[156:159], v143 offset:3072
	v_add_u32_e32 v143, s51, v140
	ds_read_b128 v[160:163], v143
	ds_read_b128 v[164:167], v143 offset:1024
	ds_read_b128 v[168:171], v143 offset:2048
	ds_read_b128 v[172:175], v143 offset:3072
	s_add_u32 s30, s30, 0x40000
	s_addc_u32 s31, s31, 0
	s_mov_b32 m0, s37
	v_lshl_add_u64 v[222:223], s[30:31], 0, v[132:133]
	ds_read_b128 v[176:179], v142 offset:32768
	ds_read_b128 v[180:183], v142 offset:33792
	ds_read_b128 v[184:187], v142 offset:34816
	ds_read_b128 v[188:191], v142 offset:35840
	ds_read_b128 v[204:207], v142 offset:36864
	ds_read_b128 v[208:211], v142 offset:37888
	ds_read_b128 v[212:215], v142 offset:38912
	ds_read_b128 v[216:219], v142 offset:39936
	global_load_lds_dwordx4 v[222:223], off
	s_mov_b32 m0, s38
	v_lshl_add_u64 v[222:223], s[30:31], 0, v[130:131]
	global_load_lds_dwordx4 v[222:223], off
	s_waitcnt vmcnt(8)
	s_waitcnt lgkmcnt(0)
	s_barrier
	s_setprio 1
	s_waitcnt lgkmcnt(0)
	v_mfma_f32_16x16x32_bf16 v[126:129], v[144:147], v[176:179], v[126:129]
	v_mfma_f32_16x16x32_bf16 v[122:125], v[152:155], v[176:179], v[122:125]
	v_mfma_f32_16x16x32_bf16 v[118:121], v[144:147], v[184:187], v[118:121]
	v_mfma_f32_16x16x32_bf16 v[114:117], v[152:155], v[184:187], v[114:117]
	v_mfma_f32_16x16x32_bf16 v[102:105], v[144:147], v[204:207], v[102:105]
	v_mfma_f32_16x16x32_bf16 v[98:101], v[152:155], v[204:207], v[98:101]
	v_mfma_f32_16x16x32_bf16 v[86:89], v[144:147], v[212:215], v[86:89]
	v_mfma_f32_16x16x32_bf16 v[82:85], v[152:155], v[212:215], v[82:85]
	v_mfma_f32_16x16x32_bf16 v[126:129], v[148:151], v[180:183], v[126:129]
	v_mfma_f32_16x16x32_bf16 v[122:125], v[156:159], v[180:183], v[122:125]
	v_mfma_f32_16x16x32_bf16 v[118:121], v[148:151], v[188:191], v[118:121]
	v_mfma_f32_16x16x32_bf16 v[114:117], v[156:159], v[188:191], v[114:117]
	v_mfma_f32_16x16x32_bf16 v[102:105], v[148:151], v[208:211], v[102:105]
	v_mfma_f32_16x16x32_bf16 v[98:101], v[156:159], v[208:211], v[98:101]
	v_mfma_f32_16x16x32_bf16 v[86:89], v[148:151], v[216:219], v[86:89]
	v_mfma_f32_16x16x32_bf16 v[82:85], v[156:159], v[216:219], v[82:85]
	s_setprio 0
	s_setprio 1
	v_mfma_f32_16x16x32_bf16 v[110:113], v[160:163], v[176:179], v[110:113]
	v_mfma_f32_16x16x32_bf16 v[106:109], v[168:171], v[176:179], v[106:109]
	v_mfma_f32_16x16x32_bf16 v[94:97], v[160:163], v[184:187], v[94:97]
	v_mfma_f32_16x16x32_bf16 v[90:93], v[168:171], v[184:187], v[90:93]
	v_mfma_f32_16x16x32_bf16 v[78:81], v[160:163], v[204:207], v[78:81]
	v_mfma_f32_16x16x32_bf16 v[74:77], v[168:171], v[204:207], v[74:77]
	v_mfma_f32_16x16x32_bf16 v[70:73], v[160:163], v[212:215], v[70:73]
	v_mfma_f32_16x16x32_bf16 v[66:69], v[168:171], v[212:215], v[66:69]
	v_mfma_f32_16x16x32_bf16 v[110:113], v[164:167], v[180:183], v[110:113]
	v_mfma_f32_16x16x32_bf16 v[106:109], v[172:175], v[180:183], v[106:109]
	v_mfma_f32_16x16x32_bf16 v[94:97], v[164:167], v[188:191], v[94:97]
	v_mfma_f32_16x16x32_bf16 v[90:93], v[172:175], v[188:191], v[90:93]
	v_mfma_f32_16x16x32_bf16 v[78:81], v[164:167], v[208:211], v[78:81]
	v_mfma_f32_16x16x32_bf16 v[74:77], v[172:175], v[208:211], v[74:77]
	v_mfma_f32_16x16x32_bf16 v[70:73], v[164:167], v[216:219], v[70:73]
	v_mfma_f32_16x16x32_bf16 v[66:69], v[172:175], v[216:219], v[66:69]
	s_setprio 0
	s_barrier
; #define PG8_STAGE_B(bufoff, gbase) do { _Pragma("unroll") for (int _i = 0; _i < 2; ++_i) \
;         __builtin_amdgcn_global_load_lds((const unsigned*)((const char*)(gbase) + voffB[_i]), (LAS unsigned*)(lds + (bufoff) + ldsw + _i * 8192), 16, 0, 0); } while (0)
; #define PG8_LDA(dst, b, h) do { _Pragma("unroll") for (int m = 0; m < 4; ++m) _Pragma("unroll") for (int k = 0; k < 2; ++k) dst[m][k] = *(const LAS bf16x8*)(lds + PG8_SA(b, h) + aoff + m * 2048 + k * 1024); } while (0)
; #define PG8_MMA(ai, bj, At, Bt) do { __builtin_amdgcn_s_setprio(1); _Pragma("unroll") for (int m = 0; m < 4; ++m) _Pragma("unroll") for (int n = 0; n < 2; ++n) _Pragma("unroll") for (int k = 0; k < 2; ++k) \
;         acc[ai][bj][m][n] = __builtin_amdgcn_mfma_f32_16x16x32_bf16(Bt[n][k], At[m][k], acc[ai][bj][m][n], 0, 0, 0); __builtin_amdgcn_s_setprio(0); } while (0)
; #define PG8_WAIT_V(n) asm volatile("s_waitcnt vmcnt(" #n ")" ::: "memory")
; #define PG8_WAIT_L(n) asm volatile("s_waitcnt lgkmcnt(" #n ")" ::: "memory")
; #define PG8_BAR __builtin_amdgcn_s_barrier()
; #define PG8_SCHED __builtin_amdgcn_sched_barrier(0)
; template <class Epi, class Sched, bool GATHER = false>
; __device__ __forceinline__ void gemm_phase(LAS unsigned char* lds, const Gemm g, const Sched& S, const Epi& E) {
;     ...
;             PG8_LDA(At, 1, 1); PG8_STAGE_B(PG8_SB(1, 0), b3); PG8_STAGE_B(PG8_SB(1, 1), b3 + hstepB); PG8_STAGE_A(PG8_SA(1, 0), a3, vo2, 0);
;             PG8_WAIT_V(8); PG8_WAIT_L(0); PG8_BAR; PG8_MMA(1, 0, At, B0); PG8_MMA(1, 1, At, B1); PG8_BAR; PG8_SCHED;
;         }
	s_add_i32 s30, s50, s34
	v_lshl_add_u64 v[192:193], v[192:193], 0, s[66:67]
	s_mov_b32 m0, s30
	ds_read_b128 v[176:179], v142 offset:49152
	ds_read_b128 v[180:183], v142 offset:50176
	ds_read_b128 v[184:187], v142 offset:51200
	ds_read_b128 v[188:191], v142 offset:52224
	ds_read_b128 v[204:207], v142 offset:53248
	ds_read_b128 v[208:211], v142 offset:54272
	ds_read_b128 v[212:215], v142 offset:55296
	ds_read_b128 v[216:219], v142 offset:56320
	global_load_lds_dwordx4 v[192:193], off
	s_add_i32 m0, s30, 0x2000
	s_add_u32 s14, s14, 0x40080
	v_lshl_add_u64 v[192:193], v[198:199], 0, s[66:67]
	s_addc_u32 s15, s15, 0
	s_add_i32 s30, s51, s34
	global_load_lds_dwordx4 v[192:193], off
	s_mov_b32 m0, s30
	v_lshl_add_u64 v[192:193], s[14:15], 0, v[194:195]
	global_load_lds_dwordx4 v[192:193], off
	s_add_i32 m0, s30, 0x2000
	v_lshl_add_u64 v[192:193], s[14:15], 0, v[134:135]
	global_load_lds_dwordx4 v[192:193], off
	s_mov_b32 m0, s40
	v_lshl_add_u64 v[192:193], v[200:201], 0, s[66:67]
	global_load_lds_dwordx4 v[192:193], off
	s_mov_b32 m0, s41
	v_lshl_add_u64 v[192:193], v[220:221], 0, s[66:67]
	global_load_lds_dwordx4 v[192:193], off
	s_waitcnt vmcnt(8)
	s_waitcnt lgkmcnt(0)
	s_barrier
	s_setprio 1
	s_waitcnt lgkmcnt(0)
	v_mfma_f32_16x16x32_bf16 v[62:65], v[144:147], v[176:179], v[62:65]
	v_mfma_f32_16x16x32_bf16 v[58:61], v[152:155], v[176:179], v[58:61]
	v_mfma_f32_16x16x32_bf16 v[54:57], v[144:147], v[184:187], v[54:57]
	v_mfma_f32_16x16x32_bf16 v[50:53], v[152:155], v[184:187], v[50:53]
	v_mfma_f32_16x16x32_bf16 v[38:41], v[144:147], v[204:207], v[38:41]
	v_mfma_f32_16x16x32_bf16 v[34:37], v[152:155], v[204:207], v[34:37]
	v_mfma_f32_16x16x32_bf16 v[22:25], v[144:147], v[212:215], v[22:25]
	v_mfma_f32_16x16x32_bf16 v[18:21], v[152:155], v[212:215], v[18:21]
	v_mfma_f32_16x16x32_bf16 v[62:65], v[148:151], v[180:183], v[62:65]
	v_mfma_f32_16x16x32_bf16 v[58:61], v[156:159], v[180:183], v[58:61]
	v_mfma_f32_16x16x32_bf16 v[54:57], v[148:151], v[188:191], v[54:57]
	v_mfma_f32_16x16x32_bf16 v[50:53], v[156:159], v[188:191], v[50:53]
	v_mfma_f32_16x16x32_bf16 v[38:41], v[148:151], v[208:211], v[38:41]
	v_mfma_f32_16x16x32_bf16 v[34:37], v[156:159], v[208:211], v[34:37]
	v_mfma_f32_16x16x32_bf16 v[22:25], v[148:151], v[216:219], v[22:25]
	v_mfma_f32_16x16x32_bf16 v[18:21], v[156:159], v[216:219], v[18:21]
	s_setprio 0
	s_setprio 1
	v_mfma_f32_16x16x32_bf16 v[46:49], v[160:163], v[176:179], v[46:49]
	v_mfma_f32_16x16x32_bf16 v[42:45], v[168:171], v[176:179], v[42:45]
	v_mfma_f32_16x16x32_bf16 v[30:33], v[160:163], v[184:187], v[30:33]
	v_mfma_f32_16x16x32_bf16 v[26:29], v[168:171], v[184:187], v[26:29]
	v_mfma_f32_16x16x32_bf16 v[14:17], v[160:163], v[204:207], v[14:17]
	v_mfma_f32_16x16x32_bf16 v[10:13], v[168:171], v[204:207], v[10:13]
	v_mfma_f32_16x16x32_bf16 v[6:9], v[160:163], v[212:215], v[6:9]
	v_mfma_f32_16x16x32_bf16 v[2:5], v[168:171], v[212:215], v[2:5]
	v_mfma_f32_16x16x32_bf16 v[46:49], v[164:167], v[180:183], v[46:49]
	v_mfma_f32_16x16x32_bf16 v[42:45], v[172:175], v[180:183], v[42:45]
	v_mfma_f32_16x16x32_bf16 v[30:33], v[164:167], v[188:191], v[30:33]
	v_mfma_f32_16x16x32_bf16 v[26:29], v[172:175], v[188:191], v[26:29]
	v_mfma_f32_16x16x32_bf16 v[14:17], v[164:167], v[208:211], v[14:17]
	v_mfma_f32_16x16x32_bf16 v[10:13], v[172:175], v[208:211], v[10:13]
	v_mfma_f32_16x16x32_bf16 v[6:9], v[164:167], v[216:219], v[6:9]
	v_mfma_f32_16x16x32_bf16 v[2:5], v[172:175], v[216:219], v[2:5]
	s_setprio 0
	s_barrier
	s_add_i32 s49, s49, 2
	s_add_u32 s28, s28, 0x100
	s_addc_u32 s29, s29, 0
	s_add_u32 s47, s47, 0x100
	s_addc_u32 s48, s48, 0
	s_cmp_gt_u32 s49, 13
	s_cbranch_scc0 .LBB0_733
	s_and_b64 vcc, exec, s[8:9]
	s_cbranch_vccz .LBB0_736
	s_barrier

; #define PG8_STAGE_B(bufoff, gbase) do { _Pragma("unroll") for (int _i = 0; _i < 2; ++_i) \
;         __builtin_amdgcn_global_load_lds((const unsigned*)((const char*)(gbase) + voffB[_i]), (LAS unsigned*)(lds + (bufoff) + ldsw + _i * 8192), 16, 0, 0); } while (0)
; #define PG8_LDA(dst, b, h) do { _Pragma("unroll") for (int m = 0; m < 4; ++m) _Pragma("unroll") for (int k = 0; k < 2; ++k) dst[m][k] = *(const LAS bf16x8*)(lds + PG8_SA(b, h) + aoff + m * 2048 + k * 1024); } while (0)
; #define PG8_LDB(dst, b, h) do { _Pragma("unroll") for (int n = 0; n < 2; ++n) _Pragma("unroll") for (int k = 0; k < 2; ++k) dst[n][k] = *(const LAS bf16x8*)(lds + PG8_SB(b, h) + boff + n * 2048 + k * 1024); } while (0)
; #define PG8_MMA(ai, bj, At, Bt) do { __builtin_amdgcn_s_setprio(1); _Pragma("unroll") for (int m = 0; m < 4; ++m) _Pragma("unroll") for (int n = 0; n < 2; ++n) _Pragma("unroll") for (int k = 0; k < 2; ++k) \
;         acc[ai][bj][m][n] = __builtin_amdgcn_mfma_f32_16x16x32_bf16(Bt[n][k], At[m][k], acc[ai][bj][m][n], 0, 0, 0); __builtin_amdgcn_s_setprio(0); } while (0)
; #define PG8_WAIT_V(n) asm volatile("s_waitcnt vmcnt(" #n ")" ::: "memory")
; #define PG8_WAIT_L(n) asm volatile("s_waitcnt lgkmcnt(" #n ")" ::: "memory")
; #define PG8_BAR __builtin_amdgcn_s_barrier()
; #define PG8_SCHED __builtin_amdgcn_sched_barrier(0)
; template <class Epi, class Sched, bool GATHER = false>
; __device__ __forceinline__ void gemm_phase(LAS unsigned char* lds, const Gemm g, const Sched& S, const Epi& E) {
;     ...
;             PG8_LDB(B0, 0, 0); PG8_LDB(B1, 0, 1); PG8_SCHED; PG8_LDA(At, 0, 0); PG8_STAGE_A(PG8_SA(1, 1), a1, voC, 1);
;             PG8_WAIT_V(8); PG8_WAIT_L(0); PG8_BAR; PG8_MMA(0, 0, At, B0); PG8_MMA(0, 1, At, B1); PG8_BAR; PG8_SCHED;
;             PG8_LDA(At, 0, 1); PG8_STAGE_B(PG8_SB(0, 0), b2); PG8_STAGE_B(PG8_SB(0, 1), b2 + hstepB); PG8_STAGE_A(PG8_SA(0, 0), a2, vo2, 0);
;             PG8_WAIT_V(8); PG8_WAIT_L(0); PG8_BAR; PG8_MMA(1, 0, At, B0); PG8_MMA(1, 1, At, B1); PG8_BAR; PG8_SCHED;
.LBB0_749:
	s_add_u32 s14, s36, 0xfffc0080
	s_addc_u32 s15, s37, -1
	s_add_i32 s54, 0, 0x10000
	s_cmp_eq_u32 s53, 12
	s_cselect_b32 s31, s27, s15
	s_cselect_b32 s30, s49, s14
	v_add_u32_e32 v143, s54, v140
	s_cselect_b32 s15, s23, s52
	s_cselect_b32 s14, s50, s51
	s_add_i32 s58, 0, 0x14000
	ds_read_b128 v[144:147], v143
	ds_read_b128 v[148:151], v143 offset:1024
	ds_read_b128 v[152:155], v143 offset:2048
	ds_read_b128 v[156:159], v143 offset:3072
	v_add_u32_e32 v143, s58, v140
	ds_read_b128 v[160:163], v143
	ds_read_b128 v[164:167], v143 offset:1024
	ds_read_b128 v[168:171], v143 offset:2048
	ds_read_b128 v[172:175], v143 offset:3072
	v_lshl_add_u64 v[192:193], s[36:37], 0, v[136:137]
	s_add_i32 m0, s9, 0xc000
	ds_read_b128 v[176:179], v142
	ds_read_b128 v[180:183], v142 offset:1024
	ds_read_b128 v[184:187], v142 offset:2048
	ds_read_b128 v[188:191], v142 offset:3072
	ds_read_b128 v[204:207], v142 offset:4096
	ds_read_b128 v[208:211], v142 offset:5120
	ds_read_b128 v[212:215], v142 offset:6144
	ds_read_b128 v[216:219], v142 offset:7168
	global_load_lds_dwordx4 v[192:193], off
	s_add_i32 m0, s9, 0xe000
	v_lshl_add_u64 v[192:193], s[36:37], 0, v[138:139]
	global_load_lds_dwordx4 v[192:193], off
	s_waitcnt vmcnt(8)
	s_waitcnt lgkmcnt(0)
	s_barrier
	s_setprio 1
	s_waitcnt lgkmcnt(0)
	v_mfma_f32_16x16x32_bf16 v[126:129], v[144:147], v[176:179], v[126:129]
	v_mfma_f32_16x16x32_bf16 v[122:125], v[152:155], v[176:179], v[122:125]
	v_mfma_f32_16x16x32_bf16 v[118:121], v[144:147], v[184:187], v[118:121]
	v_mfma_f32_16x16x32_bf16 v[114:117], v[152:155], v[184:187], v[114:117]
	v_mfma_f32_16x16x32_bf16 v[102:105], v[144:147], v[204:207], v[102:105]
	v_mfma_f32_16x16x32_bf16 v[98:101], v[152:155], v[204:207], v[98:101]
	v_mfma_f32_16x16x32_bf16 v[86:89], v[144:147], v[212:215], v[86:89]
	v_mfma_f32_16x16x32_bf16 v[82:85], v[152:155], v[212:215], v[82:85]
	v_mfma_f32_16x16x32_bf16 v[126:129], v[148:151], v[180:183], v[126:129]
	v_mfma_f32_16x16x32_bf16 v[122:125], v[156:159], v[180:183], v[122:125]
	v_mfma_f32_16x16x32_bf16 v[118:121], v[148:151], v[188:191], v[118:121]
	v_mfma_f32_16x16x32_bf16 v[114:117], v[156:159], v[188:191], v[114:117]
	v_mfma_f32_16x16x32_bf16 v[102:105], v[148:151], v[208:211], v[102:105]
	v_mfma_f32_16x16x32_bf16 v[98:101], v[156:159], v[208:211], v[98:101]
	v_mfma_f32_16x16x32_bf16 v[86:89], v[148:151], v[216:219], v[86:89]
	v_mfma_f32_16x16x32_bf16 v[82:85], v[156:159], v[216:219], v[82:85]
	s_setprio 0
	s_setprio 1
	v_mfma_f32_16x16x32_bf16 v[110:113], v[160:163], v[176:179], v[110:113]
	v_mfma_f32_16x16x32_bf16 v[106:109], v[168:171], v[176:179], v[106:109]
	v_mfma_f32_16x16x32_bf16 v[94:97], v[160:163], v[184:187], v[94:97]
	v_mfma_f32_16x16x32_bf16 v[90:93], v[168:171], v[184:187], v[90:93]
	v_mfma_f32_16x16x32_bf16 v[78:81], v[160:163], v[204:207], v[78:81]
	v_mfma_f32_16x16x32_bf16 v[74:77], v[168:171], v[204:207], v[74:77]
	v_mfma_f32_16x16x32_bf16 v[70:73], v[160:163], v[212:215], v[70:73]
	v_mfma_f32_16x16x32_bf16 v[66:69], v[168:171], v[212:215], v[66:69]
	v_mfma_f32_16x16x32_bf16 v[110:113], v[164:167], v[180:183], v[110:113]
	v_mfma_f32_16x16x32_bf16 v[106:109], v[172:175], v[180:183], v[106:109]
	v_mfma_f32_16x16x32_bf16 v[94:97], v[164:167], v[188:191], v[94:97]
	v_mfma_f32_16x16x32_bf16 v[90:93], v[172:175], v[188:191], v[90:93]
	v_mfma_f32_16x16x32_bf16 v[78:81], v[164:167], v[208:211], v[78:81]
	v_mfma_f32_16x16x32_bf16 v[74:77], v[172:175], v[208:211], v[74:77]
	v_mfma_f32_16x16x32_bf16 v[70:73], v[164:167], v[216:219], v[70:73]
	v_mfma_f32_16x16x32_bf16 v[66:69], v[172:175], v[216:219], v[66:69]
	s_setprio 0
	s_barrier
	s_add_i32 s54, s54, s40
	v_lshl_add_u64 v[192:193], s[14:15], 0, v[194:195]
	s_mov_b32 m0, s54
	ds_read_b128 v[176:179], v142 offset:16384
	ds_read_b128 v[180:183], v142 offset:17408
	ds_read_b128 v[184:187], v142 offset:18432
	ds_read_b128 v[188:191], v142 offset:19456
	ds_read_b128 v[204:207], v142 offset:20480
	ds_read_b128 v[208:211], v142 offset:21504
	ds_read_b128 v[212:215], v142 offset:22528
	ds_read_b128 v[216:219], v142 offset:23552
	global_load_lds_dwordx4 v[192:193], off
	s_add_i32 m0, s54, 0x2000
	s_add_u32 s54, s14, 0x40000
	v_lshl_add_u64 v[198:199], s[14:15], 0, v[134:135]
	s_addc_u32 s55, s15, 0
	s_add_i32 s58, s58, s40
	global_load_lds_dwordx4 v[198:199], off
	v_lshl_add_u64 v[200:201], s[54:55], 0, v[194:195]
	s_mov_b32 m0, s58
	v_lshl_add_u64 v[220:221], s[30:31], 0, v[130:131]
	global_load_lds_dwordx4 v[200:201], off
	s_add_i32 m0, s58, 0x2000
	v_lshl_add_u64 v[200:201], s[54:55], 0, v[134:135]
	global_load_lds_dwordx4 v[200:201], off
	s_mov_b32 m0, s9
	v_lshl_add_u64 v[200:201], s[30:31], 0, v[132:133]
	global_load_lds_dwordx4 v[200:201], off
	s_mov_b32 m0, s42
	s_nop 0
	global_load_lds_dwordx4 v[220:221], off
	s_waitcnt vmcnt(8)
	s_waitcnt lgkmcnt(0)
	s_barrier
; #define PG8_LDA(dst, b, h) do { _Pragma("unroll") for (int m = 0; m < 4; ++m) _Pragma("unroll") for (int k = 0; k < 2; ++k) dst[m][k] = *(const LAS bf16x8*)(lds + PG8_SA(b, h) + aoff + m * 2048 + k * 1024); } while (0)
; #define PG8_LDB(dst, b, h) do { _Pragma("unroll") for (int n = 0; n < 2; ++n) _Pragma("unroll") for (int k = 0; k < 2; ++k) dst[n][k] = *(const LAS bf16x8*)(lds + PG8_SB(b, h) + boff + n * 2048 + k * 1024); } while (0)
; #define PG8_MMA(ai, bj, At, Bt) do { __builtin_amdgcn_s_setprio(1); _Pragma("unroll") for (int m = 0; m < 4; ++m) _Pragma("unroll") for (int n = 0; n < 2; ++n) _Pragma("unroll") for (int k = 0; k < 2; ++k) \
;         acc[ai][bj][m][n] = __builtin_amdgcn_mfma_f32_16x16x32_bf16(Bt[n][k], At[m][k], acc[ai][bj][m][n], 0, 0, 0); __builtin_amdgcn_s_setprio(0); } while (0)
; #define PG8_WAIT_V(n) asm volatile("s_waitcnt vmcnt(" #n ")" ::: "memory")
; #define PG8_WAIT_L(n) asm volatile("s_waitcnt lgkmcnt(" #n ")" ::: "memory")
; #define PG8_BAR __builtin_amdgcn_s_barrier()
; #define PG8_SCHED __builtin_amdgcn_sched_barrier(0)
; template <class Epi, class Sched, bool GATHER = false>
; __device__ __forceinline__ void gemm_phase(LAS unsigned char* lds, const Gemm g, const Sched& S, const Epi& E) {
;     ...
;             PG8_WAIT_V(8); PG8_WAIT_L(0); PG8_BAR; PG8_MMA(1, 0, At, B0); PG8_MMA(1, 1, At, B1); PG8_BAR; PG8_SCHED;
;             PG8_LDB(B0, 1, 0); PG8_LDB(B1, 1, 1); PG8_SCHED; PG8_LDA(At, 1, 0); PG8_STAGE_A(PG8_SA(0, 1), a2, vo2, 1);
;             PG8_WAIT_V(8); PG8_WAIT_L(0); PG8_BAR; PG8_MMA(0, 0, At, B0); PG8_MMA(0, 1, At, B1); PG8_BAR; PG8_SCHED;
	s_setprio 1
	s_waitcnt lgkmcnt(0)
	v_mfma_f32_16x16x32_bf16 v[62:65], v[144:147], v[176:179], v[62:65]
	v_mfma_f32_16x16x32_bf16 v[58:61], v[152:155], v[176:179], v[58:61]
	v_mfma_f32_16x16x32_bf16 v[54:57], v[144:147], v[184:187], v[54:57]
	v_mfma_f32_16x16x32_bf16 v[50:53], v[152:155], v[184:187], v[50:53]
	v_mfma_f32_16x16x32_bf16 v[38:41], v[144:147], v[204:207], v[38:41]
	v_mfma_f32_16x16x32_bf16 v[34:37], v[152:155], v[204:207], v[34:37]
	v_mfma_f32_16x16x32_bf16 v[22:25], v[144:147], v[212:215], v[22:25]
	v_mfma_f32_16x16x32_bf16 v[18:21], v[152:155], v[212:215], v[18:21]
	v_mfma_f32_16x16x32_bf16 v[62:65], v[148:151], v[180:183], v[62:65]
	v_mfma_f32_16x16x32_bf16 v[58:61], v[156:159], v[180:183], v[58:61]
	v_mfma_f32_16x16x32_bf16 v[54:57], v[148:151], v[188:191], v[54:57]
	v_mfma_f32_16x16x32_bf16 v[50:53], v[156:159], v[188:191], v[50:53]
	v_mfma_f32_16x16x32_bf16 v[38:41], v[148:151], v[208:211], v[38:41]
	v_mfma_f32_16x16x32_bf16 v[34:37], v[156:159], v[208:211], v[34:37]
	v_mfma_f32_16x16x32_bf16 v[22:25], v[148:151], v[216:219], v[22:25]
	v_mfma_f32_16x16x32_bf16 v[18:21], v[156:159], v[216:219], v[18:21]
	s_setprio 0
	s_setprio 1
	v_mfma_f32_16x16x32_bf16 v[46:49], v[160:163], v[176:179], v[46:49]
	v_mfma_f32_16x16x32_bf16 v[42:45], v[168:171], v[176:179], v[42:45]
	v_mfma_f32_16x16x32_bf16 v[30:33], v[160:163], v[184:187], v[30:33]
	v_mfma_f32_16x16x32_bf16 v[26:29], v[168:171], v[184:187], v[26:29]
	v_mfma_f32_16x16x32_bf16 v[14:17], v[160:163], v[204:207], v[14:17]
	v_mfma_f32_16x16x32_bf16 v[10:13], v[168:171], v[204:207], v[10:13]
	v_mfma_f32_16x16x32_bf16 v[6:9], v[160:163], v[212:215], v[6:9]
	v_mfma_f32_16x16x32_bf16 v[2:5], v[168:171], v[212:215], v[2:5]
	v_mfma_f32_16x16x32_bf16 v[46:49], v[164:167], v[180:183], v[46:49]
	v_mfma_f32_16x16x32_bf16 v[42:45], v[172:175], v[180:183], v[42:45]
	v_mfma_f32_16x16x32_bf16 v[30:33], v[164:167], v[188:191], v[30:33]
	v_mfma_f32_16x16x32_bf16 v[26:29], v[172:175], v[188:191], v[26:29]
	v_mfma_f32_16x16x32_bf16 v[14:17], v[164:167], v[208:211], v[14:17]
	v_mfma_f32_16x16x32_bf16 v[10:13], v[172:175], v[208:211], v[10:13]
	v_mfma_f32_16x16x32_bf16 v[6:9], v[164:167], v[216:219], v[6:9]
	v_mfma_f32_16x16x32_bf16 v[2:5], v[172:175], v[216:219], v[2:5]
	s_setprio 0
	s_barrier
	s_add_i32 s54, 0, 0x18000
	v_add_u32_e32 v143, s54, v140
	s_add_i32 s55, 0, 0x1c000
	ds_read_b128 v[144:147], v143
	ds_read_b128 v[148:151], v143 offset:1024
	ds_read_b128 v[152:155], v143 offset:2048
	ds_read_b128 v[156:159], v143 offset:3072
	v_add_u32_e32 v143, s55, v140
	ds_read_b128 v[160:163], v143
	ds_read_b128 v[164:167], v143 offset:1024
	ds_read_b128 v[168:171], v143 offset:2048
	ds_read_b128 v[172:175], v143 offset:3072
	s_add_u32 s30, s30, 0x40000
	s_addc_u32 s31, s31, 0
	s_mov_b32 m0, s43
	v_lshl_add_u64 v[222:223], s[30:31], 0, v[132:133]
	ds_read_b128 v[176:179], v142 offset:32768
	ds_read_b128 v[180:183], v142 offset:33792
	ds_read_b128 v[184:187], v142 offset:34816
	ds_read_b128 v[188:191], v142 offset:35840
	ds_read_b128 v[204:207], v142 offset:36864
	ds_read_b128 v[208:211], v142 offset:37888
	ds_read_b128 v[212:215], v142 offset:38912
	ds_read_b128 v[216:219], v142 offset:39936
	global_load_lds_dwordx4 v[222:223], off
	s_mov_b32 m0, s44
	v_lshl_add_u64 v[222:223], s[30:31], 0, v[130:131]
	global_load_lds_dwordx4 v[222:223], off
	s_waitcnt vmcnt(8)
	s_waitcnt lgkmcnt(0)
	s_barrier
	s_setprio 1
	s_waitcnt lgkmcnt(0)
	v_mfma_f32_16x16x32_bf16 v[126:129], v[144:147], v[176:179], v[126:129]
	v_mfma_f32_16x16x32_bf16 v[122:125], v[152:155], v[176:179], v[122:125]
	v_mfma_f32_16x16x32_bf16 v[118:121], v[144:147], v[184:187], v[118:121]
	v_mfma_f32_16x16x32_bf16 v[114:117], v[152:155], v[184:187], v[114:117]
	v_mfma_f32_16x16x32_bf16 v[102:105], v[144:147], v[204:207], v[102:105]
	v_mfma_f32_16x16x32_bf16 v[98:101], v[152:155], v[204:207], v[98:101]
	v_mfma_f32_16x16x32_bf16 v[86:89], v[144:147], v[212:215], v[86:89]
	v_mfma_f32_16x16x32_bf16 v[82:85], v[152:155], v[212:215], v[82:85]
	v_mfma_f32_16x16x32_bf16 v[126:129], v[148:151], v[180:183], v[126:129]
	v_mfma_f32_16x16x32_bf16 v[122:125], v[156:159], v[180:183], v[122:125]
	v_mfma_f32_16x16x32_bf16 v[118:121], v[148:151], v[188:191], v[118:121]
	v_mfma_f32_16x16x32_bf16 v[114:117], v[156:159], v[188:191], v[114:117]
	v_mfma_f32_16x16x32_bf16 v[102:105], v[148:151], v[208:211], v[102:105]
	v_mfma_f32_16x16x32_bf16 v[98:101], v[156:159], v[208:211], v[98:101]
	v_mfma_f32_16x16x32_bf16 v[86:89], v[148:151], v[216:219], v[86:89]
	v_mfma_f32_16x16x32_bf16 v[82:85], v[156:159], v[216:219], v[82:85]
	s_setprio 0
	s_setprio 1
	v_mfma_f32_16x16x32_bf16 v[110:113], v[160:163], v[176:179], v[110:113]
	v_mfma_f32_16x16x32_bf16 v[106:109], v[168:171], v[176:179], v[106:109]
	v_mfma_f32_16x16x32_bf16 v[94:97], v[160:163], v[184:187], v[94:97]
	v_mfma_f32_16x16x32_bf16 v[90:93], v[168:171], v[184:187], v[90:93]
	v_mfma_f32_16x16x32_bf16 v[78:81], v[160:163], v[204:207], v[78:81]
	v_mfma_f32_16x16x32_bf16 v[74:77], v[168:171], v[204:207], v[74:77]
	v_mfma_f32_16x16x32_bf16 v[70:73], v[160:163], v[212:215], v[70:73]
	v_mfma_f32_16x16x32_bf16 v[66:69], v[168:171], v[212:215], v[66:69]
	v_mfma_f32_16x16x32_bf16 v[110:113], v[164:167], v[180:183], v[110:113]
	v_mfma_f32_16x16x32_bf16 v[106:109], v[172:175], v[180:183], v[106:109]
	v_mfma_f32_16x16x32_bf16 v[94:97], v[164:167], v[188:191], v[94:97]
	v_mfma_f32_16x16x32_bf16 v[90:93], v[172:175], v[188:191], v[90:93]
	v_mfma_f32_16x16x32_bf16 v[78:81], v[164:167], v[208:211], v[78:81]
	v_mfma_f32_16x16x32_bf16 v[74:77], v[172:175], v[208:211], v[74:77]
	v_mfma_f32_16x16x32_bf16 v[70:73], v[164:167], v[216:219], v[70:73]
	v_mfma_f32_16x16x32_bf16 v[66:69], v[172:175], v[216:219], v[66:69]
	s_setprio 0
	s_barrier
; #define PG8_STAGE_B(bufoff, gbase) do { _Pragma("unroll") for (int _i = 0; _i < 2; ++_i) \
;         __builtin_amdgcn_global_load_lds((const unsigned*)((const char*)(gbase) + voffB[_i]), (LAS unsigned*)(lds + (bufoff) + ldsw + _i * 8192), 16, 0, 0); } while (0)
; #define PG8_LDA(dst, b, h) do { _Pragma("unroll") for (int m = 0; m < 4; ++m) _Pragma("unroll") for (int k = 0; k < 2; ++k) dst[m][k] = *(const LAS bf16x8*)(lds + PG8_SA(b, h) + aoff + m * 2048 + k * 1024); } while (0)
; #define PG8_MMA(ai, bj, At, Bt) do { __builtin_amdgcn_s_setprio(1); _Pragma("unroll") for (int m = 0; m < 4; ++m) _Pragma("unroll") for (int n = 0; n < 2; ++n) _Pragma("unroll") for (int k = 0; k < 2; ++k) \
;         acc[ai][bj][m][n] = __builtin_amdgcn_mfma_f32_16x16x32_bf16(Bt[n][k], At[m][k], acc[ai][bj][m][n], 0, 0, 0); __builtin_amdgcn_s_setprio(0); } while (0)
; #define PG8_WAIT_V(n) asm volatile("s_waitcnt vmcnt(" #n ")" ::: "memory")
; #define PG8_WAIT_L(n) asm volatile("s_waitcnt lgkmcnt(" #n ")" ::: "memory")
; #define PG8_BAR __builtin_amdgcn_s_barrier()
; #define PG8_SCHED __builtin_amdgcn_sched_barrier(0)
; template <class Epi, class Sched, bool GATHER = false>
; __device__ __forceinline__ void gemm_phase(LAS unsigned char* lds, const Gemm g, const Sched& S, const Epi& E) {
;     ...
;             PG8_LDA(At, 1, 1); PG8_STAGE_B(PG8_SB(1, 0), b3); PG8_STAGE_B(PG8_SB(1, 1), b3 + hstepB); PG8_STAGE_A(PG8_SA(1, 0), a3, vo2, 0);
;             PG8_WAIT_V(8); PG8_WAIT_L(0); PG8_BAR; PG8_MMA(1, 0, At, B0); PG8_MMA(1, 1, At, B1); PG8_BAR; PG8_SCHED;
;         }
	s_add_i32 s30, s54, s40
	v_lshl_add_u64 v[192:193], v[192:193], 0, s[66:67]
	s_mov_b32 m0, s30
	ds_read_b128 v[176:179], v142 offset:49152
	ds_read_b128 v[180:183], v142 offset:50176
	ds_read_b128 v[184:187], v142 offset:51200
	ds_read_b128 v[188:191], v142 offset:52224
	ds_read_b128 v[204:207], v142 offset:53248
	ds_read_b128 v[208:211], v142 offset:54272
	ds_read_b128 v[212:215], v142 offset:55296
	ds_read_b128 v[216:219], v142 offset:56320
	global_load_lds_dwordx4 v[192:193], off
	s_add_i32 m0, s30, 0x2000
	s_add_u32 s14, s14, 0x40080
	v_lshl_add_u64 v[192:193], v[198:199], 0, s[66:67]
	s_addc_u32 s15, s15, 0
	s_add_i32 s30, s55, s40
	global_load_lds_dwordx4 v[192:193], off
	s_mov_b32 m0, s30
	v_lshl_add_u64 v[192:193], s[14:15], 0, v[194:195]
	global_load_lds_dwordx4 v[192:193], off
	s_add_i32 m0, s30, 0x2000
	v_lshl_add_u64 v[192:193], s[14:15], 0, v[134:135]
	global_load_lds_dwordx4 v[192:193], off
	s_mov_b32 m0, s45
	v_lshl_add_u64 v[192:193], v[200:201], 0, s[66:67]
	global_load_lds_dwordx4 v[192:193], off
	s_mov_b32 m0, s46
	v_lshl_add_u64 v[192:193], v[220:221], 0, s[66:67]
	global_load_lds_dwordx4 v[192:193], off
	s_waitcnt vmcnt(8)
	s_waitcnt lgkmcnt(0)
	s_barrier
	s_setprio 1
	s_waitcnt lgkmcnt(0)
	v_mfma_f32_16x16x32_bf16 v[62:65], v[144:147], v[176:179], v[62:65]
	v_mfma_f32_16x16x32_bf16 v[58:61], v[152:155], v[176:179], v[58:61]
	v_mfma_f32_16x16x32_bf16 v[54:57], v[144:147], v[184:187], v[54:57]
	v_mfma_f32_16x16x32_bf16 v[50:53], v[152:155], v[184:187], v[50:53]
	v_mfma_f32_16x16x32_bf16 v[38:41], v[144:147], v[204:207], v[38:41]
	v_mfma_f32_16x16x32_bf16 v[34:37], v[152:155], v[204:207], v[34:37]
	v_mfma_f32_16x16x32_bf16 v[22:25], v[144:147], v[212:215], v[22:25]
	v_mfma_f32_16x16x32_bf16 v[18:21], v[152:155], v[212:215], v[18:21]
	v_mfma_f32_16x16x32_bf16 v[62:65], v[148:151], v[180:183], v[62:65]
	v_mfma_f32_16x16x32_bf16 v[58:61], v[156:159], v[180:183], v[58:61]
	v_mfma_f32_16x16x32_bf16 v[54:57], v[148:151], v[188:191], v[54:57]
	v_mfma_f32_16x16x32_bf16 v[50:53], v[156:159], v[188:191], v[50:53]
	v_mfma_f32_16x16x32_bf16 v[38:41], v[148:151], v[208:211], v[38:41]
	v_mfma_f32_16x16x32_bf16 v[34:37], v[156:159], v[208:211], v[34:37]
	v_mfma_f32_16x16x32_bf16 v[22:25], v[148:151], v[216:219], v[22:25]
	v_mfma_f32_16x16x32_bf16 v[18:21], v[156:159], v[216:219], v[18:21]
	s_setprio 0
	s_setprio 1
	v_mfma_f32_16x16x32_bf16 v[46:49], v[160:163], v[176:179], v[46:49]
	v_mfma_f32_16x16x32_bf16 v[42:45], v[168:171], v[176:179], v[42:45]
	v_mfma_f32_16x16x32_bf16 v[30:33], v[160:163], v[184:187], v[30:33]
	v_mfma_f32_16x16x32_bf16 v[26:29], v[168:171], v[184:187], v[26:29]
	v_mfma_f32_16x16x32_bf16 v[14:17], v[160:163], v[204:207], v[14:17]
	v_mfma_f32_16x16x32_bf16 v[10:13], v[168:171], v[204:207], v[10:13]
	v_mfma_f32_16x16x32_bf16 v[6:9], v[160:163], v[212:215], v[6:9]
	v_mfma_f32_16x16x32_bf16 v[2:5], v[168:171], v[212:215], v[2:5]
	v_mfma_f32_16x16x32_bf16 v[46:49], v[164:167], v[180:183], v[46:49]
	v_mfma_f32_16x16x32_bf16 v[42:45], v[172:175], v[180:183], v[42:45]
	v_mfma_f32_16x16x32_bf16 v[30:33], v[164:167], v[188:191], v[30:33]
	v_mfma_f32_16x16x32_bf16 v[26:29], v[172:175], v[188:191], v[26:29]
	v_mfma_f32_16x16x32_bf16 v[14:17], v[164:167], v[208:211], v[14:17]
	v_mfma_f32_16x16x32_bf16 v[10:13], v[172:175], v[208:211], v[10:13]
	v_mfma_f32_16x16x32_bf16 v[6:9], v[164:167], v[216:219], v[6:9]
	v_mfma_f32_16x16x32_bf16 v[2:5], v[172:175], v[216:219], v[2:5]
	s_setprio 0
	s_barrier
	s_add_i32 s53, s53, 2
	s_add_u32 s36, s36, 0x100
	s_addc_u32 s37, s37, 0
	s_add_u32 s51, s51, 0x100
	s_addc_u32 s52, s52, 0
	s_cmp_gt_u32 s53, 13
	s_cbranch_scc0 .LBB0_749
	s_and_b64 vcc, exec, s[20:21]
	s_cbranch_vccz .LBB0_752
	s_barrier

; template <int DQK, int DV, bool LEAD> ...
;     ...
;     const int tid = tid_, lane = tid & 63, q16 = lane & 15, g4 = lane >> 4, hi = lane >> 5; const int wid = __builtin_amdgcn_readfirstlane(tid >> 6);
;     const int kg = KS ? (wid >> 2) : 0, qoff = KS ? (wid & 3) * 64 : wid * 32;
;     const unsigned lds0 = (unsigned)(uintptr_t)shm;
;     const int krow_l = wid * 8 + (lane >> 3);
;     const int kc_l = (lane & 7) ^ (((krow_l >> 1) & 1) | (((krow_l >> 3) & 1) << 1) | (((krow_l >> 4) & 1) << 2));
;     const int vc_l = (lane & 7) ^ ((krow_l >> 1) & 7);
;     const bf16_t* ksrc = K + (size_t)(krow0 + krow_l) * kpitch + kc_l * 8;
;     const int rrow_l = (wid & 3) * 16 + (lane >> 2), rc_l = (lane & 3) ^ (((rrow_l >> 4) & 1) << 1);
;     const bf16_t* krsrc = (DQK == 96) ? KR + (size_t)(krow0 + rrow_l) * 32 + rc_l * 8 : nullptr;
;     const bf16_t* vsrc = Vt + (size_t)krow_l * NR + krow0 + vc_l * 8;
;     const unsigned kdst = lds0 + KOFF + wid * 1024, krdst = lds0 + KOFF + 8192 + (wid & 3) * 1024, vdst = lds0 + VOFF + wid * 1024;
;     ...
;     ATT_DMA_K(0, 0); ATT_DMA_V(0, 0); ATT_DMA_K(1, 1); ATT_DMA_K(2, 2);
;     bf16x8 qf[NQB * NDS];
;     {
;       const float c2 = (DQK == 64) ? C2_EVEN : C2_ODD; const bool lat = tq0 >= 0;
; #pragma unroll
;       for (int qb = 0; qb < NQB; ++qb) {
;           const bf16_t* qp = Q + (size_t)(qrow0 + qoff + qb * 16 + q16) * qpitch + g4 * 8;
;           bf16x8 raw[NDS];
; #pragma unroll
;           for (int ds = 0; ds < NDS; ++ds) raw[ds] = *(const bf16x8*)(qp + ds * 32);
;           float x[NDS][8];
; #pragma unroll
;           for (int ds = 0; ds < NDS; ++ds)
; #pragma unroll
;               for (int j = 0; j < 8; ++j) x[ds][j] = __uint_as_float(((unsigned)(unsigned short)raw[ds][j]) << 16);
;           const int tq = tq0 + qoff + qb * 16 + q16, prow = (tq >> 6) & 127, pcol = tq & 63;
;           float sn = 0.f;
; #pragma unroll
;           for (int ds = 0; ds < 2; ++ds)
; #pragma unroll
;               for (int j = 0; j < 8; ++j) sn += x[ds][j] * x[ds][j];
;           sn = lanes4_sum(sn);
;           const float rn = rsqrtf(sn * (1.f / 64.f) + EPS);
; #pragma unroll
;           for (int ds = 0; ds < 2; ++ds)
; #pragma unroll
;               for (int j = 0; j < 8; ++j) x[ds][j] *= rn * qgain[32 * ds + 8 * g4 + j];
;           if constexpr (DQK == 64) {
; #pragma unroll
;               for (int ds = 0; ds < 2; ++ds)
; #pragma unroll
.LBB0_939:
	s_lshl_b32 s6, s4, 1
	s_and_b32 s6, s6, 0x180
	s_lshr_b32 s5, s4, 8
	s_lshl_b32 s7, s6, 1
	s_add_u32 s16, s18, s7
	s_addc_u32 s22, s19, 0
	s_lshl_b32 s23, s4, 2
	s_and_b32 s23, s23, 0x80
	s_add_u32 s36, s16, s23
	s_addc_u32 s37, s22, 0
	s_add_u32 s7, s15, s7
	s_addc_u32 s16, s17, 0
	s_add_u32 s40, s7, s23
	s_addc_u32 s41, s16, 0
	s_mul_i32 s6, s6, 0x21000
	s_add_u32 s44, s10, s6
	s_addc_u32 s45, s11, 0
	s_lshl_b32 s6, s4, 3
	s_and_b32 s6, s6, 0x700
	s_add_u32 s26, s3, s6
	s_mov_b64 s[6:7], s[0:1]
	s_load_dwordx2 s[6:7], s[6:7], 0x48
	s_addc_u32 s27, s14, 0
	s_lshl_b32 s25, s4, 8
	s_mul_i32 s46, s5, 0x2100
	s_and_b32 s4, s25, 0x1f00
	s_add_i32 s30, s46, s4
	s_lshl_b64 s[22:23], s[20:21], 2
	s_waitcnt lgkmcnt(0)
	s_add_u32 s28, s6, s22
	s_addc_u32 s29, s7, s23
	v_readfirstlane_b32 s4, v0
	s_cmpk_gt_u32 s4, 0xff
	s_mov_b64 s[4:5], -1
	s_cbranch_scc0 .LBB0_946
	v_mov_b32_e32 v79, v0
	s_ashr_i32 s47, s46, 31
	v_readfirstlane_b32 s4, v79
	s_ashr_i32 s42, s4, 6
	v_bfe_u32 v1, v79, 3, 3
	v_lshl_or_b32 v6, s42, 3, v1
	s_lshl_b32 s5, s42, 1
	s_lshr_b32 s4, s4, 5
	v_ashrrev_i32_e32 v2, 1, v6
	s_and_b32 s5, s5, 2
	s_and_b32 s4, s4, 4
	v_and_b32_e32 v203, 7, v79
	v_and_b32_e32 v3, 1, v2
	s_or_b32 s4, s5, s4
	v_bitop3_b32 v7, s4, v203, v3 bitop3:0x36
	v_xor_b32_e32 v8, v2, v79
	v_add_u32_e32 v4, s46, v6
	v_mov_b64_e32 v[2:3], s[40:41]
	v_mad_i64_i32 v[2:3], s[4:5], v4, s92, v[2:3]
	v_mov_b64_e32 v[4:5], s[44:45]
	v_lshlrev_b32_e32 v194, 4, v7
	s_lshl_b32 s43, s42, 10
	v_mad_i64_i32 v[4:5], s[4:5], v6, s91, v[4:5]
	v_lshl_add_u64 v[204:205], v[2:3], 0, v[194:195]
	v_lshlrev_b32_e32 v2, 4, v8
	s_add_i32 s43, s43, 0
	v_lshl_add_u64 v[4:5], s[46:47], 1, v[4:5]
	v_and_b32_e32 v194, 0x70, v2
	s_mov_b32 m0, s43
	s_nop 0
	global_load_lds_dwordx4 v[204:205], off
	v_lshl_add_u64 v[206:207], v[4:5], 0, v[194:195]
	s_add_i32 s16, s43, 0x9000
	s_mov_b32 m0, s16
	s_nop 0
	global_load_lds_dwordx4 v[206:207], off
	s_mov_b64 s[4:5], 0x840000
	v_lshl_add_u64 v[208:209], v[206:207], 0, s[4:5]
	s_add_i32 s4, s16, 0x2000
	s_mov_b32 m0, s4
	s_nop 0
	global_load_lds_dwordx4 v[208:209], off
	s_mov_b64 s[4:5], 0x38000
	v_lshl_add_u64 v[2:3], v[204:205], 0, s[4:5]
	s_add_i32 s4, s43, 0x2000
	s_mov_b32 m0, s4
	s_nop 0
	global_load_lds_dwordx4 v[2:3], off
	s_lshl_b32 s6, s42, 5
	s_mov_b64 s[4:5], 0x70000
	v_and_b32_e32 v78, 15, v79
	v_lshl_add_u64 v[2:3], v[204:205], 0, s[4:5]
	s_add_i32 s31, s6, s30
	v_and_b32_e32 v194, 48, v79
	s_add_i32 s4, s43, 0x4000
	s_mov_b32 m0, s4
	s_nop 0
	global_load_lds_dwordx4 v[2:3], off
	v_or_b32_e32 v4, s31, v78
	v_lshl_add_u64 v[2:3], s[36:37], 0, v[194:195]
	v_lshrrev_b32_e32 v38, 1, v79
	v_or_b32_e32 v5, s6, v78
	v_mad_i64_i32 v[26:27], s[4:5], v4, s92, v[2:3]
	v_and_b32_e32 v28, 8, v38
	v_lshlrev_b32_e32 v5, 4, v5
	s_movk_i32 s4, 0x2f0
	v_or_b32_e32 v4, 16, v4
	v_and_or_b32 v5, v5, s4, v28
	v_mad_i64_i32 v[30:31], s[4:5], v4, s92, v[2:3]
	s_add_i32 s6, s6, s25
	s_lshr_b32 s4, s6, 2
	v_lshlrev_b32_e32 v22, 3, v5
	s_and_b32 s4, s4, 0x7f0
	global_load_dwordx4 v[50:53], v[26:27], off offset:64
	global_load_dwordx4 v[60:63], v22, s[8:9] offset:48
	global_load_dwordx4 v[70:73], v[30:31], off offset:64
	global_load_dwordx4 v[6:9], v22, s[8:9] offset:2096
	global_load_dwordx4 v[54:57], v22, s[8:9] offset:32
	global_load_dwordx4 v[14:17], v22, s[8:9] offset:2080
	global_load_dwordx4 v[2:5], v22, s[8:9] offset:16
	global_load_dwordx4 v[18:21], v22, s[8:9] offset:2064
	global_load_dwordx4 v[10:13], v22, s[8:9]
	s_nop 0
	global_load_dwordx4 v[22:25], v22, s[8:9] offset:2048
	s_nop 0
	global_load_dwordx4 v[82:85], v[26:27], off
	v_or_b32_e32 v26, s4, v28
	v_lshlrev_b32_e32 v39, 3, v26
	global_load_dwordx4 v[26:29], v39, s[8:9] offset:48
	global_load_dwordx4 v[86:89], v[30:31], off
	s_nop 0
	global_load_dwordx4 v[30:33], v39, s[8:9] offset:32
	global_load_dwordx4 v[34:37], v39, s[8:9] offset:16
	v_bfe_u32 v214, v79, 4, 2
	v_lshlrev_b32_e32 v215, 1, v79
	v_and_b32_e32 v40, 3, v79
	v_and_or_b32 v40, v215, 24, v40
	v_bitop3_b32 v38, v214, v38, 7 bitop3:0x78
	v_lshlrev_b32_e32 v59, 5, v214
	v_lshl_add_u32 v81, v40, 7, 0
	v_lshlrev_b32_e32 v80, 4, v38
	global_load_dwordx4 v[38:41], v39, s[8:9]
	s_nop 0
	global_load_dwordx4 v[42:45], v59, s[28:29] offset:144
	global_load_dwordx4 v[46:49], v59, s[28:29] offset:128
	v_and_b32_e32 v58, 63, v79
	v_cmp_gt_u32_e32 vcc, 32, v58
	s_mov_b32 s4, 0x3c800000
	v_add_u32_e32 v194, v81, v80
	v_lshlrev_b32_e32 v217, 7, v78
	s_mov_b32 s47, 1
	s_mov_b32 s48, 2
	v_or_b32_e32 v216, 4, v214
	s_waitcnt vmcnt(15)
	v_and_b32_e32 v65, 0xffff0000, v73
	v_lshlrev_b32_e32 v64, 16, v73
	v_and_b32_e32 v67, 0xffff0000, v72
	v_lshlrev_b32_e32 v66, 16, v72
	s_waitcnt vmcnt(13)
	v_cndmask_b32_e64 v95, v57, -v57, vcc
	v_cndmask_b32_e64 v94, v55, -v55, vcc
	v_and_b32_e32 v91, 0xffff0000, v53
	v_lshlrev_b32_e32 v90, 16, v53
	v_and_b32_e32 v93, 0xffff0000, v52
	s_waitcnt vmcnt(5)
; template <int DQK, int DV, bool LEAD> ...
;     ...
;           const bf16_t* qp = Q + (size_t)(qrow0 + qoff + qb * 16 + q16) * qpitch + g4 * 8;
;           bf16x8 raw[NDS];
; #pragma unroll
;           for (int ds = 0; ds < NDS; ++ds) raw[ds] = *(const bf16x8*)(qp + ds * 32);
;           float x[NDS][8];
; #pragma unroll
;           for (int ds = 0; ds < NDS; ++ds)
; #pragma unroll
;               for (int j = 0; j < 8; ++j) x[ds][j] = __uint_as_float(((unsigned)(unsigned short)raw[ds][j]) << 16);
;           const int tq = tq0 + qoff + qb * 16 + q16, prow = (tq >> 6) & 127, pcol = tq & 63;
;           float sn = 0.f;
; #pragma unroll
;           for (int ds = 0; ds < 2; ++ds)
; #pragma unroll
;               for (int j = 0; j < 8; ++j) sn += x[ds][j] * x[ds][j];
;           sn = lanes4_sum(sn);
;           const float rn = rsqrtf(sn * (1.f / 64.f) + EPS);
; #pragma unroll
;           for (int ds = 0; ds < 2; ++ds)
; #pragma unroll
;               for (int j = 0; j < 8; ++j) x[ds][j] *= rn * qgain[32 * ds + 8 * g4 + j];
;           if constexpr (DQK == 64) {
; #pragma unroll
;               for (int ds = 0; ds < 2; ++ds)
; #pragma unroll
;                   for (int j = 0; j < 8; ++j) {
;                       auto rr = __builtin_amdgcn_permlane32_swap(__float_as_uint(x[ds][j]), __float_as_uint(x[ds][j]), false, false);
;                       const float other = hi ? __uint_as_float(rr[0]) : __uint_as_float(rr[1]);
;                       float cc = 1.f, sg = 0.f;
;                       if (lat) { const f32x2 cs = rope[(ds ? pcol : prow) * 16 + 8 * (g4 & 1) + j]; cc = cs.x; sg = hi ? cs.y : -cs.y; }
;                       x[ds][j] = x[ds][j] * cc + other * sg; }
	v_and_b32_e32 v73, 0xffff0000, v89
	v_lshlrev_b32_e32 v72, 16, v89
	v_and_b32_e32 v75, 0xffff0000, v88
	v_lshlrev_b32_e32 v74, 16, v88
	v_and_b32_e32 v89, 0xffff0000, v83
	v_lshlrev_b32_e32 v88, 16, v83
	v_and_b32_e32 v83, 0xffff0000, v82
	v_lshlrev_b32_e32 v92, 16, v52
	v_mov_b32_e32 v55, v56
	v_and_b32_e32 v97, 0xffff0000, v51
	v_lshlrev_b32_e32 v96, 16, v51
	v_cndmask_b32_e64 v98, v3, -v3, vcc
	v_mov_b32_e32 v3, v4
	v_and_b32_e32 v101, 0xffff0000, v50
	v_lshlrev_b32_e32 v100, 16, v50
	global_load_dwordx4 v[50:53], v59, s[28:29] offset:16
	s_nop 0
	global_load_dwordx4 v[56:59], v59, s[28:29]
	v_lshlrev_b32_e32 v82, 16, v82
	v_mul_f32_e32 v4, v83, v83
	v_cndmask_b32_e64 v99, v5, -v5, vcc
	v_pk_fma_f32 v[4:5], v[82:83], v[82:83], v[4:5] op_sel_hi:[1,1,0]
	v_mul_f32_e32 v104, v89, v89
	v_pk_fma_f32 v[4:5], v[88:89], v[88:89], v[4:5]
	v_cndmask_b32_e64 v103, v13, -v13, vcc
	v_cndmask_b32_e64 v102, v11, -v11, vcc
	v_mov_b32_e32 v11, v12
	v_and_b32_e32 v13, 0xffff0000, v85
	v_lshlrev_b32_e32 v12, 16, v85
	v_and_b32_e32 v85, 0xffff0000, v84
	v_lshlrev_b32_e32 v84, 16, v84
	v_pk_add_f32 v[4:5], v[104:105], v[4:5] op_sel_hi:[0,1]
	v_pk_fma_f32 v[4:5], v[84:85], v[84:85], v[4:5]
	v_mul_f32_e32 v104, v85, v85
	v_pk_add_f32 v[4:5], v[104:105], v[4:5] op_sel_hi:[0,1]
	v_pk_fma_f32 v[4:5], v[12:13], v[12:13], v[4:5]
	v_mul_f32_e32 v104, v13, v13
	v_pk_add_f32 v[4:5], v[104:105], v[4:5] op_sel_hi:[0,1]
	v_pk_fma_f32 v[4:5], v[100:101], v[100:101], v[4:5]
	v_mul_f32_e32 v104, v101, v101
	v_pk_add_f32 v[4:5], v[104:105], v[4:5] op_sel_hi:[0,1]
	v_pk_fma_f32 v[4:5], v[96:97], v[96:97], v[4:5]
	v_mul_f32_e32 v104, v97, v97
	v_pk_add_f32 v[4:5], v[104:105], v[4:5] op_sel_hi:[0,1]
	v_pk_fma_f32 v[4:5], v[92:93], v[92:93], v[4:5]
	v_mul_f32_e32 v104, v93, v93
	v_pk_add_f32 v[4:5], v[104:105], v[4:5] op_sel_hi:[0,1]
	v_pk_fma_f32 v[4:5], v[90:91], v[90:91], v[4:5]
	v_mul_f32_e32 v104, v91, v91
	v_pk_add_f32 v[4:5], v[104:105], v[4:5] op_sel_hi:[0,1]
	v_mov_b32_e32 v5, v4
	s_nop 1
	v_permlane16_swap_b32_e32 v4, v5
	v_add_f32_e32 v5, v4, v5
	v_cndmask_b32_e64 v77, v63, -v63, vcc
	v_cndmask_b32_e64 v76, v61, -v61, vcc
	v_mov_b32_e32 v61, v62
	v_cndmask_b32_e64 v63, v9, -v9, vcc
	v_cndmask_b32_e64 v62, v7, -v7, vcc
	v_mov_b32_e32 v7, v8
	v_cndmask_b32_e64 v9, v17, -v17, vcc
	v_cndmask_b32_e64 v8, v15, -v15, vcc
	v_mov_b32_e32 v15, v16
	v_cndmask_b32_e64 v17, v21, -v21, vcc
	v_cndmask_b32_e64 v16, v19, -v19, vcc
	v_mov_b32_e32 v19, v20
	v_cndmask_b32_e64 v21, v25, -v25, vcc
	v_cndmask_b32_e64 v20, v23, -v23, vcc
	v_mov_b32_e32 v23, v24
	v_cndmask_b32_e64 v25, v29, -v29, vcc
	v_cndmask_b32_e64 v24, v27, -v27, vcc
	v_mov_b32_e32 v27, v28
	s_waitcnt vmcnt(6)
	v_cndmask_b32_e64 v29, v33, -v33, vcc
	v_cndmask_b32_e64 v28, v31, -v31, vcc
	v_mov_b32_e32 v31, v32
	s_waitcnt vmcnt(5)
	v_cndmask_b32_e64 v33, v37, -v37, vcc
	v_cndmask_b32_e64 v32, v35, -v35, vcc
	v_mov_b32_e32 v35, v36
	v_and_b32_e32 v37, 0xffff0000, v87
	v_lshlrev_b32_e32 v36, 16, v87
	v_mov_b32_e32 v87, v5
	v_and_b32_e32 v105, 0xffff0000, v86
	s_nop 0
	v_permlane32_swap_b32_e32 v5, v87
	v_lshlrev_b32_e32 v104, 16, v86
	v_mul_f32_e32 v4, v105, v105
	v_pk_fma_f32 v[106:107], v[104:105], v[104:105], v[4:5] op_sel_hi:[1,1,0]
	v_mul_f32_e32 v4, v37, v37
	v_pk_fma_f32 v[106:107], v[36:37], v[36:37], v[106:107]
	v_and_b32_e32 v69, 0xffff0000, v71
	v_pk_add_f32 v[106:107], v[4:5], v[106:107] op_sel_hi:[0,1]
	v_pk_fma_f32 v[106:107], v[74:75], v[74:75], v[106:107]
	v_mul_f32_e32 v4, v75, v75
	v_pk_add_f32 v[106:107], v[4:5], v[106:107] op_sel_hi:[0,1]
	v_pk_fma_f32 v[106:107], v[72:73], v[72:73], v[106:107]
	v_mul_f32_e32 v4, v73, v73
	v_lshlrev_b32_e32 v68, 16, v71
	v_and_b32_e32 v71, 0xffff0000, v70
	v_lshlrev_b32_e32 v70, 16, v70
	v_pk_add_f32 v[106:107], v[4:5], v[106:107] op_sel_hi:[0,1]
	v_pk_fma_f32 v[106:107], v[70:71], v[70:71], v[106:107]
	v_mul_f32_e32 v4, v71, v71
	v_pk_add_f32 v[106:107], v[4:5], v[106:107] op_sel_hi:[0,1]
	v_pk_fma_f32 v[106:107], v[68:69], v[68:69], v[106:107]
	v_mul_f32_e32 v4, v69, v69
	v_pk_add_f32 v[106:107], v[4:5], v[106:107] op_sel_hi:[0,1]
	v_pk_fma_f32 v[106:107], v[66:67], v[66:67], v[106:107]
	v_mul_f32_e32 v4, v67, v67
	v_pk_add_f32 v[106:107], v[4:5], v[106:107] op_sel_hi:[0,1]
	v_pk_fma_f32 v[106:107], v[64:65], v[64:65], v[106:107]
	v_mul_f32_e32 v4, v65, v65
	v_pk_add_f32 v[106:107], v[4:5], v[106:107] op_sel_hi:[0,1]
	v_mov_b32_e32 v4, v106
	s_nop 1
	v_permlane16_swap_b32_e32 v106, v4
	v_add_f32_e32 v4, v106, v4
	v_mov_b32_e32 v86, v4
	s_nop 1
	v_permlane32_swap_b32_e32 v4, v86
	v_pk_add_f32 v[4:5], v[4:5], v[86:87]
	s_waitcnt vmcnt(4)
	v_cndmask_b32_e64 v106, v39, -v39, vcc
	v_pk_fma_f32 v[86:87], v[4:5], s[4:5], v[196:197] op_sel_hi:[1,0,0]
	v_mov_b32_e32 v39, v40
	v_mul_f32_e32 v4, 0x4b800000, v87
	v_cmp_gt_f32_e64 s[4:5], s95, v87
	v_cndmask_b32_e64 v107, v41, -v41, vcc
	s_nop 0
	v_cndmask_b32_e64 v4, v87, v4, s[4:5]
	v_rsq_f32_e32 v4, v4
	s_nop 0
	v_mul_f32_e32 v5, 0x45800000, v4
	v_cndmask_b32_e64 v40, v4, v5, s[4:5]
	s_waitcnt vmcnt(3)
	v_pk_mul_f32 v[4:5], v[40:41], v[44:45] op_sel_hi:[0,1]
	v_pk_mul_f32 v[4:5], v[4:5], v[90:91]
	v_cmp_gt_f32_e64 s[4:5], s95, v86
	v_mov_b32_e32 v41, v4
	v_mov_b32_e32 v87, v4
	v_mov_b32_e32 v90, v5
	v_mov_b32_e32 v91, v5
	v_permlane32_swap_b32_e32 v41, v87
	s_nop 0
	v_permlane32_swap_b32_e32 v90, v91
	v_cndmask_b32_e32 v91, v90, v91, vcc
	v_cndmask_b32_e32 v90, v41, v87, vcc
	v_pk_mul_f32 v[76:77], v[76:77], v[90:91]
	s_nop 0
	v_pk_fma_f32 v[4:5], v[4:5], v[60:61], v[76:77]
	v_pk_mul_f32 v[60:61], v[40:41], v[42:43] op_sel_hi:[0,1]
	v_pk_mul_f32 v[4:5], v[4:5], s[94:95] op_sel_hi:[1,0]
	v_pk_mul_f32 v[60:61], v[60:61], v[92:93]
	v_cvt_pk_bf16_f32 v5, v4, v5
	v_mov_b32_e32 v4, v60
	v_mov_b32_e32 v41, v60
	v_mov_b32_e32 v76, v61
	v_mov_b32_e32 v77, v61
	v_permlane32_swap_b32_e32 v4, v41
	s_nop 0
	v_permlane32_swap_b32_e32 v76, v77
	v_cndmask_b32_e32 v77, v76, v77, vcc
	v_cndmask_b32_e32 v76, v4, v41, vcc
	v_pk_mul_f32 v[76:77], v[94:95], v[76:77]
	s_nop 0
	v_pk_fma_f32 v[54:55], v[60:61], v[54:55], v[76:77]
	s_nop 0
	v_pk_mul_f32 v[54:55], v[54:55], s[94:95] op_sel_hi:[1,0]
	s_nop 0
	v_cvt_pk_bf16_f32 v4, v54, v55
	s_waitcnt vmcnt(2)
; __device__ __forceinline__ unsigned cvtpk(float lo, float hi) { f32x2 v = {lo, hi}; bf16x2_t b = __builtin_convertvector(v, bf16x2_t); return __builtin_bit_cast(unsigned, b); }
; template <int DQK, int DV, bool LEAD> ...
;     ...
;           for (int ds = 0; ds < 2; ++ds)
; #pragma unroll
;               for (int j = 0; j < 8; ++j) x[ds][j] *= rn * qgain[32 * ds + 8 * g4 + j];
;           if constexpr (DQK == 64) {
; #pragma unroll
;               for (int ds = 0; ds < 2; ++ds)
; #pragma unroll
;                   for (int j = 0; j < 8; ++j) {
;                       auto rr = __builtin_amdgcn_permlane32_swap(__float_as_uint(x[ds][j]), __float_as_uint(x[ds][j]), false, false);
;                       const float other = hi ? __uint_as_float(rr[0]) : __uint_as_float(rr[1]);
;                       float cc = 1.f, sg = 0.f;
;                       if (lat) { const f32x2 cs = rope[(ds ? pcol : prow) * 16 + 8 * (g4 & 1) + j]; cc = cs.x; sg = hi ? cs.y : -cs.y; }
;                       x[ds][j] = x[ds][j] * cc + other * sg; }
;           } else {
;               float sr = 0.f;
; #pragma unroll
;               for (int j = 0; j < 8; ++j) sr += x[2][j] * x[2][j];
;               sr = lanes4_sum(sr);
;               const float rq = rsqrtf(sr * (1.f / 32.f) + EPS);
; #pragma unroll
;               for (int j = 0; j < 8; ++j) { const float av = x[2][j] * rq * qgain[64 + 8 * g4 + j];
;                   auto rr = __builtin_amdgcn_permlane16_swap(__float_as_uint(av), __float_as_uint(av), false, false);
;                   const float other = (g4 & 1) ? __uint_as_float(rr[0]) : __uint_as_float(rr[1]);
;                   float cc = 1.f, sg = 0.f;
;                   if (lat) { const f32x2 cs = rope[((g4 & 2) ? pcol : prow) * 8 + j]; cc = cs.x; sg = (g4 & 1) ? cs.y : -cs.y; }
;                   x[2][j] = av * cc + other * sg; }
;           }
; #pragma unroll
;           for (int ds = 0; ds < NDS; ++ds) { u32x4 w;
; #pragma unroll
;               for (int i = 0; i < 4; ++i) w[i] = cvtpk(x[ds][2 * i] * c2, x[ds][2 * i + 1] * c2);
;               qf[qb * NDS + ds] = __builtin_bit_cast(bf16x8, w); }
	v_pk_mul_f32 v[54:55], v[40:41], v[48:49] op_sel_hi:[0,1]
	v_pk_mul_f32 v[54:55], v[54:55], v[96:97]
	s_nop 0
	v_mov_b32_e32 v41, v54
	v_mov_b32_e32 v60, v54
	v_mov_b32_e32 v61, v55
	v_mov_b32_e32 v76, v55
	v_permlane32_swap_b32_e32 v41, v60
	s_nop 0
	v_permlane32_swap_b32_e32 v61, v76
	v_cndmask_b32_e32 v61, v61, v76, vcc
	v_cndmask_b32_e32 v60, v41, v60, vcc
	v_pk_mul_f32 v[60:61], v[98:99], v[60:61]
	s_nop 0
	v_pk_fma_f32 v[2:3], v[54:55], v[2:3], v[60:61]
	v_pk_mul_f32 v[54:55], v[46:47], v[40:41] op_sel_hi:[1,0]
	v_pk_mul_f32 v[2:3], v[2:3], s[94:95] op_sel_hi:[1,0]
	v_pk_mul_f32 v[54:55], v[54:55], v[100:101]
	v_cvt_pk_bf16_f32 v3, v2, v3
	v_mov_b32_e32 v2, v54
	v_mov_b32_e32 v41, v54
	v_mov_b32_e32 v60, v55
	v_mov_b32_e32 v61, v55
	v_permlane32_swap_b32_e32 v2, v41
	s_nop 0
	v_permlane32_swap_b32_e32 v60, v61
	v_cndmask_b32_e32 v61, v60, v61, vcc
	v_cndmask_b32_e32 v60, v2, v41, vcc
	v_pk_mul_f32 v[60:61], v[102:103], v[60:61]
	s_nop 0
	v_pk_fma_f32 v[10:11], v[54:55], v[10:11], v[60:61]
	s_nop 0
	v_pk_mul_f32 v[10:11], v[10:11], s[94:95] op_sel_hi:[1,0]
	s_nop 0
	v_cvt_pk_bf16_f32 v2, v10, v11
	s_waitcnt vmcnt(1)
	v_pk_mul_f32 v[10:11], v[52:53], v[40:41] op_sel_hi:[1,0]
	s_nop 0
	v_pk_mul_f32 v[10:11], v[10:11], v[12:13]
	s_nop 0
	v_mov_b32_e32 v12, v10
	v_mov_b32_e32 v41, v10
	v_mov_b32_e32 v13, v11
	v_mov_b32_e32 v54, v11
	v_permlane32_swap_b32_e32 v12, v41
	s_nop 0
	v_permlane32_swap_b32_e32 v13, v54
	v_cndmask_b32_e32 v13, v13, v54, vcc
	v_cndmask_b32_e32 v12, v12, v41, vcc
	v_pk_mul_f32 v[12:13], v[24:25], v[12:13]
	s_nop 0
	v_pk_fma_f32 v[10:11], v[10:11], v[26:27], v[12:13]
	s_nop 0
	v_pk_mul_f32 v[10:11], v[10:11], s[94:95] op_sel_hi:[1,0]
	s_nop 0
	v_cvt_pk_bf16_f32 v13, v10, v11
	v_pk_mul_f32 v[10:11], v[50:51], v[40:41] op_sel_hi:[1,0]
	s_nop 0
	v_pk_mul_f32 v[10:11], v[10:11], v[84:85]
	s_nop 0
	v_mov_b32_e32 v12, v10
	v_mov_b32_e32 v41, v10
	v_mov_b32_e32 v54, v11
	v_mov_b32_e32 v55, v11
	v_permlane32_swap_b32_e32 v12, v41
	s_nop 0
	v_permlane32_swap_b32_e32 v54, v55
	v_cndmask_b32_e32 v55, v54, v55, vcc
	v_cndmask_b32_e32 v54, v12, v41, vcc
	v_pk_mul_f32 v[54:55], v[28:29], v[54:55]
	s_nop 0
	v_pk_fma_f32 v[10:11], v[10:11], v[30:31], v[54:55]
	s_nop 0
	v_pk_mul_f32 v[10:11], v[10:11], s[94:95] op_sel_hi:[1,0]
	s_nop 0
	v_cvt_pk_bf16_f32 v12, v10, v11
	s_waitcnt vmcnt(0)
	v_pk_mul_f32 v[10:11], v[58:59], v[40:41] op_sel_hi:[1,0]
	s_nop 0
	v_pk_mul_f32 v[10:11], v[10:11], v[88:89]
	s_nop 0
	v_mov_b32_e32 v41, v10
	v_mov_b32_e32 v54, v10
	v_mov_b32_e32 v55, v11
	v_mov_b32_e32 v60, v11
	v_permlane32_swap_b32_e32 v41, v54
	s_nop 0
	v_permlane32_swap_b32_e32 v55, v60
	v_cndmask_b32_e32 v55, v55, v60, vcc
	v_cndmask_b32_e32 v54, v41, v54, vcc
	v_pk_mul_f32 v[54:55], v[32:33], v[54:55]
	v_pk_mul_f32 v[40:41], v[56:57], v[40:41] op_sel_hi:[1,0]
	v_pk_fma_f32 v[10:11], v[10:11], v[34:35], v[54:55]
	v_pk_mul_f32 v[40:41], v[40:41], v[82:83]
	v_pk_mul_f32 v[10:11], v[10:11], s[94:95] op_sel_hi:[1,0]
	v_mov_b32_e32 v54, v40
	v_cvt_pk_bf16_f32 v11, v10, v11
	v_mov_b32_e32 v10, v40
	s_nop 1
	v_permlane32_swap_b32_e32 v10, v54
	v_mov_b32_e32 v55, v41
	v_mov_b32_e32 v60, v41
	v_cndmask_b32_e32 v54, v10, v54, vcc
	v_mul_f32_e32 v10, 0x4b800000, v86
	v_permlane32_swap_b32_e32 v55, v60
	v_cndmask_b32_e64 v10, v86, v10, s[4:5]
	v_cndmask_b32_e32 v55, v55, v60, vcc
	v_rsq_f32_e32 v60, v10
	v_pk_mul_f32 v[54:55], v[106:107], v[54:55]
	s_nop 0
	v_pk_fma_f32 v[40:41], v[40:41], v[38:39], v[54:55]
	s_nop 0
	v_pk_mul_f32 v[40:41], v[40:41], s[94:95] op_sel_hi:[1,0]
	s_nop 0
	v_cvt_pk_bf16_f32 v10, v40, v41
	v_mul_f32_e32 v40, 0x45800000, v60
	v_cndmask_b32_e64 v40, v60, v40, s[4:5]
	v_pk_mul_f32 v[54:55], v[56:57], v[40:41] op_sel_hi:[1,0]
	v_pk_mul_f32 v[56:57], v[58:59], v[40:41] op_sel_hi:[1,0]
	v_pk_mul_f32 v[54:55], v[54:55], v[104:105]
	v_pk_mul_f32 v[36:37], v[56:57], v[36:37]
	v_pk_mul_f32 v[50:51], v[50:51], v[40:41] op_sel_hi:[1,0]
	v_pk_mul_f32 v[52:53], v[52:53], v[40:41] op_sel_hi:[1,0]
	v_pk_mul_f32 v[46:47], v[46:47], v[40:41] op_sel_hi:[1,0]
	v_pk_mul_f32 v[48:49], v[48:49], v[40:41] op_sel_hi:[1,0]
	v_pk_mul_f32 v[42:43], v[42:43], v[40:41] op_sel_hi:[1,0]
	v_pk_mul_f32 v[40:41], v[44:45], v[40:41] op_sel_hi:[1,0]
	v_mov_b32_e32 v44, v54
	v_mov_b32_e32 v56, v54
	v_mov_b32_e32 v45, v55
	v_mov_b32_e32 v57, v55
	v_permlane32_swap_b32_e32 v44, v56
	s_nop 0
	v_permlane32_swap_b32_e32 v45, v57
	v_cndmask_b32_e32 v45, v45, v57, vcc
	v_cndmask_b32_e32 v44, v44, v56, vcc
	v_pk_mul_f32 v[38:39], v[38:39], v[54:55]
	v_mov_b32_e32 v54, v36
	v_pk_fma_f32 v[38:39], v[106:107], v[44:45], v[38:39]
	v_mov_b32_e32 v44, v36
	v_mov_b32_e32 v45, v37
	v_mov_b32_e32 v55, v37
	v_permlane32_swap_b32_e32 v44, v54
	s_nop 0
	v_permlane32_swap_b32_e32 v45, v55
	v_pk_mul_f32 v[50:51], v[50:51], v[74:75]
	v_cndmask_b32_e32 v45, v45, v55, vcc
	v_cndmask_b32_e32 v44, v44, v54, vcc
	v_pk_mul_f32 v[34:35], v[34:35], v[36:37]
	v_mov_b32_e32 v36, v50
	v_pk_fma_f32 v[32:33], v[32:33], v[44:45], v[34:35]
	v_mov_b32_e32 v34, v50
	v_mov_b32_e32 v35, v51
	v_mov_b32_e32 v37, v51
	v_permlane32_swap_b32_e32 v34, v36
	s_nop 0
	v_permlane32_swap_b32_e32 v35, v37
	v_cndmask_b32_e32 v35, v35, v37, vcc
	v_cndmask_b32_e32 v34, v34, v36, vcc
	v_pk_mul_f32 v[52:53], v[52:53], v[72:73]
	v_pk_mul_f32 v[28:29], v[28:29], v[34:35]
	v_mov_b32_e32 v34, v52
	v_pk_fma_f32 v[28:29], v[30:31], v[50:51], v[28:29]
	v_mov_b32_e32 v30, v52
	v_mov_b32_e32 v31, v53
	v_mov_b32_e32 v35, v53
	v_permlane32_swap_b32_e32 v30, v34
	s_nop 0
	v_permlane32_swap_b32_e32 v31, v35
	v_cndmask_b32_e32 v31, v31, v35, vcc
	v_cndmask_b32_e32 v30, v30, v34, vcc
	v_pk_mul_f32 v[46:47], v[46:47], v[70:71]
; __device__ __forceinline__ unsigned cvtpk(float lo, float hi) { f32x2 v = {lo, hi}; bf16x2_t b = __builtin_convertvector(v, bf16x2_t); return __builtin_bit_cast(unsigned, b); }
; #define ATT_SB() __builtin_amdgcn_sched_barrier(0)
; #define ATT_DMA_K(t, sl) do { glds16(ksrc + (size_t)(t) * 64 * kpitch, (unsigned)__builtin_amdgcn_readfirstlane(kdst + (sl) * KSLOT)); \
;         if constexpr (DQK == 96) glds16(krsrc + (size_t)(t) * 64 * 32, (unsigned)__builtin_amdgcn_readfirstlane(krdst + (sl) * KSLOT)); } while (0)
; #define ATT_DMA_V(t, sl) do { glds16(vsrc + (size_t)(t) * 64, (unsigned)__builtin_amdgcn_readfirstlane(vdst + (sl) * VSLOT)); \
;         if constexpr (DV == 128) glds16(vsrc + (size_t)64 * NR + (size_t)(t) * 64, (unsigned)__builtin_amdgcn_readfirstlane(vdst + (sl) * VSLOT + 8192)); } while (0)
; #define ATT_KLOAD(sl) do { _Pragma("unroll") for (int kb_ = 0; kb_ < NKW; ++kb_) _Pragma("unroll") for (int ds_ = 0; ds_ < NDS; ++ds_) { \
;         if (ds_ < 2) kf[kb_ * NDS + ds_] = *(const LAS bf16x8*)(kp[ds_ & 1] + (sl) * KSLOT + (kb_ & 1) * 512 + (kb_ >> 1) * 4096); \
;         else kf[kb_ * NDS + ds_] = *(const LAS bf16x8*)(krp + (sl) * KSLOT + (kb_ & 1) * 256 + (kb_ >> 1) * 2048); } } while (0)
; template <int DQK, int DV, bool LEAD> ...
;     ...
;           for (int ds = 0; ds < NDS; ++ds) { u32x4 w;
; #pragma unroll
;               for (int i = 0; i < 4; ++i) w[i] = cvtpk(x[ds][2 * i] * c2, x[ds][2 * i + 1] * c2);
;               qf[qb * NDS + ds] = __builtin_bit_cast(bf16x8, w); }
;       }
; #pragma unroll
;       for (int d0 = 0; d0 < NQB * NDS; ++d0) asm volatile("" : "+v"(qf[d0])); }
;     wait_bar<0>();
;     bf16x8 kf[NKW * NDS], vf[NVF];
;     ATT_KLOAD(0);
;     asm volatile("s_waitcnt lgkmcnt(0)\n\ts_barrier" ::: "memory");
;     float lsum[NQB];
; #pragma unroll
;     for (int qb = 0; qb < NQB; ++qb) lsum[qb] = 0.f;
;     const f32x4 zero4 = {0.f, 0.f, 0.f, 0.f};
;     f32x4 o[NDB][NQB], c[NKW][NQB]; u32x4 pw[4];
; #pragma unroll
;     for (int i = 0; i < NDB; ++i)
; #pragma unroll
;         for (int qb = 0; qb < NQB; ++qb) o[i][qb] = zero4;
;     ATT_DMA_K(3, 0); ATT_DMA_V(1, 1);
;     ATT_QK(); ATT_SB();
;     ATT_KLOAD(1); ATT_SB();
;     if constexpr (LEAD) { ATT_EXP(); ATT_SUMPACK(); }
;     wait_bar<NDMA>();
;     int s_prev = 0, s_cur = 1, s_next = 2;
;     int one_ = 1; asm volatile("" : "+s"(one_));
	v_pk_mul_f32 v[24:25], v[24:25], v[30:31]
	v_mov_b32_e32 v30, v46
	v_pk_fma_f32 v[24:25], v[52:53], v[26:27], v[24:25]
	v_mov_b32_e32 v26, v46
	v_mov_b32_e32 v27, v47
	v_mov_b32_e32 v31, v47
	v_permlane32_swap_b32_e32 v26, v30
	s_nop 0
	v_permlane32_swap_b32_e32 v27, v31
	v_cndmask_b32_e32 v27, v27, v31, vcc
	v_cndmask_b32_e32 v26, v26, v30, vcc
	v_pk_mul_f32 v[48:49], v[48:49], v[68:69]
	v_pk_mul_f32 v[20:21], v[20:21], v[26:27]
	v_mov_b32_e32 v26, v48
	v_pk_fma_f32 v[20:21], v[46:47], v[22:23], v[20:21]
	v_mov_b32_e32 v22, v48
	v_mov_b32_e32 v23, v49
	v_mov_b32_e32 v27, v49
	v_permlane32_swap_b32_e32 v22, v26
	s_nop 0
	v_permlane32_swap_b32_e32 v23, v27
	v_cndmask_b32_e32 v23, v23, v27, vcc
	v_cndmask_b32_e32 v22, v22, v26, vcc
	v_pk_mul_f32 v[42:43], v[42:43], v[66:67]
	v_pk_mul_f32 v[16:17], v[16:17], v[22:23]
	v_mov_b32_e32 v22, v42
	v_pk_fma_f32 v[16:17], v[48:49], v[18:19], v[16:17]
	v_mov_b32_e32 v18, v42
	v_mov_b32_e32 v19, v43
	v_mov_b32_e32 v23, v43
	v_permlane32_swap_b32_e32 v18, v22
	s_nop 0
	v_permlane32_swap_b32_e32 v19, v23
	v_cndmask_b32_e32 v19, v19, v23, vcc
	v_cndmask_b32_e32 v18, v18, v22, vcc
	v_pk_mul_f32 v[40:41], v[40:41], v[64:65]
	v_pk_mul_f32 v[8:9], v[8:9], v[18:19]
	v_mov_b32_e32 v18, v40
	v_pk_fma_f32 v[8:9], v[42:43], v[14:15], v[8:9]
	v_mov_b32_e32 v14, v40
	v_mov_b32_e32 v15, v41
	v_mov_b32_e32 v19, v41
	v_permlane32_swap_b32_e32 v14, v18
	s_nop 0
	v_permlane32_swap_b32_e32 v15, v19
	v_cndmask_b32_e32 v15, v15, v19, vcc
	v_cndmask_b32_e32 v14, v14, v18, vcc
	v_pk_mul_f32 v[14:15], v[62:63], v[14:15]
	v_pk_mul_f32 v[8:9], v[8:9], s[94:95] op_sel_hi:[1,0]
	v_pk_fma_f32 v[6:7], v[40:41], v[6:7], v[14:15]
	v_pk_mul_f32 v[14:15], v[38:39], s[94:95] op_sel_hi:[1,0]
	v_pk_mul_f32 v[6:7], v[6:7], s[94:95] op_sel_hi:[1,0]
	v_cvt_pk_bf16_f32 v58, v14, v15
	v_pk_mul_f32 v[14:15], v[32:33], s[94:95] op_sel_hi:[1,0]
	v_cvt_pk_bf16_f32 v68, v8, v9
	v_cvt_pk_bf16_f32 v59, v14, v15
	v_pk_mul_f32 v[14:15], v[28:29], s[94:95] op_sel_hi:[1,0]
	v_cvt_pk_bf16_f32 v69, v6, v7
	v_cvt_pk_bf16_f32 v60, v14, v15
	v_pk_mul_f32 v[14:15], v[24:25], s[94:95] op_sel_hi:[1,0]
	v_bfe_u32 v22, v79, 1, 3
	v_cvt_pk_bf16_f32 v61, v14, v15
	v_pk_mul_f32 v[14:15], v[20:21], s[94:95] op_sel_hi:[1,0]
	v_bitop3_b32 v22, v214, v22, 4 bitop3:0x36
	v_cvt_pk_bf16_f32 v66, v14, v15
	v_pk_mul_f32 v[14:15], v[16:17], s[94:95] op_sel_hi:[1,0]
	v_lshlrev_b32_e32 v30, 4, v22
	v_cvt_pk_bf16_f32 v67, v14, v15
	s_waitcnt vmcnt(0) lgkmcnt(0)
	s_barrier
	ds_read_b128 v[6:9], v194
	ds_read_b128 v[14:17], v194 offset:512
	v_add_u32_e32 v220, v81, v30
	s_waitcnt lgkmcnt(1)
	v_mfma_f32_16x16x32_bf16 v[18:21], v[6:9], v[10:13], 0
	ds_read_b128 v[22:25], v220
	ds_read_b128 v[26:29], v220 offset:512
	v_add_u32_e32 v31, 0, v217
	v_add_u32_e32 v218, v31, v80
	v_mfma_f32_16x16x32_bf16 v[6:9], v[6:9], v[58:61], 0
	v_add_u32_e32 v219, v31, v30
	s_waitcnt lgkmcnt(1)
	v_mfma_f32_16x16x32_bf16 v[126:129], v[22:25], v[66:69], v[6:9]
	v_mfma_f32_16x16x32_bf16 v[6:9], v[14:17], v[10:13], 0
	s_waitcnt lgkmcnt(0)
	v_mfma_f32_16x16x32_bf16 v[122:125], v[26:29], v[2:5], v[6:9]
	v_mfma_f32_16x16x32_bf16 v[14:17], v[14:17], v[58:61], 0
	s_nop 4
	ds_read_b128 v[6:9], v194 offset:4096
	v_mfma_f32_16x16x32_bf16 v[138:141], v[22:25], v[2:5], v[18:21]
	v_mfma_f32_16x16x32_bf16 v[114:117], v[26:29], v[66:69], v[14:17]
	s_nop 2
	ds_read_b128 v[14:17], v220 offset:4096
	ds_read_b128 v[18:21], v194 offset:4608
	ds_read_b128 v[26:29], v220 offset:4608
	s_waitcnt lgkmcnt(0)
	s_barrier
	s_waitcnt lgkmcnt(3)
	v_mfma_f32_16x16x32_bf16 v[22:25], v[6:9], v[10:13], 0
	v_mfma_f32_16x16x32_bf16 v[6:9], v[6:9], v[58:61], 0
	s_waitcnt lgkmcnt(2)
	v_mfma_f32_16x16x32_bf16 v[130:133], v[14:17], v[2:5], v[22:25]
	s_nop 4
	v_lshl_add_u64 v[22:23], v[204:205], 0, s[96:97]
	v_mfma_f32_16x16x32_bf16 v[118:121], v[14:17], v[66:69], v[6:9]
	s_mov_b32 m0, s43
	s_nop 0
	global_load_lds_dwordx4 v[22:23], off
	v_lshl_add_u64 v[14:15], v[206:207], 0, s[66:67]
	s_add_i32 s4, s16, 0x4000
	s_waitcnt lgkmcnt(1)
	v_mfma_f32_16x16x32_bf16 v[6:9], v[18:21], v[10:13], 0
	s_mov_b32 m0, s4
	s_nop 0
	global_load_lds_dwordx4 v[14:15], off
	s_mov_b64 s[4:5], 0x840080
	v_lshl_add_u64 v[22:23], v[206:207], 0, s[4:5]
	v_mfma_f32_16x16x32_bf16 v[14:17], v[18:21], v[58:61], 0
	s_add_i32 s4, s16, 0x6000
	s_mov_b32 m0, s4
	s_nop 0
	global_load_lds_dwordx4 v[22:23], off
	s_mov_b32 s4, 0
	s_waitcnt lgkmcnt(0)
	v_mfma_f32_16x16x32_bf16 v[142:145], v[26:29], v[2:5], v[6:9]
	s_mov_b32 s6, s4
	s_mov_b32 s7, s4
	s_mov_b32 s5, s4
	v_mfma_f32_16x16x32_bf16 v[134:137], v[26:29], v[66:69], v[14:17]
	v_mov_b64_e32 v[8:9], s[6:7]
	v_mov_b64_e32 v[6:7], s[4:5]
	ds_read_b128 v[82:85], v194 offset:8192
	ds_read_b128 v[86:89], v194 offset:8704
	ds_read_b128 v[90:93], v220 offset:8192
	ds_read_b128 v[94:97], v220 offset:8704
	ds_read_b128 v[98:101], v194 offset:12288
	ds_read_b128 v[102:105], v194 offset:12800
	ds_read_b128 v[106:109], v220 offset:12288
	ds_read_b128 v[110:113], v220 offset:12800
	s_waitcnt vmcnt(3) lgkmcnt(0)
	s_barrier
	s_mov_b32 s5, 1
	v_mov_b32_e32 v42, 0
	s_cmp_lg_u32 s5, 0
	v_mov_b64_e32 v[16:17], v[8:9]
	v_mov_b64_e32 v[20:21], v[8:9]
	v_mov_b64_e32 v[24:25], v[8:9]
	v_mov_b64_e32 v[28:29], v[8:9]
	v_mov_b64_e32 v[32:33], v[8:9]
	v_mov_b64_e32 v[36:37], v[8:9]
	v_mov_b64_e32 v[40:41], v[8:9]
	s_cselect_b64 s[6:7], -1, 0
	v_mov_b64_e32 v[14:15], v[6:7]
	v_mov_b64_e32 v[18:19], v[6:7]
	v_mov_b64_e32 v[22:23], v[6:7]
	v_mov_b64_e32 v[26:27], v[6:7]
	v_mov_b64_e32 v[30:31], v[6:7]
	v_mov_b64_e32 v[34:35], v[6:7]
	v_mov_b64_e32 v[38:39], v[6:7]
	s_mov_b32 s38, 2
	v_mov_b32_e32 v43, v42
	v_mov_b32_e32 v44, v42
	v_mov_b32_e32 v45, v42
	v_mov_b32_e32 v46, v42
	v_mov_b32_e32 v47, v42
	v_mov_b32_e32 v48, v42
	v_mov_b32_e32 v49, v42
	v_mov_b32_e32 v50, v42
	v_mov_b32_e32 v51, v42
	v_mov_b32_e32 v52, v42
	v_mov_b32_e32 v53, v42
	v_mov_b32_e32 v54, v42
	v_mov_b32_e32 v55, v42
	v_mov_b32_e32 v56, v42
	v_mov_b32_e32 v57, v42
	v_mov_b32_e32 v62, v42
	v_mov_b32_e32 v63, v42
	v_mov_b32_e32 v64, v42
	v_mov_b32_e32 v65, v42
	v_mov_b32_e32 v70, v42
	v_mov_b32_e32 v71, v42
	v_mov_b32_e32 v72, v42
	v_mov_b32_e32 v73, v42
	v_mov_b32_e32 v74, v42
	v_mov_b32_e32 v75, v42
	v_mov_b32_e32 v76, v42
	v_mov_b32_e32 v77, v42
	v_mov_b32_e32 v78, v42
	v_mov_b32_e32 v79, v42
	v_mov_b32_e32 v80, v42
	v_mov_b32_e32 v81, v42
	v_mov_b32_e32 v210, v42
	v_mov_b32_e32 v211, v42
; #define ATT_SB() __builtin_amdgcn_sched_barrier(0)
; #define ATT_DMA_K(t, sl) do { glds16(ksrc + (size_t)(t) * 64 * kpitch, (unsigned)__builtin_amdgcn_readfirstlane(kdst + (sl) * KSLOT)); \
;         if constexpr (DQK == 96) glds16(krsrc + (size_t)(t) * 64 * 32, (unsigned)__builtin_amdgcn_readfirstlane(krdst + (sl) * KSLOT)); } while (0)
; #define ATT_DMA_V(t, sl) do { glds16(vsrc + (size_t)(t) * 64, (unsigned)__builtin_amdgcn_readfirstlane(vdst + (sl) * VSLOT)); \
;         if constexpr (DV == 128) glds16(vsrc + (size_t)64 * NR + (size_t)(t) * 64, (unsigned)__builtin_amdgcn_readfirstlane(vdst + (sl) * VSLOT + 8192)); } while (0)
; #define ATT_KLOAD(sl) do { _Pragma("unroll") for (int kb_ = 0; kb_ < NKW; ++kb_) _Pragma("unroll") for (int ds_ = 0; ds_ < NDS; ++ds_) { \
;         if (ds_ < 2) kf[kb_ * NDS + ds_] = *(const LAS bf16x8*)(kp[ds_ & 1] + (sl) * KSLOT + (kb_ & 1) * 512 + (kb_ >> 1) * 4096); \
;         else kf[kb_ * NDS + ds_] = *(const LAS bf16x8*)(krp + (sl) * KSLOT + (kb_ & 1) * 256 + (kb_ >> 1) * 2048); } } while (0)
; template <int DQK, int DV, bool LEAD> ...
;     ...
;     for (int t = 1; t < NT; ++t) {
;         __builtin_amdgcn_s_waitcnt(0xC07F);
;         if constexpr (!LEAD) { ATT_EXP(); ATT_SUMPACK(); ATT_SB(); }
;         ATT_VLOAD(s_prev, 0); ATT_SB();
;         { const int tk = (t + 3 < NT) ? t + 3 : NT - 1; ATT_DMA_K(tk, s_cur); }
;         { const int tv = (t + 1 < NT) ? t + 1 : NT - 1; ATT_DMA_V(tv, s_next); }
;         ATT_SB();
;         if constexpr (LEAD) {
;             ATT_QK(); ATT_SB();
;             ATT_PVP(0); ATT_SB();
;             if constexpr (DV == 128) { ATT_VLOAD(s_prev, 1); ATT_SB(); ATT_EXP(); ATT_SB(); ATT_PVP(1); ATT_SB(); }
;             if (one_) ATT_KLOAD(s_next);
;             ATT_SB();
;             if constexpr (DV == 64) ATT_EXP();
;             ATT_SUMPACK();
;             asm volatile("" : "+v"(pw[0]), "+v"(pw[1]), "+v"(pw[2]), "+v"(pw[3]));
; #pragma unroll
;             for (int qb = 0; qb < NQB; ++qb) asm volatile("" : "+v"(lsum[qb]));
;         } else {
;             if constexpr (DV == 128) {
;                 ATT_PVP(0); ATT_SB();
;                 ATT_VLOAD(s_prev, 1); ATT_SB();
;                 ATT_QK(); ATT_SB();
;                 if (one_) { ATT_KLOAD(s_next); ATT_SB(); ATT_PVP(1); }
;                 ATT_SB();
.LBB0_941:
	v_exp_f32_e32 v138, v138
	v_exp_f32_e32 v139, v139
	v_exp_f32_e32 v140, v140
	v_exp_f32_e32 v141, v141
	v_exp_f32_e32 v126, v126
	v_exp_f32_e32 v127, v127
	v_exp_f32_e32 v128, v128
	v_exp_f32_e32 v129, v129
	v_exp_f32_e32 v122, v122
	v_exp_f32_e32 v114, v114
	v_add_f32_e32 v146, v138, v139
	v_add_f32_e32 v147, v140, v141
	v_exp_f32_e32 v123, v123
	v_exp_f32_e32 v115, v115
	v_add_f32_e32 v146, v146, v147
	v_add_f32_e32 v147, v126, v127
	v_add_f32_e32 v148, v128, v129
	v_add_f32_e32 v147, v147, v148
	v_exp_f32_e32 v124, v124
	v_exp_f32_e32 v116, v116
	v_add_f32_e32 v146, v122, v146
	v_add_f32_e32 v147, v114, v147
	s_waitcnt lgkmcnt(0)
	v_exp_f32_e32 v125, v125
	v_exp_f32_e32 v117, v117
	v_add_f32_e32 v146, v123, v146
	v_add_f32_e32 v147, v115, v147
	v_exp_f32_e32 v130, v130
	v_exp_f32_e32 v118, v118
	v_add_f32_e32 v146, v124, v146
	v_add_f32_e32 v147, v116, v147
	v_exp_f32_e32 v131, v131
	v_exp_f32_e32 v119, v119
	v_add_f32_e32 v146, v125, v146
	v_add_f32_e32 v147, v117, v147
	v_exp_f32_e32 v132, v132
	v_exp_f32_e32 v120, v120
	v_add_f32_e32 v146, v130, v146
	v_add_f32_e32 v147, v118, v147
	v_exp_f32_e32 v133, v133
	v_exp_f32_e32 v121, v121
	v_add_f32_e32 v146, v131, v146
	v_add_f32_e32 v147, v119, v147
	v_exp_f32_e32 v142, v142
	v_exp_f32_e32 v134, v134
	v_add_f32_e32 v146, v132, v146
	v_add_f32_e32 v147, v120, v147
	v_exp_f32_e32 v143, v143
	v_exp_f32_e32 v135, v135
	v_add_f32_e32 v146, v133, v146
	v_add_f32_e32 v147, v121, v147
	v_exp_f32_e32 v144, v144
	v_exp_f32_e32 v136, v136
	v_add_f32_e32 v146, v142, v146
	v_add_f32_e32 v147, v134, v147
	v_exp_f32_e32 v145, v145
	v_exp_f32_e32 v137, v137
	v_add_f32_e32 v146, v143, v146
	v_add_f32_e32 v147, v135, v147
	s_mov_b32 s5, s47
	v_add_f32_e32 v146, v144, v146
	v_add_f32_e32 v147, v136, v147
	s_mov_b32 s47, s38
	v_add_f32_e32 v213, v145, v146
	v_add_f32_e32 v212, v137, v147
	v_cvt_pk_bf16_f32 v146, v138, v139
	v_cvt_pk_bf16_f32 v147, v140, v141
	v_cvt_pk_bf16_f32 v148, v122, v123
	v_cvt_pk_bf16_f32 v149, v124, v125
	v_cvt_pk_bf16_f32 v150, v126, v127
	v_cvt_pk_bf16_f32 v151, v128, v129
	v_cvt_pk_bf16_f32 v152, v114, v115
	v_cvt_pk_bf16_f32 v153, v116, v117
	v_cvt_pk_bf16_f32 v154, v130, v131
	v_cvt_pk_bf16_f32 v155, v132, v133
	v_cvt_pk_bf16_f32 v156, v142, v143
	v_cvt_pk_bf16_f32 v157, v144, v145
	v_cvt_pk_bf16_f32 v158, v118, v119
	v_cvt_pk_bf16_f32 v159, v120, v121
	v_cvt_pk_bf16_f32 v160, v134, v135
	v_cvt_pk_bf16_f32 v161, v136, v137
	s_add_i32 s38, s48, -1
	s_lshl_b32 s49, s4, 14
	v_add_u32_e32 v164, s49, v218
	v_add_u32_e32 v166, s49, v219
	ds_read_b128 v[114:117], v164 offset:36864
	ds_read_b128 v[118:121], v164 offset:38912
	ds_read_b128 v[122:125], v166 offset:36864
	ds_read_b128 v[126:129], v166 offset:38912
	ds_read_b128 v[130:133], v164 offset:40960
	ds_read_b128 v[134:137], v164 offset:43008
	ds_read_b128 v[138:141], v166 offset:40960
	ds_read_b128 v[142:145], v166 offset:43008
	s_min_u32 s38, s38, 0x80
	s_mul_i32 s38, s38, 0x38000
	v_lshl_add_u64 v[162:163], v[204:205], 0, s[38:39]
	s_lshl_b32 s38, s5, 13
	s_add_i32 s38, s38, s43
	v_lshl_add_u64 v[162:163], v[162:163], 0, s[96:97]
	s_mov_b32 m0, s38
	s_nop 0
	global_load_lds_dwordx4 v[162:163], off
	s_min_u32 s38, s48, 0x83
	s_lshl_b32 s38, s38, 7
	s_lshl_b32 s49, s47, 14
	v_lshl_add_u64 v[162:163], v[206:207], 0, s[38:39]
	s_add_i32 s49, s49, s16
	s_mov_b32 m0, s49
	s_nop 0
	global_load_lds_dwordx4 v[162:163], off
	v_lshl_add_u64 v[162:163], v[208:209], 0, s[38:39]
	s_add_i32 s38, s49, 0x2000
	s_mov_b32 m0, s38
	s_nop 0
	global_load_lds_dwordx4 v[162:163], off
	s_waitcnt lgkmcnt(7)
	v_mfma_f32_16x16x32_bf16 v[78:81], v[114:117], v[146:149], v[78:81]
	v_mfma_f32_16x16x32_bf16 v[74:77], v[114:117], v[150:153], v[74:77]
	s_waitcnt lgkmcnt(6)
	v_mfma_f32_16x16x32_bf16 v[70:73], v[118:121], v[146:149], v[70:73]
	v_mfma_f32_16x16x32_bf16 v[62:65], v[118:121], v[150:153], v[62:65]
	s_waitcnt lgkmcnt(3)
	v_mfma_f32_16x16x32_bf16 v[54:57], v[130:133], v[146:149], v[54:57]
	v_mfma_f32_16x16x32_bf16 v[50:53], v[130:133], v[150:153], v[50:53]
	s_waitcnt lgkmcnt(2)
	v_mfma_f32_16x16x32_bf16 v[46:49], v[134:137], v[146:149], v[46:49]
	v_mfma_f32_16x16x32_bf16 v[42:45], v[134:137], v[150:153], v[42:45]
	v_mfma_f32_16x16x32_bf16 v[78:81], v[122:125], v[154:157], v[78:81]
	v_mfma_f32_16x16x32_bf16 v[74:77], v[122:125], v[158:161], v[74:77]
	v_mfma_f32_16x16x32_bf16 v[70:73], v[126:129], v[154:157], v[70:73]
	v_mfma_f32_16x16x32_bf16 v[62:65], v[126:129], v[158:161], v[62:65]
	s_waitcnt lgkmcnt(1)
	v_mfma_f32_16x16x32_bf16 v[54:57], v[138:141], v[154:157], v[54:57]
	v_mfma_f32_16x16x32_bf16 v[50:53], v[138:141], v[158:161], v[50:53]
	s_waitcnt lgkmcnt(0)
	v_mfma_f32_16x16x32_bf16 v[46:49], v[142:145], v[154:157], v[46:49]
	v_mfma_f32_16x16x32_bf16 v[42:45], v[142:145], v[158:161], v[42:45]
	ds_read_b128 v[186:189], v164 offset:45056
	ds_read_b128 v[174:177], v164 offset:47104
	ds_read_b128 v[190:193], v166 offset:45056
	ds_read_b128 v[178:181], v166 offset:47104
	ds_read_b128 v[170:173], v164 offset:49152
	ds_read_b128 v[162:165], v164 offset:51200
	ds_read_b128 v[182:185], v166 offset:49152
	ds_read_b128 v[166:169], v166 offset:51200
	v_mfma_f32_16x16x32_bf16 v[114:117], v[82:85], v[10:13], 0
	v_mfma_f32_16x16x32_bf16 v[118:121], v[82:85], v[58:61], 0
	v_mfma_f32_16x16x32_bf16 v[138:141], v[90:93], v[2:5], v[114:117]
	v_mfma_f32_16x16x32_bf16 v[126:129], v[90:93], v[66:69], v[118:121]
	v_mfma_f32_16x16x32_bf16 v[114:117], v[86:89], v[10:13], 0
	v_mfma_f32_16x16x32_bf16 v[118:121], v[86:89], v[58:61], 0
	v_mfma_f32_16x16x32_bf16 v[122:125], v[94:97], v[2:5], v[114:117]
	v_mfma_f32_16x16x32_bf16 v[114:117], v[94:97], v[66:69], v[118:121]
	v_mfma_f32_16x16x32_bf16 v[118:121], v[98:101], v[10:13], 0
	v_mfma_f32_16x16x32_bf16 v[134:137], v[98:101], v[58:61], 0
	v_mfma_f32_16x16x32_bf16 v[130:133], v[106:109], v[2:5], v[118:121]
	v_mfma_f32_16x16x32_bf16 v[118:121], v[106:109], v[66:69], v[134:137]
	v_mfma_f32_16x16x32_bf16 v[134:137], v[102:105], v[10:13], 0
	v_mfma_f32_16x16x32_bf16 v[236:239], v[102:105], v[58:61], 0
	v_mfma_f32_16x16x32_bf16 v[142:145], v[110:113], v[2:5], v[134:137]
	v_mfma_f32_16x16x32_bf16 v[134:137], v[110:113], v[66:69], v[236:239]
	s_andn2_b64 vcc, exec, s[6:7]
	s_cbranch_vccnz .LBB0_943
; #define ATT_SB() __builtin_amdgcn_sched_barrier(0)
; #define ATT_KLOAD(sl) do { _Pragma("unroll") for (int kb_ = 0; kb_ < NKW; ++kb_) _Pragma("unroll") for (int ds_ = 0; ds_ < NDS; ++ds_) { \
;         if (ds_ < 2) kf[kb_ * NDS + ds_] = *(const LAS bf16x8*)(kp[ds_ & 1] + (sl) * KSLOT + (kb_ & 1) * 512 + (kb_ >> 1) * 4096); \
;         else kf[kb_ * NDS + ds_] = *(const LAS bf16x8*)(krp + (sl) * KSLOT + (kb_ & 1) * 256 + (kb_ >> 1) * 2048); } } while (0)
; #define ATT_QK() do { _Pragma("unroll") for (int kb_ = 0; kb_ < NKW; ++kb_) _Pragma("unroll") for (int ds_ = 0; ds_ < NDS; ++ds_) _Pragma("unroll") for (int qb_ = 0; qb_ < NQB; ++qb_) \
;         c[kb_][qb_] = __builtin_amdgcn_mfma_f32_16x16x32_bf16(kf[kb_ * NDS + ds_], qf[qb_ * NDS + ds_], ds_ == 0 ? zero4 : c[kb_][qb_], 0, 0, 0); } while (0)
; #define ATT_VLOAD(sl, h_) do { _Pragma("unroll") for (int g_ = 0; g_ < NVF; ++g_) { \
;         if constexpr (KS) vf[g_] = *(const LAS bf16x8*)(vpk + (sl) * VSLOT + g_ * 2048); \
;         else vf[g_] = *(const LAS bf16x8*)(vp[g_ & 1] + (sl) * VSLOT + ((h_) * 4 + (g_ >> 1)) * 2048); } } while (0)
; #define ATT_PVP(h_) do { _Pragma("unroll") for (int g_ = 0; g_ < NVF; ++g_) _Pragma("unroll") for (int qb_ = 0; qb_ < NQB; ++qb_) { \
;         const int db_ = KS ? g_ : (h_) * 4 + (g_ >> 1), sq_ = KS ? 0 : (g_ & 1); \
;         o[db_][qb_] = __builtin_amdgcn_mfma_f32_16x16x32_bf16(vf[g_], __builtin_bit_cast(bf16x8, pw[sq_ * NQB + qb_]), o[db_][qb_], 0, 0, 0); } } while (0)
; template <int DQK, int DV, bool LEAD> ...
;     ...
;             if constexpr (DV == 128) {
;                 ATT_PVP(0); ATT_SB();
;                 ATT_VLOAD(s_prev, 1); ATT_SB();
;                 ATT_QK(); ATT_SB();
;                 if (one_) { ATT_KLOAD(s_next); ATT_SB(); ATT_PVP(1); }
;                 ATT_SB();
	s_lshl_b32 s38, s47, 13
	v_add_u32_e32 v102, s38, v194
	v_add_u32_e32 v110, s38, v220
	ds_read_b128 v[82:85], v102
	ds_read_b128 v[86:89], v102 offset:512
	ds_read_b128 v[90:93], v110
	ds_read_b128 v[94:97], v110 offset:512
	ds_read_b128 v[98:101], v102 offset:4096
	ds_read_b128 v[102:105], v102 offset:4608
	ds_read_b128 v[106:109], v110 offset:4096
	ds_read_b128 v[110:113], v110 offset:4608
	s_waitcnt lgkmcnt(14)
	v_mfma_f32_16x16x32_bf16 v[38:41], v[186:189], v[146:149], v[38:41]
	v_mfma_f32_16x16x32_bf16 v[34:37], v[186:189], v[150:153], v[34:37]
	v_mfma_f32_16x16x32_bf16 v[30:33], v[174:177], v[146:149], v[30:33]
	v_mfma_f32_16x16x32_bf16 v[26:29], v[174:177], v[150:153], v[26:29]
	s_waitcnt lgkmcnt(11)
	v_mfma_f32_16x16x32_bf16 v[22:25], v[170:173], v[146:149], v[22:25]
	v_mfma_f32_16x16x32_bf16 v[18:21], v[170:173], v[150:153], v[18:21]
	s_waitcnt lgkmcnt(10)
	v_mfma_f32_16x16x32_bf16 v[14:17], v[162:165], v[146:149], v[14:17]
	v_mfma_f32_16x16x32_bf16 v[6:9], v[162:165], v[150:153], v[6:9]
	v_mfma_f32_16x16x32_bf16 v[38:41], v[190:193], v[154:157], v[38:41]
	v_mfma_f32_16x16x32_bf16 v[34:37], v[190:193], v[158:161], v[34:37]
	v_mfma_f32_16x16x32_bf16 v[30:33], v[178:181], v[154:157], v[30:33]
	v_mfma_f32_16x16x32_bf16 v[26:29], v[178:181], v[158:161], v[26:29]
	s_waitcnt lgkmcnt(9)
	v_mfma_f32_16x16x32_bf16 v[22:25], v[182:185], v[154:157], v[22:25]
	v_mfma_f32_16x16x32_bf16 v[18:21], v[182:185], v[158:161], v[18:21]
	s_waitcnt lgkmcnt(8)
	v_mfma_f32_16x16x32_bf16 v[14:17], v[166:169], v[154:157], v[14:17]
	v_mfma_f32_16x16x32_bf16 v[6:9], v[166:169], v[158:161], v[6:9]

; template <int DQK, int DV, bool LEAD> ...
;     ...
;     const int krow_l = wid * 8 + (lane >> 3);
;     const int kc_l = (lane & 7) ^ (((krow_l >> 1) & 1) | (((krow_l >> 3) & 1) << 1) | (((krow_l >> 4) & 1) << 2));
;     const int vc_l = (lane & 7) ^ ((krow_l >> 1) & 7);
;     const bf16_t* ksrc = K + (size_t)(krow0 + krow_l) * kpitch + kc_l * 8;
;     const int rrow_l = (wid & 3) * 16 + (lane >> 2), rc_l = (lane & 3) ^ (((rrow_l >> 4) & 1) << 1);
;     const bf16_t* krsrc = (DQK == 96) ? KR + (size_t)(krow0 + rrow_l) * 32 + rc_l * 8 : nullptr;
;     const bf16_t* vsrc = Vt + (size_t)krow_l * NR + krow0 + vc_l * 8;
;     const unsigned kdst = lds0 + KOFF + wid * 1024, krdst = lds0 + KOFF + 8192 + (wid & 3) * 1024, vdst = lds0 + VOFF + wid * 1024;
;     ...
;     const int kr0 = 8 * (q16 >> 2) + (q16 & 3);
;     const int fk = ((kr0 >> 1) & 1) | (((kr0 >> 3) & 1) << 1) | (((kr0 >> 4) & 1) << 2);
;     const LAS unsigned char* kp[2]; const LAS unsigned char* vp[2];
; #pragma unroll
;     for (int ds = 0; ds < 2; ++ds) kp[ds] = shm + KOFF + kr0 * 128 + ((((ds << 2) | g4) ^ fk) << 4) + kg * 4096;
;     const LAS unsigned char* krp = shm + KOFF + 8192 + kr0 * 64 + ((g4 ^ (((kr0 >> 4) & 1) << 1)) << 4) + kg * 2048;
; #pragma unroll
;     for (int s_ = 0; s_ < 2; ++s_) vp[s_] = shm + VOFF + q16 * 128 + ((((s_ << 2) | g4) ^ ((q16 >> 1) & 7)) << 4);
;     const LAS unsigned char* vpk = kg ? vp[1] : vp[0];
;     ...
;     ATT_DMA_K(0, 0); ATT_DMA_V(0, 0); ATT_DMA_K(1, 1); ATT_DMA_K(2, 2);
;     bf16x8 qf[NQB * NDS];
;     {
;       const float c2 = (DQK == 64) ? C2_EVEN : C2_ODD; const bool lat = tq0 >= 0;
; #pragma unroll
;       for (int qb = 0; qb < NQB; ++qb) {
;           const bf16_t* qp = Q + (size_t)(qrow0 + qoff + qb * 16 + q16) * qpitch + g4 * 8;
;           bf16x8 raw[NDS];
; #pragma unroll
;           for (int ds = 0; ds < NDS; ++ds) raw[ds] = *(const bf16x8*)(qp + ds * 32);
;           float x[NDS][8];
; #pragma unroll
;           for (int ds = 0; ds < NDS; ++ds)
; #pragma unroll
;               for (int j = 0; j < 8; ++j) x[ds][j] = __uint_as_float(((unsigned)(unsigned short)raw[ds][j]) << 16);
;           const int tq = tq0 + qoff + qb * 16 + q16, prow = (tq >> 6) & 127, pcol = tq & 63;
;           float sn = 0.f;
; #pragma unroll
;           for (int ds = 0; ds < 2; ++ds)
; #pragma unroll
;               for (int j = 0; j < 8; ++j) sn += x[ds][j] * x[ds][j];
.LBB0_946:
	s_and_b64 vcc, exec, s[4:5]
	s_cbranch_vccz .LBB0_938
	v_mov_b32_e32 v79, v0
	s_ashr_i32 s47, s46, 31
	v_readfirstlane_b32 s4, v79
	s_ashr_i32 s7, s4, 6
	v_bfe_u32 v1, v79, 3, 3
	v_lshl_or_b32 v6, s7, 3, v1
	s_lshl_b32 s5, s7, 1
	s_lshr_b32 s4, s4, 5
	v_ashrrev_i32_e32 v2, 1, v6
	s_and_b32 s5, s5, 2
	s_and_b32 s4, s4, 4
	v_and_b32_e32 v170, 7, v79
	v_and_b32_e32 v3, 1, v2
	s_or_b32 s4, s5, s4
	v_bitop3_b32 v7, s4, v170, v3 bitop3:0x36
	v_xor_b32_e32 v8, v2, v79
	v_add_u32_e32 v4, s46, v6
	s_lshl_b32 s4, s7, 10
	v_mov_b64_e32 v[2:3], s[40:41]
	s_add_i32 s31, s4, 0
	v_mad_i64_i32 v[2:3], s[4:5], v4, s92, v[2:3]
	v_mov_b64_e32 v[4:5], s[44:45]
	v_lshlrev_b32_e32 v194, 4, v7
	v_mad_i64_i32 v[4:5], s[4:5], v6, s91, v[4:5]
	v_lshl_add_u64 v[162:163], v[2:3], 0, v[194:195]
	v_lshlrev_b32_e32 v2, 4, v8
	v_lshl_add_u64 v[4:5], s[46:47], 1, v[4:5]
	v_and_b32_e32 v194, 0x70, v2
	s_mov_b32 m0, s31
	s_nop 0
	global_load_lds_dwordx4 v[162:163], off
	v_lshl_add_u64 v[164:165], v[4:5], 0, v[194:195]
	s_add_i32 s40, s31, 0x9000
	s_mov_b32 m0, s40
	s_nop 0
	global_load_lds_dwordx4 v[164:165], off
	s_mov_b64 s[4:5], 0x840000
	v_lshl_add_u64 v[166:167], v[164:165], 0, s[4:5]
	s_add_i32 s4, s40, 0x2000
	s_mov_b32 m0, s4
	s_nop 0
	global_load_lds_dwordx4 v[166:167], off
	s_mov_b64 s[4:5], 0x38000
	v_lshl_add_u64 v[2:3], v[162:163], 0, s[4:5]
	s_add_i32 s4, s31, 0x2000
	s_mov_b32 m0, s4
	s_nop 0
	global_load_lds_dwordx4 v[2:3], off
	s_lshl_b32 s16, s7, 5
	s_mov_b64 s[4:5], 0x70000
	v_and_b32_e32 v78, 15, v79
	v_lshl_add_u64 v[2:3], v[162:163], 0, s[4:5]
	s_add_i32 s6, s16, s30
	v_and_b32_e32 v194, 48, v79
	s_add_i32 s4, s31, 0x4000
	s_mov_b32 m0, s4
	s_nop 0
	global_load_lds_dwordx4 v[2:3], off
	v_or_b32_e32 v4, s6, v78
	v_lshl_add_u64 v[2:3], s[36:37], 0, v[194:195]
	v_lshrrev_b32_e32 v38, 1, v79
	v_or_b32_e32 v5, s16, v78
	v_mad_i64_i32 v[26:27], s[4:5], v4, s92, v[2:3]
	v_and_b32_e32 v28, 8, v38
	v_lshlrev_b32_e32 v5, 4, v5
	s_movk_i32 s4, 0x2f0
	v_or_b32_e32 v4, 16, v4
	v_and_or_b32 v5, v5, s4, v28
	v_mad_i64_i32 v[30:31], s[4:5], v4, s92, v[2:3]
	s_add_i32 s16, s16, s25
	s_lshr_b32 s4, s16, 2
	v_lshlrev_b32_e32 v22, 3, v5
	s_and_b32 s4, s4, 0x7f0
	global_load_dwordx4 v[50:53], v[26:27], off offset:64
	global_load_dwordx4 v[60:63], v22, s[8:9] offset:48
	global_load_dwordx4 v[70:73], v[30:31], off offset:64
	global_load_dwordx4 v[10:13], v22, s[8:9] offset:2096
	global_load_dwordx4 v[54:57], v22, s[8:9] offset:32
	global_load_dwordx4 v[14:17], v22, s[8:9] offset:2080
	global_load_dwordx4 v[2:5], v22, s[8:9] offset:16
	global_load_dwordx4 v[18:21], v22, s[8:9] offset:2064
	global_load_dwordx4 v[6:9], v22, s[8:9]
	s_nop 0
	global_load_dwordx4 v[22:25], v22, s[8:9] offset:2048
	s_nop 0
	global_load_dwordx4 v[82:85], v[26:27], off
	v_or_b32_e32 v26, s4, v28
	v_lshlrev_b32_e32 v39, 3, v26
	global_load_dwordx4 v[26:29], v39, s[8:9] offset:48
	global_load_dwordx4 v[86:89], v[30:31], off
	s_nop 0
	global_load_dwordx4 v[30:33], v39, s[8:9] offset:32
	global_load_dwordx4 v[34:37], v39, s[8:9] offset:16
	v_bfe_u32 v171, v79, 4, 2
	v_lshlrev_b32_e32 v172, 1, v79
	v_and_b32_e32 v40, 3, v79
	v_and_or_b32 v40, v172, 24, v40
	v_bitop3_b32 v38, v171, v38, 7 bitop3:0x78
	v_lshlrev_b32_e32 v59, 5, v171
	v_lshl_add_u32 v81, v40, 7, 0
	v_lshlrev_b32_e32 v80, 4, v38
	global_load_dwordx4 v[38:41], v39, s[8:9]
	s_nop 0
	global_load_dwordx4 v[42:45], v59, s[28:29] offset:144
	global_load_dwordx4 v[46:49], v59, s[28:29] offset:128
	v_and_b32_e32 v58, 63, v79
	v_cmp_gt_u32_e32 vcc, 32, v58
	s_mov_b32 s4, 0x3c800000
	v_add_u32_e32 v173, v81, v80
	v_lshlrev_b32_e32 v175, 7, v78
	s_mov_b32 s25, 1
	s_mov_b32 s16, 2
	v_or_b32_e32 v174, 4, v171
	s_waitcnt vmcnt(15)
	v_and_b32_e32 v65, 0xffff0000, v73
	v_lshlrev_b32_e32 v64, 16, v73
	v_and_b32_e32 v67, 0xffff0000, v72
	v_lshlrev_b32_e32 v66, 16, v72
	s_waitcnt vmcnt(13)
	v_cndmask_b32_e64 v95, v57, -v57, vcc
	v_cndmask_b32_e64 v94, v55, -v55, vcc
	v_and_b32_e32 v91, 0xffff0000, v53
	v_lshlrev_b32_e32 v90, 16, v53
	v_and_b32_e32 v93, 0xffff0000, v52
	s_waitcnt vmcnt(5)
	v_and_b32_e32 v73, 0xffff0000, v89
	v_lshlrev_b32_e32 v72, 16, v89
	v_and_b32_e32 v75, 0xffff0000, v88
	v_lshlrev_b32_e32 v74, 16, v88
	v_and_b32_e32 v89, 0xffff0000, v83
	v_lshlrev_b32_e32 v88, 16, v83
	v_and_b32_e32 v83, 0xffff0000, v82
	v_lshlrev_b32_e32 v92, 16, v52
	v_mov_b32_e32 v55, v56
	v_and_b32_e32 v97, 0xffff0000, v51
	v_lshlrev_b32_e32 v96, 16, v51
	v_cndmask_b32_e64 v98, v3, -v3, vcc
	v_mov_b32_e32 v3, v4
	v_and_b32_e32 v101, 0xffff0000, v50
	v_lshlrev_b32_e32 v100, 16, v50
	global_load_dwordx4 v[50:53], v59, s[28:29] offset:16
	s_nop 0
	global_load_dwordx4 v[56:59], v59, s[28:29]
	v_lshlrev_b32_e32 v82, 16, v82
	v_mul_f32_e32 v4, v83, v83
	v_cndmask_b32_e64 v99, v5, -v5, vcc
	v_pk_fma_f32 v[4:5], v[82:83], v[82:83], v[4:5] op_sel_hi:[1,1,0]
	v_mul_f32_e32 v104, v89, v89
	v_pk_fma_f32 v[4:5], v[88:89], v[88:89], v[4:5]
	v_cndmask_b32_e64 v103, v9, -v9, vcc
	v_cndmask_b32_e64 v102, v7, -v7, vcc
	v_mov_b32_e32 v7, v8
	v_and_b32_e32 v9, 0xffff0000, v85
	v_lshlrev_b32_e32 v8, 16, v85
	v_and_b32_e32 v85, 0xffff0000, v84
	v_lshlrev_b32_e32 v84, 16, v84
	v_pk_add_f32 v[4:5], v[104:105], v[4:5] op_sel_hi:[0,1]
	v_pk_fma_f32 v[4:5], v[84:85], v[84:85], v[4:5]
	v_mul_f32_e32 v104, v85, v85
	v_pk_add_f32 v[4:5], v[104:105], v[4:5] op_sel_hi:[0,1]
	v_pk_fma_f32 v[4:5], v[8:9], v[8:9], v[4:5]
	v_mul_f32_e32 v104, v9, v9
	v_pk_add_f32 v[4:5], v[104:105], v[4:5] op_sel_hi:[0,1]
	v_pk_fma_f32 v[4:5], v[100:101], v[100:101], v[4:5]
	v_mul_f32_e32 v104, v101, v101
	v_pk_add_f32 v[4:5], v[104:105], v[4:5] op_sel_hi:[0,1]
	v_pk_fma_f32 v[4:5], v[96:97], v[96:97], v[4:5]
	v_mul_f32_e32 v104, v97, v97
	v_pk_add_f32 v[4:5], v[104:105], v[4:5] op_sel_hi:[0,1]
	v_pk_fma_f32 v[4:5], v[92:93], v[92:93], v[4:5]
	v_mul_f32_e32 v104, v93, v93
	v_pk_add_f32 v[4:5], v[104:105], v[4:5] op_sel_hi:[0,1]
	v_pk_fma_f32 v[4:5], v[90:91], v[90:91], v[4:5]
	v_mul_f32_e32 v104, v91, v91
	v_pk_add_f32 v[4:5], v[104:105], v[4:5] op_sel_hi:[0,1]
	v_mov_b32_e32 v5, v4
	s_nop 1
	v_permlane16_swap_b32_e32 v4, v5
	v_add_f32_e32 v5, v4, v5
	v_cndmask_b32_e64 v77, v63, -v63, vcc
	v_cndmask_b32_e64 v76, v61, -v61, vcc
	v_mov_b32_e32 v61, v62
	v_cndmask_b32_e64 v63, v13, -v13, vcc
	v_cndmask_b32_e64 v62, v11, -v11, vcc
	v_mov_b32_e32 v11, v12
	v_cndmask_b32_e64 v13, v17, -v17, vcc
	v_cndmask_b32_e64 v12, v15, -v15, vcc
	v_mov_b32_e32 v15, v16
	v_cndmask_b32_e64 v17, v21, -v21, vcc
	v_cndmask_b32_e64 v16, v19, -v19, vcc
	v_mov_b32_e32 v19, v20
	v_cndmask_b32_e64 v21, v25, -v25, vcc
	v_cndmask_b32_e64 v20, v23, -v23, vcc
	v_mov_b32_e32 v23, v24
	v_cndmask_b32_e64 v25, v29, -v29, vcc
	v_cndmask_b32_e64 v24, v27, -v27, vcc
	v_mov_b32_e32 v27, v28
	s_waitcnt vmcnt(6)
; template <int DQK, int DV, bool LEAD> ...
;     ...
;           float sn = 0.f;
; #pragma unroll
;           for (int ds = 0; ds < 2; ++ds)
; #pragma unroll
;               for (int j = 0; j < 8; ++j) sn += x[ds][j] * x[ds][j];
;           sn = lanes4_sum(sn);
;           const float rn = rsqrtf(sn * (1.f / 64.f) + EPS);
; #pragma unroll
;           for (int ds = 0; ds < 2; ++ds)
; #pragma unroll
;               for (int j = 0; j < 8; ++j) x[ds][j] *= rn * qgain[32 * ds + 8 * g4 + j];
;           if constexpr (DQK == 64) {
; #pragma unroll
;               for (int ds = 0; ds < 2; ++ds)
; #pragma unroll
;                   for (int j = 0; j < 8; ++j) {
;                       auto rr = __builtin_amdgcn_permlane32_swap(__float_as_uint(x[ds][j]), __float_as_uint(x[ds][j]), false, false);
;                       const float other = hi ? __uint_as_float(rr[0]) : __uint_as_float(rr[1]);
;                       float cc = 1.f, sg = 0.f;
;                       if (lat) { const f32x2 cs = rope[(ds ? pcol : prow) * 16 + 8 * (g4 & 1) + j]; cc = cs.x; sg = hi ? cs.y : -cs.y; }
;                       x[ds][j] = x[ds][j] * cc + other * sg; }
	v_cndmask_b32_e64 v29, v33, -v33, vcc
	v_cndmask_b32_e64 v28, v31, -v31, vcc
	v_mov_b32_e32 v31, v32
	s_waitcnt vmcnt(5)
	v_cndmask_b32_e64 v33, v37, -v37, vcc
	v_cndmask_b32_e64 v32, v35, -v35, vcc
	v_mov_b32_e32 v35, v36
	v_and_b32_e32 v37, 0xffff0000, v87
	v_lshlrev_b32_e32 v36, 16, v87
	v_mov_b32_e32 v87, v5
	v_and_b32_e32 v105, 0xffff0000, v86
	s_nop 0
	v_permlane32_swap_b32_e32 v5, v87
	v_lshlrev_b32_e32 v104, 16, v86
	v_mul_f32_e32 v4, v105, v105
	v_pk_fma_f32 v[106:107], v[104:105], v[104:105], v[4:5] op_sel_hi:[1,1,0]
	v_mul_f32_e32 v4, v37, v37
	v_pk_fma_f32 v[106:107], v[36:37], v[36:37], v[106:107]
	v_and_b32_e32 v69, 0xffff0000, v71
	v_pk_add_f32 v[106:107], v[4:5], v[106:107] op_sel_hi:[0,1]
	v_pk_fma_f32 v[106:107], v[74:75], v[74:75], v[106:107]
	v_mul_f32_e32 v4, v75, v75
	v_pk_add_f32 v[106:107], v[4:5], v[106:107] op_sel_hi:[0,1]
	v_pk_fma_f32 v[106:107], v[72:73], v[72:73], v[106:107]
	v_mul_f32_e32 v4, v73, v73
	v_lshlrev_b32_e32 v68, 16, v71
	v_and_b32_e32 v71, 0xffff0000, v70
	v_lshlrev_b32_e32 v70, 16, v70
	v_pk_add_f32 v[106:107], v[4:5], v[106:107] op_sel_hi:[0,1]
	v_pk_fma_f32 v[106:107], v[70:71], v[70:71], v[106:107]
	v_mul_f32_e32 v4, v71, v71
	v_pk_add_f32 v[106:107], v[4:5], v[106:107] op_sel_hi:[0,1]
	v_pk_fma_f32 v[106:107], v[68:69], v[68:69], v[106:107]
	v_mul_f32_e32 v4, v69, v69
	v_pk_add_f32 v[106:107], v[4:5], v[106:107] op_sel_hi:[0,1]
	v_pk_fma_f32 v[106:107], v[66:67], v[66:67], v[106:107]
	v_mul_f32_e32 v4, v67, v67
	v_pk_add_f32 v[106:107], v[4:5], v[106:107] op_sel_hi:[0,1]
	v_pk_fma_f32 v[106:107], v[64:65], v[64:65], v[106:107]
	v_mul_f32_e32 v4, v65, v65
	v_pk_add_f32 v[106:107], v[4:5], v[106:107] op_sel_hi:[0,1]
	v_mov_b32_e32 v4, v106
	s_nop 1
	v_permlane16_swap_b32_e32 v106, v4
	v_add_f32_e32 v4, v106, v4
	v_mov_b32_e32 v86, v4
	s_nop 1
	v_permlane32_swap_b32_e32 v4, v86
	v_pk_add_f32 v[4:5], v[4:5], v[86:87]
	s_waitcnt vmcnt(4)
	v_cndmask_b32_e64 v106, v39, -v39, vcc
	v_pk_fma_f32 v[86:87], v[4:5], s[4:5], v[196:197] op_sel_hi:[1,0,0]
	v_mov_b32_e32 v39, v40
	v_mul_f32_e32 v4, 0x4b800000, v87
	v_cmp_gt_f32_e64 s[4:5], s95, v87
	v_cndmask_b32_e64 v107, v41, -v41, vcc
	s_mov_b32 s28, 0
	v_cndmask_b32_e64 v4, v87, v4, s[4:5]
	v_rsq_f32_e32 v4, v4
	s_nop 0
	v_mul_f32_e32 v5, 0x45800000, v4
	v_cndmask_b32_e64 v40, v4, v5, s[4:5]
	s_waitcnt vmcnt(3)
	v_pk_mul_f32 v[4:5], v[40:41], v[44:45] op_sel_hi:[0,1]
	v_pk_mul_f32 v[4:5], v[4:5], v[90:91]
	v_cmp_gt_f32_e64 s[4:5], s95, v86
	v_mov_b32_e32 v41, v4
	v_mov_b32_e32 v87, v4
	v_mov_b32_e32 v90, v5
	v_mov_b32_e32 v91, v5
	v_permlane32_swap_b32_e32 v41, v87
	s_nop 0
	v_permlane32_swap_b32_e32 v90, v91
	v_cndmask_b32_e32 v91, v90, v91, vcc
	v_cndmask_b32_e32 v90, v41, v87, vcc
	v_pk_mul_f32 v[76:77], v[76:77], v[90:91]
	s_nop 0
	v_pk_fma_f32 v[4:5], v[4:5], v[60:61], v[76:77]
	v_pk_mul_f32 v[60:61], v[40:41], v[42:43] op_sel_hi:[0,1]
	v_pk_mul_f32 v[4:5], v[4:5], s[94:95] op_sel_hi:[1,0]
	v_pk_mul_f32 v[60:61], v[60:61], v[92:93]
	v_cvt_pk_bf16_f32 v5, v4, v5
	v_mov_b32_e32 v4, v60
	v_mov_b32_e32 v41, v60
	v_mov_b32_e32 v76, v61
	v_mov_b32_e32 v77, v61
	v_permlane32_swap_b32_e32 v4, v41
	s_nop 0
	v_permlane32_swap_b32_e32 v76, v77
	v_cndmask_b32_e32 v77, v76, v77, vcc
	v_cndmask_b32_e32 v76, v4, v41, vcc
	v_pk_mul_f32 v[76:77], v[94:95], v[76:77]
	s_nop 0
	v_pk_fma_f32 v[54:55], v[60:61], v[54:55], v[76:77]
	s_nop 0
	v_pk_mul_f32 v[54:55], v[54:55], s[94:95] op_sel_hi:[1,0]
	s_nop 0
	v_cvt_pk_bf16_f32 v4, v54, v55
	s_waitcnt vmcnt(2)
	v_pk_mul_f32 v[54:55], v[40:41], v[48:49] op_sel_hi:[0,1]
	v_pk_mul_f32 v[54:55], v[54:55], v[96:97]
	s_nop 0
	v_mov_b32_e32 v41, v54
	v_mov_b32_e32 v60, v54
	v_mov_b32_e32 v61, v55
	v_mov_b32_e32 v76, v55
	v_permlane32_swap_b32_e32 v41, v60
	s_nop 0
	v_permlane32_swap_b32_e32 v61, v76
	v_cndmask_b32_e32 v61, v61, v76, vcc
	v_cndmask_b32_e32 v60, v41, v60, vcc
	v_pk_mul_f32 v[60:61], v[98:99], v[60:61]
	s_nop 0
	v_pk_fma_f32 v[2:3], v[54:55], v[2:3], v[60:61]
	v_pk_mul_f32 v[54:55], v[46:47], v[40:41] op_sel_hi:[1,0]
	v_pk_mul_f32 v[2:3], v[2:3], s[94:95] op_sel_hi:[1,0]
	v_pk_mul_f32 v[54:55], v[54:55], v[100:101]
	v_cvt_pk_bf16_f32 v3, v2, v3
	v_mov_b32_e32 v2, v54
	v_mov_b32_e32 v41, v54
	v_mov_b32_e32 v60, v55
	v_mov_b32_e32 v61, v55
	v_permlane32_swap_b32_e32 v2, v41
	s_nop 0
	v_permlane32_swap_b32_e32 v60, v61
	v_cndmask_b32_e32 v61, v60, v61, vcc
	v_cndmask_b32_e32 v60, v2, v41, vcc
	v_pk_mul_f32 v[60:61], v[102:103], v[60:61]
	s_nop 0
	v_pk_fma_f32 v[6:7], v[54:55], v[6:7], v[60:61]
	s_nop 0
	v_pk_mul_f32 v[6:7], v[6:7], s[94:95] op_sel_hi:[1,0]
	s_nop 0
	v_cvt_pk_bf16_f32 v2, v6, v7
	s_waitcnt vmcnt(1)
	v_pk_mul_f32 v[6:7], v[52:53], v[40:41] op_sel_hi:[1,0]
	s_nop 0
	v_pk_mul_f32 v[6:7], v[6:7], v[8:9]
	s_nop 0
	v_mov_b32_e32 v8, v6
	v_mov_b32_e32 v41, v6
	v_mov_b32_e32 v9, v7
	v_mov_b32_e32 v54, v7
	v_permlane32_swap_b32_e32 v8, v41
	s_nop 0
	v_permlane32_swap_b32_e32 v9, v54
	v_cndmask_b32_e32 v9, v9, v54, vcc
	v_cndmask_b32_e32 v8, v8, v41, vcc
	v_pk_mul_f32 v[8:9], v[24:25], v[8:9]
	s_nop 0
	v_pk_fma_f32 v[6:7], v[6:7], v[26:27], v[8:9]
	s_nop 0
	v_pk_mul_f32 v[6:7], v[6:7], s[94:95] op_sel_hi:[1,0]
	s_nop 0
	v_cvt_pk_bf16_f32 v9, v6, v7
	v_pk_mul_f32 v[6:7], v[50:51], v[40:41] op_sel_hi:[1,0]
	s_nop 0
	v_pk_mul_f32 v[6:7], v[6:7], v[84:85]
	s_nop 0
	v_mov_b32_e32 v8, v6
	v_mov_b32_e32 v41, v6
	v_mov_b32_e32 v54, v7
	v_mov_b32_e32 v55, v7
	v_permlane32_swap_b32_e32 v8, v41
	s_nop 0
	v_permlane32_swap_b32_e32 v54, v55
	v_cndmask_b32_e32 v55, v54, v55, vcc
	v_cndmask_b32_e32 v54, v8, v41, vcc
	v_pk_mul_f32 v[54:55], v[28:29], v[54:55]
	s_nop 0
	v_pk_fma_f32 v[6:7], v[6:7], v[30:31], v[54:55]
	s_nop 0
	v_pk_mul_f32 v[6:7], v[6:7], s[94:95] op_sel_hi:[1,0]
	s_nop 0
	v_cvt_pk_bf16_f32 v8, v6, v7
	s_waitcnt vmcnt(0)
; __device__ __forceinline__ unsigned cvtpk(float lo, float hi) { f32x2 v = {lo, hi}; bf16x2_t b = __builtin_convertvector(v, bf16x2_t); return __builtin_bit_cast(unsigned, b); }
; template <int DQK, int DV, bool LEAD> ...
;     ...
; #pragma unroll
;           for (int ds = 0; ds < 2; ++ds)
; #pragma unroll
;               for (int j = 0; j < 8; ++j) x[ds][j] *= rn * qgain[32 * ds + 8 * g4 + j];
;           if constexpr (DQK == 64) {
; #pragma unroll
;               for (int ds = 0; ds < 2; ++ds)
; #pragma unroll
;                   for (int j = 0; j < 8; ++j) {
;                       auto rr = __builtin_amdgcn_permlane32_swap(__float_as_uint(x[ds][j]), __float_as_uint(x[ds][j]), false, false);
;                       const float other = hi ? __uint_as_float(rr[0]) : __uint_as_float(rr[1]);
;                       float cc = 1.f, sg = 0.f;
;                       if (lat) { const f32x2 cs = rope[(ds ? pcol : prow) * 16 + 8 * (g4 & 1) + j]; cc = cs.x; sg = hi ? cs.y : -cs.y; }
;                       x[ds][j] = x[ds][j] * cc + other * sg; }
;           } else {
;               float sr = 0.f;
; #pragma unroll
;               for (int j = 0; j < 8; ++j) sr += x[2][j] * x[2][j];
;               sr = lanes4_sum(sr);
;               const float rq = rsqrtf(sr * (1.f / 32.f) + EPS);
; #pragma unroll
;               for (int j = 0; j < 8; ++j) { const float av = x[2][j] * rq * qgain[64 + 8 * g4 + j];
;                   auto rr = __builtin_amdgcn_permlane16_swap(__float_as_uint(av), __float_as_uint(av), false, false);
;                   const float other = (g4 & 1) ? __uint_as_float(rr[0]) : __uint_as_float(rr[1]);
;                   float cc = 1.f, sg = 0.f;
;                   if (lat) { const f32x2 cs = rope[((g4 & 2) ? pcol : prow) * 8 + j]; cc = cs.x; sg = (g4 & 1) ? cs.y : -cs.y; }
;                   x[2][j] = av * cc + other * sg; }
;           }
; #pragma unroll
;           for (int ds = 0; ds < NDS; ++ds) { u32x4 w;
; #pragma unroll
;               for (int i = 0; i < 4; ++i) w[i] = cvtpk(x[ds][2 * i] * c2, x[ds][2 * i + 1] * c2);
;               qf[qb * NDS + ds] = __builtin_bit_cast(bf16x8, w); }
;       }
; #pragma unroll
;       for (int d0 = 0; d0 < NQB * NDS; ++d0) asm volatile("" : "+v"(qf[d0])); }
;     wait_bar<0>();
	v_pk_mul_f32 v[6:7], v[58:59], v[40:41] op_sel_hi:[1,0]
	s_nop 0
	v_pk_mul_f32 v[6:7], v[6:7], v[88:89]
	s_nop 0
	v_mov_b32_e32 v41, v6
	v_mov_b32_e32 v54, v6
	v_mov_b32_e32 v55, v7
	v_mov_b32_e32 v60, v7
	v_permlane32_swap_b32_e32 v41, v54
	s_nop 0
	v_permlane32_swap_b32_e32 v55, v60
	v_cndmask_b32_e32 v55, v55, v60, vcc
	v_cndmask_b32_e32 v54, v41, v54, vcc
	v_pk_mul_f32 v[54:55], v[32:33], v[54:55]
	v_pk_mul_f32 v[40:41], v[56:57], v[40:41] op_sel_hi:[1,0]
	v_pk_fma_f32 v[6:7], v[6:7], v[34:35], v[54:55]
	v_pk_mul_f32 v[40:41], v[40:41], v[82:83]
	v_pk_mul_f32 v[6:7], v[6:7], s[94:95] op_sel_hi:[1,0]
	v_mov_b32_e32 v54, v40
	v_cvt_pk_bf16_f32 v7, v6, v7
	v_mov_b32_e32 v6, v40
	s_nop 1
	v_permlane32_swap_b32_e32 v6, v54
	v_mov_b32_e32 v55, v41
	v_mov_b32_e32 v60, v41
	v_cndmask_b32_e32 v54, v6, v54, vcc
	v_mul_f32_e32 v6, 0x4b800000, v86
	v_permlane32_swap_b32_e32 v55, v60
	v_cndmask_b32_e64 v6, v86, v6, s[4:5]
	v_cndmask_b32_e32 v55, v55, v60, vcc
	v_rsq_f32_e32 v60, v6
	v_pk_mul_f32 v[54:55], v[106:107], v[54:55]
	s_nop 0
	v_pk_fma_f32 v[40:41], v[40:41], v[38:39], v[54:55]
	s_nop 0
	v_pk_mul_f32 v[40:41], v[40:41], s[94:95] op_sel_hi:[1,0]
	s_nop 0
	v_cvt_pk_bf16_f32 v6, v40, v41
	v_mul_f32_e32 v40, 0x45800000, v60
	v_cndmask_b32_e64 v40, v60, v40, s[4:5]
	v_pk_mul_f32 v[54:55], v[56:57], v[40:41] op_sel_hi:[1,0]
	v_pk_mul_f32 v[56:57], v[58:59], v[40:41] op_sel_hi:[1,0]
	v_pk_mul_f32 v[54:55], v[54:55], v[104:105]
	v_pk_mul_f32 v[36:37], v[56:57], v[36:37]
	v_pk_mul_f32 v[50:51], v[50:51], v[40:41] op_sel_hi:[1,0]
	v_pk_mul_f32 v[52:53], v[52:53], v[40:41] op_sel_hi:[1,0]
	v_pk_mul_f32 v[46:47], v[46:47], v[40:41] op_sel_hi:[1,0]
	v_pk_mul_f32 v[48:49], v[48:49], v[40:41] op_sel_hi:[1,0]
	v_pk_mul_f32 v[42:43], v[42:43], v[40:41] op_sel_hi:[1,0]
	v_pk_mul_f32 v[40:41], v[44:45], v[40:41] op_sel_hi:[1,0]
	v_mov_b32_e32 v44, v54
	v_mov_b32_e32 v56, v54
	v_mov_b32_e32 v45, v55
	v_mov_b32_e32 v57, v55
	v_permlane32_swap_b32_e32 v44, v56
	s_nop 0
	v_permlane32_swap_b32_e32 v45, v57
	v_cndmask_b32_e32 v45, v45, v57, vcc
	v_cndmask_b32_e32 v44, v44, v56, vcc
	v_pk_mul_f32 v[38:39], v[38:39], v[54:55]
	v_mov_b32_e32 v54, v36
	v_pk_fma_f32 v[38:39], v[106:107], v[44:45], v[38:39]
	v_mov_b32_e32 v44, v36
	v_mov_b32_e32 v45, v37
	v_mov_b32_e32 v55, v37
	v_permlane32_swap_b32_e32 v44, v54
	s_nop 0
	v_permlane32_swap_b32_e32 v45, v55
	v_pk_mul_f32 v[50:51], v[50:51], v[74:75]
	v_cndmask_b32_e32 v45, v45, v55, vcc
	v_cndmask_b32_e32 v44, v44, v54, vcc
	v_pk_mul_f32 v[34:35], v[34:35], v[36:37]
	v_mov_b32_e32 v36, v50
	v_pk_fma_f32 v[32:33], v[32:33], v[44:45], v[34:35]
	v_mov_b32_e32 v34, v50
	v_mov_b32_e32 v35, v51
	v_mov_b32_e32 v37, v51
	v_permlane32_swap_b32_e32 v34, v36
	s_nop 0
	v_permlane32_swap_b32_e32 v35, v37
	v_cndmask_b32_e32 v35, v35, v37, vcc
	v_cndmask_b32_e32 v34, v34, v36, vcc
	v_pk_mul_f32 v[52:53], v[52:53], v[72:73]
	v_pk_mul_f32 v[28:29], v[28:29], v[34:35]
	v_mov_b32_e32 v34, v52
	v_pk_fma_f32 v[28:29], v[30:31], v[50:51], v[28:29]
	v_mov_b32_e32 v30, v52
	v_mov_b32_e32 v31, v53
	v_mov_b32_e32 v35, v53
	v_permlane32_swap_b32_e32 v30, v34
	s_nop 0
	v_permlane32_swap_b32_e32 v31, v35
	v_cndmask_b32_e32 v31, v31, v35, vcc
	v_cndmask_b32_e32 v30, v30, v34, vcc
	v_pk_mul_f32 v[46:47], v[46:47], v[70:71]
	v_pk_mul_f32 v[24:25], v[24:25], v[30:31]
	v_mov_b32_e32 v30, v46
	v_pk_fma_f32 v[24:25], v[52:53], v[26:27], v[24:25]
	v_mov_b32_e32 v26, v46
	v_mov_b32_e32 v27, v47
	v_mov_b32_e32 v31, v47
	v_permlane32_swap_b32_e32 v26, v30
	s_nop 0
	v_permlane32_swap_b32_e32 v27, v31
	v_cndmask_b32_e32 v27, v27, v31, vcc
	v_cndmask_b32_e32 v26, v26, v30, vcc
	v_pk_mul_f32 v[48:49], v[48:49], v[68:69]
	v_pk_mul_f32 v[20:21], v[20:21], v[26:27]
	v_mov_b32_e32 v26, v48
	v_pk_fma_f32 v[20:21], v[46:47], v[22:23], v[20:21]
	v_mov_b32_e32 v22, v48
	v_mov_b32_e32 v23, v49
	v_mov_b32_e32 v27, v49
	v_permlane32_swap_b32_e32 v22, v26
	s_nop 0
	v_permlane32_swap_b32_e32 v23, v27
	v_cndmask_b32_e32 v23, v23, v27, vcc
	v_cndmask_b32_e32 v22, v22, v26, vcc
	v_pk_mul_f32 v[42:43], v[42:43], v[66:67]
	v_pk_mul_f32 v[16:17], v[16:17], v[22:23]
	v_mov_b32_e32 v22, v42
	v_pk_fma_f32 v[16:17], v[48:49], v[18:19], v[16:17]
	v_mov_b32_e32 v18, v42
	v_mov_b32_e32 v19, v43
	v_mov_b32_e32 v23, v43
	v_permlane32_swap_b32_e32 v18, v22
	s_nop 0
	v_permlane32_swap_b32_e32 v19, v23
	v_cndmask_b32_e32 v19, v19, v23, vcc
	v_cndmask_b32_e32 v18, v18, v22, vcc
	v_pk_mul_f32 v[40:41], v[40:41], v[64:65]
	v_pk_mul_f32 v[12:13], v[12:13], v[18:19]
	v_pk_mul_f32 v[16:17], v[16:17], s[94:95] op_sel_hi:[1,0]
	v_pk_fma_f32 v[18:19], v[42:43], v[14:15], v[12:13]
	v_mov_b32_e32 v12, v40
	v_mov_b32_e32 v14, v40
	v_mov_b32_e32 v13, v41
	v_mov_b32_e32 v15, v41
	v_permlane32_swap_b32_e32 v12, v14
	s_nop 0
	v_permlane32_swap_b32_e32 v13, v15
	v_cndmask_b32_e32 v13, v13, v15, vcc
	v_cndmask_b32_e32 v12, v12, v14, vcc
	v_pk_mul_f32 v[12:13], v[62:63], v[12:13]
	v_pk_mul_f32 v[14:15], v[24:25], s[94:95] op_sel_hi:[1,0]
	v_pk_fma_f32 v[22:23], v[40:41], v[10:11], v[12:13]
	v_pk_mul_f32 v[10:11], v[38:39], s[94:95] op_sel_hi:[1,0]
	v_pk_mul_f32 v[12:13], v[32:33], s[94:95] op_sel_hi:[1,0]
	v_cvt_pk_bf16_f32 v10, v10, v11
	v_cvt_pk_bf16_f32 v11, v12, v13
	v_pk_mul_f32 v[12:13], v[28:29], s[94:95] op_sel_hi:[1,0]
	v_bfe_u32 v30, v79, 1, 3
	v_cvt_pk_bf16_f32 v12, v12, v13
	v_cvt_pk_bf16_f32 v13, v14, v15
	v_pk_mul_f32 v[14:15], v[20:21], s[94:95] op_sel_hi:[1,0]
	v_bitop3_b32 v30, v171, v30, 4 bitop3:0x36
	v_cvt_pk_bf16_f32 v14, v14, v15
	v_cvt_pk_bf16_f32 v15, v16, v17
	v_pk_mul_f32 v[16:17], v[18:19], s[94:95] op_sel_hi:[1,0]
	v_pk_mul_f32 v[18:19], v[22:23], s[94:95] op_sel_hi:[1,0]
	v_cvt_pk_bf16_f32 v16, v16, v17
	v_cvt_pk_bf16_f32 v17, v18, v19
	s_waitcnt vmcnt(0) lgkmcnt(0)
	s_barrier
; #define ATT_SB() __builtin_amdgcn_sched_barrier(0)
; #define ATT_DMA_K(t, sl) do { glds16(ksrc + (size_t)(t) * 64 * kpitch, (unsigned)__builtin_amdgcn_readfirstlane(kdst + (sl) * KSLOT)); \
;         if constexpr (DQK == 96) glds16(krsrc + (size_t)(t) * 64 * 32, (unsigned)__builtin_amdgcn_readfirstlane(krdst + (sl) * KSLOT)); } while (0)
; #define ATT_DMA_V(t, sl) do { glds16(vsrc + (size_t)(t) * 64, (unsigned)__builtin_amdgcn_readfirstlane(vdst + (sl) * VSLOT)); \
;         if constexpr (DV == 128) glds16(vsrc + (size_t)64 * NR + (size_t)(t) * 64, (unsigned)__builtin_amdgcn_readfirstlane(vdst + (sl) * VSLOT + 8192)); } while (0)
; #define ATT_KLOAD(sl) do { _Pragma("unroll") for (int kb_ = 0; kb_ < NKW; ++kb_) _Pragma("unroll") for (int ds_ = 0; ds_ < NDS; ++ds_) { \
;         if (ds_ < 2) kf[kb_ * NDS + ds_] = *(const LAS bf16x8*)(kp[ds_ & 1] + (sl) * KSLOT + (kb_ & 1) * 512 + (kb_ >> 1) * 4096); \
;         else kf[kb_ * NDS + ds_] = *(const LAS bf16x8*)(krp + (sl) * KSLOT + (kb_ & 1) * 256 + (kb_ >> 1) * 2048); } } while (0)
; #define ATT_QK() do { _Pragma("unroll") for (int kb_ = 0; kb_ < NKW; ++kb_) _Pragma("unroll") for (int ds_ = 0; ds_ < NDS; ++ds_) _Pragma("unroll") for (int qb_ = 0; qb_ < NQB; ++qb_) \
;         c[kb_][qb_] = __builtin_amdgcn_mfma_f32_16x16x32_bf16(kf[kb_ * NDS + ds_], qf[qb_ * NDS + ds_], ds_ == 0 ? zero4 : c[kb_][qb_], 0, 0, 0); } while (0)
; #define ATT_EXP() do { _Pragma("unroll") for (int kb_ = 0; kb_ < NKW; ++kb_) _Pragma("unroll") for (int qb_ = 0; qb_ < NQB; ++qb_) _Pragma("unroll") for (int i_ = 0; i_ < 4; ++i_) \
;         c[kb_][qb_][i_] = __builtin_amdgcn_exp2f(c[kb_][qb_][i_]); } while (0)
; template <int DQK, int DV, bool LEAD> ...
;     ...
;     wait_bar<0>();
;     bf16x8 kf[NKW * NDS], vf[NVF];
;     ATT_KLOAD(0);
;     asm volatile("s_waitcnt lgkmcnt(0)\n\ts_barrier" ::: "memory");
;     float lsum[NQB];
; #pragma unroll
;     for (int qb = 0; qb < NQB; ++qb) lsum[qb] = 0.f;
;     const f32x4 zero4 = {0.f, 0.f, 0.f, 0.f};
;     f32x4 o[NDB][NQB], c[NKW][NQB]; u32x4 pw[4];
; #pragma unroll
;     for (int i = 0; i < NDB; ++i)
; #pragma unroll
;         for (int qb = 0; qb < NQB; ++qb) o[i][qb] = zero4;
;     ATT_DMA_K(3, 0); ATT_DMA_V(1, 1);
;     ATT_QK(); ATT_SB();
;     ATT_KLOAD(1); ATT_SB();
;     if constexpr (LEAD) { ATT_EXP(); ATT_SUMPACK(); }
;     wait_bar<NDMA>();
;     int s_prev = 0, s_cur = 1, s_next = 2;
	ds_read_b128 v[18:21], v173
	ds_read_b128 v[22:25], v173 offset:512
	v_lshlrev_b32_e32 v54, 4, v30
	v_add_u32_e32 v176, v81, v54
	s_waitcnt lgkmcnt(1)
	v_mfma_f32_16x16x32_bf16 v[26:29], v[18:21], v[6:9], 0
	ds_read_b128 v[30:33], v176
	ds_read_b128 v[34:37], v176 offset:512
	v_add_u32_e32 v55, 0, v175
	v_add_u32_e32 v178, v55, v80
	v_mfma_f32_16x16x32_bf16 v[18:21], v[18:21], v[10:13], 0
	v_add_u32_e32 v177, v55, v54
	s_waitcnt lgkmcnt(1)
	v_mfma_f32_16x16x32_bf16 v[26:29], v[30:33], v[2:5], v[26:29]
	v_mfma_f32_16x16x32_bf16 v[18:21], v[30:33], v[14:17], v[18:21]
	v_mfma_f32_16x16x32_bf16 v[30:33], v[22:25], v[6:9], 0
	v_mfma_f32_16x16x32_bf16 v[22:25], v[22:25], v[10:13], 0
	s_waitcnt lgkmcnt(0)
	v_mfma_f32_16x16x32_bf16 v[30:33], v[34:37], v[2:5], v[30:33]
	v_mfma_f32_16x16x32_bf16 v[22:25], v[34:37], v[14:17], v[22:25]
	ds_read_b128 v[34:37], v173 offset:4096
	ds_read_b128 v[38:41], v173 offset:4608
	ds_read_b128 v[46:49], v176 offset:4096
	ds_read_b128 v[50:53], v176 offset:4608
	s_waitcnt lgkmcnt(3)
	v_mfma_f32_16x16x32_bf16 v[42:45], v[34:37], v[6:9], 0
	s_waitcnt lgkmcnt(0)
	s_barrier
	v_mfma_f32_16x16x32_bf16 v[34:37], v[34:37], v[10:13], 0
	s_waitcnt lgkmcnt(1)
	v_mfma_f32_16x16x32_bf16 v[58:61], v[46:49], v[14:17], v[34:37]
	v_mfma_f32_16x16x32_bf16 v[34:37], v[38:41], v[6:9], 0
	v_mfma_f32_16x16x32_bf16 v[38:41], v[38:41], v[10:13], 0
	v_mfma_f32_16x16x32_bf16 v[42:45], v[46:49], v[2:5], v[42:45]
	v_lshl_add_u64 v[46:47], v[162:163], 0, s[96:97]
	s_mov_b32 m0, s31
	s_nop 0
	global_load_lds_dwordx4 v[46:47], off
	v_lshl_add_u64 v[46:47], v[164:165], 0, s[66:67]
	s_add_i32 s4, s40, 0x4000
	s_mov_b32 m0, s4
	s_nop 0
	global_load_lds_dwordx4 v[46:47], off
	s_mov_b64 s[4:5], 0x840080
	s_waitcnt lgkmcnt(0)
	v_mfma_f32_16x16x32_bf16 v[74:77], v[50:53], v[2:5], v[34:37]
	v_lshl_add_u64 v[46:47], v[164:165], 0, s[4:5]
	s_add_i32 s4, s40, 0x6000
	s_mov_b32 m0, s4
	s_nop 0
	global_load_lds_dwordx4 v[46:47], off
	v_mfma_f32_16x16x32_bf16 v[78:81], v[50:53], v[14:17], v[38:41]
	ds_read_b128 v[34:37], v173 offset:8192
	s_nop 1
	ds_read_b128 v[38:41], v173 offset:8704
	ds_read_b128 v[46:49], v176 offset:8192
	ds_read_b128 v[50:53], v176 offset:8704
	ds_read_b128 v[54:57], v173 offset:12288
	ds_read_b128 v[62:65], v173 offset:12800
	ds_read_b128 v[66:69], v176 offset:12288
	ds_read_b128 v[70:73], v176 offset:12800
	v_exp_f32_e32 v26, v26
	v_exp_f32_e32 v27, v27
	v_exp_f32_e32 v28, v28
	v_exp_f32_e32 v29, v29
	v_exp_f32_e32 v86, v18
	v_exp_f32_e32 v87, v19
	v_exp_f32_e32 v20, v20
	v_exp_f32_e32 v21, v21
	v_exp_f32_e32 v30, v30
	v_exp_f32_e32 v22, v22
	v_add_f32_e32 v18, v26, v27
	v_add_f32_e32 v19, v28, v29
	v_exp_f32_e32 v31, v31
	v_exp_f32_e32 v23, v23
	v_add_f32_e32 v18, v18, v19
	v_add_f32_e32 v19, v86, v87
	v_add_f32_e32 v82, v20, v21
	v_add_f32_e32 v19, v19, v82
	v_exp_f32_e32 v32, v32
	v_exp_f32_e32 v24, v24
	v_add_f32_e32 v18, v18, v30
	v_add_f32_e32 v19, v19, v22
	v_exp_f32_e32 v33, v33
	v_exp_f32_e32 v25, v25
	v_add_f32_e32 v18, v31, v18
	v_add_f32_e32 v19, v23, v19
	v_exp_f32_e32 v42, v42
	v_exp_f32_e32 v58, v58
	v_add_f32_e32 v18, v32, v18
	v_add_f32_e32 v19, v24, v19
	v_exp_f32_e32 v43, v43
	v_exp_f32_e32 v59, v59
	v_add_f32_e32 v18, v33, v18
	v_add_f32_e32 v19, v25, v19
	v_exp_f32_e32 v44, v44
	v_exp_f32_e32 v60, v60
	v_add_f32_e32 v18, v42, v18
	v_add_f32_e32 v19, v58, v19
	v_exp_f32_e32 v45, v45
	v_exp_f32_e32 v61, v61
	v_add_f32_e32 v18, v43, v18
	v_add_f32_e32 v19, v59, v19
	v_exp_f32_e32 v74, v74
	v_exp_f32_e32 v78, v78
	v_add_f32_e32 v18, v44, v18
	v_add_f32_e32 v19, v60, v19
	v_exp_f32_e32 v75, v75
	v_exp_f32_e32 v79, v79
	v_add_f32_e32 v18, v45, v18
	v_add_f32_e32 v19, v61, v19
	v_exp_f32_e32 v76, v76
	v_exp_f32_e32 v80, v80
	v_add_f32_e32 v18, v74, v18
	v_add_f32_e32 v19, v78, v19
	v_exp_f32_e32 v77, v77
	v_exp_f32_e32 v81, v81
	v_add_f32_e32 v18, v75, v18
	v_add_f32_e32 v19, v79, v19
	s_mov_b32 s4, 1
	v_add_f32_e32 v18, v76, v18
	v_add_f32_e32 v82, v80, v19
	v_cvt_pk_bf16_f32 v83, v28, v29
	v_add_f32_e32 v19, v77, v18
	v_add_f32_e32 v18, v81, v82
	s_waitcnt vmcnt(3) lgkmcnt(0)
	s_barrier
	s_cmp_lg_u32 s4, 0
	v_pk_add_f32 v[168:169], v[18:19], 0 op_sel_hi:[1,0]
	v_mov_b32_e32 v18, 0
	v_cvt_pk_bf16_f32 v82, v26, v27
	v_cvt_pk_bf16_f32 v84, v30, v31
	v_cvt_pk_bf16_f32 v85, v32, v33
	v_cvt_pk_bf16_f32 v94, v86, v87
	v_cvt_pk_bf16_f32 v95, v20, v21
	v_cvt_pk_bf16_f32 v96, v22, v23
	v_cvt_pk_bf16_f32 v97, v24, v25
	v_cvt_pk_bf16_f32 v98, v42, v43
	v_cvt_pk_bf16_f32 v99, v44, v45
	v_cvt_pk_bf16_f32 v100, v74, v75
	v_cvt_pk_bf16_f32 v101, v76, v77
	v_cvt_pk_bf16_f32 v102, v58, v59
	v_cvt_pk_bf16_f32 v103, v60, v61
	v_cvt_pk_bf16_f32 v104, v78, v79
	v_cvt_pk_bf16_f32 v105, v80, v81
	s_cselect_b64 s[4:5], -1, 0
	s_mov_b32 s30, 2
	v_mov_b32_e32 v19, v18
	v_mov_b32_e32 v20, v18
	v_mov_b32_e32 v21, v18
	v_mov_b32_e32 v22, v18
	v_mov_b32_e32 v23, v18
	v_mov_b32_e32 v24, v18
	v_mov_b32_e32 v25, v18
	v_mov_b32_e32 v26, v18
	v_mov_b32_e32 v27, v18
	v_mov_b32_e32 v28, v18
	v_mov_b32_e32 v29, v18
	v_mov_b32_e32 v30, v18
	v_mov_b32_e32 v31, v18
	v_mov_b32_e32 v32, v18
	v_mov_b32_e32 v33, v18
	v_mov_b32_e32 v42, v18
	v_mov_b32_e32 v43, v18
	v_mov_b32_e32 v44, v18
	v_mov_b32_e32 v45, v18
	v_mov_b32_e32 v58, v18
	v_mov_b32_e32 v59, v18
	v_mov_b32_e32 v60, v18
	v_mov_b32_e32 v61, v18
	v_mov_b32_e32 v74, v18
	v_mov_b32_e32 v75, v18
	v_mov_b32_e32 v76, v18
	v_mov_b32_e32 v77, v18
	v_mov_b32_e32 v78, v18
	v_mov_b32_e32 v79, v18
	v_mov_b32_e32 v80, v18
	v_mov_b32_e32 v81, v18
	v_mov_b32_e32 v86, v18
	v_mov_b32_e32 v87, v18
	v_mov_b32_e32 v88, v18
	v_mov_b32_e32 v89, v18
	v_mov_b32_e32 v90, v18
	v_mov_b32_e32 v91, v18
	v_mov_b32_e32 v92, v18
	v_mov_b32_e32 v93, v18
	v_mov_b32_e32 v106, v18
	v_mov_b32_e32 v107, v18
	v_mov_b32_e32 v108, v18
	v_mov_b32_e32 v109, v18
	v_mov_b32_e32 v110, v18
	v_mov_b32_e32 v111, v18
	v_mov_b32_e32 v112, v18
	v_mov_b32_e32 v113, v18
	v_mov_b32_e32 v114, v18
	v_mov_b32_e32 v115, v18
	v_mov_b32_e32 v116, v18
	v_mov_b32_e32 v117, v18
	v_mov_b32_e32 v118, v18
	v_mov_b32_e32 v119, v18
	v_mov_b32_e32 v120, v18
	v_mov_b32_e32 v121, v18
	v_mov_b32_e32 v122, v18
	v_mov_b32_e32 v123, v18
	v_mov_b32_e32 v124, v18
	v_mov_b32_e32 v125, v18
	v_mov_b32_e32 v126, v18
	v_mov_b32_e32 v127, v18
	v_mov_b32_e32 v128, v18
	v_mov_b32_e32 v129, v18
; #define ATT_SB() __builtin_amdgcn_sched_barrier(0)
; #define ATT_DMA_K(t, sl) do { glds16(ksrc + (size_t)(t) * 64 * kpitch, (unsigned)__builtin_amdgcn_readfirstlane(kdst + (sl) * KSLOT)); \
;         if constexpr (DQK == 96) glds16(krsrc + (size_t)(t) * 64 * 32, (unsigned)__builtin_amdgcn_readfirstlane(krdst + (sl) * KSLOT)); } while (0)
; #define ATT_DMA_V(t, sl) do { glds16(vsrc + (size_t)(t) * 64, (unsigned)__builtin_amdgcn_readfirstlane(vdst + (sl) * VSLOT)); \
;         if constexpr (DV == 128) glds16(vsrc + (size_t)64 * NR + (size_t)(t) * 64, (unsigned)__builtin_amdgcn_readfirstlane(vdst + (sl) * VSLOT + 8192)); } while (0)
; #define ATT_KLOAD(sl) do { _Pragma("unroll") for (int kb_ = 0; kb_ < NKW; ++kb_) _Pragma("unroll") for (int ds_ = 0; ds_ < NDS; ++ds_) { \
;         if (ds_ < 2) kf[kb_ * NDS + ds_] = *(const LAS bf16x8*)(kp[ds_ & 1] + (sl) * KSLOT + (kb_ & 1) * 512 + (kb_ >> 1) * 4096); \
;         else kf[kb_ * NDS + ds_] = *(const LAS bf16x8*)(krp + (sl) * KSLOT + (kb_ & 1) * 256 + (kb_ >> 1) * 2048); } } while (0)
; #define ATT_QK() do { _Pragma("unroll") for (int kb_ = 0; kb_ < NKW; ++kb_) _Pragma("unroll") for (int ds_ = 0; ds_ < NDS; ++ds_) _Pragma("unroll") for (int qb_ = 0; qb_ < NQB; ++qb_) \
;         c[kb_][qb_] = __builtin_amdgcn_mfma_f32_16x16x32_bf16(kf[kb_ * NDS + ds_], qf[qb_ * NDS + ds_], ds_ == 0 ? zero4 : c[kb_][qb_], 0, 0, 0); } while (0)
; template <int DQK, int DV, bool LEAD> ...
;     ...
;     for (int t = 1; t < NT; ++t) {
;         __builtin_amdgcn_s_waitcnt(0xC07F);
;         if constexpr (!LEAD) { ATT_EXP(); ATT_SUMPACK(); ATT_SB(); }
;         ATT_VLOAD(s_prev, 0); ATT_SB();
;         { const int tk = (t + 3 < NT) ? t + 3 : NT - 1; ATT_DMA_K(tk, s_cur); }
;         { const int tv = (t + 1 < NT) ? t + 1 : NT - 1; ATT_DMA_V(tv, s_next); }
;         ATT_SB();
;         if constexpr (LEAD) {
;             ATT_QK(); ATT_SB();
;             ATT_PVP(0); ATT_SB();
;             if constexpr (DV == 128) { ATT_VLOAD(s_prev, 1); ATT_SB(); ATT_EXP(); ATT_SB(); ATT_PVP(1); ATT_SB(); }
;             if (one_) ATT_KLOAD(s_next);
;             ATT_SB();
;             if constexpr (DV == 64) ATT_EXP();
;             ATT_SUMPACK();
;             asm volatile("" : "+v"(pw[0]), "+v"(pw[1]), "+v"(pw[2]), "+v"(pw[3]));
; #pragma unroll
;             for (int qb = 0; qb < NQB; ++qb) asm volatile("" : "+v"(lsum[qb]));
.LBB0_948:
	s_lshl_b32 s29, s28, 14
	v_add_u32_e32 v179, s29, v178
	s_waitcnt lgkmcnt(0)
	v_add_u32_e32 v192, s29, v177
	ds_read_b128 v[180:183], v179 offset:36864
	ds_read_b128 v[184:187], v179 offset:38912
	ds_read_b128 v[188:191], v192 offset:36864
	ds_read_b128 v[204:207], v192 offset:38912
	ds_read_b128 v[208:211], v179 offset:40960
	ds_read_b128 v[212:215], v179 offset:43008
	ds_read_b128 v[216:219], v192 offset:40960
	ds_read_b128 v[236:239], v192 offset:43008
	s_mov_b32 s29, s25
	s_mov_b32 s25, s30
	s_add_i32 s30, s16, -1
	s_min_u32 s30, s30, 0x80
	s_mul_i32 s38, s30, 0x38000
	s_lshl_b32 s30, s29, 13
	v_lshl_add_u64 v[130:131], v[162:163], 0, s[38:39]
	s_add_i32 s30, s30, s31
	v_lshl_add_u64 v[130:131], v[130:131], 0, s[96:97]
	s_mov_b32 m0, s30
	s_nop 0
	global_load_lds_dwordx4 v[130:131], off
	s_min_u32 s30, s16, 0x83
	s_lshl_b32 s38, s30, 7
	s_lshl_b32 s30, s25, 14
	v_lshl_add_u64 v[130:131], v[164:165], 0, s[38:39]
	s_add_i32 s30, s30, s40
	s_mov_b32 m0, s30
	s_nop 0
	global_load_lds_dwordx4 v[130:131], off
	v_lshl_add_u64 v[130:131], v[166:167], 0, s[38:39]
	s_addk_i32 s30, 0x2000
	s_mov_b32 m0, s30
	s_nop 0
	global_load_lds_dwordx4 v[130:131], off
	v_mfma_f32_16x16x32_bf16 v[130:133], v[34:37], v[6:9], 0
	v_mfma_f32_16x16x32_bf16 v[134:137], v[34:37], v[10:13], 0
	v_mfma_f32_16x16x32_bf16 v[158:161], v[46:49], v[2:5], v[130:133]
	v_mfma_f32_16x16x32_bf16 v[130:133], v[38:41], v[6:9], 0
	v_mfma_f32_16x16x32_bf16 v[154:157], v[46:49], v[14:17], v[134:137]
	v_mfma_f32_16x16x32_bf16 v[134:137], v[38:41], v[10:13], 0
	v_mfma_f32_16x16x32_bf16 v[150:153], v[50:53], v[2:5], v[130:133]
	v_mfma_f32_16x16x32_bf16 v[130:133], v[54:57], v[6:9], 0
	v_mfma_f32_16x16x32_bf16 v[146:149], v[50:53], v[14:17], v[134:137]
	v_mfma_f32_16x16x32_bf16 v[134:137], v[54:57], v[10:13], 0
	v_mfma_f32_16x16x32_bf16 v[142:145], v[66:69], v[2:5], v[130:133]
	v_mfma_f32_16x16x32_bf16 v[130:133], v[62:65], v[6:9], 0
	v_mfma_f32_16x16x32_bf16 v[240:243], v[62:65], v[10:13], 0
	v_mfma_f32_16x16x32_bf16 v[138:141], v[66:69], v[14:17], v[134:137]
	v_mfma_f32_16x16x32_bf16 v[134:137], v[70:73], v[2:5], v[130:133]
	v_mfma_f32_16x16x32_bf16 v[130:133], v[70:73], v[14:17], v[240:243]
	s_waitcnt lgkmcnt(7)
	v_mfma_f32_16x16x32_bf16 v[126:129], v[180:183], v[82:85], v[126:129]
	v_mfma_f32_16x16x32_bf16 v[122:125], v[180:183], v[94:97], v[122:125]
	s_waitcnt lgkmcnt(6)
	v_mfma_f32_16x16x32_bf16 v[118:121], v[184:187], v[82:85], v[118:121]
	v_mfma_f32_16x16x32_bf16 v[114:117], v[184:187], v[94:97], v[114:117]
	s_waitcnt lgkmcnt(3)
	v_mfma_f32_16x16x32_bf16 v[110:113], v[208:211], v[82:85], v[110:113]
	v_mfma_f32_16x16x32_bf16 v[106:109], v[208:211], v[94:97], v[106:109]
	s_waitcnt lgkmcnt(2)
	v_mfma_f32_16x16x32_bf16 v[90:93], v[212:215], v[82:85], v[90:93]
	v_mfma_f32_16x16x32_bf16 v[86:89], v[212:215], v[94:97], v[86:89]
	v_mfma_f32_16x16x32_bf16 v[126:129], v[188:191], v[98:101], v[126:129]
	v_mfma_f32_16x16x32_bf16 v[122:125], v[188:191], v[102:105], v[122:125]
	v_mfma_f32_16x16x32_bf16 v[118:121], v[204:207], v[98:101], v[118:121]
	v_mfma_f32_16x16x32_bf16 v[114:117], v[204:207], v[102:105], v[114:117]
	s_waitcnt lgkmcnt(1)
	v_mfma_f32_16x16x32_bf16 v[110:113], v[216:219], v[98:101], v[110:113]
	v_mfma_f32_16x16x32_bf16 v[106:109], v[216:219], v[102:105], v[106:109]
	s_waitcnt lgkmcnt(0)
	v_mfma_f32_16x16x32_bf16 v[90:93], v[236:239], v[98:101], v[90:93]
	v_mfma_f32_16x16x32_bf16 v[86:89], v[236:239], v[102:105], v[86:89]
	ds_read_b128 v[180:183], v179 offset:45056
	ds_read_b128 v[184:187], v179 offset:47104
	ds_read_b128 v[188:191], v192 offset:45056
	ds_read_b128 v[204:207], v192 offset:47104
	ds_read_b128 v[208:211], v179 offset:49152
	ds_read_b128 v[212:215], v179 offset:51200
	ds_read_b128 v[216:219], v192 offset:49152
	ds_read_b128 v[236:239], v192 offset:51200
	s_waitcnt lgkmcnt(7)
	v_mfma_f32_16x16x32_bf16 v[78:81], v[180:183], v[82:85], v[78:81]
	v_mfma_f32_16x16x32_bf16 v[74:77], v[180:183], v[94:97], v[74:77]
	s_waitcnt lgkmcnt(6)
	v_mfma_f32_16x16x32_bf16 v[58:61], v[184:187], v[82:85], v[58:61]
	v_mfma_f32_16x16x32_bf16 v[42:45], v[184:187], v[94:97], v[42:45]
	s_waitcnt lgkmcnt(3)
	v_mfma_f32_16x16x32_bf16 v[30:33], v[208:211], v[82:85], v[30:33]
	v_mfma_f32_16x16x32_bf16 v[26:29], v[208:211], v[94:97], v[26:29]
	s_waitcnt lgkmcnt(2)
	v_mfma_f32_16x16x32_bf16 v[22:25], v[212:215], v[82:85], v[22:25]
	v_mfma_f32_16x16x32_bf16 v[18:21], v[212:215], v[94:97], v[18:21]
	v_mfma_f32_16x16x32_bf16 v[78:81], v[188:191], v[98:101], v[78:81]
	v_mfma_f32_16x16x32_bf16 v[74:77], v[188:191], v[102:105], v[74:77]
	v_mfma_f32_16x16x32_bf16 v[58:61], v[204:207], v[98:101], v[58:61]
	v_mfma_f32_16x16x32_bf16 v[42:45], v[204:207], v[102:105], v[42:45]
	s_waitcnt lgkmcnt(1)
	v_mfma_f32_16x16x32_bf16 v[30:33], v[216:219], v[98:101], v[30:33]
	v_mfma_f32_16x16x32_bf16 v[26:29], v[216:219], v[102:105], v[26:29]
	s_waitcnt lgkmcnt(0)
	v_mfma_f32_16x16x32_bf16 v[22:25], v[236:239], v[98:101], v[22:25]
	v_mfma_f32_16x16x32_bf16 v[18:21], v[236:239], v[102:105], v[18:21]
	s_andn2_b64 vcc, exec, s[4:5]
	s_cbranch_vccnz .LBB0_950
	s_lshl_b32 s30, s25, 13
	v_add_u32_e32 v62, s30, v173
	v_add_u32_e32 v70, s30, v176
	ds_read_b128 v[34:37], v62
	ds_read_b128 v[38:41], v62 offset:512
	ds_read_b128 v[46:49], v70
	ds_read_b128 v[50:53], v70 offset:512
	ds_read_b128 v[54:57], v62 offset:4096
	ds_read_b128 v[62:65], v62 offset:4608
	ds_read_b128 v[66:69], v70 offset:4096
	ds_read_b128 v[70:73], v70 offset:4608

; #define LAS __attribute__((address_space(3)))
; template <int DQK, int DV, bool LEAD> ...
;     ...
;     const int tid = tid_, lane = tid & 63, q16 = lane & 15, g4 = lane >> 4, hi = lane >> 5; const int wid = __builtin_amdgcn_readfirstlane(tid >> 6);
;     const int kg = KS ? (wid >> 2) : 0, qoff = KS ? (wid & 3) * 64 : wid * 32;
;     const unsigned lds0 = (unsigned)(uintptr_t)shm;
;     const int krow_l = wid * 8 + (lane >> 3);
;     const int kc_l = (lane & 7) ^ (((krow_l >> 1) & 1) | (((krow_l >> 3) & 1) << 1) | (((krow_l >> 4) & 1) << 2));
;     const int vc_l = (lane & 7) ^ ((krow_l >> 1) & 7);
;     const bf16_t* ksrc = K + (size_t)(krow0 + krow_l) * kpitch + kc_l * 8;
;     const int rrow_l = (wid & 3) * 16 + (lane >> 2), rc_l = (lane & 3) ^ (((rrow_l >> 4) & 1) << 1);
;     const bf16_t* krsrc = (DQK == 96) ? KR + (size_t)(krow0 + rrow_l) * 32 + rc_l * 8 : nullptr;
;     const bf16_t* vsrc = Vt + (size_t)krow_l * NR + krow0 + vc_l * 8;
;     const unsigned kdst = lds0 + KOFF + wid * 1024, krdst = lds0 + KOFF + 8192 + (wid & 3) * 1024, vdst = lds0 + VOFF + wid * 1024;
;     ...
;     const int kr0 = 8 * (q16 >> 2) + (q16 & 3);
;     const int fk = ((kr0 >> 1) & 1) | (((kr0 >> 3) & 1) << 1) | (((kr0 >> 4) & 1) << 2);
;     const LAS unsigned char* kp[2]; const LAS unsigned char* vp[2];
; #pragma unroll
;     for (int ds = 0; ds < 2; ++ds) kp[ds] = shm + KOFF + kr0 * 128 + ((((ds << 2) | g4) ^ fk) << 4) + kg * 4096;
;     const LAS unsigned char* krp = shm + KOFF + 8192 + kr0 * 64 + ((g4 ^ (((kr0 >> 4) & 1) << 1)) << 4) + kg * 2048;
; #pragma unroll
;     for (int s_ = 0; s_ < 2; ++s_) vp[s_] = shm + VOFF + q16 * 128 + ((((s_ << 2) | g4) ^ ((q16 >> 1) & 7)) << 4);
;     const LAS unsigned char* vpk = kg ? vp[1] : vp[0];
;     ...
;     ATT_DMA_K(0, 0); ATT_DMA_V(0, 0); ATT_DMA_K(1, 1); ATT_DMA_K(2, 2);
;     bf16x8 qf[NQB * NDS];
;     {
;       const float c2 = (DQK == 64) ? C2_EVEN : C2_ODD; const bool lat = tq0 >= 0;
; #pragma unroll
;       for (int qb = 0; qb < NQB; ++qb) {
;           const bf16_t* qp = Q + (size_t)(qrow0 + qoff + qb * 16 + q16) * qpitch + g4 * 8;
;           bf16x8 raw[NDS];
; #pragma unroll
;           for (int ds = 0; ds < NDS; ++ds) raw[ds] = *(const bf16x8*)(qp + ds * 32);
.LBB0_955:
	s_bfe_u32 s46, s4, 0x10007
	s_lshr_b32 s5, s4, 8
	s_lshl_b32 s6, s46, 9
	s_add_u32 s6, s15, s6
	s_addc_u32 s7, s17, 0
	s_lshl_b32 s16, s4, 1
	s_and_b32 s16, s16, 0xc0
	s_lshl_b32 s43, s16, 1
	s_add_u32 s28, s6, s43
	s_addc_u32 s29, s7, 0
	s_lshl_b32 s6, s46, 7
	s_add_u32 s36, s24, s6
	s_addc_u32 s37, s25, 0
	s_mul_i32 s6, s46, 0x840000
	s_add_u32 s6, s10, s6
	s_addc_u32 s7, s11, 0
	s_add_u32 s40, s6, 0x4200000
	s_addc_u32 s41, s7, 0
	s_mov_b64 s[6:7], s[0:1]
	s_load_dwordx2 s[6:7], s[6:7], 0x60
	s_lshl_b32 s47, s4, 8
	s_mul_i32 s44, s5, 0x2100
	s_and_b32 s4, s47, 0x1f00
	s_add_i32 s48, s44, s4
	s_waitcnt lgkmcnt(0)
	s_add_u32 s26, s6, s22
	s_addc_u32 s27, s7, s23
	v_readfirstlane_b32 s4, v0
	s_cmpk_gt_u32 s4, 0xff
	s_mov_b64 s[4:5], -1
	s_cbranch_scc0 .LBB0_962
	v_mov_b32_e32 v162, v0
	s_ashr_i32 s45, s44, 31
	v_readfirstlane_b32 s6, v162
	s_ashr_i32 s4, s6, 6
	v_bfe_u32 v2, v162, 3, 3
	v_lshl_or_b32 v6, s4, 3, v2
	s_lshl_b32 s5, s4, 1
	s_lshr_b32 s7, s6, 5
	v_ashrrev_i32_e32 v3, 1, v6
	s_and_b32 s5, s5, 2
	s_and_b32 s7, s7, 4
	v_and_b32_e32 v2, 7, v162
	v_and_b32_e32 v4, 1, v3
	s_or_b32 s5, s5, s7
	v_bitop3_b32 v7, s5, v2, v4 bitop3:0x36
	v_xor_b32_e32 v8, v3, v162
	v_add_u32_e32 v4, s44, v6
	v_mov_b64_e32 v[2:3], s[36:37]
	s_and_b32 s49, s4, 3
	s_lshl_b32 s50, s4, 10
	v_mad_i64_i32 v[2:3], s[4:5], v4, s92, v[2:3]
	v_mov_b64_e32 v[4:5], s[40:41]
	v_lshlrev_b32_e32 v194, 4, v7
	v_mad_i64_i32 v[4:5], s[4:5], v6, s91, v[4:5]
	v_lshl_add_u64 v[164:165], v[2:3], 0, v[194:195]
	v_lshlrev_b32_e32 v2, 4, v8
	s_add_i32 s50, s50, 0
	v_lshl_add_u64 v[4:5], s[44:45], 1, v[4:5]
	v_and_b32_e32 v194, 0x70, v2
	s_mov_b32 m0, s50
	s_nop 0
	global_load_lds_dwordx4 v[164:165], off
	v_lshl_add_u64 v[166:167], v[4:5], 0, v[194:195]
	s_add_i32 s45, s50, 0x9000
	s_mov_b32 m0, s45
	s_nop 0
	global_load_lds_dwordx4 v[166:167], off
	s_mov_b64 s[4:5], 0x38000
	v_and_b32_e32 v1, 15, v162
	s_lshl_b32 s7, s49, 6
	v_lshl_add_u64 v[2:3], v[164:165], 0, s[4:5]
	s_add_i32 s4, s50, 0x2000
	s_mov_b32 m0, s4
	s_nop 0
	global_load_lds_dwordx4 v[2:3], off
	v_lshlrev_b32_e32 v163, 7, v1
	s_mov_b64 s[4:5], 0x70000
	v_or_b32_e32 v1, s7, v1
	v_and_b32_e32 v194, 48, v162
	v_lshrrev_b32_e32 v34, 1, v162
	v_lshl_add_u64 v[2:3], v[164:165], 0, s[4:5]
	s_add_i32 s4, s50, 0x4000
	v_or_b32_e32 v1, s48, v1
	v_lshl_add_u64 v[6:7], s[28:29], 0, v[194:195]
	s_mov_b32 m0, s4
	s_nop 0
	global_load_lds_dwordx4 v[2:3], off
	v_and_b32_e32 v35, 8, v34
	v_mad_i64_i32 v[8:9], s[4:5], v1, s92, v[6:7]
	v_or_b32_e32 v10, 16, v1
	v_or_b32_e32 v14, 32, v1
	v_or_b32_e32 v1, 48, v1
	v_lshl_or_b32 v194, v35, 3, v163
	v_mad_i64_i32 v[24:25], s[4:5], v10, s92, v[6:7]
	v_mad_i64_i32 v[26:27], s[4:5], v14, s92, v[6:7]
	v_mad_i64_i32 v[30:31], s[4:5], v1, s92, v[6:7]
	v_lshl_add_u64 v[22:23], s[8:9], 0, v[194:195]
	s_mov_b64 s[4:5], 0x1800
	v_lshl_add_u64 v[28:29], v[22:23], 0, s[60:61]
	v_lshl_add_u64 v[32:33], v[22:23], 0, s[4:5]
	s_movk_i32 s4, 0x1000
	global_load_dwordx4 v[72:75], v[8:9], off offset:64
	global_load_dwordx4 v[2:5], v194, s[8:9] offset:48
	global_load_dwordx4 v[128:131], v[24:25], off offset:64
	global_load_dwordx4 v[10:13], v194, s[8:9] offset:2096
	global_load_dwordx4 v[152:155], v[26:27], off offset:64
	global_load_dwordx4 v[68:71], v[28:29], off offset:48
	global_load_dwordx4 v[176:179], v[30:31], off offset:64
	global_load_dwordx4 v[14:17], v[32:33], off offset:48
	global_load_dwordx4 v[102:105], v194, s[8:9] offset:32
	global_load_dwordx4 v[94:97], v194, s[8:9] offset:2080
	global_load_dwordx4 v[64:67], v[28:29], off offset:32
	global_load_dwordx4 v[18:21], v[32:33], off offset:32
	global_load_dwordx4 v[110:113], v[8:9], off
	s_nop 0
	global_load_dwordx4 v[6:9], v194, s[8:9]
	global_load_dwordx4 v[106:109], v[24:25], off
	global_load_dwordx4 v[98:101], v194, s[8:9] offset:16
	global_load_dwordx4 v[82:85], v[26:27], off
	global_load_dwordx4 v[86:89], v194, s[8:9] offset:2064
	v_add_co_u32_e32 v26, vcc, s4, v22
	v_lshlrev_b32_e32 v22, 1, v162
	s_nop 0
	v_addc_co_u32_e32 v27, vcc, 0, v23, vcc
	v_and_b32_e32 v23, 3, v162
	global_load_dwordx4 v[56:59], v[26:27], off
	global_load_dwordx4 v[78:81], v[30:31], off
	global_load_dwordx4 v[60:63], v[28:29], off offset:16
	global_load_dwordx4 v[90:93], v194, s[8:9] offset:2048
	v_and_or_b32 v28, v22, 24, v23
	global_load_dwordx4 v[22:25], v[32:33], off offset:16
	s_lshl_b32 s4, s6, 4
	s_and_b32 s4, s4, 0xfffff000
	s_add_i32 s4, s4, 0
	v_lshl_add_u32 v170, v28, 7, s4
	s_or_b32 s4, s7, s47
	v_bfe_u32 v169, v162, 4, 2
	s_lshr_b32 s4, s4, 2
	v_bitop3_b32 v28, v169, v34, 7 bitop3:0x78
	s_and_b32 s4, s4, 0x7f0
	v_lshlrev_b32_e32 v168, 4, v28
	v_or_b32_e32 v28, s4, v35
	v_lshlrev_b32_e32 v28, 3, v28
	v_lshlrev_b32_e32 v76, 5, v169
	global_load_dwordx4 v[32:35], v28, s[8:9] offset:48
	global_load_dwordx4 v[36:39], v28, s[8:9] offset:32
	global_load_dwordx4 v[40:43], v28, s[8:9] offset:16
	global_load_dwordx4 v[44:47], v28, s[8:9]
	s_nop 0
	global_load_dwordx4 v[28:31], v[26:27], off offset:2048
	global_load_dwordx4 v[48:51], v76, s[26:27] offset:144
	global_load_dwordx4 v[52:55], v76, s[26:27] offset:128
	v_and_b32_e32 v1, 63, v162
	v_cmp_gt_u32_e32 vcc, 32, v1
	s_mov_b32 s4, 0x358637bd
	s_mov_b32 s12, 0x3c800000
	v_add_u32_e32 v174, v170, v168
	s_cmpk_lt_u32 s6, 0x100
	s_mov_b32 s51, 1
	s_mov_b32 s16, 2
	s_waitcnt vmcnt(22)
	v_cndmask_b32_e64 v115, v17, -v17, vcc
	v_cndmask_b32_e64 v114, v15, -v15, vcc
	v_mov_b32_e32 v15, v16
	s_waitcnt vmcnt(20)
	v_cndmask_b32_e64 v135, v97, -v97, vcc
	v_cndmask_b32_e64 v134, v95, -v95, vcc
	v_cndmask_b32_e64 v144, v3, -v3, vcc
	v_mov_b32_e32 v3, v4
	v_cndmask_b32_e64 v27, v13, -v13, vcc
	v_cndmask_b32_e64 v26, v11, -v11, vcc
	v_and_b32_e32 v117, 0xffff0000, v179
	v_lshlrev_b32_e32 v116, 16, v179
	s_waitcnt vmcnt(17)
; template <int DQK, int DV, bool LEAD> ...
;     ...
;           float x[NDS][8];
; #pragma unroll
;           for (int ds = 0; ds < NDS; ++ds)
; #pragma unroll
;               for (int j = 0; j < 8; ++j) x[ds][j] = __uint_as_float(((unsigned)(unsigned short)raw[ds][j]) << 16);
;           const int tq = tq0 + qoff + qb * 16 + q16, prow = (tq >> 6) & 127, pcol = tq & 63;
;           float sn = 0.f;
; #pragma unroll
;           for (int ds = 0; ds < 2; ++ds)
; #pragma unroll
;               for (int j = 0; j < 8; ++j) sn += x[ds][j] * x[ds][j];
;           sn = lanes4_sum(sn);
;           const float rn = rsqrtf(sn * (1.f / 64.f) + EPS);
; #pragma unroll
;           for (int ds = 0; ds < 2; ++ds)
; #pragma unroll
;               for (int j = 0; j < 8; ++j) x[ds][j] *= rn * qgain[32 * ds + 8 * g4 + j];
	v_and_b32_e32 v179, 0xffff0000, v110
	v_mov_b32_e32 v11, v12
	v_cndmask_b32_e64 v13, v105, -v105, vcc
	v_cndmask_b32_e64 v12, v103, -v103, vcc
	v_mov_b32_e32 v103, v104
	v_cndmask_b32_e64 v105, v67, -v67, vcc
	v_cndmask_b32_e64 v104, v65, -v65, vcc
	v_mov_b32_e32 v65, v66
	v_and_b32_e32 v67, 0xffff0000, v178
	v_lshlrev_b32_e32 v66, 16, v178
	v_lshlrev_b32_e32 v178, 16, v110
	v_mul_f32_e32 v4, v179, v179
	v_cndmask_b32_e64 v145, v5, -v5, vcc
	v_mov_b32_e32 v95, v96
	v_cndmask_b32_e64 v17, v21, -v21, vcc
	v_cndmask_b32_e64 v16, v19, -v19, vcc
	v_mov_b32_e32 v19, v20
	v_and_b32_e32 v97, 0xffff0000, v177
	v_lshlrev_b32_e32 v96, 16, v177
	s_waitcnt vmcnt(7)
	v_cndmask_b32_e64 v21, v25, -v25, vcc
	v_cndmask_b32_e64 v20, v23, -v23, vcc
	v_mov_b32_e32 v23, v24
	v_cndmask_b32_e64 v25, v93, -v93, vcc
	v_cndmask_b32_e64 v24, v91, -v91, vcc
	v_mov_b32_e32 v91, v92
	v_and_b32_e32 v93, 0xffff0000, v176
	v_lshlrev_b32_e32 v92, 16, v176
	v_and_b32_e32 v177, 0xffff0000, v111
	v_lshlrev_b32_e32 v176, 16, v111
	v_pk_fma_f32 v[4:5], v[178:179], v[178:179], v[4:5] op_sel_hi:[1,1,0]
	v_and_b32_e32 v149, 0xffff0000, v75
	v_lshlrev_b32_e32 v148, 16, v75
	v_cndmask_b32_e64 v119, v71, -v71, vcc
	v_cndmask_b32_e64 v118, v69, -v69, vcc
	v_mov_b32_e32 v69, v70
	v_and_b32_e32 v151, 0xffff0000, v74
	v_lshlrev_b32_e32 v150, 16, v74
	v_and_b32_e32 v157, 0xffff0000, v73
	v_lshlrev_b32_e32 v156, 16, v73
	v_and_b32_e32 v161, 0xffff0000, v72
	v_lshlrev_b32_e32 v160, 16, v72
	global_load_dwordx4 v[70:73], v76, s[26:27] offset:16
	s_nop 0
	global_load_dwordx4 v[74:77], v76, s[26:27]
	v_pk_fma_f32 v[4:5], v[176:177], v[176:177], v[4:5]
	v_mul_f32_e32 v110, v177, v177
	v_and_b32_e32 v173, 0xffff0000, v112
	v_lshlrev_b32_e32 v172, 16, v112
	v_pk_add_f32 v[4:5], v[110:111], v[4:5] op_sel_hi:[0,1]
	v_pk_fma_f32 v[4:5], v[172:173], v[172:173], v[4:5]
	v_mul_f32_e32 v110, v173, v173
	v_cndmask_b32_e64 v159, v9, -v9, vcc
	v_cndmask_b32_e64 v158, v7, -v7, vcc
	v_mov_b32_e32 v7, v8
	v_and_b32_e32 v9, 0xffff0000, v113
	v_lshlrev_b32_e32 v8, 16, v113
	v_pk_add_f32 v[4:5], v[110:111], v[4:5] op_sel_hi:[0,1]
	v_pk_fma_f32 v[4:5], v[8:9], v[8:9], v[4:5]
	v_mul_f32_e32 v110, v9, v9
	v_pk_add_f32 v[4:5], v[110:111], v[4:5] op_sel_hi:[0,1]
	v_pk_fma_f32 v[4:5], v[160:161], v[160:161], v[4:5]
	v_mul_f32_e32 v110, v161, v161
	v_pk_add_f32 v[4:5], v[110:111], v[4:5] op_sel_hi:[0,1]
	v_pk_fma_f32 v[4:5], v[156:157], v[156:157], v[4:5]
	v_mul_f32_e32 v110, v157, v157
	v_pk_add_f32 v[4:5], v[110:111], v[4:5] op_sel_hi:[0,1]
	v_pk_fma_f32 v[4:5], v[150:151], v[150:151], v[4:5]
	v_mul_f32_e32 v110, v151, v151
	v_pk_add_f32 v[4:5], v[110:111], v[4:5] op_sel_hi:[0,1]
	v_pk_fma_f32 v[4:5], v[148:149], v[148:149], v[4:5]
	v_mul_f32_e32 v110, v149, v149
	v_pk_add_f32 v[4:5], v[110:111], v[4:5] op_sel_hi:[0,1]
	v_mov_b32_e32 v5, v4
	s_nop 1
	v_permlane16_swap_b32_e32 v4, v5
	v_add_f32_e32 v5, v4, v5
	v_and_b32_e32 v127, 0xffff0000, v153
	v_lshlrev_b32_e32 v126, 16, v153
	v_and_b32_e32 v147, 0xffff0000, v107
	v_lshlrev_b32_e32 v146, 16, v107
	v_mov_b32_e32 v107, v5
	v_and_b32_e32 v153, 0xffff0000, v106
	v_and_b32_e32 v133, 0xffff0000, v131
	v_lshlrev_b32_e32 v132, 16, v131
	v_and_b32_e32 v137, 0xffff0000, v130
	v_lshlrev_b32_e32 v136, 16, v130
	v_and_b32_e32 v131, 0xffff0000, v152
	v_lshlrev_b32_e32 v130, 16, v152
	v_permlane32_swap_b32_e32 v5, v107
	v_lshlrev_b32_e32 v152, 16, v106
	v_mul_f32_e32 v4, v153, v153
	v_pk_fma_f32 v[110:111], v[152:153], v[152:153], v[4:5] op_sel_hi:[1,1,0]
	v_mul_f32_e32 v4, v147, v147
	v_pk_fma_f32 v[110:111], v[146:147], v[146:147], v[110:111]
	v_and_b32_e32 v113, 0xffff0000, v108
	v_lshlrev_b32_e32 v112, 16, v108
	v_pk_add_f32 v[110:111], v[4:5], v[110:111] op_sel_hi:[0,1]
	v_pk_fma_f32 v[110:111], v[112:113], v[112:113], v[110:111]
	v_mul_f32_e32 v4, v113, v113
	v_and_b32_e32 v143, 0xffff0000, v109
	v_lshlrev_b32_e32 v142, 16, v109
	v_pk_add_f32 v[110:111], v[4:5], v[110:111] op_sel_hi:[0,1]
	v_pk_fma_f32 v[110:111], v[142:143], v[142:143], v[110:111]
	v_mul_f32_e32 v4, v143, v143
	v_cndmask_b32_e64 v125, v63, -v63, vcc
	v_cndmask_b32_e64 v124, v61, -v61, vcc
	v_mov_b32_e32 v61, v62
	v_and_b32_e32 v63, 0xffff0000, v128
	v_lshlrev_b32_e32 v62, 16, v128
	v_pk_add_f32 v[110:111], v[4:5], v[110:111] op_sel_hi:[0,1]
	v_pk_fma_f32 v[110:111], v[62:63], v[62:63], v[110:111]
	v_mul_f32_e32 v4, v63, v63
	v_and_b32_e32 v141, 0xffff0000, v129
	v_lshlrev_b32_e32 v140, 16, v129
	v_pk_add_f32 v[110:111], v[4:5], v[110:111] op_sel_hi:[0,1]
	v_pk_fma_f32 v[110:111], v[140:141], v[140:141], v[110:111]
	v_mul_f32_e32 v4, v141, v141
	v_pk_add_f32 v[110:111], v[4:5], v[110:111] op_sel_hi:[0,1]
	v_pk_fma_f32 v[110:111], v[136:137], v[136:137], v[110:111]
	v_mul_f32_e32 v4, v137, v137
	v_pk_add_f32 v[110:111], v[4:5], v[110:111] op_sel_hi:[0,1]
	v_pk_fma_f32 v[110:111], v[132:133], v[132:133], v[110:111]
	v_mul_f32_e32 v4, v133, v133
	v_pk_add_f32 v[110:111], v[4:5], v[110:111] op_sel_hi:[0,1]
	v_mov_b32_e32 v4, v110
	s_nop 1
	v_permlane16_swap_b32_e32 v110, v4
	v_add_f32_e32 v4, v110, v4
	v_mov_b32_e32 v106, v4
	s_nop 1
	v_permlane32_swap_b32_e32 v4, v106
	v_pk_add_f32 v[4:5], v[4:5], v[106:107]
	v_mov_b64_e32 v[110:111], s[4:5]
	v_pk_fma_f32 v[180:181], v[4:5], s[12:13], v[110:111] op_sel_hi:[1,0,0]
	s_waitcnt vmcnt(5)
	v_cndmask_b32_e64 v106, v45, -v45, vcc
	v_mul_f32_e32 v4, 0x4b800000, v181
	v_cmp_gt_f32_e64 s[4:5], s95, v181
	v_mov_b32_e32 v45, v46
	v_cndmask_b32_e64 v139, v89, -v89, vcc
	v_cndmask_b32_e64 v4, v181, v4, s[4:5]
	v_rsq_f32_e32 v4, v4
	v_cndmask_b32_e64 v138, v87, -v87, vcc
	v_mov_b32_e32 v87, v88
	s_waitcnt vmcnt(4)
; __device__ __forceinline__ unsigned cvtpk(float lo, float hi) { f32x2 v = {lo, hi}; bf16x2_t b = __builtin_convertvector(v, bf16x2_t); return __builtin_bit_cast(unsigned, b); }
; template <int DQK, int DV, bool LEAD> ...
;     ...
; #pragma unroll
;           for (int ds = 0; ds < 2; ++ds)
; #pragma unroll
;               for (int j = 0; j < 8; ++j) x[ds][j] *= rn * qgain[32 * ds + 8 * g4 + j];
;           if constexpr (DQK == 64) {
; #pragma unroll
;               for (int ds = 0; ds < 2; ++ds)
; #pragma unroll
;                   for (int j = 0; j < 8; ++j) {
;                       auto rr = __builtin_amdgcn_permlane32_swap(__float_as_uint(x[ds][j]), __float_as_uint(x[ds][j]), false, false);
;                       const float other = hi ? __uint_as_float(rr[0]) : __uint_as_float(rr[1]);
;                       float cc = 1.f, sg = 0.f;
;                       if (lat) { const f32x2 cs = rope[(ds ? pcol : prow) * 16 + 8 * (g4 & 1) + j]; cc = cs.x; sg = hi ? cs.y : -cs.y; }
;                       x[ds][j] = x[ds][j] * cc + other * sg; }
;           } else {
;               float sr = 0.f;
; #pragma unroll
;               for (int j = 0; j < 8; ++j) sr += x[2][j] * x[2][j];
;               sr = lanes4_sum(sr);
;               const float rq = rsqrtf(sr * (1.f / 32.f) + EPS);
; #pragma unroll
;               for (int j = 0; j < 8; ++j) { const float av = x[2][j] * rq * qgain[64 + 8 * g4 + j];
;                   auto rr = __builtin_amdgcn_permlane16_swap(__float_as_uint(av), __float_as_uint(av), false, false);
;                   const float other = (g4 & 1) ? __uint_as_float(rr[0]) : __uint_as_float(rr[1]);
;                   float cc = 1.f, sg = 0.f;
;                   if (lat) { const f32x2 cs = rope[((g4 & 2) ? pcol : prow) * 8 + j]; cc = cs.x; sg = (g4 & 1) ? cs.y : -cs.y; }
;                   x[2][j] = av * cc + other * sg; }
;           }
; #pragma unroll
;           for (int ds = 0; ds < NDS; ++ds) { u32x4 w;
; #pragma unroll
;               for (int i = 0; i < 4; ++i) w[i] = cvtpk(x[ds][2 * i] * c2, x[ds][2 * i + 1] * c2);
;               qf[qb * NDS + ds] = __builtin_bit_cast(bf16x8, w); }
	v_cndmask_b32_e64 v89, v31, -v31, vcc
	v_mul_f32_e32 v5, 0x45800000, v4
	v_cndmask_b32_e64 v46, v4, v5, s[4:5]
	s_waitcnt vmcnt(3)
	v_pk_mul_f32 v[4:5], v[46:47], v[50:51] op_sel_hi:[0,1]
	v_pk_mul_f32 v[4:5], v[4:5], v[148:149]
	v_cndmask_b32_e64 v88, v29, -v29, vcc
	v_mov_b32_e32 v29, v30
	v_cndmask_b32_e64 v31, v35, -v35, vcc
	v_cndmask_b32_e64 v30, v33, -v33, vcc
	v_mov_b32_e32 v33, v34
	v_cndmask_b32_e64 v35, v39, -v39, vcc
	v_cndmask_b32_e64 v34, v37, -v37, vcc
	v_mov_b32_e32 v37, v38
	v_cndmask_b32_e64 v39, v43, -v43, vcc
	v_cndmask_b32_e64 v38, v41, -v41, vcc
	v_mov_b32_e32 v41, v42
	v_and_b32_e32 v109, 0xffff0000, v83
	v_lshlrev_b32_e32 v108, 16, v83
	v_and_b32_e32 v43, 0xffff0000, v79
	v_lshlrev_b32_e32 v42, 16, v79
	v_cndmask_b32_e64 v107, v47, -v47, vcc
	v_mov_b32_e32 v47, v4
	v_mov_b32_e32 v79, v4
	v_mov_b32_e32 v83, v5
	v_mov_b32_e32 v148, v5
	v_permlane32_swap_b32_e32 v47, v79
	s_nop 0
	v_permlane32_swap_b32_e32 v83, v148
	v_cndmask_b32_e32 v149, v83, v148, vcc
	v_cndmask_b32_e32 v148, v47, v79, vcc
	v_pk_mul_f32 v[144:145], v[144:145], v[148:149]
	v_and_b32_e32 v121, 0xffff0000, v155
	v_pk_fma_f32 v[2:3], v[4:5], v[2:3], v[144:145]
	v_lshlrev_b32_e32 v120, 16, v155
	v_pk_mul_f32 v[2:3], v[2:3], s[94:95] op_sel_hi:[1,0]
	v_and_b32_e32 v123, 0xffff0000, v154
	v_cvt_pk_bf16_f32 v5, v2, v3
	v_pk_mul_f32 v[2:3], v[46:47], v[48:49] op_sel_hi:[0,1]
	v_pk_mul_f32 v[2:3], v[2:3], v[150:151]
	v_lshlrev_b32_e32 v122, 16, v154
	v_mov_b32_e32 v4, v2
	v_mov_b32_e32 v47, v2
	v_mov_b32_e32 v79, v3
	v_mov_b32_e32 v83, v3
	v_permlane32_swap_b32_e32 v4, v47
	s_nop 0
	v_permlane32_swap_b32_e32 v79, v83
	v_cndmask_b32_e32 v145, v79, v83, vcc
	v_cndmask_b32_e32 v144, v4, v47, vcc
	v_pk_mul_f32 v[12:13], v[12:13], v[144:145]
	v_cndmask_b32_e64 v155, v101, -v101, vcc
	v_pk_fma_f32 v[2:3], v[2:3], v[102:103], v[12:13]
	v_cndmask_b32_e64 v154, v99, -v99, vcc
	v_pk_mul_f32 v[2:3], v[2:3], s[94:95] op_sel_hi:[1,0]
	v_mov_b32_e32 v99, v100
	v_cvt_pk_bf16_f32 v4, v2, v3
	s_waitcnt vmcnt(2)
	v_pk_mul_f32 v[2:3], v[46:47], v[54:55] op_sel_hi:[0,1]
	v_pk_mul_f32 v[2:3], v[2:3], v[156:157]
	v_cmp_gt_f32_e64 s[4:5], s95, v180
	v_mov_b32_e32 v12, v2
	v_mov_b32_e32 v47, v2
	v_mov_b32_e32 v13, v3
	v_mov_b32_e32 v79, v3
	v_permlane32_swap_b32_e32 v12, v47
	s_nop 0
	v_permlane32_swap_b32_e32 v13, v79
	v_cndmask_b32_e32 v13, v13, v79, vcc
	v_cndmask_b32_e32 v12, v12, v47, vcc
	v_pk_mul_f32 v[12:13], v[154:155], v[12:13]
	v_cndmask_b32_e64 v129, v59, -v59, vcc
	v_pk_fma_f32 v[2:3], v[2:3], v[98:99], v[12:13]
	v_pk_mul_f32 v[12:13], v[52:53], v[46:47] op_sel_hi:[1,0]
	v_pk_mul_f32 v[2:3], v[2:3], s[94:95] op_sel_hi:[1,0]
	v_pk_mul_f32 v[12:13], v[12:13], v[160:161]
	v_cvt_pk_bf16_f32 v3, v2, v3
	v_mov_b32_e32 v2, v12
	v_mov_b32_e32 v47, v12
	v_mov_b32_e32 v79, v13
	v_mov_b32_e32 v83, v13
	v_permlane32_swap_b32_e32 v2, v47
	s_nop 0
	v_permlane32_swap_b32_e32 v79, v83
	v_cndmask_b32_e32 v99, v79, v83, vcc
	v_cndmask_b32_e32 v98, v2, v47, vcc
	v_pk_mul_f32 v[98:99], v[158:159], v[98:99]
	v_cndmask_b32_e64 v128, v57, -v57, vcc
	v_pk_fma_f32 v[6:7], v[12:13], v[6:7], v[98:99]
	v_mov_b32_e32 v57, v58
	v_pk_mul_f32 v[6:7], v[6:7], s[94:95] op_sel_hi:[1,0]
	v_and_b32_e32 v59, 0xffff0000, v85
	v_cvt_pk_bf16_f32 v2, v6, v7
	s_waitcnt vmcnt(1)
	v_pk_mul_f32 v[6:7], v[72:73], v[46:47] op_sel_hi:[1,0]
	v_lshlrev_b32_e32 v58, 16, v85
	v_pk_mul_f32 v[6:7], v[6:7], v[8:9]
	v_and_b32_e32 v85, 0xffff0000, v84
	v_mov_b32_e32 v8, v6
	v_mov_b32_e32 v12, v6
	v_mov_b32_e32 v9, v7
	v_mov_b32_e32 v13, v7
	v_permlane32_swap_b32_e32 v8, v12
	s_nop 0
	v_permlane32_swap_b32_e32 v9, v13
	v_cndmask_b32_e32 v9, v9, v13, vcc
	v_cndmask_b32_e32 v8, v8, v12, vcc
	v_pk_mul_f32 v[8:9], v[30:31], v[8:9]
	v_lshlrev_b32_e32 v84, 16, v84
	v_pk_fma_f32 v[6:7], v[6:7], v[32:33], v[8:9]
	v_and_b32_e32 v101, 0xffff0000, v81
	v_pk_mul_f32 v[6:7], v[6:7], s[94:95] op_sel_hi:[1,0]
	v_lshlrev_b32_e32 v100, 16, v81
	v_cvt_pk_bf16_f32 v9, v6, v7
	v_pk_mul_f32 v[6:7], v[70:71], v[46:47] op_sel_hi:[1,0]
	v_and_b32_e32 v81, 0xffff0000, v80
	v_pk_mul_f32 v[6:7], v[6:7], v[172:173]
	v_lshlrev_b32_e32 v80, 16, v80
	v_mov_b32_e32 v8, v6
	v_mov_b32_e32 v12, v6
	v_mov_b32_e32 v13, v7
	v_mov_b32_e32 v47, v7
	v_permlane32_swap_b32_e32 v8, v12
	s_nop 0
	v_permlane32_swap_b32_e32 v13, v47
	v_cndmask_b32_e32 v13, v13, v47, vcc
	v_cndmask_b32_e32 v12, v8, v12, vcc
	v_pk_mul_f32 v[12:13], v[34:35], v[12:13]
	s_nop 0
	v_pk_fma_f32 v[6:7], v[6:7], v[36:37], v[12:13]
	s_nop 0
	v_pk_mul_f32 v[6:7], v[6:7], s[94:95] op_sel_hi:[1,0]
	s_nop 0
	v_cvt_pk_bf16_f32 v8, v6, v7
	s_waitcnt vmcnt(0)
; __device__ __forceinline__ unsigned cvtpk(float lo, float hi) { f32x2 v = {lo, hi}; bf16x2_t b = __builtin_convertvector(v, bf16x2_t); return __builtin_bit_cast(unsigned, b); }
; template <int DQK, int DV, bool LEAD> ...
;     ...
; #pragma unroll
;           for (int ds = 0; ds < 2; ++ds)
; #pragma unroll
;               for (int j = 0; j < 8; ++j) x[ds][j] *= rn * qgain[32 * ds + 8 * g4 + j];
;           if constexpr (DQK == 64) {
; #pragma unroll
;               for (int ds = 0; ds < 2; ++ds)
; #pragma unroll
;                   for (int j = 0; j < 8; ++j) {
;                       auto rr = __builtin_amdgcn_permlane32_swap(__float_as_uint(x[ds][j]), __float_as_uint(x[ds][j]), false, false);
;                       const float other = hi ? __uint_as_float(rr[0]) : __uint_as_float(rr[1]);
;                       float cc = 1.f, sg = 0.f;
;                       if (lat) { const f32x2 cs = rope[(ds ? pcol : prow) * 16 + 8 * (g4 & 1) + j]; cc = cs.x; sg = hi ? cs.y : -cs.y; }
;                       x[ds][j] = x[ds][j] * cc + other * sg; }
;           } else {
;               float sr = 0.f;
; #pragma unroll
;               for (int j = 0; j < 8; ++j) sr += x[2][j] * x[2][j];
;               sr = lanes4_sum(sr);
;               const float rq = rsqrtf(sr * (1.f / 32.f) + EPS);
; #pragma unroll
;               for (int j = 0; j < 8; ++j) { const float av = x[2][j] * rq * qgain[64 + 8 * g4 + j];
;                   auto rr = __builtin_amdgcn_permlane16_swap(__float_as_uint(av), __float_as_uint(av), false, false);
;                   const float other = (g4 & 1) ? __uint_as_float(rr[0]) : __uint_as_float(rr[1]);
;                   float cc = 1.f, sg = 0.f;
;                   if (lat) { const f32x2 cs = rope[((g4 & 2) ? pcol : prow) * 8 + j]; cc = cs.x; sg = (g4 & 1) ? cs.y : -cs.y; }
;                   x[2][j] = av * cc + other * sg; }
;           }
; #pragma unroll
;           for (int ds = 0; ds < NDS; ++ds) { u32x4 w;
; #pragma unroll
;               for (int i = 0; i < 4; ++i) w[i] = cvtpk(x[ds][2 * i] * c2, x[ds][2 * i + 1] * c2);
;               qf[qb * NDS + ds] = __builtin_bit_cast(bf16x8, w); }
	v_pk_mul_f32 v[6:7], v[76:77], v[46:47] op_sel_hi:[1,0]
	s_nop 0
	v_pk_mul_f32 v[6:7], v[6:7], v[176:177]
	s_nop 0
	v_mov_b32_e32 v12, v6
	v_mov_b32_e32 v47, v6
	v_mov_b32_e32 v13, v7
	v_mov_b32_e32 v79, v7
	v_permlane32_swap_b32_e32 v12, v47
	s_nop 0
	v_permlane32_swap_b32_e32 v13, v79
	v_cndmask_b32_e32 v13, v13, v79, vcc
	v_cndmask_b32_e32 v12, v12, v47, vcc
	v_pk_mul_f32 v[12:13], v[38:39], v[12:13]
	s_nop 0
	v_pk_fma_f32 v[6:7], v[6:7], v[40:41], v[12:13]
	v_pk_mul_f32 v[12:13], v[74:75], v[46:47] op_sel_hi:[1,0]
	v_pk_mul_f32 v[6:7], v[6:7], s[94:95] op_sel_hi:[1,0]
	v_pk_mul_f32 v[12:13], v[12:13], v[178:179]
	v_cvt_pk_bf16_f32 v7, v6, v7
	v_mov_b32_e32 v6, v12
	v_mov_b32_e32 v46, v12
	s_nop 1
	v_permlane32_swap_b32_e32 v6, v46
	v_mov_b32_e32 v47, v13
	v_mov_b32_e32 v79, v13
	v_cndmask_b32_e32 v46, v6, v46, vcc
	v_mul_f32_e32 v6, 0x4b800000, v180
	v_permlane32_swap_b32_e32 v47, v79
	v_cndmask_b32_e64 v6, v180, v6, s[4:5]
	v_cndmask_b32_e32 v47, v47, v79, vcc
	v_rsq_f32_e32 v79, v6
	v_pk_mul_f32 v[46:47], v[106:107], v[46:47]
	s_nop 0
	v_pk_fma_f32 v[12:13], v[12:13], v[44:45], v[46:47]
	s_nop 0
	v_pk_mul_f32 v[12:13], v[12:13], s[94:95] op_sel_hi:[1,0]
	s_nop 0
	v_cvt_pk_bf16_f32 v6, v12, v13
	v_mul_f32_e32 v12, 0x45800000, v79
	v_cndmask_b32_e64 v46, v79, v12, s[4:5]
	v_pk_mul_f32 v[12:13], v[50:51], v[46:47] op_sel_hi:[1,0]
	s_nop 0
	v_pk_mul_f32 v[12:13], v[12:13], v[132:133]
	s_nop 0
	v_mov_b32_e32 v47, v12
	v_mov_b32_e32 v79, v12
	v_mov_b32_e32 v83, v13
	v_mov_b32_e32 v98, v13
	v_permlane32_swap_b32_e32 v47, v79
	s_nop 0
	v_permlane32_swap_b32_e32 v83, v98
	v_cndmask_b32_e32 v99, v83, v98, vcc
	v_cndmask_b32_e32 v98, v47, v79, vcc
	v_pk_mul_f32 v[26:27], v[26:27], v[98:99]
	v_and_b32_e32 v83, 0xffff0000, v82
	v_pk_fma_f32 v[10:11], v[12:13], v[10:11], v[26:27]
	v_lshlrev_b32_e32 v82, 16, v82
	v_pk_mul_f32 v[10:11], v[10:11], s[94:95] op_sel_hi:[1,0]
	s_nop 0
	v_cvt_pk_bf16_f32 v13, v10, v11
	v_pk_mul_f32 v[10:11], v[48:49], v[46:47] op_sel_hi:[1,0]
	s_nop 0
	v_pk_mul_f32 v[10:11], v[10:11], v[136:137]
	s_nop 0
	v_mov_b32_e32 v12, v10
	v_mov_b32_e32 v26, v10
	v_mov_b32_e32 v27, v11
	v_mov_b32_e32 v47, v11
	v_permlane32_swap_b32_e32 v12, v26
	s_nop 0
	v_permlane32_swap_b32_e32 v27, v47
	v_cndmask_b32_e32 v27, v27, v47, vcc
	v_cndmask_b32_e32 v26, v12, v26, vcc
	v_pk_mul_f32 v[26:27], v[134:135], v[26:27]
	s_nop 0
	v_pk_fma_f32 v[10:11], v[10:11], v[94:95], v[26:27]
	s_nop 0
	v_pk_mul_f32 v[10:11], v[10:11], s[94:95] op_sel_hi:[1,0]
	s_nop 0
	v_cvt_pk_bf16_f32 v12, v10, v11
	v_pk_mul_f32 v[10:11], v[54:55], v[46:47] op_sel_hi:[1,0]
	s_nop 0
	v_pk_mul_f32 v[10:11], v[10:11], v[140:141]
	s_nop 0
	v_mov_b32_e32 v26, v10
	v_mov_b32_e32 v47, v10
	v_mov_b32_e32 v27, v11
	v_mov_b32_e32 v79, v11
	v_permlane32_swap_b32_e32 v26, v47
	s_nop 0
	v_permlane32_swap_b32_e32 v27, v79
	v_cndmask_b32_e32 v27, v27, v79, vcc
	v_cndmask_b32_e32 v26, v26, v47, vcc
	v_pk_mul_f32 v[26:27], v[138:139], v[26:27]
	s_nop 0
	v_pk_fma_f32 v[10:11], v[10:11], v[86:87], v[26:27]
	v_pk_mul_f32 v[26:27], v[52:53], v[46:47] op_sel_hi:[1,0]
	v_pk_mul_f32 v[10:11], v[10:11], s[94:95] op_sel_hi:[1,0]
	v_pk_mul_f32 v[26:27], v[26:27], v[62:63]
	v_cvt_pk_bf16_f32 v11, v10, v11
	v_mov_b32_e32 v10, v26
	v_mov_b32_e32 v47, v26
	v_mov_b32_e32 v62, v27
	v_mov_b32_e32 v63, v27
	v_permlane32_swap_b32_e32 v10, v47
	s_nop 0
	v_permlane32_swap_b32_e32 v62, v63
	v_cndmask_b32_e32 v63, v62, v63, vcc
	v_cndmask_b32_e32 v62, v10, v47, vcc
	v_pk_mul_f32 v[24:25], v[24:25], v[62:63]
	s_nop 0
	v_pk_fma_f32 v[24:25], v[26:27], v[90:91], v[24:25]
	v_and_b32_e32 v91, 0xffff0000, v78
	v_pk_mul_f32 v[24:25], v[24:25], s[94:95] op_sel_hi:[1,0]
	v_lshlrev_b32_e32 v90, 16, v78
	v_cvt_pk_bf16_f32 v10, v24, v25
	v_pk_mul_f32 v[24:25], v[72:73], v[46:47] op_sel_hi:[1,0]
	s_nop 0
	v_pk_mul_f32 v[24:25], v[24:25], v[142:143]
	s_nop 0
	v_mov_b32_e32 v26, v24
	v_mov_b32_e32 v47, v24
	v_mov_b32_e32 v27, v25
	v_mov_b32_e32 v62, v25
	v_permlane32_swap_b32_e32 v26, v47
	s_nop 0
	v_permlane32_swap_b32_e32 v27, v62
	v_cndmask_b32_e32 v27, v27, v62, vcc
	v_cndmask_b32_e32 v26, v26, v47, vcc
	v_pk_mul_f32 v[26:27], v[30:31], v[26:27]
	s_nop 0
	v_pk_fma_f32 v[24:25], v[24:25], v[32:33], v[26:27]
	s_nop 0
	v_pk_mul_f32 v[24:25], v[24:25], s[94:95] op_sel_hi:[1,0]
	s_nop 0
	v_cvt_pk_bf16_f32 v27, v24, v25
	v_pk_mul_f32 v[24:25], v[70:71], v[46:47] op_sel_hi:[1,0]
	s_nop 0
	v_pk_mul_f32 v[24:25], v[24:25], v[112:113]
	s_nop 0
	v_mov_b32_e32 v26, v24
	v_mov_b32_e32 v47, v24
	v_mov_b32_e32 v62, v25
	v_mov_b32_e32 v63, v25
	v_permlane32_swap_b32_e32 v26, v47
	s_nop 0
	v_permlane32_swap_b32_e32 v62, v63
	v_cndmask_b32_e32 v63, v62, v63, vcc
	v_cndmask_b32_e32 v62, v26, v47, vcc
	v_pk_mul_f32 v[62:63], v[34:35], v[62:63]
	s_nop 0
	v_pk_fma_f32 v[24:25], v[36:37], v[24:25], v[62:63]
	s_nop 0
	v_pk_mul_f32 v[24:25], v[24:25], s[94:95] op_sel_hi:[1,0]
	s_nop 0
	v_cvt_pk_bf16_f32 v26, v24, v25
	v_pk_mul_f32 v[24:25], v[76:77], v[46:47] op_sel_hi:[1,0]
	s_nop 0
	v_pk_mul_f32 v[24:25], v[24:25], v[146:147]
	s_nop 0
	v_mov_b32_e32 v47, v24
	v_mov_b32_e32 v62, v24
	v_mov_b32_e32 v63, v25
	v_mov_b32_e32 v79, v25
	v_permlane32_swap_b32_e32 v47, v62
	s_nop 0
	v_permlane32_swap_b32_e32 v63, v79
	v_cndmask_b32_e32 v63, v63, v79, vcc
	v_cndmask_b32_e32 v62, v47, v62, vcc
	v_pk_mul_f32 v[24:25], v[40:41], v[24:25]
	v_pk_mul_f32 v[46:47], v[74:75], v[46:47] op_sel_hi:[1,0]
	v_pk_fma_f32 v[24:25], v[38:39], v[62:63], v[24:25]
	v_pk_mul_f32 v[46:47], v[46:47], v[152:153]
	v_pk_mul_f32 v[24:25], v[24:25], s[94:95] op_sel_hi:[1,0]
	v_mov_b32_e32 v62, v46
	v_cvt_pk_bf16_f32 v25, v24, v25
	v_mov_b32_e32 v24, v46
	s_nop 1
; template <int DQK, int DV, bool LEAD> ...
;     ...
;           float sn = 0.f;
; #pragma unroll
;           for (int ds = 0; ds < 2; ++ds)
; #pragma unroll
;               for (int j = 0; j < 8; ++j) sn += x[ds][j] * x[ds][j];
;           sn = lanes4_sum(sn);
;           const float rn = rsqrtf(sn * (1.f / 64.f) + EPS);
; #pragma unroll
;           for (int ds = 0; ds < 2; ++ds)
; #pragma unroll
;               for (int j = 0; j < 8; ++j) x[ds][j] *= rn * qgain[32 * ds + 8 * g4 + j];
;           if constexpr (DQK == 64) {
; #pragma unroll
;               for (int ds = 0; ds < 2; ++ds)
; #pragma unroll
;                   for (int j = 0; j < 8; ++j) {
;                       auto rr = __builtin_amdgcn_permlane32_swap(__float_as_uint(x[ds][j]), __float_as_uint(x[ds][j]), false, false);
;                       const float other = hi ? __uint_as_float(rr[0]) : __uint_as_float(rr[1]);
;                       float cc = 1.f, sg = 0.f;
;                       if (lat) { const f32x2 cs = rope[(ds ? pcol : prow) * 16 + 8 * (g4 & 1) + j]; cc = cs.x; sg = hi ? cs.y : -cs.y; }
;                       x[ds][j] = x[ds][j] * cc + other * sg; }
;           } else {
;               float sr = 0.f;
; #pragma unroll
;               for (int j = 0; j < 8; ++j) sr += x[2][j] * x[2][j];
;               sr = lanes4_sum(sr);
;               const float rq = rsqrtf(sr * (1.f / 32.f) + EPS);
; #pragma unroll
;               for (int j = 0; j < 8; ++j) { const float av = x[2][j] * rq * qgain[64 + 8 * g4 + j];
;                   auto rr = __builtin_amdgcn_permlane16_swap(__float_as_uint(av), __float_as_uint(av), false, false);
;                   const float other = (g4 & 1) ? __uint_as_float(rr[0]) : __uint_as_float(rr[1]);
;                   float cc = 1.f, sg = 0.f;
;                   if (lat) { const f32x2 cs = rope[((g4 & 2) ? pcol : prow) * 8 + j]; cc = cs.x; sg = (g4 & 1) ? cs.y : -cs.y; }
;                   x[2][j] = av * cc + other * sg; }
;           }
; #pragma unroll
;           for (int ds = 0; ds < NDS; ++ds) { u32x4 w;
; #pragma unroll
;               for (int i = 0; i < 4; ++i) w[i] = cvtpk(x[ds][2 * i] * c2, x[ds][2 * i + 1] * c2);
;               qf[qb * NDS + ds] = __builtin_bit_cast(bf16x8, w); }
	v_permlane32_swap_b32_e32 v24, v62
	v_cndmask_b32_e32 v62, v24, v62, vcc
	v_mul_f32_e32 v24, v83, v83
	v_pk_fma_f32 v[86:87], v[82:83], v[82:83], v[24:25] op_sel_hi:[1,1,0]
	v_mul_f32_e32 v24, v109, v109
	v_pk_fma_f32 v[86:87], v[108:109], v[108:109], v[86:87]
	v_mov_b32_e32 v63, v47
	v_pk_add_f32 v[86:87], v[24:25], v[86:87] op_sel_hi:[0,1]
	v_pk_fma_f32 v[86:87], v[84:85], v[84:85], v[86:87]
	v_mul_f32_e32 v24, v85, v85
	v_pk_add_f32 v[86:87], v[24:25], v[86:87] op_sel_hi:[0,1]
	v_pk_fma_f32 v[86:87], v[58:59], v[58:59], v[86:87]
	v_mul_f32_e32 v24, v59, v59
	v_pk_add_f32 v[86:87], v[24:25], v[86:87] op_sel_hi:[0,1]
	v_pk_fma_f32 v[86:87], v[130:131], v[130:131], v[86:87]
	v_mul_f32_e32 v24, v131, v131
	v_pk_add_f32 v[86:87], v[24:25], v[86:87] op_sel_hi:[0,1]
	v_pk_fma_f32 v[86:87], v[126:127], v[126:127], v[86:87]
	v_mul_f32_e32 v24, v127, v127
	v_pk_add_f32 v[86:87], v[24:25], v[86:87] op_sel_hi:[0,1]
	v_pk_fma_f32 v[86:87], v[122:123], v[122:123], v[86:87]
	v_mul_f32_e32 v24, v123, v123
	v_pk_add_f32 v[86:87], v[24:25], v[86:87] op_sel_hi:[0,1]
	v_pk_fma_f32 v[86:87], v[120:121], v[120:121], v[86:87]
	v_mul_f32_e32 v24, v121, v121
	v_pk_add_f32 v[86:87], v[24:25], v[86:87] op_sel_hi:[0,1]
	v_mov_b32_e32 v79, v47
	v_mov_b32_e32 v24, v86
	s_nop 0
	v_permlane32_swap_b32_e32 v63, v79
	v_permlane16_swap_b32_e32 v86, v24
	v_cndmask_b32_e32 v63, v63, v79, vcc
	v_add_f32_e32 v79, v86, v24
	v_mul_f32_e32 v24, v91, v91
	v_pk_fma_f32 v[94:95], v[90:91], v[90:91], v[24:25] op_sel_hi:[1,1,0]
	v_mul_f32_e32 v24, v43, v43
	v_pk_fma_f32 v[94:95], v[42:43], v[42:43], v[94:95]
	v_mov_b32_e32 v87, v79
	v_pk_add_f32 v[94:95], v[24:25], v[94:95] op_sel_hi:[0,1]
	v_pk_fma_f32 v[94:95], v[80:81], v[80:81], v[94:95]
	v_mul_f32_e32 v24, v81, v81
	v_pk_add_f32 v[94:95], v[24:25], v[94:95] op_sel_hi:[0,1]
	v_pk_fma_f32 v[94:95], v[100:101], v[100:101], v[94:95]
	v_mul_f32_e32 v24, v101, v101
	v_pk_add_f32 v[94:95], v[24:25], v[94:95] op_sel_hi:[0,1]
	v_pk_fma_f32 v[94:95], v[92:93], v[92:93], v[94:95]
	v_mul_f32_e32 v24, v93, v93
	v_pk_add_f32 v[94:95], v[24:25], v[94:95] op_sel_hi:[0,1]
	v_pk_fma_f32 v[94:95], v[96:97], v[96:97], v[94:95]
	v_mul_f32_e32 v24, v97, v97
	v_pk_add_f32 v[94:95], v[24:25], v[94:95] op_sel_hi:[0,1]
	v_pk_fma_f32 v[94:95], v[66:67], v[66:67], v[94:95]
	v_mul_f32_e32 v24, v67, v67
	v_pk_add_f32 v[94:95], v[24:25], v[94:95] op_sel_hi:[0,1]
	v_pk_fma_f32 v[94:95], v[116:117], v[116:117], v[94:95]
	v_mul_f32_e32 v24, v117, v117
	v_pk_add_f32 v[94:95], v[24:25], v[94:95] op_sel_hi:[0,1]
	v_mov_b32_e32 v24, v94
	s_nop 1
	v_permlane16_swap_b32_e32 v94, v24
	v_add_f32_e32 v78, v94, v24
	v_mov_b32_e32 v86, v78
	v_permlane32_swap_b32_e32 v79, v87
	s_nop 0
	v_permlane32_swap_b32_e32 v78, v86
	v_pk_add_f32 v[78:79], v[78:79], v[86:87]
	v_pk_mul_f32 v[46:47], v[44:45], v[46:47]
	v_pk_fma_f32 v[78:79], v[78:79], s[12:13], v[110:111] op_sel_hi:[1,0,0]
	v_pk_fma_f32 v[46:47], v[106:107], v[62:63], v[46:47]
	v_mul_f32_e32 v24, 0x4b800000, v79
	v_cmp_gt_f32_e64 s[4:5], s95, v79
	v_pk_mul_f32 v[46:47], v[46:47], s[94:95] op_sel_hi:[1,0]
	s_nop 0
	v_cndmask_b32_e64 v24, v79, v24, s[4:5]
	v_rsq_f32_e32 v79, v24
	v_cvt_pk_bf16_f32 v24, v46, v47
	v_mul_f32_e32 v46, 0x45800000, v79
	v_cndmask_b32_e64 v46, v79, v46, s[4:5]
	v_pk_mul_f32 v[62:63], v[50:51], v[46:47] op_sel_hi:[1,0]
	v_cmp_gt_f32_e64 s[4:5], s95, v78
	v_pk_mul_f32 v[62:63], v[62:63], v[120:121]
	s_nop 0
	v_mov_b32_e32 v47, v62
	v_mov_b32_e32 v79, v62
	v_mov_b32_e32 v86, v63
	v_mov_b32_e32 v87, v63
	v_permlane32_swap_b32_e32 v47, v79
	s_nop 0
	v_permlane32_swap_b32_e32 v86, v87
	v_cndmask_b32_e32 v87, v86, v87, vcc
	v_cndmask_b32_e32 v86, v47, v79, vcc
	v_pk_mul_f32 v[86:87], v[118:119], v[86:87]
	s_nop 0
	v_pk_fma_f32 v[62:63], v[62:63], v[68:69], v[86:87]
	v_pk_mul_f32 v[68:69], v[48:49], v[46:47] op_sel_hi:[1,0]
	v_pk_mul_f32 v[62:63], v[62:63], s[94:95] op_sel_hi:[1,0]
	v_pk_mul_f32 v[68:69], v[68:69], v[122:123]
	v_cvt_pk_bf16_f32 v63, v62, v63
	v_mov_b32_e32 v47, v68
	v_mov_b32_e32 v62, v68
	v_mov_b32_e32 v79, v69
	v_mov_b32_e32 v86, v69
	v_permlane32_swap_b32_e32 v47, v62
	s_nop 0
	v_permlane32_swap_b32_e32 v79, v86
	v_cndmask_b32_e32 v87, v79, v86, vcc
	v_cndmask_b32_e32 v86, v47, v62, vcc
	v_pk_mul_f32 v[86:87], v[104:105], v[86:87]
	s_nop 0
	v_pk_fma_f32 v[64:65], v[68:69], v[64:65], v[86:87]
	s_nop 0
	v_pk_mul_f32 v[64:65], v[64:65], s[94:95] op_sel_hi:[1,0]
	s_nop 0
	v_cvt_pk_bf16_f32 v62, v64, v65
	v_pk_mul_f32 v[64:65], v[54:55], v[46:47] op_sel_hi:[1,0]
	s_nop 0
	v_pk_mul_f32 v[64:65], v[64:65], v[126:127]
	s_nop 0
	v_mov_b32_e32 v47, v64
	v_mov_b32_e32 v68, v64
	v_mov_b32_e32 v69, v65
	v_mov_b32_e32 v79, v65
	v_permlane32_swap_b32_e32 v47, v68
	s_nop 0
	v_permlane32_swap_b32_e32 v69, v79
	v_cndmask_b32_e32 v69, v69, v79, vcc
	v_cndmask_b32_e32 v68, v47, v68, vcc
	v_pk_mul_f32 v[68:69], v[124:125], v[68:69]
	s_nop 0
	v_pk_fma_f32 v[60:61], v[64:65], v[60:61], v[68:69]
	v_pk_mul_f32 v[64:65], v[52:53], v[46:47] op_sel_hi:[1,0]
	v_pk_mul_f32 v[60:61], v[60:61], s[94:95] op_sel_hi:[1,0]
	v_pk_mul_f32 v[64:65], v[64:65], v[130:131]
	v_cvt_pk_bf16_f32 v61, v60, v61
	v_mov_b32_e32 v47, v64
	v_mov_b32_e32 v60, v64
	v_mov_b32_e32 v68, v65
	v_mov_b32_e32 v69, v65
	v_permlane32_swap_b32_e32 v47, v60
	s_nop 0
	v_permlane32_swap_b32_e32 v68, v69
	v_cndmask_b32_e32 v69, v68, v69, vcc
	v_cndmask_b32_e32 v68, v47, v60, vcc
	v_pk_mul_f32 v[68:69], v[128:129], v[68:69]
	s_nop 0
	v_pk_fma_f32 v[56:57], v[64:65], v[56:57], v[68:69]
	s_nop 0
	v_pk_mul_f32 v[56:57], v[56:57], s[94:95] op_sel_hi:[1,0]
	s_nop 0
	v_cvt_pk_bf16_f32 v60, v56, v57
	v_pk_mul_f32 v[56:57], v[72:73], v[46:47] op_sel_hi:[1,0]
; __device__ __forceinline__ unsigned cvtpk(float lo, float hi) { f32x2 v = {lo, hi}; bf16x2_t b = __builtin_convertvector(v, bf16x2_t); return __builtin_bit_cast(unsigned, b); }
; template <int DQK, int DV, bool LEAD> ...
;     ...
; #pragma unroll
;           for (int ds = 0; ds < 2; ++ds)
; #pragma unroll
;               for (int j = 0; j < 8; ++j) x[ds][j] *= rn * qgain[32 * ds + 8 * g4 + j];
;           if constexpr (DQK == 64) {
; #pragma unroll
;               for (int ds = 0; ds < 2; ++ds)
; #pragma unroll
;                   for (int j = 0; j < 8; ++j) {
;                       auto rr = __builtin_amdgcn_permlane32_swap(__float_as_uint(x[ds][j]), __float_as_uint(x[ds][j]), false, false);
;                       const float other = hi ? __uint_as_float(rr[0]) : __uint_as_float(rr[1]);
;                       float cc = 1.f, sg = 0.f;
;                       if (lat) { const f32x2 cs = rope[(ds ? pcol : prow) * 16 + 8 * (g4 & 1) + j]; cc = cs.x; sg = hi ? cs.y : -cs.y; }
;                       x[ds][j] = x[ds][j] * cc + other * sg; }
;           } else {
;               float sr = 0.f;
; #pragma unroll
;               for (int j = 0; j < 8; ++j) sr += x[2][j] * x[2][j];
;               sr = lanes4_sum(sr);
;               const float rq = rsqrtf(sr * (1.f / 32.f) + EPS);
; #pragma unroll
;               for (int j = 0; j < 8; ++j) { const float av = x[2][j] * rq * qgain[64 + 8 * g4 + j];
;                   auto rr = __builtin_amdgcn_permlane16_swap(__float_as_uint(av), __float_as_uint(av), false, false);
;                   const float other = (g4 & 1) ? __uint_as_float(rr[0]) : __uint_as_float(rr[1]);
;                   float cc = 1.f, sg = 0.f;
;                   if (lat) { const f32x2 cs = rope[((g4 & 2) ? pcol : prow) * 8 + j]; cc = cs.x; sg = (g4 & 1) ? cs.y : -cs.y; }
;                   x[2][j] = av * cc + other * sg; }
;           }
; #pragma unroll
;           for (int ds = 0; ds < NDS; ++ds) { u32x4 w;
; #pragma unroll
;               for (int i = 0; i < 4; ++i) w[i] = cvtpk(x[ds][2 * i] * c2, x[ds][2 * i + 1] * c2);
;               qf[qb * NDS + ds] = __builtin_bit_cast(bf16x8, w); }
;       }
; #pragma unroll
;       for (int d0 = 0; d0 < NQB * NDS; ++d0) asm volatile("" : "+v"(qf[d0])); }
;     wait_bar<0>();
	s_nop 0
	v_pk_mul_f32 v[56:57], v[56:57], v[58:59]
	s_nop 0
	v_mov_b32_e32 v47, v56
	v_mov_b32_e32 v58, v56
	v_mov_b32_e32 v59, v57
	v_mov_b32_e32 v64, v57
	v_permlane32_swap_b32_e32 v47, v58
	s_nop 0
	v_permlane32_swap_b32_e32 v59, v64
	v_cndmask_b32_e32 v59, v59, v64, vcc
	v_cndmask_b32_e32 v58, v47, v58, vcc
	v_pk_mul_f32 v[58:59], v[30:31], v[58:59]
	s_nop 0
	v_pk_fma_f32 v[56:57], v[56:57], v[32:33], v[58:59]
	s_nop 0
	v_pk_mul_f32 v[56:57], v[56:57], s[94:95] op_sel_hi:[1,0]
	s_nop 0
	v_cvt_pk_bf16_f32 v59, v56, v57
	v_pk_mul_f32 v[56:57], v[70:71], v[46:47] op_sel_hi:[1,0]
	s_nop 0
	v_pk_mul_f32 v[56:57], v[56:57], v[84:85]
	s_nop 0
	v_mov_b32_e32 v47, v56
	v_mov_b32_e32 v58, v56
	v_mov_b32_e32 v64, v57
	v_mov_b32_e32 v65, v57
	v_permlane32_swap_b32_e32 v47, v58
	s_nop 0
	v_permlane32_swap_b32_e32 v64, v65
	v_cndmask_b32_e32 v65, v64, v65, vcc
	v_cndmask_b32_e32 v64, v47, v58, vcc
	v_pk_mul_f32 v[64:65], v[34:35], v[64:65]
	s_nop 0
	v_pk_fma_f32 v[56:57], v[36:37], v[56:57], v[64:65]
	s_nop 0
	v_pk_mul_f32 v[56:57], v[56:57], s[94:95] op_sel_hi:[1,0]
	s_nop 0
	v_cvt_pk_bf16_f32 v58, v56, v57
	v_pk_mul_f32 v[56:57], v[76:77], v[46:47] op_sel_hi:[1,0]
	s_nop 0
	v_pk_mul_f32 v[56:57], v[56:57], v[108:109]
	s_nop 0
	v_mov_b32_e32 v47, v56
	v_mov_b32_e32 v64, v56
	v_mov_b32_e32 v65, v57
	v_mov_b32_e32 v68, v57
	v_permlane32_swap_b32_e32 v47, v64
	s_nop 0
	v_permlane32_swap_b32_e32 v65, v68
	v_cndmask_b32_e32 v65, v65, v68, vcc
	v_cndmask_b32_e32 v64, v47, v64, vcc
	v_pk_mul_f32 v[56:57], v[40:41], v[56:57]
	v_pk_mul_f32 v[46:47], v[74:75], v[46:47] op_sel_hi:[1,0]
	v_pk_fma_f32 v[56:57], v[38:39], v[64:65], v[56:57]
	v_pk_mul_f32 v[46:47], v[46:47], v[82:83]
	v_pk_mul_f32 v[56:57], v[56:57], s[94:95] op_sel_hi:[1,0]
	v_mov_b32_e32 v64, v46
	v_cvt_pk_bf16_f32 v57, v56, v57
	v_mov_b32_e32 v56, v46
	s_nop 1
	v_permlane32_swap_b32_e32 v56, v64
	v_mov_b32_e32 v65, v47
	v_mov_b32_e32 v68, v47
	v_cndmask_b32_e32 v64, v56, v64, vcc
	v_mul_f32_e32 v56, 0x4b800000, v78
	v_permlane32_swap_b32_e32 v65, v68
	v_cndmask_b32_e64 v56, v78, v56, s[4:5]
	v_cndmask_b32_e32 v65, v65, v68, vcc
	v_rsq_f32_e32 v68, v56
	v_pk_mul_f32 v[46:47], v[44:45], v[46:47]
	s_nop 0
	v_pk_fma_f32 v[46:47], v[106:107], v[64:65], v[46:47]
	s_nop 0
	v_pk_mul_f32 v[46:47], v[46:47], s[94:95] op_sel_hi:[1,0]
	s_nop 0
	v_cvt_pk_bf16_f32 v56, v46, v47
	v_mul_f32_e32 v46, 0x45800000, v68
	v_cndmask_b32_e64 v46, v68, v46, s[4:5]
	v_pk_mul_f32 v[64:65], v[74:75], v[46:47] op_sel_hi:[1,0]
	v_pk_mul_f32 v[68:69], v[76:77], v[46:47] op_sel_hi:[1,0]
	v_pk_mul_f32 v[64:65], v[64:65], v[90:91]
	v_pk_mul_f32 v[48:49], v[48:49], v[46:47] op_sel_hi:[1,0]
	v_pk_mul_f32 v[42:43], v[68:69], v[42:43]
	v_pk_mul_f32 v[68:69], v[70:71], v[46:47] op_sel_hi:[1,0]
	v_pk_mul_f32 v[70:71], v[72:73], v[46:47] op_sel_hi:[1,0]
	v_pk_mul_f32 v[52:53], v[52:53], v[46:47] op_sel_hi:[1,0]
	v_pk_mul_f32 v[54:55], v[54:55], v[46:47] op_sel_hi:[1,0]
	v_pk_mul_f32 v[48:49], v[48:49], v[66:67]
	v_pk_mul_f32 v[46:47], v[50:51], v[46:47] op_sel_hi:[1,0]
	v_mov_b32_e32 v50, v64
	v_mov_b32_e32 v66, v64
	v_mov_b32_e32 v51, v65
	v_mov_b32_e32 v67, v65
	v_permlane32_swap_b32_e32 v50, v66
	s_nop 0
	v_permlane32_swap_b32_e32 v51, v67
	v_cndmask_b32_e32 v51, v51, v67, vcc
	v_cndmask_b32_e32 v50, v50, v66, vcc
	v_pk_mul_f32 v[44:45], v[44:45], v[64:65]
	v_mov_b32_e32 v64, v42
	v_pk_fma_f32 v[44:45], v[106:107], v[50:51], v[44:45]
	v_mov_b32_e32 v50, v42
	v_mov_b32_e32 v51, v43
	v_mov_b32_e32 v65, v43
	v_permlane32_swap_b32_e32 v50, v64
	s_nop 0
	v_permlane32_swap_b32_e32 v51, v65
	v_pk_mul_f32 v[68:69], v[68:69], v[80:81]
	v_cndmask_b32_e32 v51, v51, v65, vcc
	v_cndmask_b32_e32 v50, v50, v64, vcc
	v_pk_mul_f32 v[40:41], v[40:41], v[42:43]
	v_mov_b32_e32 v42, v68
	v_pk_fma_f32 v[38:39], v[38:39], v[50:51], v[40:41]
	v_mov_b32_e32 v40, v68
	v_mov_b32_e32 v41, v69
	v_mov_b32_e32 v43, v69
	v_permlane32_swap_b32_e32 v40, v42
	s_nop 0
	v_permlane32_swap_b32_e32 v41, v43
	v_cndmask_b32_e32 v41, v41, v43, vcc
	v_cndmask_b32_e32 v40, v40, v42, vcc
	v_pk_mul_f32 v[70:71], v[70:71], v[100:101]
	v_pk_mul_f32 v[34:35], v[34:35], v[40:41]
	v_mov_b32_e32 v40, v70
	v_pk_fma_f32 v[34:35], v[36:37], v[68:69], v[34:35]
	v_mov_b32_e32 v36, v70
	v_mov_b32_e32 v37, v71
	v_mov_b32_e32 v41, v71
	v_permlane32_swap_b32_e32 v36, v40
	s_nop 0
	v_permlane32_swap_b32_e32 v37, v41
	v_cndmask_b32_e32 v37, v37, v41, vcc
	v_cndmask_b32_e32 v36, v36, v40, vcc
	v_pk_mul_f32 v[52:53], v[52:53], v[92:93]
	v_pk_mul_f32 v[30:31], v[30:31], v[36:37]
	v_mov_b32_e32 v36, v52
	v_pk_fma_f32 v[30:31], v[70:71], v[32:33], v[30:31]
	v_mov_b32_e32 v32, v52
	v_mov_b32_e32 v33, v53
	v_mov_b32_e32 v37, v53
	v_permlane32_swap_b32_e32 v32, v36
	s_nop 0
	v_permlane32_swap_b32_e32 v33, v37
	v_cndmask_b32_e32 v33, v33, v37, vcc
	v_cndmask_b32_e32 v32, v32, v36, vcc
	v_pk_mul_f32 v[54:55], v[54:55], v[96:97]
	v_pk_mul_f32 v[32:33], v[88:89], v[32:33]
	v_mov_b32_e32 v36, v54
	v_pk_fma_f32 v[28:29], v[52:53], v[28:29], v[32:33]
	v_mov_b32_e32 v32, v54
	v_mov_b32_e32 v33, v55
	v_mov_b32_e32 v37, v55
	v_permlane32_swap_b32_e32 v32, v36
	s_nop 0
	v_permlane32_swap_b32_e32 v33, v37
	v_cndmask_b32_e32 v33, v33, v37, vcc
	v_cndmask_b32_e32 v32, v32, v36, vcc
	v_pk_mul_f32 v[20:21], v[20:21], v[32:33]
	v_mov_b32_e32 v32, v48
	v_pk_fma_f32 v[20:21], v[54:55], v[22:23], v[20:21]
	v_mov_b32_e32 v22, v48
	v_mov_b32_e32 v23, v49
	v_mov_b32_e32 v33, v49
	v_permlane32_swap_b32_e32 v22, v32
	s_nop 0
	v_permlane32_swap_b32_e32 v23, v33
	v_cndmask_b32_e32 v23, v23, v33, vcc
	v_cndmask_b32_e32 v22, v22, v32, vcc
	v_pk_mul_f32 v[46:47], v[46:47], v[116:117]
	v_pk_mul_f32 v[16:17], v[16:17], v[22:23]
	v_mov_b32_e32 v22, v46
	v_pk_fma_f32 v[16:17], v[48:49], v[18:19], v[16:17]
	v_mov_b32_e32 v18, v46
	v_mov_b32_e32 v19, v47
	v_mov_b32_e32 v23, v47
	v_permlane32_swap_b32_e32 v18, v22
	s_nop 0
	v_permlane32_swap_b32_e32 v19, v23
	v_cndmask_b32_e32 v19, v19, v23, vcc
	v_cndmask_b32_e32 v18, v18, v22, vcc
	v_pk_mul_f32 v[18:19], v[114:115], v[18:19]
	v_pk_mul_f32 v[16:17], v[16:17], s[94:95] op_sel_hi:[1,0]
	v_pk_fma_f32 v[14:15], v[46:47], v[14:15], v[18:19]
	v_pk_mul_f32 v[18:19], v[44:45], s[94:95] op_sel_hi:[1,0]
	v_pk_mul_f32 v[14:15], v[14:15], s[94:95] op_sel_hi:[1,0]
	v_cvt_pk_bf16_f32 v76, v18, v19
	v_pk_mul_f32 v[18:19], v[38:39], s[94:95] op_sel_hi:[1,0]
	v_cvt_pk_bf16_f32 v86, v16, v17
	v_cvt_pk_bf16_f32 v77, v18, v19
	v_pk_mul_f32 v[18:19], v[34:35], s[94:95] op_sel_hi:[1,0]
	v_cvt_pk_bf16_f32 v87, v14, v15
	v_cvt_pk_bf16_f32 v78, v18, v19
	v_pk_mul_f32 v[18:19], v[30:31], s[94:95] op_sel_hi:[1,0]
	v_bfe_u32 v22, v162, 1, 3
	v_cvt_pk_bf16_f32 v79, v18, v19
	v_pk_mul_f32 v[18:19], v[28:29], s[94:95] op_sel_hi:[1,0]
	v_bitop3_b32 v22, v169, v22, 4 bitop3:0x36
	v_cvt_pk_bf16_f32 v84, v18, v19
	v_pk_mul_f32 v[18:19], v[20:21], s[94:95] op_sel_hi:[1,0]
	v_lshlrev_b32_e32 v22, 4, v22
	v_cvt_pk_bf16_f32 v85, v18, v19
	s_waitcnt vmcnt(0) lgkmcnt(0)
	s_barrier
; #define ATT_SB() __builtin_amdgcn_sched_barrier(0)
; #define ATT_DMA_K(t, sl) do { glds16(ksrc + (size_t)(t) * 64 * kpitch, (unsigned)__builtin_amdgcn_readfirstlane(kdst + (sl) * KSLOT)); \
;         if constexpr (DQK == 96) glds16(krsrc + (size_t)(t) * 64 * 32, (unsigned)__builtin_amdgcn_readfirstlane(krdst + (sl) * KSLOT)); } while (0)
; #define ATT_DMA_V(t, sl) do { glds16(vsrc + (size_t)(t) * 64, (unsigned)__builtin_amdgcn_readfirstlane(vdst + (sl) * VSLOT)); \
;         if constexpr (DV == 128) glds16(vsrc + (size_t)64 * NR + (size_t)(t) * 64, (unsigned)__builtin_amdgcn_readfirstlane(vdst + (sl) * VSLOT + 8192)); } while (0)
; #define ATT_KLOAD(sl) do { _Pragma("unroll") for (int kb_ = 0; kb_ < NKW; ++kb_) _Pragma("unroll") for (int ds_ = 0; ds_ < NDS; ++ds_) { \
;         if (ds_ < 2) kf[kb_ * NDS + ds_] = *(const LAS bf16x8*)(kp[ds_ & 1] + (sl) * KSLOT + (kb_ & 1) * 512 + (kb_ >> 1) * 4096); \
;         else kf[kb_ * NDS + ds_] = *(const LAS bf16x8*)(krp + (sl) * KSLOT + (kb_ & 1) * 256 + (kb_ >> 1) * 2048); } } while (0)
; #define ATT_QK() do { _Pragma("unroll") for (int kb_ = 0; kb_ < NKW; ++kb_) _Pragma("unroll") for (int ds_ = 0; ds_ < NDS; ++ds_) _Pragma("unroll") for (int qb_ = 0; qb_ < NQB; ++qb_) \
;         c[kb_][qb_] = __builtin_amdgcn_mfma_f32_16x16x32_bf16(kf[kb_ * NDS + ds_], qf[qb_ * NDS + ds_], ds_ == 0 ? zero4 : c[kb_][qb_], 0, 0, 0); } while (0)
; template <int DQK, int DV, bool LEAD> ...
;     ...
;     wait_bar<0>();
;     bf16x8 kf[NKW * NDS], vf[NVF];
;     ATT_KLOAD(0);
;     asm volatile("s_waitcnt lgkmcnt(0)\n\ts_barrier" ::: "memory");
;     float lsum[NQB];
; #pragma unroll
;     for (int qb = 0; qb < NQB; ++qb) lsum[qb] = 0.f;
;     const f32x4 zero4 = {0.f, 0.f, 0.f, 0.f};
;     f32x4 o[NDB][NQB], c[NKW][NQB]; u32x4 pw[4];
; #pragma unroll
;     for (int i = 0; i < NDB; ++i)
; #pragma unroll
;         for (int qb = 0; qb < NQB; ++qb) o[i][qb] = zero4;
;     ATT_DMA_K(3, 0); ATT_DMA_V(1, 1);
;     ATT_QK(); ATT_SB();
;     ATT_KLOAD(1); ATT_SB();
;     if constexpr (LEAD) { ATT_EXP(); ATT_SUMPACK(); }
;     wait_bar<NDMA>();
;     int s_prev = 0, s_cur = 1, s_next = 2;
;     int one_ = 1; asm volatile("" : "+s"(one_));
	ds_read_b128 v[14:17], v174
	ds_read_b128 v[18:21], v174 offset:512
	v_add_u32_e32 v176, v170, v22
	s_waitcnt lgkmcnt(1)
	v_mfma_f32_16x16x32_bf16 v[28:31], v[14:17], v[6:9], 0
	ds_read_b128 v[40:43], v176
	ds_read_b128 v[44:47], v176 offset:512
	s_waitcnt lgkmcnt(0)
	s_barrier
	s_mov_b32 s4, 0
	v_mfma_f32_16x16x32_bf16 v[32:35], v[14:17], v[24:27], 0
	s_cselect_b64 vcc, -1, 0
	s_mov_b32 s7, s4
	v_mfma_f32_16x16x32_bf16 v[36:39], v[14:17], v[56:59], 0
	v_mfma_f32_16x16x32_bf16 v[14:17], v[14:17], v[76:79], 0
	s_waitcnt lgkmcnt(1)
	v_mfma_f32_16x16x32_bf16 v[116:119], v[40:43], v[84:87], v[14:17]
	v_mfma_f32_16x16x32_bf16 v[14:17], v[18:21], v[6:9], 0
	v_mfma_f32_16x16x32_bf16 v[144:147], v[40:43], v[2:5], v[28:31]
	v_mfma_f32_16x16x32_bf16 v[140:143], v[40:43], v[10:13], v[32:35]
	v_mfma_f32_16x16x32_bf16 v[28:31], v[18:21], v[24:27], 0
	v_mfma_f32_16x16x32_bf16 v[32:35], v[18:21], v[56:59], 0
	v_mfma_f32_16x16x32_bf16 v[18:21], v[18:21], v[76:79], 0
	s_waitcnt lgkmcnt(0)
	v_mfma_f32_16x16x32_bf16 v[136:139], v[44:47], v[2:5], v[14:17]
	s_nop 2
	v_lshl_add_u64 v[14:15], v[164:165], 0, s[96:97]
	s_mov_b32 m0, s50
	s_nop 0
	global_load_lds_dwordx4 v[14:15], off
	v_mfma_f32_16x16x32_bf16 v[128:131], v[40:43], v[60:63], v[36:39]
	v_lshl_add_u64 v[14:15], v[166:167], 0, s[66:67]
	s_add_i32 s5, s45, 0x2000
	s_mov_b32 m0, s5
	s_nop 0
	global_load_lds_dwordx4 v[14:15], off
	v_mfma_f32_16x16x32_bf16 v[132:135], v[44:47], v[10:13], v[28:31]
	s_mov_b32 s6, s4
	s_mov_b32 s5, s4
	v_mov_b64_e32 v[16:17], s[6:7]
	v_mfma_f32_16x16x32_bf16 v[124:127], v[44:47], v[60:63], v[32:35]
	v_mov_b64_e32 v[14:15], s[4:5]
	v_mfma_f32_16x16x32_bf16 v[120:123], v[44:47], v[84:87], v[18:21]
	ds_read_b128 v[100:103], v174 offset:8192
	ds_read_b128 v[108:111], v174 offset:8704
	ds_read_b128 v[104:107], v176 offset:8192
	ds_read_b128 v[112:115], v176 offset:8704
	v_cndmask_b32_e32 v18, v22, v168, vcc
	v_add3_u32 v175, 0, v163, v18
	s_waitcnt vmcnt(2) lgkmcnt(0)
	s_barrier
	s_mov_b32 s5, 1
	v_mov_b32_e32 v22, 0
	s_cmp_lg_u32 s5, 0
	v_mov_b64_e32 v[20:21], v[16:17]
	v_mov_b64_e32 v[30:31], v[16:17]
	v_mov_b64_e32 v[34:35], v[16:17]
	v_mov_b64_e32 v[38:39], v[16:17]
	v_mov_b64_e32 v[42:43], v[16:17]
	v_mov_b64_e32 v[46:47], v[16:17]
	v_mov_b64_e32 v[50:51], v[16:17]
	v_mov_b64_e32 v[54:55], v[16:17]
	v_mov_b64_e32 v[66:67], v[16:17]
	v_mov_b64_e32 v[70:71], v[16:17]
	v_mov_b64_e32 v[74:75], v[16:17]
	v_mov_b64_e32 v[82:83], v[16:17]
	v_mov_b64_e32 v[90:91], v[16:17]
	v_mov_b64_e32 v[94:95], v[16:17]
	v_mov_b64_e32 v[98:99], v[16:17]
	s_cselect_b64 s[6:7], -1, 0
	v_mov_b64_e32 v[18:19], v[14:15]
	v_mov_b64_e32 v[28:29], v[14:15]
	v_mov_b64_e32 v[32:33], v[14:15]
	v_mov_b64_e32 v[36:37], v[14:15]
	v_mov_b64_e32 v[40:41], v[14:15]
	v_mov_b64_e32 v[44:45], v[14:15]
	v_mov_b64_e32 v[48:49], v[14:15]
	v_mov_b64_e32 v[52:53], v[14:15]
	v_mov_b64_e32 v[64:65], v[14:15]
	v_mov_b64_e32 v[68:69], v[14:15]
	v_mov_b64_e32 v[72:73], v[14:15]
	v_mov_b64_e32 v[80:81], v[14:15]
	v_mov_b64_e32 v[88:89], v[14:15]
	v_mov_b64_e32 v[92:93], v[14:15]
	v_mov_b64_e32 v[96:97], v[14:15]
	s_mov_b32 s38, 2
	v_mov_b32_e32 v23, v22
	v_mov_b32_e32 v168, v22
	v_mov_b32_e32 v169, v22
; #define ATT_SB() __builtin_amdgcn_sched_barrier(0)
; #define ATT_DMA_K(t, sl) do { glds16(ksrc + (size_t)(t) * 64 * kpitch, (unsigned)__builtin_amdgcn_readfirstlane(kdst + (sl) * KSLOT)); \
;         if constexpr (DQK == 96) glds16(krsrc + (size_t)(t) * 64 * 32, (unsigned)__builtin_amdgcn_readfirstlane(krdst + (sl) * KSLOT)); } while (0)
; #define ATT_DMA_V(t, sl) do { glds16(vsrc + (size_t)(t) * 64, (unsigned)__builtin_amdgcn_readfirstlane(vdst + (sl) * VSLOT)); \
;         if constexpr (DV == 128) glds16(vsrc + (size_t)64 * NR + (size_t)(t) * 64, (unsigned)__builtin_amdgcn_readfirstlane(vdst + (sl) * VSLOT + 8192)); } while (0)
; template <int DQK, int DV, bool LEAD> ...
;     ...
;     for (int t = 1; t < NT; ++t) {
;         __builtin_amdgcn_s_waitcnt(0xC07F);
;         if constexpr (!LEAD) { ATT_EXP(); ATT_SUMPACK(); ATT_SB(); }
;         ATT_VLOAD(s_prev, 0); ATT_SB();
;         { const int tk = (t + 3 < NT) ? t + 3 : NT - 1; ATT_DMA_K(tk, s_cur); }
;         { const int tv = (t + 1 < NT) ? t + 1 : NT - 1; ATT_DMA_V(tv, s_next); }
;         ATT_SB();
;         if constexpr (LEAD) {
;             ATT_QK(); ATT_SB();
;             ATT_PVP(0); ATT_SB();
;             if constexpr (DV == 128) { ATT_VLOAD(s_prev, 1); ATT_SB(); ATT_EXP(); ATT_SB(); ATT_PVP(1); ATT_SB(); }
;             if (one_) ATT_KLOAD(s_next);
;             ATT_SB();
;             if constexpr (DV == 64) ATT_EXP();
;             ATT_SUMPACK();
;             asm volatile("" : "+v"(pw[0]), "+v"(pw[1]), "+v"(pw[2]), "+v"(pw[3]));
; #pragma unroll
;             for (int qb = 0; qb < NQB; ++qb) asm volatile("" : "+v"(lsum[qb]));
;         } else {
;             if constexpr (DV == 128) {
;                 ATT_PVP(0); ATT_SB();
;                 ATT_VLOAD(s_prev, 1); ATT_SB();
;                 ATT_QK(); ATT_SB();
;                 if (one_) { ATT_KLOAD(s_next); ATT_SB(); ATT_PVP(1); }
;                 ATT_SB();
;             } else {
;                 __builtin_amdgcn_s_setprio(1);
;                 ATT_QK(); ATT_SB();
;                 if (one_) { ATT_KLOAD(s_next); ATT_SB(); ATT_PVP(0); }
;                 ATT_SB();
;                 __builtin_amdgcn_s_setprio(0);
;             }
; #pragma unroll
;             for (int kb = 0; kb < NKW; ++kb)
; #pragma unroll
;                 for (int qb = 0; qb < NQB; ++qb) asm volatile("" : "+v"(c[kb][qb]));
.LBB0_957:
	v_exp_f32_e32 v177, v144
	v_exp_f32_e32 v178, v145
	v_exp_f32_e32 v179, v146
	v_exp_f32_e32 v180, v147
	v_exp_f32_e32 v181, v140
	v_exp_f32_e32 v182, v141
	v_exp_f32_e32 v183, v142
	v_exp_f32_e32 v184, v143
	v_exp_f32_e32 v185, v128
	v_exp_f32_e32 v186, v129
	v_exp_f32_e32 v188, v130
	v_exp_f32_e32 v190, v131
	v_exp_f32_e32 v193, v116
	v_exp_f32_e32 v194, v117
	v_exp_f32_e32 v204, v118
	v_exp_f32_e32 v206, v119
	v_add_f32_e32 v116, v177, v178
	v_add_f32_e32 v117, v179, v180
	v_exp_f32_e32 v187, v136
	v_exp_f32_e32 v203, v132
	v_exp_f32_e32 v197, v124
	v_exp_f32_e32 v212, v120
	v_add_f32_e32 v116, v116, v117
	v_add_f32_e32 v117, v181, v182
	v_add_f32_e32 v118, v183, v184
	v_add_f32_e32 v117, v117, v118
	v_add_f32_e32 v118, v185, v186
	v_add_f32_e32 v119, v188, v190
	v_exp_f32_e32 v189, v137
	v_exp_f32_e32 v205, v133
	v_exp_f32_e32 v209, v125
	v_exp_f32_e32 v213, v121
	v_add_f32_e32 v118, v118, v119
	v_add_f32_e32 v119, v193, v194
	v_add_f32_e32 v120, v204, v206
	v_add_f32_e32 v119, v119, v120
	v_exp_f32_e32 v191, v138
	v_exp_f32_e32 v207, v134
	v_exp_f32_e32 v210, v126
	v_exp_f32_e32 v214, v122
	v_add_f32_e32 v116, v187, v116
	v_add_f32_e32 v117, v203, v117
	v_add_f32_e32 v118, v197, v118
	v_add_f32_e32 v119, v212, v119
	s_waitcnt lgkmcnt(0)
	v_exp_f32_e32 v192, v139
	v_exp_f32_e32 v208, v135
	v_exp_f32_e32 v211, v127
	v_exp_f32_e32 v215, v123
	s_mov_b32 s5, s51
	v_add_f32_e32 v116, v189, v116
	v_add_f32_e32 v117, v205, v117
	v_add_f32_e32 v118, v209, v118
	v_add_f32_e32 v119, v213, v119
	s_mov_b32 s51, s38
	v_add_f32_e32 v116, v191, v116
	v_add_f32_e32 v117, v207, v117
	v_add_f32_e32 v118, v210, v118
	v_add_f32_e32 v119, v214, v119
	s_add_i32 s38, s16, -1
	s_nop 0
	v_add_f32_e32 v173, v192, v116
	v_add_f32_e32 v172, v208, v117
	v_add_f32_e32 v171, v211, v118
	v_add_f32_e32 v170, v215, v119
	v_lshl_add_u32 v116, s4, 13, v175
	ds_read_b128 v[160:163], v116 offset:36864
	ds_read_b128 v[156:159], v116 offset:38912
	ds_read_b128 v[152:155], v116 offset:40960
	ds_read_b128 v[148:151], v116 offset:43008
	s_min_u32 s38, s38, 0x80
	s_mul_i32 s38, s38, 0x38000
	s_lshl_b32 s52, s5, 13
	v_lshl_add_u64 v[116:117], v[164:165], 0, s[38:39]
	s_add_i32 s38, s52, s50
	v_lshl_add_u64 v[116:117], v[116:117], 0, s[96:97]
	s_mov_b32 m0, s38
	s_nop 0
	global_load_lds_dwordx4 v[116:117], off
	s_min_u32 s38, s16, 0x83
	s_lshl_b32 s38, s38, 7
	v_lshl_add_u64 v[116:117], v[166:167], 0, s[38:39]
	s_lshl_b32 s38, s51, 13
	s_add_i32 s53, s38, s45
	s_mov_b32 m0, s53
	s_nop 0
	global_load_lds_dwordx4 v[116:117], off
	s_setprio 1
	v_mfma_f32_16x16x32_bf16 v[120:123], v[100:103], v[24:27], 0
	v_mfma_f32_16x16x32_bf16 v[124:127], v[100:103], v[56:59], 0
	v_mfma_f32_16x16x32_bf16 v[116:119], v[100:103], v[6:9], 0
	v_mfma_f32_16x16x32_bf16 v[132:135], v[100:103], v[76:79], 0
	v_mfma_f32_16x16x32_bf16 v[140:143], v[104:107], v[10:13], v[120:123]
	v_mfma_f32_16x16x32_bf16 v[128:131], v[104:107], v[60:63], v[124:127]
	v_mfma_f32_16x16x32_bf16 v[120:123], v[108:111], v[6:9], 0
	v_mfma_f32_16x16x32_bf16 v[124:127], v[108:111], v[24:27], 0
	v_mfma_f32_16x16x32_bf16 v[216:219], v[108:111], v[56:59], 0
	v_mfma_f32_16x16x32_bf16 v[236:239], v[108:111], v[76:79], 0
	v_mfma_f32_16x16x32_bf16 v[144:147], v[104:107], v[2:5], v[116:119]
	v_mfma_f32_16x16x32_bf16 v[116:119], v[104:107], v[84:87], v[132:135]
	v_mfma_f32_16x16x32_bf16 v[136:139], v[112:115], v[2:5], v[120:123]
	v_mfma_f32_16x16x32_bf16 v[132:135], v[112:115], v[10:13], v[124:127]
	v_mfma_f32_16x16x32_bf16 v[124:127], v[112:115], v[60:63], v[216:219]
	v_mfma_f32_16x16x32_bf16 v[120:123], v[112:115], v[84:87], v[236:239]
	s_andn2_b64 vcc, exec, s[6:7]
	s_cbranch_vccnz .LBB0_959
	v_add_u32_e32 v108, s38, v174
	v_add_u32_e32 v112, s38, v176
	ds_read_b128 v[100:103], v108
	ds_read_b128 v[104:107], v112
	ds_read_b128 v[108:111], v108 offset:512
	ds_read_b128 v[112:115], v112 offset:512
	v_cvt_pk_bf16_f32 v215, v214, v215
	v_cvt_pk_bf16_f32 v214, v212, v213
	v_cvt_pk_bf16_f32 v213, v204, v206
	v_cvt_pk_bf16_f32 v212, v193, v194
	v_cvt_pk_bf16_f32 v219, v210, v211
	v_cvt_pk_bf16_f32 v218, v197, v209
	v_cvt_pk_bf16_f32 v217, v188, v190
	v_cvt_pk_bf16_f32 v216, v185, v186
	v_cvt_pk_bf16_f32 v207, v207, v208
	v_cvt_pk_bf16_f32 v206, v203, v205
	v_cvt_pk_bf16_f32 v205, v183, v184
	v_cvt_pk_bf16_f32 v204, v181, v182
	v_cvt_pk_bf16_f32 v183, v191, v192
	v_cvt_pk_bf16_f32 v182, v187, v189
	v_cvt_pk_bf16_f32 v181, v179, v180
	v_cvt_pk_bf16_f32 v180, v177, v178
	s_waitcnt lgkmcnt(7)
	s_nop 0
	v_mfma_f32_16x16x32_bf16 v[96:99], v[160:163], v[180:183], v[96:99]
	v_mfma_f32_16x16x32_bf16 v[92:95], v[160:163], v[204:207], v[92:95]
	v_mfma_f32_16x16x32_bf16 v[88:91], v[160:163], v[216:219], v[88:91]
	v_mfma_f32_16x16x32_bf16 v[80:83], v[160:163], v[212:215], v[80:83]
	s_waitcnt lgkmcnt(6)
	v_mfma_f32_16x16x32_bf16 v[72:75], v[156:159], v[180:183], v[72:75]
	v_mfma_f32_16x16x32_bf16 v[68:71], v[156:159], v[204:207], v[68:71]
	v_mfma_f32_16x16x32_bf16 v[64:67], v[156:159], v[216:219], v[64:67]
	v_mfma_f32_16x16x32_bf16 v[52:55], v[156:159], v[212:215], v[52:55]
	s_waitcnt lgkmcnt(5)
	v_mfma_f32_16x16x32_bf16 v[48:51], v[152:155], v[180:183], v[48:51]
	v_mfma_f32_16x16x32_bf16 v[44:47], v[152:155], v[204:207], v[44:47]
	v_mfma_f32_16x16x32_bf16 v[40:43], v[152:155], v[216:219], v[40:43]
	v_mfma_f32_16x16x32_bf16 v[36:39], v[152:155], v[212:215], v[36:39]
	s_waitcnt lgkmcnt(4)
	v_mfma_f32_16x16x32_bf16 v[32:35], v[148:151], v[180:183], v[32:35]
	v_mfma_f32_16x16x32_bf16 v[28:31], v[148:151], v[204:207], v[28:31]
	v_mfma_f32_16x16x32_bf16 v[18:21], v[148:151], v[216:219], v[18:21]
	v_mfma_f32_16x16x32_bf16 v[14:17], v[148:151], v[212:215], v[14:17]

; #define LAS __attribute__((address_space(3)))
; template <int DQK, int DV, bool LEAD> ...
;     ...
;     const int tid = tid_, lane = tid & 63, q16 = lane & 15, g4 = lane >> 4, hi = lane >> 5; const int wid = __builtin_amdgcn_readfirstlane(tid >> 6);
;     const int kg = KS ? (wid >> 2) : 0, qoff = KS ? (wid & 3) * 64 : wid * 32;
;     const unsigned lds0 = (unsigned)(uintptr_t)shm;
;     const int krow_l = wid * 8 + (lane >> 3);
;     const int kc_l = (lane & 7) ^ (((krow_l >> 1) & 1) | (((krow_l >> 3) & 1) << 1) | (((krow_l >> 4) & 1) << 2));
;     const int vc_l = (lane & 7) ^ ((krow_l >> 1) & 7);
;     const bf16_t* ksrc = K + (size_t)(krow0 + krow_l) * kpitch + kc_l * 8;
;     const int rrow_l = (wid & 3) * 16 + (lane >> 2), rc_l = (lane & 3) ^ (((rrow_l >> 4) & 1) << 1);
;     const bf16_t* krsrc = (DQK == 96) ? KR + (size_t)(krow0 + rrow_l) * 32 + rc_l * 8 : nullptr;
;     const bf16_t* vsrc = Vt + (size_t)krow_l * NR + krow0 + vc_l * 8;
;     const unsigned kdst = lds0 + KOFF + wid * 1024, krdst = lds0 + KOFF + 8192 + (wid & 3) * 1024, vdst = lds0 + VOFF + wid * 1024;
;     ...
;     const int kr0 = 8 * (q16 >> 2) + (q16 & 3);
;     const int fk = ((kr0 >> 1) & 1) | (((kr0 >> 3) & 1) << 1) | (((kr0 >> 4) & 1) << 2);
;     const LAS unsigned char* kp[2]; const LAS unsigned char* vp[2];
; #pragma unroll
;     for (int ds = 0; ds < 2; ++ds) kp[ds] = shm + KOFF + kr0 * 128 + ((((ds << 2) | g4) ^ fk) << 4) + kg * 4096;
;     const LAS unsigned char* krp = shm + KOFF + 8192 + kr0 * 64 + ((g4 ^ (((kr0 >> 4) & 1) << 1)) << 4) + kg * 2048;
; #pragma unroll
;     for (int s_ = 0; s_ < 2; ++s_) vp[s_] = shm + VOFF + q16 * 128 + ((((s_ << 2) | g4) ^ ((q16 >> 1) & 7)) << 4);
;     const LAS unsigned char* vpk = kg ? vp[1] : vp[0];
;     ...
;     ATT_DMA_K(0, 0); ATT_DMA_V(0, 0); ATT_DMA_K(1, 1); ATT_DMA_K(2, 2);
;     bf16x8 qf[NQB * NDS];
;     {
;       const float c2 = (DQK == 64) ? C2_EVEN : C2_ODD; const bool lat = tq0 >= 0;
; #pragma unroll
;       for (int qb = 0; qb < NQB; ++qb) {
;           const bf16_t* qp = Q + (size_t)(qrow0 + qoff + qb * 16 + q16) * qpitch + g4 * 8;
;           bf16x8 raw[NDS];
; #pragma unroll
;           for (int ds = 0; ds < NDS; ++ds) raw[ds] = *(const bf16x8*)(qp + ds * 32);
.LBB0_962:
	s_and_b64 vcc, exec, s[4:5]
	s_cbranch_vccz .LBB0_954
	v_mov_b32_e32 v168, v0
	s_ashr_i32 s45, s44, 31
	v_readfirstlane_b32 s16, v168
	s_ashr_i32 s4, s16, 6
	v_bfe_u32 v1, v168, 3, 3
	v_lshl_or_b32 v7, s4, 3, v1
	s_lshl_b32 s5, s4, 1
	s_lshr_b32 s6, s16, 5
	v_ashrrev_i32_e32 v2, 1, v7
	s_and_b32 s5, s5, 2
	s_and_b32 s6, s6, 4
	v_and_b32_e32 v170, 7, v168
	v_and_b32_e32 v3, 1, v2
	s_or_b32 s5, s5, s6
	s_and_b32 s7, s4, 3
	v_bitop3_b32 v8, s5, v170, v3 bitop3:0x36
	v_xor_b32_e32 v9, v2, v168
	v_add_u32_e32 v4, s44, v7
	s_lshl_b32 s4, s4, 10
	v_mov_b64_e32 v[2:3], s[36:37]
	s_add_i32 s49, s4, 0
	v_mad_i64_i32 v[2:3], s[4:5], v4, s92, v[2:3]
	v_mov_b64_e32 v[4:5], s[40:41]
	v_lshlrev_b32_e32 v194, 4, v8
	v_mad_i64_i32 v[4:5], s[4:5], v7, s91, v[4:5]
	v_lshl_add_u64 v[162:163], v[2:3], 0, v[194:195]
	v_lshlrev_b32_e32 v2, 4, v9
	v_lshl_add_u64 v[4:5], s[44:45], 1, v[4:5]
	v_and_b32_e32 v194, 0x70, v2
	s_mov_b32 m0, s49
	s_nop 0
	global_load_lds_dwordx4 v[162:163], off
	v_lshl_add_u64 v[164:165], v[4:5], 0, v[194:195]
	s_add_i32 s36, s49, 0x9000
	s_mov_b32 m0, s36
	s_nop 0
	global_load_lds_dwordx4 v[164:165], off
	s_mov_b64 s[4:5], 0x38000
	s_lshl_b32 s37, s7, 6
	v_lshl_add_u64 v[2:3], v[162:163], 0, s[4:5]
	s_add_i32 s4, s49, 0x2000
	s_mov_b32 m0, s4
	s_nop 0
	global_load_lds_dwordx4 v[2:3], off
	v_and_b32_e32 v6, 15, v168
	s_mov_b64 s[4:5], 0x70000
	s_or_b32 s6, s37, s48
	v_and_b32_e32 v194, 48, v168
	v_lshrrev_b32_e32 v40, 1, v168
	v_lshlrev_b32_e32 v173, 7, v6
	v_lshl_add_u64 v[2:3], v[162:163], 0, s[4:5]
	s_add_i32 s4, s49, 0x4000
	v_or_b32_e32 v22, s6, v6
	v_lshl_add_u64 v[6:7], s[28:29], 0, v[194:195]
	s_mov_b32 m0, s4
	s_nop 0
	global_load_lds_dwordx4 v[2:3], off
	v_and_b32_e32 v41, 8, v40
	v_mad_i64_i32 v[8:9], s[4:5], v22, s92, v[6:7]
	v_or_b32_e32 v10, 16, v22
	v_or_b32_e32 v18, 32, v22
	v_or_b32_e32 v22, 48, v22
	v_lshl_or_b32 v194, v41, 3, v173
	v_mad_i64_i32 v[16:17], s[4:5], v10, s92, v[6:7]
	v_mad_i64_i32 v[18:19], s[4:5], v18, s92, v[6:7]
	v_mad_i64_i32 v[34:35], s[4:5], v22, s92, v[6:7]
	v_lshl_add_u64 v[14:15], s[8:9], 0, v[194:195]
	s_mov_b64 s[4:5], 0x1800
	v_lshl_add_u64 v[36:37], v[14:15], 0, s[4:5]
	s_movk_i32 s4, 0x1000
	v_add_co_u32_e32 v38, vcc, s4, v14
	global_load_dwordx4 v[2:5], v194, s[8:9] offset:48
	v_lshl_add_u64 v[20:21], v[14:15], 0, s[60:61]
	v_addc_co_u32_e32 v39, vcc, 0, v15, vcc
	global_load_dwordx4 v[74:77], v[8:9], off offset:64
	global_load_dwordx4 v[124:127], v[16:17], off offset:64
	global_load_dwordx4 v[10:13], v194, s[8:9] offset:2096
	global_load_dwordx4 v[142:145], v[18:19], off offset:64
	global_load_dwordx4 v[70:73], v[20:21], off offset:48
	global_load_dwordx4 v[154:157], v[34:35], off offset:64
	global_load_dwordx4 v[26:29], v[36:37], off offset:48
	global_load_dwordx4 v[100:103], v194, s[8:9] offset:32
	global_load_dwordx4 v[92:95], v194, s[8:9] offset:2080
	global_load_dwordx4 v[66:69], v[20:21], off offset:32
	global_load_dwordx4 v[30:33], v[36:37], off offset:32
	global_load_dwordx4 v[108:111], v[8:9], off
	s_nop 0
	global_load_dwordx4 v[6:9], v194, s[8:9]
	global_load_dwordx4 v[104:107], v[16:17], off
	global_load_dwordx4 v[96:99], v194, s[8:9] offset:16
	global_load_dwordx4 v[80:83], v[18:19], off
	global_load_dwordx4 v[84:87], v194, s[8:9] offset:2064
	global_load_dwordx4 v[22:25], v[38:39], off
	s_nop 0
	global_load_dwordx4 v[14:17], v[34:35], off
	global_load_dwordx4 v[88:91], v194, s[8:9] offset:2048
	s_lshl_b32 s4, s16, 4
	global_load_dwordx4 v[18:21], v[20:21], off offset:16
	v_lshlrev_b32_e32 v172, 1, v168
	v_and_b32_e32 v34, 3, v168
	s_and_b32 s4, s4, 0xfffff000
	v_and_or_b32 v42, v172, 24, v34
	s_add_i32 s4, s4, 0
	v_lshl_add_u32 v169, v42, 7, s4
	s_or_b32 s4, s47, s37
	v_bfe_u32 v171, v168, 4, 2
	s_lshr_b32 s4, s4, 2
	v_bitop3_b32 v40, v171, v40, 7 bitop3:0x78
	s_and_b32 s4, s4, 0x7f0
	v_lshlrev_b32_e32 v177, 4, v40
	v_or_b32_e32 v40, s4, v41
	v_lshlrev_b32_e32 v40, 3, v40
	global_load_dwordx4 v[34:37], v[36:37], off offset:16
	v_lshlrev_b32_e32 v78, 5, v171
	global_load_dwordx4 v[42:45], v40, s[8:9] offset:48
	global_load_dwordx4 v[46:49], v40, s[8:9] offset:32
	global_load_dwordx4 v[50:53], v40, s[8:9] offset:16
	global_load_dwordx4 v[54:57], v40, s[8:9]
	s_nop 0
	global_load_dwordx4 v[38:41], v[38:39], off offset:2048
	s_nop 0
	global_load_dwordx4 v[58:61], v78, s[26:27] offset:144
	global_load_dwordx4 v[62:65], v78, s[26:27] offset:128
	v_and_b32_e32 v174, 63, v168
	v_cmp_gt_u32_e32 vcc, 32, v174
	s_mov_b32 s4, 0x358637bd
	s_mov_b32 s12, 0x3c800000
	v_add_u32_e32 v175, v169, v177
	s_mov_b32 s28, 1
	v_or_b32_e32 v176, 4, v171
	s_mov_b32 s29, 0
	s_waitcnt vmcnt(22)
	v_cndmask_b32_e64 v113, v29, -v29, vcc
	v_cndmask_b32_e64 v146, v3, -v3, vcc
	v_mov_b32_e32 v3, v4
	v_cndmask_b32_e64 v147, v5, -v5, vcc
	s_waitcnt vmcnt(20)
	v_cndmask_b32_e64 v133, v95, -v95, vcc
	s_waitcnt vmcnt(17)
	v_and_b32_e32 v181, 0xffff0000, v108
	v_lshlrev_b32_e32 v180, 16, v108
	v_mul_f32_e32 v4, v181, v181
	v_and_b32_e32 v131, 0xffff0000, v127
	v_lshlrev_b32_e32 v130, 16, v127
	v_cndmask_b32_e64 v129, v13, -v13, vcc
	v_cndmask_b32_e64 v128, v11, -v11, vcc
	v_mov_b32_e32 v11, v12
	v_and_b32_e32 v119, 0xffff0000, v145
	v_lshlrev_b32_e32 v118, 16, v145
	v_and_b32_e32 v115, 0xffff0000, v157
	v_lshlrev_b32_e32 v114, 16, v157
	v_cndmask_b32_e64 v13, v103, -v103, vcc
	v_cndmask_b32_e64 v12, v101, -v101, vcc
	v_mov_b32_e32 v101, v102
	v_and_b32_e32 v135, 0xffff0000, v126
	v_lshlrev_b32_e32 v134, 16, v126
	v_cndmask_b32_e64 v132, v93, -v93, vcc
	v_mov_b32_e32 v93, v94
	v_and_b32_e32 v103, 0xffff0000, v144
	v_lshlrev_b32_e32 v102, 16, v144
	v_cndmask_b32_e64 v95, v69, -v69, vcc
	v_cndmask_b32_e64 v94, v67, -v67, vcc
	v_mov_b32_e32 v67, v68
	v_and_b32_e32 v69, 0xffff0000, v156
	v_lshlrev_b32_e32 v68, 16, v156
	s_waitcnt vmcnt(14)
; template <int DQK, int DV, bool LEAD> ...
;     ...
;           float x[NDS][8];
; #pragma unroll
;           for (int ds = 0; ds < NDS; ++ds)
; #pragma unroll
;               for (int j = 0; j < 8; ++j) x[ds][j] = __uint_as_float(((unsigned)(unsigned short)raw[ds][j]) << 16);
;           const int tq = tq0 + qoff + qb * 16 + q16, prow = (tq >> 6) & 127, pcol = tq & 63;
;           float sn = 0.f;
; #pragma unroll
;           for (int ds = 0; ds < 2; ++ds)
; #pragma unroll
;               for (int j = 0; j < 8; ++j) sn += x[ds][j] * x[ds][j];
;           sn = lanes4_sum(sn);
;           const float rn = rsqrtf(sn * (1.f / 64.f) + EPS);
; #pragma unroll
;           for (int ds = 0; ds < 2; ++ds)
; #pragma unroll
;               for (int j = 0; j < 8; ++j) x[ds][j] *= rn * qgain[32 * ds + 8 * g4 + j];
	v_cndmask_b32_e64 v157, v99, -v99, vcc
	v_cndmask_b32_e64 v156, v97, -v97, vcc
	v_mov_b32_e32 v97, v98
	v_and_b32_e32 v139, 0xffff0000, v125
	v_lshlrev_b32_e32 v138, 16, v125
	v_and_b32_e32 v123, 0xffff0000, v143
	v_lshlrev_b32_e32 v122, 16, v143
	v_and_b32_e32 v141, 0xffff0000, v124
	v_lshlrev_b32_e32 v140, 16, v124
	v_and_b32_e32 v127, 0xffff0000, v142
	v_lshlrev_b32_e32 v126, 16, v142
	s_waitcnt vmcnt(11)
	v_cndmask_b32_e64 v125, v25, -v25, vcc
	v_cndmask_b32_e64 v124, v23, -v23, vcc
	v_mov_b32_e32 v23, v24
	v_and_b32_e32 v143, 0xffff0000, v107
	v_lshlrev_b32_e32 v142, 16, v107
	v_and_b32_e32 v25, 0xffff0000, v83
	v_lshlrev_b32_e32 v24, 16, v83
	s_waitcnt vmcnt(10)
	v_and_b32_e32 v99, 0xffff0000, v17
	v_lshlrev_b32_e32 v98, 16, v17
	v_and_b32_e32 v145, 0xffff0000, v106
	v_lshlrev_b32_e32 v144, 16, v106
	v_and_b32_e32 v107, 0xffff0000, v82
	v_lshlrev_b32_e32 v106, 16, v82
	v_and_b32_e32 v83, 0xffff0000, v16
	v_lshlrev_b32_e32 v82, 16, v16
	v_and_b32_e32 v17, 0xffff0000, v109
	v_lshlrev_b32_e32 v16, 16, v109
	v_pk_fma_f32 v[4:5], v[180:181], v[180:181], v[4:5] op_sel_hi:[1,1,0]
	v_and_b32_e32 v151, 0xffff0000, v77
	v_lshlrev_b32_e32 v150, 16, v77
	v_cndmask_b32_e64 v117, v73, -v73, vcc
	v_cndmask_b32_e64 v116, v71, -v71, vcc
	v_mov_b32_e32 v71, v72
	v_and_b32_e32 v153, 0xffff0000, v76
	v_lshlrev_b32_e32 v152, 16, v76
	v_and_b32_e32 v159, 0xffff0000, v75
	v_lshlrev_b32_e32 v158, 16, v75
	v_and_b32_e32 v167, 0xffff0000, v74
	v_lshlrev_b32_e32 v166, 16, v74
	global_load_dwordx4 v[72:75], v78, s[26:27] offset:16
	s_nop 0
	global_load_dwordx4 v[76:79], v78, s[26:27]
	v_pk_fma_f32 v[4:5], v[16:17], v[16:17], v[4:5]
	v_mul_f32_e32 v108, v17, v17
	v_and_b32_e32 v179, 0xffff0000, v110
	v_lshlrev_b32_e32 v178, 16, v110
	v_pk_add_f32 v[4:5], v[108:109], v[4:5] op_sel_hi:[0,1]
	v_pk_fma_f32 v[4:5], v[178:179], v[178:179], v[4:5]
	v_mul_f32_e32 v108, v179, v179
	v_cndmask_b32_e64 v161, v9, -v9, vcc
	v_cndmask_b32_e64 v160, v7, -v7, vcc
	v_mov_b32_e32 v7, v8
	v_and_b32_e32 v9, 0xffff0000, v111
	v_lshlrev_b32_e32 v8, 16, v111
	v_pk_add_f32 v[4:5], v[108:109], v[4:5] op_sel_hi:[0,1]
	v_pk_fma_f32 v[4:5], v[8:9], v[8:9], v[4:5]
	v_mul_f32_e32 v108, v9, v9
	v_pk_add_f32 v[4:5], v[108:109], v[4:5] op_sel_hi:[0,1]
	v_pk_fma_f32 v[4:5], v[166:167], v[166:167], v[4:5]
	v_mul_f32_e32 v108, v167, v167
	v_pk_add_f32 v[4:5], v[108:109], v[4:5] op_sel_hi:[0,1]
	v_pk_fma_f32 v[4:5], v[158:159], v[158:159], v[4:5]
	v_mul_f32_e32 v108, v159, v159
	v_pk_add_f32 v[4:5], v[108:109], v[4:5] op_sel_hi:[0,1]
	v_pk_fma_f32 v[4:5], v[152:153], v[152:153], v[4:5]
	v_mul_f32_e32 v108, v153, v153
	v_pk_add_f32 v[4:5], v[108:109], v[4:5] op_sel_hi:[0,1]
	v_pk_fma_f32 v[4:5], v[150:151], v[150:151], v[4:5]
	v_mul_f32_e32 v108, v151, v151
	v_pk_add_f32 v[4:5], v[108:109], v[4:5] op_sel_hi:[0,1]
	v_mov_b32_e32 v5, v4
	s_nop 1
	v_permlane16_swap_b32_e32 v4, v5
	v_add_f32_e32 v5, v4, v5
	v_cndmask_b32_e64 v137, v87, -v87, vcc
	v_cndmask_b32_e64 v136, v85, -v85, vcc
	v_mov_b32_e32 v85, v86
	v_and_b32_e32 v87, 0xffff0000, v155
	v_lshlrev_b32_e32 v86, 16, v155
	v_and_b32_e32 v149, 0xffff0000, v105
	v_lshlrev_b32_e32 v148, 16, v105
	v_mov_b32_e32 v105, v5
	v_and_b32_e32 v155, 0xffff0000, v104
	s_waitcnt vmcnt(10)
	v_cndmask_b32_e64 v121, v21, -v21, vcc
	v_cndmask_b32_e64 v120, v19, -v19, vcc
	v_mov_b32_e32 v19, v20
	v_cndmask_b32_e64 v21, v91, -v91, vcc
	v_cndmask_b32_e64 v20, v89, -v89, vcc
	v_mov_b32_e32 v89, v90
	v_and_b32_e32 v91, 0xffff0000, v154
	v_lshlrev_b32_e32 v90, 16, v154
	v_permlane32_swap_b32_e32 v5, v105
	v_lshlrev_b32_e32 v154, 16, v104
	v_mul_f32_e32 v4, v155, v155
	v_pk_fma_f32 v[108:109], v[154:155], v[154:155], v[4:5] op_sel_hi:[1,1,0]
	v_mul_f32_e32 v4, v149, v149
	v_pk_fma_f32 v[108:109], v[148:149], v[148:149], v[108:109]
	v_cndmask_b32_e64 v112, v27, -v27, vcc
	v_pk_add_f32 v[108:109], v[4:5], v[108:109] op_sel_hi:[0,1]
	v_pk_fma_f32 v[108:109], v[144:145], v[144:145], v[108:109]
	v_mul_f32_e32 v4, v145, v145
	v_pk_add_f32 v[108:109], v[4:5], v[108:109] op_sel_hi:[0,1]
	v_pk_fma_f32 v[108:109], v[142:143], v[142:143], v[108:109]
	v_mul_f32_e32 v4, v143, v143
	v_pk_add_f32 v[108:109], v[4:5], v[108:109] op_sel_hi:[0,1]
	v_pk_fma_f32 v[108:109], v[140:141], v[140:141], v[108:109]
	v_mul_f32_e32 v4, v141, v141
	v_pk_add_f32 v[108:109], v[4:5], v[108:109] op_sel_hi:[0,1]
	v_pk_fma_f32 v[108:109], v[138:139], v[138:139], v[108:109]
	v_mul_f32_e32 v4, v139, v139
	v_pk_add_f32 v[108:109], v[4:5], v[108:109] op_sel_hi:[0,1]
	v_pk_fma_f32 v[108:109], v[134:135], v[134:135], v[108:109]
	v_mul_f32_e32 v4, v135, v135
	v_pk_add_f32 v[108:109], v[4:5], v[108:109] op_sel_hi:[0,1]
	v_pk_fma_f32 v[108:109], v[130:131], v[130:131], v[108:109]
	v_mul_f32_e32 v4, v131, v131
	v_pk_add_f32 v[108:109], v[4:5], v[108:109] op_sel_hi:[0,1]
	v_mov_b32_e32 v4, v108
	s_nop 1
	v_permlane16_swap_b32_e32 v108, v4
	v_add_f32_e32 v4, v108, v4
	v_mov_b32_e32 v104, v4
	s_nop 1
	v_permlane32_swap_b32_e32 v4, v104
	v_pk_add_f32 v[4:5], v[4:5], v[104:105]
	v_mov_b64_e32 v[108:109], s[4:5]
	v_pk_fma_f32 v[182:183], v[4:5], s[12:13], v[108:109] op_sel_hi:[1,0,0]
	s_waitcnt vmcnt(5)
	v_cndmask_b32_e64 v104, v55, -v55, vcc
	v_mul_f32_e32 v4, 0x4b800000, v183
	v_cmp_gt_f32_e64 s[4:5], s95, v183
	v_mov_b32_e32 v55, v56
	v_mov_b32_e32 v27, v28
	v_cndmask_b32_e64 v4, v183, v4, s[4:5]
	v_rsq_f32_e32 v4, v4
	v_cndmask_b32_e64 v29, v33, -v33, vcc
	v_cndmask_b32_e64 v28, v31, -v31, vcc
	v_mov_b32_e32 v31, v32
	v_mul_f32_e32 v5, 0x45800000, v4
	v_cndmask_b32_e64 v56, v4, v5, s[4:5]
	s_waitcnt vmcnt(3)
; __device__ __forceinline__ unsigned cvtpk(float lo, float hi) { f32x2 v = {lo, hi}; bf16x2_t b = __builtin_convertvector(v, bf16x2_t); return __builtin_bit_cast(unsigned, b); }
; template <int DQK, int DV, bool LEAD> ...
;     ...
; #pragma unroll
;           for (int ds = 0; ds < 2; ++ds)
; #pragma unroll
;               for (int j = 0; j < 8; ++j) x[ds][j] *= rn * qgain[32 * ds + 8 * g4 + j];
;           if constexpr (DQK == 64) {
; #pragma unroll
;               for (int ds = 0; ds < 2; ++ds)
; #pragma unroll
;                   for (int j = 0; j < 8; ++j) {
;                       auto rr = __builtin_amdgcn_permlane32_swap(__float_as_uint(x[ds][j]), __float_as_uint(x[ds][j]), false, false);
;                       const float other = hi ? __uint_as_float(rr[0]) : __uint_as_float(rr[1]);
;                       float cc = 1.f, sg = 0.f;
;                       if (lat) { const f32x2 cs = rope[(ds ? pcol : prow) * 16 + 8 * (g4 & 1) + j]; cc = cs.x; sg = hi ? cs.y : -cs.y; }
;                       x[ds][j] = x[ds][j] * cc + other * sg; }
;           } else {
;               float sr = 0.f;
; #pragma unroll
;               for (int j = 0; j < 8; ++j) sr += x[2][j] * x[2][j];
;               sr = lanes4_sum(sr);
;               const float rq = rsqrtf(sr * (1.f / 32.f) + EPS);
; #pragma unroll
;               for (int j = 0; j < 8; ++j) { const float av = x[2][j] * rq * qgain[64 + 8 * g4 + j];
;                   auto rr = __builtin_amdgcn_permlane16_swap(__float_as_uint(av), __float_as_uint(av), false, false);
;                   const float other = (g4 & 1) ? __uint_as_float(rr[0]) : __uint_as_float(rr[1]);
;                   float cc = 1.f, sg = 0.f;
;                   if (lat) { const f32x2 cs = rope[((g4 & 2) ? pcol : prow) * 8 + j]; cc = cs.x; sg = (g4 & 1) ? cs.y : -cs.y; }
;                   x[2][j] = av * cc + other * sg; }
;           }
; #pragma unroll
;           for (int ds = 0; ds < NDS; ++ds) { u32x4 w;
; #pragma unroll
;               for (int i = 0; i < 4; ++i) w[i] = cvtpk(x[ds][2 * i] * c2, x[ds][2 * i + 1] * c2);
;               qf[qb * NDS + ds] = __builtin_bit_cast(bf16x8, w); }
	v_pk_mul_f32 v[4:5], v[56:57], v[60:61] op_sel_hi:[0,1]
	v_pk_mul_f32 v[4:5], v[4:5], v[150:151]
	v_cndmask_b32_e64 v33, v37, -v37, vcc
	v_cndmask_b32_e64 v32, v35, -v35, vcc
	v_mov_b32_e32 v35, v36
	v_cndmask_b32_e64 v37, v41, -v41, vcc
	v_cndmask_b32_e64 v36, v39, -v39, vcc
	v_mov_b32_e32 v39, v40
	v_cndmask_b32_e64 v41, v45, -v45, vcc
	v_cndmask_b32_e64 v40, v43, -v43, vcc
	v_mov_b32_e32 v43, v44
	v_cndmask_b32_e64 v45, v49, -v49, vcc
	v_cndmask_b32_e64 v44, v47, -v47, vcc
	v_mov_b32_e32 v47, v48
	v_cndmask_b32_e64 v49, v53, -v53, vcc
	v_cndmask_b32_e64 v48, v51, -v51, vcc
	v_mov_b32_e32 v51, v52
	v_and_b32_e32 v111, 0xffff0000, v81
	v_lshlrev_b32_e32 v110, 16, v81
	v_and_b32_e32 v53, 0xffff0000, v15
	v_lshlrev_b32_e32 v52, 16, v15
	v_cndmask_b32_e64 v105, v57, -v57, vcc
	v_mov_b32_e32 v15, v4
	v_mov_b32_e32 v57, v4
	v_mov_b32_e32 v81, v5
	v_mov_b32_e32 v150, v5
	v_permlane32_swap_b32_e32 v15, v57
	s_nop 0
	v_permlane32_swap_b32_e32 v81, v150
	v_cndmask_b32_e32 v151, v81, v150, vcc
	v_cndmask_b32_e32 v150, v15, v57, vcc
	v_pk_mul_f32 v[146:147], v[146:147], v[150:151]
	v_cmp_gt_f32_e64 s[4:5], s95, v182
	v_pk_fma_f32 v[2:3], v[4:5], v[2:3], v[146:147]
	s_lshl_b32 s26, s46, 8
	v_pk_mul_f32 v[2:3], v[2:3], s[94:95] op_sel_hi:[1,0]
	s_cmpk_lt_u32 s16, 0x100
	v_cvt_pk_bf16_f32 v5, v2, v3
	v_pk_mul_f32 v[2:3], v[56:57], v[58:59] op_sel_hi:[0,1]
	v_pk_mul_f32 v[2:3], v[2:3], v[152:153]
	s_mov_b32 s27, 2
	v_mov_b32_e32 v4, v2
	v_mov_b32_e32 v15, v2
	v_mov_b32_e32 v57, v3
	v_mov_b32_e32 v81, v3
	v_permlane32_swap_b32_e32 v4, v15
	s_nop 0
	v_permlane32_swap_b32_e32 v57, v81
	v_cndmask_b32_e32 v147, v57, v81, vcc
	v_cndmask_b32_e32 v146, v4, v15, vcc
	v_pk_mul_f32 v[12:13], v[12:13], v[146:147]
	s_nop 0
	v_pk_fma_f32 v[2:3], v[2:3], v[100:101], v[12:13]
	s_nop 0
	v_pk_mul_f32 v[2:3], v[2:3], s[94:95] op_sel_hi:[1,0]
	s_nop 0
	v_cvt_pk_bf16_f32 v4, v2, v3
	s_waitcnt vmcnt(2)
	v_pk_mul_f32 v[2:3], v[56:57], v[64:65] op_sel_hi:[0,1]
	v_pk_mul_f32 v[2:3], v[2:3], v[158:159]
	s_nop 0
	v_mov_b32_e32 v12, v2
	v_mov_b32_e32 v15, v2
	v_mov_b32_e32 v13, v3
	v_mov_b32_e32 v57, v3
	v_permlane32_swap_b32_e32 v12, v15
	s_nop 0
	v_permlane32_swap_b32_e32 v13, v57
	v_cndmask_b32_e32 v13, v13, v57, vcc
	v_cndmask_b32_e32 v12, v12, v15, vcc
	v_pk_mul_f32 v[12:13], v[156:157], v[12:13]
	s_nop 0
	v_pk_fma_f32 v[2:3], v[2:3], v[96:97], v[12:13]
	v_pk_mul_f32 v[12:13], v[62:63], v[56:57] op_sel_hi:[1,0]
	v_pk_mul_f32 v[2:3], v[2:3], s[94:95] op_sel_hi:[1,0]
	v_pk_mul_f32 v[12:13], v[12:13], v[166:167]
	v_cvt_pk_bf16_f32 v3, v2, v3
	v_mov_b32_e32 v2, v12
	v_mov_b32_e32 v15, v12
	v_mov_b32_e32 v57, v13
	v_mov_b32_e32 v81, v13
	v_permlane32_swap_b32_e32 v2, v15
	s_nop 0
	v_permlane32_swap_b32_e32 v57, v81
	v_cndmask_b32_e32 v97, v57, v81, vcc
	v_cndmask_b32_e32 v96, v2, v15, vcc
	v_pk_mul_f32 v[96:97], v[160:161], v[96:97]
	s_nop 0
	v_pk_fma_f32 v[6:7], v[12:13], v[6:7], v[96:97]
	s_nop 0
	v_pk_mul_f32 v[6:7], v[6:7], s[94:95] op_sel_hi:[1,0]
	s_nop 0
	v_cvt_pk_bf16_f32 v2, v6, v7
	s_waitcnt vmcnt(1)
	v_pk_mul_f32 v[6:7], v[74:75], v[56:57] op_sel_hi:[1,0]
	s_nop 0
	v_pk_mul_f32 v[6:7], v[6:7], v[8:9]
	s_nop 0
	v_mov_b32_e32 v8, v6
	v_mov_b32_e32 v12, v6
	v_mov_b32_e32 v9, v7
	v_mov_b32_e32 v13, v7
	v_permlane32_swap_b32_e32 v8, v12
	s_nop 0
	v_permlane32_swap_b32_e32 v9, v13
	v_cndmask_b32_e32 v9, v9, v13, vcc
	v_cndmask_b32_e32 v8, v8, v12, vcc
	v_pk_mul_f32 v[8:9], v[40:41], v[8:9]
	s_nop 0
	v_pk_fma_f32 v[6:7], v[6:7], v[42:43], v[8:9]
	s_nop 0
	v_pk_mul_f32 v[6:7], v[6:7], s[94:95] op_sel_hi:[1,0]
	s_nop 0
	v_cvt_pk_bf16_f32 v9, v6, v7
	v_pk_mul_f32 v[6:7], v[72:73], v[56:57] op_sel_hi:[1,0]
	s_nop 0
	v_pk_mul_f32 v[6:7], v[6:7], v[178:179]
	s_nop 0
	v_mov_b32_e32 v8, v6
	v_mov_b32_e32 v12, v6
	v_mov_b32_e32 v13, v7
	v_mov_b32_e32 v15, v7
	v_permlane32_swap_b32_e32 v8, v12
	s_nop 0
	v_permlane32_swap_b32_e32 v13, v15
	v_cndmask_b32_e32 v13, v13, v15, vcc
	v_cndmask_b32_e32 v12, v8, v12, vcc
	v_pk_mul_f32 v[12:13], v[44:45], v[12:13]
	s_nop 0
	v_pk_fma_f32 v[6:7], v[6:7], v[46:47], v[12:13]
	s_nop 0
	v_pk_mul_f32 v[6:7], v[6:7], s[94:95] op_sel_hi:[1,0]
	s_nop 0
	v_cvt_pk_bf16_f32 v8, v6, v7
	s_waitcnt vmcnt(0)
	v_pk_mul_f32 v[6:7], v[78:79], v[56:57] op_sel_hi:[1,0]
	s_nop 0
	v_pk_mul_f32 v[6:7], v[6:7], v[16:17]
	s_nop 0
	v_mov_b32_e32 v12, v6
	v_mov_b32_e32 v15, v6
	v_mov_b32_e32 v13, v7
	v_mov_b32_e32 v16, v7
	v_permlane32_swap_b32_e32 v12, v15
	s_nop 0
	v_permlane32_swap_b32_e32 v13, v16
	v_cndmask_b32_e32 v13, v13, v16, vcc
	v_cndmask_b32_e32 v12, v12, v15, vcc
	v_pk_mul_f32 v[12:13], v[48:49], v[12:13]
	s_nop 0
	v_pk_fma_f32 v[6:7], v[6:7], v[50:51], v[12:13]
	v_pk_mul_f32 v[12:13], v[76:77], v[56:57] op_sel_hi:[1,0]
	v_pk_mul_f32 v[6:7], v[6:7], s[94:95] op_sel_hi:[1,0]
	v_pk_mul_f32 v[12:13], v[12:13], v[180:181]
	v_cvt_pk_bf16_f32 v7, v6, v7
	v_mov_b32_e32 v6, v12
	v_mov_b32_e32 v15, v12
	v_mov_b32_e32 v16, v13
	v_mov_b32_e32 v17, v13
	v_permlane32_swap_b32_e32 v6, v15
	s_nop 0
	v_permlane32_swap_b32_e32 v16, v17
	v_cndmask_b32_e32 v17, v16, v17, vcc
	v_cndmask_b32_e32 v16, v6, v15, vcc
	v_mul_f32_e32 v6, 0x4b800000, v182
	v_cndmask_b32_e64 v6, v182, v6, s[4:5]
	v_rsq_f32_e32 v15, v6
	v_pk_mul_f32 v[16:17], v[104:105], v[16:17]
	s_nop 0
	v_pk_fma_f32 v[12:13], v[12:13], v[54:55], v[16:17]
	s_nop 0
	v_pk_mul_f32 v[12:13], v[12:13], s[94:95] op_sel_hi:[1,0]
	s_nop 0
	v_cvt_pk_bf16_f32 v6, v12, v13
	v_mul_f32_e32 v12, 0x45800000, v15
	v_cndmask_b32_e64 v56, v15, v12, s[4:5]
	v_pk_mul_f32 v[12:13], v[60:61], v[56:57] op_sel_hi:[1,0]
	s_nop 0
	v_pk_mul_f32 v[12:13], v[12:13], v[130:131]
	s_nop 0
	v_mov_b32_e32 v15, v12
	v_mov_b32_e32 v16, v12
	v_mov_b32_e32 v17, v13
; template <int DQK, int DV, bool LEAD> ...
;     ...
;           float sn = 0.f;
; #pragma unroll
;           for (int ds = 0; ds < 2; ++ds)
; #pragma unroll
;               for (int j = 0; j < 8; ++j) sn += x[ds][j] * x[ds][j];
;           sn = lanes4_sum(sn);
;           const float rn = rsqrtf(sn * (1.f / 64.f) + EPS);
; #pragma unroll
;           for (int ds = 0; ds < 2; ++ds)
; #pragma unroll
;               for (int j = 0; j < 8; ++j) x[ds][j] *= rn * qgain[32 * ds + 8 * g4 + j];
;           if constexpr (DQK == 64) {
; #pragma unroll
;               for (int ds = 0; ds < 2; ++ds)
; #pragma unroll
;                   for (int j = 0; j < 8; ++j) {
;                       auto rr = __builtin_amdgcn_permlane32_swap(__float_as_uint(x[ds][j]), __float_as_uint(x[ds][j]), false, false);
;                       const float other = hi ? __uint_as_float(rr[0]) : __uint_as_float(rr[1]);
;                       float cc = 1.f, sg = 0.f;
;                       if (lat) { const f32x2 cs = rope[(ds ? pcol : prow) * 16 + 8 * (g4 & 1) + j]; cc = cs.x; sg = hi ? cs.y : -cs.y; }
;                       x[ds][j] = x[ds][j] * cc + other * sg; }
;           } else {
;               float sr = 0.f;
; #pragma unroll
;               for (int j = 0; j < 8; ++j) sr += x[2][j] * x[2][j];
;               sr = lanes4_sum(sr);
;               const float rq = rsqrtf(sr * (1.f / 32.f) + EPS);
; #pragma unroll
;               for (int j = 0; j < 8; ++j) { const float av = x[2][j] * rq * qgain[64 + 8 * g4 + j];
;                   auto rr = __builtin_amdgcn_permlane16_swap(__float_as_uint(av), __float_as_uint(av), false, false);
;                   const float other = (g4 & 1) ? __uint_as_float(rr[0]) : __uint_as_float(rr[1]);
;                   float cc = 1.f, sg = 0.f;
;                   if (lat) { const f32x2 cs = rope[((g4 & 2) ? pcol : prow) * 8 + j]; cc = cs.x; sg = (g4 & 1) ? cs.y : -cs.y; }
;                   x[2][j] = av * cc + other * sg; }
;           }
; #pragma unroll
;           for (int ds = 0; ds < NDS; ++ds) { u32x4 w;
; #pragma unroll
;               for (int i = 0; i < 4; ++i) w[i] = cvtpk(x[ds][2 * i] * c2, x[ds][2 * i + 1] * c2);
;               qf[qb * NDS + ds] = __builtin_bit_cast(bf16x8, w); }
	v_mov_b32_e32 v57, v13
	v_permlane32_swap_b32_e32 v15, v16
	s_nop 0
	v_permlane32_swap_b32_e32 v17, v57
	v_cndmask_b32_e32 v17, v17, v57, vcc
	v_cndmask_b32_e32 v16, v15, v16, vcc
	v_pk_mul_f32 v[16:17], v[128:129], v[16:17]
	s_nop 0
	v_pk_fma_f32 v[10:11], v[12:13], v[10:11], v[16:17]
	s_nop 0
	v_pk_mul_f32 v[10:11], v[10:11], s[94:95] op_sel_hi:[1,0]
	s_nop 0
	v_cvt_pk_bf16_f32 v13, v10, v11
	v_pk_mul_f32 v[10:11], v[58:59], v[56:57] op_sel_hi:[1,0]
	s_nop 0
	v_pk_mul_f32 v[10:11], v[10:11], v[134:135]
	s_nop 0
	v_mov_b32_e32 v12, v10
	v_mov_b32_e32 v15, v10
	v_mov_b32_e32 v16, v11
	v_mov_b32_e32 v17, v11
	v_permlane32_swap_b32_e32 v12, v15
	s_nop 0
	v_permlane32_swap_b32_e32 v16, v17
	v_cndmask_b32_e32 v17, v16, v17, vcc
	v_cndmask_b32_e32 v16, v12, v15, vcc
	v_pk_mul_f32 v[16:17], v[132:133], v[16:17]
	s_nop 0
	v_pk_fma_f32 v[10:11], v[10:11], v[92:93], v[16:17]
	v_and_b32_e32 v93, 0xffff0000, v14
	v_pk_mul_f32 v[10:11], v[10:11], s[94:95] op_sel_hi:[1,0]
	v_lshlrev_b32_e32 v92, 16, v14
	v_cvt_pk_bf16_f32 v12, v10, v11
	v_pk_mul_f32 v[10:11], v[64:65], v[56:57] op_sel_hi:[1,0]
	v_mul_f32_e32 v14, v93, v93
	v_pk_mul_f32 v[10:11], v[10:11], v[138:139]
	s_nop 0
	v_mov_b32_e32 v15, v10
	v_mov_b32_e32 v16, v10
	v_mov_b32_e32 v17, v11
	v_mov_b32_e32 v57, v11
	v_permlane32_swap_b32_e32 v15, v16
	s_nop 0
	v_permlane32_swap_b32_e32 v17, v57
	v_cndmask_b32_e32 v17, v17, v57, vcc
	v_cndmask_b32_e32 v16, v15, v16, vcc
	v_pk_mul_f32 v[16:17], v[136:137], v[16:17]
	s_nop 0
	v_pk_fma_f32 v[10:11], v[10:11], v[84:85], v[16:17]
	v_pk_mul_f32 v[16:17], v[62:63], v[56:57] op_sel_hi:[1,0]
	v_pk_mul_f32 v[10:11], v[10:11], s[94:95] op_sel_hi:[1,0]
	v_pk_mul_f32 v[16:17], v[16:17], v[140:141]
	v_cvt_pk_bf16_f32 v11, v10, v11
	v_mov_b32_e32 v10, v16
	v_mov_b32_e32 v15, v16
	v_mov_b32_e32 v57, v17
	v_mov_b32_e32 v81, v17
	v_permlane32_swap_b32_e32 v10, v15
	s_nop 0
	v_permlane32_swap_b32_e32 v57, v81
	v_cndmask_b32_e32 v85, v57, v81, vcc
	v_cndmask_b32_e32 v84, v10, v15, vcc
	v_pk_mul_f32 v[20:21], v[20:21], v[84:85]
	s_nop 0
	v_pk_fma_f32 v[16:17], v[16:17], v[88:89], v[20:21]
	v_mul_f32_e32 v88, v111, v111
	v_pk_mul_f32 v[16:17], v[16:17], s[94:95] op_sel_hi:[1,0]
	s_nop 0
	v_cvt_pk_bf16_f32 v10, v16, v17
	v_pk_mul_f32 v[16:17], v[74:75], v[56:57] op_sel_hi:[1,0]
	s_nop 0
	v_pk_mul_f32 v[16:17], v[16:17], v[142:143]
	s_nop 0
	v_mov_b32_e32 v15, v16
	v_mov_b32_e32 v20, v16
	v_mov_b32_e32 v21, v17
	v_mov_b32_e32 v57, v17
	v_permlane32_swap_b32_e32 v15, v20
	s_nop 0
	v_permlane32_swap_b32_e32 v21, v57
	v_cndmask_b32_e32 v21, v21, v57, vcc
	v_cndmask_b32_e32 v20, v15, v20, vcc
	v_pk_mul_f32 v[20:21], v[40:41], v[20:21]
	s_nop 0
	v_pk_fma_f32 v[16:17], v[16:17], v[42:43], v[20:21]
	v_pk_mul_f32 v[20:21], v[72:73], v[56:57] op_sel_hi:[1,0]
	v_pk_mul_f32 v[16:17], v[16:17], s[94:95] op_sel_hi:[1,0]
	v_pk_mul_f32 v[20:21], v[20:21], v[144:145]
	v_cvt_pk_bf16_f32 v17, v16, v17
	v_mov_b32_e32 v15, v20
	v_mov_b32_e32 v16, v20
	v_mov_b32_e32 v57, v21
	v_mov_b32_e32 v81, v21
	v_permlane32_swap_b32_e32 v15, v16
	s_nop 0
	v_permlane32_swap_b32_e32 v57, v81
	v_cndmask_b32_e32 v85, v57, v81, vcc
	v_cndmask_b32_e32 v84, v15, v16, vcc
	v_pk_mul_f32 v[84:85], v[44:45], v[84:85]
	s_nop 0
	v_pk_fma_f32 v[20:21], v[46:47], v[20:21], v[84:85]
	s_nop 0
	v_pk_mul_f32 v[20:21], v[20:21], s[94:95] op_sel_hi:[1,0]
	s_nop 0
	v_cvt_pk_bf16_f32 v16, v20, v21
	v_pk_mul_f32 v[20:21], v[78:79], v[56:57] op_sel_hi:[1,0]
	s_nop 0
	v_pk_mul_f32 v[20:21], v[20:21], v[148:149]
	s_nop 0
	v_mov_b32_e32 v15, v20
	v_mov_b32_e32 v57, v20
	v_mov_b32_e32 v81, v21
	v_mov_b32_e32 v84, v21
	v_permlane32_swap_b32_e32 v15, v57
	s_nop 0
	v_permlane32_swap_b32_e32 v81, v84
	v_cndmask_b32_e32 v85, v81, v84, vcc
	v_cndmask_b32_e32 v84, v15, v57, vcc
	v_pk_mul_f32 v[20:21], v[50:51], v[20:21]
	s_nop 0
	v_pk_fma_f32 v[20:21], v[48:49], v[84:85], v[20:21]
	s_nop 0
	v_pk_mul_f32 v[20:21], v[20:21], s[94:95] op_sel_hi:[1,0]
	s_nop 0
	v_cvt_pk_bf16_f32 v15, v20, v21
	v_pk_mul_f32 v[20:21], v[76:77], v[56:57] op_sel_hi:[1,0]
	v_pk_fma_f32 v[96:97], v[92:93], v[92:93], v[14:15] op_sel_hi:[1,1,0]
	v_pk_mul_f32 v[20:21], v[20:21], v[154:155]
	v_pk_fma_f32 v[96:97], v[52:53], v[52:53], v[96:97]
	v_mov_b32_e32 v56, v20
	v_mov_b32_e32 v81, v20
	s_nop 1
	v_permlane32_swap_b32_e32 v56, v81
	v_mov_b32_e32 v57, v21
	v_mov_b32_e32 v84, v21
	s_nop 1
	v_permlane32_swap_b32_e32 v57, v84
	v_cndmask_b32_e32 v56, v56, v81, vcc
	v_and_b32_e32 v81, 0xffff0000, v80
	v_cndmask_b32_e32 v57, v57, v84, vcc
	v_lshlrev_b32_e32 v80, 16, v80
	v_mul_f32_e32 v84, v81, v81
	v_pk_fma_f32 v[84:85], v[80:81], v[80:81], v[84:85] op_sel_hi:[1,1,0]
	v_mul_f32_e32 v14, v53, v53
	v_pk_fma_f32 v[84:85], v[110:111], v[110:111], v[84:85]
	v_pk_add_f32 v[96:97], v[14:15], v[96:97] op_sel_hi:[0,1]
	v_pk_add_f32 v[84:85], v[88:89], v[84:85] op_sel_hi:[0,1]
	v_pk_fma_f32 v[84:85], v[106:107], v[106:107], v[84:85]
	v_mul_f32_e32 v88, v107, v107
	v_pk_fma_f32 v[96:97], v[82:83], v[82:83], v[96:97]
	v_mul_f32_e32 v14, v83, v83
	v_pk_add_f32 v[84:85], v[88:89], v[84:85] op_sel_hi:[0,1]
	v_pk_add_f32 v[96:97], v[14:15], v[96:97] op_sel_hi:[0,1]
	v_pk_fma_f32 v[84:85], v[24:25], v[24:25], v[84:85]
	v_mul_f32_e32 v88, v25, v25
	v_pk_fma_f32 v[96:97], v[98:99], v[98:99], v[96:97]
	v_mul_f32_e32 v14, v99, v99
	v_pk_add_f32 v[84:85], v[88:89], v[84:85] op_sel_hi:[0,1]
	v_pk_add_f32 v[96:97], v[14:15], v[96:97] op_sel_hi:[0,1]
	v_pk_fma_f32 v[84:85], v[126:127], v[126:127], v[84:85]
	v_mul_f32_e32 v88, v127, v127
	v_pk_fma_f32 v[96:97], v[90:91], v[90:91], v[96:97]
	v_mul_f32_e32 v14, v91, v91
	v_pk_add_f32 v[84:85], v[88:89], v[84:85] op_sel_hi:[0,1]
; template <int DQK, int DV, bool LEAD> ...
;     ...
;           float sn = 0.f;
; #pragma unroll
;           for (int ds = 0; ds < 2; ++ds)
; #pragma unroll
;               for (int j = 0; j < 8; ++j) sn += x[ds][j] * x[ds][j];
;           sn = lanes4_sum(sn);
;           const float rn = rsqrtf(sn * (1.f / 64.f) + EPS);
; #pragma unroll
;           for (int ds = 0; ds < 2; ++ds)
; #pragma unroll
;               for (int j = 0; j < 8; ++j) x[ds][j] *= rn * qgain[32 * ds + 8 * g4 + j];
;           if constexpr (DQK == 64) {
; #pragma unroll
;               for (int ds = 0; ds < 2; ++ds)
; #pragma unroll
;                   for (int j = 0; j < 8; ++j) {
;                       auto rr = __builtin_amdgcn_permlane32_swap(__float_as_uint(x[ds][j]), __float_as_uint(x[ds][j]), false, false);
;                       const float other = hi ? __uint_as_float(rr[0]) : __uint_as_float(rr[1]);
;                       float cc = 1.f, sg = 0.f;
;                       if (lat) { const f32x2 cs = rope[(ds ? pcol : prow) * 16 + 8 * (g4 & 1) + j]; cc = cs.x; sg = hi ? cs.y : -cs.y; }
;                       x[ds][j] = x[ds][j] * cc + other * sg; }
;           } else {
;               float sr = 0.f;
; #pragma unroll
;               for (int j = 0; j < 8; ++j) sr += x[2][j] * x[2][j];
;               sr = lanes4_sum(sr);
;               const float rq = rsqrtf(sr * (1.f / 32.f) + EPS);
; #pragma unroll
;               for (int j = 0; j < 8; ++j) { const float av = x[2][j] * rq * qgain[64 + 8 * g4 + j];
;                   auto rr = __builtin_amdgcn_permlane16_swap(__float_as_uint(av), __float_as_uint(av), false, false);
;                   const float other = (g4 & 1) ? __uint_as_float(rr[0]) : __uint_as_float(rr[1]);
;                   float cc = 1.f, sg = 0.f;
;                   if (lat) { const f32x2 cs = rope[((g4 & 2) ? pcol : prow) * 8 + j]; cc = cs.x; sg = (g4 & 1) ? cs.y : -cs.y; }
;                   x[2][j] = av * cc + other * sg; }
;           }
; #pragma unroll
;           for (int ds = 0; ds < NDS; ++ds) { u32x4 w;
; #pragma unroll
;               for (int i = 0; i < 4; ++i) w[i] = cvtpk(x[ds][2 * i] * c2, x[ds][2 * i + 1] * c2);
;               qf[qb * NDS + ds] = __builtin_bit_cast(bf16x8, w); }
	v_pk_add_f32 v[96:97], v[14:15], v[96:97] op_sel_hi:[0,1]
	v_pk_fma_f32 v[84:85], v[122:123], v[122:123], v[84:85]
	v_mul_f32_e32 v88, v123, v123
	v_pk_fma_f32 v[96:97], v[86:87], v[86:87], v[96:97]
	v_mul_f32_e32 v14, v87, v87
	v_pk_add_f32 v[84:85], v[88:89], v[84:85] op_sel_hi:[0,1]
	v_pk_add_f32 v[96:97], v[14:15], v[96:97] op_sel_hi:[0,1]
	v_pk_fma_f32 v[84:85], v[102:103], v[102:103], v[84:85]
	v_mul_f32_e32 v88, v103, v103
	v_pk_fma_f32 v[96:97], v[68:69], v[68:69], v[96:97]
	v_mul_f32_e32 v14, v69, v69
	v_pk_add_f32 v[84:85], v[88:89], v[84:85] op_sel_hi:[0,1]
	v_pk_add_f32 v[96:97], v[14:15], v[96:97] op_sel_hi:[0,1]
	v_pk_fma_f32 v[84:85], v[118:119], v[118:119], v[84:85]
	v_mul_f32_e32 v88, v119, v119
	v_pk_fma_f32 v[96:97], v[114:115], v[114:115], v[96:97]
	v_mul_f32_e32 v14, v115, v115
	v_pk_add_f32 v[84:85], v[88:89], v[84:85] op_sel_hi:[0,1]
	v_pk_add_f32 v[96:97], v[14:15], v[96:97] op_sel_hi:[0,1]
	v_mov_b32_e32 v85, v84
	v_mov_b32_e32 v14, v96
	s_nop 0
	v_permlane16_swap_b32_e32 v84, v85
	v_permlane16_swap_b32_e32 v96, v14
	v_add_f32_e32 v85, v84, v85
	v_add_f32_e32 v84, v96, v14
	v_mov_b32_e32 v89, v85
	v_mov_b32_e32 v88, v84
	s_nop 0
	v_permlane32_swap_b32_e32 v85, v89
	v_permlane32_swap_b32_e32 v84, v88
	v_pk_add_f32 v[84:85], v[84:85], v[88:89]
	v_pk_mul_f32 v[20:21], v[54:55], v[20:21]
	v_pk_fma_f32 v[84:85], v[84:85], s[12:13], v[108:109] op_sel_hi:[1,0,0]
	v_pk_fma_f32 v[20:21], v[104:105], v[56:57], v[20:21]
	v_mul_f32_e32 v14, 0x4b800000, v85
	v_cmp_gt_f32_e64 s[4:5], s95, v85
	v_pk_mul_f32 v[20:21], v[20:21], s[94:95] op_sel_hi:[1,0]
	s_nop 0
	v_cndmask_b32_e64 v14, v85, v14, s[4:5]
	v_rsq_f32_e32 v85, v14
	v_cvt_pk_bf16_f32 v14, v20, v21
	v_mul_f32_e32 v20, 0x45800000, v85
	v_cndmask_b32_e64 v56, v85, v20, s[4:5]
	v_pk_mul_f32 v[20:21], v[60:61], v[56:57] op_sel_hi:[1,0]
	v_cmp_gt_f32_e64 s[4:5], s95, v84
	v_pk_mul_f32 v[20:21], v[20:21], v[118:119]
	s_nop 0
	v_mov_b32_e32 v57, v20
	v_mov_b32_e32 v85, v20
	v_mov_b32_e32 v88, v21
	v_mov_b32_e32 v89, v21
	v_permlane32_swap_b32_e32 v57, v85
	s_nop 0
	v_permlane32_swap_b32_e32 v88, v89
	v_cndmask_b32_e32 v89, v88, v89, vcc
	v_cndmask_b32_e32 v88, v57, v85, vcc
	v_pk_mul_f32 v[88:89], v[116:117], v[88:89]
	s_nop 0
	v_pk_fma_f32 v[20:21], v[20:21], v[70:71], v[88:89]
	v_pk_mul_f32 v[70:71], v[58:59], v[56:57] op_sel_hi:[1,0]
	v_pk_mul_f32 v[20:21], v[20:21], s[94:95] op_sel_hi:[1,0]
	v_pk_mul_f32 v[70:71], v[70:71], v[102:103]
	v_cvt_pk_bf16_f32 v21, v20, v21
	v_mov_b32_e32 v20, v70
	v_mov_b32_e32 v57, v70
	v_mov_b32_e32 v85, v71
	v_mov_b32_e32 v88, v71
	v_permlane32_swap_b32_e32 v20, v57
	s_nop 0
	v_permlane32_swap_b32_e32 v85, v88
	v_cndmask_b32_e32 v89, v85, v88, vcc
	v_cndmask_b32_e32 v88, v20, v57, vcc
	v_pk_mul_f32 v[88:89], v[94:95], v[88:89]
	s_nop 0
	v_pk_fma_f32 v[66:67], v[70:71], v[66:67], v[88:89]
	s_nop 0
	v_pk_mul_f32 v[66:67], v[66:67], s[94:95] op_sel_hi:[1,0]
	s_nop 0
	v_cvt_pk_bf16_f32 v20, v66, v67
	v_pk_mul_f32 v[66:67], v[64:65], v[56:57] op_sel_hi:[1,0]
	s_nop 0
	v_pk_mul_f32 v[66:67], v[66:67], v[122:123]
	s_nop 0
	v_mov_b32_e32 v57, v66
	v_mov_b32_e32 v70, v66
	v_mov_b32_e32 v71, v67
	v_mov_b32_e32 v85, v67
	v_permlane32_swap_b32_e32 v57, v70
	s_nop 0
	v_permlane32_swap_b32_e32 v71, v85
	v_cndmask_b32_e32 v71, v71, v85, vcc
	v_cndmask_b32_e32 v70, v57, v70, vcc
	v_pk_mul_f32 v[70:71], v[120:121], v[70:71]
	s_nop 0
	v_pk_fma_f32 v[18:19], v[66:67], v[18:19], v[70:71]
	v_pk_mul_f32 v[66:67], v[62:63], v[56:57] op_sel_hi:[1,0]
	v_pk_mul_f32 v[18:19], v[18:19], s[94:95] op_sel_hi:[1,0]
	v_pk_mul_f32 v[66:67], v[66:67], v[126:127]
	v_cvt_pk_bf16_f32 v19, v18, v19
	v_mov_b32_e32 v18, v66
	v_mov_b32_e32 v57, v66
	v_mov_b32_e32 v70, v67
	v_mov_b32_e32 v71, v67
	v_permlane32_swap_b32_e32 v18, v57
	s_nop 0
	v_permlane32_swap_b32_e32 v70, v71
	v_cndmask_b32_e32 v71, v70, v71, vcc
	v_cndmask_b32_e32 v70, v18, v57, vcc
	v_pk_mul_f32 v[70:71], v[124:125], v[70:71]
	s_nop 0
	v_pk_fma_f32 v[22:23], v[66:67], v[22:23], v[70:71]
	s_nop 0
	v_pk_mul_f32 v[22:23], v[22:23], s[94:95] op_sel_hi:[1,0]
	s_nop 0
	v_cvt_pk_bf16_f32 v18, v22, v23
	v_pk_mul_f32 v[22:23], v[74:75], v[56:57] op_sel_hi:[1,0]
	s_nop 0
	v_pk_mul_f32 v[22:23], v[22:23], v[24:25]
	s_nop 0
	v_mov_b32_e32 v24, v22
	v_mov_b32_e32 v57, v22
	v_mov_b32_e32 v25, v23
	v_mov_b32_e32 v66, v23
	v_permlane32_swap_b32_e32 v24, v57
	s_nop 0
	v_permlane32_swap_b32_e32 v25, v66
	v_cndmask_b32_e32 v25, v25, v66, vcc
	v_cndmask_b32_e32 v24, v24, v57, vcc
	v_pk_mul_f32 v[24:25], v[40:41], v[24:25]
	s_nop 0
	v_pk_fma_f32 v[22:23], v[22:23], v[42:43], v[24:25]
	s_nop 0
	v_pk_mul_f32 v[22:23], v[22:23], s[94:95] op_sel_hi:[1,0]
	s_nop 0
	v_cvt_pk_bf16_f32 v25, v22, v23
	v_pk_mul_f32 v[22:23], v[72:73], v[56:57] op_sel_hi:[1,0]
	s_nop 0
	v_pk_mul_f32 v[22:23], v[22:23], v[106:107]
	s_nop 0
	v_mov_b32_e32 v24, v22
	v_mov_b32_e32 v57, v22
	v_mov_b32_e32 v66, v23
	v_mov_b32_e32 v67, v23
	v_permlane32_swap_b32_e32 v24, v57
	s_nop 0
	v_permlane32_swap_b32_e32 v66, v67
	v_cndmask_b32_e32 v67, v66, v67, vcc
	v_cndmask_b32_e32 v66, v24, v57, vcc
	v_pk_mul_f32 v[66:67], v[44:45], v[66:67]
	s_nop 0
	v_pk_fma_f32 v[22:23], v[46:47], v[22:23], v[66:67]
	s_nop 0
	v_pk_mul_f32 v[22:23], v[22:23], s[94:95] op_sel_hi:[1,0]
	s_nop 0
	v_cvt_pk_bf16_f32 v24, v22, v23
	v_pk_mul_f32 v[22:23], v[78:79], v[56:57] op_sel_hi:[1,0]
	s_nop 0
	v_pk_mul_f32 v[22:23], v[22:23], v[110:111]
	s_nop 0
	v_mov_b32_e32 v57, v22
	v_mov_b32_e32 v66, v22
	v_mov_b32_e32 v67, v23
	v_mov_b32_e32 v70, v23
	v_permlane32_swap_b32_e32 v57, v66
	s_nop 0
	v_permlane32_swap_b32_e32 v67, v70
	v_cndmask_b32_e32 v67, v67, v70, vcc
	v_cndmask_b32_e32 v66, v57, v66, vcc
; __device__ __forceinline__ unsigned cvtpk(float lo, float hi) { f32x2 v = {lo, hi}; bf16x2_t b = __builtin_convertvector(v, bf16x2_t); return __builtin_bit_cast(unsigned, b); }
; template <int DQK, int DV, bool LEAD> ...
;     ...
;           if constexpr (DQK == 64) {
; #pragma unroll
;               for (int ds = 0; ds < 2; ++ds)
; #pragma unroll
;                   for (int j = 0; j < 8; ++j) {
;                       auto rr = __builtin_amdgcn_permlane32_swap(__float_as_uint(x[ds][j]), __float_as_uint(x[ds][j]), false, false);
;                       const float other = hi ? __uint_as_float(rr[0]) : __uint_as_float(rr[1]);
;                       float cc = 1.f, sg = 0.f;
;                       if (lat) { const f32x2 cs = rope[(ds ? pcol : prow) * 16 + 8 * (g4 & 1) + j]; cc = cs.x; sg = hi ? cs.y : -cs.y; }
;                       x[ds][j] = x[ds][j] * cc + other * sg; }
;           } else {
;               float sr = 0.f;
; #pragma unroll
;               for (int j = 0; j < 8; ++j) sr += x[2][j] * x[2][j];
;               sr = lanes4_sum(sr);
;               const float rq = rsqrtf(sr * (1.f / 32.f) + EPS);
; #pragma unroll
;               for (int j = 0; j < 8; ++j) { const float av = x[2][j] * rq * qgain[64 + 8 * g4 + j];
;                   auto rr = __builtin_amdgcn_permlane16_swap(__float_as_uint(av), __float_as_uint(av), false, false);
;                   const float other = (g4 & 1) ? __uint_as_float(rr[0]) : __uint_as_float(rr[1]);
;                   float cc = 1.f, sg = 0.f;
;                   if (lat) { const f32x2 cs = rope[((g4 & 2) ? pcol : prow) * 8 + j]; cc = cs.x; sg = (g4 & 1) ? cs.y : -cs.y; }
;                   x[2][j] = av * cc + other * sg; }
;           }
; #pragma unroll
;           for (int ds = 0; ds < NDS; ++ds) { u32x4 w;
; #pragma unroll
;               for (int i = 0; i < 4; ++i) w[i] = cvtpk(x[ds][2 * i] * c2, x[ds][2 * i + 1] * c2);
;               qf[qb * NDS + ds] = __builtin_bit_cast(bf16x8, w); }
;       }
; #pragma unroll
;       for (int d0 = 0; d0 < NQB * NDS; ++d0) asm volatile("" : "+v"(qf[d0])); }
;     wait_bar<0>();
;     bf16x8 kf[NKW * NDS], vf[NVF];
;     ATT_KLOAD(0);
;     asm volatile("s_waitcnt lgkmcnt(0)\n\ts_barrier" ::: "memory");
	v_pk_mul_f32 v[22:23], v[50:51], v[22:23]
	v_pk_mul_f32 v[56:57], v[76:77], v[56:57] op_sel_hi:[1,0]
	v_pk_fma_f32 v[22:23], v[48:49], v[66:67], v[22:23]
	v_pk_mul_f32 v[56:57], v[56:57], v[80:81]
	v_pk_mul_f32 v[22:23], v[22:23], s[94:95] op_sel_hi:[1,0]
	v_mov_b32_e32 v66, v56
	v_cvt_pk_bf16_f32 v23, v22, v23
	v_mov_b32_e32 v22, v56
	s_nop 1
	v_permlane32_swap_b32_e32 v22, v66
	v_mov_b32_e32 v67, v57
	v_mov_b32_e32 v70, v57
	v_cndmask_b32_e32 v66, v22, v66, vcc
	v_mul_f32_e32 v22, 0x4b800000, v84
	v_permlane32_swap_b32_e32 v67, v70
	v_cndmask_b32_e64 v22, v84, v22, s[4:5]
	v_cndmask_b32_e32 v67, v67, v70, vcc
	v_rsq_f32_e32 v70, v22
	v_pk_mul_f32 v[56:57], v[54:55], v[56:57]
	s_nop 0
	v_pk_fma_f32 v[56:57], v[104:105], v[66:67], v[56:57]
	s_nop 0
	v_pk_mul_f32 v[56:57], v[56:57], s[94:95] op_sel_hi:[1,0]
	s_nop 0
	v_cvt_pk_bf16_f32 v22, v56, v57
	v_mul_f32_e32 v56, 0x45800000, v70
	v_cndmask_b32_e64 v56, v70, v56, s[4:5]
	v_pk_mul_f32 v[66:67], v[76:77], v[56:57] op_sel_hi:[1,0]
	v_pk_mul_f32 v[70:71], v[78:79], v[56:57] op_sel_hi:[1,0]
	v_pk_mul_f32 v[66:67], v[66:67], v[92:93]
	v_pk_mul_f32 v[58:59], v[58:59], v[56:57] op_sel_hi:[1,0]
	v_pk_mul_f32 v[52:53], v[70:71], v[52:53]
	v_pk_mul_f32 v[70:71], v[72:73], v[56:57] op_sel_hi:[1,0]
	v_pk_mul_f32 v[72:73], v[74:75], v[56:57] op_sel_hi:[1,0]
	v_pk_mul_f32 v[62:63], v[62:63], v[56:57] op_sel_hi:[1,0]
	v_pk_mul_f32 v[64:65], v[64:65], v[56:57] op_sel_hi:[1,0]
	v_pk_mul_f32 v[58:59], v[58:59], v[68:69]
	v_pk_mul_f32 v[56:57], v[60:61], v[56:57] op_sel_hi:[1,0]
	v_mov_b32_e32 v60, v66
	v_mov_b32_e32 v68, v66
	v_mov_b32_e32 v61, v67
	v_mov_b32_e32 v69, v67
	v_permlane32_swap_b32_e32 v60, v68
	s_nop 0
	v_permlane32_swap_b32_e32 v61, v69
	v_cndmask_b32_e32 v61, v61, v69, vcc
	v_cndmask_b32_e32 v60, v60, v68, vcc
	v_pk_mul_f32 v[54:55], v[54:55], v[66:67]
	v_mov_b32_e32 v66, v52
	v_pk_fma_f32 v[54:55], v[104:105], v[60:61], v[54:55]
	v_mov_b32_e32 v60, v52
	v_mov_b32_e32 v61, v53
	v_mov_b32_e32 v67, v53
	v_permlane32_swap_b32_e32 v60, v66
	s_nop 0
	v_permlane32_swap_b32_e32 v61, v67
	v_pk_mul_f32 v[70:71], v[70:71], v[82:83]
	v_cndmask_b32_e32 v61, v61, v67, vcc
	v_cndmask_b32_e32 v60, v60, v66, vcc
	v_pk_mul_f32 v[50:51], v[50:51], v[52:53]
	v_mov_b32_e32 v52, v70
	v_pk_fma_f32 v[48:49], v[48:49], v[60:61], v[50:51]
	v_mov_b32_e32 v50, v70
	v_mov_b32_e32 v51, v71
	v_mov_b32_e32 v53, v71
	v_permlane32_swap_b32_e32 v50, v52
	s_nop 0
	v_permlane32_swap_b32_e32 v51, v53
	v_cndmask_b32_e32 v51, v51, v53, vcc
	v_cndmask_b32_e32 v50, v50, v52, vcc
	v_pk_mul_f32 v[72:73], v[72:73], v[98:99]
	v_pk_mul_f32 v[44:45], v[44:45], v[50:51]
	v_mov_b32_e32 v50, v72
	v_pk_fma_f32 v[44:45], v[46:47], v[70:71], v[44:45]
	v_mov_b32_e32 v46, v72
	v_mov_b32_e32 v47, v73
	v_mov_b32_e32 v51, v73
	v_permlane32_swap_b32_e32 v46, v50
	s_nop 0
	v_permlane32_swap_b32_e32 v47, v51
	v_cndmask_b32_e32 v47, v47, v51, vcc
	v_cndmask_b32_e32 v46, v46, v50, vcc
	v_pk_mul_f32 v[62:63], v[62:63], v[90:91]
	v_pk_mul_f32 v[40:41], v[40:41], v[46:47]
	v_mov_b32_e32 v46, v62
	v_pk_fma_f32 v[40:41], v[72:73], v[42:43], v[40:41]
	v_mov_b32_e32 v42, v62
	v_mov_b32_e32 v43, v63
	v_mov_b32_e32 v47, v63
	v_permlane32_swap_b32_e32 v42, v46
	s_nop 0
	v_permlane32_swap_b32_e32 v43, v47
	v_cndmask_b32_e32 v43, v43, v47, vcc
	v_cndmask_b32_e32 v42, v42, v46, vcc
	v_pk_mul_f32 v[64:65], v[64:65], v[86:87]
	v_pk_mul_f32 v[36:37], v[36:37], v[42:43]
	v_mov_b32_e32 v42, v64
	v_pk_fma_f32 v[36:37], v[62:63], v[38:39], v[36:37]
	v_mov_b32_e32 v38, v64
	v_mov_b32_e32 v39, v65
	v_mov_b32_e32 v43, v65
	v_permlane32_swap_b32_e32 v38, v42
	s_nop 0
	v_permlane32_swap_b32_e32 v39, v43
	v_cndmask_b32_e32 v39, v39, v43, vcc
	v_cndmask_b32_e32 v38, v38, v42, vcc
	v_pk_mul_f32 v[32:33], v[32:33], v[38:39]
	v_mov_b32_e32 v38, v58
	v_pk_fma_f32 v[32:33], v[64:65], v[34:35], v[32:33]
	v_mov_b32_e32 v34, v58
	v_mov_b32_e32 v35, v59
	v_mov_b32_e32 v39, v59
	v_permlane32_swap_b32_e32 v34, v38
	s_nop 0
	v_permlane32_swap_b32_e32 v35, v39
	v_cndmask_b32_e32 v35, v35, v39, vcc
	v_cndmask_b32_e32 v34, v34, v38, vcc
	v_pk_mul_f32 v[56:57], v[56:57], v[114:115]
	v_pk_mul_f32 v[28:29], v[28:29], v[34:35]
	v_pk_mul_f32 v[32:33], v[32:33], s[94:95] op_sel_hi:[1,0]
	v_pk_fma_f32 v[34:35], v[58:59], v[30:31], v[28:29]
	v_mov_b32_e32 v28, v56
	v_mov_b32_e32 v30, v56
	v_mov_b32_e32 v29, v57
	v_mov_b32_e32 v31, v57
	v_permlane32_swap_b32_e32 v28, v30
	s_nop 0
	v_permlane32_swap_b32_e32 v29, v31
	v_cndmask_b32_e32 v29, v29, v31, vcc
	v_cndmask_b32_e32 v28, v28, v30, vcc
	v_pk_mul_f32 v[28:29], v[112:113], v[28:29]
	v_pk_mul_f32 v[30:31], v[40:41], s[94:95] op_sel_hi:[1,0]
	v_pk_fma_f32 v[38:39], v[56:57], v[26:27], v[28:29]
	v_pk_mul_f32 v[26:27], v[54:55], s[94:95] op_sel_hi:[1,0]
	v_pk_mul_f32 v[28:29], v[48:49], s[94:95] op_sel_hi:[1,0]
	v_cvt_pk_bf16_f32 v26, v26, v27
	v_cvt_pk_bf16_f32 v27, v28, v29
	v_pk_mul_f32 v[28:29], v[44:45], s[94:95] op_sel_hi:[1,0]
	v_bfe_u32 v54, v168, 1, 3
	v_cvt_pk_bf16_f32 v28, v28, v29
	v_cvt_pk_bf16_f32 v29, v30, v31
	v_pk_mul_f32 v[30:31], v[36:37], s[94:95] op_sel_hi:[1,0]
	v_bitop3_b32 v54, v171, v54, 4 bitop3:0x36
	v_cvt_pk_bf16_f32 v30, v30, v31
	v_cvt_pk_bf16_f32 v31, v32, v33
	v_pk_mul_f32 v[32:33], v[34:35], s[94:95] op_sel_hi:[1,0]
	v_pk_mul_f32 v[34:35], v[38:39], s[94:95] op_sel_hi:[1,0]
	v_cvt_pk_bf16_f32 v32, v32, v33
	v_cvt_pk_bf16_f32 v33, v34, v35
	s_waitcnt vmcnt(0) lgkmcnt(0)
	s_barrier
	ds_read_b128 v[34:37], v175
	ds_read_b128 v[38:41], v175 offset:512
	v_lshlrev_b32_e32 v82, 4, v54
	v_add_u32_e32 v178, v169, v82
	s_waitcnt lgkmcnt(1)
	v_mfma_f32_16x16x32_bf16 v[42:45], v[34:37], v[6:9], 0
	ds_read_b128 v[54:57], v178
	ds_read_b128 v[58:61], v178 offset:512
	s_waitcnt lgkmcnt(0)
	s_barrier
; #define ATT_SB() __builtin_amdgcn_sched_barrier(0)
; #define ATT_DMA_K(t, sl) do { glds16(ksrc + (size_t)(t) * 64 * kpitch, (unsigned)__builtin_amdgcn_readfirstlane(kdst + (sl) * KSLOT)); \
;         if constexpr (DQK == 96) glds16(krsrc + (size_t)(t) * 64 * 32, (unsigned)__builtin_amdgcn_readfirstlane(krdst + (sl) * KSLOT)); } while (0)
; #define ATT_DMA_V(t, sl) do { glds16(vsrc + (size_t)(t) * 64, (unsigned)__builtin_amdgcn_readfirstlane(vdst + (sl) * VSLOT)); \
;         if constexpr (DV == 128) glds16(vsrc + (size_t)64 * NR + (size_t)(t) * 64, (unsigned)__builtin_amdgcn_readfirstlane(vdst + (sl) * VSLOT + 8192)); } while (0)
; #define ATT_KLOAD(sl) do { _Pragma("unroll") for (int kb_ = 0; kb_ < NKW; ++kb_) _Pragma("unroll") for (int ds_ = 0; ds_ < NDS; ++ds_) { \
;         if (ds_ < 2) kf[kb_ * NDS + ds_] = *(const LAS bf16x8*)(kp[ds_ & 1] + (sl) * KSLOT + (kb_ & 1) * 512 + (kb_ >> 1) * 4096); \
;         else kf[kb_ * NDS + ds_] = *(const LAS bf16x8*)(krp + (sl) * KSLOT + (kb_ & 1) * 256 + (kb_ >> 1) * 2048); } } while (0)
; #define ATT_QK() do { _Pragma("unroll") for (int kb_ = 0; kb_ < NKW; ++kb_) _Pragma("unroll") for (int ds_ = 0; ds_ < NDS; ++ds_) _Pragma("unroll") for (int qb_ = 0; qb_ < NQB; ++qb_) \
;         c[kb_][qb_] = __builtin_amdgcn_mfma_f32_16x16x32_bf16(kf[kb_ * NDS + ds_], qf[qb_ * NDS + ds_], ds_ == 0 ? zero4 : c[kb_][qb_], 0, 0, 0); } while (0)
; #define ATT_EXP() do { _Pragma("unroll") for (int kb_ = 0; kb_ < NKW; ++kb_) _Pragma("unroll") for (int qb_ = 0; qb_ < NQB; ++qb_) _Pragma("unroll") for (int i_ = 0; i_ < 4; ++i_) \
;         c[kb_][qb_][i_] = __builtin_amdgcn_exp2f(c[kb_][qb_][i_]); } while (0)
; template <int DQK, int DV, bool LEAD> ...
;     ...
; #pragma unroll
;     for (int qb = 0; qb < NQB; ++qb) lsum[qb] = 0.f;
;     const f32x4 zero4 = {0.f, 0.f, 0.f, 0.f};
;     f32x4 o[NDB][NQB], c[NKW][NQB]; u32x4 pw[4];
; #pragma unroll
;     for (int i = 0; i < NDB; ++i)
; #pragma unroll
;         for (int qb = 0; qb < NQB; ++qb) o[i][qb] = zero4;
;     ATT_DMA_K(3, 0); ATT_DMA_V(1, 1);
;     ATT_QK(); ATT_SB();
;     ATT_KLOAD(1); ATT_SB();
;     if constexpr (LEAD) { ATT_EXP(); ATT_SUMPACK(); }
;     wait_bar<NDMA>();
;     int s_prev = 0, s_cur = 1, s_next = 2;
	s_cselect_b64 vcc, -1, 0
	v_mfma_f32_16x16x32_bf16 v[46:49], v[34:37], v[14:17], 0
	v_mfma_f32_16x16x32_bf16 v[50:53], v[34:37], v[22:25], 0
	v_mfma_f32_16x16x32_bf16 v[34:37], v[34:37], v[26:29], 0
	s_waitcnt lgkmcnt(1)
	v_mfma_f32_16x16x32_bf16 v[62:65], v[54:57], v[2:5], v[42:45]
	v_mfma_f32_16x16x32_bf16 v[66:69], v[54:57], v[10:13], v[46:49]
	v_mfma_f32_16x16x32_bf16 v[50:53], v[54:57], v[18:21], v[50:53]
	v_mfma_f32_16x16x32_bf16 v[54:57], v[54:57], v[30:33], v[34:37]
	v_mfma_f32_16x16x32_bf16 v[34:37], v[38:41], v[6:9], 0
	v_mfma_f32_16x16x32_bf16 v[42:45], v[38:41], v[14:17], 0
	v_mfma_f32_16x16x32_bf16 v[46:49], v[38:41], v[22:25], 0
	v_mfma_f32_16x16x32_bf16 v[38:41], v[38:41], v[26:29], 0
	s_waitcnt lgkmcnt(0)
	v_mfma_f32_16x16x32_bf16 v[70:73], v[58:61], v[2:5], v[34:37]
	v_mfma_f32_16x16x32_bf16 v[74:77], v[58:61], v[10:13], v[42:45]
	s_nop 1
	v_lshl_add_u64 v[34:35], v[162:163], 0, s[96:97]
	s_mov_b32 m0, s49
	s_nop 0
	global_load_lds_dwordx4 v[34:35], off
	v_lshl_add_u64 v[34:35], v[164:165], 0, s[66:67]
	v_mfma_f32_16x16x32_bf16 v[78:81], v[58:61], v[18:21], v[46:49]
	s_add_i32 s4, s36, 0x2000
	s_mov_b32 m0, s4
	s_nop 0
	global_load_lds_dwordx4 v[34:35], off
	v_mfma_f32_16x16x32_bf16 v[58:61], v[58:61], v[30:33], v[38:41]
	ds_read_b128 v[34:37], v175 offset:8192
	s_nop 1
	ds_read_b128 v[38:41], v175 offset:8704
	ds_read_b128 v[42:45], v178 offset:8192
	ds_read_b128 v[46:49], v178 offset:8704
	v_exp_f32_e32 v62, v62
	v_exp_f32_e32 v63, v63
	v_exp_f32_e32 v64, v64
	v_exp_f32_e32 v65, v65
	v_exp_f32_e32 v66, v66
	v_exp_f32_e32 v67, v67
	v_exp_f32_e32 v68, v68
	v_exp_f32_e32 v69, v69
	v_exp_f32_e32 v83, v50
	v_exp_f32_e32 v84, v51
	v_exp_f32_e32 v85, v52
	v_exp_f32_e32 v86, v53
	v_exp_f32_e32 v54, v54
	v_exp_f32_e32 v55, v55
	v_exp_f32_e32 v56, v56
	v_exp_f32_e32 v57, v57
	v_add_f32_e32 v50, v62, v63
	v_add_f32_e32 v51, v64, v65
	v_exp_f32_e32 v70, v70
	v_exp_f32_e32 v74, v74
	v_exp_f32_e32 v78, v78
	v_exp_f32_e32 v58, v58
	v_add_f32_e32 v50, v50, v51
	v_add_f32_e32 v51, v66, v67
	v_add_f32_e32 v52, v68, v69
	v_add_f32_e32 v51, v51, v52
	v_add_f32_e32 v52, v83, v84
	v_add_f32_e32 v53, v85, v86
	v_exp_f32_e32 v71, v71
	v_exp_f32_e32 v75, v75
	v_exp_f32_e32 v79, v79
	v_exp_f32_e32 v59, v59
	v_add_f32_e32 v52, v52, v53
	v_add_f32_e32 v53, v54, v55
	v_add_f32_e32 v87, v56, v57
	v_add_f32_e32 v53, v53, v87
	v_exp_f32_e32 v72, v72
	v_exp_f32_e32 v76, v76
	v_exp_f32_e32 v80, v80
	v_exp_f32_e32 v60, v60
	v_add_f32_e32 v50, v50, v70
	v_add_f32_e32 v51, v51, v74
	v_add_f32_e32 v52, v52, v78
	v_add_f32_e32 v53, v53, v58
	v_exp_f32_e32 v73, v73
	v_exp_f32_e32 v77, v77
	v_exp_f32_e32 v81, v81
	v_exp_f32_e32 v61, v61
	v_add_f32_e32 v50, v71, v50
	v_add_f32_e32 v51, v75, v51
	v_add_f32_e32 v52, v79, v52
	v_add_f32_e32 v53, v59, v53
	s_mov_b32 s4, 1
	v_add_f32_e32 v50, v72, v50
	v_add_f32_e32 v87, v76, v51
	v_add_f32_e32 v52, v80, v52
	v_add_f32_e32 v88, v60, v53
	v_cvt_pk_bf16_f32 v102, v62, v63
	v_add_f32_e32 v51, v73, v50
	v_add_f32_e32 v50, v77, v87
	v_add_f32_e32 v53, v81, v52
	v_add_f32_e32 v52, v61, v88
	s_waitcnt vmcnt(2) lgkmcnt(0)
	s_barrier
	s_cmp_lg_u32 s4, 0
	v_pk_add_f32 v[168:169], v[50:51], 0 op_sel_hi:[1,0]
	v_cndmask_b32_e32 v50, v82, v177, vcc
	v_add3_u32 v177, 0, v173, v50
	v_mov_b32_e32 v50, 0
	v_pk_add_f32 v[166:167], v[52:53], 0 op_sel_hi:[1,0]
	v_cvt_pk_bf16_f32 v103, v64, v65
	v_cvt_pk_bf16_f32 v104, v70, v71
	v_cvt_pk_bf16_f32 v105, v72, v73
	v_cvt_pk_bf16_f32 v114, v66, v67
	v_cvt_pk_bf16_f32 v115, v68, v69
	v_cvt_pk_bf16_f32 v116, v74, v75
	v_cvt_pk_bf16_f32 v117, v76, v77
	v_cvt_pk_bf16_f32 v122, v83, v84
	v_cvt_pk_bf16_f32 v123, v85, v86
	v_cvt_pk_bf16_f32 v124, v78, v79
	v_cvt_pk_bf16_f32 v125, v80, v81
	v_cvt_pk_bf16_f32 v126, v54, v55
	v_cvt_pk_bf16_f32 v127, v56, v57
	v_cvt_pk_bf16_f32 v128, v58, v59
	v_cvt_pk_bf16_f32 v129, v60, v61
	s_cselect_b64 s[4:5], -1, 0
	s_mov_b32 s37, 2
	v_mov_b32_e32 v51, v50
	v_mov_b32_e32 v52, v50
	v_mov_b32_e32 v53, v50
	v_mov_b32_e32 v54, v50
	v_mov_b32_e32 v55, v50
	v_mov_b32_e32 v56, v50
	v_mov_b32_e32 v57, v50
	v_mov_b32_e32 v58, v50
	v_mov_b32_e32 v59, v50
	v_mov_b32_e32 v60, v50
	v_mov_b32_e32 v61, v50
	v_mov_b32_e32 v62, v50
	v_mov_b32_e32 v63, v50
	v_mov_b32_e32 v64, v50
	v_mov_b32_e32 v65, v50
	v_mov_b32_e32 v66, v50
	v_mov_b32_e32 v67, v50
	v_mov_b32_e32 v68, v50
	v_mov_b32_e32 v69, v50
	v_mov_b32_e32 v70, v50
	v_mov_b32_e32 v71, v50
	v_mov_b32_e32 v72, v50
	v_mov_b32_e32 v73, v50
	v_mov_b32_e32 v74, v50
	v_mov_b32_e32 v75, v50
	v_mov_b32_e32 v76, v50
	v_mov_b32_e32 v77, v50
	v_mov_b32_e32 v78, v50
	v_mov_b32_e32 v79, v50
	v_mov_b32_e32 v80, v50
	v_mov_b32_e32 v81, v50
	v_mov_b32_e32 v82, v50
	v_mov_b32_e32 v83, v50
	v_mov_b32_e32 v84, v50
	v_mov_b32_e32 v85, v50
	v_mov_b32_e32 v86, v50
	v_mov_b32_e32 v87, v50
	v_mov_b32_e32 v88, v50
	v_mov_b32_e32 v89, v50
	v_mov_b32_e32 v90, v50
	v_mov_b32_e32 v91, v50
	v_mov_b32_e32 v92, v50
	v_mov_b32_e32 v93, v50
	v_mov_b32_e32 v94, v50
	v_mov_b32_e32 v95, v50
	v_mov_b32_e32 v96, v50
	v_mov_b32_e32 v97, v50
	v_mov_b32_e32 v98, v50
	v_mov_b32_e32 v99, v50
	v_mov_b32_e32 v100, v50
	v_mov_b32_e32 v101, v50
	v_mov_b32_e32 v106, v50
	v_mov_b32_e32 v107, v50
	v_mov_b32_e32 v108, v50
	v_mov_b32_e32 v109, v50
	v_mov_b32_e32 v110, v50
	v_mov_b32_e32 v111, v50
	v_mov_b32_e32 v112, v50
	v_mov_b32_e32 v113, v50
	v_mov_b32_e32 v118, v50
	v_mov_b32_e32 v119, v50
	v_mov_b32_e32 v120, v50
	v_mov_b32_e32 v121, v50
	s_branch .LBB0_965

; #define ATT_SB() __builtin_amdgcn_sched_barrier(0)
; #define ATT_DMA_K(t, sl) do { glds16(ksrc + (size_t)(t) * 64 * kpitch, (unsigned)__builtin_amdgcn_readfirstlane(kdst + (sl) * KSLOT)); \
;         if constexpr (DQK == 96) glds16(krsrc + (size_t)(t) * 64 * 32, (unsigned)__builtin_amdgcn_readfirstlane(krdst + (sl) * KSLOT)); } while (0)
; #define ATT_DMA_V(t, sl) do { glds16(vsrc + (size_t)(t) * 64, (unsigned)__builtin_amdgcn_readfirstlane(vdst + (sl) * VSLOT)); \
;         if constexpr (DV == 128) glds16(vsrc + (size_t)64 * NR + (size_t)(t) * 64, (unsigned)__builtin_amdgcn_readfirstlane(vdst + (sl) * VSLOT + 8192)); } while (0)
; #define ATT_KLOAD(sl) do { _Pragma("unroll") for (int kb_ = 0; kb_ < NKW; ++kb_) _Pragma("unroll") for (int ds_ = 0; ds_ < NDS; ++ds_) { \
;         if (ds_ < 2) kf[kb_ * NDS + ds_] = *(const LAS bf16x8*)(kp[ds_ & 1] + (sl) * KSLOT + (kb_ & 1) * 512 + (kb_ >> 1) * 4096); \
;         else kf[kb_ * NDS + ds_] = *(const LAS bf16x8*)(krp + (sl) * KSLOT + (kb_ & 1) * 256 + (kb_ >> 1) * 2048); } } while (0)
; #define ATT_QK() do { _Pragma("unroll") for (int kb_ = 0; kb_ < NKW; ++kb_) _Pragma("unroll") for (int ds_ = 0; ds_ < NDS; ++ds_) _Pragma("unroll") for (int qb_ = 0; qb_ < NQB; ++qb_) \
;         c[kb_][qb_] = __builtin_amdgcn_mfma_f32_16x16x32_bf16(kf[kb_ * NDS + ds_], qf[qb_ * NDS + ds_], ds_ == 0 ? zero4 : c[kb_][qb_], 0, 0, 0); } while (0)
; template <int DQK, int DV, bool LEAD> ...
;     ...
;     for (int t = 1; t < NT; ++t) {
;         __builtin_amdgcn_s_waitcnt(0xC07F);
;         if constexpr (!LEAD) { ATT_EXP(); ATT_SUMPACK(); ATT_SB(); }
;         ATT_VLOAD(s_prev, 0); ATT_SB();
;         { const int tk = (t + 3 < NT) ? t + 3 : NT - 1; ATT_DMA_K(tk, s_cur); }
;         { const int tv = (t + 1 < NT) ? t + 1 : NT - 1; ATT_DMA_V(tv, s_next); }
;         ATT_SB();
;         if constexpr (LEAD) {
;             ATT_QK(); ATT_SB();
;             ATT_PVP(0); ATT_SB();
;             if constexpr (DV == 128) { ATT_VLOAD(s_prev, 1); ATT_SB(); ATT_EXP(); ATT_SB(); ATT_PVP(1); ATT_SB(); }
;             if (one_) ATT_KLOAD(s_next);
;             ATT_SB();
;             if constexpr (DV == 64) ATT_EXP();
;             ATT_SUMPACK();
;             asm volatile("" : "+v"(pw[0]), "+v"(pw[1]), "+v"(pw[2]), "+v"(pw[3]));
; #pragma unroll
;             for (int qb = 0; qb < NQB; ++qb) asm volatile("" : "+v"(lsum[qb]));
.LBB0_965:
	v_lshl_add_u32 v130, s29, 13, v177
	s_waitcnt lgkmcnt(0)
	ds_read_b128 v[180:183], v130 offset:36864
	ds_read_b128 v[184:187], v130 offset:38912
	ds_read_b128 v[188:191], v130 offset:40960
	ds_read_b128 v[204:207], v130 offset:43008
	s_mov_b32 s40, s28
	s_mov_b32 s28, s37
	s_add_i32 s16, s27, -1
	s_min_u32 s16, s16, 0x80
	s_mul_i32 s38, s16, 0x38000
	s_lshl_b32 s16, s40, 13
	v_lshl_add_u64 v[130:131], v[162:163], 0, s[38:39]
	s_add_i32 s37, s16, s49
	v_lshl_add_u64 v[130:131], v[130:131], 0, s[96:97]
	s_mov_b32 m0, s37
	s_nop 0
	global_load_lds_dwordx4 v[130:131], off
	s_min_u32 s37, s27, 0x83
	s_lshl_b32 s38, s37, 7
	s_lshl_b32 s37, s28, 13
	v_lshl_add_u64 v[130:131], v[164:165], 0, s[38:39]
	s_add_i32 s38, s37, s36
	s_mov_b32 m0, s38
	s_nop 0
	global_load_lds_dwordx4 v[130:131], off
	v_mfma_f32_16x16x32_bf16 v[130:133], v[34:37], v[6:9], 0
	v_mfma_f32_16x16x32_bf16 v[134:137], v[34:37], v[14:17], 0
	v_mfma_f32_16x16x32_bf16 v[138:141], v[34:37], v[22:25], 0
	v_mfma_f32_16x16x32_bf16 v[142:145], v[34:37], v[26:29], 0
	v_mfma_f32_16x16x32_bf16 v[158:161], v[42:45], v[2:5], v[130:133]
	v_mfma_f32_16x16x32_bf16 v[154:157], v[42:45], v[10:13], v[134:137]
	v_mfma_f32_16x16x32_bf16 v[130:133], v[38:41], v[6:9], 0
	v_mfma_f32_16x16x32_bf16 v[134:137], v[38:41], v[14:17], 0
	v_mfma_f32_16x16x32_bf16 v[208:211], v[38:41], v[22:25], 0
	v_mfma_f32_16x16x32_bf16 v[212:215], v[38:41], v[26:29], 0
	v_mfma_f32_16x16x32_bf16 v[150:153], v[42:45], v[18:21], v[138:141]
	v_mfma_f32_16x16x32_bf16 v[142:145], v[42:45], v[30:33], v[142:145]
	v_mfma_f32_16x16x32_bf16 v[146:149], v[46:49], v[2:5], v[130:133]
	v_mfma_f32_16x16x32_bf16 v[138:141], v[46:49], v[10:13], v[134:137]
	v_mfma_f32_16x16x32_bf16 v[134:137], v[46:49], v[18:21], v[208:211]
	v_mfma_f32_16x16x32_bf16 v[130:133], v[46:49], v[30:33], v[212:215]
	s_waitcnt lgkmcnt(3)
	v_mfma_f32_16x16x32_bf16 v[118:121], v[180:183], v[102:105], v[118:121]
	v_mfma_f32_16x16x32_bf16 v[110:113], v[180:183], v[114:117], v[110:113]
	v_mfma_f32_16x16x32_bf16 v[106:109], v[180:183], v[122:125], v[106:109]
	v_mfma_f32_16x16x32_bf16 v[98:101], v[180:183], v[126:129], v[98:101]
	s_waitcnt lgkmcnt(2)
	v_mfma_f32_16x16x32_bf16 v[94:97], v[184:187], v[102:105], v[94:97]
	v_mfma_f32_16x16x32_bf16 v[90:93], v[184:187], v[114:117], v[90:93]
	v_mfma_f32_16x16x32_bf16 v[86:89], v[184:187], v[122:125], v[86:89]
	v_mfma_f32_16x16x32_bf16 v[82:85], v[184:187], v[126:129], v[82:85]
	s_waitcnt lgkmcnt(1)
	v_mfma_f32_16x16x32_bf16 v[78:81], v[188:191], v[102:105], v[78:81]
	v_mfma_f32_16x16x32_bf16 v[74:77], v[188:191], v[114:117], v[74:77]
	v_mfma_f32_16x16x32_bf16 v[70:73], v[188:191], v[122:125], v[70:73]
	v_mfma_f32_16x16x32_bf16 v[66:69], v[188:191], v[126:129], v[66:69]
	s_waitcnt lgkmcnt(0)
	v_mfma_f32_16x16x32_bf16 v[62:65], v[204:207], v[102:105], v[62:65]
	v_mfma_f32_16x16x32_bf16 v[58:61], v[204:207], v[114:117], v[58:61]
	v_mfma_f32_16x16x32_bf16 v[54:57], v[204:207], v[122:125], v[54:57]
	v_mfma_f32_16x16x32_bf16 v[50:53], v[204:207], v[126:129], v[50:53]
	s_andn2_b64 vcc, exec, s[4:5]
	s_cbranch_vccnz .LBB0_964
	v_add_u32_e32 v38, s37, v175
	v_add_u32_e32 v46, s37, v178
	ds_read_b128 v[34:37], v38
	ds_read_b128 v[38:41], v38 offset:512
	ds_read_b128 v[42:45], v46
	ds_read_b128 v[46:49], v46 offset:512
	s_branch .LBB0_964

; #define ATT_DMA_K(t, sl) do { glds16(ksrc + (size_t)(t) * 64 * kpitch, (unsigned)__builtin_amdgcn_readfirstlane(kdst + (sl) * KSLOT)); \
;         if constexpr (DQK == 96) glds16(krsrc + (size_t)(t) * 64 * 32, (unsigned)__builtin_amdgcn_readfirstlane(krdst + (sl) * KSLOT)); } while (0)
; #define ATT_DMA_V(t, sl) do { glds16(vsrc + (size_t)(t) * 64, (unsigned)__builtin_amdgcn_readfirstlane(vdst + (sl) * VSLOT)); \
;         if constexpr (DV == 128) glds16(vsrc + (size_t)64 * NR + (size_t)(t) * 64, (unsigned)__builtin_amdgcn_readfirstlane(vdst + (sl) * VSLOT + 8192)); } while (0)
; template <int DQK, int DV, bool LEAD> ...
;     ...
;     ATT_DMA_K(0, 0); ATT_DMA_V(0, 0); ATT_DMA_K(1, 1); ATT_DMA_K(2, 2);
;     bf16x8 qf[NQB * NDS];
;     {
;       const float c2 = (DQK == 64) ? C2_EVEN : C2_ODD; const bool lat = tq0 >= 0;
; #pragma unroll
;       for (int qb = 0; qb < NQB; ++qb) {
;           const bf16_t* qp = Q + (size_t)(qrow0 + qoff + qb * 16 + q16) * qpitch + g4 * 8;
;           bf16x8 raw[NDS];
; #pragma unroll
;           for (int ds = 0; ds < NDS; ++ds) raw[ds] = *(const bf16x8*)(qp + ds * 32);
;           float x[NDS][8];
; #pragma unroll
;           for (int ds = 0; ds < NDS; ++ds)
; #pragma unroll
;               for (int j = 0; j < 8; ++j) x[ds][j] = __uint_as_float(((unsigned)(unsigned short)raw[ds][j]) << 16);
;           const int tq = tq0 + qoff + qb * 16 + q16, prow = (tq >> 6) & 127, pcol = tq & 63;
;           float sn = 0.f;
; #pragma unroll
;           for (int ds = 0; ds < 2; ++ds)
; #pragma unroll
;               for (int j = 0; j < 8; ++j) sn += x[ds][j] * x[ds][j];
;           sn = lanes4_sum(sn);
;           const float rn = rsqrtf(sn * (1.f / 64.f) + EPS);
.LBB0_973:
	v_mov_b32_e32 v37, v0
	s_ashr_i32 s29, s28, 31
	v_readfirstlane_b32 s4, v37
	s_ashr_i32 s30, s4, 6
	v_bfe_u32 v1, v37, 3, 3
	v_lshl_or_b32 v6, s30, 3, v1
	s_lshl_b32 s5, s30, 1
	s_lshr_b32 s4, s4, 5
	v_ashrrev_i32_e32 v2, 1, v6
	s_and_b32 s5, s5, 2
	s_and_b32 s4, s4, 4
	v_and_b32_e32 v203, 7, v37
	v_and_b32_e32 v3, 1, v2
	s_or_b32 s4, s5, s4
	v_bitop3_b32 v7, s4, v203, v3 bitop3:0x36
	v_xor_b32_e32 v8, v2, v37
	v_add_u32_e32 v4, s28, v6
	v_mov_b64_e32 v[2:3], s[36:37]
	v_mad_i64_i32 v[2:3], s[4:5], v4, s92, v[2:3]
	v_mov_b64_e32 v[4:5], s[40:41]
	v_lshlrev_b32_e32 v194, 4, v7
	s_lshl_b32 s16, s30, 10
	v_mad_i64_i32 v[4:5], s[4:5], v6, s91, v[4:5]
	v_lshl_add_u64 v[22:23], v[2:3], 0, v[194:195]
	v_lshlrev_b32_e32 v2, 4, v8
	s_add_i32 s16, s16, 0
	v_lshl_add_u64 v[4:5], s[28:29], 1, v[4:5]
	v_and_b32_e32 v194, 0x70, v2
	s_mov_b32 m0, s16
	s_nop 0
	global_load_lds_dwordx4 v[22:23], off
	v_lshl_add_u64 v[204:205], v[4:5], 0, v[194:195]
	s_add_i32 s29, s16, 0x9000
	s_mov_b32 m0, s29
	s_nop 0
	global_load_lds_dwordx4 v[204:205], off
	s_mov_b64 s[4:5], 0x840000
	v_lshl_add_u64 v[206:207], v[204:205], 0, s[4:5]
	s_add_i32 s4, s29, 0x2000
	s_mov_b32 m0, s4
	s_nop 0
	global_load_lds_dwordx4 v[206:207], off
	s_mov_b64 s[4:5], 0x38000
	s_lshl_b32 s25, s30, 5
	v_lshl_add_u64 v[2:3], v[22:23], 0, s[4:5]
	s_add_i32 s4, s16, 0x2000
	s_mov_b32 m0, s4
	s_nop 0
	global_load_lds_dwordx4 v[2:3], off
	v_and_b32_e32 v36, 15, v37
	s_mov_b64 s[4:5], 0x70000
	s_add_i32 s25, s25, s28
	v_and_b32_e32 v194, 48, v37
	v_lshl_add_u64 v[2:3], v[22:23], 0, s[4:5]
	s_add_i32 s4, s16, 0x4000
	v_or_b32_e32 v10, s25, v36
	v_lshl_add_u64 v[6:7], s[26:27], 0, v[194:195]
	s_mov_b32 m0, s4
	s_nop 0
	global_load_lds_dwordx4 v[2:3], off
	v_bfe_u32 v214, v37, 4, 2
	v_mad_i64_i32 v[8:9], s[4:5], v10, s92, v[6:7]
	v_or_b32_e32 v10, 16, v10
	v_mad_i64_i32 v[6:7], s[4:5], v10, s92, v[6:7]
	global_load_dwordx4 v[2:5], v[8:9], off offset:64
	global_load_dwordx4 v[10:13], v[6:7], off offset:64
	global_load_dwordx4 v[38:41], v[8:9], off
	global_load_dwordx4 v[42:45], v[6:7], off
	v_lshlrev_b32_e32 v215, 1, v37
	v_and_b32_e32 v6, 3, v37
	v_lshrrev_b32_e32 v7, 1, v37
	v_and_or_b32 v6, v215, 24, v6
	v_lshlrev_b32_e32 v62, 5, v214
	v_bitop3_b32 v60, v214, v7, 7 bitop3:0x78
	v_lshl_add_u32 v66, v6, 7, 0
	global_load_dwordx4 v[6:9], v62, s[22:23] offset:144
	global_load_dwordx4 v[14:17], v62, s[22:23] offset:128
	global_load_dwordx4 v[18:21], v62, s[22:23] offset:16
	s_mov_b32 s4, 0x3c800000
	v_and_b32_e32 v61, 63, v37
	v_lshlrev_b32_e32 v67, 4, v60
	v_add_u32_e32 v217, v66, v67
	v_lshl_add_u64 v[210:211], v[22:23], 0, s[96:97]
	v_lshlrev_b32_e32 v194, 7, v36
	s_mov_b32 s31, 1
	s_mov_b32 s42, 2
	v_or_b32_e32 v216, 4, v214
	s_waitcnt vmcnt(5)
	v_and_b32_e32 v25, 0xffff0000, v13
	s_waitcnt vmcnt(4)
	v_and_b32_e32 v57, 0xffff0000, v38
	v_and_b32_e32 v51, 0xffff0000, v2
	v_lshlrev_b32_e32 v50, 16, v2
	v_lshlrev_b32_e32 v56, 16, v38
	v_mul_f32_e32 v2, v57, v57
	v_lshlrev_b32_e32 v24, 16, v13
	v_and_b32_e32 v27, 0xffff0000, v12
	v_lshlrev_b32_e32 v26, 16, v12
	v_and_b32_e32 v13, 0xffff0000, v3
	v_lshlrev_b32_e32 v12, 16, v3
	s_waitcnt vmcnt(3)
	v_and_b32_e32 v33, 0xffff0000, v45
	v_lshlrev_b32_e32 v32, 16, v45
	v_and_b32_e32 v35, 0xffff0000, v44
	v_lshlrev_b32_e32 v34, 16, v44
	v_and_b32_e32 v45, 0xffff0000, v39
	v_lshlrev_b32_e32 v44, 16, v39
	v_pk_fma_f32 v[2:3], v[56:57], v[56:57], v[2:3] op_sel_hi:[1,1,0]
	v_and_b32_e32 v49, 0xffff0000, v4
	v_lshlrev_b32_e32 v48, 16, v4
	v_pk_fma_f32 v[2:3], v[44:45], v[44:45], v[2:3]
	v_mul_f32_e32 v4, v45, v45
	v_and_b32_e32 v53, 0xffff0000, v40
	v_lshlrev_b32_e32 v52, 16, v40
	v_pk_add_f32 v[2:3], v[4:5], v[2:3] op_sel_hi:[0,1]
	v_pk_fma_f32 v[2:3], v[52:53], v[52:53], v[2:3]
	v_mul_f32_e32 v4, v53, v53
	v_and_b32_e32 v29, 0xffff0000, v11
	v_lshlrev_b32_e32 v28, 16, v11
	v_and_b32_e32 v31, 0xffff0000, v10
	v_lshlrev_b32_e32 v30, 16, v10
	v_and_b32_e32 v11, 0xffff0000, v41
	v_lshlrev_b32_e32 v10, 16, v41
	v_pk_add_f32 v[2:3], v[4:5], v[2:3] op_sel_hi:[0,1]
	v_pk_fma_f32 v[2:3], v[10:11], v[10:11], v[2:3]
	v_mul_f32_e32 v4, v11, v11
	v_pk_add_f32 v[2:3], v[4:5], v[2:3] op_sel_hi:[0,1]
	v_pk_fma_f32 v[2:3], v[50:51], v[50:51], v[2:3]
	v_mul_f32_e32 v4, v51, v51
	v_pk_add_f32 v[2:3], v[4:5], v[2:3] op_sel_hi:[0,1]
	v_pk_fma_f32 v[2:3], v[12:13], v[12:13], v[2:3]
	v_mul_f32_e32 v4, v13, v13
	v_pk_add_f32 v[2:3], v[4:5], v[2:3] op_sel_hi:[0,1]
	v_pk_fma_f32 v[2:3], v[48:49], v[48:49], v[2:3]
	v_mul_f32_e32 v4, v49, v49
	v_and_b32_e32 v47, 0xffff0000, v5
	v_lshlrev_b32_e32 v46, 16, v5
	v_pk_add_f32 v[2:3], v[4:5], v[2:3] op_sel_hi:[0,1]
	v_pk_fma_f32 v[2:3], v[46:47], v[46:47], v[2:3]
	v_mul_f32_e32 v4, v47, v47
	v_pk_add_f32 v[2:3], v[4:5], v[2:3] op_sel_hi:[0,1]
	v_mov_b32_e32 v3, v2
	s_nop 1
	v_permlane16_swap_b32_e32 v2, v3
	v_add_f32_e32 v3, v2, v3
	v_and_b32_e32 v55, 0xffff0000, v43
	v_lshlrev_b32_e32 v54, 16, v43
	v_mov_b32_e32 v5, v3
	v_and_b32_e32 v43, 0xffff0000, v42
	s_nop 0
	v_permlane32_swap_b32_e32 v3, v5
	v_lshlrev_b32_e32 v42, 16, v42
	v_mul_f32_e32 v2, v43, v43
	v_pk_fma_f32 v[38:39], v[42:43], v[42:43], v[2:3] op_sel_hi:[1,1,0]
	v_mul_f32_e32 v2, v55, v55
	v_pk_fma_f32 v[38:39], v[54:55], v[54:55], v[38:39]
	s_nop 0
	v_pk_add_f32 v[38:39], v[2:3], v[38:39] op_sel_hi:[0,1]
	v_pk_fma_f32 v[38:39], v[34:35], v[34:35], v[38:39]
	v_mul_f32_e32 v2, v35, v35
	v_pk_add_f32 v[38:39], v[2:3], v[38:39] op_sel_hi:[0,1]
	v_pk_fma_f32 v[38:39], v[32:33], v[32:33], v[38:39]
	v_mul_f32_e32 v2, v33, v33
	v_pk_add_f32 v[38:39], v[2:3], v[38:39] op_sel_hi:[0,1]
	v_pk_fma_f32 v[38:39], v[30:31], v[30:31], v[38:39]
	v_mul_f32_e32 v2, v31, v31
	v_pk_add_f32 v[38:39], v[2:3], v[38:39] op_sel_hi:[0,1]
	v_pk_fma_f32 v[38:39], v[28:29], v[28:29], v[38:39]
	v_mul_f32_e32 v2, v29, v29
	v_pk_add_f32 v[38:39], v[2:3], v[38:39] op_sel_hi:[0,1]
	v_pk_fma_f32 v[38:39], v[26:27], v[26:27], v[38:39]
	v_mul_f32_e32 v2, v27, v27
	v_pk_add_f32 v[38:39], v[2:3], v[38:39] op_sel_hi:[0,1]
	v_pk_fma_f32 v[38:39], v[24:25], v[24:25], v[38:39]
	v_mul_f32_e32 v2, v25, v25
	v_pk_add_f32 v[38:39], v[2:3], v[38:39] op_sel_hi:[0,1]
	v_mov_b32_e32 v2, v38
	s_nop 1
	v_permlane16_swap_b32_e32 v38, v2
	v_add_f32_e32 v2, v38, v2
	global_load_dwordx4 v[38:41], v62, s[22:23]
	v_mov_b32_e32 v4, v2
	s_nop 1
	v_permlane32_swap_b32_e32 v2, v4
	v_pk_add_f32 v[2:3], v[2:3], v[4:5]
	s_nop 0
	v_pk_fma_f32 v[58:59], v[2:3], s[4:5], v[196:197] op_sel_hi:[1,0,0]
	s_nop 0
	v_mul_f32_e32 v2, 0x4b800000, v59
	v_cmp_gt_f32_e32 vcc, s95, v59
	v_cmp_gt_f32_e64 s[4:5], s95, v58
	s_nop 0
	v_cndmask_b32_e32 v2, v59, v2, vcc
	v_rsq_f32_e32 v2, v2
	s_nop 0
	v_mul_f32_e32 v3, 0x45800000, v2
	v_cndmask_b32_e32 v60, v2, v3, vcc
	s_waitcnt vmcnt(3)
; __device__ __forceinline__ unsigned cvtpk(float lo, float hi) { f32x2 v = {lo, hi}; bf16x2_t b = __builtin_convertvector(v, bf16x2_t); return __builtin_bit_cast(unsigned, b); }
; template <int DQK, int DV, bool LEAD> ...
;     ...
; #pragma unroll
;           for (int ds = 0; ds < 2; ++ds)
; #pragma unroll
;               for (int j = 0; j < 8; ++j) x[ds][j] *= rn * qgain[32 * ds + 8 * g4 + j];
;           if constexpr (DQK == 64) {
; #pragma unroll
;               for (int ds = 0; ds < 2; ++ds)
; #pragma unroll
;                   for (int j = 0; j < 8; ++j) {
;                       auto rr = __builtin_amdgcn_permlane32_swap(__float_as_uint(x[ds][j]), __float_as_uint(x[ds][j]), false, false);
;                       const float other = hi ? __uint_as_float(rr[0]) : __uint_as_float(rr[1]);
;                       float cc = 1.f, sg = 0.f;
;                       if (lat) { const f32x2 cs = rope[(ds ? pcol : prow) * 16 + 8 * (g4 & 1) + j]; cc = cs.x; sg = hi ? cs.y : -cs.y; }
;                       x[ds][j] = x[ds][j] * cc + other * sg; }
;           } else {
;               float sr = 0.f;
; #pragma unroll
;               for (int j = 0; j < 8; ++j) sr += x[2][j] * x[2][j];
;               sr = lanes4_sum(sr);
;               const float rq = rsqrtf(sr * (1.f / 32.f) + EPS);
; #pragma unroll
;               for (int j = 0; j < 8; ++j) { const float av = x[2][j] * rq * qgain[64 + 8 * g4 + j];
;                   auto rr = __builtin_amdgcn_permlane16_swap(__float_as_uint(av), __float_as_uint(av), false, false);
;                   const float other = (g4 & 1) ? __uint_as_float(rr[0]) : __uint_as_float(rr[1]);
;                   float cc = 1.f, sg = 0.f;
;                   if (lat) { const f32x2 cs = rope[((g4 & 2) ? pcol : prow) * 8 + j]; cc = cs.x; sg = (g4 & 1) ? cs.y : -cs.y; }
;                   x[2][j] = av * cc + other * sg; }
;           }
; #pragma unroll
;           for (int ds = 0; ds < NDS; ++ds) { u32x4 w;
; #pragma unroll
;               for (int i = 0; i < 4; ++i) w[i] = cvtpk(x[ds][2 * i] * c2, x[ds][2 * i + 1] * c2);
;               qf[qb * NDS + ds] = __builtin_bit_cast(bf16x8, w); }
	v_pk_mul_f32 v[2:3], v[60:61], v[8:9] op_sel_hi:[0,1]
	v_pk_mul_f32 v[2:3], v[2:3], v[46:47]
	v_cmp_gt_u32_e32 vcc, 32, v61
	v_mov_b32_e32 v4, v2
	v_mov_b32_e32 v46, v2
	v_mov_b32_e32 v5, v3
	v_mov_b32_e32 v47, v3
	v_permlane32_swap_b32_e32 v4, v46
	s_nop 0
	v_permlane32_swap_b32_e32 v5, v47
	v_cndmask_b32_e32 v5, v5, v47, vcc
	v_cndmask_b32_e32 v4, v4, v46, vcc
	v_pk_fma_f32 v[2:3], v[4:5], 0, v[2:3] op_sel_hi:[1,0,1]
	s_nop 0
	v_pk_mul_f32 v[2:3], v[2:3], s[94:95] op_sel_hi:[1,0]
	s_nop 0
	v_cvt_pk_bf16_f32 v5, v2, v3
	v_pk_mul_f32 v[2:3], v[60:61], v[6:7] op_sel_hi:[0,1]
	v_pk_mul_f32 v[2:3], v[2:3], v[48:49]
	s_nop 0
	v_mov_b32_e32 v4, v2
	v_mov_b32_e32 v46, v2
	v_mov_b32_e32 v47, v3
	v_mov_b32_e32 v48, v3
	v_permlane32_swap_b32_e32 v4, v46
	s_nop 0
	v_permlane32_swap_b32_e32 v47, v48
	v_cndmask_b32_e32 v47, v47, v48, vcc
	v_cndmask_b32_e32 v46, v4, v46, vcc
	v_pk_fma_f32 v[2:3], v[46:47], 0, v[2:3] op_sel_hi:[1,0,1]
	s_nop 0
	v_pk_mul_f32 v[2:3], v[2:3], s[94:95] op_sel_hi:[1,0]
	s_nop 0
	v_cvt_pk_bf16_f32 v4, v2, v3
	s_waitcnt vmcnt(2)
	v_pk_mul_f32 v[2:3], v[60:61], v[16:17] op_sel_hi:[0,1]
	v_pk_mul_f32 v[2:3], v[2:3], v[12:13]
	s_nop 0
	v_mov_b32_e32 v12, v2
	v_mov_b32_e32 v46, v2
	v_mov_b32_e32 v13, v3
	v_mov_b32_e32 v47, v3
	v_permlane32_swap_b32_e32 v12, v46
	s_nop 0
	v_permlane32_swap_b32_e32 v13, v47
	v_cndmask_b32_e32 v13, v13, v47, vcc
	v_cndmask_b32_e32 v12, v12, v46, vcc
	v_pk_fma_f32 v[2:3], v[12:13], 0, v[2:3] op_sel_hi:[1,0,1]
	v_pk_mul_f32 v[12:13], v[14:15], v[60:61] op_sel_hi:[1,0]
	v_pk_mul_f32 v[2:3], v[2:3], s[94:95] op_sel_hi:[1,0]
	v_pk_mul_f32 v[12:13], v[12:13], v[50:51]
	v_cvt_pk_bf16_f32 v3, v2, v3
	v_mov_b32_e32 v2, v12
	v_mov_b32_e32 v46, v12
	v_mov_b32_e32 v47, v13
	v_mov_b32_e32 v48, v13
	v_permlane32_swap_b32_e32 v2, v46
	s_nop 0
	v_permlane32_swap_b32_e32 v47, v48
	v_cndmask_b32_e32 v47, v47, v48, vcc
	v_cndmask_b32_e32 v46, v2, v46, vcc
	v_pk_fma_f32 v[12:13], v[46:47], 0, v[12:13] op_sel_hi:[1,0,1]
	s_nop 0
	v_pk_mul_f32 v[12:13], v[12:13], s[94:95] op_sel_hi:[1,0]
	s_nop 0
	v_cvt_pk_bf16_f32 v2, v12, v13
	s_waitcnt vmcnt(1)
	v_pk_mul_f32 v[12:13], v[20:21], v[60:61] op_sel_hi:[1,0]
	s_nop 0
	v_pk_mul_f32 v[10:11], v[12:13], v[10:11]
	s_nop 0
	v_mov_b32_e32 v12, v10
	v_mov_b32_e32 v46, v10
	v_mov_b32_e32 v13, v11
	v_mov_b32_e32 v47, v11
	v_permlane32_swap_b32_e32 v12, v46
	s_nop 0
	v_permlane32_swap_b32_e32 v13, v47
	v_cndmask_b32_e32 v13, v13, v47, vcc
	v_cndmask_b32_e32 v12, v12, v46, vcc
	v_pk_fma_f32 v[10:11], v[12:13], 0, v[10:11] op_sel_hi:[1,0,1]
	s_nop 0
	v_pk_mul_f32 v[10:11], v[10:11], s[94:95] op_sel_hi:[1,0]
	s_nop 0
	v_cvt_pk_bf16_f32 v13, v10, v11
	v_pk_mul_f32 v[10:11], v[18:19], v[60:61] op_sel_hi:[1,0]
	s_nop 0
	v_pk_mul_f32 v[10:11], v[10:11], v[52:53]
	s_nop 0
	v_mov_b32_e32 v12, v10
	v_mov_b32_e32 v46, v10
	v_mov_b32_e32 v47, v11
	v_mov_b32_e32 v48, v11
	v_permlane32_swap_b32_e32 v12, v46
	s_nop 0
	v_permlane32_swap_b32_e32 v47, v48
	v_cndmask_b32_e32 v47, v47, v48, vcc
	v_cndmask_b32_e32 v46, v12, v46, vcc
	v_pk_fma_f32 v[10:11], v[46:47], 0, v[10:11] op_sel_hi:[1,0,1]
	s_nop 0
	v_pk_mul_f32 v[10:11], v[10:11], s[94:95] op_sel_hi:[1,0]
	s_nop 0
	v_cvt_pk_bf16_f32 v12, v10, v11
	s_waitcnt vmcnt(0)
	v_pk_mul_f32 v[10:11], v[40:41], v[60:61] op_sel_hi:[1,0]
	s_nop 0
	v_pk_mul_f32 v[10:11], v[10:11], v[44:45]
	s_nop 0
	v_mov_b32_e32 v44, v10
	v_mov_b32_e32 v46, v10
	v_mov_b32_e32 v45, v11
	v_mov_b32_e32 v47, v11
	v_permlane32_swap_b32_e32 v44, v46
	s_nop 0
	v_permlane32_swap_b32_e32 v45, v47
	v_cndmask_b32_e32 v45, v45, v47, vcc
	v_cndmask_b32_e32 v44, v44, v46, vcc
	v_pk_fma_f32 v[10:11], v[44:45], 0, v[10:11] op_sel_hi:[1,0,1]
	v_pk_mul_f32 v[44:45], v[38:39], v[60:61] op_sel_hi:[1,0]
	v_pk_mul_f32 v[10:11], v[10:11], s[94:95] op_sel_hi:[1,0]
	v_pk_mul_f32 v[44:45], v[44:45], v[56:57]
	v_cvt_pk_bf16_f32 v11, v10, v11
	v_mov_b32_e32 v10, v44
	v_mov_b32_e32 v46, v44
	s_nop 1
	v_permlane32_swap_b32_e32 v10, v46
	v_mov_b32_e32 v47, v45
	v_mov_b32_e32 v48, v45
	v_cndmask_b32_e32 v46, v10, v46, vcc
	v_mul_f32_e32 v10, 0x4b800000, v58
	v_permlane32_swap_b32_e32 v47, v48
	v_cndmask_b32_e64 v10, v58, v10, s[4:5]
	v_cndmask_b32_e32 v47, v47, v48, vcc
	v_rsq_f32_e32 v48, v10
	v_pk_fma_f32 v[44:45], v[46:47], 0, v[44:45] op_sel_hi:[1,0,1]
	s_nop 0
	v_pk_mul_f32 v[44:45], v[44:45], s[94:95] op_sel_hi:[1,0]
	s_nop 0
	v_cvt_pk_bf16_f32 v10, v44, v45
	v_mul_f32_e32 v44, 0x45800000, v48
	v_cndmask_b32_e64 v44, v48, v44, s[4:5]
	v_pk_mul_f32 v[38:39], v[38:39], v[44:45] op_sel_hi:[1,0]
	v_pk_mul_f32 v[6:7], v[6:7], v[44:45] op_sel_hi:[1,0]
	v_pk_mul_f32 v[38:39], v[38:39], v[42:43]
	v_pk_mul_f32 v[8:9], v[8:9], v[44:45] op_sel_hi:[1,0]
	v_pk_mul_f32 v[40:41], v[40:41], v[44:45] op_sel_hi:[1,0]
	v_pk_mul_f32 v[6:7], v[6:7], v[26:27]
	v_pk_mul_f32 v[8:9], v[8:9], v[24:25]
	v_mov_b32_e32 v24, v38
	v_mov_b32_e32 v26, v38
	v_mov_b32_e32 v25, v39
	v_mov_b32_e32 v27, v39
	v_pk_mul_f32 v[40:41], v[40:41], v[54:55]
	v_pk_mul_f32 v[16:17], v[16:17], v[44:45] op_sel_hi:[1,0]
	v_permlane32_swap_b32_e32 v24, v26
	v_permlane32_swap_b32_e32 v25, v27
	v_pk_mul_f32 v[18:19], v[18:19], v[44:45] op_sel_hi:[1,0]
	v_pk_mul_f32 v[16:17], v[16:17], v[28:29]
	v_cndmask_b32_e32 v25, v25, v27, vcc
	v_cndmask_b32_e32 v24, v24, v26, vcc
	v_mov_b32_e32 v26, v40
	v_mov_b32_e32 v28, v40
	v_mov_b32_e32 v27, v41
	v_mov_b32_e32 v29, v41
	v_pk_mul_f32 v[18:19], v[18:19], v[34:35]
	v_pk_mul_f32 v[14:15], v[14:15], v[44:45] op_sel_hi:[1,0]
	v_permlane32_swap_b32_e32 v26, v28
	v_permlane32_swap_b32_e32 v27, v29
	v_pk_mul_f32 v[14:15], v[14:15], v[30:31]
	v_cndmask_b32_e32 v27, v27, v29, vcc
	v_cndmask_b32_e32 v26, v26, v28, vcc
; __device__ __forceinline__ unsigned cvtpk(float lo, float hi) { f32x2 v = {lo, hi}; bf16x2_t b = __builtin_convertvector(v, bf16x2_t); return __builtin_bit_cast(unsigned, b); }
; #define ATT_SB() __builtin_amdgcn_sched_barrier(0)
; #define ATT_DMA_K(t, sl) do { glds16(ksrc + (size_t)(t) * 64 * kpitch, (unsigned)__builtin_amdgcn_readfirstlane(kdst + (sl) * KSLOT)); \
;         if constexpr (DQK == 96) glds16(krsrc + (size_t)(t) * 64 * 32, (unsigned)__builtin_amdgcn_readfirstlane(krdst + (sl) * KSLOT)); } while (0)
; #define ATT_DMA_V(t, sl) do { glds16(vsrc + (size_t)(t) * 64, (unsigned)__builtin_amdgcn_readfirstlane(vdst + (sl) * VSLOT)); \
;         if constexpr (DV == 128) glds16(vsrc + (size_t)64 * NR + (size_t)(t) * 64, (unsigned)__builtin_amdgcn_readfirstlane(vdst + (sl) * VSLOT + 8192)); } while (0)
; #define ATT_KLOAD(sl) do { _Pragma("unroll") for (int kb_ = 0; kb_ < NKW; ++kb_) _Pragma("unroll") for (int ds_ = 0; ds_ < NDS; ++ds_) { \
;         if (ds_ < 2) kf[kb_ * NDS + ds_] = *(const LAS bf16x8*)(kp[ds_ & 1] + (sl) * KSLOT + (kb_ & 1) * 512 + (kb_ >> 1) * 4096); \
;         else kf[kb_ * NDS + ds_] = *(const LAS bf16x8*)(krp + (sl) * KSLOT + (kb_ & 1) * 256 + (kb_ >> 1) * 2048); } } while (0)
; template <int DQK, int DV, bool LEAD> ...
;     ...
; #pragma unroll
;           for (int ds = 0; ds < NDS; ++ds) { u32x4 w;
; #pragma unroll
;               for (int i = 0; i < 4; ++i) w[i] = cvtpk(x[ds][2 * i] * c2, x[ds][2 * i + 1] * c2);
;               qf[qb * NDS + ds] = __builtin_bit_cast(bf16x8, w); }
;       }
; #pragma unroll
;       for (int d0 = 0; d0 < NQB * NDS; ++d0) asm volatile("" : "+v"(qf[d0])); }
;     wait_bar<0>();
;     bf16x8 kf[NKW * NDS], vf[NVF];
;     ATT_KLOAD(0);
;     asm volatile("s_waitcnt lgkmcnt(0)\n\ts_barrier" ::: "memory");
;     float lsum[NQB];
; #pragma unroll
;     for (int qb = 0; qb < NQB; ++qb) lsum[qb] = 0.f;
;     const f32x4 zero4 = {0.f, 0.f, 0.f, 0.f};
;     f32x4 o[NDB][NQB], c[NKW][NQB]; u32x4 pw[4];
; #pragma unroll
;     for (int i = 0; i < NDB; ++i)
; #pragma unroll
;         for (int qb = 0; qb < NQB; ++qb) o[i][qb] = zero4;
;     ATT_DMA_K(3, 0); ATT_DMA_V(1, 1);
;     ATT_QK(); ATT_SB();
;     ATT_KLOAD(1); ATT_SB();
;     if constexpr (LEAD) { ATT_EXP(); ATT_SUMPACK(); }
;     wait_bar<NDMA>();
;     int s_prev = 0, s_cur = 1, s_next = 2;
	v_mov_b32_e32 v28, v18
	v_mov_b32_e32 v30, v18
	v_mov_b32_e32 v29, v19
	v_mov_b32_e32 v31, v19
	v_pk_mul_f32 v[20:21], v[20:21], v[44:45] op_sel_hi:[1,0]
	v_permlane32_swap_b32_e32 v28, v30
	v_permlane32_swap_b32_e32 v29, v31
	v_pk_mul_f32 v[20:21], v[20:21], v[32:33]
	v_cndmask_b32_e32 v29, v29, v31, vcc
	v_cndmask_b32_e32 v28, v28, v30, vcc
	v_pk_fma_f32 v[18:19], v[28:29], 0, v[18:19] op_sel_hi:[1,0,1]
	v_mov_b32_e32 v28, v20
	v_mov_b32_e32 v30, v20
	v_mov_b32_e32 v29, v21
	v_mov_b32_e32 v31, v21
	v_permlane32_swap_b32_e32 v28, v30
	s_nop 0
	v_permlane32_swap_b32_e32 v29, v31
	v_cndmask_b32_e32 v29, v29, v31, vcc
	v_cndmask_b32_e32 v28, v28, v30, vcc
	v_pk_fma_f32 v[20:21], v[28:29], 0, v[20:21] op_sel_hi:[1,0,1]
	v_mov_b32_e32 v28, v14
	v_mov_b32_e32 v30, v14
	v_mov_b32_e32 v29, v15
	v_mov_b32_e32 v31, v15
	v_permlane32_swap_b32_e32 v28, v30
	s_nop 0
	v_permlane32_swap_b32_e32 v29, v31
	v_cndmask_b32_e32 v29, v29, v31, vcc
	v_cndmask_b32_e32 v28, v28, v30, vcc
	v_pk_fma_f32 v[14:15], v[28:29], 0, v[14:15] op_sel_hi:[1,0,1]
	v_mov_b32_e32 v28, v16
	v_mov_b32_e32 v30, v16
	v_mov_b32_e32 v29, v17
	v_mov_b32_e32 v31, v17
	v_permlane32_swap_b32_e32 v28, v30
	s_nop 0
	v_permlane32_swap_b32_e32 v29, v31
	v_cndmask_b32_e32 v29, v29, v31, vcc
	v_cndmask_b32_e32 v28, v28, v30, vcc
	v_pk_fma_f32 v[16:17], v[28:29], 0, v[16:17] op_sel_hi:[1,0,1]
	v_mov_b32_e32 v28, v6
	v_mov_b32_e32 v30, v6
	v_mov_b32_e32 v29, v7
	v_mov_b32_e32 v31, v7
	v_permlane32_swap_b32_e32 v28, v30
	s_nop 0
	v_permlane32_swap_b32_e32 v29, v31
	v_cndmask_b32_e32 v29, v29, v31, vcc
	v_cndmask_b32_e32 v28, v28, v30, vcc
	v_pk_fma_f32 v[6:7], v[28:29], 0, v[6:7] op_sel_hi:[1,0,1]
	v_mov_b32_e32 v28, v8
	v_mov_b32_e32 v30, v8
	v_mov_b32_e32 v29, v9
	v_mov_b32_e32 v31, v9
	v_permlane32_swap_b32_e32 v28, v30
	s_nop 0
	v_permlane32_swap_b32_e32 v29, v31
	v_pk_fma_f32 v[24:25], v[24:25], 0, v[38:39] op_sel_hi:[1,0,1]
	v_cndmask_b32_e32 v29, v29, v31, vcc
	v_cndmask_b32_e32 v28, v28, v30, vcc
	v_pk_fma_f32 v[26:27], v[26:27], 0, v[40:41] op_sel_hi:[1,0,1]
	v_pk_fma_f32 v[8:9], v[28:29], 0, v[8:9] op_sel_hi:[1,0,1]
	v_pk_mul_f32 v[24:25], v[24:25], s[94:95] op_sel_hi:[1,0]
	v_pk_mul_f32 v[18:19], v[18:19], s[94:95] op_sel_hi:[1,0]
	v_pk_mul_f32 v[14:15], v[14:15], s[94:95] op_sel_hi:[1,0]
	v_pk_mul_f32 v[6:7], v[6:7], s[94:95] op_sel_hi:[1,0]
	v_cvt_pk_bf16_f32 v58, v24, v25
	v_pk_mul_f32 v[24:25], v[26:27], s[94:95] op_sel_hi:[1,0]
	v_cvt_pk_bf16_f32 v60, v18, v19
	v_pk_mul_f32 v[18:19], v[20:21], s[94:95] op_sel_hi:[1,0]
	v_cvt_pk_bf16_f32 v62, v14, v15
	v_pk_mul_f32 v[14:15], v[16:17], s[94:95] op_sel_hi:[1,0]
	v_cvt_pk_bf16_f32 v64, v6, v7
	v_pk_mul_f32 v[6:7], v[8:9], s[94:95] op_sel_hi:[1,0]
	v_cvt_pk_bf16_f32 v59, v24, v25
	v_cvt_pk_bf16_f32 v61, v18, v19
	v_cvt_pk_bf16_f32 v63, v14, v15
	v_cvt_pk_bf16_f32 v65, v6, v7
	s_waitcnt vmcnt(0) lgkmcnt(0)
	s_barrier
	ds_read_b128 v[6:9], v217
	ds_read_b128 v[14:17], v217 offset:512
	v_bfe_u32 v24, v37, 1, 3
	v_bitop3_b32 v24, v214, v24, 4 bitop3:0x36
	v_lshlrev_b32_e32 v32, 4, v24
	v_add_u32_e32 v220, v66, v32
	s_waitcnt lgkmcnt(1)
	v_mfma_f32_16x16x32_bf16 v[18:21], v[6:9], v[10:13], 0
	ds_read_b128 v[24:27], v220
	ds_read_b128 v[28:31], v220 offset:512
	v_add_u32_e32 v33, 0, v194
	v_add_u32_e32 v218, v33, v67
	v_mfma_f32_16x16x32_bf16 v[6:9], v[6:9], v[58:61], 0
	v_add_u32_e32 v219, v33, v32
	s_waitcnt lgkmcnt(1)
	v_mfma_f32_16x16x32_bf16 v[126:129], v[24:27], v[62:65], v[6:9]
	v_mfma_f32_16x16x32_bf16 v[6:9], v[14:17], v[10:13], 0
	s_waitcnt lgkmcnt(0)
	v_mfma_f32_16x16x32_bf16 v[122:125], v[28:31], v[2:5], v[6:9]
	v_mfma_f32_16x16x32_bf16 v[14:17], v[14:17], v[58:61], 0
	s_nop 4
	ds_read_b128 v[6:9], v217 offset:4096
	v_mfma_f32_16x16x32_bf16 v[138:141], v[24:27], v[2:5], v[18:21]
	v_mfma_f32_16x16x32_bf16 v[114:117], v[28:31], v[62:65], v[14:17]
	s_nop 2
	ds_read_b128 v[14:17], v220 offset:4096
	ds_read_b128 v[18:21], v217 offset:4608
	ds_read_b128 v[28:31], v220 offset:4608
	s_waitcnt lgkmcnt(0)
	s_barrier
	s_waitcnt lgkmcnt(3)
	v_mfma_f32_16x16x32_bf16 v[24:27], v[6:9], v[10:13], 0
	s_mov_b32 m0, s16
	s_nop 0
	global_load_lds_dwordx4 v[210:211], off
	s_add_i32 s4, s29, 0x4000
	v_mfma_f32_16x16x32_bf16 v[6:9], v[6:9], v[58:61], 0
	s_waitcnt lgkmcnt(2)
	v_mfma_f32_16x16x32_bf16 v[130:133], v[14:17], v[2:5], v[24:27]
	v_mfma_f32_16x16x32_bf16 v[118:121], v[14:17], v[62:65], v[6:9]
	v_lshl_add_u64 v[14:15], v[204:205], 0, s[66:67]
	s_mov_b32 m0, s4
	s_nop 0
	global_load_lds_dwordx4 v[14:15], off
	s_mov_b64 s[4:5], 0x840080
	s_waitcnt lgkmcnt(1)
	v_mfma_f32_16x16x32_bf16 v[6:9], v[18:21], v[10:13], 0
	v_lshl_add_u64 v[22:23], v[204:205], 0, s[4:5]
	s_add_i32 s4, s29, 0x6000
	s_mov_b32 m0, s4
	s_nop 0
	global_load_lds_dwordx4 v[22:23], off
	v_mfma_f32_16x16x32_bf16 v[14:17], v[18:21], v[58:61], 0
	s_mov_b32 s4, 0
	s_mov_b32 s6, s4
	s_mov_b32 s7, s4
	s_waitcnt lgkmcnt(0)
	v_mfma_f32_16x16x32_bf16 v[142:145], v[28:31], v[2:5], v[6:9]
	s_mov_b32 s5, s4
	v_mfma_f32_16x16x32_bf16 v[134:137], v[28:31], v[62:65], v[14:17]
	s_nop 0
	v_mov_b64_e32 v[8:9], s[6:7]
	v_mov_b64_e32 v[6:7], s[4:5]
	ds_read_b128 v[82:85], v217 offset:8192
	ds_read_b128 v[86:89], v217 offset:8704
	ds_read_b128 v[90:93], v220 offset:8192
	ds_read_b128 v[94:97], v220 offset:8704
	ds_read_b128 v[98:101], v217 offset:12288
	ds_read_b128 v[102:105], v217 offset:12800
	ds_read_b128 v[106:109], v220 offset:12288
	ds_read_b128 v[110:113], v220 offset:12800
	s_waitcnt vmcnt(3) lgkmcnt(0)
	s_barrier
	s_mov_b32 s5, 1
	v_mov_b32_e32 v42, 0
	s_cmp_lg_u32 s5, 0
	v_mov_b64_e32 v[16:17], v[8:9]
	v_mov_b64_e32 v[20:21], v[8:9]
	v_mov_b64_e32 v[24:25], v[8:9]
	v_mov_b64_e32 v[28:29], v[8:9]
	v_mov_b64_e32 v[32:33], v[8:9]
	v_mov_b64_e32 v[36:37], v[8:9]
	v_mov_b64_e32 v[40:41], v[8:9]
	s_cselect_b64 s[6:7], -1, 0
	v_mov_b64_e32 v[14:15], v[6:7]
	v_mov_b64_e32 v[18:19], v[6:7]
	v_mov_b64_e32 v[22:23], v[6:7]
	v_mov_b64_e32 v[26:27], v[6:7]
	v_mov_b64_e32 v[30:31], v[6:7]
	v_mov_b64_e32 v[34:35], v[6:7]
	v_mov_b64_e32 v[38:39], v[6:7]
	s_mov_b32 s38, 2
	v_mov_b32_e32 v43, v42
	v_mov_b32_e32 v44, v42
	v_mov_b32_e32 v45, v42
	v_mov_b32_e32 v46, v42
	v_mov_b32_e32 v47, v42
	v_mov_b32_e32 v48, v42
	v_mov_b32_e32 v49, v42
	v_mov_b32_e32 v50, v42
	v_mov_b32_e32 v51, v42
	v_mov_b32_e32 v52, v42
	v_mov_b32_e32 v53, v42
	v_mov_b32_e32 v54, v42
	v_mov_b32_e32 v55, v42
	v_mov_b32_e32 v56, v42
	v_mov_b32_e32 v57, v42
	v_mov_b32_e32 v66, v42
	v_mov_b32_e32 v67, v42
	v_mov_b32_e32 v68, v42
	v_mov_b32_e32 v69, v42
	v_mov_b32_e32 v70, v42
	v_mov_b32_e32 v71, v42
	v_mov_b32_e32 v72, v42
	v_mov_b32_e32 v73, v42
	v_mov_b32_e32 v74, v42
	v_mov_b32_e32 v75, v42
	v_mov_b32_e32 v76, v42
	v_mov_b32_e32 v77, v42
	v_mov_b32_e32 v78, v42
	v_mov_b32_e32 v79, v42
	v_mov_b32_e32 v80, v42
	v_mov_b32_e32 v81, v42
	v_mov_b32_e32 v208, v42
	v_mov_b32_e32 v209, v42
; #define ATT_SB() __builtin_amdgcn_sched_barrier(0)
; #define ATT_DMA_K(t, sl) do { glds16(ksrc + (size_t)(t) * 64 * kpitch, (unsigned)__builtin_amdgcn_readfirstlane(kdst + (sl) * KSLOT)); \
;         if constexpr (DQK == 96) glds16(krsrc + (size_t)(t) * 64 * 32, (unsigned)__builtin_amdgcn_readfirstlane(krdst + (sl) * KSLOT)); } while (0)
; #define ATT_DMA_V(t, sl) do { glds16(vsrc + (size_t)(t) * 64, (unsigned)__builtin_amdgcn_readfirstlane(vdst + (sl) * VSLOT)); \
;         if constexpr (DV == 128) glds16(vsrc + (size_t)64 * NR + (size_t)(t) * 64, (unsigned)__builtin_amdgcn_readfirstlane(vdst + (sl) * VSLOT + 8192)); } while (0)
; #define ATT_KLOAD(sl) do { _Pragma("unroll") for (int kb_ = 0; kb_ < NKW; ++kb_) _Pragma("unroll") for (int ds_ = 0; ds_ < NDS; ++ds_) { \
;         if (ds_ < 2) kf[kb_ * NDS + ds_] = *(const LAS bf16x8*)(kp[ds_ & 1] + (sl) * KSLOT + (kb_ & 1) * 512 + (kb_ >> 1) * 4096); \
;         else kf[kb_ * NDS + ds_] = *(const LAS bf16x8*)(krp + (sl) * KSLOT + (kb_ & 1) * 256 + (kb_ >> 1) * 2048); } } while (0)
; template <int DQK, int DV, bool LEAD> ...
;     ...
;     for (int t = 1; t < NT; ++t) {
;         __builtin_amdgcn_s_waitcnt(0xC07F);
;         if constexpr (!LEAD) { ATT_EXP(); ATT_SUMPACK(); ATT_SB(); }
;         ATT_VLOAD(s_prev, 0); ATT_SB();
;         { const int tk = (t + 3 < NT) ? t + 3 : NT - 1; ATT_DMA_K(tk, s_cur); }
;         { const int tv = (t + 1 < NT) ? t + 1 : NT - 1; ATT_DMA_V(tv, s_next); }
;         ATT_SB();
;         if constexpr (LEAD) {
;             ATT_QK(); ATT_SB();
;             ATT_PVP(0); ATT_SB();
;             if constexpr (DV == 128) { ATT_VLOAD(s_prev, 1); ATT_SB(); ATT_EXP(); ATT_SB(); ATT_PVP(1); ATT_SB(); }
;             if (one_) ATT_KLOAD(s_next);
;             ATT_SB();
;             if constexpr (DV == 64) ATT_EXP();
;             ATT_SUMPACK();
;             asm volatile("" : "+v"(pw[0]), "+v"(pw[1]), "+v"(pw[2]), "+v"(pw[3]));
; #pragma unroll
;             for (int qb = 0; qb < NQB; ++qb) asm volatile("" : "+v"(lsum[qb]));
;         } else {
;             if constexpr (DV == 128) {
;                 ATT_PVP(0); ATT_SB();
;                 ATT_VLOAD(s_prev, 1); ATT_SB();
;                 ATT_QK(); ATT_SB();
;                 if (one_) { ATT_KLOAD(s_next); ATT_SB(); ATT_PVP(1); }
;                 ATT_SB();
.LBB0_974:
	v_exp_f32_e32 v138, v138
	v_exp_f32_e32 v139, v139
	v_exp_f32_e32 v140, v140
	v_exp_f32_e32 v141, v141
	v_exp_f32_e32 v126, v126
	v_exp_f32_e32 v127, v127
	v_exp_f32_e32 v128, v128
	v_exp_f32_e32 v129, v129
	v_exp_f32_e32 v122, v122
	v_exp_f32_e32 v114, v114
	v_add_f32_e32 v146, v138, v139
	v_add_f32_e32 v147, v140, v141
	v_exp_f32_e32 v123, v123
	v_exp_f32_e32 v115, v115
	v_add_f32_e32 v146, v146, v147
	v_add_f32_e32 v147, v126, v127
	v_add_f32_e32 v148, v128, v129
	v_add_f32_e32 v147, v147, v148
	v_exp_f32_e32 v124, v124
	v_exp_f32_e32 v116, v116
	v_add_f32_e32 v146, v122, v146
	v_add_f32_e32 v147, v114, v147
	s_waitcnt lgkmcnt(0)
	v_exp_f32_e32 v125, v125
	v_exp_f32_e32 v117, v117
	v_add_f32_e32 v146, v123, v146
	v_add_f32_e32 v147, v115, v147
	v_exp_f32_e32 v130, v130
	v_exp_f32_e32 v118, v118
	v_add_f32_e32 v146, v124, v146
	v_add_f32_e32 v147, v116, v147
	v_exp_f32_e32 v131, v131
	v_exp_f32_e32 v119, v119
	v_add_f32_e32 v146, v125, v146
	v_add_f32_e32 v147, v117, v147
	v_exp_f32_e32 v132, v132
	v_exp_f32_e32 v120, v120
	v_add_f32_e32 v146, v130, v146
	v_add_f32_e32 v147, v118, v147
	v_exp_f32_e32 v133, v133
	v_exp_f32_e32 v121, v121
	v_add_f32_e32 v146, v131, v146
	v_add_f32_e32 v147, v119, v147
	v_exp_f32_e32 v142, v142
	v_exp_f32_e32 v134, v134
	v_add_f32_e32 v146, v132, v146
	v_add_f32_e32 v147, v120, v147
	v_exp_f32_e32 v143, v143
	v_exp_f32_e32 v135, v135
	v_add_f32_e32 v146, v133, v146
	v_add_f32_e32 v147, v121, v147
	v_exp_f32_e32 v144, v144
	v_exp_f32_e32 v136, v136
	v_add_f32_e32 v146, v142, v146
	v_add_f32_e32 v147, v134, v147
	v_exp_f32_e32 v145, v145
	v_exp_f32_e32 v137, v137
	v_add_f32_e32 v146, v143, v146
	v_add_f32_e32 v147, v135, v147
	s_mov_b32 s5, s31
	v_add_f32_e32 v146, v144, v146
	v_add_f32_e32 v147, v136, v147
	s_mov_b32 s31, s38
	v_add_f32_e32 v213, v145, v146
	v_add_f32_e32 v212, v137, v147
	v_cvt_pk_bf16_f32 v146, v138, v139
	v_cvt_pk_bf16_f32 v147, v140, v141
	v_cvt_pk_bf16_f32 v148, v122, v123
	v_cvt_pk_bf16_f32 v149, v124, v125
	v_cvt_pk_bf16_f32 v150, v126, v127
	v_cvt_pk_bf16_f32 v151, v128, v129
	v_cvt_pk_bf16_f32 v152, v114, v115
	v_cvt_pk_bf16_f32 v153, v116, v117
	v_cvt_pk_bf16_f32 v154, v130, v131
	v_cvt_pk_bf16_f32 v155, v132, v133
	v_cvt_pk_bf16_f32 v156, v142, v143
	v_cvt_pk_bf16_f32 v157, v144, v145
	v_cvt_pk_bf16_f32 v158, v118, v119
	v_cvt_pk_bf16_f32 v159, v120, v121
	v_cvt_pk_bf16_f32 v160, v134, v135
	v_cvt_pk_bf16_f32 v161, v136, v137
	s_lshl_b32 s38, s4, 14
	v_add_u32_e32 v164, s38, v218
	v_add_u32_e32 v166, s38, v219
	ds_read_b128 v[114:117], v164 offset:36864
	ds_read_b128 v[118:121], v164 offset:38912
	ds_read_b128 v[122:125], v166 offset:36864
	ds_read_b128 v[126:129], v166 offset:38912
	ds_read_b128 v[130:133], v164 offset:40960
	ds_read_b128 v[134:137], v164 offset:43008
	ds_read_b128 v[138:141], v166 offset:40960
	ds_read_b128 v[142:145], v166 offset:43008
	s_lshl_b32 s38, s5, 13
	s_add_i32 s38, s38, s16
	s_mov_b32 m0, s38
	s_nop 0
	global_load_lds_dwordx4 v[210:211], off
	s_min_u32 s38, s42, 3
	s_lshl_b32 s38, s38, 7
	s_lshl_b32 s43, s31, 14
	v_lshl_add_u64 v[162:163], v[204:205], 0, s[38:39]
	s_add_i32 s43, s43, s29
	s_mov_b32 m0, s43
	s_nop 0
	global_load_lds_dwordx4 v[162:163], off
	v_lshl_add_u64 v[162:163], v[206:207], 0, s[38:39]
	s_add_i32 s38, s43, 0x2000
	s_mov_b32 m0, s38
	s_nop 0
	global_load_lds_dwordx4 v[162:163], off
	s_waitcnt lgkmcnt(7)
	v_mfma_f32_16x16x32_bf16 v[78:81], v[114:117], v[146:149], v[78:81]
	v_mfma_f32_16x16x32_bf16 v[74:77], v[114:117], v[150:153], v[74:77]
	s_waitcnt lgkmcnt(6)
	v_mfma_f32_16x16x32_bf16 v[70:73], v[118:121], v[146:149], v[70:73]
	v_mfma_f32_16x16x32_bf16 v[66:69], v[118:121], v[150:153], v[66:69]
	s_waitcnt lgkmcnt(3)
	v_mfma_f32_16x16x32_bf16 v[54:57], v[130:133], v[146:149], v[54:57]
	v_mfma_f32_16x16x32_bf16 v[50:53], v[130:133], v[150:153], v[50:53]
	s_waitcnt lgkmcnt(2)
	v_mfma_f32_16x16x32_bf16 v[46:49], v[134:137], v[146:149], v[46:49]
	v_mfma_f32_16x16x32_bf16 v[42:45], v[134:137], v[150:153], v[42:45]
	v_mfma_f32_16x16x32_bf16 v[78:81], v[122:125], v[154:157], v[78:81]
	v_mfma_f32_16x16x32_bf16 v[74:77], v[122:125], v[158:161], v[74:77]
	v_mfma_f32_16x16x32_bf16 v[70:73], v[126:129], v[154:157], v[70:73]
	v_mfma_f32_16x16x32_bf16 v[66:69], v[126:129], v[158:161], v[66:69]
	s_waitcnt lgkmcnt(1)
	v_mfma_f32_16x16x32_bf16 v[54:57], v[138:141], v[154:157], v[54:57]
	v_mfma_f32_16x16x32_bf16 v[50:53], v[138:141], v[158:161], v[50:53]
	s_waitcnt lgkmcnt(0)
	v_mfma_f32_16x16x32_bf16 v[46:49], v[142:145], v[154:157], v[46:49]
	v_mfma_f32_16x16x32_bf16 v[42:45], v[142:145], v[158:161], v[42:45]
	ds_read_b128 v[186:189], v164 offset:45056
	ds_read_b128 v[174:177], v164 offset:47104
	ds_read_b128 v[190:193], v166 offset:45056
	ds_read_b128 v[178:181], v166 offset:47104
	ds_read_b128 v[170:173], v164 offset:49152
	ds_read_b128 v[162:165], v164 offset:51200
	ds_read_b128 v[182:185], v166 offset:49152
	ds_read_b128 v[166:169], v166 offset:51200
	v_mfma_f32_16x16x32_bf16 v[114:117], v[82:85], v[10:13], 0
	v_mfma_f32_16x16x32_bf16 v[118:121], v[82:85], v[58:61], 0
	v_mfma_f32_16x16x32_bf16 v[138:141], v[90:93], v[2:5], v[114:117]
	v_mfma_f32_16x16x32_bf16 v[126:129], v[90:93], v[62:65], v[118:121]
	v_mfma_f32_16x16x32_bf16 v[114:117], v[86:89], v[10:13], 0
	v_mfma_f32_16x16x32_bf16 v[118:121], v[86:89], v[58:61], 0
	v_mfma_f32_16x16x32_bf16 v[122:125], v[94:97], v[2:5], v[114:117]
	v_mfma_f32_16x16x32_bf16 v[114:117], v[94:97], v[62:65], v[118:121]
	v_mfma_f32_16x16x32_bf16 v[118:121], v[98:101], v[10:13], 0
	v_mfma_f32_16x16x32_bf16 v[134:137], v[98:101], v[58:61], 0
	v_mfma_f32_16x16x32_bf16 v[130:133], v[106:109], v[2:5], v[118:121]
	v_mfma_f32_16x16x32_bf16 v[118:121], v[106:109], v[62:65], v[134:137]
	v_mfma_f32_16x16x32_bf16 v[134:137], v[102:105], v[10:13], 0
	v_mfma_f32_16x16x32_bf16 v[236:239], v[102:105], v[58:61], 0
	v_mfma_f32_16x16x32_bf16 v[142:145], v[110:113], v[2:5], v[134:137]
	v_mfma_f32_16x16x32_bf16 v[134:137], v[110:113], v[62:65], v[236:239]
	s_andn2_b64 vcc, exec, s[6:7]
	s_cbranch_vccnz .LBB0_976
; #define ATT_SB() __builtin_amdgcn_sched_barrier(0)
; #define ATT_KLOAD(sl) do { _Pragma("unroll") for (int kb_ = 0; kb_ < NKW; ++kb_) _Pragma("unroll") for (int ds_ = 0; ds_ < NDS; ++ds_) { \
;         if (ds_ < 2) kf[kb_ * NDS + ds_] = *(const LAS bf16x8*)(kp[ds_ & 1] + (sl) * KSLOT + (kb_ & 1) * 512 + (kb_ >> 1) * 4096); \
;         else kf[kb_ * NDS + ds_] = *(const LAS bf16x8*)(krp + (sl) * KSLOT + (kb_ & 1) * 256 + (kb_ >> 1) * 2048); } } while (0)
; #define ATT_QK() do { _Pragma("unroll") for (int kb_ = 0; kb_ < NKW; ++kb_) _Pragma("unroll") for (int ds_ = 0; ds_ < NDS; ++ds_) _Pragma("unroll") for (int qb_ = 0; qb_ < NQB; ++qb_) \
;         c[kb_][qb_] = __builtin_amdgcn_mfma_f32_16x16x32_bf16(kf[kb_ * NDS + ds_], qf[qb_ * NDS + ds_], ds_ == 0 ? zero4 : c[kb_][qb_], 0, 0, 0); } while (0)
; #define ATT_VLOAD(sl, h_) do { _Pragma("unroll") for (int g_ = 0; g_ < NVF; ++g_) { \
;         if constexpr (KS) vf[g_] = *(const LAS bf16x8*)(vpk + (sl) * VSLOT + g_ * 2048); \
;         else vf[g_] = *(const LAS bf16x8*)(vp[g_ & 1] + (sl) * VSLOT + ((h_) * 4 + (g_ >> 1)) * 2048); } } while (0)
; #define ATT_PVP(h_) do { _Pragma("unroll") for (int g_ = 0; g_ < NVF; ++g_) _Pragma("unroll") for (int qb_ = 0; qb_ < NQB; ++qb_) { \
;         const int db_ = KS ? g_ : (h_) * 4 + (g_ >> 1), sq_ = KS ? 0 : (g_ & 1); \
;         o[db_][qb_] = __builtin_amdgcn_mfma_f32_16x16x32_bf16(vf[g_], __builtin_bit_cast(bf16x8, pw[sq_ * NQB + qb_]), o[db_][qb_], 0, 0, 0); } } while (0)
; template <int DQK, int DV, bool LEAD> ...
;     ...
;         } else {
;             if constexpr (DV == 128) {
;                 ATT_PVP(0); ATT_SB();
;                 ATT_VLOAD(s_prev, 1); ATT_SB();
;                 ATT_QK(); ATT_SB();
;                 if (one_) { ATT_KLOAD(s_next); ATT_SB(); ATT_PVP(1); }
;                 ATT_SB();
	s_lshl_b32 s38, s31, 13
	v_add_u32_e32 v102, s38, v217
	v_add_u32_e32 v110, s38, v220
	ds_read_b128 v[82:85], v102
	ds_read_b128 v[86:89], v102 offset:512
	ds_read_b128 v[90:93], v110
	ds_read_b128 v[94:97], v110 offset:512
	ds_read_b128 v[98:101], v102 offset:4096
	ds_read_b128 v[102:105], v102 offset:4608
	ds_read_b128 v[106:109], v110 offset:4096
	ds_read_b128 v[110:113], v110 offset:4608
	s_waitcnt lgkmcnt(14)
	v_mfma_f32_16x16x32_bf16 v[38:41], v[186:189], v[146:149], v[38:41]
	v_mfma_f32_16x16x32_bf16 v[34:37], v[186:189], v[150:153], v[34:37]
	v_mfma_f32_16x16x32_bf16 v[30:33], v[174:177], v[146:149], v[30:33]
	v_mfma_f32_16x16x32_bf16 v[26:29], v[174:177], v[150:153], v[26:29]
	s_waitcnt lgkmcnt(11)
	v_mfma_f32_16x16x32_bf16 v[22:25], v[170:173], v[146:149], v[22:25]
	v_mfma_f32_16x16x32_bf16 v[18:21], v[170:173], v[150:153], v[18:21]
	s_waitcnt lgkmcnt(10)
	v_mfma_f32_16x16x32_bf16 v[14:17], v[162:165], v[146:149], v[14:17]
	v_mfma_f32_16x16x32_bf16 v[6:9], v[162:165], v[150:153], v[6:9]
	v_mfma_f32_16x16x32_bf16 v[38:41], v[190:193], v[154:157], v[38:41]
	v_mfma_f32_16x16x32_bf16 v[34:37], v[190:193], v[158:161], v[34:37]
	v_mfma_f32_16x16x32_bf16 v[30:33], v[178:181], v[154:157], v[30:33]
	v_mfma_f32_16x16x32_bf16 v[26:29], v[178:181], v[158:161], v[26:29]
	s_waitcnt lgkmcnt(9)
	v_mfma_f32_16x16x32_bf16 v[22:25], v[182:185], v[154:157], v[22:25]
	v_mfma_f32_16x16x32_bf16 v[18:21], v[182:185], v[158:161], v[18:21]
	s_waitcnt lgkmcnt(8)
	v_mfma_f32_16x16x32_bf16 v[14:17], v[166:169], v[154:157], v[14:17]
	v_mfma_f32_16x16x32_bf16 v[6:9], v[166:169], v[158:161], v[6:9]

; #define ATT_DMA_K(t, sl) do { glds16(ksrc + (size_t)(t) * 64 * kpitch, (unsigned)__builtin_amdgcn_readfirstlane(kdst + (sl) * KSLOT)); \
;         if constexpr (DQK == 96) glds16(krsrc + (size_t)(t) * 64 * 32, (unsigned)__builtin_amdgcn_readfirstlane(krdst + (sl) * KSLOT)); } while (0)
; #define ATT_DMA_V(t, sl) do { glds16(vsrc + (size_t)(t) * 64, (unsigned)__builtin_amdgcn_readfirstlane(vdst + (sl) * VSLOT)); \
;         if constexpr (DV == 128) glds16(vsrc + (size_t)64 * NR + (size_t)(t) * 64, (unsigned)__builtin_amdgcn_readfirstlane(vdst + (sl) * VSLOT + 8192)); } while (0)
; template <int DQK, int DV, bool LEAD> ...
;     ...
;     ATT_DMA_K(0, 0); ATT_DMA_V(0, 0); ATT_DMA_K(1, 1); ATT_DMA_K(2, 2);
;     bf16x8 qf[NQB * NDS];
;     {
;       const float c2 = (DQK == 64) ? C2_EVEN : C2_ODD; const bool lat = tq0 >= 0;
; #pragma unroll
;       for (int qb = 0; qb < NQB; ++qb) {
;           const bf16_t* qp = Q + (size_t)(qrow0 + qoff + qb * 16 + q16) * qpitch + g4 * 8;
;           bf16x8 raw[NDS];
; #pragma unroll
;           for (int ds = 0; ds < NDS; ++ds) raw[ds] = *(const bf16x8*)(qp + ds * 32);
;           float x[NDS][8];
; #pragma unroll
;           for (int ds = 0; ds < NDS; ++ds)
; #pragma unroll
;               for (int j = 0; j < 8; ++j) x[ds][j] = __uint_as_float(((unsigned)(unsigned short)raw[ds][j]) << 16);
;           const int tq = tq0 + qoff + qb * 16 + q16, prow = (tq >> 6) & 127, pcol = tq & 63;
;           float sn = 0.f;
; #pragma unroll
;           for (int ds = 0; ds < 2; ++ds)
; #pragma unroll
;               for (int j = 0; j < 8; ++j) sn += x[ds][j] * x[ds][j];
;           sn = lanes4_sum(sn);
;           const float rn = rsqrtf(sn * (1.f / 64.f) + EPS);
.LBB0_979:
	v_mov_b32_e32 v37, v0
	s_ashr_i32 s29, s28, 31
	v_readfirstlane_b32 s4, v37
	s_ashr_i32 s7, s4, 6
	v_bfe_u32 v1, v37, 3, 3
	v_lshl_or_b32 v6, s7, 3, v1
	s_lshl_b32 s5, s7, 1
	s_lshr_b32 s4, s4, 5
	v_ashrrev_i32_e32 v2, 1, v6
	s_and_b32 s5, s5, 2
	s_and_b32 s4, s4, 4
	v_and_b32_e32 v170, 7, v37
	v_and_b32_e32 v3, 1, v2
	s_or_b32 s4, s5, s4
	v_bitop3_b32 v7, s4, v170, v3 bitop3:0x36
	v_xor_b32_e32 v8, v2, v37
	v_add_u32_e32 v4, s28, v6
	s_lshl_b32 s4, s7, 10
	v_mov_b64_e32 v[2:3], s[36:37]
	s_add_i32 s25, s4, 0
	v_mad_i64_i32 v[2:3], s[4:5], v4, s92, v[2:3]
	v_mov_b64_e32 v[4:5], s[40:41]
	v_lshlrev_b32_e32 v194, 4, v7
	v_mad_i64_i32 v[4:5], s[4:5], v6, s91, v[4:5]
	v_lshl_add_u64 v[22:23], v[2:3], 0, v[194:195]
	v_lshlrev_b32_e32 v2, 4, v8
	v_lshl_add_u64 v[4:5], s[28:29], 1, v[4:5]
	v_and_b32_e32 v194, 0x70, v2
	s_mov_b32 m0, s25
	s_nop 0
	global_load_lds_dwordx4 v[22:23], off
	v_lshl_add_u64 v[162:163], v[4:5], 0, v[194:195]
	s_add_i32 s29, s25, 0x9000
	s_mov_b32 m0, s29
	s_nop 0
	global_load_lds_dwordx4 v[162:163], off
	s_mov_b64 s[4:5], 0x840000
	v_lshl_add_u64 v[164:165], v[162:163], 0, s[4:5]
	s_add_i32 s4, s29, 0x2000
	s_mov_b32 m0, s4
	s_nop 0
	global_load_lds_dwordx4 v[164:165], off
	s_mov_b64 s[4:5], 0x38000
	s_lshl_b32 s6, s7, 5
	v_lshl_add_u64 v[2:3], v[22:23], 0, s[4:5]
	s_add_i32 s4, s25, 0x2000
	s_mov_b32 m0, s4
	s_nop 0
	global_load_lds_dwordx4 v[2:3], off
	v_and_b32_e32 v36, 15, v37
	s_mov_b64 s[4:5], 0x70000
	s_add_i32 s6, s6, s28
	v_and_b32_e32 v194, 48, v37
	v_lshl_add_u64 v[2:3], v[22:23], 0, s[4:5]
	s_add_i32 s4, s25, 0x4000
	v_or_b32_e32 v8, s6, v36
	v_lshl_add_u64 v[6:7], s[26:27], 0, v[194:195]
	s_mov_b32 m0, s4
	s_nop 0
	global_load_lds_dwordx4 v[2:3], off
	v_bfe_u32 v171, v37, 4, 2
	v_mad_i64_i32 v[10:11], s[4:5], v8, s92, v[6:7]
	v_or_b32_e32 v8, 16, v8
	v_mad_i64_i32 v[12:13], s[4:5], v8, s92, v[6:7]
	global_load_dwordx4 v[2:5], v[10:11], off offset:64
	global_load_dwordx4 v[6:9], v[12:13], off offset:64
	global_load_dwordx4 v[38:41], v[10:11], off
	global_load_dwordx4 v[42:45], v[12:13], off
	v_lshlrev_b32_e32 v172, 1, v37
	v_and_b32_e32 v10, 3, v37
	v_lshrrev_b32_e32 v11, 1, v37
	v_and_or_b32 v10, v172, 24, v10
	v_lshlrev_b32_e32 v62, 5, v171
	v_bitop3_b32 v60, v171, v11, 7 bitop3:0x78
	v_lshl_add_u32 v63, v10, 7, 0
	global_load_dwordx4 v[10:13], v62, s[22:23] offset:144
	global_load_dwordx4 v[14:17], v62, s[22:23] offset:128
	global_load_dwordx4 v[18:21], v62, s[22:23] offset:16
	s_mov_b32 s4, 0x3c800000
	v_and_b32_e32 v61, 63, v37
	v_lshlrev_b32_e32 v64, 4, v60
	v_add_u32_e32 v175, v63, v64
	v_lshlrev_b32_e32 v174, 7, v36
	v_lshl_add_u64 v[168:169], v[22:23], 0, s[96:97]
	v_lshl_add_u64 v[22:23], v[162:163], 0, s[66:67]
	s_mov_b32 s16, 2
	v_or_b32_e32 v173, 4, v171
	s_waitcnt vmcnt(5)
	v_and_b32_e32 v25, 0xffff0000, v9
	s_waitcnt vmcnt(4)
	v_and_b32_e32 v57, 0xffff0000, v38
	v_and_b32_e32 v51, 0xffff0000, v2
	v_lshlrev_b32_e32 v50, 16, v2
	v_lshlrev_b32_e32 v56, 16, v38
	v_mul_f32_e32 v2, v57, v57
	v_lshlrev_b32_e32 v24, 16, v9
	v_and_b32_e32 v27, 0xffff0000, v8
	v_lshlrev_b32_e32 v26, 16, v8
	v_and_b32_e32 v9, 0xffff0000, v3
	v_lshlrev_b32_e32 v8, 16, v3
	s_waitcnt vmcnt(3)
	v_and_b32_e32 v33, 0xffff0000, v45
	v_lshlrev_b32_e32 v32, 16, v45
	v_and_b32_e32 v35, 0xffff0000, v44
	v_lshlrev_b32_e32 v34, 16, v44
	v_and_b32_e32 v45, 0xffff0000, v39
	v_lshlrev_b32_e32 v44, 16, v39
	v_pk_fma_f32 v[2:3], v[56:57], v[56:57], v[2:3] op_sel_hi:[1,1,0]
	v_and_b32_e32 v49, 0xffff0000, v4
	v_lshlrev_b32_e32 v48, 16, v4
	v_pk_fma_f32 v[2:3], v[44:45], v[44:45], v[2:3]
	v_mul_f32_e32 v4, v45, v45
	v_and_b32_e32 v53, 0xffff0000, v40
	v_lshlrev_b32_e32 v52, 16, v40
	v_pk_add_f32 v[2:3], v[4:5], v[2:3] op_sel_hi:[0,1]
	v_pk_fma_f32 v[2:3], v[52:53], v[52:53], v[2:3]
	v_mul_f32_e32 v4, v53, v53
	v_and_b32_e32 v29, 0xffff0000, v7
	v_lshlrev_b32_e32 v28, 16, v7
	v_and_b32_e32 v31, 0xffff0000, v6
	v_lshlrev_b32_e32 v30, 16, v6
	v_and_b32_e32 v7, 0xffff0000, v41
	v_lshlrev_b32_e32 v6, 16, v41
	v_pk_add_f32 v[2:3], v[4:5], v[2:3] op_sel_hi:[0,1]
	v_pk_fma_f32 v[2:3], v[6:7], v[6:7], v[2:3]
	v_mul_f32_e32 v4, v7, v7
	v_pk_add_f32 v[2:3], v[4:5], v[2:3] op_sel_hi:[0,1]
	v_pk_fma_f32 v[2:3], v[50:51], v[50:51], v[2:3]
	v_mul_f32_e32 v4, v51, v51
	v_pk_add_f32 v[2:3], v[4:5], v[2:3] op_sel_hi:[0,1]
	v_pk_fma_f32 v[2:3], v[8:9], v[8:9], v[2:3]
	v_mul_f32_e32 v4, v9, v9
	v_pk_add_f32 v[2:3], v[4:5], v[2:3] op_sel_hi:[0,1]
	v_pk_fma_f32 v[2:3], v[48:49], v[48:49], v[2:3]
	v_mul_f32_e32 v4, v49, v49
	v_and_b32_e32 v47, 0xffff0000, v5
	v_lshlrev_b32_e32 v46, 16, v5
	v_pk_add_f32 v[2:3], v[4:5], v[2:3] op_sel_hi:[0,1]
	v_pk_fma_f32 v[2:3], v[46:47], v[46:47], v[2:3]
	v_mul_f32_e32 v4, v47, v47
	v_pk_add_f32 v[2:3], v[4:5], v[2:3] op_sel_hi:[0,1]
	v_mov_b32_e32 v3, v2
	s_nop 1
	v_permlane16_swap_b32_e32 v2, v3
	v_add_f32_e32 v3, v2, v3
	v_and_b32_e32 v55, 0xffff0000, v43
	v_lshlrev_b32_e32 v54, 16, v43
	v_mov_b32_e32 v5, v3
	v_and_b32_e32 v43, 0xffff0000, v42
	s_nop 0
	v_permlane32_swap_b32_e32 v3, v5
	v_lshlrev_b32_e32 v42, 16, v42
	v_mul_f32_e32 v2, v43, v43
	v_pk_fma_f32 v[38:39], v[42:43], v[42:43], v[2:3] op_sel_hi:[1,1,0]
	v_mul_f32_e32 v2, v55, v55
	v_pk_fma_f32 v[38:39], v[54:55], v[54:55], v[38:39]
	s_nop 0
	v_pk_add_f32 v[38:39], v[2:3], v[38:39] op_sel_hi:[0,1]
	v_pk_fma_f32 v[38:39], v[34:35], v[34:35], v[38:39]
	v_mul_f32_e32 v2, v35, v35
	v_pk_add_f32 v[38:39], v[2:3], v[38:39] op_sel_hi:[0,1]
	v_pk_fma_f32 v[38:39], v[32:33], v[32:33], v[38:39]
	v_mul_f32_e32 v2, v33, v33
	v_pk_add_f32 v[38:39], v[2:3], v[38:39] op_sel_hi:[0,1]
	v_pk_fma_f32 v[38:39], v[30:31], v[30:31], v[38:39]
	v_mul_f32_e32 v2, v31, v31
	v_pk_add_f32 v[38:39], v[2:3], v[38:39] op_sel_hi:[0,1]
	v_pk_fma_f32 v[38:39], v[28:29], v[28:29], v[38:39]
	v_mul_f32_e32 v2, v29, v29
	v_pk_add_f32 v[38:39], v[2:3], v[38:39] op_sel_hi:[0,1]
	v_pk_fma_f32 v[38:39], v[26:27], v[26:27], v[38:39]
	v_mul_f32_e32 v2, v27, v27
	v_pk_add_f32 v[38:39], v[2:3], v[38:39] op_sel_hi:[0,1]
	v_pk_fma_f32 v[38:39], v[24:25], v[24:25], v[38:39]
	v_mul_f32_e32 v2, v25, v25
	v_pk_add_f32 v[38:39], v[2:3], v[38:39] op_sel_hi:[0,1]
	v_mov_b32_e32 v2, v38
	s_nop 1
	v_permlane16_swap_b32_e32 v38, v2
	v_add_f32_e32 v2, v38, v2
	global_load_dwordx4 v[38:41], v62, s[22:23]
	v_mov_b32_e32 v4, v2
	s_nop 1
	v_permlane32_swap_b32_e32 v2, v4
	v_pk_add_f32 v[2:3], v[2:3], v[4:5]
	s_mov_b32 s22, 1
	v_pk_fma_f32 v[58:59], v[2:3], s[4:5], v[196:197] op_sel_hi:[1,0,0]
	s_mov_b32 s23, 0
	v_mul_f32_e32 v2, 0x4b800000, v59
	v_cmp_gt_f32_e32 vcc, s95, v59
	v_cmp_gt_f32_e64 s[4:5], s95, v58
	s_nop 0
	v_cndmask_b32_e32 v2, v59, v2, vcc
	v_rsq_f32_e32 v2, v2
	s_nop 0
	v_mul_f32_e32 v3, 0x45800000, v2
	v_cndmask_b32_e32 v60, v2, v3, vcc
	s_waitcnt vmcnt(3)
; __device__ __forceinline__ unsigned cvtpk(float lo, float hi) { f32x2 v = {lo, hi}; bf16x2_t b = __builtin_convertvector(v, bf16x2_t); return __builtin_bit_cast(unsigned, b); }
; template <int DQK, int DV, bool LEAD> ...
;     ...
; #pragma unroll
;           for (int ds = 0; ds < 2; ++ds)
; #pragma unroll
;               for (int j = 0; j < 8; ++j) x[ds][j] *= rn * qgain[32 * ds + 8 * g4 + j];
;           if constexpr (DQK == 64) {
; #pragma unroll
;               for (int ds = 0; ds < 2; ++ds)
; #pragma unroll
;                   for (int j = 0; j < 8; ++j) {
;                       auto rr = __builtin_amdgcn_permlane32_swap(__float_as_uint(x[ds][j]), __float_as_uint(x[ds][j]), false, false);
;                       const float other = hi ? __uint_as_float(rr[0]) : __uint_as_float(rr[1]);
;                       float cc = 1.f, sg = 0.f;
;                       if (lat) { const f32x2 cs = rope[(ds ? pcol : prow) * 16 + 8 * (g4 & 1) + j]; cc = cs.x; sg = hi ? cs.y : -cs.y; }
;                       x[ds][j] = x[ds][j] * cc + other * sg; }
;           } else {
;               float sr = 0.f;
; #pragma unroll
;               for (int j = 0; j < 8; ++j) sr += x[2][j] * x[2][j];
;               sr = lanes4_sum(sr);
;               const float rq = rsqrtf(sr * (1.f / 32.f) + EPS);
; #pragma unroll
;               for (int j = 0; j < 8; ++j) { const float av = x[2][j] * rq * qgain[64 + 8 * g4 + j];
;                   auto rr = __builtin_amdgcn_permlane16_swap(__float_as_uint(av), __float_as_uint(av), false, false);
;                   const float other = (g4 & 1) ? __uint_as_float(rr[0]) : __uint_as_float(rr[1]);
;                   float cc = 1.f, sg = 0.f;
;                   if (lat) { const f32x2 cs = rope[((g4 & 2) ? pcol : prow) * 8 + j]; cc = cs.x; sg = (g4 & 1) ? cs.y : -cs.y; }
;                   x[2][j] = av * cc + other * sg; }
;           }
; #pragma unroll
;           for (int ds = 0; ds < NDS; ++ds) { u32x4 w;
; #pragma unroll
;               for (int i = 0; i < 4; ++i) w[i] = cvtpk(x[ds][2 * i] * c2, x[ds][2 * i + 1] * c2);
;               qf[qb * NDS + ds] = __builtin_bit_cast(bf16x8, w); }
	v_pk_mul_f32 v[2:3], v[60:61], v[12:13] op_sel_hi:[0,1]
	v_pk_mul_f32 v[2:3], v[2:3], v[46:47]
	v_cmp_gt_u32_e32 vcc, 32, v61
	v_mov_b32_e32 v4, v2
	v_mov_b32_e32 v46, v2
	v_mov_b32_e32 v5, v3
	v_mov_b32_e32 v47, v3
	v_permlane32_swap_b32_e32 v4, v46
	s_nop 0
	v_permlane32_swap_b32_e32 v5, v47
	v_cndmask_b32_e32 v5, v5, v47, vcc
	v_cndmask_b32_e32 v4, v4, v46, vcc
	v_pk_fma_f32 v[2:3], v[4:5], 0, v[2:3] op_sel_hi:[1,0,1]
	s_nop 0
	v_pk_mul_f32 v[2:3], v[2:3], s[94:95] op_sel_hi:[1,0]
	s_nop 0
	v_cvt_pk_bf16_f32 v5, v2, v3
	v_pk_mul_f32 v[2:3], v[60:61], v[10:11] op_sel_hi:[0,1]
	v_pk_mul_f32 v[2:3], v[2:3], v[48:49]
	s_nop 0
	v_mov_b32_e32 v4, v2
	v_mov_b32_e32 v46, v2
	v_mov_b32_e32 v47, v3
	v_mov_b32_e32 v48, v3
	v_permlane32_swap_b32_e32 v4, v46
	s_nop 0
	v_permlane32_swap_b32_e32 v47, v48
	v_cndmask_b32_e32 v47, v47, v48, vcc
	v_cndmask_b32_e32 v46, v4, v46, vcc
	v_pk_fma_f32 v[2:3], v[46:47], 0, v[2:3] op_sel_hi:[1,0,1]
	s_nop 0
	v_pk_mul_f32 v[2:3], v[2:3], s[94:95] op_sel_hi:[1,0]
	s_nop 0
	v_cvt_pk_bf16_f32 v4, v2, v3
	s_waitcnt vmcnt(2)
	v_pk_mul_f32 v[2:3], v[60:61], v[16:17] op_sel_hi:[0,1]
	v_pk_mul_f32 v[2:3], v[2:3], v[8:9]
	s_nop 0
	v_mov_b32_e32 v8, v2
	v_mov_b32_e32 v46, v2
	v_mov_b32_e32 v9, v3
	v_mov_b32_e32 v47, v3
	v_permlane32_swap_b32_e32 v8, v46
	s_nop 0
	v_permlane32_swap_b32_e32 v9, v47
	v_cndmask_b32_e32 v9, v9, v47, vcc
	v_cndmask_b32_e32 v8, v8, v46, vcc
	v_pk_fma_f32 v[2:3], v[8:9], 0, v[2:3] op_sel_hi:[1,0,1]
	v_pk_mul_f32 v[8:9], v[14:15], v[60:61] op_sel_hi:[1,0]
	v_pk_mul_f32 v[2:3], v[2:3], s[94:95] op_sel_hi:[1,0]
	v_pk_mul_f32 v[8:9], v[8:9], v[50:51]
	v_cvt_pk_bf16_f32 v3, v2, v3
	v_mov_b32_e32 v2, v8
	v_mov_b32_e32 v46, v8
	v_mov_b32_e32 v47, v9
	v_mov_b32_e32 v48, v9
	v_permlane32_swap_b32_e32 v2, v46
	s_nop 0
	v_permlane32_swap_b32_e32 v47, v48
	v_cndmask_b32_e32 v47, v47, v48, vcc
	v_cndmask_b32_e32 v46, v2, v46, vcc
	v_pk_fma_f32 v[8:9], v[46:47], 0, v[8:9] op_sel_hi:[1,0,1]
	s_nop 0
	v_pk_mul_f32 v[8:9], v[8:9], s[94:95] op_sel_hi:[1,0]
	s_nop 0
	v_cvt_pk_bf16_f32 v2, v8, v9
	s_waitcnt vmcnt(1)
	v_pk_mul_f32 v[8:9], v[20:21], v[60:61] op_sel_hi:[1,0]
	s_nop 0
	v_pk_mul_f32 v[6:7], v[8:9], v[6:7]
	s_nop 0
	v_mov_b32_e32 v8, v6
	v_mov_b32_e32 v46, v6
	v_mov_b32_e32 v9, v7
	v_mov_b32_e32 v47, v7
	v_permlane32_swap_b32_e32 v8, v46
	s_nop 0
	v_permlane32_swap_b32_e32 v9, v47
	v_cndmask_b32_e32 v9, v9, v47, vcc
	v_cndmask_b32_e32 v8, v8, v46, vcc
	v_pk_fma_f32 v[6:7], v[8:9], 0, v[6:7] op_sel_hi:[1,0,1]
	s_nop 0
	v_pk_mul_f32 v[6:7], v[6:7], s[94:95] op_sel_hi:[1,0]
	s_nop 0
	v_cvt_pk_bf16_f32 v9, v6, v7
	v_pk_mul_f32 v[6:7], v[18:19], v[60:61] op_sel_hi:[1,0]
	s_nop 0
	v_pk_mul_f32 v[6:7], v[6:7], v[52:53]
	s_nop 0
	v_mov_b32_e32 v8, v6
	v_mov_b32_e32 v46, v6
	v_mov_b32_e32 v47, v7
	v_mov_b32_e32 v48, v7
	v_permlane32_swap_b32_e32 v8, v46
	s_nop 0
	v_permlane32_swap_b32_e32 v47, v48
	v_cndmask_b32_e32 v47, v47, v48, vcc
	v_cndmask_b32_e32 v46, v8, v46, vcc
	v_pk_fma_f32 v[6:7], v[46:47], 0, v[6:7] op_sel_hi:[1,0,1]
	s_nop 0
	v_pk_mul_f32 v[6:7], v[6:7], s[94:95] op_sel_hi:[1,0]
	s_nop 0
	v_cvt_pk_bf16_f32 v8, v6, v7
	s_waitcnt vmcnt(0)
	v_pk_mul_f32 v[6:7], v[40:41], v[60:61] op_sel_hi:[1,0]
	s_nop 0
	v_pk_mul_f32 v[6:7], v[6:7], v[44:45]
	s_nop 0
	v_mov_b32_e32 v44, v6
	v_mov_b32_e32 v46, v6
	v_mov_b32_e32 v45, v7
	v_mov_b32_e32 v47, v7
	v_permlane32_swap_b32_e32 v44, v46
	s_nop 0
	v_permlane32_swap_b32_e32 v45, v47
	v_cndmask_b32_e32 v45, v45, v47, vcc
	v_cndmask_b32_e32 v44, v44, v46, vcc
	v_pk_fma_f32 v[6:7], v[44:45], 0, v[6:7] op_sel_hi:[1,0,1]
	v_pk_mul_f32 v[44:45], v[38:39], v[60:61] op_sel_hi:[1,0]
	v_pk_mul_f32 v[6:7], v[6:7], s[94:95] op_sel_hi:[1,0]
	v_pk_mul_f32 v[44:45], v[44:45], v[56:57]
	v_cvt_pk_bf16_f32 v7, v6, v7
	v_mov_b32_e32 v6, v44
	v_mov_b32_e32 v46, v44
	s_nop 1
	v_permlane32_swap_b32_e32 v6, v46
	v_mov_b32_e32 v47, v45
	v_mov_b32_e32 v48, v45
	v_cndmask_b32_e32 v46, v6, v46, vcc
	v_mul_f32_e32 v6, 0x4b800000, v58
	v_permlane32_swap_b32_e32 v47, v48
	v_cndmask_b32_e64 v6, v58, v6, s[4:5]
	v_cndmask_b32_e32 v47, v47, v48, vcc
	v_rsq_f32_e32 v48, v6
	v_pk_fma_f32 v[44:45], v[46:47], 0, v[44:45] op_sel_hi:[1,0,1]
	s_nop 0
	v_pk_mul_f32 v[44:45], v[44:45], s[94:95] op_sel_hi:[1,0]
	s_nop 0
	v_cvt_pk_bf16_f32 v6, v44, v45
	v_mul_f32_e32 v44, 0x45800000, v48
	v_cndmask_b32_e64 v44, v48, v44, s[4:5]
	v_pk_mul_f32 v[38:39], v[38:39], v[44:45] op_sel_hi:[1,0]
	v_pk_mul_f32 v[10:11], v[10:11], v[44:45] op_sel_hi:[1,0]
	v_pk_mul_f32 v[38:39], v[38:39], v[42:43]
	v_pk_mul_f32 v[12:13], v[12:13], v[44:45] op_sel_hi:[1,0]
	v_pk_mul_f32 v[40:41], v[40:41], v[44:45] op_sel_hi:[1,0]
	v_pk_mul_f32 v[10:11], v[10:11], v[26:27]
	v_pk_mul_f32 v[12:13], v[12:13], v[24:25]
	v_mov_b32_e32 v24, v38
	v_mov_b32_e32 v26, v38
	v_mov_b32_e32 v25, v39
	v_mov_b32_e32 v27, v39
	v_pk_mul_f32 v[40:41], v[40:41], v[54:55]
	v_pk_mul_f32 v[16:17], v[16:17], v[44:45] op_sel_hi:[1,0]
	v_permlane32_swap_b32_e32 v24, v26
	v_permlane32_swap_b32_e32 v25, v27
	v_pk_mul_f32 v[18:19], v[18:19], v[44:45] op_sel_hi:[1,0]
	v_pk_mul_f32 v[16:17], v[16:17], v[28:29]
	v_cndmask_b32_e32 v25, v25, v27, vcc
	v_cndmask_b32_e32 v24, v24, v26, vcc
	v_mov_b32_e32 v26, v40
	v_mov_b32_e32 v28, v40
	v_mov_b32_e32 v27, v41
	v_mov_b32_e32 v29, v41
	v_pk_mul_f32 v[18:19], v[18:19], v[34:35]
	v_pk_mul_f32 v[14:15], v[14:15], v[44:45] op_sel_hi:[1,0]
	v_permlane32_swap_b32_e32 v26, v28
	v_permlane32_swap_b32_e32 v27, v29
	v_pk_mul_f32 v[14:15], v[14:15], v[30:31]
	v_cndmask_b32_e32 v27, v27, v29, vcc
	v_cndmask_b32_e32 v26, v26, v28, vcc
	v_mov_b32_e32 v28, v18
	v_mov_b32_e32 v30, v18
	v_mov_b32_e32 v29, v19
	v_mov_b32_e32 v31, v19
; __device__ __forceinline__ unsigned cvtpk(float lo, float hi) { f32x2 v = {lo, hi}; bf16x2_t b = __builtin_convertvector(v, bf16x2_t); return __builtin_bit_cast(unsigned, b); }
; #define ATT_KLOAD(sl) do { _Pragma("unroll") for (int kb_ = 0; kb_ < NKW; ++kb_) _Pragma("unroll") for (int ds_ = 0; ds_ < NDS; ++ds_) { \
;         if (ds_ < 2) kf[kb_ * NDS + ds_] = *(const LAS bf16x8*)(kp[ds_ & 1] + (sl) * KSLOT + (kb_ & 1) * 512 + (kb_ >> 1) * 4096); \
;         else kf[kb_ * NDS + ds_] = *(const LAS bf16x8*)(krp + (sl) * KSLOT + (kb_ & 1) * 256 + (kb_ >> 1) * 2048); } } while (0)
; template <int DQK, int DV, bool LEAD> ...
;     ...
; #pragma unroll
;           for (int ds = 0; ds < NDS; ++ds) { u32x4 w;
; #pragma unroll
;               for (int i = 0; i < 4; ++i) w[i] = cvtpk(x[ds][2 * i] * c2, x[ds][2 * i + 1] * c2);
;               qf[qb * NDS + ds] = __builtin_bit_cast(bf16x8, w); }
;       }
; #pragma unroll
;       for (int d0 = 0; d0 < NQB * NDS; ++d0) asm volatile("" : "+v"(qf[d0])); }
;     wait_bar<0>();
;     bf16x8 kf[NKW * NDS], vf[NVF];
;     ATT_KLOAD(0);
;     asm volatile("s_waitcnt lgkmcnt(0)\n\ts_barrier" ::: "memory");
	v_pk_mul_f32 v[20:21], v[20:21], v[44:45] op_sel_hi:[1,0]
	v_permlane32_swap_b32_e32 v28, v30
	v_permlane32_swap_b32_e32 v29, v31
	v_pk_mul_f32 v[20:21], v[20:21], v[32:33]
	v_cndmask_b32_e32 v29, v29, v31, vcc
	v_cndmask_b32_e32 v28, v28, v30, vcc
	v_pk_fma_f32 v[18:19], v[28:29], 0, v[18:19] op_sel_hi:[1,0,1]
	v_mov_b32_e32 v28, v20
	v_mov_b32_e32 v30, v20
	v_mov_b32_e32 v29, v21
	v_mov_b32_e32 v31, v21
	v_permlane32_swap_b32_e32 v28, v30
	s_nop 0
	v_permlane32_swap_b32_e32 v29, v31
	v_cndmask_b32_e32 v29, v29, v31, vcc
	v_cndmask_b32_e32 v28, v28, v30, vcc
	v_pk_fma_f32 v[20:21], v[28:29], 0, v[20:21] op_sel_hi:[1,0,1]
	v_mov_b32_e32 v28, v14
	v_mov_b32_e32 v30, v14
	v_mov_b32_e32 v29, v15
	v_mov_b32_e32 v31, v15
	v_permlane32_swap_b32_e32 v28, v30
	s_nop 0
	v_permlane32_swap_b32_e32 v29, v31
	v_cndmask_b32_e32 v29, v29, v31, vcc
	v_cndmask_b32_e32 v28, v28, v30, vcc
	v_pk_fma_f32 v[14:15], v[28:29], 0, v[14:15] op_sel_hi:[1,0,1]
	v_mov_b32_e32 v28, v16
	v_mov_b32_e32 v30, v16
	v_mov_b32_e32 v29, v17
	v_mov_b32_e32 v31, v17
	v_permlane32_swap_b32_e32 v28, v30
	s_nop 0
	v_permlane32_swap_b32_e32 v29, v31
	v_cndmask_b32_e32 v29, v29, v31, vcc
	v_cndmask_b32_e32 v28, v28, v30, vcc
	v_pk_fma_f32 v[16:17], v[28:29], 0, v[16:17] op_sel_hi:[1,0,1]
	v_mov_b32_e32 v28, v10
	v_mov_b32_e32 v30, v10
	v_mov_b32_e32 v29, v11
	v_mov_b32_e32 v31, v11
	v_permlane32_swap_b32_e32 v28, v30
	s_nop 0
	v_permlane32_swap_b32_e32 v29, v31
	v_cndmask_b32_e32 v29, v29, v31, vcc
	v_cndmask_b32_e32 v28, v28, v30, vcc
	v_pk_fma_f32 v[28:29], v[28:29], 0, v[10:11] op_sel_hi:[1,0,1]
	v_mov_b32_e32 v10, v12
	v_mov_b32_e32 v30, v12
	v_mov_b32_e32 v11, v13
	v_mov_b32_e32 v31, v13
	v_permlane32_swap_b32_e32 v10, v30
	s_nop 0
	v_permlane32_swap_b32_e32 v11, v31
	v_pk_fma_f32 v[24:25], v[24:25], 0, v[38:39] op_sel_hi:[1,0,1]
	v_pk_fma_f32 v[26:27], v[26:27], 0, v[40:41] op_sel_hi:[1,0,1]
	v_cndmask_b32_e32 v11, v11, v31, vcc
	v_cndmask_b32_e32 v10, v10, v30, vcc
	v_pk_fma_f32 v[30:31], v[10:11], 0, v[12:13] op_sel_hi:[1,0,1]
	v_pk_mul_f32 v[10:11], v[24:25], s[94:95] op_sel_hi:[1,0]
	v_pk_mul_f32 v[12:13], v[26:27], s[94:95] op_sel_hi:[1,0]
	v_cvt_pk_bf16_f32 v10, v10, v11
	v_cvt_pk_bf16_f32 v11, v12, v13
	v_pk_mul_f32 v[12:13], v[18:19], s[94:95] op_sel_hi:[1,0]
	v_pk_mul_f32 v[18:19], v[20:21], s[94:95] op_sel_hi:[1,0]
	v_pk_mul_f32 v[14:15], v[14:15], s[94:95] op_sel_hi:[1,0]
	v_pk_mul_f32 v[16:17], v[16:17], s[94:95] op_sel_hi:[1,0]
	v_cvt_pk_bf16_f32 v12, v12, v13
	v_cvt_pk_bf16_f32 v13, v18, v19
	v_cvt_pk_bf16_f32 v14, v14, v15
	v_cvt_pk_bf16_f32 v15, v16, v17
	v_pk_mul_f32 v[16:17], v[28:29], s[94:95] op_sel_hi:[1,0]
	v_pk_mul_f32 v[18:19], v[30:31], s[94:95] op_sel_hi:[1,0]
	v_cvt_pk_bf16_f32 v16, v16, v17
	v_cvt_pk_bf16_f32 v17, v18, v19
	s_waitcnt vmcnt(0) lgkmcnt(0)
	s_barrier
	ds_read_b128 v[18:21], v175
	ds_read_b128 v[24:27], v175 offset:512
	v_bfe_u32 v32, v37, 1, 3
	v_bitop3_b32 v32, v171, v32, 4 bitop3:0x36
	v_lshlrev_b32_e32 v37, 4, v32
	v_add_u32_e32 v178, v63, v37
	s_waitcnt lgkmcnt(1)
	v_mfma_f32_16x16x32_bf16 v[28:31], v[18:21], v[6:9], 0
	ds_read_b128 v[32:35], v178
	ds_read_b128 v[38:41], v178 offset:512
	v_mfma_f32_16x16x32_bf16 v[18:21], v[18:21], v[10:13], 0
	s_waitcnt lgkmcnt(1)
	v_mfma_f32_16x16x32_bf16 v[42:45], v[32:35], v[2:5], v[28:31]
	v_mfma_f32_16x16x32_bf16 v[28:31], v[24:27], v[6:9], 0
	v_mfma_f32_16x16x32_bf16 v[24:27], v[24:27], v[10:13], 0
	v_mfma_f32_16x16x32_bf16 v[18:21], v[32:35], v[14:17], v[18:21]
	s_waitcnt lgkmcnt(0)
	v_mfma_f32_16x16x32_bf16 v[30:33], v[38:41], v[2:5], v[28:31]
	v_mfma_f32_16x16x32_bf16 v[58:61], v[38:41], v[14:17], v[24:27]
	s_nop 3
	ds_read_b128 v[24:27], v175 offset:4096
	ds_read_b128 v[38:41], v175 offset:4608
	ds_read_b128 v[50:53], v178 offset:4096
	ds_read_b128 v[54:57], v178 offset:4608
	s_waitcnt lgkmcnt(3)
	v_mfma_f32_16x16x32_bf16 v[46:49], v[24:27], v[6:9], 0
	v_add_u32_e32 v28, 0, v174
	v_add_u32_e32 v177, v28, v37
	s_waitcnt lgkmcnt(0)
	s_barrier
; #define ATT_SB() __builtin_amdgcn_sched_barrier(0)
; #define ATT_DMA_K(t, sl) do { glds16(ksrc + (size_t)(t) * 64 * kpitch, (unsigned)__builtin_amdgcn_readfirstlane(kdst + (sl) * KSLOT)); \
;         if constexpr (DQK == 96) glds16(krsrc + (size_t)(t) * 64 * 32, (unsigned)__builtin_amdgcn_readfirstlane(krdst + (sl) * KSLOT)); } while (0)
; #define ATT_DMA_V(t, sl) do { glds16(vsrc + (size_t)(t) * 64, (unsigned)__builtin_amdgcn_readfirstlane(vdst + (sl) * VSLOT)); \
;         if constexpr (DV == 128) glds16(vsrc + (size_t)64 * NR + (size_t)(t) * 64, (unsigned)__builtin_amdgcn_readfirstlane(vdst + (sl) * VSLOT + 8192)); } while (0)
; #define ATT_KLOAD(sl) do { _Pragma("unroll") for (int kb_ = 0; kb_ < NKW; ++kb_) _Pragma("unroll") for (int ds_ = 0; ds_ < NDS; ++ds_) { \
;         if (ds_ < 2) kf[kb_ * NDS + ds_] = *(const LAS bf16x8*)(kp[ds_ & 1] + (sl) * KSLOT + (kb_ & 1) * 512 + (kb_ >> 1) * 4096); \
;         else kf[kb_ * NDS + ds_] = *(const LAS bf16x8*)(krp + (sl) * KSLOT + (kb_ & 1) * 256 + (kb_ >> 1) * 2048); } } while (0)
; #define ATT_QK() do { _Pragma("unroll") for (int kb_ = 0; kb_ < NKW; ++kb_) _Pragma("unroll") for (int ds_ = 0; ds_ < NDS; ++ds_) _Pragma("unroll") for (int qb_ = 0; qb_ < NQB; ++qb_) \
;         c[kb_][qb_] = __builtin_amdgcn_mfma_f32_16x16x32_bf16(kf[kb_ * NDS + ds_], qf[qb_ * NDS + ds_], ds_ == 0 ? zero4 : c[kb_][qb_], 0, 0, 0); } while (0)
; #define ATT_EXP() do { _Pragma("unroll") for (int kb_ = 0; kb_ < NKW; ++kb_) _Pragma("unroll") for (int qb_ = 0; qb_ < NQB; ++qb_) _Pragma("unroll") for (int i_ = 0; i_ < 4; ++i_) \
;         c[kb_][qb_][i_] = __builtin_amdgcn_exp2f(c[kb_][qb_][i_]); } while (0)
; template <int DQK, int DV, bool LEAD> ...
;     ...
;     ATT_DMA_K(3, 0); ATT_DMA_V(1, 1);
;     ATT_QK(); ATT_SB();
;     ATT_KLOAD(1); ATT_SB();
;     if constexpr (LEAD) { ATT_EXP(); ATT_SUMPACK(); }
;     wait_bar<NDMA>();
;     int s_prev = 0, s_cur = 1, s_next = 2;
	v_mfma_f32_16x16x32_bf16 v[24:27], v[24:27], v[10:13], 0
	s_mov_b32 m0, s25
	s_nop 0
	global_load_lds_dwordx4 v[168:169], off
	s_add_i32 s4, s29, 0x4000
	s_mov_b32 m0, s4
	s_nop 0
	global_load_lds_dwordx4 v[22:23], off
	s_waitcnt lgkmcnt(1)
	v_mfma_f32_16x16x32_bf16 v[74:77], v[50:53], v[14:17], v[24:27]
	s_mov_b64 s[4:5], 0x840080
	v_add_u32_e32 v176, v28, v64
	v_lshl_add_u64 v[28:29], v[162:163], 0, s[4:5]
	v_mfma_f32_16x16x32_bf16 v[24:27], v[38:41], v[6:9], 0
	s_add_i32 s4, s29, 0x6000
	s_mov_b32 m0, s4
	s_nop 0
	global_load_lds_dwordx4 v[28:29], off
	v_mfma_f32_16x16x32_bf16 v[34:37], v[38:41], v[10:13], 0
	v_mfma_f32_16x16x32_bf16 v[70:73], v[50:53], v[2:5], v[46:49]
	s_waitcnt lgkmcnt(0)
	v_mfma_f32_16x16x32_bf16 v[22:25], v[54:57], v[2:5], v[24:27]
	v_mfma_f32_16x16x32_bf16 v[78:81], v[54:57], v[14:17], v[34:37]
	s_nop 1
	ds_read_b128 v[26:29], v175 offset:8192
	s_nop 0
	ds_read_b128 v[34:37], v175 offset:8704
	ds_read_b128 v[38:41], v178 offset:8192
	ds_read_b128 v[46:49], v178 offset:8704
	ds_read_b128 v[50:53], v175 offset:12288
	ds_read_b128 v[54:57], v175 offset:12800
	ds_read_b128 v[62:65], v178 offset:12288
	ds_read_b128 v[66:69], v178 offset:12800
	v_exp_f32_e32 v42, v42
	v_exp_f32_e32 v43, v43
	v_exp_f32_e32 v44, v44
	v_exp_f32_e32 v45, v45
	v_exp_f32_e32 v86, v18
	v_exp_f32_e32 v87, v19
	v_exp_f32_e32 v20, v20
	v_exp_f32_e32 v21, v21
	v_exp_f32_e32 v30, v30
	v_exp_f32_e32 v58, v58
	v_add_f32_e32 v18, v42, v43
	v_add_f32_e32 v19, v44, v45
	v_exp_f32_e32 v31, v31
	v_exp_f32_e32 v59, v59
	v_add_f32_e32 v18, v18, v19
	v_add_f32_e32 v19, v86, v87
	v_add_f32_e32 v82, v20, v21
	v_add_f32_e32 v19, v19, v82
	v_exp_f32_e32 v32, v32
	v_exp_f32_e32 v60, v60
	v_add_f32_e32 v18, v18, v30
	v_add_f32_e32 v19, v19, v58
	v_exp_f32_e32 v33, v33
	v_exp_f32_e32 v61, v61
	v_add_f32_e32 v18, v31, v18
	v_add_f32_e32 v19, v59, v19
	v_exp_f32_e32 v70, v70
	v_exp_f32_e32 v74, v74
	v_add_f32_e32 v18, v32, v18
	v_add_f32_e32 v19, v60, v19
	v_exp_f32_e32 v71, v71
	v_exp_f32_e32 v75, v75
	v_add_f32_e32 v18, v33, v18
	v_add_f32_e32 v19, v61, v19
	v_exp_f32_e32 v72, v72
	v_exp_f32_e32 v76, v76
	v_add_f32_e32 v18, v70, v18
	v_add_f32_e32 v19, v74, v19
	v_exp_f32_e32 v73, v73
	v_exp_f32_e32 v77, v77
	v_add_f32_e32 v18, v71, v18
	v_add_f32_e32 v19, v75, v19
	v_exp_f32_e32 v22, v22
	v_exp_f32_e32 v78, v78
	v_add_f32_e32 v18, v72, v18
	v_add_f32_e32 v19, v76, v19
	v_exp_f32_e32 v23, v23
	v_exp_f32_e32 v79, v79
	v_add_f32_e32 v18, v73, v18
	v_add_f32_e32 v19, v77, v19
	v_exp_f32_e32 v24, v24
	v_exp_f32_e32 v80, v80
	v_add_f32_e32 v18, v22, v18
	v_add_f32_e32 v19, v78, v19
	v_exp_f32_e32 v25, v25
	v_exp_f32_e32 v81, v81
	v_add_f32_e32 v18, v23, v18
	v_add_f32_e32 v19, v79, v19
	s_mov_b32 s4, 1
	v_add_f32_e32 v18, v24, v18
	v_add_f32_e32 v82, v80, v19
	v_cvt_pk_bf16_f32 v83, v44, v45
	v_add_f32_e32 v19, v25, v18
	v_add_f32_e32 v18, v81, v82
	s_waitcnt vmcnt(3) lgkmcnt(0)
	s_barrier
	s_cmp_lg_u32 s4, 0
	v_pk_add_f32 v[166:167], v[18:19], 0 op_sel_hi:[1,0]
	v_mov_b32_e32 v18, 0
	v_cvt_pk_bf16_f32 v82, v42, v43
	v_cvt_pk_bf16_f32 v84, v30, v31
	v_cvt_pk_bf16_f32 v85, v32, v33
	v_cvt_pk_bf16_f32 v90, v86, v87
	v_cvt_pk_bf16_f32 v91, v20, v21
	v_cvt_pk_bf16_f32 v92, v58, v59
	v_cvt_pk_bf16_f32 v93, v60, v61
	v_cvt_pk_bf16_f32 v98, v70, v71
	v_cvt_pk_bf16_f32 v99, v72, v73
	v_cvt_pk_bf16_f32 v100, v22, v23
	v_cvt_pk_bf16_f32 v101, v24, v25
	v_cvt_pk_bf16_f32 v102, v74, v75
	v_cvt_pk_bf16_f32 v103, v76, v77
	v_cvt_pk_bf16_f32 v104, v78, v79
	v_cvt_pk_bf16_f32 v105, v80, v81
	s_cselect_b64 s[4:5], -1, 0
	s_mov_b32 s27, 2
	v_mov_b32_e32 v19, v18
	v_mov_b32_e32 v20, v18
	v_mov_b32_e32 v21, v18
	v_mov_b32_e32 v22, v18
	v_mov_b32_e32 v23, v18
	v_mov_b32_e32 v24, v18
	v_mov_b32_e32 v25, v18
	v_mov_b32_e32 v30, v18
	v_mov_b32_e32 v31, v18
	v_mov_b32_e32 v32, v18
	v_mov_b32_e32 v33, v18
	v_mov_b32_e32 v42, v18
	v_mov_b32_e32 v43, v18
	v_mov_b32_e32 v44, v18
	v_mov_b32_e32 v45, v18
	v_mov_b32_e32 v58, v18
	v_mov_b32_e32 v59, v18
	v_mov_b32_e32 v60, v18
	v_mov_b32_e32 v61, v18
	v_mov_b32_e32 v70, v18
	v_mov_b32_e32 v71, v18
	v_mov_b32_e32 v72, v18
	v_mov_b32_e32 v73, v18
	v_mov_b32_e32 v74, v18
	v_mov_b32_e32 v75, v18
	v_mov_b32_e32 v76, v18
	v_mov_b32_e32 v77, v18
	v_mov_b32_e32 v78, v18
	v_mov_b32_e32 v79, v18
	v_mov_b32_e32 v80, v18
	v_mov_b32_e32 v81, v18
	v_mov_b32_e32 v86, v18
	v_mov_b32_e32 v87, v18
	v_mov_b32_e32 v88, v18
	v_mov_b32_e32 v89, v18
	v_mov_b32_e32 v94, v18
	v_mov_b32_e32 v95, v18
	v_mov_b32_e32 v96, v18
	v_mov_b32_e32 v97, v18
	v_mov_b32_e32 v106, v18
	v_mov_b32_e32 v107, v18
	v_mov_b32_e32 v108, v18
	v_mov_b32_e32 v109, v18
	v_mov_b32_e32 v110, v18
	v_mov_b32_e32 v111, v18
	v_mov_b32_e32 v112, v18
	v_mov_b32_e32 v113, v18
	v_mov_b32_e32 v114, v18
	v_mov_b32_e32 v115, v18
	v_mov_b32_e32 v116, v18
	v_mov_b32_e32 v117, v18
	v_mov_b32_e32 v118, v18
	v_mov_b32_e32 v119, v18
	v_mov_b32_e32 v120, v18
	v_mov_b32_e32 v121, v18
	v_mov_b32_e32 v122, v18
	v_mov_b32_e32 v123, v18
	v_mov_b32_e32 v124, v18
	v_mov_b32_e32 v125, v18
	v_mov_b32_e32 v126, v18
	v_mov_b32_e32 v127, v18
	v_mov_b32_e32 v128, v18
	v_mov_b32_e32 v129, v18
	s_branch .LBB0_981

; #define ATT_SB() __builtin_amdgcn_sched_barrier(0)
; #define ATT_DMA_K(t, sl) do { glds16(ksrc + (size_t)(t) * 64 * kpitch, (unsigned)__builtin_amdgcn_readfirstlane(kdst + (sl) * KSLOT)); \
;         if constexpr (DQK == 96) glds16(krsrc + (size_t)(t) * 64 * 32, (unsigned)__builtin_amdgcn_readfirstlane(krdst + (sl) * KSLOT)); } while (0)
; #define ATT_DMA_V(t, sl) do { glds16(vsrc + (size_t)(t) * 64, (unsigned)__builtin_amdgcn_readfirstlane(vdst + (sl) * VSLOT)); \
;         if constexpr (DV == 128) glds16(vsrc + (size_t)64 * NR + (size_t)(t) * 64, (unsigned)__builtin_amdgcn_readfirstlane(vdst + (sl) * VSLOT + 8192)); } while (0)
; #define ATT_KLOAD(sl) do { _Pragma("unroll") for (int kb_ = 0; kb_ < NKW; ++kb_) _Pragma("unroll") for (int ds_ = 0; ds_ < NDS; ++ds_) { \
;         if (ds_ < 2) kf[kb_ * NDS + ds_] = *(const LAS bf16x8*)(kp[ds_ & 1] + (sl) * KSLOT + (kb_ & 1) * 512 + (kb_ >> 1) * 4096); \
;         else kf[kb_ * NDS + ds_] = *(const LAS bf16x8*)(krp + (sl) * KSLOT + (kb_ & 1) * 256 + (kb_ >> 1) * 2048); } } while (0)
; #define ATT_QK() do { _Pragma("unroll") for (int kb_ = 0; kb_ < NKW; ++kb_) _Pragma("unroll") for (int ds_ = 0; ds_ < NDS; ++ds_) _Pragma("unroll") for (int qb_ = 0; qb_ < NQB; ++qb_) \
;         c[kb_][qb_] = __builtin_amdgcn_mfma_f32_16x16x32_bf16(kf[kb_ * NDS + ds_], qf[qb_ * NDS + ds_], ds_ == 0 ? zero4 : c[kb_][qb_], 0, 0, 0); } while (0)
; template <int DQK, int DV, bool LEAD> ...
;     ...
;     for (int t = 1; t < NT; ++t) {
;         __builtin_amdgcn_s_waitcnt(0xC07F);
;         if constexpr (!LEAD) { ATT_EXP(); ATT_SUMPACK(); ATT_SB(); }
;         ATT_VLOAD(s_prev, 0); ATT_SB();
;         { const int tk = (t + 3 < NT) ? t + 3 : NT - 1; ATT_DMA_K(tk, s_cur); }
;         { const int tv = (t + 1 < NT) ? t + 1 : NT - 1; ATT_DMA_V(tv, s_next); }
;         ATT_SB();
;         if constexpr (LEAD) {
;             ATT_QK(); ATT_SB();
;             ATT_PVP(0); ATT_SB();
;             if constexpr (DV == 128) { ATT_VLOAD(s_prev, 1); ATT_SB(); ATT_EXP(); ATT_SB(); ATT_PVP(1); ATT_SB(); }
;             if (one_) ATT_KLOAD(s_next);
;             ATT_SB();
;             if constexpr (DV == 64) ATT_EXP();
;             ATT_SUMPACK();
;             asm volatile("" : "+v"(pw[0]), "+v"(pw[1]), "+v"(pw[2]), "+v"(pw[3]));
; #pragma unroll
;             for (int qb = 0; qb < NQB; ++qb) asm volatile("" : "+v"(lsum[qb]));
.LBB0_981:
	s_lshl_b32 s26, s23, 14
	v_add_u32_e32 v179, s26, v176
	s_waitcnt lgkmcnt(0)
	v_add_u32_e32 v192, s26, v177
	ds_read_b128 v[180:183], v179 offset:36864
	ds_read_b128 v[184:187], v179 offset:38912
	ds_read_b128 v[188:191], v192 offset:36864
	ds_read_b128 v[204:207], v192 offset:38912
	ds_read_b128 v[208:211], v179 offset:40960
	ds_read_b128 v[212:215], v179 offset:43008
	ds_read_b128 v[216:219], v192 offset:40960
	ds_read_b128 v[236:239], v192 offset:43008
	s_mov_b32 s26, s22
	s_mov_b32 s22, s27
	s_lshl_b32 s27, s26, 13
	s_add_i32 s27, s27, s25
	s_mov_b32 m0, s27
	s_nop 0
	global_load_lds_dwordx4 v[168:169], off
	s_min_u32 s27, s16, 3
	s_lshl_b32 s38, s27, 7
	s_lshl_b32 s27, s22, 14
	v_lshl_add_u64 v[130:131], v[162:163], 0, s[38:39]
	s_add_i32 s27, s27, s29
	s_mov_b32 m0, s27
	s_nop 0
	global_load_lds_dwordx4 v[130:131], off
	v_lshl_add_u64 v[130:131], v[164:165], 0, s[38:39]
	s_addk_i32 s27, 0x2000
	s_mov_b32 m0, s27
	s_nop 0
	global_load_lds_dwordx4 v[130:131], off
	v_mfma_f32_16x16x32_bf16 v[130:133], v[26:29], v[6:9], 0
	v_mfma_f32_16x16x32_bf16 v[134:137], v[26:29], v[10:13], 0
	v_mfma_f32_16x16x32_bf16 v[158:161], v[38:41], v[2:5], v[130:133]
	v_mfma_f32_16x16x32_bf16 v[130:133], v[34:37], v[6:9], 0
	v_mfma_f32_16x16x32_bf16 v[154:157], v[38:41], v[14:17], v[134:137]
	v_mfma_f32_16x16x32_bf16 v[134:137], v[34:37], v[10:13], 0
	v_mfma_f32_16x16x32_bf16 v[150:153], v[46:49], v[2:5], v[130:133]
	v_mfma_f32_16x16x32_bf16 v[130:133], v[50:53], v[6:9], 0
	v_mfma_f32_16x16x32_bf16 v[146:149], v[46:49], v[14:17], v[134:137]
	v_mfma_f32_16x16x32_bf16 v[134:137], v[50:53], v[10:13], 0
	v_mfma_f32_16x16x32_bf16 v[142:145], v[62:65], v[2:5], v[130:133]
	v_mfma_f32_16x16x32_bf16 v[130:133], v[54:57], v[6:9], 0
	v_mfma_f32_16x16x32_bf16 v[240:243], v[54:57], v[10:13], 0
	v_mfma_f32_16x16x32_bf16 v[138:141], v[62:65], v[14:17], v[134:137]
	v_mfma_f32_16x16x32_bf16 v[134:137], v[66:69], v[2:5], v[130:133]
	v_mfma_f32_16x16x32_bf16 v[130:133], v[66:69], v[14:17], v[240:243]
	s_waitcnt lgkmcnt(7)
	v_mfma_f32_16x16x32_bf16 v[126:129], v[180:183], v[82:85], v[126:129]
	v_mfma_f32_16x16x32_bf16 v[122:125], v[180:183], v[90:93], v[122:125]
	s_waitcnt lgkmcnt(6)
	v_mfma_f32_16x16x32_bf16 v[118:121], v[184:187], v[82:85], v[118:121]
	v_mfma_f32_16x16x32_bf16 v[114:117], v[184:187], v[90:93], v[114:117]
	s_waitcnt lgkmcnt(3)
	v_mfma_f32_16x16x32_bf16 v[110:113], v[208:211], v[82:85], v[110:113]
	v_mfma_f32_16x16x32_bf16 v[106:109], v[208:211], v[90:93], v[106:109]
	s_waitcnt lgkmcnt(2)
	v_mfma_f32_16x16x32_bf16 v[94:97], v[212:215], v[82:85], v[94:97]
	v_mfma_f32_16x16x32_bf16 v[86:89], v[212:215], v[90:93], v[86:89]
	v_mfma_f32_16x16x32_bf16 v[126:129], v[188:191], v[98:101], v[126:129]
	v_mfma_f32_16x16x32_bf16 v[122:125], v[188:191], v[102:105], v[122:125]
	v_mfma_f32_16x16x32_bf16 v[118:121], v[204:207], v[98:101], v[118:121]
	v_mfma_f32_16x16x32_bf16 v[114:117], v[204:207], v[102:105], v[114:117]
	s_waitcnt lgkmcnt(1)
	v_mfma_f32_16x16x32_bf16 v[110:113], v[216:219], v[98:101], v[110:113]
	v_mfma_f32_16x16x32_bf16 v[106:109], v[216:219], v[102:105], v[106:109]
	s_waitcnt lgkmcnt(0)
	v_mfma_f32_16x16x32_bf16 v[94:97], v[236:239], v[98:101], v[94:97]
	v_mfma_f32_16x16x32_bf16 v[86:89], v[236:239], v[102:105], v[86:89]
	ds_read_b128 v[180:183], v179 offset:45056
	ds_read_b128 v[184:187], v179 offset:47104
	ds_read_b128 v[188:191], v192 offset:45056
	ds_read_b128 v[204:207], v192 offset:47104
	ds_read_b128 v[208:211], v179 offset:49152
	ds_read_b128 v[212:215], v179 offset:51200
	ds_read_b128 v[216:219], v192 offset:49152
	ds_read_b128 v[236:239], v192 offset:51200
	s_waitcnt lgkmcnt(7)
	v_mfma_f32_16x16x32_bf16 v[78:81], v[180:183], v[82:85], v[78:81]
	v_mfma_f32_16x16x32_bf16 v[74:77], v[180:183], v[90:93], v[74:77]
	s_waitcnt lgkmcnt(6)
	v_mfma_f32_16x16x32_bf16 v[70:73], v[184:187], v[82:85], v[70:73]
	v_mfma_f32_16x16x32_bf16 v[58:61], v[184:187], v[90:93], v[58:61]
	s_waitcnt lgkmcnt(3)
	v_mfma_f32_16x16x32_bf16 v[42:45], v[208:211], v[82:85], v[42:45]
	v_mfma_f32_16x16x32_bf16 v[30:33], v[208:211], v[90:93], v[30:33]
	s_waitcnt lgkmcnt(2)
	v_mfma_f32_16x16x32_bf16 v[22:25], v[212:215], v[82:85], v[22:25]
	v_mfma_f32_16x16x32_bf16 v[18:21], v[212:215], v[90:93], v[18:21]
	v_mfma_f32_16x16x32_bf16 v[78:81], v[188:191], v[98:101], v[78:81]
	v_mfma_f32_16x16x32_bf16 v[74:77], v[188:191], v[102:105], v[74:77]
	v_mfma_f32_16x16x32_bf16 v[70:73], v[204:207], v[98:101], v[70:73]
	v_mfma_f32_16x16x32_bf16 v[58:61], v[204:207], v[102:105], v[58:61]
	s_waitcnt lgkmcnt(1)
	v_mfma_f32_16x16x32_bf16 v[42:45], v[216:219], v[98:101], v[42:45]
	v_mfma_f32_16x16x32_bf16 v[30:33], v[216:219], v[102:105], v[30:33]
	s_waitcnt lgkmcnt(0)
	v_mfma_f32_16x16x32_bf16 v[22:25], v[236:239], v[98:101], v[22:25]
	v_mfma_f32_16x16x32_bf16 v[18:21], v[236:239], v[102:105], v[18:21]
	s_andn2_b64 vcc, exec, s[4:5]
	s_cbranch_vccnz .LBB0_980
	s_lshl_b32 s27, s22, 13
	v_add_u32_e32 v54, s27, v175
	v_add_u32_e32 v66, s27, v178
	ds_read_b128 v[26:29], v54
	ds_read_b128 v[34:37], v54 offset:512
	ds_read_b128 v[38:41], v66
	ds_read_b128 v[46:49], v66 offset:512
	ds_read_b128 v[50:53], v54 offset:4096
	ds_read_b128 v[54:57], v54 offset:4608
	ds_read_b128 v[62:65], v66 offset:4096
	ds_read_b128 v[66:69], v66 offset:4608
	s_branch .LBB0_980

; #define ATT_DMA_K(t, sl) do { glds16(ksrc + (size_t)(t) * 64 * kpitch, (unsigned)__builtin_amdgcn_readfirstlane(kdst + (sl) * KSLOT)); \
;         if constexpr (DQK == 96) glds16(krsrc + (size_t)(t) * 64 * 32, (unsigned)__builtin_amdgcn_readfirstlane(krdst + (sl) * KSLOT)); } while (0)
; #define ATT_DMA_V(t, sl) do { glds16(vsrc + (size_t)(t) * 64, (unsigned)__builtin_amdgcn_readfirstlane(vdst + (sl) * VSLOT)); \
;         if constexpr (DV == 128) glds16(vsrc + (size_t)64 * NR + (size_t)(t) * 64, (unsigned)__builtin_amdgcn_readfirstlane(vdst + (sl) * VSLOT + 8192)); } while (0)
; __device__ __forceinline__ const float* IN(KArgs a, int i) { return (const float*)a->in[i]; }
; #define a launder(kargs)
; template <int DQK, int DV, bool LEAD> ...
;     ...
;     ATT_DMA_K(0, 0); ATT_DMA_V(0, 0); ATT_DMA_K(1, 1); ATT_DMA_K(2, 2);
;     bf16x8 qf[NQB * NDS];
;     {
;       const float c2 = (DQK == 64) ? C2_EVEN : C2_ODD; const bool lat = tq0 >= 0;
; #pragma unroll
;       for (int qb = 0; qb < NQB; ++qb) {
;           const bf16_t* qp = Q + (size_t)(qrow0 + qoff + qb * 16 + q16) * qpitch + g4 * 8;
;           bf16x8 raw[NDS];
; #pragma unroll
;           for (int ds = 0; ds < NDS; ++ds) raw[ds] = *(const bf16x8*)(qp + ds * 32);
;           float x[NDS][8];
; #pragma unroll
;           for (int ds = 0; ds < NDS; ++ds)
; #pragma unroll
;               for (int j = 0; j < 8; ++j) x[ds][j] = __uint_as_float(((unsigned)(unsigned short)raw[ds][j]) << 16);
; __global__ void __launch_bounds__(NWAVES * 64, 2) mega_fwd(Args args_) {
;     ...
;                 for (int u = F.vcu - 64; u < 64; u += F.G) { if (u < 0) continue; const int b = u >> 3, kvh = (u >> 2) & 1, g = u & 3;
;                     att::attn_unit<64, 64>(QK + 1024 + kvh * 256 + g * 64, QKW, QK + 1536 + kvh * 64, QKW, nullptr, VTE + (size_t)(512 + kvh * 64) * NR, H + 512 + kvh * 256 + g * 64, 1024, b * TPS + SEQ, b * TPS + SEQ, 4, F.lds, IN(a, I_BQK) + j * 128, (const f32x2*)(ws + WS_ROPE64), -100000); }
.LBB0_987:
	s_cmp_lt_i32 s3, 0
	s_cbranch_scc1 .LBB0_986
	s_bfe_u32 s30, s3, 0x10002
	s_lshr_b32 s6, s3, 3
	s_lshl_b32 s4, s30, 9
	s_add_u32 s4, s14, s4
	s_addc_u32 s5, s15, 0
	s_lshl_b32 s7, s3, 6
	s_and_b32 s7, s7, 0xc0
	s_lshl_b32 s29, s7, 1
	s_add_u32 s12, s4, s29
	s_addc_u32 s13, s5, 0
	s_lshl_b32 s4, s30, 7
	s_add_u32 s22, s17, s4
	s_addc_u32 s23, s24, 0
	s_mul_i32 s4, s30, 0x840000
	s_add_u32 s4, s10, s4
	s_addc_u32 s7, s11, 0
	s_add_u32 s26, s4, 0x4200000
	s_mov_b64 s[4:5], s[0:1]
	s_load_dwordx2 s[4:5], s[4:5], 0x60
	s_mulk_i32 s6, 0x2100
	s_addc_u32 s27, s7, 0
	s_add_i32 s18, s6, 0x2000
	s_lshl_b64 s[6:7], s[20:21], 2
	s_waitcnt lgkmcnt(0)
	s_add_u32 s8, s4, s6
	s_addc_u32 s9, s5, s7
	v_readfirstlane_b32 s4, v0
	s_cmpk_gt_u32 s4, 0xff
	s_mov_b64 s[4:5], -1
	s_cbranch_scc0 .LBB0_995
	v_mov_b32_e32 v83, v0
	s_mov_b32 s19, s39
	v_readfirstlane_b32 s6, v83
	s_ashr_i32 s4, s6, 6
	v_bfe_u32 v1, v83, 3, 3
	v_lshl_or_b32 v1, s4, 3, v1
	s_lshl_b32 s5, s4, 1
	s_lshr_b32 s7, s6, 5
	v_ashrrev_i32_e32 v3, 1, v1
	s_and_b32 s5, s5, 2
	s_and_b32 s7, s7, 4
	v_and_b32_e32 v2, 7, v83
	v_and_b32_e32 v4, 1, v3
	s_or_b32 s5, s5, s7
	v_bitop3_b32 v6, s5, v2, v4 bitop3:0x36
	v_xor_b32_e32 v7, v3, v83
	v_add_u32_e32 v4, s18, v1
	v_mov_b64_e32 v[2:3], s[22:23]
	s_and_b32 s31, s4, 3
	s_lshl_b32 s36, s4, 10
	v_mad_i64_i32 v[2:3], s[4:5], v4, s92, v[2:3]
	v_mov_b64_e32 v[4:5], s[26:27]
	v_mad_i64_i32 v[4:5], s[4:5], v1, s91, v[4:5]
	v_lshlrev_b32_e32 v194, 4, v6
	v_lshlrev_b32_e32 v1, 4, v7
	s_add_i32 s36, s36, 0
	v_lshl_add_u64 v[4:5], s[18:19], 1, v[4:5]
	v_lshl_add_u64 v[42:43], v[2:3], 0, v[194:195]
	v_and_b32_e32 v194, 0x70, v1
	s_mov_b32 m0, s36
	s_nop 0
	global_load_lds_dwordx4 v[42:43], off
	v_lshl_add_u64 v[162:163], v[4:5], 0, v[194:195]
	s_add_i32 s19, s36, 0x9000
	s_mov_b32 m0, s19
	s_nop 0
	global_load_lds_dwordx4 v[162:163], off
	v_and_b32_e32 v82, 15, v83
	s_mov_b64 s[4:5], 0x38000
	v_lshl_add_u64 v[2:3], v[42:43], 0, s[4:5]
	s_add_i32 s4, s36, 0x2000
	s_mov_b32 m0, s4
	s_nop 0
	global_load_lds_dwordx4 v[2:3], off
	v_lshl_or_b32 v1, s31, 6, v82
	s_mov_b64 s[4:5], 0x70000
	v_or_b32_e32 v1, s18, v1
	v_and_b32_e32 v194, 48, v83
	v_lshl_add_u64 v[2:3], v[42:43], 0, s[4:5]
	s_add_i32 s4, s36, 0x4000
	v_lshl_add_u64 v[10:11], s[12:13], 0, v[194:195]
	v_or_b32_e32 v16, 32, v1
	s_mov_b32 m0, s4
	s_nop 0
	global_load_lds_dwordx4 v[2:3], off
	v_or_b32_e32 v6, 16, v1
	v_mad_u64_u32 v[16:17], s[4:5], v16, s92, v[10:11]
	global_load_dwordx4 v[34:37], v[16:17], off offset:64
	v_mad_u64_u32 v[12:13], s[4:5], v1, s92, v[10:11]
	v_or_b32_e32 v1, 48, v1
	global_load_dwordx4 v[2:5], v[12:13], off offset:64
	v_mad_u64_u32 v[14:15], s[4:5], v6, s92, v[10:11]
	v_mad_u64_u32 v[10:11], s[4:5], v1, s92, v[10:11]
	global_load_dwordx4 v[6:9], v[14:15], off offset:64
	global_load_dwordx4 v[38:41], v[10:11], off offset:64
	global_load_dwordx4 v[64:67], v[12:13], off
	global_load_dwordx4 v[86:89], v[14:15], off
	global_load_dwordx4 v[18:21], v[16:17], off
	s_nop 0
	global_load_dwordx4 v[14:17], v[10:11], off
	v_bfe_u32 v85, v83, 4, 2
	s_waitcnt vmcnt(8)
	v_lshlrev_b32_e32 v52, 5, v85
	global_load_dwordx4 v[22:25], v52, s[8:9] offset:144
	global_load_dwordx4 v[26:29], v52, s[8:9] offset:128
	s_lshl_b32 s4, s6, 4
	v_lshlrev_b32_e32 v10, 1, v83
	v_and_b32_e32 v11, 3, v83
	v_lshrrev_b32_e32 v12, 1, v83
	s_and_b32 s4, s4, 0xfffff000
	v_and_or_b32 v10, v10, 24, v11
	v_bitop3_b32 v11, v85, v12, 7 bitop3:0x78
	s_add_i32 s4, s4, 0
	v_lshlrev_b32_e32 v84, 4, v11
	v_lshl_add_u32 v90, v10, 7, s4
	s_mov_b32 s4, 0x358637bd
	s_mov_b32 s16, 0x3c800000
	v_and_b32_e32 v1, 63, v83
	v_add_u32_e32 v174, v90, v84
	s_cmpk_lt_u32 s6, 0x100
	v_lshl_add_u64 v[168:169], v[42:43], 0, s[96:97]
	s_mov_b32 s37, 2
	s_waitcnt vmcnt(9)
	v_and_b32_e32 v31, 0xffff0000, v37
	v_lshlrev_b32_e32 v30, 16, v37
	v_and_b32_e32 v33, 0xffff0000, v36
	v_lshlrev_b32_e32 v32, 16, v36
	v_and_b32_e32 v57, 0xffff0000, v35
	v_lshlrev_b32_e32 v56, 16, v35
	s_waitcnt vmcnt(6)
	v_and_b32_e32 v45, 0xffff0000, v41
	v_lshlrev_b32_e32 v44, 16, v41
	v_and_b32_e32 v47, 0xffff0000, v40
	v_lshlrev_b32_e32 v46, 16, v40
	v_and_b32_e32 v49, 0xffff0000, v39
	v_lshlrev_b32_e32 v48, 16, v39
	v_and_b32_e32 v59, 0xffff0000, v34
	v_lshlrev_b32_e32 v58, 16, v34
	v_and_b32_e32 v51, 0xffff0000, v38
	v_lshlrev_b32_e32 v50, 16, v38
	global_load_dwordx4 v[34:37], v52, s[8:9] offset:16
	global_load_dwordx4 v[38:41], v52, s[8:9]
	s_waitcnt vmcnt(6)
	v_and_b32_e32 v75, 0xffff0000, v89
	v_lshlrev_b32_e32 v74, 16, v89
	v_and_b32_e32 v89, 0xffff0000, v64
	v_and_b32_e32 v95, 0xffff0000, v2
	v_lshlrev_b32_e32 v94, 16, v2
	v_and_b32_e32 v77, 0xffff0000, v88
	v_lshlrev_b32_e32 v76, 16, v88
	v_lshlrev_b32_e32 v88, 16, v64
	v_mul_f32_e32 v2, v89, v89
	v_and_b32_e32 v11, 0xffff0000, v9
	v_lshlrev_b32_e32 v10, 16, v9
	v_and_b32_e32 v69, 0xffff0000, v8
	v_lshlrev_b32_e32 v68, 16, v8
	v_and_b32_e32 v9, 0xffff0000, v3
	v_lshlrev_b32_e32 v8, 16, v3
	s_waitcnt vmcnt(4)
; template <int DQK, int DV, bool LEAD> ...
;     ...
;           float sn = 0.f;
; #pragma unroll
;           for (int ds = 0; ds < 2; ++ds)
; #pragma unroll
;               for (int j = 0; j < 8; ++j) sn += x[ds][j] * x[ds][j];
;           sn = lanes4_sum(sn);
;           const float rn = rsqrtf(sn * (1.f / 64.f) + EPS);
; #pragma unroll
;           for (int ds = 0; ds < 2; ++ds)
; #pragma unroll
;               for (int j = 0; j < 8; ++j) x[ds][j] *= rn * qgain[32 * ds + 8 * g4 + j];
;           if constexpr (DQK == 64) {
; #pragma unroll
;               for (int ds = 0; ds < 2; ++ds)
; #pragma unroll
;                   for (int j = 0; j < 8; ++j) {
;                       auto rr = __builtin_amdgcn_permlane32_swap(__float_as_uint(x[ds][j]), __float_as_uint(x[ds][j]), false, false);
;                       const float other = hi ? __uint_as_float(rr[0]) : __uint_as_float(rr[1]);
;                       float cc = 1.f, sg = 0.f;
;                       if (lat) { const f32x2 cs = rope[(ds ? pcol : prow) * 16 + 8 * (g4 & 1) + j]; cc = cs.x; sg = hi ? cs.y : -cs.y; }
;                       x[ds][j] = x[ds][j] * cc + other * sg; }
;           } else {
;               float sr = 0.f;
; #pragma unroll
;               for (int j = 0; j < 8; ++j) sr += x[2][j] * x[2][j];
;               sr = lanes4_sum(sr);
;               const float rq = rsqrtf(sr * (1.f / 32.f) + EPS);
; #pragma unroll
;               for (int j = 0; j < 8; ++j) { const float av = x[2][j] * rq * qgain[64 + 8 * g4 + j];
;                   auto rr = __builtin_amdgcn_permlane16_swap(__float_as_uint(av), __float_as_uint(av), false, false);
;                   const float other = (g4 & 1) ? __uint_as_float(rr[0]) : __uint_as_float(rr[1]);
;                   float cc = 1.f, sg = 0.f;
;                   if (lat) { const f32x2 cs = rope[((g4 & 2) ? pcol : prow) * 8 + j]; cc = cs.x; sg = (g4 & 1) ? cs.y : -cs.y; }
;                   x[2][j] = av * cc + other * sg; }
;           }
; #pragma unroll
;           for (int ds = 0; ds < NDS; ++ds) { u32x4 w;
; #pragma unroll
;               for (int i = 0; i < 4; ++i) w[i] = cvtpk(x[ds][2 * i] * c2, x[ds][2 * i + 1] * c2);
;               qf[qb * NDS + ds] = __builtin_bit_cast(bf16x8, w); }
	v_and_b32_e32 v53, 0xffff0000, v17
	v_lshlrev_b32_e32 v52, 16, v17
	v_and_b32_e32 v55, 0xffff0000, v16
	v_lshlrev_b32_e32 v54, 16, v16
	v_and_b32_e32 v17, 0xffff0000, v65
	v_lshlrev_b32_e32 v16, 16, v65
	v_pk_fma_f32 v[2:3], v[88:89], v[88:89], v[2:3] op_sel_hi:[1,1,0]
	v_and_b32_e32 v93, 0xffff0000, v4
	v_lshlrev_b32_e32 v92, 16, v4
	v_pk_fma_f32 v[2:3], v[16:17], v[16:17], v[2:3]
	v_mul_f32_e32 v4, v17, v17
	v_and_b32_e32 v97, 0xffff0000, v66
	v_lshlrev_b32_e32 v96, 16, v66
	v_pk_add_f32 v[2:3], v[4:5], v[2:3] op_sel_hi:[0,1]
	v_pk_fma_f32 v[2:3], v[96:97], v[96:97], v[2:3]
	v_mul_f32_e32 v4, v97, v97
	v_and_b32_e32 v71, 0xffff0000, v7
	v_lshlrev_b32_e32 v70, 16, v7
	v_and_b32_e32 v73, 0xffff0000, v6
	v_lshlrev_b32_e32 v72, 16, v6
	v_and_b32_e32 v7, 0xffff0000, v67
	v_lshlrev_b32_e32 v6, 16, v67
	v_pk_add_f32 v[2:3], v[4:5], v[2:3] op_sel_hi:[0,1]
	v_pk_fma_f32 v[2:3], v[6:7], v[6:7], v[2:3]
	v_mul_f32_e32 v4, v7, v7
	v_pk_add_f32 v[2:3], v[4:5], v[2:3] op_sel_hi:[0,1]
	v_pk_fma_f32 v[2:3], v[94:95], v[94:95], v[2:3]
	v_mul_f32_e32 v4, v95, v95
	v_pk_add_f32 v[2:3], v[4:5], v[2:3] op_sel_hi:[0,1]
	v_pk_fma_f32 v[2:3], v[8:9], v[8:9], v[2:3]
	v_mul_f32_e32 v4, v9, v9
	v_pk_add_f32 v[2:3], v[4:5], v[2:3] op_sel_hi:[0,1]
	v_pk_fma_f32 v[2:3], v[92:93], v[92:93], v[2:3]
	v_mul_f32_e32 v4, v93, v93
	v_and_b32_e32 v13, 0xffff0000, v5
	v_lshlrev_b32_e32 v12, 16, v5
	v_pk_add_f32 v[2:3], v[4:5], v[2:3] op_sel_hi:[0,1]
	v_pk_fma_f32 v[2:3], v[12:13], v[12:13], v[2:3]
	v_mul_f32_e32 v4, v13, v13
	v_pk_add_f32 v[2:3], v[4:5], v[2:3] op_sel_hi:[0,1]
	v_mov_b32_e32 v3, v2
	s_nop 1
	v_permlane16_swap_b32_e32 v2, v3
	v_add_f32_e32 v3, v2, v3
	v_mov_b32_e32 v5, v3
	v_and_b32_e32 v81, 0xffff0000, v86
	s_nop 0
	v_permlane32_swap_b32_e32 v3, v5
	v_lshlrev_b32_e32 v80, 16, v86
	v_mul_f32_e32 v2, v81, v81
	v_and_b32_e32 v61, 0xffff0000, v21
	v_lshlrev_b32_e32 v60, 16, v21
	v_and_b32_e32 v63, 0xffff0000, v20
	v_lshlrev_b32_e32 v62, 16, v20
	v_and_b32_e32 v79, 0xffff0000, v87
	v_lshlrev_b32_e32 v78, 16, v87
	v_pk_fma_f32 v[20:21], v[80:81], v[80:81], v[2:3] op_sel_hi:[1,1,0]
	v_mul_f32_e32 v2, v79, v79
	v_pk_fma_f32 v[20:21], v[78:79], v[78:79], v[20:21]
	v_and_b32_e32 v67, 0xffff0000, v15
	v_pk_add_f32 v[20:21], v[2:3], v[20:21] op_sel_hi:[0,1]
	v_pk_fma_f32 v[20:21], v[76:77], v[76:77], v[20:21]
	v_mul_f32_e32 v2, v77, v77
	v_pk_add_f32 v[20:21], v[2:3], v[20:21] op_sel_hi:[0,1]
	v_pk_fma_f32 v[20:21], v[74:75], v[74:75], v[20:21]
	v_mul_f32_e32 v2, v75, v75
	v_pk_add_f32 v[20:21], v[2:3], v[20:21] op_sel_hi:[0,1]
	v_pk_fma_f32 v[20:21], v[72:73], v[72:73], v[20:21]
	v_mul_f32_e32 v2, v73, v73
	v_pk_add_f32 v[20:21], v[2:3], v[20:21] op_sel_hi:[0,1]
	v_pk_fma_f32 v[20:21], v[70:71], v[70:71], v[20:21]
	v_mul_f32_e32 v2, v71, v71
	v_pk_add_f32 v[20:21], v[2:3], v[20:21] op_sel_hi:[0,1]
	v_pk_fma_f32 v[20:21], v[68:69], v[68:69], v[20:21]
	v_mul_f32_e32 v2, v69, v69
	v_pk_add_f32 v[20:21], v[2:3], v[20:21] op_sel_hi:[0,1]
	v_pk_fma_f32 v[20:21], v[10:11], v[10:11], v[20:21]
	v_mul_f32_e32 v2, v11, v11
	v_pk_add_f32 v[20:21], v[2:3], v[20:21] op_sel_hi:[0,1]
	v_mov_b32_e32 v2, v20
	s_nop 1
	v_permlane16_swap_b32_e32 v20, v2
	v_add_f32_e32 v2, v20, v2
	v_mov_b32_e32 v4, v2
	s_nop 1
	v_permlane32_swap_b32_e32 v2, v4
	v_pk_add_f32 v[2:3], v[2:3], v[4:5]
	v_mov_b64_e32 v[20:21], s[4:5]
	v_pk_fma_f32 v[86:87], v[2:3], s[16:17], v[20:21] op_sel_hi:[1,0,0]
	v_lshlrev_b32_e32 v66, 16, v15
	v_mul_f32_e32 v2, 0x4b800000, v87
	v_cmp_gt_f32_e32 vcc, s95, v87
	v_cmp_gt_f32_e64 s[4:5], s95, v86
	v_and_b32_e32 v65, 0xffff0000, v19
	v_cndmask_b32_e32 v2, v87, v2, vcc
	v_rsq_f32_e32 v2, v2
	v_lshlrev_b32_e32 v64, 16, v19
	v_mul_f32_e32 v3, 0x45800000, v2
	v_cndmask_b32_e32 v98, v2, v3, vcc
	s_waitcnt vmcnt(3)
	v_pk_mul_f32 v[2:3], v[98:99], v[24:25] op_sel_hi:[0,1]
	v_pk_mul_f32 v[2:3], v[2:3], v[12:13]
	v_cmp_gt_u32_e32 vcc, 32, v1
	v_mov_b32_e32 v4, v2
	v_mov_b32_e32 v12, v2
	v_mov_b32_e32 v5, v3
	v_mov_b32_e32 v13, v3
	v_permlane32_swap_b32_e32 v4, v12
	s_nop 0
	v_permlane32_swap_b32_e32 v5, v13
	v_cndmask_b32_e32 v5, v5, v13, vcc
	v_cndmask_b32_e32 v4, v4, v12, vcc
	v_pk_fma_f32 v[2:3], v[4:5], 0, v[2:3] op_sel_hi:[1,0,1]
	s_nop 0
	v_pk_mul_f32 v[2:3], v[2:3], s[94:95] op_sel_hi:[1,0]
	s_nop 0
	v_cvt_pk_bf16_f32 v5, v2, v3
	v_pk_mul_f32 v[2:3], v[98:99], v[22:23] op_sel_hi:[0,1]
	v_pk_mul_f32 v[2:3], v[2:3], v[92:93]
	s_nop 0
	v_mov_b32_e32 v4, v2
	v_mov_b32_e32 v12, v2
	v_mov_b32_e32 v13, v3
	v_mov_b32_e32 v15, v3
	v_permlane32_swap_b32_e32 v4, v12
	s_nop 0
	v_permlane32_swap_b32_e32 v13, v15
	v_cndmask_b32_e32 v13, v13, v15, vcc
	v_cndmask_b32_e32 v12, v4, v12, vcc
	v_pk_fma_f32 v[2:3], v[12:13], 0, v[2:3] op_sel_hi:[1,0,1]
	s_nop 0
	v_pk_mul_f32 v[2:3], v[2:3], s[94:95] op_sel_hi:[1,0]
	s_nop 0
	v_cvt_pk_bf16_f32 v4, v2, v3
	s_waitcnt vmcnt(2)
	v_pk_mul_f32 v[2:3], v[98:99], v[28:29] op_sel_hi:[0,1]
	v_pk_mul_f32 v[2:3], v[2:3], v[8:9]
	s_nop 0
	v_mov_b32_e32 v8, v2
	v_mov_b32_e32 v12, v2
	v_mov_b32_e32 v9, v3
	v_mov_b32_e32 v13, v3
	v_permlane32_swap_b32_e32 v8, v12
	s_nop 0
	v_permlane32_swap_b32_e32 v9, v13
	v_cndmask_b32_e32 v9, v9, v13, vcc
	v_cndmask_b32_e32 v8, v8, v12, vcc
	v_pk_fma_f32 v[2:3], v[8:9], 0, v[2:3] op_sel_hi:[1,0,1]
	v_pk_mul_f32 v[8:9], v[26:27], v[98:99] op_sel_hi:[1,0]
	v_pk_mul_f32 v[2:3], v[2:3], s[94:95] op_sel_hi:[1,0]
	v_pk_mul_f32 v[8:9], v[8:9], v[94:95]
	v_cvt_pk_bf16_f32 v3, v2, v3
	v_mov_b32_e32 v2, v8
	v_mov_b32_e32 v12, v8
	v_mov_b32_e32 v13, v9
	v_mov_b32_e32 v15, v9
	v_permlane32_swap_b32_e32 v2, v12
	s_nop 0
	v_permlane32_swap_b32_e32 v13, v15
	v_cndmask_b32_e32 v13, v13, v15, vcc
	v_cndmask_b32_e32 v12, v2, v12, vcc
	v_pk_fma_f32 v[8:9], v[12:13], 0, v[8:9] op_sel_hi:[1,0,1]
	s_nop 0
	v_pk_mul_f32 v[8:9], v[8:9], s[94:95] op_sel_hi:[1,0]
	s_nop 0
	v_cvt_pk_bf16_f32 v2, v8, v9
	s_waitcnt vmcnt(1)
; __device__ __forceinline__ unsigned cvtpk(float lo, float hi) { f32x2 v = {lo, hi}; bf16x2_t b = __builtin_convertvector(v, bf16x2_t); return __builtin_bit_cast(unsigned, b); }
; template <int DQK, int DV, bool LEAD> ...
;     ...
;           const float rn = rsqrtf(sn * (1.f / 64.f) + EPS);
; #pragma unroll
;           for (int ds = 0; ds < 2; ++ds)
; #pragma unroll
;               for (int j = 0; j < 8; ++j) x[ds][j] *= rn * qgain[32 * ds + 8 * g4 + j];
;           if constexpr (DQK == 64) {
; #pragma unroll
;               for (int ds = 0; ds < 2; ++ds)
; #pragma unroll
;                   for (int j = 0; j < 8; ++j) {
;                       auto rr = __builtin_amdgcn_permlane32_swap(__float_as_uint(x[ds][j]), __float_as_uint(x[ds][j]), false, false);
;                       const float other = hi ? __uint_as_float(rr[0]) : __uint_as_float(rr[1]);
;                       float cc = 1.f, sg = 0.f;
;                       if (lat) { const f32x2 cs = rope[(ds ? pcol : prow) * 16 + 8 * (g4 & 1) + j]; cc = cs.x; sg = hi ? cs.y : -cs.y; }
;                       x[ds][j] = x[ds][j] * cc + other * sg; }
;           } else {
;               float sr = 0.f;
; #pragma unroll
;               for (int j = 0; j < 8; ++j) sr += x[2][j] * x[2][j];
;               sr = lanes4_sum(sr);
;               const float rq = rsqrtf(sr * (1.f / 32.f) + EPS);
; #pragma unroll
;               for (int j = 0; j < 8; ++j) { const float av = x[2][j] * rq * qgain[64 + 8 * g4 + j];
;                   auto rr = __builtin_amdgcn_permlane16_swap(__float_as_uint(av), __float_as_uint(av), false, false);
;                   const float other = (g4 & 1) ? __uint_as_float(rr[0]) : __uint_as_float(rr[1]);
;                   float cc = 1.f, sg = 0.f;
;                   if (lat) { const f32x2 cs = rope[((g4 & 2) ? pcol : prow) * 8 + j]; cc = cs.x; sg = (g4 & 1) ? cs.y : -cs.y; }
;                   x[2][j] = av * cc + other * sg; }
;           }
; #pragma unroll
;           for (int ds = 0; ds < NDS; ++ds) { u32x4 w;
; #pragma unroll
;               for (int i = 0; i < 4; ++i) w[i] = cvtpk(x[ds][2 * i] * c2, x[ds][2 * i + 1] * c2);
;               qf[qb * NDS + ds] = __builtin_bit_cast(bf16x8, w); }
	v_pk_mul_f32 v[8:9], v[36:37], v[98:99] op_sel_hi:[1,0]
	s_nop 0
	v_pk_mul_f32 v[6:7], v[8:9], v[6:7]
	s_nop 0
	v_mov_b32_e32 v8, v6
	v_mov_b32_e32 v12, v6
	v_mov_b32_e32 v9, v7
	v_mov_b32_e32 v13, v7
	v_permlane32_swap_b32_e32 v8, v12
	s_nop 0
	v_permlane32_swap_b32_e32 v9, v13
	v_cndmask_b32_e32 v9, v9, v13, vcc
	v_cndmask_b32_e32 v8, v8, v12, vcc
	v_pk_fma_f32 v[6:7], v[8:9], 0, v[6:7] op_sel_hi:[1,0,1]
	s_nop 0
	v_pk_mul_f32 v[6:7], v[6:7], s[94:95] op_sel_hi:[1,0]
	s_nop 0
	v_cvt_pk_bf16_f32 v9, v6, v7
	v_pk_mul_f32 v[6:7], v[34:35], v[98:99] op_sel_hi:[1,0]
	s_nop 0
	v_pk_mul_f32 v[6:7], v[6:7], v[96:97]
	s_nop 0
	v_mov_b32_e32 v8, v6
	v_mov_b32_e32 v12, v6
	v_mov_b32_e32 v13, v7
	v_mov_b32_e32 v15, v7
	v_permlane32_swap_b32_e32 v8, v12
	s_nop 0
	v_permlane32_swap_b32_e32 v13, v15
	v_cndmask_b32_e32 v13, v13, v15, vcc
	v_cndmask_b32_e32 v12, v8, v12, vcc
	v_pk_fma_f32 v[6:7], v[12:13], 0, v[6:7] op_sel_hi:[1,0,1]
	s_nop 0
	v_pk_mul_f32 v[6:7], v[6:7], s[94:95] op_sel_hi:[1,0]
	s_nop 0
	v_cvt_pk_bf16_f32 v8, v6, v7
	s_waitcnt vmcnt(0)
	v_pk_mul_f32 v[6:7], v[40:41], v[98:99] op_sel_hi:[1,0]
	s_nop 0
	v_pk_mul_f32 v[6:7], v[6:7], v[16:17]
	s_nop 0
	v_mov_b32_e32 v12, v6
	v_mov_b32_e32 v15, v6
	v_mov_b32_e32 v13, v7
	v_mov_b32_e32 v16, v7
	v_permlane32_swap_b32_e32 v12, v15
	s_nop 0
	v_permlane32_swap_b32_e32 v13, v16
	v_cndmask_b32_e32 v13, v13, v16, vcc
	v_cndmask_b32_e32 v12, v12, v15, vcc
	v_pk_fma_f32 v[6:7], v[12:13], 0, v[6:7] op_sel_hi:[1,0,1]
	v_pk_mul_f32 v[12:13], v[38:39], v[98:99] op_sel_hi:[1,0]
	v_pk_mul_f32 v[6:7], v[6:7], s[94:95] op_sel_hi:[1,0]
	v_pk_mul_f32 v[12:13], v[12:13], v[88:89]
	v_cvt_pk_bf16_f32 v7, v6, v7
	v_mov_b32_e32 v6, v12
	v_mov_b32_e32 v15, v12
	v_mov_b32_e32 v16, v13
	v_mov_b32_e32 v17, v13
	v_permlane32_swap_b32_e32 v6, v15
	s_nop 0
	v_permlane32_swap_b32_e32 v16, v17
	v_cndmask_b32_e32 v17, v16, v17, vcc
	v_cndmask_b32_e32 v16, v6, v15, vcc
	v_mul_f32_e32 v6, 0x4b800000, v86
	v_cndmask_b32_e64 v6, v86, v6, s[4:5]
	v_rsq_f32_e32 v15, v6
	v_pk_fma_f32 v[12:13], v[16:17], 0, v[12:13] op_sel_hi:[1,0,1]
	s_nop 0
	v_pk_mul_f32 v[12:13], v[12:13], s[94:95] op_sel_hi:[1,0]
	s_nop 0
	v_cvt_pk_bf16_f32 v6, v12, v13
	v_mul_f32_e32 v12, 0x45800000, v15
	v_cndmask_b32_e64 v86, v15, v12, s[4:5]
	v_pk_mul_f32 v[12:13], v[24:25], v[86:87] op_sel_hi:[1,0]
	s_nop 0
	v_pk_mul_f32 v[10:11], v[12:13], v[10:11]
	s_nop 0
	v_mov_b32_e32 v12, v10
	v_mov_b32_e32 v15, v10
	v_mov_b32_e32 v13, v11
	v_mov_b32_e32 v16, v11
	v_permlane32_swap_b32_e32 v12, v15
	s_nop 0
	v_permlane32_swap_b32_e32 v13, v16
	v_cndmask_b32_e32 v13, v13, v16, vcc
	v_cndmask_b32_e32 v12, v12, v15, vcc
	v_pk_fma_f32 v[10:11], v[12:13], 0, v[10:11] op_sel_hi:[1,0,1]
	s_nop 0
	v_pk_mul_f32 v[10:11], v[10:11], s[94:95] op_sel_hi:[1,0]
	s_nop 0
	v_cvt_pk_bf16_f32 v13, v10, v11
	v_pk_mul_f32 v[10:11], v[22:23], v[86:87] op_sel_hi:[1,0]
	s_nop 0
	v_pk_mul_f32 v[10:11], v[10:11], v[68:69]
	s_nop 0
	v_mov_b32_e32 v12, v10
	v_mov_b32_e32 v15, v10
	v_mov_b32_e32 v16, v11
	v_mov_b32_e32 v17, v11
	v_permlane32_swap_b32_e32 v12, v15
	s_nop 0
	v_permlane32_swap_b32_e32 v16, v17
	v_cndmask_b32_e32 v17, v16, v17, vcc
	v_cndmask_b32_e32 v16, v12, v15, vcc
	v_pk_fma_f32 v[10:11], v[16:17], 0, v[10:11] op_sel_hi:[1,0,1]
	s_nop 0
	v_pk_mul_f32 v[10:11], v[10:11], s[94:95] op_sel_hi:[1,0]
	s_nop 0
	v_cvt_pk_bf16_f32 v12, v10, v11
	v_pk_mul_f32 v[10:11], v[28:29], v[86:87] op_sel_hi:[1,0]
	s_nop 0
	v_pk_mul_f32 v[10:11], v[10:11], v[70:71]
	s_nop 0
	v_mov_b32_e32 v15, v10
	v_mov_b32_e32 v16, v10
	v_mov_b32_e32 v17, v11
	v_mov_b32_e32 v19, v11
	v_permlane32_swap_b32_e32 v15, v16
	s_nop 0
	v_permlane32_swap_b32_e32 v17, v19
	v_cndmask_b32_e32 v17, v17, v19, vcc
	v_cndmask_b32_e32 v16, v15, v16, vcc
	v_pk_fma_f32 v[10:11], v[16:17], 0, v[10:11] op_sel_hi:[1,0,1]
	v_pk_mul_f32 v[16:17], v[26:27], v[86:87] op_sel_hi:[1,0]
	v_pk_mul_f32 v[10:11], v[10:11], s[94:95] op_sel_hi:[1,0]
	v_pk_mul_f32 v[16:17], v[16:17], v[72:73]
	v_cvt_pk_bf16_f32 v11, v10, v11
	v_mov_b32_e32 v10, v16
	v_mov_b32_e32 v15, v16
	v_mov_b32_e32 v19, v17
	v_mov_b32_e32 v68, v17
	v_permlane32_swap_b32_e32 v10, v15
	s_nop 0
	v_permlane32_swap_b32_e32 v19, v68
	v_cndmask_b32_e32 v69, v19, v68, vcc
	v_cndmask_b32_e32 v68, v10, v15, vcc
	v_pk_fma_f32 v[16:17], v[68:69], 0, v[16:17] op_sel_hi:[1,0,1]
	v_and_b32_e32 v73, 0xffff0000, v18
	v_pk_mul_f32 v[16:17], v[16:17], s[94:95] op_sel_hi:[1,0]
	s_nop 0
	v_cvt_pk_bf16_f32 v10, v16, v17
	v_pk_mul_f32 v[16:17], v[36:37], v[86:87] op_sel_hi:[1,0]
	s_nop 0
	v_pk_mul_f32 v[16:17], v[16:17], v[74:75]
	v_mul_f32_e32 v74, v65, v65
	v_mov_b32_e32 v15, v16
	v_mov_b32_e32 v19, v16
	v_mov_b32_e32 v68, v17
	v_mov_b32_e32 v69, v17
	v_permlane32_swap_b32_e32 v15, v19
	s_nop 0
	v_permlane32_swap_b32_e32 v68, v69
	v_cndmask_b32_e32 v69, v68, v69, vcc
	v_cndmask_b32_e32 v68, v15, v19, vcc
	v_pk_fma_f32 v[16:17], v[68:69], 0, v[16:17] op_sel_hi:[1,0,1]
	v_pk_mul_f32 v[68:69], v[34:35], v[86:87] op_sel_hi:[1,0]
	v_pk_mul_f32 v[16:17], v[16:17], s[94:95] op_sel_hi:[1,0]
	v_pk_mul_f32 v[68:69], v[68:69], v[76:77]
	v_cvt_pk_bf16_f32 v17, v16, v17
	v_mov_b32_e32 v15, v68
	v_mov_b32_e32 v16, v68
	v_mov_b32_e32 v19, v69
	v_mov_b32_e32 v70, v69
	v_permlane32_swap_b32_e32 v15, v16
	s_nop 0
	v_permlane32_swap_b32_e32 v19, v70
	v_cndmask_b32_e32 v71, v19, v70, vcc
	v_cndmask_b32_e32 v70, v15, v16, vcc
	v_pk_fma_f32 v[68:69], v[70:71], 0, v[68:69] op_sel_hi:[1,0,1]
	v_and_b32_e32 v77, 0xffff0000, v14
	v_pk_mul_f32 v[68:69], v[68:69], s[94:95] op_sel_hi:[1,0]
	v_lshlrev_b32_e32 v76, 16, v14
	v_cvt_pk_bf16_f32 v16, v68, v69
	v_pk_mul_f32 v[68:69], v[40:41], v[86:87] op_sel_hi:[1,0]
; template <int DQK, int DV, bool LEAD> ...
;     ...
;           float sn = 0.f;
; #pragma unroll
;           for (int ds = 0; ds < 2; ++ds)
; #pragma unroll
;               for (int j = 0; j < 8; ++j) sn += x[ds][j] * x[ds][j];
;           sn = lanes4_sum(sn);
;           const float rn = rsqrtf(sn * (1.f / 64.f) + EPS);
; #pragma unroll
;           for (int ds = 0; ds < 2; ++ds)
; #pragma unroll
;               for (int j = 0; j < 8; ++j) x[ds][j] *= rn * qgain[32 * ds + 8 * g4 + j];
;           if constexpr (DQK == 64) {
; #pragma unroll
;               for (int ds = 0; ds < 2; ++ds)
; #pragma unroll
;                   for (int j = 0; j < 8; ++j) {
;                       auto rr = __builtin_amdgcn_permlane32_swap(__float_as_uint(x[ds][j]), __float_as_uint(x[ds][j]), false, false);
;                       const float other = hi ? __uint_as_float(rr[0]) : __uint_as_float(rr[1]);
;                       float cc = 1.f, sg = 0.f;
;                       if (lat) { const f32x2 cs = rope[(ds ? pcol : prow) * 16 + 8 * (g4 & 1) + j]; cc = cs.x; sg = hi ? cs.y : -cs.y; }
;                       x[ds][j] = x[ds][j] * cc + other * sg; }
;           } else {
;               float sr = 0.f;
; #pragma unroll
;               for (int j = 0; j < 8; ++j) sr += x[2][j] * x[2][j];
;               sr = lanes4_sum(sr);
;               const float rq = rsqrtf(sr * (1.f / 32.f) + EPS);
; #pragma unroll
;               for (int j = 0; j < 8; ++j) { const float av = x[2][j] * rq * qgain[64 + 8 * g4 + j];
;                   auto rr = __builtin_amdgcn_permlane16_swap(__float_as_uint(av), __float_as_uint(av), false, false);
;                   const float other = (g4 & 1) ? __uint_as_float(rr[0]) : __uint_as_float(rr[1]);
;                   float cc = 1.f, sg = 0.f;
;                   if (lat) { const f32x2 cs = rope[((g4 & 2) ? pcol : prow) * 8 + j]; cc = cs.x; sg = (g4 & 1) ? cs.y : -cs.y; }
;                   x[2][j] = av * cc + other * sg; }
;           }
; #pragma unroll
;           for (int ds = 0; ds < NDS; ++ds) { u32x4 w;
; #pragma unroll
;               for (int i = 0; i < 4; ++i) w[i] = cvtpk(x[ds][2 * i] * c2, x[ds][2 * i + 1] * c2);
;               qf[qb * NDS + ds] = __builtin_bit_cast(bf16x8, w); }
	v_mul_f32_e32 v14, v77, v77
	v_pk_mul_f32 v[68:69], v[68:69], v[78:79]
	s_nop 0
	v_mov_b32_e32 v15, v68
	v_mov_b32_e32 v19, v68
	v_mov_b32_e32 v70, v69
	v_mov_b32_e32 v71, v69
	v_permlane32_swap_b32_e32 v15, v19
	s_nop 0
	v_permlane32_swap_b32_e32 v70, v71
	v_cndmask_b32_e32 v71, v70, v71, vcc
	v_cndmask_b32_e32 v70, v15, v19, vcc
	v_pk_fma_f32 v[68:69], v[70:71], 0, v[68:69] op_sel_hi:[1,0,1]
	s_nop 0
	v_pk_mul_f32 v[68:69], v[68:69], s[94:95] op_sel_hi:[1,0]
	s_nop 0
	v_cvt_pk_bf16_f32 v15, v68, v69
	v_pk_mul_f32 v[68:69], v[38:39], v[86:87] op_sel_hi:[1,0]
	v_pk_fma_f32 v[78:79], v[76:77], v[76:77], v[14:15] op_sel_hi:[1,1,0]
	v_pk_mul_f32 v[68:69], v[68:69], v[80:81]
	v_pk_fma_f32 v[78:79], v[66:67], v[66:67], v[78:79]
	v_mov_b32_e32 v71, v69
	v_mov_b32_e32 v72, v69
	v_mov_b32_e32 v19, v68
	v_mov_b32_e32 v70, v68
	v_permlane32_swap_b32_e32 v71, v72
	s_nop 0
	v_permlane32_swap_b32_e32 v19, v70
	v_cndmask_b32_e32 v71, v71, v72, vcc
	v_lshlrev_b32_e32 v72, 16, v18
	v_mul_f32_e32 v18, v73, v73
	v_cndmask_b32_e32 v70, v19, v70, vcc
	v_pk_fma_f32 v[18:19], v[72:73], v[72:73], v[18:19] op_sel_hi:[1,1,0]
	v_mul_f32_e32 v14, v67, v67
	v_pk_fma_f32 v[18:19], v[64:65], v[64:65], v[18:19]
	v_pk_add_f32 v[78:79], v[14:15], v[78:79] op_sel_hi:[0,1]
	v_pk_add_f32 v[18:19], v[74:75], v[18:19] op_sel_hi:[0,1]
	v_pk_fma_f32 v[18:19], v[62:63], v[62:63], v[18:19]
	v_mul_f32_e32 v74, v63, v63
	v_pk_fma_f32 v[78:79], v[54:55], v[54:55], v[78:79]
	v_mul_f32_e32 v14, v55, v55
	v_pk_add_f32 v[18:19], v[74:75], v[18:19] op_sel_hi:[0,1]
	v_pk_add_f32 v[78:79], v[14:15], v[78:79] op_sel_hi:[0,1]
	v_pk_fma_f32 v[18:19], v[60:61], v[60:61], v[18:19]
	v_mul_f32_e32 v74, v61, v61
	v_pk_fma_f32 v[78:79], v[52:53], v[52:53], v[78:79]
	v_mul_f32_e32 v14, v53, v53
	v_pk_add_f32 v[18:19], v[74:75], v[18:19] op_sel_hi:[0,1]
	v_pk_add_f32 v[78:79], v[14:15], v[78:79] op_sel_hi:[0,1]
	v_pk_fma_f32 v[18:19], v[58:59], v[58:59], v[18:19]
	v_mul_f32_e32 v74, v59, v59
	v_pk_fma_f32 v[78:79], v[50:51], v[50:51], v[78:79]
	v_mul_f32_e32 v14, v51, v51
	v_pk_add_f32 v[18:19], v[74:75], v[18:19] op_sel_hi:[0,1]
	v_pk_add_f32 v[78:79], v[14:15], v[78:79] op_sel_hi:[0,1]
	v_pk_fma_f32 v[18:19], v[56:57], v[56:57], v[18:19]
	v_mul_f32_e32 v74, v57, v57
	v_pk_fma_f32 v[78:79], v[48:49], v[48:49], v[78:79]
	v_mul_f32_e32 v14, v49, v49
	v_pk_add_f32 v[18:19], v[74:75], v[18:19] op_sel_hi:[0,1]
	v_pk_add_f32 v[78:79], v[14:15], v[78:79] op_sel_hi:[0,1]
	v_pk_fma_f32 v[18:19], v[32:33], v[32:33], v[18:19]
	v_mul_f32_e32 v74, v33, v33
	v_pk_fma_f32 v[78:79], v[46:47], v[46:47], v[78:79]
	v_mul_f32_e32 v14, v47, v47
	v_pk_add_f32 v[18:19], v[74:75], v[18:19] op_sel_hi:[0,1]
	v_pk_add_f32 v[78:79], v[14:15], v[78:79] op_sel_hi:[0,1]
	v_pk_fma_f32 v[18:19], v[30:31], v[30:31], v[18:19]
	v_mul_f32_e32 v74, v31, v31
	v_pk_fma_f32 v[78:79], v[44:45], v[44:45], v[78:79]
	v_mul_f32_e32 v14, v45, v45
	v_pk_add_f32 v[18:19], v[74:75], v[18:19] op_sel_hi:[0,1]
	v_pk_add_f32 v[78:79], v[14:15], v[78:79] op_sel_hi:[0,1]
	v_mov_b32_e32 v19, v18
	v_mov_b32_e32 v14, v78
	s_nop 0
	v_permlane16_swap_b32_e32 v18, v19
	v_permlane16_swap_b32_e32 v78, v14
	v_add_f32_e32 v19, v18, v19
	v_add_f32_e32 v18, v78, v14
	v_mov_b32_e32 v75, v19
	v_mov_b32_e32 v74, v18
	s_nop 0
	v_permlane32_swap_b32_e32 v19, v75
	v_permlane32_swap_b32_e32 v18, v74
	v_pk_add_f32 v[18:19], v[18:19], v[74:75]
	s_nop 0
	v_pk_fma_f32 v[74:75], v[18:19], s[16:17], v[20:21] op_sel_hi:[1,0,0]
	v_pk_fma_f32 v[18:19], v[70:71], 0, v[68:69] op_sel_hi:[1,0,1]
	v_mul_f32_e32 v14, 0x4b800000, v75
	v_cmp_gt_f32_e64 s[4:5], s95, v75
	v_pk_mul_f32 v[18:19], v[18:19], s[94:95] op_sel_hi:[1,0]
	s_mov_b32 s16, 1
	v_cndmask_b32_e64 v14, v75, v14, s[4:5]
	v_rsq_f32_e32 v20, v14
	v_cvt_pk_bf16_f32 v14, v18, v19
	v_mul_f32_e32 v18, 0x45800000, v20
	v_cndmask_b32_e64 v68, v20, v18, s[4:5]
	v_pk_mul_f32 v[18:19], v[24:25], v[68:69] op_sel_hi:[1,0]
	v_cmp_gt_f32_e64 s[4:5], s95, v74
	v_pk_mul_f32 v[18:19], v[18:19], v[30:31]
	s_nop 0
	v_mov_b32_e32 v20, v18
	v_mov_b32_e32 v30, v18
	v_mov_b32_e32 v21, v19
	v_mov_b32_e32 v31, v19
	v_permlane32_swap_b32_e32 v20, v30
	s_nop 0
	v_permlane32_swap_b32_e32 v21, v31
	v_cndmask_b32_e32 v21, v21, v31, vcc
	v_cndmask_b32_e32 v20, v20, v30, vcc
	v_pk_fma_f32 v[18:19], v[20:21], 0, v[18:19] op_sel_hi:[1,0,1]
	s_nop 0
	v_pk_mul_f32 v[18:19], v[18:19], s[94:95] op_sel_hi:[1,0]
	s_nop 0
	v_cvt_pk_bf16_f32 v21, v18, v19
	v_pk_mul_f32 v[18:19], v[22:23], v[68:69] op_sel_hi:[1,0]
	s_nop 0
	v_pk_mul_f32 v[18:19], v[18:19], v[32:33]
	s_nop 0
	v_mov_b32_e32 v20, v18
	v_mov_b32_e32 v30, v18
	v_mov_b32_e32 v31, v19
	v_mov_b32_e32 v32, v19
	v_permlane32_swap_b32_e32 v20, v30
	s_nop 0
	v_permlane32_swap_b32_e32 v31, v32
	v_cndmask_b32_e32 v31, v31, v32, vcc
	v_cndmask_b32_e32 v30, v20, v30, vcc
	v_pk_fma_f32 v[18:19], v[30:31], 0, v[18:19] op_sel_hi:[1,0,1]
	s_nop 0
	v_pk_mul_f32 v[18:19], v[18:19], s[94:95] op_sel_hi:[1,0]
	s_nop 0
	v_cvt_pk_bf16_f32 v20, v18, v19
	v_pk_mul_f32 v[18:19], v[28:29], v[68:69] op_sel_hi:[1,0]
	s_nop 0
	v_pk_mul_f32 v[18:19], v[18:19], v[56:57]
	s_nop 0
	v_mov_b32_e32 v30, v18
	v_mov_b32_e32 v32, v18
	v_mov_b32_e32 v31, v19
	v_mov_b32_e32 v33, v19
	v_permlane32_swap_b32_e32 v30, v32
	s_nop 0
	v_permlane32_swap_b32_e32 v31, v33
	v_cndmask_b32_e32 v31, v31, v33, vcc
	v_cndmask_b32_e32 v30, v30, v32, vcc
	v_pk_fma_f32 v[18:19], v[30:31], 0, v[18:19] op_sel_hi:[1,0,1]
	v_pk_mul_f32 v[30:31], v[26:27], v[68:69] op_sel_hi:[1,0]
	v_pk_mul_f32 v[18:19], v[18:19], s[94:95] op_sel_hi:[1,0]
	v_pk_mul_f32 v[30:31], v[30:31], v[58:59]
	v_cvt_pk_bf16_f32 v19, v18, v19
	v_mov_b32_e32 v18, v30
	v_mov_b32_e32 v32, v30
; __device__ __forceinline__ unsigned cvtpk(float lo, float hi) { f32x2 v = {lo, hi}; bf16x2_t b = __builtin_convertvector(v, bf16x2_t); return __builtin_bit_cast(unsigned, b); }
; template <int DQK, int DV, bool LEAD> ...
;     ...
;           if constexpr (DQK == 64) {
; #pragma unroll
;               for (int ds = 0; ds < 2; ++ds)
; #pragma unroll
;                   for (int j = 0; j < 8; ++j) {
;                       auto rr = __builtin_amdgcn_permlane32_swap(__float_as_uint(x[ds][j]), __float_as_uint(x[ds][j]), false, false);
;                       const float other = hi ? __uint_as_float(rr[0]) : __uint_as_float(rr[1]);
;                       float cc = 1.f, sg = 0.f;
;                       if (lat) { const f32x2 cs = rope[(ds ? pcol : prow) * 16 + 8 * (g4 & 1) + j]; cc = cs.x; sg = hi ? cs.y : -cs.y; }
;                       x[ds][j] = x[ds][j] * cc + other * sg; }
;           } else {
;               float sr = 0.f;
; #pragma unroll
;               for (int j = 0; j < 8; ++j) sr += x[2][j] * x[2][j];
;               sr = lanes4_sum(sr);
;               const float rq = rsqrtf(sr * (1.f / 32.f) + EPS);
; #pragma unroll
;               for (int j = 0; j < 8; ++j) { const float av = x[2][j] * rq * qgain[64 + 8 * g4 + j];
;                   auto rr = __builtin_amdgcn_permlane16_swap(__float_as_uint(av), __float_as_uint(av), false, false);
;                   const float other = (g4 & 1) ? __uint_as_float(rr[0]) : __uint_as_float(rr[1]);
;                   float cc = 1.f, sg = 0.f;
;                   if (lat) { const f32x2 cs = rope[((g4 & 2) ? pcol : prow) * 8 + j]; cc = cs.x; sg = (g4 & 1) ? cs.y : -cs.y; }
;                   x[2][j] = av * cc + other * sg; }
;           }
; #pragma unroll
;           for (int ds = 0; ds < NDS; ++ds) { u32x4 w;
; #pragma unroll
;               for (int i = 0; i < 4; ++i) w[i] = cvtpk(x[ds][2 * i] * c2, x[ds][2 * i + 1] * c2);
;               qf[qb * NDS + ds] = __builtin_bit_cast(bf16x8, w); }
;       }
; #pragma unroll
;       for (int d0 = 0; d0 < NQB * NDS; ++d0) asm volatile("" : "+v"(qf[d0])); }
;     wait_bar<0>();
	v_mov_b32_e32 v33, v31
	v_mov_b32_e32 v56, v31
	v_permlane32_swap_b32_e32 v18, v32
	s_nop 0
	v_permlane32_swap_b32_e32 v33, v56
	v_cndmask_b32_e32 v33, v33, v56, vcc
	v_cndmask_b32_e32 v32, v18, v32, vcc
	v_pk_fma_f32 v[30:31], v[32:33], 0, v[30:31] op_sel_hi:[1,0,1]
	s_nop 0
	v_pk_mul_f32 v[30:31], v[30:31], s[94:95] op_sel_hi:[1,0]
	s_nop 0
	v_cvt_pk_bf16_f32 v18, v30, v31
	v_pk_mul_f32 v[30:31], v[36:37], v[68:69] op_sel_hi:[1,0]
	s_nop 0
	v_pk_mul_f32 v[30:31], v[30:31], v[60:61]
	s_nop 0
	v_mov_b32_e32 v32, v30
	v_mov_b32_e32 v56, v30
	v_mov_b32_e32 v33, v31
	v_mov_b32_e32 v57, v31
	v_permlane32_swap_b32_e32 v32, v56
	s_nop 0
	v_permlane32_swap_b32_e32 v33, v57
	v_cndmask_b32_e32 v33, v33, v57, vcc
	v_cndmask_b32_e32 v32, v32, v56, vcc
	v_pk_fma_f32 v[30:31], v[32:33], 0, v[30:31] op_sel_hi:[1,0,1]
	s_nop 0
	v_pk_mul_f32 v[30:31], v[30:31], s[94:95] op_sel_hi:[1,0]
	s_nop 0
	v_cvt_pk_bf16_f32 v33, v30, v31
	v_pk_mul_f32 v[30:31], v[34:35], v[68:69] op_sel_hi:[1,0]
	s_nop 0
	v_pk_mul_f32 v[30:31], v[30:31], v[62:63]
	s_nop 0
	v_mov_b32_e32 v32, v30
	v_mov_b32_e32 v56, v30
	v_mov_b32_e32 v57, v31
	v_mov_b32_e32 v58, v31
	v_permlane32_swap_b32_e32 v32, v56
	s_nop 0
	v_permlane32_swap_b32_e32 v57, v58
	v_cndmask_b32_e32 v57, v57, v58, vcc
	v_cndmask_b32_e32 v56, v32, v56, vcc
	v_pk_fma_f32 v[30:31], v[56:57], 0, v[30:31] op_sel_hi:[1,0,1]
	s_nop 0
	v_pk_mul_f32 v[30:31], v[30:31], s[94:95] op_sel_hi:[1,0]
	s_nop 0
	v_cvt_pk_bf16_f32 v32, v30, v31
	v_pk_mul_f32 v[30:31], v[40:41], v[68:69] op_sel_hi:[1,0]
	s_nop 0
	v_pk_mul_f32 v[30:31], v[30:31], v[64:65]
	s_nop 0
	v_mov_b32_e32 v56, v30
	v_mov_b32_e32 v58, v30
	v_mov_b32_e32 v57, v31
	v_mov_b32_e32 v59, v31
	v_permlane32_swap_b32_e32 v56, v58
	s_nop 0
	v_permlane32_swap_b32_e32 v57, v59
	v_cndmask_b32_e32 v57, v57, v59, vcc
	v_cndmask_b32_e32 v56, v56, v58, vcc
	v_pk_fma_f32 v[30:31], v[56:57], 0, v[30:31] op_sel_hi:[1,0,1]
	v_pk_mul_f32 v[56:57], v[38:39], v[68:69] op_sel_hi:[1,0]
	v_pk_mul_f32 v[30:31], v[30:31], s[94:95] op_sel_hi:[1,0]
	v_pk_mul_f32 v[56:57], v[56:57], v[72:73]
	v_cvt_pk_bf16_f32 v31, v30, v31
	v_mov_b32_e32 v30, v56
	v_mov_b32_e32 v58, v56
	s_nop 1
	v_permlane32_swap_b32_e32 v30, v58
	v_mov_b32_e32 v59, v57
	v_mov_b32_e32 v60, v57
	v_cndmask_b32_e32 v58, v30, v58, vcc
	v_mul_f32_e32 v30, 0x4b800000, v74
	v_permlane32_swap_b32_e32 v59, v60
	v_cndmask_b32_e64 v30, v74, v30, s[4:5]
	v_cndmask_b32_e32 v59, v59, v60, vcc
	v_rsq_f32_e32 v60, v30
	v_pk_fma_f32 v[56:57], v[58:59], 0, v[56:57] op_sel_hi:[1,0,1]
	s_nop 0
	v_pk_mul_f32 v[56:57], v[56:57], s[94:95] op_sel_hi:[1,0]
	s_nop 0
	v_cvt_pk_bf16_f32 v30, v56, v57
	v_mul_f32_e32 v56, 0x45800000, v60
	v_cndmask_b32_e64 v56, v60, v56, s[4:5]
	v_pk_mul_f32 v[38:39], v[38:39], v[56:57] op_sel_hi:[1,0]
	v_pk_mul_f32 v[22:23], v[22:23], v[56:57] op_sel_hi:[1,0]
	v_pk_mul_f32 v[38:39], v[38:39], v[76:77]
	v_pk_mul_f32 v[24:25], v[24:25], v[56:57] op_sel_hi:[1,0]
	v_pk_mul_f32 v[22:23], v[22:23], v[46:47]
	v_pk_mul_f32 v[24:25], v[24:25], v[44:45]
	v_mov_b32_e32 v44, v38
	v_mov_b32_e32 v46, v38
	v_mov_b32_e32 v45, v39
	v_mov_b32_e32 v47, v39
	v_pk_mul_f32 v[40:41], v[40:41], v[56:57] op_sel_hi:[1,0]
	v_permlane32_swap_b32_e32 v44, v46
	v_permlane32_swap_b32_e32 v45, v47
	v_pk_mul_f32 v[40:41], v[40:41], v[66:67]
	v_cndmask_b32_e32 v45, v45, v47, vcc
	v_cndmask_b32_e32 v44, v44, v46, vcc
	v_pk_fma_f32 v[38:39], v[44:45], 0, v[38:39] op_sel_hi:[1,0,1]
	v_mov_b32_e32 v44, v40
	v_mov_b32_e32 v46, v40
	v_mov_b32_e32 v45, v41
	v_mov_b32_e32 v47, v41
	v_pk_mul_f32 v[34:35], v[34:35], v[56:57] op_sel_hi:[1,0]
	v_permlane32_swap_b32_e32 v44, v46
	v_permlane32_swap_b32_e32 v45, v47
	v_pk_mul_f32 v[34:35], v[34:35], v[54:55]
	v_cndmask_b32_e32 v45, v45, v47, vcc
	v_cndmask_b32_e32 v44, v44, v46, vcc
	v_pk_fma_f32 v[40:41], v[44:45], 0, v[40:41] op_sel_hi:[1,0,1]
	v_mov_b32_e32 v44, v34
	v_mov_b32_e32 v46, v34
	v_mov_b32_e32 v45, v35
	v_mov_b32_e32 v47, v35
	v_pk_mul_f32 v[36:37], v[36:37], v[56:57] op_sel_hi:[1,0]
	v_permlane32_swap_b32_e32 v44, v46
	v_permlane32_swap_b32_e32 v45, v47
	v_pk_mul_f32 v[36:37], v[36:37], v[52:53]
	v_cndmask_b32_e32 v45, v45, v47, vcc
	v_cndmask_b32_e32 v44, v44, v46, vcc
	v_pk_fma_f32 v[34:35], v[44:45], 0, v[34:35] op_sel_hi:[1,0,1]
	v_mov_b32_e32 v44, v36
	v_mov_b32_e32 v46, v36
	v_mov_b32_e32 v45, v37
	v_mov_b32_e32 v47, v37
	v_pk_mul_f32 v[26:27], v[26:27], v[56:57] op_sel_hi:[1,0]
	v_permlane32_swap_b32_e32 v44, v46
	v_permlane32_swap_b32_e32 v45, v47
	v_pk_mul_f32 v[26:27], v[26:27], v[50:51]
	v_cndmask_b32_e32 v45, v45, v47, vcc
	v_cndmask_b32_e32 v44, v44, v46, vcc
	v_pk_fma_f32 v[36:37], v[44:45], 0, v[36:37] op_sel_hi:[1,0,1]
	v_mov_b32_e32 v44, v26
	v_mov_b32_e32 v46, v26
	v_mov_b32_e32 v45, v27
	v_mov_b32_e32 v47, v27
	v_pk_mul_f32 v[28:29], v[28:29], v[56:57] op_sel_hi:[1,0]
	v_permlane32_swap_b32_e32 v44, v46
	v_permlane32_swap_b32_e32 v45, v47
	v_pk_mul_f32 v[28:29], v[28:29], v[48:49]
	v_cndmask_b32_e32 v45, v45, v47, vcc
	v_cndmask_b32_e32 v44, v44, v46, vcc
	v_pk_fma_f32 v[26:27], v[44:45], 0, v[26:27] op_sel_hi:[1,0,1]
	v_mov_b32_e32 v44, v28
	v_mov_b32_e32 v46, v28
	v_mov_b32_e32 v45, v29
	v_mov_b32_e32 v47, v29
	v_permlane32_swap_b32_e32 v44, v46
	s_nop 0
	v_permlane32_swap_b32_e32 v45, v47
	v_cndmask_b32_e32 v45, v45, v47, vcc
	v_cndmask_b32_e32 v44, v44, v46, vcc
	v_pk_fma_f32 v[28:29], v[44:45], 0, v[28:29] op_sel_hi:[1,0,1]
	v_mov_b32_e32 v44, v22
	v_mov_b32_e32 v46, v22
	v_mov_b32_e32 v45, v23
	v_mov_b32_e32 v47, v23
	v_permlane32_swap_b32_e32 v44, v46
	s_nop 0
	v_permlane32_swap_b32_e32 v45, v47
	v_cndmask_b32_e32 v45, v45, v47, vcc
	v_cndmask_b32_e32 v44, v44, v46, vcc
	v_pk_fma_f32 v[22:23], v[44:45], 0, v[22:23] op_sel_hi:[1,0,1]
	v_mov_b32_e32 v44, v24
	v_mov_b32_e32 v46, v24
	v_mov_b32_e32 v45, v25
	v_mov_b32_e32 v47, v25
	v_permlane32_swap_b32_e32 v44, v46
	s_nop 0
	v_permlane32_swap_b32_e32 v45, v47
	v_cndmask_b32_e32 v45, v45, v47, vcc
	v_cndmask_b32_e32 v44, v44, v46, vcc
	v_pk_fma_f32 v[24:25], v[44:45], 0, v[24:25] op_sel_hi:[1,0,1]
	v_pk_mul_f32 v[38:39], v[38:39], s[94:95] op_sel_hi:[1,0]
	v_pk_mul_f32 v[34:35], v[34:35], s[94:95] op_sel_hi:[1,0]
	v_pk_mul_f32 v[26:27], v[26:27], s[94:95] op_sel_hi:[1,0]
	v_pk_mul_f32 v[22:23], v[22:23], s[94:95] op_sel_hi:[1,0]
	v_cvt_pk_bf16_f32 v58, v38, v39
	v_pk_mul_f32 v[38:39], v[40:41], s[94:95] op_sel_hi:[1,0]
	v_cvt_pk_bf16_f32 v60, v34, v35
	v_pk_mul_f32 v[34:35], v[36:37], s[94:95] op_sel_hi:[1,0]
	v_cvt_pk_bf16_f32 v86, v26, v27
	v_pk_mul_f32 v[26:27], v[28:29], s[94:95] op_sel_hi:[1,0]
	v_cvt_pk_bf16_f32 v88, v22, v23
	v_pk_mul_f32 v[22:23], v[24:25], s[94:95] op_sel_hi:[1,0]
	v_cvt_pk_bf16_f32 v59, v38, v39
	v_cvt_pk_bf16_f32 v61, v34, v35
	v_cvt_pk_bf16_f32 v87, v26, v27
	v_cvt_pk_bf16_f32 v89, v22, v23
	s_waitcnt vmcnt(0) lgkmcnt(0)
	s_barrier
; #define ATT_SB() __builtin_amdgcn_sched_barrier(0)
; #define ATT_DMA_K(t, sl) do { glds16(ksrc + (size_t)(t) * 64 * kpitch, (unsigned)__builtin_amdgcn_readfirstlane(kdst + (sl) * KSLOT)); \
;         if constexpr (DQK == 96) glds16(krsrc + (size_t)(t) * 64 * 32, (unsigned)__builtin_amdgcn_readfirstlane(krdst + (sl) * KSLOT)); } while (0)
; #define ATT_DMA_V(t, sl) do { glds16(vsrc + (size_t)(t) * 64, (unsigned)__builtin_amdgcn_readfirstlane(vdst + (sl) * VSLOT)); \
;         if constexpr (DV == 128) glds16(vsrc + (size_t)64 * NR + (size_t)(t) * 64, (unsigned)__builtin_amdgcn_readfirstlane(vdst + (sl) * VSLOT + 8192)); } while (0)
; #define ATT_KLOAD(sl) do { _Pragma("unroll") for (int kb_ = 0; kb_ < NKW; ++kb_) _Pragma("unroll") for (int ds_ = 0; ds_ < NDS; ++ds_) { \
;         if (ds_ < 2) kf[kb_ * NDS + ds_] = *(const LAS bf16x8*)(kp[ds_ & 1] + (sl) * KSLOT + (kb_ & 1) * 512 + (kb_ >> 1) * 4096); \
;         else kf[kb_ * NDS + ds_] = *(const LAS bf16x8*)(krp + (sl) * KSLOT + (kb_ & 1) * 256 + (kb_ >> 1) * 2048); } } while (0)
; #define ATT_QK() do { _Pragma("unroll") for (int kb_ = 0; kb_ < NKW; ++kb_) _Pragma("unroll") for (int ds_ = 0; ds_ < NDS; ++ds_) _Pragma("unroll") for (int qb_ = 0; qb_ < NQB; ++qb_) \
;         c[kb_][qb_] = __builtin_amdgcn_mfma_f32_16x16x32_bf16(kf[kb_ * NDS + ds_], qf[qb_ * NDS + ds_], ds_ == 0 ? zero4 : c[kb_][qb_], 0, 0, 0); } while (0)
; #define ATT_EXP() do { _Pragma("unroll") for (int kb_ = 0; kb_ < NKW; ++kb_) _Pragma("unroll") for (int qb_ = 0; qb_ < NQB; ++qb_) _Pragma("unroll") for (int i_ = 0; i_ < 4; ++i_) \
;         c[kb_][qb_][i_] = __builtin_amdgcn_exp2f(c[kb_][qb_][i_]); } while (0)
; template <int DQK, int DV, bool LEAD> ...
;     ...
;     bf16x8 kf[NKW * NDS], vf[NVF];
;     ATT_KLOAD(0);
;     asm volatile("s_waitcnt lgkmcnt(0)\n\ts_barrier" ::: "memory");
;     float lsum[NQB];
; #pragma unroll
;     for (int qb = 0; qb < NQB; ++qb) lsum[qb] = 0.f;
;     const f32x4 zero4 = {0.f, 0.f, 0.f, 0.f};
;     f32x4 o[NDB][NQB], c[NKW][NQB]; u32x4 pw[4];
; #pragma unroll
;     for (int i = 0; i < NDB; ++i)
; #pragma unroll
;         for (int qb = 0; qb < NQB; ++qb) o[i][qb] = zero4;
;     ATT_DMA_K(3, 0); ATT_DMA_V(1, 1);
;     ATT_QK(); ATT_SB();
;     ATT_KLOAD(1); ATT_SB();
;     if constexpr (LEAD) { ATT_EXP(); ATT_SUMPACK(); }
;     wait_bar<NDMA>();
;     int s_prev = 0, s_cur = 1, s_next = 2;
	ds_read_b128 v[22:25], v174
	ds_read_b128 v[26:29], v174 offset:512
	v_bfe_u32 v48, v83, 1, 3
	v_bitop3_b32 v48, v85, v48, 4 bitop3:0x36
	v_lshlrev_b32_e32 v56, 4, v48
	v_add_u32_e32 v176, v90, v56
	s_waitcnt lgkmcnt(1)
	v_mfma_f32_16x16x32_bf16 v[34:37], v[22:25], v[6:9], 0
	ds_read_b128 v[48:51], v176
	ds_read_b128 v[52:55], v176 offset:512
	s_waitcnt lgkmcnt(0)
	s_barrier
	s_mov_b32 m0, s36
	s_nop 0
	global_load_lds_dwordx4 v[168:169], off
	v_mfma_f32_16x16x32_bf16 v[38:41], v[22:25], v[14:17], 0
	s_cselect_b64 vcc, -1, 0
	s_add_i32 s4, s19, 0x2000
	v_mfma_f32_16x16x32_bf16 v[44:47], v[22:25], v[30:33], 0
	v_mfma_f32_16x16x32_bf16 v[22:25], v[22:25], v[58:61], 0
	s_waitcnt lgkmcnt(1)
	v_mfma_f32_16x16x32_bf16 v[142:145], v[48:51], v[2:5], v[34:37]
	v_mfma_f32_16x16x32_bf16 v[138:141], v[48:51], v[10:13], v[38:41]
	v_mfma_f32_16x16x32_bf16 v[110:113], v[48:51], v[86:89], v[22:25]
	v_mfma_f32_16x16x32_bf16 v[22:25], v[26:29], v[6:9], 0
	v_mfma_f32_16x16x32_bf16 v[34:37], v[26:29], v[14:17], 0
	v_mfma_f32_16x16x32_bf16 v[38:41], v[26:29], v[30:33], 0
	v_mfma_f32_16x16x32_bf16 v[26:29], v[26:29], v[58:61], 0
	v_mfma_f32_16x16x32_bf16 v[126:129], v[48:51], v[18:21], v[44:47]
	s_waitcnt lgkmcnt(0)
	v_mfma_f32_16x16x32_bf16 v[134:137], v[52:55], v[2:5], v[22:25]
	s_nop 0
	v_lshlrev_b32_e32 v44, 7, v82
	s_nop 0
	v_lshl_add_u64 v[22:23], v[162:163], 0, s[66:67]
	v_mfma_f32_16x16x32_bf16 v[130:133], v[52:55], v[10:13], v[34:37]
	s_mov_b32 m0, s4
	s_nop 0
	global_load_lds_dwordx4 v[22:23], off
	s_mov_b32 s4, 0
	s_mov_b32 s6, s4
	v_mfma_f32_16x16x32_bf16 v[122:125], v[52:55], v[18:21], v[38:41]
	s_mov_b32 s7, s4
	s_mov_b32 s5, s4
	v_mov_b64_e32 v[24:25], s[6:7]
	v_mfma_f32_16x16x32_bf16 v[114:117], v[52:55], v[86:89], v[26:29]
	v_mov_b64_e32 v[22:23], s[4:5]
	ds_read_b128 v[98:101], v174 offset:8192
	ds_read_b128 v[106:109], v174 offset:8704
	ds_read_b128 v[102:105], v176 offset:8192
	ds_read_b128 v[118:121], v176 offset:8704
	v_cndmask_b32_e32 v26, v56, v84, vcc
	v_add3_u32 v175, 0, v44, v26
	s_waitcnt vmcnt(2) lgkmcnt(0)
	s_barrier
	s_mov_b32 s5, 1
	v_mov_b32_e32 v164, 0
	s_cmp_lg_u32 s5, 0
	v_mov_b64_e32 v[28:29], v[24:25]
	v_mov_b64_e32 v[36:37], v[24:25]
	v_mov_b64_e32 v[40:41], v[24:25]
	v_mov_b64_e32 v[44:45], v[24:25]
	v_mov_b64_e32 v[48:49], v[24:25]
	v_mov_b64_e32 v[52:53], v[24:25]
	v_mov_b64_e32 v[56:57], v[24:25]
	v_mov_b64_e32 v[64:65], v[24:25]
	v_mov_b64_e32 v[68:69], v[24:25]
	v_mov_b64_e32 v[72:73], v[24:25]
	v_mov_b64_e32 v[76:77], v[24:25]
	v_mov_b64_e32 v[80:81], v[24:25]
	v_mov_b64_e32 v[84:85], v[24:25]
	v_mov_b64_e32 v[92:93], v[24:25]
	v_mov_b64_e32 v[96:97], v[24:25]
	s_cselect_b64 s[6:7], -1, 0
	v_mov_b64_e32 v[26:27], v[22:23]
	v_mov_b64_e32 v[34:35], v[22:23]
	v_mov_b64_e32 v[38:39], v[22:23]
	v_mov_b64_e32 v[42:43], v[22:23]
	v_mov_b64_e32 v[46:47], v[22:23]
	v_mov_b64_e32 v[50:51], v[22:23]
	v_mov_b64_e32 v[54:55], v[22:23]
	v_mov_b64_e32 v[62:63], v[22:23]
	v_mov_b64_e32 v[66:67], v[22:23]
	v_mov_b64_e32 v[70:71], v[22:23]
	v_mov_b64_e32 v[74:75], v[22:23]
	v_mov_b64_e32 v[78:79], v[22:23]
	v_mov_b64_e32 v[82:83], v[22:23]
	v_mov_b64_e32 v[90:91], v[22:23]
	v_mov_b64_e32 v[94:95], v[22:23]
	s_mov_b32 s38, 2
	v_mov_b32_e32 v165, v164
	v_mov_b32_e32 v166, v164
	v_mov_b32_e32 v167, v164
; #define ATT_SB() __builtin_amdgcn_sched_barrier(0)
; #define ATT_DMA_K(t, sl) do { glds16(ksrc + (size_t)(t) * 64 * kpitch, (unsigned)__builtin_amdgcn_readfirstlane(kdst + (sl) * KSLOT)); \
;         if constexpr (DQK == 96) glds16(krsrc + (size_t)(t) * 64 * 32, (unsigned)__builtin_amdgcn_readfirstlane(krdst + (sl) * KSLOT)); } while (0)
; #define ATT_DMA_V(t, sl) do { glds16(vsrc + (size_t)(t) * 64, (unsigned)__builtin_amdgcn_readfirstlane(vdst + (sl) * VSLOT)); \
;         if constexpr (DV == 128) glds16(vsrc + (size_t)64 * NR + (size_t)(t) * 64, (unsigned)__builtin_amdgcn_readfirstlane(vdst + (sl) * VSLOT + 8192)); } while (0)
; template <int DQK, int DV, bool LEAD> ...
;     ...
;     for (int t = 1; t < NT; ++t) {
;         __builtin_amdgcn_s_waitcnt(0xC07F);
;         if constexpr (!LEAD) { ATT_EXP(); ATT_SUMPACK(); ATT_SB(); }
;         ATT_VLOAD(s_prev, 0); ATT_SB();
;         { const int tk = (t + 3 < NT) ? t + 3 : NT - 1; ATT_DMA_K(tk, s_cur); }
;         { const int tv = (t + 1 < NT) ? t + 1 : NT - 1; ATT_DMA_V(tv, s_next); }
;         ATT_SB();
;         if constexpr (LEAD) {
;             ATT_QK(); ATT_SB();
;             ATT_PVP(0); ATT_SB();
;             if constexpr (DV == 128) { ATT_VLOAD(s_prev, 1); ATT_SB(); ATT_EXP(); ATT_SB(); ATT_PVP(1); ATT_SB(); }
;             if (one_) ATT_KLOAD(s_next);
;             ATT_SB();
;             if constexpr (DV == 64) ATT_EXP();
;             ATT_SUMPACK();
;             asm volatile("" : "+v"(pw[0]), "+v"(pw[1]), "+v"(pw[2]), "+v"(pw[3]));
; #pragma unroll
;             for (int qb = 0; qb < NQB; ++qb) asm volatile("" : "+v"(lsum[qb]));
;         } else {
;             if constexpr (DV == 128) {
;                 ATT_PVP(0); ATT_SB();
;                 ATT_VLOAD(s_prev, 1); ATT_SB();
;                 ATT_QK(); ATT_SB();
;                 if (one_) { ATT_KLOAD(s_next); ATT_SB(); ATT_PVP(1); }
;                 ATT_SB();
;             } else {
;                 __builtin_amdgcn_s_setprio(1);
;                 ATT_QK(); ATT_SB();
;                 if (one_) { ATT_KLOAD(s_next); ATT_SB(); ATT_PVP(0); }
;                 ATT_SB();
;                 __builtin_amdgcn_s_setprio(0);
;             }
; #pragma unroll
;             for (int kb = 0; kb < NKW; ++kb)
; #pragma unroll
;                 for (int qb = 0; qb < NQB; ++qb) asm volatile("" : "+v"(c[kb][qb]));
.LBB0_990:
	v_exp_f32_e32 v177, v142
	v_exp_f32_e32 v178, v143
	v_exp_f32_e32 v179, v144
	v_exp_f32_e32 v180, v145
	v_exp_f32_e32 v181, v138
	v_exp_f32_e32 v182, v139
	v_exp_f32_e32 v183, v140
	v_exp_f32_e32 v184, v141
	v_exp_f32_e32 v185, v126
	v_exp_f32_e32 v186, v127
	v_exp_f32_e32 v188, v128
	v_exp_f32_e32 v190, v129
	v_exp_f32_e32 v193, v110
	v_exp_f32_e32 v194, v111
	v_exp_f32_e32 v203, v112
	v_exp_f32_e32 v205, v113
	v_add_f32_e32 v110, v177, v178
	v_add_f32_e32 v111, v179, v180
	v_exp_f32_e32 v187, v134
	v_exp_f32_e32 v197, v130
	v_exp_f32_e32 v208, v122
	v_exp_f32_e32 v212, v114
	v_add_f32_e32 v110, v110, v111
	v_add_f32_e32 v111, v181, v182
	v_add_f32_e32 v112, v183, v184
	v_add_f32_e32 v111, v111, v112
	v_add_f32_e32 v112, v185, v186
	v_add_f32_e32 v113, v188, v190
	v_exp_f32_e32 v189, v135
	v_exp_f32_e32 v204, v131
	v_exp_f32_e32 v209, v123
	v_exp_f32_e32 v213, v115
	v_add_f32_e32 v112, v112, v113
	v_add_f32_e32 v113, v193, v194
	v_add_f32_e32 v114, v203, v205
	v_add_f32_e32 v113, v113, v114
	v_exp_f32_e32 v191, v136
	v_exp_f32_e32 v206, v132
	v_exp_f32_e32 v210, v124
	v_exp_f32_e32 v214, v116
	v_add_f32_e32 v110, v187, v110
	v_add_f32_e32 v111, v197, v111
	v_add_f32_e32 v112, v208, v112
	v_add_f32_e32 v113, v212, v113
	s_waitcnt lgkmcnt(0)
	v_exp_f32_e32 v192, v137
	v_exp_f32_e32 v207, v133
	v_exp_f32_e32 v211, v125
	v_exp_f32_e32 v215, v117
	s_mov_b32 s5, s16
	v_add_f32_e32 v110, v189, v110
	v_add_f32_e32 v111, v204, v111
	v_add_f32_e32 v112, v209, v112
	v_add_f32_e32 v113, v213, v113
	s_mov_b32 s16, s38
	v_add_f32_e32 v110, v191, v110
	v_add_f32_e32 v111, v206, v111
	v_add_f32_e32 v112, v210, v112
	v_add_f32_e32 v113, v214, v113
	s_nop 0
	v_add_f32_e32 v173, v192, v110
	v_add_f32_e32 v172, v207, v111
	v_add_f32_e32 v171, v211, v112
	v_add_f32_e32 v170, v215, v113
	v_lshl_add_u32 v110, s4, 13, v175
	ds_read_b128 v[158:161], v110 offset:36864
	ds_read_b128 v[154:157], v110 offset:38912
	ds_read_b128 v[150:153], v110 offset:40960
	ds_read_b128 v[146:149], v110 offset:43008
	s_lshl_b32 s38, s5, 13
	s_add_i32 s38, s38, s36
	s_mov_b32 m0, s38
	s_nop 0
	global_load_lds_dwordx4 v[168:169], off
	s_min_u32 s38, s37, 3
	s_lshl_b32 s38, s38, 7
	v_lshl_add_u64 v[110:111], v[162:163], 0, s[38:39]
	s_lshl_b32 s38, s16, 13
	s_add_i32 s40, s38, s19
	s_mov_b32 m0, s40
	s_nop 0
	global_load_lds_dwordx4 v[110:111], off
	s_setprio 1
	v_mfma_f32_16x16x32_bf16 v[114:117], v[98:101], v[14:17], 0
	v_mfma_f32_16x16x32_bf16 v[122:125], v[98:101], v[30:33], 0
	v_mfma_f32_16x16x32_bf16 v[110:113], v[98:101], v[6:9], 0
	v_mfma_f32_16x16x32_bf16 v[130:133], v[98:101], v[58:61], 0
	v_mfma_f32_16x16x32_bf16 v[138:141], v[102:105], v[10:13], v[114:117]
	v_mfma_f32_16x16x32_bf16 v[126:129], v[102:105], v[18:21], v[122:125]
	v_mfma_f32_16x16x32_bf16 v[114:117], v[106:109], v[6:9], 0
	v_mfma_f32_16x16x32_bf16 v[122:125], v[106:109], v[14:17], 0
	v_mfma_f32_16x16x32_bf16 v[216:219], v[106:109], v[30:33], 0
	v_mfma_f32_16x16x32_bf16 v[236:239], v[106:109], v[58:61], 0
	v_mfma_f32_16x16x32_bf16 v[142:145], v[102:105], v[2:5], v[110:113]
	v_mfma_f32_16x16x32_bf16 v[110:113], v[102:105], v[86:89], v[130:133]
	v_mfma_f32_16x16x32_bf16 v[134:137], v[118:121], v[2:5], v[114:117]
	v_mfma_f32_16x16x32_bf16 v[130:133], v[118:121], v[10:13], v[122:125]
	v_mfma_f32_16x16x32_bf16 v[122:125], v[118:121], v[18:21], v[216:219]
	v_mfma_f32_16x16x32_bf16 v[114:117], v[118:121], v[86:89], v[236:239]
	s_andn2_b64 vcc, exec, s[6:7]
	s_cbranch_vccnz .LBB0_992
	v_add_u32_e32 v106, s38, v174
	v_add_u32_e32 v118, s38, v176
	ds_read_b128 v[98:101], v106
	ds_read_b128 v[102:105], v118
	ds_read_b128 v[106:109], v106 offset:512
	ds_read_b128 v[118:121], v118 offset:512
	v_cvt_pk_bf16_f32 v215, v214, v215
	v_cvt_pk_bf16_f32 v214, v212, v213
	v_cvt_pk_bf16_f32 v213, v203, v205
	v_cvt_pk_bf16_f32 v212, v193, v194
	v_cvt_pk_bf16_f32 v211, v210, v211
	v_cvt_pk_bf16_f32 v210, v208, v209
	v_cvt_pk_bf16_f32 v209, v188, v190
	v_cvt_pk_bf16_f32 v208, v185, v186
	v_cvt_pk_bf16_f32 v207, v206, v207
	v_cvt_pk_bf16_f32 v206, v197, v204
	v_cvt_pk_bf16_f32 v205, v183, v184
	v_cvt_pk_bf16_f32 v204, v181, v182
	v_cvt_pk_bf16_f32 v183, v191, v192
	v_cvt_pk_bf16_f32 v182, v187, v189
	v_cvt_pk_bf16_f32 v181, v179, v180
	v_cvt_pk_bf16_f32 v180, v177, v178
	s_waitcnt lgkmcnt(7)
	s_nop 0
	v_mfma_f32_16x16x32_bf16 v[94:97], v[158:161], v[180:183], v[94:97]
	v_mfma_f32_16x16x32_bf16 v[90:93], v[158:161], v[204:207], v[90:93]
	v_mfma_f32_16x16x32_bf16 v[82:85], v[158:161], v[208:211], v[82:85]
	v_mfma_f32_16x16x32_bf16 v[78:81], v[158:161], v[212:215], v[78:81]
	s_waitcnt lgkmcnt(6)
	v_mfma_f32_16x16x32_bf16 v[74:77], v[154:157], v[180:183], v[74:77]
	v_mfma_f32_16x16x32_bf16 v[70:73], v[154:157], v[204:207], v[70:73]
	v_mfma_f32_16x16x32_bf16 v[66:69], v[154:157], v[208:211], v[66:69]
	v_mfma_f32_16x16x32_bf16 v[62:65], v[154:157], v[212:215], v[62:65]
	s_waitcnt lgkmcnt(5)
	v_mfma_f32_16x16x32_bf16 v[54:57], v[150:153], v[180:183], v[54:57]
	v_mfma_f32_16x16x32_bf16 v[50:53], v[150:153], v[204:207], v[50:53]
	v_mfma_f32_16x16x32_bf16 v[46:49], v[150:153], v[208:211], v[46:49]
	v_mfma_f32_16x16x32_bf16 v[42:45], v[150:153], v[212:215], v[42:45]
	s_waitcnt lgkmcnt(4)
	v_mfma_f32_16x16x32_bf16 v[38:41], v[146:149], v[180:183], v[38:41]
	v_mfma_f32_16x16x32_bf16 v[34:37], v[146:149], v[204:207], v[34:37]
	v_mfma_f32_16x16x32_bf16 v[26:29], v[146:149], v[208:211], v[26:29]
	v_mfma_f32_16x16x32_bf16 v[22:25], v[146:149], v[212:215], v[22:25]

; #define ATT_DMA_K(t, sl) do { glds16(ksrc + (size_t)(t) * 64 * kpitch, (unsigned)__builtin_amdgcn_readfirstlane(kdst + (sl) * KSLOT)); \
;         if constexpr (DQK == 96) glds16(krsrc + (size_t)(t) * 64 * 32, (unsigned)__builtin_amdgcn_readfirstlane(krdst + (sl) * KSLOT)); } while (0)
; #define ATT_DMA_V(t, sl) do { glds16(vsrc + (size_t)(t) * 64, (unsigned)__builtin_amdgcn_readfirstlane(vdst + (sl) * VSLOT)); \
;         if constexpr (DV == 128) glds16(vsrc + (size_t)64 * NR + (size_t)(t) * 64, (unsigned)__builtin_amdgcn_readfirstlane(vdst + (sl) * VSLOT + 8192)); } while (0)
; template <int DQK, int DV, bool LEAD> ...
;     ...
;     ATT_DMA_K(0, 0); ATT_DMA_V(0, 0); ATT_DMA_K(1, 1); ATT_DMA_K(2, 2);
;     bf16x8 qf[NQB * NDS];
;     {
;       const float c2 = (DQK == 64) ? C2_EVEN : C2_ODD; const bool lat = tq0 >= 0;
; #pragma unroll
;       for (int qb = 0; qb < NQB; ++qb) {
;           const bf16_t* qp = Q + (size_t)(qrow0 + qoff + qb * 16 + q16) * qpitch + g4 * 8;
;           bf16x8 raw[NDS];
; #pragma unroll
;           for (int ds = 0; ds < NDS; ++ds) raw[ds] = *(const bf16x8*)(qp + ds * 32);
;           float x[NDS][8];
; #pragma unroll
;           for (int ds = 0; ds < NDS; ++ds)
; #pragma unroll
;               for (int j = 0; j < 8; ++j) x[ds][j] = __uint_as_float(((unsigned)(unsigned short)raw[ds][j]) << 16);
.LBB0_995:
	s_and_b64 vcc, exec, s[4:5]
	s_cbranch_vccz .LBB0_986
	v_mov_b32_e32 v84, v0
	s_mov_b32 s19, s39
	v_readfirstlane_b32 s16, v84
	s_ashr_i32 s4, s16, 6
	v_bfe_u32 v1, v84, 3, 3
	v_lshl_or_b32 v6, s4, 3, v1
	s_lshl_b32 s5, s4, 1
	s_lshr_b32 s6, s16, 5
	v_ashrrev_i32_e32 v2, 1, v6
	s_and_b32 s5, s5, 2
	s_and_b32 s6, s6, 4
	v_and_b32_e32 v170, 7, v84
	v_and_b32_e32 v3, 1, v2
	s_or_b32 s5, s5, s6
	s_and_b32 s7, s4, 3
	v_bitop3_b32 v7, s5, v170, v3 bitop3:0x36
	v_xor_b32_e32 v8, v2, v84
	v_add_u32_e32 v4, s18, v6
	s_lshl_b32 s4, s4, 10
	v_mov_b64_e32 v[2:3], s[22:23]
	s_add_i32 s31, s4, 0
	v_mad_i64_i32 v[2:3], s[4:5], v4, s92, v[2:3]
	v_mov_b64_e32 v[4:5], s[26:27]
	v_lshlrev_b32_e32 v194, 4, v7
	v_mad_i64_i32 v[4:5], s[4:5], v6, s91, v[4:5]
	v_lshl_add_u64 v[42:43], v[2:3], 0, v[194:195]
	v_lshlrev_b32_e32 v2, 4, v8
	v_lshl_add_u64 v[4:5], s[18:19], 1, v[4:5]
	v_and_b32_e32 v194, 0x70, v2
	s_mov_b32 m0, s31
	s_nop 0
	global_load_lds_dwordx4 v[42:43], off
	v_lshl_add_u64 v[162:163], v[4:5], 0, v[194:195]
	s_add_i32 s19, s31, 0x9000
	s_mov_b32 m0, s19
	s_nop 0
	global_load_lds_dwordx4 v[162:163], off
	s_mov_b64 s[22:23], 0x38000
	v_lshl_add_u64 v[2:3], v[42:43], 0, s[22:23]
	s_add_i32 s5, s31, 0x2000
	s_mov_b32 m0, s5
	s_nop 0
	global_load_lds_dwordx4 v[2:3], off
	s_mov_b64 s[22:23], 0x70000
	s_lshl_b32 s4, s7, 6
	v_lshl_add_u64 v[2:3], v[42:43], 0, s[22:23]
	s_add_i32 s5, s31, 0x4000
	s_mov_b32 m0, s5
	s_nop 0
	global_load_lds_dwordx4 v[2:3], off
	v_and_b32_e32 v83, 15, v84
	s_or_b32 s6, s4, s18
	v_or_b32_e32 v18, s6, v83
	v_and_b32_e32 v194, 48, v84
	v_lshl_add_u64 v[10:11], s[12:13], 0, v[194:195]
	v_or_b32_e32 v16, 32, v18
	v_mad_u64_u32 v[16:17], s[4:5], v16, s92, v[10:11]
	global_load_dwordx4 v[34:37], v[16:17], off offset:64
	v_mad_u64_u32 v[12:13], s[4:5], v18, s92, v[10:11]
	v_or_b32_e32 v6, 16, v18
	v_or_b32_e32 v18, 48, v18
	global_load_dwordx4 v[2:5], v[12:13], off offset:64
	v_mad_u64_u32 v[14:15], s[4:5], v6, s92, v[10:11]
	v_mad_u64_u32 v[10:11], s[4:5], v18, s92, v[10:11]
	global_load_dwordx4 v[6:9], v[14:15], off offset:64
	global_load_dwordx4 v[38:41], v[10:11], off offset:64
	global_load_dwordx4 v[64:67], v[12:13], off
	global_load_dwordx4 v[86:89], v[14:15], off
	global_load_dwordx4 v[18:21], v[16:17], off
	s_nop 0
	global_load_dwordx4 v[14:17], v[10:11], off
	v_bfe_u32 v171, v84, 4, 2
	s_waitcnt vmcnt(8)
	v_lshlrev_b32_e32 v52, 5, v171
	global_load_dwordx4 v[26:29], v52, s[8:9] offset:144
	global_load_dwordx4 v[30:33], v52, s[8:9] offset:128
	s_lshl_b32 s4, s16, 4
	v_lshlrev_b32_e32 v172, 1, v84
	v_and_b32_e32 v10, 3, v84
	v_lshrrev_b32_e32 v11, 1, v84
	s_and_b32 s4, s4, 0xfffff000
	v_and_or_b32 v10, v172, 24, v10
	v_bitop3_b32 v11, v171, v11, 7 bitop3:0x78
	s_add_i32 s4, s4, 0
	v_lshlrev_b32_e32 v82, 4, v11
	v_lshl_add_u32 v85, v10, 7, s4
	s_mov_b32 s4, 0x358637bd
	v_and_b32_e32 v173, 63, v84
	v_add_u32_e32 v174, v85, v82
	v_lshl_add_u64 v[168:169], v[42:43], 0, s[96:97]
	s_mov_b32 s12, 2
	v_or_b32_e32 v175, 4, v171
	v_lshlrev_b32_e32 v176, 7, v83
	s_mov_b32 s13, 0
	s_waitcnt vmcnt(9)
	v_and_b32_e32 v23, 0xffff0000, v37
	v_lshlrev_b32_e32 v22, 16, v37
	v_and_b32_e32 v25, 0xffff0000, v36
	v_lshlrev_b32_e32 v24, 16, v36
	v_and_b32_e32 v57, 0xffff0000, v35
	v_lshlrev_b32_e32 v56, 16, v35
	v_and_b32_e32 v59, 0xffff0000, v34
	s_waitcnt vmcnt(6)
	v_and_b32_e32 v45, 0xffff0000, v41
	v_lshlrev_b32_e32 v44, 16, v41
	v_and_b32_e32 v47, 0xffff0000, v40
	v_lshlrev_b32_e32 v46, 16, v40
	v_and_b32_e32 v49, 0xffff0000, v39
	v_lshlrev_b32_e32 v48, 16, v39
	v_lshlrev_b32_e32 v58, 16, v34
	v_and_b32_e32 v51, 0xffff0000, v38
	v_lshlrev_b32_e32 v50, 16, v38
	global_load_dwordx4 v[34:37], v52, s[8:9] offset:16
	global_load_dwordx4 v[38:41], v52, s[8:9]
	s_waitcnt vmcnt(6)
	v_and_b32_e32 v75, 0xffff0000, v89
	v_lshlrev_b32_e32 v74, 16, v89
	v_and_b32_e32 v89, 0xffff0000, v64
	v_and_b32_e32 v93, 0xffff0000, v2
	v_lshlrev_b32_e32 v92, 16, v2
	v_and_b32_e32 v77, 0xffff0000, v88
	v_lshlrev_b32_e32 v76, 16, v88
	v_lshlrev_b32_e32 v88, 16, v64
	v_mul_f32_e32 v2, v89, v89
	v_and_b32_e32 v11, 0xffff0000, v9
	v_lshlrev_b32_e32 v10, 16, v9
	v_and_b32_e32 v69, 0xffff0000, v8
	v_lshlrev_b32_e32 v68, 16, v8
	v_and_b32_e32 v9, 0xffff0000, v3
	v_lshlrev_b32_e32 v8, 16, v3
	s_waitcnt vmcnt(4)
; template <int DQK, int DV, bool LEAD> ...
;     ...
;           float sn = 0.f;
; #pragma unroll
;           for (int ds = 0; ds < 2; ++ds)
; #pragma unroll
;               for (int j = 0; j < 8; ++j) sn += x[ds][j] * x[ds][j];
;           sn = lanes4_sum(sn);
;           const float rn = rsqrtf(sn * (1.f / 64.f) + EPS);
; #pragma unroll
;           for (int ds = 0; ds < 2; ++ds)
; #pragma unroll
;               for (int j = 0; j < 8; ++j) x[ds][j] *= rn * qgain[32 * ds + 8 * g4 + j];
;           if constexpr (DQK == 64) {
; #pragma unroll
;               for (int ds = 0; ds < 2; ++ds)
; #pragma unroll
;                   for (int j = 0; j < 8; ++j) {
;                       auto rr = __builtin_amdgcn_permlane32_swap(__float_as_uint(x[ds][j]), __float_as_uint(x[ds][j]), false, false);
;                       const float other = hi ? __uint_as_float(rr[0]) : __uint_as_float(rr[1]);
;                       float cc = 1.f, sg = 0.f;
;                       if (lat) { const f32x2 cs = rope[(ds ? pcol : prow) * 16 + 8 * (g4 & 1) + j]; cc = cs.x; sg = hi ? cs.y : -cs.y; }
;                       x[ds][j] = x[ds][j] * cc + other * sg; }
;           } else {
;               float sr = 0.f;
; #pragma unroll
;               for (int j = 0; j < 8; ++j) sr += x[2][j] * x[2][j];
;               sr = lanes4_sum(sr);
;               const float rq = rsqrtf(sr * (1.f / 32.f) + EPS);
; #pragma unroll
;               for (int j = 0; j < 8; ++j) { const float av = x[2][j] * rq * qgain[64 + 8 * g4 + j];
;                   auto rr = __builtin_amdgcn_permlane16_swap(__float_as_uint(av), __float_as_uint(av), false, false);
;                   const float other = (g4 & 1) ? __uint_as_float(rr[0]) : __uint_as_float(rr[1]);
;                   float cc = 1.f, sg = 0.f;
;                   if (lat) { const f32x2 cs = rope[((g4 & 2) ? pcol : prow) * 8 + j]; cc = cs.x; sg = (g4 & 1) ? cs.y : -cs.y; }
;                   x[2][j] = av * cc + other * sg; }
;           }
; #pragma unroll
;           for (int ds = 0; ds < NDS; ++ds) { u32x4 w;
; #pragma unroll
;               for (int i = 0; i < 4; ++i) w[i] = cvtpk(x[ds][2 * i] * c2, x[ds][2 * i + 1] * c2);
;               qf[qb * NDS + ds] = __builtin_bit_cast(bf16x8, w); }
	v_and_b32_e32 v53, 0xffff0000, v17
	v_lshlrev_b32_e32 v52, 16, v17
	v_and_b32_e32 v55, 0xffff0000, v16
	v_lshlrev_b32_e32 v54, 16, v16
	v_and_b32_e32 v17, 0xffff0000, v65
	v_lshlrev_b32_e32 v16, 16, v65
	v_pk_fma_f32 v[2:3], v[88:89], v[88:89], v[2:3] op_sel_hi:[1,1,0]
	v_and_b32_e32 v91, 0xffff0000, v4
	v_lshlrev_b32_e32 v90, 16, v4
	v_pk_fma_f32 v[2:3], v[16:17], v[16:17], v[2:3]
	v_mul_f32_e32 v4, v17, v17
	v_and_b32_e32 v95, 0xffff0000, v66
	v_lshlrev_b32_e32 v94, 16, v66
	v_pk_add_f32 v[2:3], v[4:5], v[2:3] op_sel_hi:[0,1]
	v_pk_fma_f32 v[2:3], v[94:95], v[94:95], v[2:3]
	v_mul_f32_e32 v4, v95, v95
	v_and_b32_e32 v71, 0xffff0000, v7
	v_lshlrev_b32_e32 v70, 16, v7
	v_and_b32_e32 v73, 0xffff0000, v6
	v_lshlrev_b32_e32 v72, 16, v6
	v_and_b32_e32 v7, 0xffff0000, v67
	v_lshlrev_b32_e32 v6, 16, v67
	v_pk_add_f32 v[2:3], v[4:5], v[2:3] op_sel_hi:[0,1]
	v_pk_fma_f32 v[2:3], v[6:7], v[6:7], v[2:3]
	v_mul_f32_e32 v4, v7, v7
	v_pk_add_f32 v[2:3], v[4:5], v[2:3] op_sel_hi:[0,1]
	v_pk_fma_f32 v[2:3], v[92:93], v[92:93], v[2:3]
	v_mul_f32_e32 v4, v93, v93
	v_pk_add_f32 v[2:3], v[4:5], v[2:3] op_sel_hi:[0,1]
	v_pk_fma_f32 v[2:3], v[8:9], v[8:9], v[2:3]
	v_mul_f32_e32 v4, v9, v9
	v_pk_add_f32 v[2:3], v[4:5], v[2:3] op_sel_hi:[0,1]
	v_pk_fma_f32 v[2:3], v[90:91], v[90:91], v[2:3]
	v_mul_f32_e32 v4, v91, v91
	v_and_b32_e32 v13, 0xffff0000, v5
	v_lshlrev_b32_e32 v12, 16, v5
	v_pk_add_f32 v[2:3], v[4:5], v[2:3] op_sel_hi:[0,1]
	v_pk_fma_f32 v[2:3], v[12:13], v[12:13], v[2:3]
	v_mul_f32_e32 v4, v13, v13
	v_pk_add_f32 v[2:3], v[4:5], v[2:3] op_sel_hi:[0,1]
	v_mov_b32_e32 v3, v2
	s_nop 1
	v_permlane16_swap_b32_e32 v2, v3
	v_add_f32_e32 v3, v2, v3
	v_mov_b32_e32 v5, v3
	v_and_b32_e32 v81, 0xffff0000, v86
	s_nop 0
	v_permlane32_swap_b32_e32 v3, v5
	v_lshlrev_b32_e32 v80, 16, v86
	v_mul_f32_e32 v2, v81, v81
	v_and_b32_e32 v61, 0xffff0000, v21
	v_lshlrev_b32_e32 v60, 16, v21
	v_and_b32_e32 v63, 0xffff0000, v20
	v_lshlrev_b32_e32 v62, 16, v20
	v_and_b32_e32 v79, 0xffff0000, v87
	v_lshlrev_b32_e32 v78, 16, v87
	v_pk_fma_f32 v[20:21], v[80:81], v[80:81], v[2:3] op_sel_hi:[1,1,0]
	v_mul_f32_e32 v2, v79, v79
	v_pk_fma_f32 v[20:21], v[78:79], v[78:79], v[20:21]
	s_mov_b32 s8, 0x3c800000
	v_pk_add_f32 v[20:21], v[2:3], v[20:21] op_sel_hi:[0,1]
	v_pk_fma_f32 v[20:21], v[76:77], v[76:77], v[20:21]
	v_mul_f32_e32 v2, v77, v77
	v_pk_add_f32 v[20:21], v[2:3], v[20:21] op_sel_hi:[0,1]
	v_pk_fma_f32 v[20:21], v[74:75], v[74:75], v[20:21]
	v_mul_f32_e32 v2, v75, v75
	v_pk_add_f32 v[20:21], v[2:3], v[20:21] op_sel_hi:[0,1]
	v_pk_fma_f32 v[20:21], v[72:73], v[72:73], v[20:21]
	v_mul_f32_e32 v2, v73, v73
	v_pk_add_f32 v[20:21], v[2:3], v[20:21] op_sel_hi:[0,1]
	v_pk_fma_f32 v[20:21], v[70:71], v[70:71], v[20:21]
	v_mul_f32_e32 v2, v71, v71
	v_pk_add_f32 v[20:21], v[2:3], v[20:21] op_sel_hi:[0,1]
	v_pk_fma_f32 v[20:21], v[68:69], v[68:69], v[20:21]
	v_mul_f32_e32 v2, v69, v69
	v_pk_add_f32 v[20:21], v[2:3], v[20:21] op_sel_hi:[0,1]
	v_pk_fma_f32 v[20:21], v[10:11], v[10:11], v[20:21]
	v_mul_f32_e32 v2, v11, v11
	v_pk_add_f32 v[20:21], v[2:3], v[20:21] op_sel_hi:[0,1]
	v_mov_b32_e32 v2, v20
	s_nop 1
	v_permlane16_swap_b32_e32 v20, v2
	v_add_f32_e32 v2, v20, v2
	v_mov_b32_e32 v4, v2
	s_nop 1
	v_permlane32_swap_b32_e32 v2, v4
	v_pk_add_f32 v[2:3], v[2:3], v[4:5]
	v_mov_b64_e32 v[20:21], s[4:5]
	v_pk_fma_f32 v[86:87], v[2:3], s[8:9], v[20:21] op_sel_hi:[1,0,0]
	v_and_b32_e32 v67, 0xffff0000, v15
	v_mul_f32_e32 v2, 0x4b800000, v87
	v_cmp_gt_f32_e32 vcc, s95, v87
	v_lshlrev_b32_e32 v66, 16, v15
	v_cmp_gt_f32_e64 s[4:5], s95, v86
	v_cndmask_b32_e32 v2, v87, v2, vcc
	v_rsq_f32_e32 v2, v2
	v_and_b32_e32 v65, 0xffff0000, v19
	v_lshlrev_b32_e32 v64, 16, v19
	v_mul_f32_e32 v3, 0x45800000, v2
	v_cndmask_b32_e32 v96, v2, v3, vcc
	s_waitcnt vmcnt(3)
	v_pk_mul_f32 v[2:3], v[96:97], v[28:29] op_sel_hi:[0,1]
	v_pk_mul_f32 v[2:3], v[2:3], v[12:13]
	v_cmp_gt_u32_e32 vcc, 32, v173
	v_mov_b32_e32 v4, v2
	v_mov_b32_e32 v12, v2
	v_mov_b32_e32 v5, v3
	v_mov_b32_e32 v13, v3
	v_permlane32_swap_b32_e32 v4, v12
	s_nop 0
	v_permlane32_swap_b32_e32 v5, v13
	v_cndmask_b32_e32 v5, v5, v13, vcc
	v_cndmask_b32_e32 v4, v4, v12, vcc
	v_pk_fma_f32 v[2:3], v[4:5], 0, v[2:3] op_sel_hi:[1,0,1]
	s_nop 0
	v_pk_mul_f32 v[2:3], v[2:3], s[94:95] op_sel_hi:[1,0]
	s_nop 0
	v_cvt_pk_bf16_f32 v5, v2, v3
	v_pk_mul_f32 v[2:3], v[96:97], v[26:27] op_sel_hi:[0,1]
	v_pk_mul_f32 v[2:3], v[2:3], v[90:91]
	s_nop 0
	v_mov_b32_e32 v4, v2
	v_mov_b32_e32 v12, v2
	v_mov_b32_e32 v13, v3
	v_mov_b32_e32 v15, v3
	v_permlane32_swap_b32_e32 v4, v12
	s_nop 0
	v_permlane32_swap_b32_e32 v13, v15
	v_cndmask_b32_e32 v13, v13, v15, vcc
	v_cndmask_b32_e32 v12, v4, v12, vcc
	v_pk_fma_f32 v[2:3], v[12:13], 0, v[2:3] op_sel_hi:[1,0,1]
	s_nop 0
	v_pk_mul_f32 v[2:3], v[2:3], s[94:95] op_sel_hi:[1,0]
	s_nop 0
	v_cvt_pk_bf16_f32 v4, v2, v3
	s_waitcnt vmcnt(2)
	v_pk_mul_f32 v[2:3], v[96:97], v[32:33] op_sel_hi:[0,1]
	v_pk_mul_f32 v[2:3], v[2:3], v[8:9]
	s_nop 0
	v_mov_b32_e32 v8, v2
	v_mov_b32_e32 v12, v2
	v_mov_b32_e32 v9, v3
	v_mov_b32_e32 v13, v3
	v_permlane32_swap_b32_e32 v8, v12
	s_nop 0
	v_permlane32_swap_b32_e32 v9, v13
	v_cndmask_b32_e32 v9, v9, v13, vcc
	v_cndmask_b32_e32 v8, v8, v12, vcc
	v_pk_fma_f32 v[2:3], v[8:9], 0, v[2:3] op_sel_hi:[1,0,1]
	v_pk_mul_f32 v[8:9], v[30:31], v[96:97] op_sel_hi:[1,0]
	v_pk_mul_f32 v[2:3], v[2:3], s[94:95] op_sel_hi:[1,0]
	v_pk_mul_f32 v[8:9], v[8:9], v[92:93]
	v_cvt_pk_bf16_f32 v3, v2, v3
	v_mov_b32_e32 v2, v8
	v_mov_b32_e32 v12, v8
	v_mov_b32_e32 v13, v9
	v_mov_b32_e32 v15, v9
	v_permlane32_swap_b32_e32 v2, v12
	s_nop 0
	v_permlane32_swap_b32_e32 v13, v15
	v_cndmask_b32_e32 v13, v13, v15, vcc
	v_cndmask_b32_e32 v12, v2, v12, vcc
	v_pk_fma_f32 v[8:9], v[12:13], 0, v[8:9] op_sel_hi:[1,0,1]
	s_nop 0
	v_pk_mul_f32 v[8:9], v[8:9], s[94:95] op_sel_hi:[1,0]
	s_nop 0
	v_cvt_pk_bf16_f32 v2, v8, v9
	s_waitcnt vmcnt(1)
; __device__ __forceinline__ unsigned cvtpk(float lo, float hi) { f32x2 v = {lo, hi}; bf16x2_t b = __builtin_convertvector(v, bf16x2_t); return __builtin_bit_cast(unsigned, b); }
; template <int DQK, int DV, bool LEAD> ...
;     ...
;               for (int j = 0; j < 8; ++j) x[ds][j] *= rn * qgain[32 * ds + 8 * g4 + j];
;           if constexpr (DQK == 64) {
; #pragma unroll
;               for (int ds = 0; ds < 2; ++ds)
; #pragma unroll
;                   for (int j = 0; j < 8; ++j) {
;                       auto rr = __builtin_amdgcn_permlane32_swap(__float_as_uint(x[ds][j]), __float_as_uint(x[ds][j]), false, false);
;                       const float other = hi ? __uint_as_float(rr[0]) : __uint_as_float(rr[1]);
;                       float cc = 1.f, sg = 0.f;
;                       if (lat) { const f32x2 cs = rope[(ds ? pcol : prow) * 16 + 8 * (g4 & 1) + j]; cc = cs.x; sg = hi ? cs.y : -cs.y; }
;                       x[ds][j] = x[ds][j] * cc + other * sg; }
;           } else {
;               float sr = 0.f;
; #pragma unroll
;               for (int j = 0; j < 8; ++j) sr += x[2][j] * x[2][j];
;               sr = lanes4_sum(sr);
;               const float rq = rsqrtf(sr * (1.f / 32.f) + EPS);
; #pragma unroll
;               for (int j = 0; j < 8; ++j) { const float av = x[2][j] * rq * qgain[64 + 8 * g4 + j];
;                   auto rr = __builtin_amdgcn_permlane16_swap(__float_as_uint(av), __float_as_uint(av), false, false);
;                   const float other = (g4 & 1) ? __uint_as_float(rr[0]) : __uint_as_float(rr[1]);
;                   float cc = 1.f, sg = 0.f;
;                   if (lat) { const f32x2 cs = rope[((g4 & 2) ? pcol : prow) * 8 + j]; cc = cs.x; sg = (g4 & 1) ? cs.y : -cs.y; }
;                   x[2][j] = av * cc + other * sg; }
;           }
; #pragma unroll
;           for (int ds = 0; ds < NDS; ++ds) { u32x4 w;
; #pragma unroll
;               for (int i = 0; i < 4; ++i) w[i] = cvtpk(x[ds][2 * i] * c2, x[ds][2 * i + 1] * c2);
;               qf[qb * NDS + ds] = __builtin_bit_cast(bf16x8, w); }
	v_pk_mul_f32 v[8:9], v[36:37], v[96:97] op_sel_hi:[1,0]
	s_nop 0
	v_pk_mul_f32 v[6:7], v[8:9], v[6:7]
	s_nop 0
	v_mov_b32_e32 v8, v6
	v_mov_b32_e32 v12, v6
	v_mov_b32_e32 v9, v7
	v_mov_b32_e32 v13, v7
	v_permlane32_swap_b32_e32 v8, v12
	s_nop 0
	v_permlane32_swap_b32_e32 v9, v13
	v_cndmask_b32_e32 v9, v9, v13, vcc
	v_cndmask_b32_e32 v8, v8, v12, vcc
	v_pk_fma_f32 v[6:7], v[8:9], 0, v[6:7] op_sel_hi:[1,0,1]
	s_nop 0
	v_pk_mul_f32 v[6:7], v[6:7], s[94:95] op_sel_hi:[1,0]
	s_nop 0
	v_cvt_pk_bf16_f32 v9, v6, v7
	v_pk_mul_f32 v[6:7], v[34:35], v[96:97] op_sel_hi:[1,0]
	s_nop 0
	v_pk_mul_f32 v[6:7], v[6:7], v[94:95]
	s_nop 0
	v_mov_b32_e32 v8, v6
	v_mov_b32_e32 v12, v6
	v_mov_b32_e32 v13, v7
	v_mov_b32_e32 v15, v7
	v_permlane32_swap_b32_e32 v8, v12
	s_nop 0
	v_permlane32_swap_b32_e32 v13, v15
	v_cndmask_b32_e32 v13, v13, v15, vcc
	v_cndmask_b32_e32 v12, v8, v12, vcc
	v_pk_fma_f32 v[6:7], v[12:13], 0, v[6:7] op_sel_hi:[1,0,1]
	s_nop 0
	v_pk_mul_f32 v[6:7], v[6:7], s[94:95] op_sel_hi:[1,0]
	s_nop 0
	v_cvt_pk_bf16_f32 v8, v6, v7
	s_waitcnt vmcnt(0)
	v_pk_mul_f32 v[6:7], v[40:41], v[96:97] op_sel_hi:[1,0]
	s_nop 0
	v_pk_mul_f32 v[6:7], v[6:7], v[16:17]
	s_nop 0
	v_mov_b32_e32 v12, v6
	v_mov_b32_e32 v15, v6
	v_mov_b32_e32 v13, v7
	v_mov_b32_e32 v16, v7
	v_permlane32_swap_b32_e32 v12, v15
	s_nop 0
	v_permlane32_swap_b32_e32 v13, v16
	v_cndmask_b32_e32 v13, v13, v16, vcc
	v_cndmask_b32_e32 v12, v12, v15, vcc
	v_pk_fma_f32 v[6:7], v[12:13], 0, v[6:7] op_sel_hi:[1,0,1]
	v_pk_mul_f32 v[12:13], v[38:39], v[96:97] op_sel_hi:[1,0]
	v_pk_mul_f32 v[6:7], v[6:7], s[94:95] op_sel_hi:[1,0]
	v_pk_mul_f32 v[12:13], v[12:13], v[88:89]
	v_cvt_pk_bf16_f32 v7, v6, v7
	v_mov_b32_e32 v6, v12
	v_mov_b32_e32 v15, v12
	v_mov_b32_e32 v16, v13
	v_mov_b32_e32 v17, v13
	v_permlane32_swap_b32_e32 v6, v15
	s_nop 0
	v_permlane32_swap_b32_e32 v16, v17
	v_cndmask_b32_e32 v17, v16, v17, vcc
	v_cndmask_b32_e32 v16, v6, v15, vcc
	v_mul_f32_e32 v6, 0x4b800000, v86
	v_cndmask_b32_e64 v6, v86, v6, s[4:5]
	v_rsq_f32_e32 v15, v6
	v_pk_fma_f32 v[12:13], v[16:17], 0, v[12:13] op_sel_hi:[1,0,1]
	s_nop 0
	v_pk_mul_f32 v[12:13], v[12:13], s[94:95] op_sel_hi:[1,0]
	s_nop 0
	v_cvt_pk_bf16_f32 v6, v12, v13
	v_mul_f32_e32 v12, 0x45800000, v15
	v_cndmask_b32_e64 v86, v15, v12, s[4:5]
	v_pk_mul_f32 v[12:13], v[28:29], v[86:87] op_sel_hi:[1,0]
	s_nop 0
	v_pk_mul_f32 v[10:11], v[12:13], v[10:11]
	s_nop 0
	v_mov_b32_e32 v12, v10
	v_mov_b32_e32 v15, v10
	v_mov_b32_e32 v13, v11
	v_mov_b32_e32 v16, v11
	v_permlane32_swap_b32_e32 v12, v15
	s_nop 0
	v_permlane32_swap_b32_e32 v13, v16
	v_cndmask_b32_e32 v13, v13, v16, vcc
	v_cndmask_b32_e32 v12, v12, v15, vcc
	v_pk_fma_f32 v[10:11], v[12:13], 0, v[10:11] op_sel_hi:[1,0,1]
	s_nop 0
	v_pk_mul_f32 v[10:11], v[10:11], s[94:95] op_sel_hi:[1,0]
	s_nop 0
	v_cvt_pk_bf16_f32 v13, v10, v11
	v_pk_mul_f32 v[10:11], v[26:27], v[86:87] op_sel_hi:[1,0]
	s_nop 0
	v_pk_mul_f32 v[10:11], v[10:11], v[68:69]
	s_nop 0
	v_mov_b32_e32 v12, v10
	v_mov_b32_e32 v15, v10
	v_mov_b32_e32 v16, v11
	v_mov_b32_e32 v17, v11
	v_permlane32_swap_b32_e32 v12, v15
	s_nop 0
	v_permlane32_swap_b32_e32 v16, v17
	v_cndmask_b32_e32 v17, v16, v17, vcc
	v_cndmask_b32_e32 v16, v12, v15, vcc
	v_pk_fma_f32 v[10:11], v[16:17], 0, v[10:11] op_sel_hi:[1,0,1]
	s_nop 0
	v_pk_mul_f32 v[10:11], v[10:11], s[94:95] op_sel_hi:[1,0]
	s_nop 0
	v_cvt_pk_bf16_f32 v12, v10, v11
	v_pk_mul_f32 v[10:11], v[32:33], v[86:87] op_sel_hi:[1,0]
	s_nop 0
	v_pk_mul_f32 v[10:11], v[10:11], v[70:71]
	s_nop 0
	v_mov_b32_e32 v15, v10
	v_mov_b32_e32 v16, v10
	v_mov_b32_e32 v17, v11
	v_mov_b32_e32 v19, v11
	v_permlane32_swap_b32_e32 v15, v16
	s_nop 0
	v_permlane32_swap_b32_e32 v17, v19
	v_cndmask_b32_e32 v17, v17, v19, vcc
	v_cndmask_b32_e32 v16, v15, v16, vcc
	v_pk_fma_f32 v[10:11], v[16:17], 0, v[10:11] op_sel_hi:[1,0,1]
	v_pk_mul_f32 v[16:17], v[30:31], v[86:87] op_sel_hi:[1,0]
	v_pk_mul_f32 v[10:11], v[10:11], s[94:95] op_sel_hi:[1,0]
	v_pk_mul_f32 v[16:17], v[16:17], v[72:73]
	v_cvt_pk_bf16_f32 v11, v10, v11
	v_mov_b32_e32 v10, v16
	v_mov_b32_e32 v15, v16
	v_mov_b32_e32 v19, v17
	v_mov_b32_e32 v68, v17
	v_permlane32_swap_b32_e32 v10, v15
	s_nop 0
	v_permlane32_swap_b32_e32 v19, v68
	v_cndmask_b32_e32 v69, v19, v68, vcc
	v_cndmask_b32_e32 v68, v10, v15, vcc
	v_pk_fma_f32 v[16:17], v[68:69], 0, v[16:17] op_sel_hi:[1,0,1]
	v_and_b32_e32 v73, 0xffff0000, v18
	v_pk_mul_f32 v[16:17], v[16:17], s[94:95] op_sel_hi:[1,0]
	s_nop 0
	v_cvt_pk_bf16_f32 v10, v16, v17
	v_pk_mul_f32 v[16:17], v[36:37], v[86:87] op_sel_hi:[1,0]
	s_nop 0
	v_pk_mul_f32 v[16:17], v[16:17], v[74:75]
	v_mul_f32_e32 v74, v65, v65
	v_mov_b32_e32 v15, v16
	v_mov_b32_e32 v19, v16
	v_mov_b32_e32 v68, v17
	v_mov_b32_e32 v69, v17
	v_permlane32_swap_b32_e32 v15, v19
	s_nop 0
	v_permlane32_swap_b32_e32 v68, v69
	v_cndmask_b32_e32 v69, v68, v69, vcc
	v_cndmask_b32_e32 v68, v15, v19, vcc
	v_pk_fma_f32 v[16:17], v[68:69], 0, v[16:17] op_sel_hi:[1,0,1]
	v_pk_mul_f32 v[68:69], v[34:35], v[86:87] op_sel_hi:[1,0]
	v_pk_mul_f32 v[16:17], v[16:17], s[94:95] op_sel_hi:[1,0]
	v_pk_mul_f32 v[68:69], v[68:69], v[76:77]
	v_cvt_pk_bf16_f32 v17, v16, v17
	v_mov_b32_e32 v15, v68
	v_mov_b32_e32 v16, v68
	v_mov_b32_e32 v19, v69
	v_mov_b32_e32 v70, v69
	v_permlane32_swap_b32_e32 v15, v16
	s_nop 0
	v_permlane32_swap_b32_e32 v19, v70
	v_cndmask_b32_e32 v71, v19, v70, vcc
	v_cndmask_b32_e32 v70, v15, v16, vcc
	v_pk_fma_f32 v[68:69], v[70:71], 0, v[68:69] op_sel_hi:[1,0,1]
	v_and_b32_e32 v77, 0xffff0000, v14
	v_pk_mul_f32 v[68:69], v[68:69], s[94:95] op_sel_hi:[1,0]
	v_lshlrev_b32_e32 v76, 16, v14
	v_cvt_pk_bf16_f32 v16, v68, v69
	v_pk_mul_f32 v[68:69], v[40:41], v[86:87] op_sel_hi:[1,0]
; template <int DQK, int DV, bool LEAD> ...
;     ...
;           float sn = 0.f;
; #pragma unroll
;           for (int ds = 0; ds < 2; ++ds)
; #pragma unroll
;               for (int j = 0; j < 8; ++j) sn += x[ds][j] * x[ds][j];
;           sn = lanes4_sum(sn);
;           const float rn = rsqrtf(sn * (1.f / 64.f) + EPS);
; #pragma unroll
;           for (int ds = 0; ds < 2; ++ds)
; #pragma unroll
;               for (int j = 0; j < 8; ++j) x[ds][j] *= rn * qgain[32 * ds + 8 * g4 + j];
;           if constexpr (DQK == 64) {
; #pragma unroll
;               for (int ds = 0; ds < 2; ++ds)
; #pragma unroll
;                   for (int j = 0; j < 8; ++j) {
;                       auto rr = __builtin_amdgcn_permlane32_swap(__float_as_uint(x[ds][j]), __float_as_uint(x[ds][j]), false, false);
;                       const float other = hi ? __uint_as_float(rr[0]) : __uint_as_float(rr[1]);
;                       float cc = 1.f, sg = 0.f;
;                       if (lat) { const f32x2 cs = rope[(ds ? pcol : prow) * 16 + 8 * (g4 & 1) + j]; cc = cs.x; sg = hi ? cs.y : -cs.y; }
;                       x[ds][j] = x[ds][j] * cc + other * sg; }
;           } else {
;               float sr = 0.f;
; #pragma unroll
;               for (int j = 0; j < 8; ++j) sr += x[2][j] * x[2][j];
;               sr = lanes4_sum(sr);
;               const float rq = rsqrtf(sr * (1.f / 32.f) + EPS);
; #pragma unroll
;               for (int j = 0; j < 8; ++j) { const float av = x[2][j] * rq * qgain[64 + 8 * g4 + j];
;                   auto rr = __builtin_amdgcn_permlane16_swap(__float_as_uint(av), __float_as_uint(av), false, false);
;                   const float other = (g4 & 1) ? __uint_as_float(rr[0]) : __uint_as_float(rr[1]);
;                   float cc = 1.f, sg = 0.f;
;                   if (lat) { const f32x2 cs = rope[((g4 & 2) ? pcol : prow) * 8 + j]; cc = cs.x; sg = (g4 & 1) ? cs.y : -cs.y; }
;                   x[2][j] = av * cc + other * sg; }
;           }
; #pragma unroll
;           for (int ds = 0; ds < NDS; ++ds) { u32x4 w;
; #pragma unroll
;               for (int i = 0; i < 4; ++i) w[i] = cvtpk(x[ds][2 * i] * c2, x[ds][2 * i + 1] * c2);
;               qf[qb * NDS + ds] = __builtin_bit_cast(bf16x8, w); }
	v_mul_f32_e32 v14, v77, v77
	v_pk_mul_f32 v[68:69], v[68:69], v[78:79]
	s_nop 0
	v_mov_b32_e32 v15, v68
	v_mov_b32_e32 v19, v68
	v_mov_b32_e32 v70, v69
	v_mov_b32_e32 v71, v69
	v_permlane32_swap_b32_e32 v15, v19
	s_nop 0
	v_permlane32_swap_b32_e32 v70, v71
	v_cndmask_b32_e32 v71, v70, v71, vcc
	v_cndmask_b32_e32 v70, v15, v19, vcc
	v_pk_fma_f32 v[68:69], v[70:71], 0, v[68:69] op_sel_hi:[1,0,1]
	s_nop 0
	v_pk_mul_f32 v[68:69], v[68:69], s[94:95] op_sel_hi:[1,0]
	s_nop 0
	v_cvt_pk_bf16_f32 v15, v68, v69
	v_pk_mul_f32 v[68:69], v[38:39], v[86:87] op_sel_hi:[1,0]
	v_pk_fma_f32 v[78:79], v[76:77], v[76:77], v[14:15] op_sel_hi:[1,1,0]
	v_pk_mul_f32 v[68:69], v[68:69], v[80:81]
	v_pk_fma_f32 v[78:79], v[66:67], v[66:67], v[78:79]
	v_mov_b32_e32 v71, v69
	v_mov_b32_e32 v72, v69
	v_mov_b32_e32 v19, v68
	v_mov_b32_e32 v70, v68
	v_permlane32_swap_b32_e32 v71, v72
	s_nop 0
	v_permlane32_swap_b32_e32 v19, v70
	v_cndmask_b32_e32 v71, v71, v72, vcc
	v_lshlrev_b32_e32 v72, 16, v18
	v_mul_f32_e32 v18, v73, v73
	v_cndmask_b32_e32 v70, v19, v70, vcc
	v_pk_fma_f32 v[18:19], v[72:73], v[72:73], v[18:19] op_sel_hi:[1,1,0]
	v_mul_f32_e32 v14, v67, v67
	v_pk_fma_f32 v[18:19], v[64:65], v[64:65], v[18:19]
	v_pk_add_f32 v[78:79], v[14:15], v[78:79] op_sel_hi:[0,1]
	v_pk_add_f32 v[18:19], v[74:75], v[18:19] op_sel_hi:[0,1]
	v_pk_fma_f32 v[18:19], v[62:63], v[62:63], v[18:19]
	v_mul_f32_e32 v74, v63, v63
	v_pk_fma_f32 v[78:79], v[54:55], v[54:55], v[78:79]
	v_mul_f32_e32 v14, v55, v55
	v_pk_add_f32 v[18:19], v[74:75], v[18:19] op_sel_hi:[0,1]
	v_pk_add_f32 v[78:79], v[14:15], v[78:79] op_sel_hi:[0,1]
	v_pk_fma_f32 v[18:19], v[60:61], v[60:61], v[18:19]
	v_mul_f32_e32 v74, v61, v61
	v_pk_fma_f32 v[78:79], v[52:53], v[52:53], v[78:79]
	v_mul_f32_e32 v14, v53, v53
	v_pk_add_f32 v[18:19], v[74:75], v[18:19] op_sel_hi:[0,1]
	v_pk_add_f32 v[78:79], v[14:15], v[78:79] op_sel_hi:[0,1]
	v_pk_fma_f32 v[18:19], v[58:59], v[58:59], v[18:19]
	v_mul_f32_e32 v74, v59, v59
	v_pk_fma_f32 v[78:79], v[50:51], v[50:51], v[78:79]
	v_mul_f32_e32 v14, v51, v51
	v_pk_add_f32 v[18:19], v[74:75], v[18:19] op_sel_hi:[0,1]
	v_pk_add_f32 v[78:79], v[14:15], v[78:79] op_sel_hi:[0,1]
	v_pk_fma_f32 v[18:19], v[56:57], v[56:57], v[18:19]
	v_mul_f32_e32 v74, v57, v57
	v_pk_fma_f32 v[78:79], v[48:49], v[48:49], v[78:79]
	v_mul_f32_e32 v14, v49, v49
	v_pk_add_f32 v[18:19], v[74:75], v[18:19] op_sel_hi:[0,1]
	v_pk_add_f32 v[78:79], v[14:15], v[78:79] op_sel_hi:[0,1]
	v_pk_fma_f32 v[18:19], v[24:25], v[24:25], v[18:19]
	v_mul_f32_e32 v74, v25, v25
	v_pk_fma_f32 v[78:79], v[46:47], v[46:47], v[78:79]
	v_mul_f32_e32 v14, v47, v47
	v_pk_add_f32 v[18:19], v[74:75], v[18:19] op_sel_hi:[0,1]
	v_pk_add_f32 v[78:79], v[14:15], v[78:79] op_sel_hi:[0,1]
	v_pk_fma_f32 v[18:19], v[22:23], v[22:23], v[18:19]
	v_mul_f32_e32 v74, v23, v23
	v_pk_fma_f32 v[78:79], v[44:45], v[44:45], v[78:79]
	v_mul_f32_e32 v14, v45, v45
	v_pk_add_f32 v[18:19], v[74:75], v[18:19] op_sel_hi:[0,1]
	v_pk_add_f32 v[78:79], v[14:15], v[78:79] op_sel_hi:[0,1]
	v_mov_b32_e32 v19, v18
	v_mov_b32_e32 v14, v78
	s_nop 0
	v_permlane16_swap_b32_e32 v18, v19
	v_permlane16_swap_b32_e32 v78, v14
	v_add_f32_e32 v19, v18, v19
	v_add_f32_e32 v18, v78, v14
	v_mov_b32_e32 v75, v19
	v_mov_b32_e32 v74, v18
	s_nop 0
	v_permlane32_swap_b32_e32 v19, v75
	v_permlane32_swap_b32_e32 v18, v74
	v_pk_add_f32 v[18:19], v[18:19], v[74:75]
	s_nop 0
	v_pk_fma_f32 v[74:75], v[18:19], s[8:9], v[20:21] op_sel_hi:[1,0,0]
	v_pk_fma_f32 v[18:19], v[70:71], 0, v[68:69] op_sel_hi:[1,0,1]
	v_mul_f32_e32 v14, 0x4b800000, v75
	v_cmp_gt_f32_e64 s[4:5], s95, v75
	v_pk_mul_f32 v[18:19], v[18:19], s[94:95] op_sel_hi:[1,0]
	s_lshl_b32 s8, s30, 8
	v_cndmask_b32_e64 v14, v75, v14, s[4:5]
	v_rsq_f32_e32 v20, v14
	v_cvt_pk_bf16_f32 v14, v18, v19
	v_mul_f32_e32 v18, 0x45800000, v20
	v_cndmask_b32_e64 v68, v20, v18, s[4:5]
	v_pk_mul_f32 v[18:19], v[28:29], v[68:69] op_sel_hi:[1,0]
	v_cmp_gt_f32_e64 s[4:5], s95, v74
	v_pk_mul_f32 v[18:19], v[18:19], v[22:23]
	s_cmpk_lt_u32 s16, 0x100
	v_mov_b32_e32 v20, v18
	v_mov_b32_e32 v22, v18
	v_mov_b32_e32 v21, v19
	v_mov_b32_e32 v23, v19
	v_permlane32_swap_b32_e32 v20, v22
	s_nop 0
	v_permlane32_swap_b32_e32 v21, v23
	v_cndmask_b32_e32 v21, v21, v23, vcc
	v_cndmask_b32_e32 v20, v20, v22, vcc
	v_pk_fma_f32 v[18:19], v[20:21], 0, v[18:19] op_sel_hi:[1,0,1]
	s_mov_b32 s9, 1
	v_pk_mul_f32 v[18:19], v[18:19], s[94:95] op_sel_hi:[1,0]
	s_nop 0
	v_cvt_pk_bf16_f32 v21, v18, v19
	v_pk_mul_f32 v[18:19], v[26:27], v[68:69] op_sel_hi:[1,0]
	s_nop 0
	v_pk_mul_f32 v[18:19], v[18:19], v[24:25]
	s_nop 0
	v_mov_b32_e32 v20, v18
	v_mov_b32_e32 v22, v18
	v_mov_b32_e32 v23, v19
	v_mov_b32_e32 v24, v19
	v_permlane32_swap_b32_e32 v20, v22
	s_nop 0
	v_permlane32_swap_b32_e32 v23, v24
	v_cndmask_b32_e32 v23, v23, v24, vcc
	v_cndmask_b32_e32 v22, v20, v22, vcc
	v_pk_fma_f32 v[18:19], v[22:23], 0, v[18:19] op_sel_hi:[1,0,1]
	s_nop 0
	v_pk_mul_f32 v[18:19], v[18:19], s[94:95] op_sel_hi:[1,0]
	s_nop 0
	v_cvt_pk_bf16_f32 v20, v18, v19
	v_pk_mul_f32 v[18:19], v[32:33], v[68:69] op_sel_hi:[1,0]
	s_nop 0
	v_pk_mul_f32 v[18:19], v[18:19], v[56:57]
	s_nop 0
	v_mov_b32_e32 v22, v18
	v_mov_b32_e32 v24, v18
	v_mov_b32_e32 v23, v19
	v_mov_b32_e32 v25, v19
	v_permlane32_swap_b32_e32 v22, v24
	s_nop 0
	v_permlane32_swap_b32_e32 v23, v25
	v_cndmask_b32_e32 v23, v23, v25, vcc
	v_cndmask_b32_e32 v22, v22, v24, vcc
	v_pk_fma_f32 v[18:19], v[22:23], 0, v[18:19] op_sel_hi:[1,0,1]
	v_pk_mul_f32 v[22:23], v[30:31], v[68:69] op_sel_hi:[1,0]
	v_pk_mul_f32 v[18:19], v[18:19], s[94:95] op_sel_hi:[1,0]
	v_pk_mul_f32 v[22:23], v[22:23], v[58:59]
	v_cvt_pk_bf16_f32 v19, v18, v19
	v_mov_b32_e32 v18, v22
; __device__ __forceinline__ unsigned cvtpk(float lo, float hi) { f32x2 v = {lo, hi}; bf16x2_t b = __builtin_convertvector(v, bf16x2_t); return __builtin_bit_cast(unsigned, b); }
; template <int DQK, int DV, bool LEAD> ...
;     ...
;               for (int j = 0; j < 8; ++j) x[ds][j] *= rn * qgain[32 * ds + 8 * g4 + j];
;           if constexpr (DQK == 64) {
; #pragma unroll
;               for (int ds = 0; ds < 2; ++ds)
; #pragma unroll
;                   for (int j = 0; j < 8; ++j) {
;                       auto rr = __builtin_amdgcn_permlane32_swap(__float_as_uint(x[ds][j]), __float_as_uint(x[ds][j]), false, false);
;                       const float other = hi ? __uint_as_float(rr[0]) : __uint_as_float(rr[1]);
;                       float cc = 1.f, sg = 0.f;
;                       if (lat) { const f32x2 cs = rope[(ds ? pcol : prow) * 16 + 8 * (g4 & 1) + j]; cc = cs.x; sg = hi ? cs.y : -cs.y; }
;                       x[ds][j] = x[ds][j] * cc + other * sg; }
;           } else {
;               float sr = 0.f;
; #pragma unroll
;               for (int j = 0; j < 8; ++j) sr += x[2][j] * x[2][j];
;               sr = lanes4_sum(sr);
;               const float rq = rsqrtf(sr * (1.f / 32.f) + EPS);
; #pragma unroll
;               for (int j = 0; j < 8; ++j) { const float av = x[2][j] * rq * qgain[64 + 8 * g4 + j];
;                   auto rr = __builtin_amdgcn_permlane16_swap(__float_as_uint(av), __float_as_uint(av), false, false);
;                   const float other = (g4 & 1) ? __uint_as_float(rr[0]) : __uint_as_float(rr[1]);
;                   float cc = 1.f, sg = 0.f;
;                   if (lat) { const f32x2 cs = rope[((g4 & 2) ? pcol : prow) * 8 + j]; cc = cs.x; sg = (g4 & 1) ? cs.y : -cs.y; }
;                   x[2][j] = av * cc + other * sg; }
;           }
; #pragma unroll
;           for (int ds = 0; ds < NDS; ++ds) { u32x4 w;
; #pragma unroll
;               for (int i = 0; i < 4; ++i) w[i] = cvtpk(x[ds][2 * i] * c2, x[ds][2 * i + 1] * c2);
;               qf[qb * NDS + ds] = __builtin_bit_cast(bf16x8, w); }
;       }
; #pragma unroll
;       for (int d0 = 0; d0 < NQB * NDS; ++d0) asm volatile("" : "+v"(qf[d0])); }
;     wait_bar<0>();
	v_mov_b32_e32 v24, v22
	v_mov_b32_e32 v25, v23
	v_mov_b32_e32 v56, v23
	v_permlane32_swap_b32_e32 v18, v24
	s_nop 0
	v_permlane32_swap_b32_e32 v25, v56
	v_cndmask_b32_e32 v25, v25, v56, vcc
	v_cndmask_b32_e32 v24, v18, v24, vcc
	v_pk_fma_f32 v[22:23], v[24:25], 0, v[22:23] op_sel_hi:[1,0,1]
	s_nop 0
	v_pk_mul_f32 v[22:23], v[22:23], s[94:95] op_sel_hi:[1,0]
	s_nop 0
	v_cvt_pk_bf16_f32 v18, v22, v23
	v_pk_mul_f32 v[22:23], v[36:37], v[68:69] op_sel_hi:[1,0]
	s_nop 0
	v_pk_mul_f32 v[22:23], v[22:23], v[60:61]
	s_nop 0
	v_mov_b32_e32 v24, v22
	v_mov_b32_e32 v56, v22
	v_mov_b32_e32 v25, v23
	v_mov_b32_e32 v57, v23
	v_permlane32_swap_b32_e32 v24, v56
	s_nop 0
	v_permlane32_swap_b32_e32 v25, v57
	v_cndmask_b32_e32 v25, v25, v57, vcc
	v_cndmask_b32_e32 v24, v24, v56, vcc
	v_pk_fma_f32 v[22:23], v[24:25], 0, v[22:23] op_sel_hi:[1,0,1]
	s_nop 0
	v_pk_mul_f32 v[22:23], v[22:23], s[94:95] op_sel_hi:[1,0]
	s_nop 0
	v_cvt_pk_bf16_f32 v25, v22, v23
	v_pk_mul_f32 v[22:23], v[34:35], v[68:69] op_sel_hi:[1,0]
	s_nop 0
	v_pk_mul_f32 v[22:23], v[22:23], v[62:63]
	s_nop 0
	v_mov_b32_e32 v24, v22
	v_mov_b32_e32 v56, v22
	v_mov_b32_e32 v57, v23
	v_mov_b32_e32 v58, v23
	v_permlane32_swap_b32_e32 v24, v56
	s_nop 0
	v_permlane32_swap_b32_e32 v57, v58
	v_cndmask_b32_e32 v57, v57, v58, vcc
	v_cndmask_b32_e32 v56, v24, v56, vcc
	v_pk_fma_f32 v[22:23], v[56:57], 0, v[22:23] op_sel_hi:[1,0,1]
	s_nop 0
	v_pk_mul_f32 v[22:23], v[22:23], s[94:95] op_sel_hi:[1,0]
	s_nop 0
	v_cvt_pk_bf16_f32 v24, v22, v23
	v_pk_mul_f32 v[22:23], v[40:41], v[68:69] op_sel_hi:[1,0]
	s_nop 0
	v_pk_mul_f32 v[22:23], v[22:23], v[64:65]
	s_nop 0
	v_mov_b32_e32 v56, v22
	v_mov_b32_e32 v58, v22
	v_mov_b32_e32 v57, v23
	v_mov_b32_e32 v59, v23
	v_permlane32_swap_b32_e32 v56, v58
	s_nop 0
	v_permlane32_swap_b32_e32 v57, v59
	v_cndmask_b32_e32 v57, v57, v59, vcc
	v_cndmask_b32_e32 v56, v56, v58, vcc
	v_pk_fma_f32 v[22:23], v[56:57], 0, v[22:23] op_sel_hi:[1,0,1]
	v_pk_mul_f32 v[56:57], v[38:39], v[68:69] op_sel_hi:[1,0]
	v_pk_mul_f32 v[22:23], v[22:23], s[94:95] op_sel_hi:[1,0]
	v_pk_mul_f32 v[56:57], v[56:57], v[72:73]
	v_cvt_pk_bf16_f32 v23, v22, v23
	v_mov_b32_e32 v22, v56
	v_mov_b32_e32 v58, v56
	s_nop 1
	v_permlane32_swap_b32_e32 v22, v58
	v_mov_b32_e32 v59, v57
	v_mov_b32_e32 v60, v57
	v_cndmask_b32_e32 v58, v22, v58, vcc
	v_mul_f32_e32 v22, 0x4b800000, v74
	v_permlane32_swap_b32_e32 v59, v60
	v_cndmask_b32_e64 v22, v74, v22, s[4:5]
	v_cndmask_b32_e32 v59, v59, v60, vcc
	v_rsq_f32_e32 v60, v22
	v_pk_fma_f32 v[56:57], v[58:59], 0, v[56:57] op_sel_hi:[1,0,1]
	s_nop 0
	v_pk_mul_f32 v[56:57], v[56:57], s[94:95] op_sel_hi:[1,0]
	s_nop 0
	v_cvt_pk_bf16_f32 v22, v56, v57
	v_mul_f32_e32 v56, 0x45800000, v60
	v_cndmask_b32_e64 v56, v60, v56, s[4:5]
	v_pk_mul_f32 v[38:39], v[38:39], v[56:57] op_sel_hi:[1,0]
	v_pk_mul_f32 v[26:27], v[26:27], v[56:57] op_sel_hi:[1,0]
	v_pk_mul_f32 v[38:39], v[38:39], v[76:77]
	v_pk_mul_f32 v[28:29], v[28:29], v[56:57] op_sel_hi:[1,0]
	v_pk_mul_f32 v[26:27], v[26:27], v[46:47]
	v_pk_mul_f32 v[28:29], v[28:29], v[44:45]
	v_mov_b32_e32 v44, v38
	v_mov_b32_e32 v46, v38
	v_mov_b32_e32 v45, v39
	v_mov_b32_e32 v47, v39
	v_pk_mul_f32 v[40:41], v[40:41], v[56:57] op_sel_hi:[1,0]
	v_permlane32_swap_b32_e32 v44, v46
	v_permlane32_swap_b32_e32 v45, v47
	v_pk_mul_f32 v[40:41], v[40:41], v[66:67]
	v_cndmask_b32_e32 v45, v45, v47, vcc
	v_cndmask_b32_e32 v44, v44, v46, vcc
	v_pk_fma_f32 v[38:39], v[44:45], 0, v[38:39] op_sel_hi:[1,0,1]
	v_mov_b32_e32 v44, v40
	v_mov_b32_e32 v46, v40
	v_mov_b32_e32 v45, v41
	v_mov_b32_e32 v47, v41
	v_pk_mul_f32 v[34:35], v[34:35], v[56:57] op_sel_hi:[1,0]
	v_permlane32_swap_b32_e32 v44, v46
	v_permlane32_swap_b32_e32 v45, v47
	v_pk_mul_f32 v[34:35], v[34:35], v[54:55]
	v_cndmask_b32_e32 v45, v45, v47, vcc
	v_cndmask_b32_e32 v44, v44, v46, vcc
	v_pk_fma_f32 v[40:41], v[44:45], 0, v[40:41] op_sel_hi:[1,0,1]
	v_mov_b32_e32 v44, v34
	v_mov_b32_e32 v46, v34
	v_mov_b32_e32 v45, v35
	v_mov_b32_e32 v47, v35
	v_pk_mul_f32 v[36:37], v[36:37], v[56:57] op_sel_hi:[1,0]
	v_permlane32_swap_b32_e32 v44, v46
	v_permlane32_swap_b32_e32 v45, v47
	v_pk_mul_f32 v[36:37], v[36:37], v[52:53]
	v_cndmask_b32_e32 v45, v45, v47, vcc
	v_cndmask_b32_e32 v44, v44, v46, vcc
	v_pk_fma_f32 v[34:35], v[44:45], 0, v[34:35] op_sel_hi:[1,0,1]
	v_mov_b32_e32 v44, v36
	v_mov_b32_e32 v46, v36
	v_mov_b32_e32 v45, v37
	v_mov_b32_e32 v47, v37
	v_pk_mul_f32 v[30:31], v[30:31], v[56:57] op_sel_hi:[1,0]
	v_permlane32_swap_b32_e32 v44, v46
	v_permlane32_swap_b32_e32 v45, v47
	v_pk_mul_f32 v[30:31], v[30:31], v[50:51]
	v_cndmask_b32_e32 v45, v45, v47, vcc
	v_cndmask_b32_e32 v44, v44, v46, vcc
	v_pk_fma_f32 v[36:37], v[44:45], 0, v[36:37] op_sel_hi:[1,0,1]
	v_mov_b32_e32 v44, v30
	v_mov_b32_e32 v46, v30
	v_mov_b32_e32 v45, v31
	v_mov_b32_e32 v47, v31
	v_pk_mul_f32 v[32:33], v[32:33], v[56:57] op_sel_hi:[1,0]
	v_permlane32_swap_b32_e32 v44, v46
	v_permlane32_swap_b32_e32 v45, v47
	v_pk_mul_f32 v[32:33], v[32:33], v[48:49]
	v_cndmask_b32_e32 v45, v45, v47, vcc
	v_cndmask_b32_e32 v44, v44, v46, vcc
	v_pk_fma_f32 v[30:31], v[44:45], 0, v[30:31] op_sel_hi:[1,0,1]
	v_mov_b32_e32 v44, v32
	v_mov_b32_e32 v46, v32
	v_mov_b32_e32 v45, v33
	v_mov_b32_e32 v47, v33
	v_permlane32_swap_b32_e32 v44, v46
	s_nop 0
	v_permlane32_swap_b32_e32 v45, v47
	v_cndmask_b32_e32 v45, v45, v47, vcc
	v_cndmask_b32_e32 v44, v44, v46, vcc
	v_pk_fma_f32 v[32:33], v[44:45], 0, v[32:33] op_sel_hi:[1,0,1]
	v_mov_b32_e32 v44, v26
	v_mov_b32_e32 v46, v26
	v_mov_b32_e32 v45, v27
	v_mov_b32_e32 v47, v27
	v_permlane32_swap_b32_e32 v44, v46
	s_nop 0
	v_permlane32_swap_b32_e32 v45, v47
	v_cndmask_b32_e32 v45, v45, v47, vcc
	v_cndmask_b32_e32 v44, v44, v46, vcc
	v_pk_fma_f32 v[44:45], v[44:45], 0, v[26:27] op_sel_hi:[1,0,1]
	v_mov_b32_e32 v26, v28
	v_mov_b32_e32 v46, v28
	v_mov_b32_e32 v27, v29
	v_mov_b32_e32 v47, v29
	v_permlane32_swap_b32_e32 v26, v46
	s_nop 0
	v_permlane32_swap_b32_e32 v27, v47
	v_cndmask_b32_e32 v27, v27, v47, vcc
	v_cndmask_b32_e32 v26, v26, v46, vcc
	v_pk_fma_f32 v[46:47], v[26:27], 0, v[28:29] op_sel_hi:[1,0,1]
	v_pk_mul_f32 v[26:27], v[38:39], s[94:95] op_sel_hi:[1,0]
	v_pk_mul_f32 v[28:29], v[40:41], s[94:95] op_sel_hi:[1,0]
	v_cvt_pk_bf16_f32 v26, v26, v27
	v_cvt_pk_bf16_f32 v27, v28, v29
	v_pk_mul_f32 v[28:29], v[34:35], s[94:95] op_sel_hi:[1,0]
	v_pk_mul_f32 v[34:35], v[36:37], s[94:95] op_sel_hi:[1,0]
	v_pk_mul_f32 v[30:31], v[30:31], s[94:95] op_sel_hi:[1,0]
	v_pk_mul_f32 v[32:33], v[32:33], s[94:95] op_sel_hi:[1,0]
	v_cvt_pk_bf16_f32 v28, v28, v29
	v_cvt_pk_bf16_f32 v29, v34, v35
	v_cvt_pk_bf16_f32 v30, v30, v31
	v_cvt_pk_bf16_f32 v31, v32, v33
	v_pk_mul_f32 v[32:33], v[44:45], s[94:95] op_sel_hi:[1,0]
	v_pk_mul_f32 v[34:35], v[46:47], s[94:95] op_sel_hi:[1,0]
	v_cvt_pk_bf16_f32 v32, v32, v33
	v_cvt_pk_bf16_f32 v33, v34, v35
	s_waitcnt vmcnt(0) lgkmcnt(0)
	s_barrier
; #define ATT_SB() __builtin_amdgcn_sched_barrier(0)
; #define ATT_DMA_K(t, sl) do { glds16(ksrc + (size_t)(t) * 64 * kpitch, (unsigned)__builtin_amdgcn_readfirstlane(kdst + (sl) * KSLOT)); \
;         if constexpr (DQK == 96) glds16(krsrc + (size_t)(t) * 64 * 32, (unsigned)__builtin_amdgcn_readfirstlane(krdst + (sl) * KSLOT)); } while (0)
; #define ATT_DMA_V(t, sl) do { glds16(vsrc + (size_t)(t) * 64, (unsigned)__builtin_amdgcn_readfirstlane(vdst + (sl) * VSLOT)); \
;         if constexpr (DV == 128) glds16(vsrc + (size_t)64 * NR + (size_t)(t) * 64, (unsigned)__builtin_amdgcn_readfirstlane(vdst + (sl) * VSLOT + 8192)); } while (0)
; #define ATT_KLOAD(sl) do { _Pragma("unroll") for (int kb_ = 0; kb_ < NKW; ++kb_) _Pragma("unroll") for (int ds_ = 0; ds_ < NDS; ++ds_) { \
;         if (ds_ < 2) kf[kb_ * NDS + ds_] = *(const LAS bf16x8*)(kp[ds_ & 1] + (sl) * KSLOT + (kb_ & 1) * 512 + (kb_ >> 1) * 4096); \
;         else kf[kb_ * NDS + ds_] = *(const LAS bf16x8*)(krp + (sl) * KSLOT + (kb_ & 1) * 256 + (kb_ >> 1) * 2048); } } while (0)
; #define ATT_QK() do { _Pragma("unroll") for (int kb_ = 0; kb_ < NKW; ++kb_) _Pragma("unroll") for (int ds_ = 0; ds_ < NDS; ++ds_) _Pragma("unroll") for (int qb_ = 0; qb_ < NQB; ++qb_) \
;         c[kb_][qb_] = __builtin_amdgcn_mfma_f32_16x16x32_bf16(kf[kb_ * NDS + ds_], qf[qb_ * NDS + ds_], ds_ == 0 ? zero4 : c[kb_][qb_], 0, 0, 0); } while (0)
; template <int DQK, int DV, bool LEAD> ...
;     ...
;     bf16x8 kf[NKW * NDS], vf[NVF];
;     ATT_KLOAD(0);
;     asm volatile("s_waitcnt lgkmcnt(0)\n\ts_barrier" ::: "memory");
;     float lsum[NQB];
; #pragma unroll
;     for (int qb = 0; qb < NQB; ++qb) lsum[qb] = 0.f;
;     const f32x4 zero4 = {0.f, 0.f, 0.f, 0.f};
;     f32x4 o[NDB][NQB], c[NKW][NQB]; u32x4 pw[4];
; #pragma unroll
;     for (int i = 0; i < NDB; ++i)
; #pragma unroll
;         for (int qb = 0; qb < NQB; ++qb) o[i][qb] = zero4;
;     ATT_DMA_K(3, 0); ATT_DMA_V(1, 1);
;     ATT_QK(); ATT_SB();
;     ATT_KLOAD(1); ATT_SB();
;     if constexpr (LEAD) { ATT_EXP(); ATT_SUMPACK(); }
;     wait_bar<NDMA>();
;     int s_prev = 0, s_cur = 1, s_next = 2;
;     int one_ = 1; asm volatile("" : "+s"(one_));
	ds_read_b128 v[34:37], v174
	ds_read_b128 v[38:41], v174 offset:512
	v_bfe_u32 v56, v84, 1, 3
	v_bitop3_b32 v56, v171, v56, 4 bitop3:0x36
	v_lshlrev_b32_e32 v80, 4, v56
	v_add_u32_e32 v177, v85, v80
	s_waitcnt lgkmcnt(1)
	v_mfma_f32_16x16x32_bf16 v[44:47], v[34:37], v[6:9], 0
	ds_read_b128 v[56:59], v177
	ds_read_b128 v[60:63], v177 offset:512
	s_waitcnt lgkmcnt(0)
	s_barrier
	s_mov_b32 m0, s31
	s_nop 0
	global_load_lds_dwordx4 v[168:169], off
	v_mfma_f32_16x16x32_bf16 v[48:51], v[34:37], v[14:17], 0
	s_cselect_b64 vcc, -1, 0
	s_add_i32 s4, s19, 0x2000
	v_mfma_f32_16x16x32_bf16 v[52:55], v[34:37], v[22:25], 0
	v_mfma_f32_16x16x32_bf16 v[34:37], v[34:37], v[26:29], 0
	s_waitcnt lgkmcnt(1)
	v_mfma_f32_16x16x32_bf16 v[64:67], v[56:59], v[2:5], v[44:47]
	v_mfma_f32_16x16x32_bf16 v[68:71], v[56:59], v[10:13], v[48:51]
	v_mfma_f32_16x16x32_bf16 v[50:53], v[56:59], v[18:21], v[52:55]
	v_mfma_f32_16x16x32_bf16 v[54:57], v[56:59], v[30:33], v[34:37]
	v_mfma_f32_16x16x32_bf16 v[34:37], v[38:41], v[6:9], 0
	v_mfma_f32_16x16x32_bf16 v[44:47], v[38:41], v[14:17], 0
	v_mfma_f32_16x16x32_bf16 v[72:75], v[38:41], v[22:25], 0
	v_mfma_f32_16x16x32_bf16 v[38:41], v[38:41], v[26:29], 0
	s_waitcnt lgkmcnt(0)
	v_mfma_f32_16x16x32_bf16 v[76:79], v[60:63], v[2:5], v[34:37]
	v_mfma_f32_16x16x32_bf16 v[84:87], v[60:63], v[10:13], v[44:47]
	s_nop 1
	v_lshl_add_u64 v[34:35], v[162:163], 0, s[66:67]
	s_mov_b32 m0, s4
	s_nop 0
	global_load_lds_dwordx4 v[34:35], off
	v_mfma_f32_16x16x32_bf16 v[72:75], v[60:63], v[18:21], v[72:75]
	v_mfma_f32_16x16x32_bf16 v[58:61], v[60:63], v[30:33], v[38:41]
	ds_read_b128 v[34:37], v174 offset:8192
	s_nop 1
	ds_read_b128 v[38:41], v174 offset:8704
	ds_read_b128 v[42:45], v177 offset:8192
	ds_read_b128 v[46:49], v177 offset:8704
	v_exp_f32_e32 v62, v64
	v_exp_f32_e32 v63, v65
	v_exp_f32_e32 v64, v66
	v_exp_f32_e32 v65, v67
	v_exp_f32_e32 v66, v68
	v_exp_f32_e32 v67, v69
	v_exp_f32_e32 v68, v70
	v_exp_f32_e32 v69, v71
	v_exp_f32_e32 v70, v50
	v_exp_f32_e32 v71, v51
	v_exp_f32_e32 v81, v52
	v_exp_f32_e32 v83, v53
	v_exp_f32_e32 v54, v54
	v_exp_f32_e32 v55, v55
	v_exp_f32_e32 v56, v56
	v_exp_f32_e32 v57, v57
	v_add_f32_e32 v50, v62, v63
	v_add_f32_e32 v51, v64, v65
	v_exp_f32_e32 v76, v76
	v_exp_f32_e32 v84, v84
	v_exp_f32_e32 v72, v72
	v_exp_f32_e32 v58, v58
	v_add_f32_e32 v50, v50, v51
	v_add_f32_e32 v51, v66, v67
	v_add_f32_e32 v52, v68, v69
	v_add_f32_e32 v51, v51, v52
	v_add_f32_e32 v52, v70, v71
	v_add_f32_e32 v53, v81, v83
	v_exp_f32_e32 v77, v77
	v_exp_f32_e32 v85, v85
	v_exp_f32_e32 v73, v73
	v_exp_f32_e32 v59, v59
	v_add_f32_e32 v52, v52, v53
	v_add_f32_e32 v53, v54, v55
	v_add_f32_e32 v88, v56, v57
	v_add_f32_e32 v53, v53, v88
	v_exp_f32_e32 v78, v78
	v_exp_f32_e32 v86, v86
	v_exp_f32_e32 v74, v74
	v_exp_f32_e32 v60, v60
	v_add_f32_e32 v50, v50, v76
	v_add_f32_e32 v51, v51, v84
	v_add_f32_e32 v52, v52, v72
	v_add_f32_e32 v53, v53, v58
	v_exp_f32_e32 v79, v79
	v_exp_f32_e32 v87, v87
	v_exp_f32_e32 v75, v75
	v_exp_f32_e32 v61, v61
	v_add_f32_e32 v50, v77, v50
	v_add_f32_e32 v51, v85, v51
	v_add_f32_e32 v52, v73, v52
	v_add_f32_e32 v53, v59, v53
	s_mov_b32 s4, 1
	v_add_f32_e32 v50, v78, v50
	v_add_f32_e32 v88, v86, v51
	v_add_f32_e32 v52, v74, v52
	v_add_f32_e32 v89, v60, v53
	v_cvt_pk_bf16_f32 v102, v62, v63
	v_add_f32_e32 v51, v79, v50
	v_add_f32_e32 v50, v87, v88
	v_add_f32_e32 v53, v75, v52
	v_add_f32_e32 v52, v61, v89
	s_waitcnt vmcnt(2) lgkmcnt(0)
	s_barrier
	s_cmp_lg_u32 s4, 0
	v_pk_add_f32 v[166:167], v[50:51], 0 op_sel_hi:[1,0]
	v_cndmask_b32_e32 v50, v80, v82, vcc
	v_add3_u32 v178, 0, v176, v50
	v_mov_b32_e32 v50, 0
	v_pk_add_f32 v[164:165], v[52:53], 0 op_sel_hi:[1,0]
	v_cvt_pk_bf16_f32 v103, v64, v65
	v_cvt_pk_bf16_f32 v104, v76, v77
	v_cvt_pk_bf16_f32 v105, v78, v79
	v_cvt_pk_bf16_f32 v110, v66, v67
	v_cvt_pk_bf16_f32 v111, v68, v69
	v_cvt_pk_bf16_f32 v112, v84, v85
	v_cvt_pk_bf16_f32 v113, v86, v87
	v_cvt_pk_bf16_f32 v122, v70, v71
	v_cvt_pk_bf16_f32 v123, v81, v83
	v_cvt_pk_bf16_f32 v124, v72, v73
	v_cvt_pk_bf16_f32 v125, v74, v75
	v_cvt_pk_bf16_f32 v126, v54, v55
	v_cvt_pk_bf16_f32 v127, v56, v57
	v_cvt_pk_bf16_f32 v128, v58, v59
	v_cvt_pk_bf16_f32 v129, v60, v61
	s_cselect_b64 s[4:5], -1, 0
	s_mov_b32 s16, 2
	v_mov_b32_e32 v51, v50
	v_mov_b32_e32 v52, v50
	v_mov_b32_e32 v53, v50
	v_mov_b32_e32 v54, v50
	v_mov_b32_e32 v55, v50
	v_mov_b32_e32 v56, v50
	v_mov_b32_e32 v57, v50
	v_mov_b32_e32 v58, v50
	v_mov_b32_e32 v59, v50
	v_mov_b32_e32 v60, v50
	v_mov_b32_e32 v61, v50
	v_mov_b32_e32 v62, v50
	v_mov_b32_e32 v63, v50
	v_mov_b32_e32 v64, v50
	v_mov_b32_e32 v65, v50
	v_mov_b32_e32 v66, v50
	v_mov_b32_e32 v67, v50
	v_mov_b32_e32 v68, v50
	v_mov_b32_e32 v69, v50
	v_mov_b32_e32 v70, v50
	v_mov_b32_e32 v71, v50
	v_mov_b32_e32 v72, v50
	v_mov_b32_e32 v73, v50
	v_mov_b32_e32 v74, v50
	v_mov_b32_e32 v75, v50
	v_mov_b32_e32 v76, v50
	v_mov_b32_e32 v77, v50
	v_mov_b32_e32 v78, v50
	v_mov_b32_e32 v79, v50
	v_mov_b32_e32 v80, v50
	v_mov_b32_e32 v81, v50
	v_mov_b32_e32 v82, v50
	v_mov_b32_e32 v83, v50
	v_mov_b32_e32 v84, v50
	v_mov_b32_e32 v85, v50
	v_mov_b32_e32 v86, v50
	v_mov_b32_e32 v87, v50
	v_mov_b32_e32 v88, v50
	v_mov_b32_e32 v89, v50
	v_mov_b32_e32 v90, v50
	v_mov_b32_e32 v91, v50
	v_mov_b32_e32 v92, v50
	v_mov_b32_e32 v93, v50
	v_mov_b32_e32 v94, v50
	v_mov_b32_e32 v95, v50
	v_mov_b32_e32 v96, v50
	v_mov_b32_e32 v97, v50
	v_mov_b32_e32 v98, v50
	v_mov_b32_e32 v99, v50
	v_mov_b32_e32 v100, v50
	v_mov_b32_e32 v101, v50
	v_mov_b32_e32 v106, v50
	v_mov_b32_e32 v107, v50
	v_mov_b32_e32 v108, v50
	v_mov_b32_e32 v109, v50
	v_mov_b32_e32 v114, v50
	v_mov_b32_e32 v115, v50
	v_mov_b32_e32 v116, v50
	v_mov_b32_e32 v117, v50
	v_mov_b32_e32 v118, v50
	v_mov_b32_e32 v119, v50
	v_mov_b32_e32 v120, v50
	v_mov_b32_e32 v121, v50
	s_branch .LBB0_998

; #define ATT_SB() __builtin_amdgcn_sched_barrier(0)
; #define ATT_DMA_K(t, sl) do { glds16(ksrc + (size_t)(t) * 64 * kpitch, (unsigned)__builtin_amdgcn_readfirstlane(kdst + (sl) * KSLOT)); \
;         if constexpr (DQK == 96) glds16(krsrc + (size_t)(t) * 64 * 32, (unsigned)__builtin_amdgcn_readfirstlane(krdst + (sl) * KSLOT)); } while (0)
; #define ATT_DMA_V(t, sl) do { glds16(vsrc + (size_t)(t) * 64, (unsigned)__builtin_amdgcn_readfirstlane(vdst + (sl) * VSLOT)); \
;         if constexpr (DV == 128) glds16(vsrc + (size_t)64 * NR + (size_t)(t) * 64, (unsigned)__builtin_amdgcn_readfirstlane(vdst + (sl) * VSLOT + 8192)); } while (0)
; #define ATT_KLOAD(sl) do { _Pragma("unroll") for (int kb_ = 0; kb_ < NKW; ++kb_) _Pragma("unroll") for (int ds_ = 0; ds_ < NDS; ++ds_) { \
;         if (ds_ < 2) kf[kb_ * NDS + ds_] = *(const LAS bf16x8*)(kp[ds_ & 1] + (sl) * KSLOT + (kb_ & 1) * 512 + (kb_ >> 1) * 4096); \
;         else kf[kb_ * NDS + ds_] = *(const LAS bf16x8*)(krp + (sl) * KSLOT + (kb_ & 1) * 256 + (kb_ >> 1) * 2048); } } while (0)
; #define ATT_QK() do { _Pragma("unroll") for (int kb_ = 0; kb_ < NKW; ++kb_) _Pragma("unroll") for (int ds_ = 0; ds_ < NDS; ++ds_) _Pragma("unroll") for (int qb_ = 0; qb_ < NQB; ++qb_) \
;         c[kb_][qb_] = __builtin_amdgcn_mfma_f32_16x16x32_bf16(kf[kb_ * NDS + ds_], qf[qb_ * NDS + ds_], ds_ == 0 ? zero4 : c[kb_][qb_], 0, 0, 0); } while (0)
; template <int DQK, int DV, bool LEAD> ...
;     ...
;     for (int t = 1; t < NT; ++t) {
;         __builtin_amdgcn_s_waitcnt(0xC07F);
;         if constexpr (!LEAD) { ATT_EXP(); ATT_SUMPACK(); ATT_SB(); }
;         ATT_VLOAD(s_prev, 0); ATT_SB();
;         { const int tk = (t + 3 < NT) ? t + 3 : NT - 1; ATT_DMA_K(tk, s_cur); }
;         { const int tv = (t + 1 < NT) ? t + 1 : NT - 1; ATT_DMA_V(tv, s_next); }
;         ATT_SB();
;         if constexpr (LEAD) {
;             ATT_QK(); ATT_SB();
;             ATT_PVP(0); ATT_SB();
;             if constexpr (DV == 128) { ATT_VLOAD(s_prev, 1); ATT_SB(); ATT_EXP(); ATT_SB(); ATT_PVP(1); ATT_SB(); }
;             if (one_) ATT_KLOAD(s_next);
;             ATT_SB();
;             if constexpr (DV == 64) ATT_EXP();
;             ATT_SUMPACK();
;             asm volatile("" : "+v"(pw[0]), "+v"(pw[1]), "+v"(pw[2]), "+v"(pw[3]));
; #pragma unroll
;             for (int qb = 0; qb < NQB; ++qb) asm volatile("" : "+v"(lsum[qb]));
.LBB0_998:
	v_lshl_add_u32 v130, s13, 13, v178
	s_waitcnt lgkmcnt(0)
	ds_read_b128 v[180:183], v130 offset:36864
	ds_read_b128 v[184:187], v130 offset:38912
	ds_read_b128 v[188:191], v130 offset:40960
	ds_read_b128 v[204:207], v130 offset:43008
	s_mov_b32 s18, s9
	s_mov_b32 s9, s16
	s_lshl_b32 s16, s18, 13
	s_add_i32 s16, s16, s31
	s_mov_b32 m0, s16
	s_nop 0
	global_load_lds_dwordx4 v[168:169], off
	s_min_u32 s16, s12, 3
	s_lshl_b32 s38, s16, 7
	s_lshl_b32 s16, s9, 13
	v_lshl_add_u64 v[130:131], v[162:163], 0, s[38:39]
	s_add_i32 s22, s16, s19
	s_mov_b32 m0, s22
	s_nop 0
	global_load_lds_dwordx4 v[130:131], off
	v_mfma_f32_16x16x32_bf16 v[130:133], v[34:37], v[6:9], 0
	v_mfma_f32_16x16x32_bf16 v[134:137], v[34:37], v[14:17], 0
	v_mfma_f32_16x16x32_bf16 v[138:141], v[34:37], v[22:25], 0
	v_mfma_f32_16x16x32_bf16 v[142:145], v[34:37], v[26:29], 0
	v_mfma_f32_16x16x32_bf16 v[158:161], v[42:45], v[2:5], v[130:133]
	v_mfma_f32_16x16x32_bf16 v[154:157], v[42:45], v[10:13], v[134:137]
	v_mfma_f32_16x16x32_bf16 v[130:133], v[38:41], v[6:9], 0
	v_mfma_f32_16x16x32_bf16 v[134:137], v[38:41], v[14:17], 0
	v_mfma_f32_16x16x32_bf16 v[208:211], v[38:41], v[22:25], 0
	v_mfma_f32_16x16x32_bf16 v[212:215], v[38:41], v[26:29], 0
	v_mfma_f32_16x16x32_bf16 v[150:153], v[42:45], v[18:21], v[138:141]
	v_mfma_f32_16x16x32_bf16 v[142:145], v[42:45], v[30:33], v[142:145]
	v_mfma_f32_16x16x32_bf16 v[146:149], v[46:49], v[2:5], v[130:133]
	v_mfma_f32_16x16x32_bf16 v[138:141], v[46:49], v[10:13], v[134:137]
	v_mfma_f32_16x16x32_bf16 v[134:137], v[46:49], v[18:21], v[208:211]
	v_mfma_f32_16x16x32_bf16 v[130:133], v[46:49], v[30:33], v[212:215]
	s_waitcnt lgkmcnt(3)
	v_mfma_f32_16x16x32_bf16 v[118:121], v[180:183], v[102:105], v[118:121]
	v_mfma_f32_16x16x32_bf16 v[114:117], v[180:183], v[110:113], v[114:117]
	v_mfma_f32_16x16x32_bf16 v[106:109], v[180:183], v[122:125], v[106:109]
	v_mfma_f32_16x16x32_bf16 v[98:101], v[180:183], v[126:129], v[98:101]
	s_waitcnt lgkmcnt(2)
	v_mfma_f32_16x16x32_bf16 v[94:97], v[184:187], v[102:105], v[94:97]
	v_mfma_f32_16x16x32_bf16 v[90:93], v[184:187], v[110:113], v[90:93]
	v_mfma_f32_16x16x32_bf16 v[86:89], v[184:187], v[122:125], v[86:89]
	v_mfma_f32_16x16x32_bf16 v[82:85], v[184:187], v[126:129], v[82:85]
	s_waitcnt lgkmcnt(1)
	v_mfma_f32_16x16x32_bf16 v[78:81], v[188:191], v[102:105], v[78:81]
	v_mfma_f32_16x16x32_bf16 v[74:77], v[188:191], v[110:113], v[74:77]
	v_mfma_f32_16x16x32_bf16 v[70:73], v[188:191], v[122:125], v[70:73]
	v_mfma_f32_16x16x32_bf16 v[66:69], v[188:191], v[126:129], v[66:69]
	s_waitcnt lgkmcnt(0)
	v_mfma_f32_16x16x32_bf16 v[62:65], v[204:207], v[102:105], v[62:65]
	v_mfma_f32_16x16x32_bf16 v[58:61], v[204:207], v[110:113], v[58:61]
	v_mfma_f32_16x16x32_bf16 v[54:57], v[204:207], v[122:125], v[54:57]
	v_mfma_f32_16x16x32_bf16 v[50:53], v[204:207], v[126:129], v[50:53]
	s_andn2_b64 vcc, exec, s[4:5]
	s_cbranch_vccnz .LBB0_997
	v_add_u32_e32 v38, s16, v174
	v_add_u32_e32 v46, s16, v177
	ds_read_b128 v[34:37], v38
	ds_read_b128 v[38:41], v38 offset:512
	ds_read_b128 v[42:45], v46
	ds_read_b128 v[46:49], v46 offset:512
	s_branch .LBB0_997

; #define PG8_STAGE_B(bufoff, gbase) do { _Pragma("unroll") for (int _i = 0; _i < 2; ++_i) \
;         __builtin_amdgcn_global_load_lds((const unsigned*)((const char*)(gbase) + voffB[_i]), (LAS unsigned*)(lds + (bufoff) + ldsw + _i * 8192), 16, 0, 0); } while (0)
; #define PG8_LDA(dst, b, h) do { _Pragma("unroll") for (int m = 0; m < 4; ++m) _Pragma("unroll") for (int k = 0; k < 2; ++k) dst[m][k] = *(const LAS bf16x8*)(lds + PG8_SA(b, h) + aoff + m * 2048 + k * 1024); } while (0)
; #define PG8_WAIT_V(n) asm volatile("s_waitcnt vmcnt(" #n ")" ::: "memory")
; template <class Epi, class Sched, bool GATHER = false>
; __device__ __forceinline__ void gemm_phase(LAS unsigned char* lds, const Gemm g, const Sched& S, const Epi& E) {
;     ...
;         for (int t = 0; t < nt; t += 2) {
;             const bool last = (t == nt - 2);
;             const char* a1 = cA + (size_t)(t + 1) * kstep;
;             const char* a2 = last ? nA : cA + (size_t)(t + 2) * kstep; const char* b2 = last ? nB : cB + (size_t)(t + 2) * kstep;
;             const char* a3 = a2 + kstep; const char* b3 = b2 + kstep;
;             unsigned vo2[2][2];
;             if constexpr (GATHER) {
; #pragma unroll
;             for (int _h = 0; _h < 2; ++_h)
; #pragma unroll
;                 for (int _i = 0; _i < 2; ++_i) vo2[_h][_i] = last ? voN[_h][_i] : voC[_h][_i]; }
;             PG8_LDB(B0, 0, 0); PG8_LDB(B1, 0, 1); PG8_SCHED; PG8_LDA(At, 0, 0); PG8_STAGE_A(PG8_SA(1, 1), a1, voC, 1);
;             PG8_WAIT_V(8); PG8_WAIT_L(0); PG8_BAR; PG8_MMA(0, 0, At, B0); PG8_MMA(0, 1, At, B1); PG8_BAR; PG8_SCHED;
;             PG8_LDA(At, 0, 1); PG8_STAGE_B(PG8_SB(0, 0), b2); PG8_STAGE_B(PG8_SB(0, 1), b2 + hstepB); PG8_STAGE_A(PG8_SA(0, 0), a2, vo2, 0);
;             PG8_WAIT_V(8); PG8_WAIT_L(0); PG8_BAR; PG8_MMA(1, 0, At, B0); PG8_MMA(1, 1, At, B1); PG8_BAR; PG8_SCHED;
;             PG8_LDB(B0, 1, 0); PG8_LDB(B1, 1, 1); PG8_SCHED; PG8_LDA(At, 1, 0); PG8_STAGE_A(PG8_SA(0, 1), a2, vo2, 1);
;             PG8_WAIT_V(8); PG8_WAIT_L(0); PG8_BAR; PG8_MMA(0, 0, At, B0); PG8_MMA(0, 1, At, B1); PG8_BAR; PG8_SCHED;
;             PG8_LDA(At, 1, 1); PG8_STAGE_B(PG8_SB(1, 0), b3); PG8_STAGE_B(PG8_SB(1, 1), b3 + hstepB); PG8_STAGE_A(PG8_SA(1, 0), a3, vo2, 0);
;             PG8_WAIT_V(8); PG8_WAIT_L(0); PG8_BAR; PG8_MMA(1, 0, At, B0); PG8_MMA(1, 1, At, B1); PG8_BAR; PG8_SCHED;
;         }
.LBB0_1123:
	s_add_u32 s14, s26, 0xfffc0080
	s_addc_u32 s15, s27, -1
	s_add_i32 s54, 0, 0x10000
	s_cmp_eq_u32 s76, 12
	s_cselect_b32 s29, s17, s15
	s_cselect_b32 s28, s23, s14
	s_cselect_b32 s15, s13, s71
	s_cselect_b32 s14, s69, s70
	s_add_i32 s62, 0, 0x14000
	v_add_u32_e32 v110, s54, v170
	v_add_u32_e32 v168, s62, v170
	ds_read_b128 v[90:93], v110
	ds_read_b128 v[98:101], v110 offset:1024
	ds_read_b128 v[102:105], v110 offset:2048
	ds_read_b128 v[110:113], v110 offset:3072
	ds_read_b128 v[174:177], v168
	ds_read_b128 v[178:181], v168 offset:1024
	ds_read_b128 v[182:185], v168 offset:2048
	ds_read_b128 v[186:189], v168 offset:3072
	v_lshl_add_u64 v[168:169], s[26:27], 0, v[164:165]
	s_add_i32 m0, s43, 0xc000
	ds_read_b128 v[190:193], v172
	ds_read_b128 v[198:201], v172 offset:1024
	ds_read_b128 v[202:205], v172 offset:2048
	ds_read_b128 v[206:209], v172 offset:3072
	ds_read_b128 v[210:213], v172 offset:4096
	ds_read_b128 v[214:217], v172 offset:5120
	ds_read_b128 v[218:221], v172 offset:6144
	ds_read_b128 v[228:231], v172 offset:7168
	global_load_lds_dwordx4 v[168:169], off
	s_add_i32 m0, s43, 0xe000
	v_lshl_add_u64 v[168:169], s[26:27], 0, v[166:167]
	global_load_lds_dwordx4 v[168:169], off
	s_waitcnt vmcnt(8)
	s_waitcnt lgkmcnt(0)
	s_barrier
	s_setprio 1
	s_waitcnt lgkmcnt(0)
	v_mfma_f32_16x16x32_bf16 v[142:145], v[90:93], v[190:193], v[142:145]
	v_mfma_f32_16x16x32_bf16 v[138:141], v[102:105], v[190:193], v[138:141]
	v_mfma_f32_16x16x32_bf16 v[126:129], v[90:93], v[202:205], v[126:129]
	v_mfma_f32_16x16x32_bf16 v[122:125], v[102:105], v[202:205], v[122:125]
	v_mfma_f32_16x16x32_bf16 v[106:109], v[90:93], v[210:213], v[106:109]
	v_mfma_f32_16x16x32_bf16 v[94:97], v[102:105], v[210:213], v[94:97]
	v_mfma_f32_16x16x32_bf16 v[78:81], v[90:93], v[218:221], v[78:81]
	v_mfma_f32_16x16x32_bf16 v[74:77], v[102:105], v[218:221], v[74:77]
	v_mfma_f32_16x16x32_bf16 v[142:145], v[98:101], v[198:201], v[142:145]
	v_mfma_f32_16x16x32_bf16 v[138:141], v[110:113], v[198:201], v[138:141]
	v_mfma_f32_16x16x32_bf16 v[126:129], v[98:101], v[206:209], v[126:129]
	v_mfma_f32_16x16x32_bf16 v[122:125], v[110:113], v[206:209], v[122:125]
	v_mfma_f32_16x16x32_bf16 v[106:109], v[98:101], v[214:217], v[106:109]
	v_mfma_f32_16x16x32_bf16 v[94:97], v[110:113], v[214:217], v[94:97]
	v_mfma_f32_16x16x32_bf16 v[78:81], v[98:101], v[228:231], v[78:81]
	v_mfma_f32_16x16x32_bf16 v[74:77], v[110:113], v[228:231], v[74:77]
	s_setprio 0
	s_setprio 1
	v_mfma_f32_16x16x32_bf16 v[134:137], v[174:177], v[190:193], v[134:137]
	v_mfma_f32_16x16x32_bf16 v[130:133], v[182:185], v[190:193], v[130:133]
	v_mfma_f32_16x16x32_bf16 v[118:121], v[174:177], v[202:205], v[118:121]
	v_mfma_f32_16x16x32_bf16 v[114:117], v[182:185], v[202:205], v[114:117]
	v_mfma_f32_16x16x32_bf16 v[86:89], v[174:177], v[210:213], v[86:89]
	v_mfma_f32_16x16x32_bf16 v[82:85], v[182:185], v[210:213], v[82:85]
	v_mfma_f32_16x16x32_bf16 v[70:73], v[174:177], v[218:221], v[70:73]
	v_mfma_f32_16x16x32_bf16 v[66:69], v[182:185], v[218:221], v[66:69]
	v_mfma_f32_16x16x32_bf16 v[134:137], v[178:181], v[198:201], v[134:137]
	v_mfma_f32_16x16x32_bf16 v[130:133], v[186:189], v[198:201], v[130:133]
	v_mfma_f32_16x16x32_bf16 v[118:121], v[178:181], v[206:209], v[118:121]
	v_mfma_f32_16x16x32_bf16 v[114:117], v[186:189], v[206:209], v[114:117]
	v_mfma_f32_16x16x32_bf16 v[86:89], v[178:181], v[214:217], v[86:89]
	v_mfma_f32_16x16x32_bf16 v[82:85], v[186:189], v[214:217], v[82:85]
	v_mfma_f32_16x16x32_bf16 v[70:73], v[178:181], v[228:231], v[70:73]
	v_mfma_f32_16x16x32_bf16 v[66:69], v[186:189], v[228:231], v[66:69]
	s_setprio 0
	s_barrier
	s_add_i32 s54, s54, s40
	v_lshl_add_u64 v[168:169], s[14:15], 0, v[194:195]
	s_mov_b32 m0, s54
	ds_read_b128 v[190:193], v172 offset:16384
	ds_read_b128 v[198:201], v172 offset:17408
	ds_read_b128 v[202:205], v172 offset:18432
	ds_read_b128 v[206:209], v172 offset:19456
	ds_read_b128 v[210:213], v172 offset:20480
	ds_read_b128 v[214:217], v172 offset:21504
	ds_read_b128 v[218:221], v172 offset:22528
	ds_read_b128 v[228:231], v172 offset:23552
	global_load_lds_dwordx4 v[168:169], off
	s_add_i32 m0, s54, 0x2000
	s_add_u32 s54, s14, 0x40000
	v_lshl_add_u64 v[222:223], s[14:15], 0, v[146:147]
	s_addc_u32 s55, s15, 0
	s_add_i32 s62, s62, s40
	global_load_lds_dwordx4 v[222:223], off
	v_lshl_add_u64 v[236:237], s[54:55], 0, v[194:195]
	s_mov_b32 m0, s62
	v_lshl_add_u64 v[238:239], s[28:29], 0, v[146:147]
	global_load_lds_dwordx4 v[236:237], off
	s_add_i32 m0, s62, 0x2000
	v_lshl_add_u64 v[236:237], s[54:55], 0, v[146:147]
	global_load_lds_dwordx4 v[236:237], off
	s_mov_b32 m0, s43
	v_lshl_add_u64 v[236:237], s[28:29], 0, v[194:195]
	global_load_lds_dwordx4 v[236:237], off
	s_mov_b32 m0, s44
	s_nop 0
	global_load_lds_dwordx4 v[238:239], off
	s_waitcnt vmcnt(8)
	s_waitcnt lgkmcnt(0)
	s_barrier
; #define PG8_STAGE_B(bufoff, gbase) do { _Pragma("unroll") for (int _i = 0; _i < 2; ++_i) \
;         __builtin_amdgcn_global_load_lds((const unsigned*)((const char*)(gbase) + voffB[_i]), (LAS unsigned*)(lds + (bufoff) + ldsw + _i * 8192), 16, 0, 0); } while (0)
; #define PG8_LDA(dst, b, h) do { _Pragma("unroll") for (int m = 0; m < 4; ++m) _Pragma("unroll") for (int k = 0; k < 2; ++k) dst[m][k] = *(const LAS bf16x8*)(lds + PG8_SA(b, h) + aoff + m * 2048 + k * 1024); } while (0)
; #define PG8_LDB(dst, b, h) do { _Pragma("unroll") for (int n = 0; n < 2; ++n) _Pragma("unroll") for (int k = 0; k < 2; ++k) dst[n][k] = *(const LAS bf16x8*)(lds + PG8_SB(b, h) + boff + n * 2048 + k * 1024); } while (0)
; #define PG8_MMA(ai, bj, At, Bt) do { __builtin_amdgcn_s_setprio(1); _Pragma("unroll") for (int m = 0; m < 4; ++m) _Pragma("unroll") for (int n = 0; n < 2; ++n) _Pragma("unroll") for (int k = 0; k < 2; ++k) \
;         acc[ai][bj][m][n] = __builtin_amdgcn_mfma_f32_16x16x32_bf16(Bt[n][k], At[m][k], acc[ai][bj][m][n], 0, 0, 0); __builtin_amdgcn_s_setprio(0); } while (0)
; #define PG8_WAIT_V(n) asm volatile("s_waitcnt vmcnt(" #n ")" ::: "memory")
; #define PG8_WAIT_L(n) asm volatile("s_waitcnt lgkmcnt(" #n ")" ::: "memory")
; #define PG8_BAR __builtin_amdgcn_s_barrier()
; #define PG8_SCHED __builtin_amdgcn_sched_barrier(0)
; template <class Epi, class Sched, bool GATHER = false>
; __device__ __forceinline__ void gemm_phase(LAS unsigned char* lds, const Gemm g, const Sched& S, const Epi& E) {
;     ...
;             PG8_WAIT_V(8); PG8_WAIT_L(0); PG8_BAR; PG8_MMA(0, 0, At, B0); PG8_MMA(0, 1, At, B1); PG8_BAR; PG8_SCHED;
;             PG8_LDA(At, 0, 1); PG8_STAGE_B(PG8_SB(0, 0), b2); PG8_STAGE_B(PG8_SB(0, 1), b2 + hstepB); PG8_STAGE_A(PG8_SA(0, 0), a2, vo2, 0);
;             PG8_WAIT_V(8); PG8_WAIT_L(0); PG8_BAR; PG8_MMA(1, 0, At, B0); PG8_MMA(1, 1, At, B1); PG8_BAR; PG8_SCHED;
;             PG8_LDB(B0, 1, 0); PG8_LDB(B1, 1, 1); PG8_SCHED; PG8_LDA(At, 1, 0); PG8_STAGE_A(PG8_SA(0, 1), a2, vo2, 1);
;             PG8_WAIT_V(8); PG8_WAIT_L(0); PG8_BAR; PG8_MMA(0, 0, At, B0); PG8_MMA(0, 1, At, B1); PG8_BAR; PG8_SCHED;
	s_setprio 1
	s_waitcnt lgkmcnt(0)
	v_mfma_f32_16x16x32_bf16 v[62:65], v[90:93], v[190:193], v[62:65]
	v_mfma_f32_16x16x32_bf16 v[58:61], v[102:105], v[190:193], v[58:61]
	v_mfma_f32_16x16x32_bf16 v[46:49], v[90:93], v[202:205], v[46:49]
	v_mfma_f32_16x16x32_bf16 v[42:45], v[102:105], v[202:205], v[42:45]
	v_mfma_f32_16x16x32_bf16 v[30:33], v[90:93], v[210:213], v[30:33]
	v_mfma_f32_16x16x32_bf16 v[26:29], v[102:105], v[210:213], v[26:29]
	v_mfma_f32_16x16x32_bf16 v[14:17], v[90:93], v[218:221], v[14:17]
	v_mfma_f32_16x16x32_bf16 v[10:13], v[102:105], v[218:221], v[10:13]
	v_mfma_f32_16x16x32_bf16 v[62:65], v[98:101], v[198:201], v[62:65]
	v_mfma_f32_16x16x32_bf16 v[58:61], v[110:113], v[198:201], v[58:61]
	v_mfma_f32_16x16x32_bf16 v[46:49], v[98:101], v[206:209], v[46:49]
	v_mfma_f32_16x16x32_bf16 v[42:45], v[110:113], v[206:209], v[42:45]
	v_mfma_f32_16x16x32_bf16 v[30:33], v[98:101], v[214:217], v[30:33]
	v_mfma_f32_16x16x32_bf16 v[26:29], v[110:113], v[214:217], v[26:29]
	v_mfma_f32_16x16x32_bf16 v[14:17], v[98:101], v[228:231], v[14:17]
	v_mfma_f32_16x16x32_bf16 v[10:13], v[110:113], v[228:231], v[10:13]
	s_setprio 0
	s_setprio 1
	v_mfma_f32_16x16x32_bf16 v[54:57], v[174:177], v[190:193], v[54:57]
	v_mfma_f32_16x16x32_bf16 v[50:53], v[182:185], v[190:193], v[50:53]
	v_mfma_f32_16x16x32_bf16 v[38:41], v[174:177], v[202:205], v[38:41]
	v_mfma_f32_16x16x32_bf16 v[34:37], v[182:185], v[202:205], v[34:37]
	v_mfma_f32_16x16x32_bf16 v[22:25], v[174:177], v[210:213], v[22:25]
	v_mfma_f32_16x16x32_bf16 v[18:21], v[182:185], v[210:213], v[18:21]
	v_mfma_f32_16x16x32_bf16 v[6:9], v[174:177], v[218:221], v[6:9]
	v_mfma_f32_16x16x32_bf16 v[2:5], v[182:185], v[218:221], v[2:5]
	v_mfma_f32_16x16x32_bf16 v[54:57], v[178:181], v[198:201], v[54:57]
	v_mfma_f32_16x16x32_bf16 v[50:53], v[186:189], v[198:201], v[50:53]
	v_mfma_f32_16x16x32_bf16 v[38:41], v[178:181], v[206:209], v[38:41]
	v_mfma_f32_16x16x32_bf16 v[34:37], v[186:189], v[206:209], v[34:37]
	v_mfma_f32_16x16x32_bf16 v[22:25], v[178:181], v[214:217], v[22:25]
	v_mfma_f32_16x16x32_bf16 v[18:21], v[186:189], v[214:217], v[18:21]
	v_mfma_f32_16x16x32_bf16 v[6:9], v[178:181], v[228:231], v[6:9]
	v_mfma_f32_16x16x32_bf16 v[2:5], v[186:189], v[228:231], v[2:5]
	s_setprio 0
	s_barrier
	s_add_i32 s54, 0, 0x18000
	s_add_i32 s55, 0, 0x1c000
	v_add_u32_e32 v110, s54, v170
	v_add_u32_e32 v173, s55, v170
	ds_read_b128 v[90:93], v110
	ds_read_b128 v[98:101], v110 offset:1024
	ds_read_b128 v[102:105], v110 offset:2048
	ds_read_b128 v[110:113], v110 offset:3072
	ds_read_b128 v[174:177], v173
	ds_read_b128 v[178:181], v173 offset:1024
	ds_read_b128 v[182:185], v173 offset:2048
	ds_read_b128 v[186:189], v173 offset:3072
	s_add_u32 s28, s28, 0x40000
	s_addc_u32 s29, s29, 0
	s_mov_b32 m0, s45
	v_lshl_add_u64 v[240:241], s[28:29], 0, v[194:195]
	ds_read_b128 v[190:193], v172 offset:32768
	ds_read_b128 v[198:201], v172 offset:33792
	ds_read_b128 v[202:205], v172 offset:34816
	ds_read_b128 v[206:209], v172 offset:35840
	ds_read_b128 v[210:213], v172 offset:36864
	ds_read_b128 v[214:217], v172 offset:37888
	ds_read_b128 v[218:221], v172 offset:38912
	ds_read_b128 v[228:231], v172 offset:39936
	global_load_lds_dwordx4 v[240:241], off
	s_mov_b32 m0, s46
	v_lshl_add_u64 v[240:241], s[28:29], 0, v[146:147]
	global_load_lds_dwordx4 v[240:241], off
	s_waitcnt vmcnt(8)
	s_waitcnt lgkmcnt(0)
	s_barrier
	s_setprio 1
	s_waitcnt lgkmcnt(0)
	v_mfma_f32_16x16x32_bf16 v[142:145], v[90:93], v[190:193], v[142:145]
	v_mfma_f32_16x16x32_bf16 v[138:141], v[102:105], v[190:193], v[138:141]
	v_mfma_f32_16x16x32_bf16 v[126:129], v[90:93], v[202:205], v[126:129]
	v_mfma_f32_16x16x32_bf16 v[122:125], v[102:105], v[202:205], v[122:125]
	v_mfma_f32_16x16x32_bf16 v[106:109], v[90:93], v[210:213], v[106:109]
	v_mfma_f32_16x16x32_bf16 v[94:97], v[102:105], v[210:213], v[94:97]
	v_mfma_f32_16x16x32_bf16 v[78:81], v[90:93], v[218:221], v[78:81]
	v_mfma_f32_16x16x32_bf16 v[74:77], v[102:105], v[218:221], v[74:77]
	v_mfma_f32_16x16x32_bf16 v[142:145], v[98:101], v[198:201], v[142:145]
	v_mfma_f32_16x16x32_bf16 v[138:141], v[110:113], v[198:201], v[138:141]
	v_mfma_f32_16x16x32_bf16 v[126:129], v[98:101], v[206:209], v[126:129]
	v_mfma_f32_16x16x32_bf16 v[122:125], v[110:113], v[206:209], v[122:125]
	v_mfma_f32_16x16x32_bf16 v[106:109], v[98:101], v[214:217], v[106:109]
	v_mfma_f32_16x16x32_bf16 v[94:97], v[110:113], v[214:217], v[94:97]
	v_mfma_f32_16x16x32_bf16 v[78:81], v[98:101], v[228:231], v[78:81]
	v_mfma_f32_16x16x32_bf16 v[74:77], v[110:113], v[228:231], v[74:77]
	s_setprio 0
	s_setprio 1
	v_mfma_f32_16x16x32_bf16 v[134:137], v[174:177], v[190:193], v[134:137]
	v_mfma_f32_16x16x32_bf16 v[130:133], v[182:185], v[190:193], v[130:133]
	v_mfma_f32_16x16x32_bf16 v[118:121], v[174:177], v[202:205], v[118:121]
	v_mfma_f32_16x16x32_bf16 v[114:117], v[182:185], v[202:205], v[114:117]
	v_mfma_f32_16x16x32_bf16 v[86:89], v[174:177], v[210:213], v[86:89]
	v_mfma_f32_16x16x32_bf16 v[82:85], v[182:185], v[210:213], v[82:85]
	v_mfma_f32_16x16x32_bf16 v[70:73], v[174:177], v[218:221], v[70:73]
	v_mfma_f32_16x16x32_bf16 v[66:69], v[182:185], v[218:221], v[66:69]
	v_mfma_f32_16x16x32_bf16 v[134:137], v[178:181], v[198:201], v[134:137]
	v_mfma_f32_16x16x32_bf16 v[130:133], v[186:189], v[198:201], v[130:133]
	v_mfma_f32_16x16x32_bf16 v[118:121], v[178:181], v[206:209], v[118:121]
	v_mfma_f32_16x16x32_bf16 v[114:117], v[186:189], v[206:209], v[114:117]
	v_mfma_f32_16x16x32_bf16 v[86:89], v[178:181], v[214:217], v[86:89]
	v_mfma_f32_16x16x32_bf16 v[82:85], v[186:189], v[214:217], v[82:85]
	v_mfma_f32_16x16x32_bf16 v[70:73], v[178:181], v[228:231], v[70:73]
	v_mfma_f32_16x16x32_bf16 v[66:69], v[186:189], v[228:231], v[66:69]
	s_setprio 0
	s_barrier
; #define PG8_STAGE_B(bufoff, gbase) do { _Pragma("unroll") for (int _i = 0; _i < 2; ++_i) \
;         __builtin_amdgcn_global_load_lds((const unsigned*)((const char*)(gbase) + voffB[_i]), (LAS unsigned*)(lds + (bufoff) + ldsw + _i * 8192), 16, 0, 0); } while (0)
; #define PG8_LDA(dst, b, h) do { _Pragma("unroll") for (int m = 0; m < 4; ++m) _Pragma("unroll") for (int k = 0; k < 2; ++k) dst[m][k] = *(const LAS bf16x8*)(lds + PG8_SA(b, h) + aoff + m * 2048 + k * 1024); } while (0)
; #define PG8_WAIT_V(n) asm volatile("s_waitcnt vmcnt(" #n ")" ::: "memory")
; template <class Epi, class Sched, bool GATHER = false>
; __device__ __forceinline__ void gemm_phase(LAS unsigned char* lds, const Gemm g, const Sched& S, const Epi& E) {
;     ...
;         for (int t = 0; t < nt; t += 2) {
;             const bool last = (t == nt - 2);
;             const char* a1 = cA + (size_t)(t + 1) * kstep;
;             const char* a2 = last ? nA : cA + (size_t)(t + 2) * kstep; const char* b2 = last ? nB : cB + (size_t)(t + 2) * kstep;
;             const char* a3 = a2 + kstep; const char* b3 = b2 + kstep;
;             unsigned vo2[2][2];
;             if constexpr (GATHER) {
; #pragma unroll
;             for (int _h = 0; _h < 2; ++_h)
; #pragma unroll
;                 for (int _i = 0; _i < 2; ++_i) vo2[_h][_i] = last ? voN[_h][_i] : voC[_h][_i]; }
;             PG8_LDB(B0, 0, 0); PG8_LDB(B1, 0, 1); PG8_SCHED; PG8_LDA(At, 0, 0); PG8_STAGE_A(PG8_SA(1, 1), a1, voC, 1);
;             PG8_WAIT_V(8); PG8_WAIT_L(0); PG8_BAR; PG8_MMA(0, 0, At, B0); PG8_MMA(0, 1, At, B1); PG8_BAR; PG8_SCHED;
;             PG8_LDA(At, 0, 1); PG8_STAGE_B(PG8_SB(0, 0), b2); PG8_STAGE_B(PG8_SB(0, 1), b2 + hstepB); PG8_STAGE_A(PG8_SA(0, 0), a2, vo2, 0);
;             PG8_WAIT_V(8); PG8_WAIT_L(0); PG8_BAR; PG8_MMA(1, 0, At, B0); PG8_MMA(1, 1, At, B1); PG8_BAR; PG8_SCHED;
;             PG8_LDB(B0, 1, 0); PG8_LDB(B1, 1, 1); PG8_SCHED; PG8_LDA(At, 1, 0); PG8_STAGE_A(PG8_SA(0, 1), a2, vo2, 1);
;             PG8_WAIT_V(8); PG8_WAIT_L(0); PG8_BAR; PG8_MMA(0, 0, At, B0); PG8_MMA(0, 1, At, B1); PG8_BAR; PG8_SCHED;
;             PG8_LDA(At, 1, 1); PG8_STAGE_B(PG8_SB(1, 0), b3); PG8_STAGE_B(PG8_SB(1, 1), b3 + hstepB); PG8_STAGE_A(PG8_SA(1, 0), a3, vo2, 0);
;             PG8_WAIT_V(8); PG8_WAIT_L(0); PG8_BAR; PG8_MMA(1, 0, At, B0); PG8_MMA(1, 1, At, B1); PG8_BAR; PG8_SCHED;
;         }
;         if (wr == 0) PG8_BAR;
	s_add_i32 s28, s54, s40
	v_lshl_add_u64 v[168:169], v[168:169], 0, s[66:67]
	s_mov_b32 m0, s28
	ds_read_b128 v[190:193], v172 offset:49152
	ds_read_b128 v[198:201], v172 offset:50176
	ds_read_b128 v[202:205], v172 offset:51200
	ds_read_b128 v[206:209], v172 offset:52224
	ds_read_b128 v[210:213], v172 offset:53248
	ds_read_b128 v[214:217], v172 offset:54272
	ds_read_b128 v[218:221], v172 offset:55296
	ds_read_b128 v[228:231], v172 offset:56320
	global_load_lds_dwordx4 v[168:169], off
	s_add_i32 m0, s28, 0x2000
	s_add_u32 s14, s14, 0x40080
	v_lshl_add_u64 v[168:169], v[222:223], 0, s[66:67]
	s_addc_u32 s15, s15, 0
	s_add_i32 s28, s55, s40
	global_load_lds_dwordx4 v[168:169], off
	s_mov_b32 m0, s28
	v_lshl_add_u64 v[168:169], s[14:15], 0, v[194:195]
	global_load_lds_dwordx4 v[168:169], off
	s_add_i32 m0, s28, 0x2000
	v_lshl_add_u64 v[168:169], s[14:15], 0, v[146:147]
	global_load_lds_dwordx4 v[168:169], off
	s_mov_b32 m0, s51
	v_lshl_add_u64 v[168:169], v[236:237], 0, s[66:67]
	global_load_lds_dwordx4 v[168:169], off
	s_mov_b32 m0, s52
	v_lshl_add_u64 v[168:169], v[238:239], 0, s[66:67]
	global_load_lds_dwordx4 v[168:169], off
	s_waitcnt vmcnt(8)
	s_waitcnt lgkmcnt(0)
	s_barrier
	s_setprio 1
	s_waitcnt lgkmcnt(0)
	v_mfma_f32_16x16x32_bf16 v[62:65], v[90:93], v[190:193], v[62:65]
	v_mfma_f32_16x16x32_bf16 v[58:61], v[102:105], v[190:193], v[58:61]
	v_mfma_f32_16x16x32_bf16 v[46:49], v[90:93], v[202:205], v[46:49]
	v_mfma_f32_16x16x32_bf16 v[42:45], v[102:105], v[202:205], v[42:45]
	v_mfma_f32_16x16x32_bf16 v[30:33], v[90:93], v[210:213], v[30:33]
	v_mfma_f32_16x16x32_bf16 v[26:29], v[102:105], v[210:213], v[26:29]
	v_mfma_f32_16x16x32_bf16 v[14:17], v[90:93], v[218:221], v[14:17]
	v_mfma_f32_16x16x32_bf16 v[10:13], v[102:105], v[218:221], v[10:13]
	v_mfma_f32_16x16x32_bf16 v[62:65], v[98:101], v[198:201], v[62:65]
	v_mfma_f32_16x16x32_bf16 v[58:61], v[110:113], v[198:201], v[58:61]
	v_mfma_f32_16x16x32_bf16 v[46:49], v[98:101], v[206:209], v[46:49]
	v_mfma_f32_16x16x32_bf16 v[42:45], v[110:113], v[206:209], v[42:45]
	v_mfma_f32_16x16x32_bf16 v[30:33], v[98:101], v[214:217], v[30:33]
	v_mfma_f32_16x16x32_bf16 v[26:29], v[110:113], v[214:217], v[26:29]
	v_mfma_f32_16x16x32_bf16 v[14:17], v[98:101], v[228:231], v[14:17]
	v_mfma_f32_16x16x32_bf16 v[10:13], v[110:113], v[228:231], v[10:13]
	s_setprio 0
	s_setprio 1
	v_mfma_f32_16x16x32_bf16 v[54:57], v[174:177], v[190:193], v[54:57]
	v_mfma_f32_16x16x32_bf16 v[50:53], v[182:185], v[190:193], v[50:53]
	v_mfma_f32_16x16x32_bf16 v[38:41], v[174:177], v[202:205], v[38:41]
	v_mfma_f32_16x16x32_bf16 v[34:37], v[182:185], v[202:205], v[34:37]
	v_mfma_f32_16x16x32_bf16 v[22:25], v[174:177], v[210:213], v[22:25]
	v_mfma_f32_16x16x32_bf16 v[18:21], v[182:185], v[210:213], v[18:21]
	v_mfma_f32_16x16x32_bf16 v[6:9], v[174:177], v[218:221], v[6:9]
	v_mfma_f32_16x16x32_bf16 v[2:5], v[182:185], v[218:221], v[2:5]
	v_mfma_f32_16x16x32_bf16 v[54:57], v[178:181], v[198:201], v[54:57]
	v_mfma_f32_16x16x32_bf16 v[50:53], v[186:189], v[198:201], v[50:53]
	v_mfma_f32_16x16x32_bf16 v[38:41], v[178:181], v[206:209], v[38:41]
	v_mfma_f32_16x16x32_bf16 v[34:37], v[186:189], v[206:209], v[34:37]
	v_mfma_f32_16x16x32_bf16 v[22:25], v[178:181], v[214:217], v[22:25]
	v_mfma_f32_16x16x32_bf16 v[18:21], v[186:189], v[214:217], v[18:21]
	v_mfma_f32_16x16x32_bf16 v[6:9], v[178:181], v[228:231], v[6:9]
	v_mfma_f32_16x16x32_bf16 v[2:5], v[186:189], v[228:231], v[2:5]
	s_setprio 0
	s_barrier
	s_add_i32 s76, s76, 2
	s_add_u32 s26, s26, 0x100
	s_addc_u32 s27, s27, 0
	s_add_u32 s70, s70, 0x100
	s_addc_u32 s71, s71, 0
	s_cmp_gt_u32 s76, 13
	s_cbranch_scc0 .LBB0_1123
	s_and_b64 vcc, exec, s[10:11]
	s_cbranch_vccz .LBB0_1126
	s_barrier

; #define PG8_STAGE_B(bufoff, gbase) do { _Pragma("unroll") for (int _i = 0; _i < 2; ++_i) \
;         __builtin_amdgcn_global_load_lds((const unsigned*)((const char*)(gbase) + voffB[_i]), (LAS unsigned*)(lds + (bufoff) + ldsw + _i * 8192), 16, 0, 0); } while (0)
; #define PG8_LDA(dst, b, h) do { _Pragma("unroll") for (int m = 0; m < 4; ++m) _Pragma("unroll") for (int k = 0; k < 2; ++k) dst[m][k] = *(const LAS bf16x8*)(lds + PG8_SA(b, h) + aoff + m * 2048 + k * 1024); } while (0)
; #define PG8_WAIT_V(n) asm volatile("s_waitcnt vmcnt(" #n ")" ::: "memory")
; template <class Epi, class Sched, bool GATHER = false>
; __device__ __forceinline__ void gemm_phase(LAS unsigned char* lds, const Gemm g, const Sched& S, const Epi& E) {
;     ...
;         for (int t = 0; t < nt; t += 2) {
;             const bool last = (t == nt - 2);
;             const char* a1 = cA + (size_t)(t + 1) * kstep;
;             const char* a2 = last ? nA : cA + (size_t)(t + 2) * kstep; const char* b2 = last ? nB : cB + (size_t)(t + 2) * kstep;
;             const char* a3 = a2 + kstep; const char* b3 = b2 + kstep;
;             unsigned vo2[2][2];
;             if constexpr (GATHER) {
; #pragma unroll
;             for (int _h = 0; _h < 2; ++_h)
; #pragma unroll
;                 for (int _i = 0; _i < 2; ++_i) vo2[_h][_i] = last ? voN[_h][_i] : voC[_h][_i]; }
;             PG8_LDB(B0, 0, 0); PG8_LDB(B1, 0, 1); PG8_SCHED; PG8_LDA(At, 0, 0); PG8_STAGE_A(PG8_SA(1, 1), a1, voC, 1);
;             PG8_WAIT_V(8); PG8_WAIT_L(0); PG8_BAR; PG8_MMA(0, 0, At, B0); PG8_MMA(0, 1, At, B1); PG8_BAR; PG8_SCHED;
;             PG8_LDA(At, 0, 1); PG8_STAGE_B(PG8_SB(0, 0), b2); PG8_STAGE_B(PG8_SB(0, 1), b2 + hstepB); PG8_STAGE_A(PG8_SA(0, 0), a2, vo2, 0);
;             PG8_WAIT_V(8); PG8_WAIT_L(0); PG8_BAR; PG8_MMA(1, 0, At, B0); PG8_MMA(1, 1, At, B1); PG8_BAR; PG8_SCHED;
;             PG8_LDB(B0, 1, 0); PG8_LDB(B1, 1, 1); PG8_SCHED; PG8_LDA(At, 1, 0); PG8_STAGE_A(PG8_SA(0, 1), a2, vo2, 1);
;             PG8_WAIT_V(8); PG8_WAIT_L(0); PG8_BAR; PG8_MMA(0, 0, At, B0); PG8_MMA(0, 1, At, B1); PG8_BAR; PG8_SCHED;
;             PG8_LDA(At, 1, 1); PG8_STAGE_B(PG8_SB(1, 0), b3); PG8_STAGE_B(PG8_SB(1, 1), b3 + hstepB); PG8_STAGE_A(PG8_SA(1, 0), a3, vo2, 0);
;             PG8_WAIT_V(8); PG8_WAIT_L(0); PG8_BAR; PG8_MMA(1, 0, At, B0); PG8_MMA(1, 1, At, B1); PG8_BAR; PG8_SCHED;
;         }
.LBB0_1402:
	s_add_u32 s28, s34, s26
	s_addc_u32 s29, s35, s27
	s_add_u32 s30, s28, 0x81ee400
	s_addc_u32 s31, s29, 0
	s_add_u32 s53, s50, s26
	s_addc_u32 s54, s51, s27
	s_cmpk_eq_i32 s26, 0x700
	s_cselect_b64 vcc, -1, 0
	s_and_b64 s[28:29], vcc, exec
	s_cselect_b32 s31, s7, s31
	s_cselect_b32 s30, s6, s30
	s_cselect_b32 s29, s19, s54
	s_cselect_b32 s28, s49, s53
	s_add_i32 s53, 0, 0x10000
	v_add_u32_e32 v141, s53, v150
	s_add_i32 s58, 0, 0x14000
	ds_read_b128 v[156:159], v141
	ds_read_b128 v[160:163], v141 offset:1024
	ds_read_b128 v[164:167], v141 offset:2048
	ds_read_b128 v[168:171], v141 offset:3072
	v_add_u32_e32 v141, s58, v150
	ds_read_b128 v[172:175], v141
	ds_read_b128 v[176:179], v141 offset:1024
	ds_read_b128 v[180:183], v141 offset:2048
	ds_read_b128 v[184:187], v141 offset:3072
	v_lshl_add_u32 v152, v244, 11, v146
	v_lshl_add_u32 v153, v245, 11, v148
	v_lshl_add_u32 v154, v246, 11, v146
	v_lshl_add_u32 v155, v247, 11, v148
	v_cndmask_b32_e32 v194, v134, v152, vcc
	v_cndmask_b32_e32 v192, v136, v153, vcc
	v_cndmask_b32_e32 v135, v138, v154, vcc
	v_cndmask_b32_e32 v139, v140, v155, vcc
	v_lshl_add_u64 v[236:237], v[144:145], 0, s[26:27]
	s_add_i32 m0, s23, 0xc000
	ds_read_b128 v[188:191], v151
	ds_read_b128 v[198:201], v151 offset:1024
	ds_read_b128 v[204:207], v151 offset:2048
	ds_read_b128 v[208:211], v151 offset:3072
	ds_read_b128 v[212:215], v151 offset:4096
	ds_read_b128 v[216:219], v151 offset:5120
	ds_read_b128 v[220:223], v151 offset:6144
	ds_read_b128 v[228:231], v151 offset:7168
	global_load_lds_dwordx4 v[236:237], off
	s_add_i32 m0, s23, 0xe000
	v_lshl_add_u64 v[236:237], v[142:143], 0, s[26:27]
	global_load_lds_dwordx4 v[236:237], off
	s_waitcnt vmcnt(8)
	s_waitcnt lgkmcnt(0)
	s_barrier
	s_setprio 1
	s_waitcnt lgkmcnt(0)
	v_mfma_f32_16x16x32_bf16 v[126:129], v[156:159], v[188:191], v[126:129]
	v_mfma_f32_16x16x32_bf16 v[122:125], v[164:167], v[188:191], v[122:125]
	v_mfma_f32_16x16x32_bf16 v[110:113], v[156:159], v[204:207], v[110:113]
	v_mfma_f32_16x16x32_bf16 v[106:109], v[164:167], v[204:207], v[106:109]
	v_mfma_f32_16x16x32_bf16 v[94:97], v[156:159], v[212:215], v[94:97]
	v_mfma_f32_16x16x32_bf16 v[90:93], v[164:167], v[212:215], v[90:93]
	v_mfma_f32_16x16x32_bf16 v[78:81], v[156:159], v[220:223], v[78:81]
	v_mfma_f32_16x16x32_bf16 v[74:77], v[164:167], v[220:223], v[74:77]
	v_mfma_f32_16x16x32_bf16 v[126:129], v[160:163], v[198:201], v[126:129]
	v_mfma_f32_16x16x32_bf16 v[122:125], v[168:171], v[198:201], v[122:125]
	v_mfma_f32_16x16x32_bf16 v[110:113], v[160:163], v[208:211], v[110:113]
	v_mfma_f32_16x16x32_bf16 v[106:109], v[168:171], v[208:211], v[106:109]
	v_mfma_f32_16x16x32_bf16 v[94:97], v[160:163], v[216:219], v[94:97]
	v_mfma_f32_16x16x32_bf16 v[90:93], v[168:171], v[216:219], v[90:93]
	v_mfma_f32_16x16x32_bf16 v[78:81], v[160:163], v[228:231], v[78:81]
	v_mfma_f32_16x16x32_bf16 v[74:77], v[168:171], v[228:231], v[74:77]
	s_setprio 0
	s_setprio 1
	v_mfma_f32_16x16x32_bf16 v[118:121], v[172:175], v[188:191], v[118:121]
	v_mfma_f32_16x16x32_bf16 v[114:117], v[180:183], v[188:191], v[114:117]
	v_mfma_f32_16x16x32_bf16 v[102:105], v[172:175], v[204:207], v[102:105]
	v_mfma_f32_16x16x32_bf16 v[98:101], v[180:183], v[204:207], v[98:101]
	v_mfma_f32_16x16x32_bf16 v[86:89], v[172:175], v[212:215], v[86:89]
	v_mfma_f32_16x16x32_bf16 v[82:85], v[180:183], v[212:215], v[82:85]
	v_mfma_f32_16x16x32_bf16 v[70:73], v[172:175], v[220:223], v[70:73]
	v_mfma_f32_16x16x32_bf16 v[66:69], v[180:183], v[220:223], v[66:69]
	v_mfma_f32_16x16x32_bf16 v[118:121], v[176:179], v[198:201], v[118:121]
	v_mfma_f32_16x16x32_bf16 v[114:117], v[184:187], v[198:201], v[114:117]
	v_mfma_f32_16x16x32_bf16 v[102:105], v[176:179], v[208:211], v[102:105]
	v_mfma_f32_16x16x32_bf16 v[98:101], v[184:187], v[208:211], v[98:101]
	v_mfma_f32_16x16x32_bf16 v[86:89], v[176:179], v[216:219], v[86:89]
	v_mfma_f32_16x16x32_bf16 v[82:85], v[184:187], v[216:219], v[82:85]
	v_mfma_f32_16x16x32_bf16 v[70:73], v[176:179], v[228:231], v[70:73]
	v_mfma_f32_16x16x32_bf16 v[66:69], v[184:187], v[228:231], v[66:69]
	s_setprio 0
	s_barrier
	s_add_i32 s53, s53, s40
	v_lshl_add_u64 v[236:237], s[28:29], 0, v[130:131]
	s_mov_b32 m0, s53
	ds_read_b128 v[188:191], v151 offset:16384
	ds_read_b128 v[198:201], v151 offset:17408
	ds_read_b128 v[204:207], v151 offset:18432
	ds_read_b128 v[208:211], v151 offset:19456
	ds_read_b128 v[212:215], v151 offset:20480
	ds_read_b128 v[216:219], v151 offset:21504
	ds_read_b128 v[220:223], v151 offset:22528
	ds_read_b128 v[228:231], v151 offset:23552
	global_load_lds_dwordx4 v[236:237], off
	s_add_i32 m0, s53, 0x2000
	s_add_u32 s54, s28, 0x40000
	v_lshl_add_u64 v[238:239], s[28:29], 0, v[132:133]
	s_addc_u32 s55, s29, 0
	s_add_i32 s53, s58, s40
	global_load_lds_dwordx4 v[238:239], off
	v_lshl_add_u64 v[240:241], s[54:55], 0, v[130:131]
	s_mov_b32 m0, s53
	v_mov_b32_e32 v193, v195
	global_load_lds_dwordx4 v[240:241], off
	s_add_i32 m0, s53, 0x2000
	v_lshl_add_u64 v[240:241], s[54:55], 0, v[132:133]
	global_load_lds_dwordx4 v[240:241], off
	s_mov_b32 m0, s23
	v_lshl_add_u64 v[240:241], s[30:31], 0, v[194:195]
	global_load_lds_dwordx4 v194, s[30:31]
	s_mov_b32 m0, s41
	s_nop 0
	global_load_lds_dwordx4 v192, s[30:31]
	s_waitcnt vmcnt(8)
	s_waitcnt lgkmcnt(0)
	v_lshl_add_u64 v[192:193], s[30:31], 0, v[192:193]
	s_barrier
; #define PG8_LDA(dst, b, h) do { _Pragma("unroll") for (int m = 0; m < 4; ++m) _Pragma("unroll") for (int k = 0; k < 2; ++k) dst[m][k] = *(const LAS bf16x8*)(lds + PG8_SA(b, h) + aoff + m * 2048 + k * 1024); } while (0)
; #define PG8_LDB(dst, b, h) do { _Pragma("unroll") for (int n = 0; n < 2; ++n) _Pragma("unroll") for (int k = 0; k < 2; ++k) dst[n][k] = *(const LAS bf16x8*)(lds + PG8_SB(b, h) + boff + n * 2048 + k * 1024); } while (0)
; #define PG8_MMA(ai, bj, At, Bt) do { __builtin_amdgcn_s_setprio(1); _Pragma("unroll") for (int m = 0; m < 4; ++m) _Pragma("unroll") for (int n = 0; n < 2; ++n) _Pragma("unroll") for (int k = 0; k < 2; ++k) \
;         acc[ai][bj][m][n] = __builtin_amdgcn_mfma_f32_16x16x32_bf16(Bt[n][k], At[m][k], acc[ai][bj][m][n], 0, 0, 0); __builtin_amdgcn_s_setprio(0); } while (0)
; #define PG8_WAIT_V(n) asm volatile("s_waitcnt vmcnt(" #n ")" ::: "memory")
; #define PG8_WAIT_L(n) asm volatile("s_waitcnt lgkmcnt(" #n ")" ::: "memory")
; #define PG8_BAR __builtin_amdgcn_s_barrier()
; #define PG8_SCHED __builtin_amdgcn_sched_barrier(0)
; template <class Epi, class Sched, bool GATHER = false>
; __device__ __forceinline__ void gemm_phase(LAS unsigned char* lds, const Gemm g, const Sched& S, const Epi& E) {
;     ...
;             PG8_WAIT_V(8); PG8_WAIT_L(0); PG8_BAR; PG8_MMA(1, 0, At, B0); PG8_MMA(1, 1, At, B1); PG8_BAR; PG8_SCHED;
;             PG8_LDB(B0, 1, 0); PG8_LDB(B1, 1, 1); PG8_SCHED; PG8_LDA(At, 1, 0); PG8_STAGE_A(PG8_SA(0, 1), a2, vo2, 1);
;             PG8_WAIT_V(8); PG8_WAIT_L(0); PG8_BAR; PG8_MMA(0, 0, At, B0); PG8_MMA(0, 1, At, B1); PG8_BAR; PG8_SCHED;
	s_setprio 1
	s_waitcnt lgkmcnt(0)
	v_mfma_f32_16x16x32_bf16 v[62:65], v[156:159], v[188:191], v[62:65]
	v_mfma_f32_16x16x32_bf16 v[58:61], v[164:167], v[188:191], v[58:61]
	v_mfma_f32_16x16x32_bf16 v[46:49], v[156:159], v[204:207], v[46:49]
	v_mfma_f32_16x16x32_bf16 v[42:45], v[164:167], v[204:207], v[42:45]
	v_mfma_f32_16x16x32_bf16 v[30:33], v[156:159], v[212:215], v[30:33]
	v_mfma_f32_16x16x32_bf16 v[26:29], v[164:167], v[212:215], v[26:29]
	v_mfma_f32_16x16x32_bf16 v[14:17], v[156:159], v[220:223], v[14:17]
	v_mfma_f32_16x16x32_bf16 v[10:13], v[164:167], v[220:223], v[10:13]
	v_mfma_f32_16x16x32_bf16 v[62:65], v[160:163], v[198:201], v[62:65]
	v_mfma_f32_16x16x32_bf16 v[58:61], v[168:171], v[198:201], v[58:61]
	v_mfma_f32_16x16x32_bf16 v[46:49], v[160:163], v[208:211], v[46:49]
	v_mfma_f32_16x16x32_bf16 v[42:45], v[168:171], v[208:211], v[42:45]
	v_mfma_f32_16x16x32_bf16 v[30:33], v[160:163], v[216:219], v[30:33]
	v_mfma_f32_16x16x32_bf16 v[26:29], v[168:171], v[216:219], v[26:29]
	v_mfma_f32_16x16x32_bf16 v[14:17], v[160:163], v[228:231], v[14:17]
	v_mfma_f32_16x16x32_bf16 v[10:13], v[168:171], v[228:231], v[10:13]
	s_setprio 0
	s_setprio 1
	v_mfma_f32_16x16x32_bf16 v[54:57], v[172:175], v[188:191], v[54:57]
	v_mfma_f32_16x16x32_bf16 v[50:53], v[180:183], v[188:191], v[50:53]
	v_mfma_f32_16x16x32_bf16 v[38:41], v[172:175], v[204:207], v[38:41]
	v_mfma_f32_16x16x32_bf16 v[34:37], v[180:183], v[204:207], v[34:37]
	v_mfma_f32_16x16x32_bf16 v[22:25], v[172:175], v[212:215], v[22:25]
	v_mfma_f32_16x16x32_bf16 v[18:21], v[180:183], v[212:215], v[18:21]
	v_mfma_f32_16x16x32_bf16 v[6:9], v[172:175], v[220:223], v[6:9]
	v_mfma_f32_16x16x32_bf16 v[2:5], v[180:183], v[220:223], v[2:5]
	v_mfma_f32_16x16x32_bf16 v[54:57], v[176:179], v[198:201], v[54:57]
	v_mfma_f32_16x16x32_bf16 v[50:53], v[184:187], v[198:201], v[50:53]
	v_mfma_f32_16x16x32_bf16 v[38:41], v[176:179], v[208:211], v[38:41]
	v_mfma_f32_16x16x32_bf16 v[34:37], v[184:187], v[208:211], v[34:37]
	v_mfma_f32_16x16x32_bf16 v[22:25], v[176:179], v[216:219], v[22:25]
	v_mfma_f32_16x16x32_bf16 v[18:21], v[184:187], v[216:219], v[18:21]
	v_mfma_f32_16x16x32_bf16 v[6:9], v[176:179], v[228:231], v[6:9]
	v_mfma_f32_16x16x32_bf16 v[2:5], v[184:187], v[228:231], v[2:5]
	s_setprio 0
	s_barrier
	s_add_i32 s53, 0, 0x18000
	v_add_u32_e32 v141, s53, v150
	s_add_i32 s54, 0, 0x1c000
	ds_read_b128 v[156:159], v141
	ds_read_b128 v[160:163], v141 offset:1024
	ds_read_b128 v[164:167], v141 offset:2048
	ds_read_b128 v[168:171], v141 offset:3072
	v_add_u32_e32 v141, s54, v150
	ds_read_b128 v[172:175], v141
	ds_read_b128 v[176:179], v141 offset:1024
	ds_read_b128 v[180:183], v141 offset:2048
	ds_read_b128 v[184:187], v141 offset:3072
	s_mov_b32 m0, s42
	ds_read_b128 v[188:191], v151 offset:32768
	ds_read_b128 v[198:201], v151 offset:33792
	ds_read_b128 v[204:207], v151 offset:34816
	ds_read_b128 v[208:211], v151 offset:35840
	ds_read_b128 v[212:215], v151 offset:36864
	ds_read_b128 v[216:219], v151 offset:37888
	ds_read_b128 v[220:223], v151 offset:38912
	ds_read_b128 v[228:231], v151 offset:39936
	global_load_lds_dwordx4 v135, s[30:31]
	s_mov_b32 m0, s43
	s_nop 0
	global_load_lds_dwordx4 v139, s[30:31]
	s_waitcnt vmcnt(8)
	s_waitcnt lgkmcnt(0)
	s_barrier
	s_setprio 1
	s_waitcnt lgkmcnt(0)
	v_mfma_f32_16x16x32_bf16 v[126:129], v[156:159], v[188:191], v[126:129]
	v_mfma_f32_16x16x32_bf16 v[122:125], v[164:167], v[188:191], v[122:125]
	v_mfma_f32_16x16x32_bf16 v[110:113], v[156:159], v[204:207], v[110:113]
	v_mfma_f32_16x16x32_bf16 v[106:109], v[164:167], v[204:207], v[106:109]
	v_mfma_f32_16x16x32_bf16 v[94:97], v[156:159], v[212:215], v[94:97]
	v_mfma_f32_16x16x32_bf16 v[90:93], v[164:167], v[212:215], v[90:93]
	v_mfma_f32_16x16x32_bf16 v[78:81], v[156:159], v[220:223], v[78:81]
	v_mfma_f32_16x16x32_bf16 v[74:77], v[164:167], v[220:223], v[74:77]
	v_mfma_f32_16x16x32_bf16 v[126:129], v[160:163], v[198:201], v[126:129]
	v_mfma_f32_16x16x32_bf16 v[122:125], v[168:171], v[198:201], v[122:125]
	v_mfma_f32_16x16x32_bf16 v[110:113], v[160:163], v[208:211], v[110:113]
	v_mfma_f32_16x16x32_bf16 v[106:109], v[168:171], v[208:211], v[106:109]
	v_mfma_f32_16x16x32_bf16 v[94:97], v[160:163], v[216:219], v[94:97]
	v_mfma_f32_16x16x32_bf16 v[90:93], v[168:171], v[216:219], v[90:93]
	v_mfma_f32_16x16x32_bf16 v[78:81], v[160:163], v[228:231], v[78:81]
	v_mfma_f32_16x16x32_bf16 v[74:77], v[168:171], v[228:231], v[74:77]
	s_setprio 0
	s_setprio 1
	v_mfma_f32_16x16x32_bf16 v[118:121], v[172:175], v[188:191], v[118:121]
	v_mfma_f32_16x16x32_bf16 v[114:117], v[180:183], v[188:191], v[114:117]
	v_mfma_f32_16x16x32_bf16 v[102:105], v[172:175], v[204:207], v[102:105]
	v_mfma_f32_16x16x32_bf16 v[98:101], v[180:183], v[204:207], v[98:101]
	v_mfma_f32_16x16x32_bf16 v[86:89], v[172:175], v[212:215], v[86:89]
	v_mfma_f32_16x16x32_bf16 v[82:85], v[180:183], v[212:215], v[82:85]
	v_mfma_f32_16x16x32_bf16 v[70:73], v[172:175], v[220:223], v[70:73]
	v_mfma_f32_16x16x32_bf16 v[66:69], v[180:183], v[220:223], v[66:69]
	v_mfma_f32_16x16x32_bf16 v[118:121], v[176:179], v[198:201], v[118:121]
	v_mfma_f32_16x16x32_bf16 v[114:117], v[184:187], v[198:201], v[114:117]
	v_mfma_f32_16x16x32_bf16 v[102:105], v[176:179], v[208:211], v[102:105]
	v_mfma_f32_16x16x32_bf16 v[98:101], v[184:187], v[208:211], v[98:101]
	v_mfma_f32_16x16x32_bf16 v[86:89], v[176:179], v[216:219], v[86:89]
	v_mfma_f32_16x16x32_bf16 v[82:85], v[184:187], v[216:219], v[82:85]
	v_mfma_f32_16x16x32_bf16 v[70:73], v[176:179], v[228:231], v[70:73]
	v_mfma_f32_16x16x32_bf16 v[66:69], v[184:187], v[228:231], v[66:69]
	s_setprio 0
	s_barrier
; #define PG8_STAGE_B(bufoff, gbase) do { _Pragma("unroll") for (int _i = 0; _i < 2; ++_i) \
;         __builtin_amdgcn_global_load_lds((const unsigned*)((const char*)(gbase) + voffB[_i]), (LAS unsigned*)(lds + (bufoff) + ldsw + _i * 8192), 16, 0, 0); } while (0)
; #define PG8_LDA(dst, b, h) do { _Pragma("unroll") for (int m = 0; m < 4; ++m) _Pragma("unroll") for (int k = 0; k < 2; ++k) dst[m][k] = *(const LAS bf16x8*)(lds + PG8_SA(b, h) + aoff + m * 2048 + k * 1024); } while (0)
; #define PG8_WAIT_V(n) asm volatile("s_waitcnt vmcnt(" #n ")" ::: "memory")
; template <class Epi, class Sched, bool GATHER = false>
; __device__ __forceinline__ void gemm_phase(LAS unsigned char* lds, const Gemm g, const Sched& S, const Epi& E) {
;     ...
;         for (int t = 0; t < nt; t += 2) {
;             const bool last = (t == nt - 2);
;             const char* a1 = cA + (size_t)(t + 1) * kstep;
;             const char* a2 = last ? nA : cA + (size_t)(t + 2) * kstep; const char* b2 = last ? nB : cB + (size_t)(t + 2) * kstep;
;             const char* a3 = a2 + kstep; const char* b3 = b2 + kstep;
;             unsigned vo2[2][2];
;             if constexpr (GATHER) {
; #pragma unroll
;             for (int _h = 0; _h < 2; ++_h)
; #pragma unroll
;                 for (int _i = 0; _i < 2; ++_i) vo2[_h][_i] = last ? voN[_h][_i] : voC[_h][_i]; }
;             PG8_LDB(B0, 0, 0); PG8_LDB(B1, 0, 1); PG8_SCHED; PG8_LDA(At, 0, 0); PG8_STAGE_A(PG8_SA(1, 1), a1, voC, 1);
;             PG8_WAIT_V(8); PG8_WAIT_L(0); PG8_BAR; PG8_MMA(0, 0, At, B0); PG8_MMA(0, 1, At, B1); PG8_BAR; PG8_SCHED;
;             PG8_LDA(At, 0, 1); PG8_STAGE_B(PG8_SB(0, 0), b2); PG8_STAGE_B(PG8_SB(0, 1), b2 + hstepB); PG8_STAGE_A(PG8_SA(0, 0), a2, vo2, 0);
;             PG8_WAIT_V(8); PG8_WAIT_L(0); PG8_BAR; PG8_MMA(1, 0, At, B0); PG8_MMA(1, 1, At, B1); PG8_BAR; PG8_SCHED;
;             PG8_LDB(B0, 1, 0); PG8_LDB(B1, 1, 1); PG8_SCHED; PG8_LDA(At, 1, 0); PG8_STAGE_A(PG8_SA(0, 1), a2, vo2, 1);
;             PG8_WAIT_V(8); PG8_WAIT_L(0); PG8_BAR; PG8_MMA(0, 0, At, B0); PG8_MMA(0, 1, At, B1); PG8_BAR; PG8_SCHED;
;             PG8_LDA(At, 1, 1); PG8_STAGE_B(PG8_SB(1, 0), b3); PG8_STAGE_B(PG8_SB(1, 1), b3 + hstepB); PG8_STAGE_A(PG8_SA(1, 0), a3, vo2, 0);
;             PG8_WAIT_V(8); PG8_WAIT_L(0); PG8_BAR; PG8_MMA(1, 0, At, B0); PG8_MMA(1, 1, At, B1); PG8_BAR; PG8_SCHED;
;         }
;         if (wr == 0) PG8_BAR;
	s_add_i32 s30, s53, s40
	v_lshl_add_u64 v[236:237], v[236:237], 0, s[66:67]
	s_mov_b32 m0, s30
	ds_read_b128 v[188:191], v151 offset:49152
	ds_read_b128 v[198:201], v151 offset:50176
	ds_read_b128 v[204:207], v151 offset:51200
	ds_read_b128 v[208:211], v151 offset:52224
	ds_read_b128 v[212:215], v151 offset:53248
	ds_read_b128 v[216:219], v151 offset:54272
	ds_read_b128 v[220:223], v151 offset:55296
	ds_read_b128 v[228:231], v151 offset:56320
	global_load_lds_dwordx4 v[236:237], off
	s_add_i32 m0, s30, 0x2000
	s_add_u32 s28, s28, 0x40080
	v_lshl_add_u64 v[236:237], v[238:239], 0, s[66:67]
	s_addc_u32 s29, s29, 0
	s_add_i32 s30, s54, s40
	global_load_lds_dwordx4 v[236:237], off
	v_lshl_add_u64 v[236:237], s[28:29], 0, v[130:131]
	s_mov_b32 m0, s30
	v_lshl_add_u64 v[192:193], v[192:193], 0, s[66:67]
	global_load_lds_dwordx4 v[236:237], off
	s_add_i32 m0, s30, 0x2000
	v_lshl_add_u64 v[236:237], s[28:29], 0, v[132:133]
	global_load_lds_dwordx4 v[236:237], off
	s_mov_b32 m0, s44
	v_lshl_add_u64 v[236:237], v[240:241], 0, s[66:67]
	global_load_lds_dwordx4 v[236:237], off
	s_mov_b32 m0, s45
	s_nop 0
	global_load_lds_dwordx4 v[192:193], off
	s_waitcnt vmcnt(8)
	s_waitcnt lgkmcnt(0)
	s_barrier
	s_setprio 1
	s_waitcnt lgkmcnt(0)
	v_mfma_f32_16x16x32_bf16 v[62:65], v[156:159], v[188:191], v[62:65]
	v_mfma_f32_16x16x32_bf16 v[58:61], v[164:167], v[188:191], v[58:61]
	v_mfma_f32_16x16x32_bf16 v[46:49], v[156:159], v[204:207], v[46:49]
	v_mfma_f32_16x16x32_bf16 v[42:45], v[164:167], v[204:207], v[42:45]
	v_mfma_f32_16x16x32_bf16 v[30:33], v[156:159], v[212:215], v[30:33]
	v_mfma_f32_16x16x32_bf16 v[26:29], v[164:167], v[212:215], v[26:29]
	v_mfma_f32_16x16x32_bf16 v[14:17], v[156:159], v[220:223], v[14:17]
	v_mfma_f32_16x16x32_bf16 v[10:13], v[164:167], v[220:223], v[10:13]
	v_mfma_f32_16x16x32_bf16 v[62:65], v[160:163], v[198:201], v[62:65]
	v_mfma_f32_16x16x32_bf16 v[58:61], v[168:171], v[198:201], v[58:61]
	v_mfma_f32_16x16x32_bf16 v[46:49], v[160:163], v[208:211], v[46:49]
	v_mfma_f32_16x16x32_bf16 v[42:45], v[168:171], v[208:211], v[42:45]
	v_mfma_f32_16x16x32_bf16 v[30:33], v[160:163], v[216:219], v[30:33]
	v_mfma_f32_16x16x32_bf16 v[26:29], v[168:171], v[216:219], v[26:29]
	v_mfma_f32_16x16x32_bf16 v[14:17], v[160:163], v[228:231], v[14:17]
	v_mfma_f32_16x16x32_bf16 v[10:13], v[168:171], v[228:231], v[10:13]
	s_setprio 0
	s_setprio 1
	v_mfma_f32_16x16x32_bf16 v[54:57], v[172:175], v[188:191], v[54:57]
	v_mfma_f32_16x16x32_bf16 v[50:53], v[180:183], v[188:191], v[50:53]
	v_mfma_f32_16x16x32_bf16 v[38:41], v[172:175], v[204:207], v[38:41]
	v_mfma_f32_16x16x32_bf16 v[34:37], v[180:183], v[204:207], v[34:37]
	v_mfma_f32_16x16x32_bf16 v[22:25], v[172:175], v[212:215], v[22:25]
	v_mfma_f32_16x16x32_bf16 v[18:21], v[180:183], v[212:215], v[18:21]
	v_mfma_f32_16x16x32_bf16 v[6:9], v[172:175], v[220:223], v[6:9]
	v_mfma_f32_16x16x32_bf16 v[2:5], v[180:183], v[220:223], v[2:5]
	v_mfma_f32_16x16x32_bf16 v[54:57], v[176:179], v[198:201], v[54:57]
	v_mfma_f32_16x16x32_bf16 v[50:53], v[184:187], v[198:201], v[50:53]
	v_mfma_f32_16x16x32_bf16 v[38:41], v[176:179], v[208:211], v[38:41]
	v_mfma_f32_16x16x32_bf16 v[34:37], v[184:187], v[208:211], v[34:37]
	v_mfma_f32_16x16x32_bf16 v[22:25], v[176:179], v[216:219], v[22:25]
	v_mfma_f32_16x16x32_bf16 v[18:21], v[184:187], v[216:219], v[18:21]
	v_mfma_f32_16x16x32_bf16 v[6:9], v[176:179], v[228:231], v[6:9]
	v_mfma_f32_16x16x32_bf16 v[2:5], v[184:187], v[228:231], v[2:5]
	s_setprio 0
	s_barrier
	s_add_i32 s52, s52, 2
	s_add_u32 s26, s26, 0x100
	s_addc_u32 s27, s27, 0
	s_cmp_gt_u32 s52, 13
	s_cbranch_scc0 .LBB0_1402
	s_and_b64 vcc, exec, s[16:17]
	s_cbranch_vccz .LBB0_1405
	s_barrier

; #define PG8_STAGE_B(bufoff, gbase) do { _Pragma("unroll") for (int _i = 0; _i < 2; ++_i) \
;         __builtin_amdgcn_global_load_lds((const unsigned*)((const char*)(gbase) + voffB[_i]), (LAS unsigned*)(lds + (bufoff) + ldsw + _i * 8192), 16, 0, 0); } while (0)
; #define PG8_LDA(dst, b, h) do { _Pragma("unroll") for (int m = 0; m < 4; ++m) _Pragma("unroll") for (int k = 0; k < 2; ++k) dst[m][k] = *(const LAS bf16x8*)(lds + PG8_SA(b, h) + aoff + m * 2048 + k * 1024); } while (0)
; #define PG8_WAIT_V(n) asm volatile("s_waitcnt vmcnt(" #n ")" ::: "memory")
; template <class Epi, class Sched, bool GATHER = false>
; __device__ __forceinline__ void gemm_phase(LAS unsigned char* lds, const Gemm g, const Sched& S, const Epi& E) {
;     ...
;         for (int t = 0; t < nt; t += 2) {
;             const bool last = (t == nt - 2);
;             const char* a1 = cA + (size_t)(t + 1) * kstep;
;             const char* a2 = last ? nA : cA + (size_t)(t + 2) * kstep; const char* b2 = last ? nB : cB + (size_t)(t + 2) * kstep;
;             const char* a3 = a2 + kstep; const char* b3 = b2 + kstep;
;             unsigned vo2[2][2];
;             if constexpr (GATHER) {
; #pragma unroll
;             for (int _h = 0; _h < 2; ++_h)
; #pragma unroll
;                 for (int _i = 0; _i < 2; ++_i) vo2[_h][_i] = last ? voN[_h][_i] : voC[_h][_i]; }
;             PG8_LDB(B0, 0, 0); PG8_LDB(B1, 0, 1); PG8_SCHED; PG8_LDA(At, 0, 0); PG8_STAGE_A(PG8_SA(1, 1), a1, voC, 1);
;             PG8_WAIT_V(8); PG8_WAIT_L(0); PG8_BAR; PG8_MMA(0, 0, At, B0); PG8_MMA(0, 1, At, B1); PG8_BAR; PG8_SCHED;
;             PG8_LDA(At, 0, 1); PG8_STAGE_B(PG8_SB(0, 0), b2); PG8_STAGE_B(PG8_SB(0, 1), b2 + hstepB); PG8_STAGE_A(PG8_SA(0, 0), a2, vo2, 0);
;             PG8_WAIT_V(8); PG8_WAIT_L(0); PG8_BAR; PG8_MMA(1, 0, At, B0); PG8_MMA(1, 1, At, B1); PG8_BAR; PG8_SCHED;
;             PG8_LDB(B0, 1, 0); PG8_LDB(B1, 1, 1); PG8_SCHED; PG8_LDA(At, 1, 0); PG8_STAGE_A(PG8_SA(0, 1), a2, vo2, 1);
;             PG8_WAIT_V(8); PG8_WAIT_L(0); PG8_BAR; PG8_MMA(0, 0, At, B0); PG8_MMA(0, 1, At, B1); PG8_BAR; PG8_SCHED;
;             PG8_LDA(At, 1, 1); PG8_STAGE_B(PG8_SB(1, 0), b3); PG8_STAGE_B(PG8_SB(1, 1), b3 + hstepB); PG8_STAGE_A(PG8_SA(1, 0), a3, vo2, 0);
;             PG8_WAIT_V(8); PG8_WAIT_L(0); PG8_BAR; PG8_MMA(1, 0, At, B0); PG8_MMA(1, 1, At, B1); PG8_BAR; PG8_SCHED;
;         }
.LBB0_1478:
	s_add_u32 s28, s26, 0xfffc0080
	s_addc_u32 s29, s27, -1
	s_add_i32 s52, 0, 0x10000
	s_cmp_eq_u32 s51, 12
	s_cselect_b32 s31, s9, s29
	s_cselect_b32 s30, s15, s28
	v_add_u32_e32 v145, s52, v142
	s_cselect_b32 s29, s19, s50
	s_cselect_b32 s28, s48, s49
	s_add_i32 s54, 0, 0x14000
	ds_read_b128 v[146:149], v145
	ds_read_b128 v[150:153], v145 offset:1024
	ds_read_b128 v[154:157], v145 offset:2048
	ds_read_b128 v[158:161], v145 offset:3072
	v_add_u32_e32 v145, s54, v142
	ds_read_b128 v[162:165], v145
	ds_read_b128 v[166:169], v145 offset:1024
	ds_read_b128 v[170:173], v145 offset:2048
	ds_read_b128 v[174:177], v145 offset:3072
	v_lshl_add_u64 v[216:217], s[26:27], 0, v[138:139]
	s_add_i32 m0, s13, 0xc000
	ds_read_b128 v[178:181], v144
	ds_read_b128 v[182:185], v144 offset:1024
	ds_read_b128 v[186:189], v144 offset:2048
	ds_read_b128 v[190:193], v144 offset:3072
	ds_read_b128 v[198:201], v144 offset:4096
	ds_read_b128 v[204:207], v144 offset:5120
	ds_read_b128 v[208:211], v144 offset:6144
	ds_read_b128 v[212:215], v144 offset:7168
	global_load_lds_dwordx4 v[216:217], off
	s_add_i32 m0, s13, 0xe000
	v_lshl_add_u64 v[216:217], s[26:27], 0, v[140:141]
	global_load_lds_dwordx4 v[216:217], off
	s_waitcnt vmcnt(8)
	s_waitcnt lgkmcnt(0)
	s_barrier
	s_setprio 1
	s_waitcnt lgkmcnt(0)
	v_mfma_f32_16x16x32_bf16 v[126:129], v[146:149], v[178:181], v[126:129]
	v_mfma_f32_16x16x32_bf16 v[122:125], v[154:157], v[178:181], v[122:125]
	v_mfma_f32_16x16x32_bf16 v[118:121], v[146:149], v[186:189], v[118:121]
	v_mfma_f32_16x16x32_bf16 v[114:117], v[154:157], v[186:189], v[114:117]
	v_mfma_f32_16x16x32_bf16 v[102:105], v[146:149], v[198:201], v[102:105]
	v_mfma_f32_16x16x32_bf16 v[98:101], v[154:157], v[198:201], v[98:101]
	v_mfma_f32_16x16x32_bf16 v[86:89], v[146:149], v[208:211], v[86:89]
	v_mfma_f32_16x16x32_bf16 v[82:85], v[154:157], v[208:211], v[82:85]
	v_mfma_f32_16x16x32_bf16 v[126:129], v[150:153], v[182:185], v[126:129]
	v_mfma_f32_16x16x32_bf16 v[122:125], v[158:161], v[182:185], v[122:125]
	v_mfma_f32_16x16x32_bf16 v[118:121], v[150:153], v[190:193], v[118:121]
	v_mfma_f32_16x16x32_bf16 v[114:117], v[158:161], v[190:193], v[114:117]
	v_mfma_f32_16x16x32_bf16 v[102:105], v[150:153], v[204:207], v[102:105]
	v_mfma_f32_16x16x32_bf16 v[98:101], v[158:161], v[204:207], v[98:101]
	v_mfma_f32_16x16x32_bf16 v[86:89], v[150:153], v[212:215], v[86:89]
	v_mfma_f32_16x16x32_bf16 v[82:85], v[158:161], v[212:215], v[82:85]
	s_setprio 0
	s_setprio 1
	v_mfma_f32_16x16x32_bf16 v[110:113], v[162:165], v[178:181], v[110:113]
	v_mfma_f32_16x16x32_bf16 v[106:109], v[170:173], v[178:181], v[106:109]
	v_mfma_f32_16x16x32_bf16 v[94:97], v[162:165], v[186:189], v[94:97]
	v_mfma_f32_16x16x32_bf16 v[90:93], v[170:173], v[186:189], v[90:93]
	v_mfma_f32_16x16x32_bf16 v[78:81], v[162:165], v[198:201], v[78:81]
	v_mfma_f32_16x16x32_bf16 v[74:77], v[170:173], v[198:201], v[74:77]
	v_mfma_f32_16x16x32_bf16 v[70:73], v[162:165], v[208:211], v[70:73]
	v_mfma_f32_16x16x32_bf16 v[66:69], v[170:173], v[208:211], v[66:69]
	v_mfma_f32_16x16x32_bf16 v[110:113], v[166:169], v[182:185], v[110:113]
	v_mfma_f32_16x16x32_bf16 v[106:109], v[174:177], v[182:185], v[106:109]
	v_mfma_f32_16x16x32_bf16 v[94:97], v[166:169], v[190:193], v[94:97]
	v_mfma_f32_16x16x32_bf16 v[90:93], v[174:177], v[190:193], v[90:93]
	v_mfma_f32_16x16x32_bf16 v[78:81], v[166:169], v[204:207], v[78:81]
	v_mfma_f32_16x16x32_bf16 v[74:77], v[174:177], v[204:207], v[74:77]
	v_mfma_f32_16x16x32_bf16 v[70:73], v[166:169], v[212:215], v[70:73]
	v_mfma_f32_16x16x32_bf16 v[66:69], v[174:177], v[212:215], v[66:69]
	s_setprio 0
	s_barrier
	s_add_i32 s52, s52, s41
	v_lshl_add_u64 v[216:217], s[28:29], 0, v[130:131]
	s_mov_b32 m0, s52
	ds_read_b128 v[178:181], v144 offset:16384
	ds_read_b128 v[182:185], v144 offset:17408
	ds_read_b128 v[186:189], v144 offset:18432
	ds_read_b128 v[190:193], v144 offset:19456
	ds_read_b128 v[198:201], v144 offset:20480
	ds_read_b128 v[204:207], v144 offset:21504
	ds_read_b128 v[208:211], v144 offset:22528
	ds_read_b128 v[212:215], v144 offset:23552
	global_load_lds_dwordx4 v[216:217], off
	s_add_i32 m0, s52, 0x2000
	s_add_u32 s52, s28, 0x40000
	v_lshl_add_u64 v[218:219], s[28:29], 0, v[132:133]
	s_addc_u32 s53, s29, 0
	s_add_i32 s54, s54, s41
	global_load_lds_dwordx4 v[218:219], off
	v_lshl_add_u64 v[220:221], s[52:53], 0, v[130:131]
	s_mov_b32 m0, s54
	v_lshl_add_u64 v[222:223], s[30:31], 0, v[136:137]
	global_load_lds_dwordx4 v[220:221], off
	s_add_i32 m0, s54, 0x2000
	v_lshl_add_u64 v[220:221], s[52:53], 0, v[132:133]
	global_load_lds_dwordx4 v[220:221], off
	s_mov_b32 m0, s13
	v_lshl_add_u64 v[220:221], s[30:31], 0, v[134:135]
	global_load_lds_dwordx4 v[220:221], off
	s_mov_b32 m0, s42
	s_nop 0
	global_load_lds_dwordx4 v[222:223], off
	s_waitcnt vmcnt(8)
	s_waitcnt lgkmcnt(0)
	s_barrier
; #define PG8_STAGE_B(bufoff, gbase) do { _Pragma("unroll") for (int _i = 0; _i < 2; ++_i) \
;         __builtin_amdgcn_global_load_lds((const unsigned*)((const char*)(gbase) + voffB[_i]), (LAS unsigned*)(lds + (bufoff) + ldsw + _i * 8192), 16, 0, 0); } while (0)
; #define PG8_LDA(dst, b, h) do { _Pragma("unroll") for (int m = 0; m < 4; ++m) _Pragma("unroll") for (int k = 0; k < 2; ++k) dst[m][k] = *(const LAS bf16x8*)(lds + PG8_SA(b, h) + aoff + m * 2048 + k * 1024); } while (0)
; #define PG8_LDB(dst, b, h) do { _Pragma("unroll") for (int n = 0; n < 2; ++n) _Pragma("unroll") for (int k = 0; k < 2; ++k) dst[n][k] = *(const LAS bf16x8*)(lds + PG8_SB(b, h) + boff + n * 2048 + k * 1024); } while (0)
; #define PG8_MMA(ai, bj, At, Bt) do { __builtin_amdgcn_s_setprio(1); _Pragma("unroll") for (int m = 0; m < 4; ++m) _Pragma("unroll") for (int n = 0; n < 2; ++n) _Pragma("unroll") for (int k = 0; k < 2; ++k) \
;         acc[ai][bj][m][n] = __builtin_amdgcn_mfma_f32_16x16x32_bf16(Bt[n][k], At[m][k], acc[ai][bj][m][n], 0, 0, 0); __builtin_amdgcn_s_setprio(0); } while (0)
; #define PG8_WAIT_V(n) asm volatile("s_waitcnt vmcnt(" #n ")" ::: "memory")
; #define PG8_WAIT_L(n) asm volatile("s_waitcnt lgkmcnt(" #n ")" ::: "memory")
; #define PG8_BAR __builtin_amdgcn_s_barrier()
; #define PG8_SCHED __builtin_amdgcn_sched_barrier(0)
; template <class Epi, class Sched, bool GATHER = false>
; __device__ __forceinline__ void gemm_phase(LAS unsigned char* lds, const Gemm g, const Sched& S, const Epi& E) {
;     ...
;             PG8_WAIT_V(8); PG8_WAIT_L(0); PG8_BAR; PG8_MMA(0, 0, At, B0); PG8_MMA(0, 1, At, B1); PG8_BAR; PG8_SCHED;
;             PG8_LDA(At, 0, 1); PG8_STAGE_B(PG8_SB(0, 0), b2); PG8_STAGE_B(PG8_SB(0, 1), b2 + hstepB); PG8_STAGE_A(PG8_SA(0, 0), a2, vo2, 0);
;             PG8_WAIT_V(8); PG8_WAIT_L(0); PG8_BAR; PG8_MMA(1, 0, At, B0); PG8_MMA(1, 1, At, B1); PG8_BAR; PG8_SCHED;
;             PG8_LDB(B0, 1, 0); PG8_LDB(B1, 1, 1); PG8_SCHED; PG8_LDA(At, 1, 0); PG8_STAGE_A(PG8_SA(0, 1), a2, vo2, 1);
;             PG8_WAIT_V(8); PG8_WAIT_L(0); PG8_BAR; PG8_MMA(0, 0, At, B0); PG8_MMA(0, 1, At, B1); PG8_BAR; PG8_SCHED;
	s_setprio 1
	s_waitcnt lgkmcnt(0)
	v_mfma_f32_16x16x32_bf16 v[62:65], v[146:149], v[178:181], v[62:65]
	v_mfma_f32_16x16x32_bf16 v[58:61], v[154:157], v[178:181], v[58:61]
	v_mfma_f32_16x16x32_bf16 v[54:57], v[146:149], v[186:189], v[54:57]
	v_mfma_f32_16x16x32_bf16 v[50:53], v[154:157], v[186:189], v[50:53]
	v_mfma_f32_16x16x32_bf16 v[38:41], v[146:149], v[198:201], v[38:41]
	v_mfma_f32_16x16x32_bf16 v[34:37], v[154:157], v[198:201], v[34:37]
	v_mfma_f32_16x16x32_bf16 v[22:25], v[146:149], v[208:211], v[22:25]
	v_mfma_f32_16x16x32_bf16 v[18:21], v[154:157], v[208:211], v[18:21]
	v_mfma_f32_16x16x32_bf16 v[62:65], v[150:153], v[182:185], v[62:65]
	v_mfma_f32_16x16x32_bf16 v[58:61], v[158:161], v[182:185], v[58:61]
	v_mfma_f32_16x16x32_bf16 v[54:57], v[150:153], v[190:193], v[54:57]
	v_mfma_f32_16x16x32_bf16 v[50:53], v[158:161], v[190:193], v[50:53]
	v_mfma_f32_16x16x32_bf16 v[38:41], v[150:153], v[204:207], v[38:41]
	v_mfma_f32_16x16x32_bf16 v[34:37], v[158:161], v[204:207], v[34:37]
	v_mfma_f32_16x16x32_bf16 v[22:25], v[150:153], v[212:215], v[22:25]
	v_mfma_f32_16x16x32_bf16 v[18:21], v[158:161], v[212:215], v[18:21]
	s_setprio 0
	s_setprio 1
	v_mfma_f32_16x16x32_bf16 v[46:49], v[162:165], v[178:181], v[46:49]
	v_mfma_f32_16x16x32_bf16 v[42:45], v[170:173], v[178:181], v[42:45]
	v_mfma_f32_16x16x32_bf16 v[30:33], v[162:165], v[186:189], v[30:33]
	v_mfma_f32_16x16x32_bf16 v[26:29], v[170:173], v[186:189], v[26:29]
	v_mfma_f32_16x16x32_bf16 v[14:17], v[162:165], v[198:201], v[14:17]
	v_mfma_f32_16x16x32_bf16 v[10:13], v[170:173], v[198:201], v[10:13]
	v_mfma_f32_16x16x32_bf16 v[6:9], v[162:165], v[208:211], v[6:9]
	v_mfma_f32_16x16x32_bf16 v[2:5], v[170:173], v[208:211], v[2:5]
	v_mfma_f32_16x16x32_bf16 v[46:49], v[166:169], v[182:185], v[46:49]
	v_mfma_f32_16x16x32_bf16 v[42:45], v[174:177], v[182:185], v[42:45]
	v_mfma_f32_16x16x32_bf16 v[30:33], v[166:169], v[190:193], v[30:33]
	v_mfma_f32_16x16x32_bf16 v[26:29], v[174:177], v[190:193], v[26:29]
	v_mfma_f32_16x16x32_bf16 v[14:17], v[166:169], v[204:207], v[14:17]
	v_mfma_f32_16x16x32_bf16 v[10:13], v[174:177], v[204:207], v[10:13]
	v_mfma_f32_16x16x32_bf16 v[6:9], v[166:169], v[212:215], v[6:9]
	v_mfma_f32_16x16x32_bf16 v[2:5], v[174:177], v[212:215], v[2:5]
	s_setprio 0
	s_barrier
	s_add_i32 s52, 0, 0x18000
	v_add_u32_e32 v145, s52, v142
	s_add_i32 s53, 0, 0x1c000
	ds_read_b128 v[146:149], v145
	ds_read_b128 v[150:153], v145 offset:1024
	ds_read_b128 v[154:157], v145 offset:2048
	ds_read_b128 v[158:161], v145 offset:3072
	v_add_u32_e32 v145, s53, v142
	ds_read_b128 v[162:165], v145
	ds_read_b128 v[166:169], v145 offset:1024
	ds_read_b128 v[170:173], v145 offset:2048
	ds_read_b128 v[174:177], v145 offset:3072
	s_add_u32 s30, s30, 0x40000
	s_addc_u32 s31, s31, 0
	s_mov_b32 m0, s43
	v_lshl_add_u64 v[228:229], s[30:31], 0, v[134:135]
	ds_read_b128 v[178:181], v144 offset:32768
	ds_read_b128 v[182:185], v144 offset:33792
	ds_read_b128 v[186:189], v144 offset:34816
	ds_read_b128 v[190:193], v144 offset:35840
	ds_read_b128 v[198:201], v144 offset:36864
	ds_read_b128 v[204:207], v144 offset:37888
	ds_read_b128 v[208:211], v144 offset:38912
	ds_read_b128 v[212:215], v144 offset:39936
	global_load_lds_dwordx4 v[228:229], off
	s_mov_b32 m0, s44
	v_lshl_add_u64 v[228:229], s[30:31], 0, v[136:137]
	global_load_lds_dwordx4 v[228:229], off
	s_waitcnt vmcnt(8)
	s_waitcnt lgkmcnt(0)
	s_barrier
	s_setprio 1
	s_waitcnt lgkmcnt(0)
	v_mfma_f32_16x16x32_bf16 v[126:129], v[146:149], v[178:181], v[126:129]
	v_mfma_f32_16x16x32_bf16 v[122:125], v[154:157], v[178:181], v[122:125]
	v_mfma_f32_16x16x32_bf16 v[118:121], v[146:149], v[186:189], v[118:121]
	v_mfma_f32_16x16x32_bf16 v[114:117], v[154:157], v[186:189], v[114:117]
	v_mfma_f32_16x16x32_bf16 v[102:105], v[146:149], v[198:201], v[102:105]
	v_mfma_f32_16x16x32_bf16 v[98:101], v[154:157], v[198:201], v[98:101]
	v_mfma_f32_16x16x32_bf16 v[86:89], v[146:149], v[208:211], v[86:89]
	v_mfma_f32_16x16x32_bf16 v[82:85], v[154:157], v[208:211], v[82:85]
	v_mfma_f32_16x16x32_bf16 v[126:129], v[150:153], v[182:185], v[126:129]
	v_mfma_f32_16x16x32_bf16 v[122:125], v[158:161], v[182:185], v[122:125]
	v_mfma_f32_16x16x32_bf16 v[118:121], v[150:153], v[190:193], v[118:121]
	v_mfma_f32_16x16x32_bf16 v[114:117], v[158:161], v[190:193], v[114:117]
	v_mfma_f32_16x16x32_bf16 v[102:105], v[150:153], v[204:207], v[102:105]
	v_mfma_f32_16x16x32_bf16 v[98:101], v[158:161], v[204:207], v[98:101]
	v_mfma_f32_16x16x32_bf16 v[86:89], v[150:153], v[212:215], v[86:89]
	v_mfma_f32_16x16x32_bf16 v[82:85], v[158:161], v[212:215], v[82:85]
	s_setprio 0
	s_setprio 1
	v_mfma_f32_16x16x32_bf16 v[110:113], v[162:165], v[178:181], v[110:113]
	v_mfma_f32_16x16x32_bf16 v[106:109], v[170:173], v[178:181], v[106:109]
	v_mfma_f32_16x16x32_bf16 v[94:97], v[162:165], v[186:189], v[94:97]
	v_mfma_f32_16x16x32_bf16 v[90:93], v[170:173], v[186:189], v[90:93]
	v_mfma_f32_16x16x32_bf16 v[78:81], v[162:165], v[198:201], v[78:81]
	v_mfma_f32_16x16x32_bf16 v[74:77], v[170:173], v[198:201], v[74:77]
	v_mfma_f32_16x16x32_bf16 v[70:73], v[162:165], v[208:211], v[70:73]
	v_mfma_f32_16x16x32_bf16 v[66:69], v[170:173], v[208:211], v[66:69]
	v_mfma_f32_16x16x32_bf16 v[110:113], v[166:169], v[182:185], v[110:113]
	v_mfma_f32_16x16x32_bf16 v[106:109], v[174:177], v[182:185], v[106:109]
	v_mfma_f32_16x16x32_bf16 v[94:97], v[166:169], v[190:193], v[94:97]
	v_mfma_f32_16x16x32_bf16 v[90:93], v[174:177], v[190:193], v[90:93]
	v_mfma_f32_16x16x32_bf16 v[78:81], v[166:169], v[204:207], v[78:81]
	v_mfma_f32_16x16x32_bf16 v[74:77], v[174:177], v[204:207], v[74:77]
	v_mfma_f32_16x16x32_bf16 v[70:73], v[166:169], v[212:215], v[70:73]
	v_mfma_f32_16x16x32_bf16 v[66:69], v[174:177], v[212:215], v[66:69]
	s_setprio 0
	s_barrier
; #define PG8_STAGE_B(bufoff, gbase) do { _Pragma("unroll") for (int _i = 0; _i < 2; ++_i) \
;         __builtin_amdgcn_global_load_lds((const unsigned*)((const char*)(gbase) + voffB[_i]), (LAS unsigned*)(lds + (bufoff) + ldsw + _i * 8192), 16, 0, 0); } while (0)
; #define PG8_LDA(dst, b, h) do { _Pragma("unroll") for (int m = 0; m < 4; ++m) _Pragma("unroll") for (int k = 0; k < 2; ++k) dst[m][k] = *(const LAS bf16x8*)(lds + PG8_SA(b, h) + aoff + m * 2048 + k * 1024); } while (0)
; #define PG8_WAIT_V(n) asm volatile("s_waitcnt vmcnt(" #n ")" ::: "memory")
; template <class Epi, class Sched, bool GATHER = false>
; __device__ __forceinline__ void gemm_phase(LAS unsigned char* lds, const Gemm g, const Sched& S, const Epi& E) {
;     ...
;         for (int t = 0; t < nt; t += 2) {
;             const bool last = (t == nt - 2);
;             const char* a1 = cA + (size_t)(t + 1) * kstep;
;             const char* a2 = last ? nA : cA + (size_t)(t + 2) * kstep; const char* b2 = last ? nB : cB + (size_t)(t + 2) * kstep;
;             const char* a3 = a2 + kstep; const char* b3 = b2 + kstep;
;             unsigned vo2[2][2];
;             if constexpr (GATHER) {
; #pragma unroll
;             for (int _h = 0; _h < 2; ++_h)
; #pragma unroll
;                 for (int _i = 0; _i < 2; ++_i) vo2[_h][_i] = last ? voN[_h][_i] : voC[_h][_i]; }
;             PG8_LDB(B0, 0, 0); PG8_LDB(B1, 0, 1); PG8_SCHED; PG8_LDA(At, 0, 0); PG8_STAGE_A(PG8_SA(1, 1), a1, voC, 1);
;             PG8_WAIT_V(8); PG8_WAIT_L(0); PG8_BAR; PG8_MMA(0, 0, At, B0); PG8_MMA(0, 1, At, B1); PG8_BAR; PG8_SCHED;
;             PG8_LDA(At, 0, 1); PG8_STAGE_B(PG8_SB(0, 0), b2); PG8_STAGE_B(PG8_SB(0, 1), b2 + hstepB); PG8_STAGE_A(PG8_SA(0, 0), a2, vo2, 0);
;             PG8_WAIT_V(8); PG8_WAIT_L(0); PG8_BAR; PG8_MMA(1, 0, At, B0); PG8_MMA(1, 1, At, B1); PG8_BAR; PG8_SCHED;
;             PG8_LDB(B0, 1, 0); PG8_LDB(B1, 1, 1); PG8_SCHED; PG8_LDA(At, 1, 0); PG8_STAGE_A(PG8_SA(0, 1), a2, vo2, 1);
;             PG8_WAIT_V(8); PG8_WAIT_L(0); PG8_BAR; PG8_MMA(0, 0, At, B0); PG8_MMA(0, 1, At, B1); PG8_BAR; PG8_SCHED;
;             PG8_LDA(At, 1, 1); PG8_STAGE_B(PG8_SB(1, 0), b3); PG8_STAGE_B(PG8_SB(1, 1), b3 + hstepB); PG8_STAGE_A(PG8_SA(1, 0), a3, vo2, 0);
;             PG8_WAIT_V(8); PG8_WAIT_L(0); PG8_BAR; PG8_MMA(1, 0, At, B0); PG8_MMA(1, 1, At, B1); PG8_BAR; PG8_SCHED;
;         }
;         if (wr == 0) PG8_BAR;
	s_add_i32 s30, s52, s41
	v_lshl_add_u64 v[216:217], v[216:217], 0, s[66:67]
	s_mov_b32 m0, s30
	ds_read_b128 v[178:181], v144 offset:49152
	ds_read_b128 v[182:185], v144 offset:50176
	ds_read_b128 v[186:189], v144 offset:51200
	ds_read_b128 v[190:193], v144 offset:52224
	ds_read_b128 v[198:201], v144 offset:53248
	ds_read_b128 v[204:207], v144 offset:54272
	ds_read_b128 v[208:211], v144 offset:55296
	ds_read_b128 v[212:215], v144 offset:56320
	global_load_lds_dwordx4 v[216:217], off
	s_add_i32 m0, s30, 0x2000
	s_add_u32 s28, s28, 0x40080
	v_lshl_add_u64 v[216:217], v[218:219], 0, s[66:67]
	s_addc_u32 s29, s29, 0
	s_add_i32 s30, s53, s41
	global_load_lds_dwordx4 v[216:217], off
	s_mov_b32 m0, s30
	v_lshl_add_u64 v[216:217], s[28:29], 0, v[130:131]
	global_load_lds_dwordx4 v[216:217], off
	s_add_i32 m0, s30, 0x2000
	v_lshl_add_u64 v[216:217], s[28:29], 0, v[132:133]
	global_load_lds_dwordx4 v[216:217], off
	s_mov_b32 m0, s45
	v_lshl_add_u64 v[216:217], v[220:221], 0, s[66:67]
	global_load_lds_dwordx4 v[216:217], off
	s_mov_b32 m0, s46
	v_lshl_add_u64 v[216:217], v[222:223], 0, s[66:67]
	global_load_lds_dwordx4 v[216:217], off
	s_waitcnt vmcnt(8)
	s_waitcnt lgkmcnt(0)
	s_barrier
	s_setprio 1
	s_waitcnt lgkmcnt(0)
	v_mfma_f32_16x16x32_bf16 v[62:65], v[146:149], v[178:181], v[62:65]
	v_mfma_f32_16x16x32_bf16 v[58:61], v[154:157], v[178:181], v[58:61]
	v_mfma_f32_16x16x32_bf16 v[54:57], v[146:149], v[186:189], v[54:57]
	v_mfma_f32_16x16x32_bf16 v[50:53], v[154:157], v[186:189], v[50:53]
	v_mfma_f32_16x16x32_bf16 v[38:41], v[146:149], v[198:201], v[38:41]
	v_mfma_f32_16x16x32_bf16 v[34:37], v[154:157], v[198:201], v[34:37]
	v_mfma_f32_16x16x32_bf16 v[22:25], v[146:149], v[208:211], v[22:25]
	v_mfma_f32_16x16x32_bf16 v[18:21], v[154:157], v[208:211], v[18:21]
	v_mfma_f32_16x16x32_bf16 v[62:65], v[150:153], v[182:185], v[62:65]
	v_mfma_f32_16x16x32_bf16 v[58:61], v[158:161], v[182:185], v[58:61]
	v_mfma_f32_16x16x32_bf16 v[54:57], v[150:153], v[190:193], v[54:57]
	v_mfma_f32_16x16x32_bf16 v[50:53], v[158:161], v[190:193], v[50:53]
	v_mfma_f32_16x16x32_bf16 v[38:41], v[150:153], v[204:207], v[38:41]
	v_mfma_f32_16x16x32_bf16 v[34:37], v[158:161], v[204:207], v[34:37]
	v_mfma_f32_16x16x32_bf16 v[22:25], v[150:153], v[212:215], v[22:25]
	v_mfma_f32_16x16x32_bf16 v[18:21], v[158:161], v[212:215], v[18:21]
	s_setprio 0
	s_setprio 1
	v_mfma_f32_16x16x32_bf16 v[46:49], v[162:165], v[178:181], v[46:49]
	v_mfma_f32_16x16x32_bf16 v[42:45], v[170:173], v[178:181], v[42:45]
	v_mfma_f32_16x16x32_bf16 v[30:33], v[162:165], v[186:189], v[30:33]
	v_mfma_f32_16x16x32_bf16 v[26:29], v[170:173], v[186:189], v[26:29]
	v_mfma_f32_16x16x32_bf16 v[14:17], v[162:165], v[198:201], v[14:17]
	v_mfma_f32_16x16x32_bf16 v[10:13], v[170:173], v[198:201], v[10:13]
	v_mfma_f32_16x16x32_bf16 v[6:9], v[162:165], v[208:211], v[6:9]
	v_mfma_f32_16x16x32_bf16 v[2:5], v[170:173], v[208:211], v[2:5]
	v_mfma_f32_16x16x32_bf16 v[46:49], v[166:169], v[182:185], v[46:49]
	v_mfma_f32_16x16x32_bf16 v[42:45], v[174:177], v[182:185], v[42:45]
	v_mfma_f32_16x16x32_bf16 v[30:33], v[166:169], v[190:193], v[30:33]
	v_mfma_f32_16x16x32_bf16 v[26:29], v[174:177], v[190:193], v[26:29]
	v_mfma_f32_16x16x32_bf16 v[14:17], v[166:169], v[204:207], v[14:17]
	v_mfma_f32_16x16x32_bf16 v[10:13], v[174:177], v[204:207], v[10:13]
	v_mfma_f32_16x16x32_bf16 v[6:9], v[166:169], v[212:215], v[6:9]
	v_mfma_f32_16x16x32_bf16 v[2:5], v[174:177], v[212:215], v[2:5]
	s_setprio 0
	s_barrier
	s_add_i32 s51, s51, 2
	s_add_u32 s26, s26, 0x100
	s_addc_u32 s27, s27, 0
	s_add_u32 s49, s49, 0x100
	s_addc_u32 s50, s50, 0
	s_cmp_gt_u32 s51, 13
	s_cbranch_scc0 .LBB0_1478
	s_and_b64 vcc, exec, s[10:11]
	s_cbranch_vccz .LBB0_1481
	s_barrier
